# adds: 4-fragment variant of MoE-up loop when a row-wave has <=64 valid rows; router K-loop weight loads hoisted (one memory round trip per k-step); MoE-down body as a loop
# speedup vs baseline: 1.0406x; 1.0065x over previous
; __device__ __forceinline__ unsigned f2bf(float f) { unsigned u = __builtin_bit_cast(unsigned, f); return (u + 0x7fffu + ((u >> 16) & 1u)) >> 16; }
; __device__ __forceinline__ void rt_step(const RtLoad& L, const bf16_t* bh, const bf16_t* bl, f32x4 (&acc)[2][5], float (&ss)[2], int ko) {
;     RtW W;
; #pragma unroll
;     for (int n = 0; n < 5; ++n) { W.wh[n] = *(const bf16x8*)(bh + (size_t)n * 16 * D + ko); W.wl[n] = *(const bf16x8*)(bl + (size_t)n * 16 * D + ko); }
;     bf16x8 ahi[2], alo[2];
; #pragma unroll
;     for (int mi = 0; mi < 2; ++mi) { const u32x4 xw = L.x[mi]; const f32x4 xa = (f32x4){bflo(xw.x), bfhi(xw.x), bflo(xw.y), bfhi(xw.y)}, xb = (f32x4){bflo(xw.z), bfhi(xw.z), bflo(xw.w), bfhi(xw.w)};
;         ss[mi] += (xa.x * xa.x + xa.y * xa.y) + (xa.z * xa.z + xa.w * xa.w) + (xb.x * xb.x + xb.y * xb.y) + (xb.z * xb.z + xb.w * xb.w);
;         const float u[8] = {xa.x * L.g[0].x, xa.y * L.g[0].y, xa.z * L.g[0].z, xa.w * L.g[0].w, xb.x * L.g[1].x, xb.y * L.g[1].y, xb.z * L.g[1].z, xb.w * L.g[1].w};
;         unsigned hb[8]; float lo[8];
; #pragma unroll
;         for (int j = 0; j < 8; ++j) { hb[j] = f2bf(u[j]); lo[j] = u[j] - __builtin_bit_cast(float, hb[j] << 16); }
;         const u32x4 hw = (u32x4){hb[0] | (hb[1] << 16), hb[2] | (hb[3] << 16), hb[4] | (hb[5] << 16), hb[6] | (hb[7] << 16)};
;         const u32x4 lw = (u32x4){pk2(lo[0], lo[1]), pk2(lo[2], lo[3]), pk2(lo[4], lo[5]), pk2(lo[6], lo[7])};
;         ahi[mi] = __builtin_bit_cast(bf16x8, hw); alo[mi] = __builtin_bit_cast(bf16x8, lw); }
; #pragma unroll
;     for (int n = 0; n < 5; ++n)
; #pragma unroll
;         for (int mi = 0; mi < 2; ++mi) { acc[mi][n] = __builtin_amdgcn_mfma_f32_16x16x32_bf16(ahi[mi], W.wh[n], acc[mi][n], 0, 0, 0);
;             acc[mi][n] = __builtin_amdgcn_mfma_f32_16x16x32_bf16(alo[mi], W.wh[n], acc[mi][n], 0, 0, 0);
;             acc[mi][n] = __builtin_amdgcn_mfma_f32_16x16x32_bf16(ahi[mi], W.wl[n], acc[mi][n], 0, 0, 0); }
; __device__ __forceinline__ void p5_router(Frame& F) {
;     ...
;           RtLoad La, Lb; rt_load(La, h0, h1, gp, 0);
; #pragma unroll 1
;           for (int ks = 0; ks < 32; ks += 2) {
;               rt_load(Lb, h0, h1, gp, (ks + 1) * 32); rt_step(La, bh, bl, acc, ss, ks * 32);
;               if (ks + 2 < 32) rt_load(La, h0, h1, gp, (ks + 2) * 32);
;               rt_step(Lb, bh, bl, acc, ss, (ks + 1) * 32); }
.LBB0_607:
	global_load_dwordx4 v[58:61], v[66:67], off offset:64
	global_load_dwordx4 v[62:65], v[124:125], off offset:64
	s_waitcnt vmcnt(0)
	global_load_dwordx4 v[196:199], v[180:181], off offset:64
	global_load_dwordx4 v[200:203], v[182:183], off offset:64
	global_load_dwordx4 v[204:207], v[184:185], off offset:64
	global_load_dwordx4 v[208:211], v[186:187], off offset:64
	global_load_dwordx4 v[212:215], v[188:189], off offset:64
	global_load_dwordx4 v[216:219], v[190:191], off offset:64
	global_load_dwordx4 v[220:223], v[192:193], off offset:64
	global_load_dwordx4 v[224:227], v[194:195], off offset:64
	v_lshlrev_b32_e32 v125, 16, v81
	v_lshlrev_b32_e32 v124, 16, v80
	v_mov_b32_e32 v162, v76
	v_mov_b32_e32 v163, v78
	v_pk_mul_f32 v[66:67], v[162:163], v[124:125]
	v_and_b32_e32 v81, 0xffff0000, v81
	v_and_b32_sdwa v86, v67, v153 dst_sel:DWORD dst_unused:UNUSED_PAD src0_sel:WORD_1 src1_sel:DWORD
	v_and_b32_sdwa v97, v66, v153 dst_sel:DWORD dst_unused:UNUSED_PAD src0_sel:WORD_1 src1_sel:DWORD
	v_and_b32_e32 v80, 0xffff0000, v80
	v_mov_b32_e32 v78, v77
	v_add3_u32 v86, v67, v86, s56
	v_add3_u32 v97, v66, v97, s56
	v_pk_mul_f32 v[76:77], v[78:79], v[80:81]
	v_and_b32_e32 v67, 0xffff0000, v86
	v_and_b32_e32 v66, 0xffff0000, v97
	v_pk_fma_f32 v[158:159], v[162:163], v[124:125], v[66:67] neg_lo:[0,0,1] neg_hi:[0,0,1]
	v_and_b32_sdwa v66, v77, v153 dst_sel:DWORD dst_unused:UNUSED_PAD src0_sel:WORD_1 src1_sel:DWORD
	v_and_b32_sdwa v67, v76, v153 dst_sel:DWORD dst_unused:UNUSED_PAD src0_sel:WORD_1 src1_sel:DWORD
	v_add3_u32 v66, v77, v66, s56
	v_add3_u32 v76, v76, v67, s56
	v_and_b32_e32 v67, 0xffff0000, v66
	v_and_b32_e32 v66, 0xffff0000, v76
	v_lshlrev_b32_e32 v77, 16, v83
	v_lshlrev_b32_e32 v76, 16, v82
	v_and_b32_e32 v83, 0xffff0000, v83
	v_and_b32_e32 v82, 0xffff0000, v82
	v_mov_b32_e32 v165, v70
	v_mov_b32_e32 v70, v69
	v_mov_b32_e32 v164, v68
	v_pk_mul_f32 v[68:69], v[70:71], v[82:83]
	v_pk_mul_f32 v[166:167], v[164:165], v[76:77]
	v_and_b32_sdwa v172, v69, v153 dst_sel:DWORD dst_unused:UNUSED_PAD src0_sel:WORD_1 src1_sel:DWORD
	v_and_b32_sdwa v173, v68, v153 dst_sel:DWORD dst_unused:UNUSED_PAD src0_sel:WORD_1 src1_sel:DWORD
	v_pk_fma_f32 v[160:161], v[78:79], v[80:81], v[66:67] neg_lo:[0,0,1] neg_hi:[0,0,1]
	v_or_b32_sdwa v66, v66, v97 dst_sel:DWORD dst_unused:UNUSED_PAD src0_sel:DWORD src1_sel:WORD_1
	v_or_b32_sdwa v67, v67, v86 dst_sel:DWORD dst_unused:UNUSED_PAD src0_sel:DWORD src1_sel:WORD_1
	v_and_b32_sdwa v86, v167, v153 dst_sel:DWORD dst_unused:UNUSED_PAD src0_sel:WORD_1 src1_sel:DWORD
	v_and_b32_sdwa v97, v166, v153 dst_sel:DWORD dst_unused:UNUSED_PAD src0_sel:WORD_1 src1_sel:DWORD
	v_add3_u32 v69, v69, v172, s56
	v_add3_u32 v68, v68, v173, s56
	v_add3_u32 v86, v167, v86, s56
	v_add3_u32 v97, v166, v97, s56
	v_and_b32_e32 v69, 0xffff0000, v69
	v_and_b32_e32 v68, 0xffff0000, v68
	v_and_b32_e32 v167, 0xffff0000, v86
	v_and_b32_e32 v166, 0xffff0000, v97
	v_pk_fma_f32 v[172:173], v[70:71], v[82:83], v[68:69] neg_lo:[0,0,1] neg_hi:[0,0,1]
	v_pk_fma_f32 v[166:167], v[164:165], v[76:77], v[166:167] neg_lo:[0,0,1] neg_hi:[0,0,1]
	v_or_b32_sdwa v68, v68, v97 dst_sel:DWORD dst_unused:UNUSED_PAD src0_sel:DWORD src1_sel:WORD_1
	v_or_b32_sdwa v69, v69, v86 dst_sel:DWORD dst_unused:UNUSED_PAD src0_sel:DWORD src1_sel:WORD_1
	v_bfe_u32 v86, v173, 16, 1
	v_bfe_u32 v97, v172, 16, 1
	v_bfe_u32 v174, v161, 16, 1
	v_bfe_u32 v175, v160, 16, 1
	v_add3_u32 v97, v172, v97, s56
	v_add3_u32 v86, v173, v86, s56
	v_bfe_u32 v172, v166, 16, 1
	v_bfe_u32 v173, v167, 16, 1
	v_add3_u32 v175, v160, v175, s56
	v_add3_u32 v174, v161, v174, s56
	v_bfe_u32 v160, v158, 16, 1
	v_bfe_u32 v161, v159, 16, 1
	v_add3_u32 v167, v167, v173, s56
	v_add3_u32 v166, v166, v172, s56
	v_add3_u32 v159, v159, v161, s56
	v_add3_u32 v158, v158, v160, s56
	v_lshrrev_b32_e32 v160, 16, v166
	v_lshrrev_b32_e32 v161, 16, v167
	v_lshlrev_b32_e32 v167, 16, v73
	v_lshlrev_b32_e32 v166, 16, v72
	v_and_b32_e32 v173, 0xffff0000, v73
	v_and_b32_e32 v172, 0xffff0000, v72
	v_pk_mul_f32 v[72:73], v[162:163], v[166:167]
	v_and_or_b32 v161, v86, s55, v161
	v_and_or_b32 v160, v97, s55, v160
	v_and_b32_sdwa v86, v73, v153 dst_sel:DWORD dst_unused:UNUSED_PAD src0_sel:WORD_1 src1_sel:DWORD
	v_and_b32_sdwa v97, v72, v153 dst_sel:DWORD dst_unused:UNUSED_PAD src0_sel:WORD_1 src1_sel:DWORD
	v_lshrrev_b32_e32 v158, 16, v158
	v_lshrrev_b32_e32 v159, 16, v159
	v_add3_u32 v86, v73, v86, s56
	v_add3_u32 v97, v72, v97, s56
	v_and_or_b32 v159, v174, s55, v159
	v_and_or_b32 v158, v175, s55, v158
	v_pk_mul_f32 v[174:175], v[78:79], v[172:173]
	v_and_b32_e32 v73, 0xffff0000, v86
	v_and_b32_e32 v72, 0xffff0000, v97
	v_pk_fma_f32 v[162:163], v[162:163], v[166:167], v[72:73] neg_lo:[0,0,1] neg_hi:[0,0,1]
	v_and_b32_sdwa v72, v175, v153 dst_sel:DWORD dst_unused:UNUSED_PAD src0_sel:WORD_1 src1_sel:DWORD
	v_and_b32_sdwa v73, v174, v153 dst_sel:DWORD dst_unused:UNUSED_PAD src0_sel:WORD_1 src1_sel:DWORD
	v_add3_u32 v72, v175, v72, s56
	v_add3_u32 v174, v174, v73, s56
	v_and_b32_e32 v73, 0xffff0000, v72
	v_and_b32_e32 v72, 0xffff0000, v174
	v_lshlrev_b32_e32 v175, 16, v75
	v_lshlrev_b32_e32 v174, 16, v74
	v_and_b32_e32 v177, 0xffff0000, v75
	v_and_b32_e32 v176, 0xffff0000, v74
	v_pk_mul_f32 v[74:75], v[164:165], v[174:175]
	v_pk_fma_f32 v[78:79], v[78:79], v[172:173], v[72:73] neg_lo:[0,0,1] neg_hi:[0,0,1]
	v_or_b32_sdwa v72, v72, v97 dst_sel:DWORD dst_unused:UNUSED_PAD src0_sel:DWORD src1_sel:WORD_1
	v_or_b32_sdwa v73, v73, v86 dst_sel:DWORD dst_unused:UNUSED_PAD src0_sel:DWORD src1_sel:WORD_1
	v_and_b32_sdwa v86, v75, v153 dst_sel:DWORD dst_unused:UNUSED_PAD src0_sel:WORD_1 src1_sel:DWORD
; __device__ __forceinline__ unsigned f2bf(float f) { unsigned u = __builtin_bit_cast(unsigned, f); return (u + 0x7fffu + ((u >> 16) & 1u)) >> 16; }
; __device__ __forceinline__ unsigned pk2(float lo, float hi) { return f2bf(lo) | (f2bf(hi) << 16); }
; __device__ __forceinline__ void rt_step(const RtLoad& L, const bf16_t* bh, const bf16_t* bl, f32x4 (&acc)[2][5], float (&ss)[2], int ko) {
;     RtW W;
; #pragma unroll
;     for (int n = 0; n < 5; ++n) { W.wh[n] = *(const bf16x8*)(bh + (size_t)n * 16 * D + ko); W.wl[n] = *(const bf16x8*)(bl + (size_t)n * 16 * D + ko); }
;     bf16x8 ahi[2], alo[2];
; #pragma unroll
;     for (int mi = 0; mi < 2; ++mi) { const u32x4 xw = L.x[mi]; const f32x4 xa = (f32x4){bflo(xw.x), bfhi(xw.x), bflo(xw.y), bfhi(xw.y)}, xb = (f32x4){bflo(xw.z), bfhi(xw.z), bflo(xw.w), bfhi(xw.w)};
;         ss[mi] += (xa.x * xa.x + xa.y * xa.y) + (xa.z * xa.z + xa.w * xa.w) + (xb.x * xb.x + xb.y * xb.y) + (xb.z * xb.z + xb.w * xb.w);
;         const float u[8] = {xa.x * L.g[0].x, xa.y * L.g[0].y, xa.z * L.g[0].z, xa.w * L.g[0].w, xb.x * L.g[1].x, xb.y * L.g[1].y, xb.z * L.g[1].z, xb.w * L.g[1].w};
;         unsigned hb[8]; float lo[8];
; #pragma unroll
;         for (int j = 0; j < 8; ++j) { hb[j] = f2bf(u[j]); lo[j] = u[j] - __builtin_bit_cast(float, hb[j] << 16); }
;         const u32x4 hw = (u32x4){hb[0] | (hb[1] << 16), hb[2] | (hb[3] << 16), hb[4] | (hb[5] << 16), hb[6] | (hb[7] << 16)};
;         const u32x4 lw = (u32x4){pk2(lo[0], lo[1]), pk2(lo[2], lo[3]), pk2(lo[4], lo[5]), pk2(lo[6], lo[7])};
;         ahi[mi] = __builtin_bit_cast(bf16x8, hw); alo[mi] = __builtin_bit_cast(bf16x8, lw); }
; #pragma unroll
;     for (int n = 0; n < 5; ++n)
; #pragma unroll
;         for (int mi = 0; mi < 2; ++mi) { acc[mi][n] = __builtin_amdgcn_mfma_f32_16x16x32_bf16(ahi[mi], W.wh[n], acc[mi][n], 0, 0, 0);
;             acc[mi][n] = __builtin_amdgcn_mfma_f32_16x16x32_bf16(alo[mi], W.wh[n], acc[mi][n], 0, 0, 0);
;             acc[mi][n] = __builtin_amdgcn_mfma_f32_16x16x32_bf16(ahi[mi], W.wl[n], acc[mi][n], 0, 0, 0); }
	v_and_b32_sdwa v97, v74, v153 dst_sel:DWORD dst_unused:UNUSED_PAD src0_sel:WORD_1 src1_sel:DWORD
	v_add3_u32 v86, v75, v86, s56
	v_add3_u32 v97, v74, v97, s56
	v_pk_mul_f32 v[178:179], v[70:71], v[176:177]
	v_and_b32_e32 v75, 0xffff0000, v86
	v_and_b32_e32 v74, 0xffff0000, v97
	v_pk_fma_f32 v[164:165], v[164:165], v[174:175], v[74:75] neg_lo:[0,0,1] neg_hi:[0,0,1]
	v_and_b32_sdwa v74, v179, v153 dst_sel:DWORD dst_unused:UNUSED_PAD src0_sel:WORD_1 src1_sel:DWORD
	v_and_b32_sdwa v75, v178, v153 dst_sel:DWORD dst_unused:UNUSED_PAD src0_sel:WORD_1 src1_sel:DWORD
	v_add3_u32 v74, v179, v74, s56
	v_add3_u32 v178, v178, v75, s56
	v_and_b32_e32 v75, 0xffff0000, v74
	v_and_b32_e32 v74, 0xffff0000, v178
	v_pk_fma_f32 v[70:71], v[70:71], v[176:177], v[74:75] neg_lo:[0,0,1] neg_hi:[0,0,1]
	v_or_b32_sdwa v74, v74, v97 dst_sel:DWORD dst_unused:UNUSED_PAD src0_sel:DWORD src1_sel:WORD_1
	v_or_b32_sdwa v75, v75, v86 dst_sel:DWORD dst_unused:UNUSED_PAD src0_sel:DWORD src1_sel:WORD_1
	v_bfe_u32 v86, v71, 16, 1
	v_bfe_u32 v97, v70, 16, 1
	v_bfe_u32 v178, v79, 16, 1
	v_bfe_u32 v179, v78, 16, 1
	v_add3_u32 v78, v78, v179, s56
	v_add3_u32 v79, v79, v178, s56
	v_add3_u32 v70, v70, v97, s56
	v_add3_u32 v71, v71, v86, s56
	v_bfe_u32 v86, v162, 16, 1
	v_bfe_u32 v97, v163, 16, 1
	v_bfe_u32 v178, v164, 16, 1
	v_bfe_u32 v179, v165, 16, 1
	v_add3_u32 v165, v165, v179, s56
	v_add3_u32 v164, v164, v178, s56
	v_add3_u32 v97, v163, v97, s56
	v_add3_u32 v86, v162, v86, s56
	v_lshrrev_b32_e32 v86, 16, v86
	v_lshrrev_b32_e32 v97, 16, v97
	v_lshrrev_b32_e32 v162, 16, v164
	v_lshrrev_b32_e32 v163, 16, v165
	v_and_or_b32 v165, v71, s55, v163
	v_and_or_b32 v164, v70, s55, v162
	v_and_or_b32 v163, v79, s55, v97
	v_and_or_b32 v162, v78, s55, v86
	v_mfma_f32_16x16x32_bf16 v[30:33], v[66:69], v[58:61], v[30:33]
	v_mul_f32_e64 v70, v110, v110
	v_mul_f32_e64 v71, v111, v111
	v_mov_b32_e32 v78, v82
	v_mov_b32_e32 v79, v176
	v_mfma_f32_16x16x32_bf16 v[18:21], v[72:75], v[58:61], v[18:21]
	v_mov_b32_e32 v176, v83
	s_add_i32 s8, s8, 2
	v_lshl_add_u64 v[104:105], v[104:105], 0, s[38:39]
	v_mfma_f32_16x16x32_bf16 v[30:33], v[158:161], v[58:61], v[30:33]
	v_lshl_add_u64 v[100:101], v[100:101], 0, s[40:41]
	v_lshl_add_u64 v[102:103], v[102:103], 0, s[40:41]
	s_and_b64 vcc, exec, s[0:1]
	v_mfma_f32_16x16x32_bf16 v[18:21], v[162:165], v[58:61], v[18:21]
	v_mfma_f32_16x16x32_bf16 v[30:33], v[66:69], v[62:65], v[30:33]
	v_mfma_f32_16x16x32_bf16 v[18:21], v[72:75], v[62:65], v[18:21]
	s_nop 0
	s_waitcnt vmcnt(0)
	v_mfma_f32_16x16x32_bf16 v[34:37], v[66:69], v[196:199], v[34:37]
	v_mfma_f32_16x16x32_bf16 v[22:25], v[72:75], v[196:199], v[22:25]
	v_mfma_f32_16x16x32_bf16 v[34:37], v[158:161], v[196:199], v[34:37]
	v_mfma_f32_16x16x32_bf16 v[22:25], v[162:165], v[196:199], v[22:25]
	v_mfma_f32_16x16x32_bf16 v[34:37], v[66:69], v[200:203], v[34:37]
	v_mfma_f32_16x16x32_bf16 v[22:25], v[72:75], v[200:203], v[22:25]
	s_nop 0
	s_waitcnt vmcnt(0)
	v_mfma_f32_16x16x32_bf16 v[38:41], v[66:69], v[204:207], v[38:41]
	v_mfma_f32_16x16x32_bf16 v[26:29], v[72:75], v[204:207], v[26:29]
	v_mfma_f32_16x16x32_bf16 v[38:41], v[158:161], v[204:207], v[38:41]
	v_mfma_f32_16x16x32_bf16 v[26:29], v[162:165], v[204:207], v[26:29]
	v_mfma_f32_16x16x32_bf16 v[38:41], v[66:69], v[208:211], v[38:41]
	v_mfma_f32_16x16x32_bf16 v[26:29], v[72:75], v[208:211], v[26:29]
	v_mul_f32_e64 v64, v116, v116
	v_mul_f32_e64 v65, v117, v117
	v_pk_fma_f32 v[62:63], v[108:109], v[108:109], v[70:71]
	v_pk_fma_f32 v[64:65], v[112:113], v[112:113], v[64:65]
	v_mfma_f32_16x16x32_bf16 v[46:49], v[66:69], v[212:215], v[46:49]
	v_add_f32_e64 v62, v62, v64
	v_add_f32_e64 v63, v63, v65
	v_pk_mul_f32 v[64:65], v[120:121], v[120:121]
	v_mov_b32_e32 v70, v80
	s_waitcnt vmcnt(0)
	v_mfma_f32_16x16x32_bf16 v[54:57], v[66:69], v[220:223], v[54:57]
	v_fma_f32 v64, v114, v114, v64
	v_fma_f32 v65, v115, v115, v65
	v_mov_b32_e32 v71, v172
	v_pk_add_f32 v[62:63], v[64:65], v[62:63]
	v_mfma_f32_16x16x32_bf16 v[42:45], v[72:75], v[212:215], v[42:45]
	v_mul_f32_e64 v64, v122, v122
	v_mul_f32_e64 v65, v123, v123
	v_pk_mul_f32 v[70:71], v[70:71], v[70:71]
	v_pk_fma_f32 v[64:65], v[118:119], v[118:119], v[64:65]
	v_mfma_f32_16x16x32_bf16 v[50:53], v[72:75], v[220:223], v[50:53]
	v_add_f32_e64 v62, v64, v62
	v_add_f32_e64 v63, v65, v63
	v_mov_b32_e32 v64, v124
	v_mov_b32_e32 v65, v166
	v_mfma_f32_16x16x32_bf16 v[46:49], v[158:161], v[212:215], v[46:49]
	v_mov_b32_e32 v172, v81
	v_pk_fma_f32 v[64:65], v[64:65], v[64:65], v[70:71]
	v_mov_b32_e32 v166, v125
	v_mfma_f32_16x16x32_bf16 v[54:57], v[158:161], v[220:223], v[54:57]
	v_mul_f32_e64 v70, v172, v172
	v_mul_f32_e64 v71, v173, v173
	v_pk_add_f32 v[62:63], v[106:107], v[62:63]
	v_pk_fma_f32 v[70:71], v[166:167], v[166:167], v[70:71]
	v_mfma_f32_16x16x32_bf16 v[42:45], v[162:165], v[212:215], v[42:45]
	v_add_f32_e64 v64, v64, v70
	v_add_f32_e64 v65, v65, v71
	v_mov_b32_e32 v70, v76
	v_mov_b32_e32 v71, v174
	v_mfma_f32_16x16x32_bf16 v[50:53], v[162:165], v[220:223], v[50:53]
	v_mov_b32_e32 v174, v77
	v_mfma_f32_16x16x32_bf16 v[46:49], v[66:69], v[216:219], v[46:49]
	v_mfma_f32_16x16x32_bf16 v[54:57], v[66:69], v[224:227], v[54:57]
	v_mul_f32_e64 v66, v78, v78
	v_mul_f32_e64 v67, v79, v79
	v_pk_mul_f32 v[68:69], v[176:177], v[176:177]
	v_pk_fma_f32 v[66:67], v[70:71], v[70:71], v[66:67]
	v_mfma_f32_16x16x32_bf16 v[42:45], v[72:75], v[216:219], v[42:45]
	v_fma_f32 v68, v174, v174, v68
	v_fma_f32 v69, v175, v175, v69
	v_pk_add_f32 v[64:65], v[66:67], v[64:65]
	v_mfma_f32_16x16x32_bf16 v[50:53], v[72:75], v[224:227], v[50:53]
	v_add_f32_e64 v64, v68, v64
	v_add_f32_e64 v65, v69, v65
	v_pk_add_f32 v[106:107], v[62:63], v[64:65]
	s_cbranch_vccnz .LBB0_610
; __device__ __forceinline__ void rt_step(const RtLoad& L, const bf16_t* bh, const bf16_t* bl, f32x4 (&acc)[2][5], float (&ss)[2], int ko) {
;     RtW W;
; #pragma unroll
;     for (int n = 0; n < 5; ++n) { W.wh[n] = *(const bf16x8*)(bh + (size_t)n * 16 * D + ko); W.wl[n] = *(const bf16x8*)(bl + (size_t)n * 16 * D + ko); }
; __device__ __forceinline__ void p5_router(Frame& F) {
;     ...
;           RtLoad La, Lb; rt_load(La, h0, h1, gp, 0);
; #pragma unroll 1
;           for (int ks = 0; ks < 32; ks += 2) {
;               rt_load(Lb, h0, h1, gp, (ks + 1) * 32); rt_step(La, bh, bl, acc, ss, ks * 32);
;               if (ks + 2 < 32) rt_load(La, h0, h1, gp, (ks + 2) * 32);
;               rt_step(Lb, bh, bl, acc, ss, (ks + 1) * 32); }
.LBB0_608:
	v_lshl_add_u64 v[68:69], v[102:103], 0, s[24:25]
	v_add_co_u32_e32 v66, vcc, s45, v68
	s_waitcnt vmcnt(0)
	v_lshlrev_b32_e32 v108, 16, v2
	v_addc_co_u32_e32 v67, vcc, 0, v69, vcc
	v_add_co_u32_e32 v124, vcc, s46, v68
	v_lshlrev_b32_e32 v112, 16, v3
	s_nop 0
	v_addc_co_u32_e32 v125, vcc, 0, v69, vcc
	global_load_dwordx4 v[58:61], v[66:67], off
	global_load_dwordx4 v[62:65], v[124:125], off
	v_add_co_u32_e32 v180, vcc, s47, v68
	s_nop 1
	v_addc_co_u32_e32 v181, vcc, 0, v69, vcc
	v_add_co_u32_e32 v182, vcc, s48, v68
	s_nop 1
	v_addc_co_u32_e32 v183, vcc, 0, v69, vcc
	v_add_co_u32_e32 v184, vcc, s49, v68
	s_nop 1
	v_addc_co_u32_e32 v185, vcc, 0, v69, vcc
	v_add_co_u32_e32 v186, vcc, s50, v68
	s_nop 1
	v_addc_co_u32_e32 v187, vcc, 0, v69, vcc
	v_add_co_u32_e32 v188, vcc, s51, v68
	s_nop 1
	v_addc_co_u32_e32 v189, vcc, 0, v69, vcc
	v_add_co_u32_e32 v190, vcc, s52, v68
	s_nop 1
	v_addc_co_u32_e32 v191, vcc, 0, v69, vcc
	v_add_co_u32_e32 v192, vcc, s53, v68
	s_nop 1
	v_addc_co_u32_e32 v193, vcc, 0, v69, vcc
	v_add_co_u32_e32 v194, vcc, s54, v68
	s_nop 1
	v_addc_co_u32_e32 v195, vcc, 0, v69, vcc
	global_load_dwordx4 v[196:199], v[180:181], off
	global_load_dwordx4 v[200:203], v[182:183], off
	global_load_dwordx4 v[204:207], v[184:185], off
	global_load_dwordx4 v[208:211], v[186:187], off
	global_load_dwordx4 v[212:215], v[188:189], off
	global_load_dwordx4 v[216:219], v[190:191], off
	global_load_dwordx4 v[220:223], v[192:193], off
	global_load_dwordx4 v[224:227], v[194:195], off
	v_mov_b32_e32 v78, v14
	v_mov_b32_e32 v79, v16
	v_mov_b32_e32 v70, v108
	v_mov_b32_e32 v71, v112
	v_pk_mul_f32 v[72:73], v[78:79], v[70:71]
	v_and_b32_e32 v110, 0xffff0000, v2
	v_and_b32_e32 v116, 0xffff0000, v3
	v_and_b32_sdwa v82, v73, v153 dst_sel:DWORD dst_unused:UNUSED_PAD src0_sel:WORD_1 src1_sel:DWORD
	v_and_b32_sdwa v83, v72, v153 dst_sel:DWORD dst_unused:UNUSED_PAD src0_sel:WORD_1 src1_sel:DWORD
	v_mov_b32_e32 v80, v15
	v_mov_b32_e32 v81, v17
	v_mov_b32_e32 v74, v110
	v_mov_b32_e32 v75, v116
	v_add3_u32 v86, v73, v82, s56
	v_add3_u32 v97, v72, v83, s56
	v_pk_mul_f32 v[76:77], v[80:81], v[74:75]
	v_and_b32_e32 v73, 0xffff0000, v86
	v_and_b32_e32 v72, 0xffff0000, v97
	v_pk_fma_f32 v[82:83], v[78:79], v[70:71], v[72:73] neg_lo:[0,0,1] neg_hi:[0,0,1]
	v_and_b32_sdwa v70, v77, v153 dst_sel:DWORD dst_unused:UNUSED_PAD src0_sel:WORD_1 src1_sel:DWORD
	v_and_b32_sdwa v71, v76, v153 dst_sel:DWORD dst_unused:UNUSED_PAD src0_sel:WORD_1 src1_sel:DWORD
	v_lshlrev_b32_e32 v114, 16, v4
	v_lshlrev_b32_e32 v118, 16, v5
	v_add3_u32 v70, v77, v70, s56
	v_add3_u32 v72, v76, v71, s56
	v_and_b32_e32 v71, 0xffff0000, v70
	v_and_b32_e32 v70, 0xffff0000, v72
	v_mov_b32_e32 v126, v10
	v_mov_b32_e32 v127, v12
	v_mov_b32_e32 v72, v114
	v_mov_b32_e32 v73, v118
	v_pk_mul_f32 v[76:77], v[126:127], v[72:73]
	v_and_b32_e32 v120, 0xffff0000, v4
	v_and_b32_e32 v122, 0xffff0000, v5
	v_pk_fma_f32 v[74:75], v[80:81], v[74:75], v[70:71] neg_lo:[0,0,1] neg_hi:[0,0,1]
	v_or_b32_sdwa v70, v70, v97 dst_sel:DWORD dst_unused:UNUSED_PAD src0_sel:DWORD src1_sel:WORD_1
	v_or_b32_sdwa v71, v71, v86 dst_sel:DWORD dst_unused:UNUSED_PAD src0_sel:DWORD src1_sel:WORD_1
	v_and_b32_sdwa v86, v77, v153 dst_sel:DWORD dst_unused:UNUSED_PAD src0_sel:WORD_1 src1_sel:DWORD
	v_and_b32_sdwa v97, v76, v153 dst_sel:DWORD dst_unused:UNUSED_PAD src0_sel:WORD_1 src1_sel:DWORD
	v_mov_b32_e32 v128, v11
	v_mov_b32_e32 v129, v13
	v_mov_b32_e32 v132, v120
	v_mov_b32_e32 v133, v122
	v_add3_u32 v86, v77, v86, s56
	v_add3_u32 v97, v76, v97, s56
	v_pk_mul_f32 v[134:135], v[128:129], v[132:133]
	v_and_b32_e32 v77, 0xffff0000, v86
	v_and_b32_e32 v76, 0xffff0000, v97
	v_pk_fma_f32 v[76:77], v[126:127], v[72:73], v[76:77] neg_lo:[0,0,1] neg_hi:[0,0,1]
	v_and_b32_sdwa v72, v135, v153 dst_sel:DWORD dst_unused:UNUSED_PAD src0_sel:WORD_1 src1_sel:DWORD
	v_and_b32_sdwa v73, v134, v153 dst_sel:DWORD dst_unused:UNUSED_PAD src0_sel:WORD_1 src1_sel:DWORD
	v_add3_u32 v72, v135, v72, s56
	v_add3_u32 v134, v134, v73, s56
	v_and_b32_e32 v73, 0xffff0000, v72
	v_and_b32_e32 v72, 0xffff0000, v134
	v_pk_fma_f32 v[132:133], v[128:129], v[132:133], v[72:73] neg_lo:[0,0,1] neg_hi:[0,0,1]
	v_or_b32_sdwa v72, v72, v97 dst_sel:DWORD dst_unused:UNUSED_PAD src0_sel:DWORD src1_sel:WORD_1
	v_or_b32_sdwa v73, v73, v86 dst_sel:DWORD dst_unused:UNUSED_PAD src0_sel:DWORD src1_sel:WORD_1
	v_bfe_u32 v86, v133, 16, 1
	v_bfe_u32 v97, v132, 16, 1
	v_add3_u32 v97, v132, v97, s56
	v_add3_u32 v86, v133, v86, s56
	v_bfe_u32 v132, v82, 16, 1
	v_bfe_u32 v133, v83, 16, 1
	v_bfe_u32 v134, v75, 16, 1
	v_bfe_u32 v135, v74, 16, 1
	v_add3_u32 v83, v83, v133, s56
	v_add3_u32 v82, v82, v132, s56
	v_lshlrev_b32_e32 v109, 16, v6
	v_lshlrev_b32_e32 v113, 16, v7
	v_add3_u32 v74, v74, v135, s56
	v_add3_u32 v75, v75, v134, s56
	v_bfe_u32 v134, v76, 16, 1
	v_bfe_u32 v135, v77, 16, 1
	v_lshrrev_b32_e32 v82, 16, v82
	v_lshrrev_b32_e32 v83, 16, v83
	v_add3_u32 v77, v77, v135, s56
	v_add3_u32 v76, v76, v134, s56
	v_and_or_b32 v75, v75, s55, v83
	v_and_or_b32 v74, v74, s55, v82
	v_mov_b32_e32 v82, v109
	v_mov_b32_e32 v83, v113
	v_lshrrev_b32_e32 v76, 16, v76
	v_lshrrev_b32_e32 v77, 16, v77
	v_pk_mul_f32 v[132:133], v[78:79], v[82:83]
	v_and_b32_e32 v111, 0xffff0000, v6
	v_and_b32_e32 v117, 0xffff0000, v7
	v_and_or_b32 v77, v86, s55, v77
	v_and_or_b32 v76, v97, s55, v76
	v_and_b32_sdwa v86, v133, v153 dst_sel:DWORD dst_unused:UNUSED_PAD src0_sel:WORD_1 src1_sel:DWORD
	v_and_b32_sdwa v97, v132, v153 dst_sel:DWORD dst_unused:UNUSED_PAD src0_sel:WORD_1 src1_sel:DWORD
	v_mov_b32_e32 v134, v111
	v_mov_b32_e32 v135, v117
	v_add3_u32 v86, v133, v86, s56
	v_add3_u32 v97, v132, v97, s56
; __device__ __forceinline__ unsigned f2bf(float f) { unsigned u = __builtin_bit_cast(unsigned, f); return (u + 0x7fffu + ((u >> 16) & 1u)) >> 16; }
; __device__ __forceinline__ void rt_step(const RtLoad& L, const bf16_t* bh, const bf16_t* bl, f32x4 (&acc)[2][5], float (&ss)[2], int ko) {
;     RtW W;
; #pragma unroll
;     for (int n = 0; n < 5; ++n) { W.wh[n] = *(const bf16x8*)(bh + (size_t)n * 16 * D + ko); W.wl[n] = *(const bf16x8*)(bl + (size_t)n * 16 * D + ko); }
;     bf16x8 ahi[2], alo[2];
; #pragma unroll
;     for (int mi = 0; mi < 2; ++mi) { const u32x4 xw = L.x[mi]; const f32x4 xa = (f32x4){bflo(xw.x), bfhi(xw.x), bflo(xw.y), bfhi(xw.y)}, xb = (f32x4){bflo(xw.z), bfhi(xw.z), bflo(xw.w), bfhi(xw.w)};
;         ss[mi] += (xa.x * xa.x + xa.y * xa.y) + (xa.z * xa.z + xa.w * xa.w) + (xb.x * xb.x + xb.y * xb.y) + (xb.z * xb.z + xb.w * xb.w);
;         const float u[8] = {xa.x * L.g[0].x, xa.y * L.g[0].y, xa.z * L.g[0].z, xa.w * L.g[0].w, xb.x * L.g[1].x, xb.y * L.g[1].y, xb.z * L.g[1].z, xb.w * L.g[1].w};
;         unsigned hb[8]; float lo[8];
; #pragma unroll
;         for (int j = 0; j < 8; ++j) { hb[j] = f2bf(u[j]); lo[j] = u[j] - __builtin_bit_cast(float, hb[j] << 16); }
;         const u32x4 hw = (u32x4){hb[0] | (hb[1] << 16), hb[2] | (hb[3] << 16), hb[4] | (hb[5] << 16), hb[6] | (hb[7] << 16)};
;         const u32x4 lw = (u32x4){pk2(lo[0], lo[1]), pk2(lo[2], lo[3]), pk2(lo[4], lo[5]), pk2(lo[6], lo[7])};
;         ahi[mi] = __builtin_bit_cast(bf16x8, hw); alo[mi] = __builtin_bit_cast(bf16x8, lw); }
; #pragma unroll
;     for (int n = 0; n < 5; ++n)
; #pragma unroll
;         for (int mi = 0; mi < 2; ++mi) { acc[mi][n] = __builtin_amdgcn_mfma_f32_16x16x32_bf16(ahi[mi], W.wh[n], acc[mi][n], 0, 0, 0);
;             acc[mi][n] = __builtin_amdgcn_mfma_f32_16x16x32_bf16(alo[mi], W.wh[n], acc[mi][n], 0, 0, 0);
;             acc[mi][n] = __builtin_amdgcn_mfma_f32_16x16x32_bf16(ahi[mi], W.wl[n], acc[mi][n], 0, 0, 0); }
; __device__ __forceinline__ void p5_router(Frame& F) {
;     ...
;           RtLoad La, Lb; rt_load(La, h0, h1, gp, 0);
; #pragma unroll 1
;           for (int ks = 0; ks < 32; ks += 2) {
;               rt_load(Lb, h0, h1, gp, (ks + 1) * 32); rt_step(La, bh, bl, acc, ss, ks * 32);
;               if (ks + 2 < 32) rt_load(La, h0, h1, gp, (ks + 2) * 32);
;               rt_step(Lb, bh, bl, acc, ss, (ks + 1) * 32); }
	v_pk_mul_f32 v[136:137], v[80:81], v[134:135]
	v_and_b32_e32 v133, 0xffff0000, v86
	v_and_b32_e32 v132, 0xffff0000, v97
	v_pk_fma_f32 v[78:79], v[78:79], v[82:83], v[132:133] neg_lo:[0,0,1] neg_hi:[0,0,1]
	v_and_b32_sdwa v82, v137, v153 dst_sel:DWORD dst_unused:UNUSED_PAD src0_sel:WORD_1 src1_sel:DWORD
	v_and_b32_sdwa v83, v136, v153 dst_sel:DWORD dst_unused:UNUSED_PAD src0_sel:WORD_1 src1_sel:DWORD
	v_add3_u32 v82, v137, v82, s56
	v_add3_u32 v132, v136, v83, s56
	v_lshlrev_b32_e32 v115, 16, v8
	v_lshlrev_b32_e32 v119, 16, v9
	v_and_b32_e32 v83, 0xffff0000, v82
	v_and_b32_e32 v82, 0xffff0000, v132
	v_pk_fma_f32 v[80:81], v[80:81], v[134:135], v[82:83] neg_lo:[0,0,1] neg_hi:[0,0,1]
	v_or_b32_sdwa v158, v82, v97 dst_sel:DWORD dst_unused:UNUSED_PAD src0_sel:DWORD src1_sel:WORD_1
	v_or_b32_sdwa v159, v83, v86 dst_sel:DWORD dst_unused:UNUSED_PAD src0_sel:DWORD src1_sel:WORD_1
	v_mov_b32_e32 v82, v115
	v_mov_b32_e32 v83, v119
	v_pk_mul_f32 v[132:133], v[126:127], v[82:83]
	v_and_b32_e32 v121, 0xffff0000, v8
	v_and_b32_e32 v123, 0xffff0000, v9
	v_and_b32_sdwa v86, v133, v153 dst_sel:DWORD dst_unused:UNUSED_PAD src0_sel:WORD_1 src1_sel:DWORD
	v_and_b32_sdwa v97, v132, v153 dst_sel:DWORD dst_unused:UNUSED_PAD src0_sel:WORD_1 src1_sel:DWORD
	v_mov_b32_e32 v134, v121
	v_mov_b32_e32 v135, v123
	v_add3_u32 v86, v133, v86, s56
	v_add3_u32 v97, v132, v97, s56
	v_pk_mul_f32 v[136:137], v[128:129], v[134:135]
	v_and_b32_e32 v133, 0xffff0000, v86
	v_and_b32_e32 v132, 0xffff0000, v97
	v_pk_fma_f32 v[82:83], v[126:127], v[82:83], v[132:133] neg_lo:[0,0,1] neg_hi:[0,0,1]
	v_and_b32_sdwa v126, v137, v153 dst_sel:DWORD dst_unused:UNUSED_PAD src0_sel:WORD_1 src1_sel:DWORD
	v_and_b32_sdwa v127, v136, v153 dst_sel:DWORD dst_unused:UNUSED_PAD src0_sel:WORD_1 src1_sel:DWORD
	v_add3_u32 v126, v137, v126, s56
	v_add3_u32 v132, v136, v127, s56
	v_and_b32_e32 v127, 0xffff0000, v126
	v_and_b32_e32 v126, 0xffff0000, v132
	v_pk_fma_f32 v[128:129], v[128:129], v[134:135], v[126:127] neg_lo:[0,0,1] neg_hi:[0,0,1]
	v_or_b32_sdwa v160, v126, v97 dst_sel:DWORD dst_unused:UNUSED_PAD src0_sel:DWORD src1_sel:WORD_1
	v_or_b32_sdwa v161, v127, v86 dst_sel:DWORD dst_unused:UNUSED_PAD src0_sel:DWORD src1_sel:WORD_1
	v_bfe_u32 v126, v81, 16, 1
	v_bfe_u32 v127, v80, 16, 1
	v_add3_u32 v80, v80, v127, s56
	v_add3_u32 v81, v81, v126, s56
	v_bfe_u32 v126, v78, 16, 1
	v_bfe_u32 v127, v79, 16, 1
	v_add3_u32 v79, v79, v127, s56
	v_add3_u32 v78, v78, v126, s56
	v_add_co_u32_e32 v126, vcc, s47, v68
	v_bfe_u32 v86, v129, 16, 1
	v_bfe_u32 v97, v128, 16, 1
	v_lshrrev_b32_e32 v78, 16, v78
	v_lshrrev_b32_e32 v79, 16, v79
	v_addc_co_u32_e32 v127, vcc, 0, v69, vcc
	v_add3_u32 v97, v128, v97, s56
	v_add3_u32 v86, v129, v86, s56
	v_bfe_u32 v128, v82, 16, 1
	v_bfe_u32 v129, v83, 16, 1
	v_and_or_b32 v163, v81, s55, v79
	v_and_or_b32 v162, v80, s55, v78
	v_add3_u32 v83, v83, v129, s56
	v_add3_u32 v82, v82, v128, s56
	v_lshrrev_b32_e32 v82, 16, v82
	v_lshrrev_b32_e32 v83, 16, v83
	v_and_or_b32 v165, v86, s55, v83
	v_and_or_b32 v164, v97, s55, v82
	s_waitcnt vmcnt(0)
	v_mfma_f32_16x16x32_bf16 v[30:33], v[70:73], v[58:61], v[30:33]
	v_add_co_u32_e32 v128, vcc, s48, v68
	s_cmp_gt_u32 s8, 29
	v_mfma_f32_16x16x32_bf16 v[18:21], v[158:161], v[58:61], v[18:21]
	v_addc_co_u32_e32 v129, vcc, 0, v69, vcc
	v_add_co_u32_e32 v132, vcc, s49, v68
	v_mfma_f32_16x16x32_bf16 v[30:33], v[74:77], v[58:61], v[30:33]
	s_nop 0
	v_addc_co_u32_e32 v133, vcc, 0, v69, vcc
	v_add_co_u32_e32 v134, vcc, s50, v68
	v_mfma_f32_16x16x32_bf16 v[18:21], v[162:165], v[58:61], v[18:21]
	v_addc_co_u32_e32 v135, vcc, 0, v69, vcc
	v_mfma_f32_16x16x32_bf16 v[30:33], v[70:73], v[62:65], v[30:33]
	v_add_co_u32_e32 v136, vcc, s51, v68
	s_cselect_b64 s[0:1], -1, 0
	v_mfma_f32_16x16x32_bf16 v[18:21], v[158:161], v[62:65], v[18:21]
	v_addc_co_u32_e32 v137, vcc, 0, v69, vcc
	v_mfma_f32_16x16x32_bf16 v[34:37], v[70:73], v[196:199], v[34:37]
	v_add_co_u32_e32 v138, vcc, s52, v68
	v_mfma_f32_16x16x32_bf16 v[22:25], v[158:161], v[196:199], v[22:25]
	s_nop 0
	v_addc_co_u32_e32 v139, vcc, 0, v69, vcc
	v_add_co_u32_e32 v140, vcc, s53, v68
	v_mfma_f32_16x16x32_bf16 v[34:37], v[74:77], v[196:199], v[34:37]
	s_nop 0
	v_addc_co_u32_e32 v141, vcc, 0, v69, vcc
	v_add_co_u32_e32 v142, vcc, s54, v68
	v_mfma_f32_16x16x32_bf16 v[22:25], v[162:165], v[196:199], v[22:25]
	v_addc_co_u32_e32 v143, vcc, 0, v69, vcc
	s_waitcnt vmcnt(0)
	v_mfma_f32_16x16x32_bf16 v[34:37], v[70:73], v[200:203], v[34:37]
	v_mfma_f32_16x16x32_bf16 v[22:25], v[158:161], v[200:203], v[22:25]
	v_mfma_f32_16x16x32_bf16 v[38:41], v[70:73], v[204:207], v[38:41]
	v_mfma_f32_16x16x32_bf16 v[26:29], v[158:161], v[204:207], v[26:29]
	v_mfma_f32_16x16x32_bf16 v[38:41], v[74:77], v[204:207], v[38:41]
	v_mfma_f32_16x16x32_bf16 v[26:29], v[162:165], v[204:207], v[26:29]
	s_waitcnt vmcnt(0)
	v_mfma_f32_16x16x32_bf16 v[38:41], v[70:73], v[208:211], v[38:41]
	v_mfma_f32_16x16x32_bf16 v[26:29], v[158:161], v[208:211], v[26:29]
	v_mfma_f32_16x16x32_bf16 v[46:49], v[70:73], v[212:215], v[46:49]
	v_mfma_f32_16x16x32_bf16 v[42:45], v[158:161], v[212:215], v[42:45]
	v_mfma_f32_16x16x32_bf16 v[46:49], v[74:77], v[212:215], v[46:49]
	v_mfma_f32_16x16x32_bf16 v[42:45], v[162:165], v[212:215], v[42:45]
	v_mfma_f32_16x16x32_bf16 v[54:57], v[70:73], v[220:223], v[54:57]
	s_waitcnt vmcnt(0)
	v_mfma_f32_16x16x32_bf16 v[46:49], v[70:73], v[216:219], v[46:49]
	v_mfma_f32_16x16x32_bf16 v[42:45], v[158:161], v[216:219], v[42:45]
	v_lshl_add_u64 v[58:59], v[100:101], 0, s[24:25]
	v_add_co_u32_e32 v60, vcc, s33, v58
	v_mfma_f32_16x16x32_bf16 v[54:57], v[74:77], v[220:223], v[54:57]
	s_nop 0
	v_addc_co_u32_e32 v61, vcc, 0, v59, vcc
	v_add_co_u32_e32 v68, vcc, s44, v58
	v_mfma_f32_16x16x32_bf16 v[54:57], v[70:73], v[224:227], v[54:57]
	s_nop 0
	v_addc_co_u32_e32 v69, vcc, 0, v59, vcc
	global_load_dwordx4 v[80:83], v[60:61], off offset:64
	global_load_dwordx4 v[72:75], v[68:69], off offset:64
	s_nop 0
	global_load_dwordx4 v[68:71], v[104:105], off offset:-128
	global_load_dwordx4 v[76:79], v[104:105], off offset:-144
	v_mfma_f32_16x16x32_bf16 v[50:53], v[158:161], v[220:223], v[50:53]
	s_and_b64 vcc, exec, s[0:1]
	v_mfma_f32_16x16x32_bf16 v[50:53], v[162:165], v[220:223], v[50:53]
	v_mfma_f32_16x16x32_bf16 v[50:53], v[158:161], v[224:227], v[50:53]
	s_cbranch_vccnz .LBB0_607
	v_add_co_u32_e32 v2, vcc, 0x29e00000, v58
	s_nop 1
	v_addc_co_u32_e32 v3, vcc, 0, v59, vcc
	v_add_co_u32_e32 v6, vcc, 0x29e20000, v58
	s_nop 1
	v_addc_co_u32_e32 v7, vcc, 0, v59, vcc
	global_load_dwordx4 v[2:5], v[2:3], off offset:128
	s_nop 0
	global_load_dwordx4 v[6:9], v[6:7], off offset:128
	s_nop 0
	global_load_dwordx4 v[10:13], v[104:105], off
	global_load_dwordx4 v[14:17], v[104:105], off offset:-16
	s_branch .LBB0_607

; #define PG8_LAS __attribute__((address_space(3)))
;     __device__ __forceinline__ unsigned row(const Unit& u, int r) const { return (unsigned)slot_tok[u.pm * 256 + r]; }
; #define MU_GLDS_A(buf, kt) do { _Pragma("unroll") for (int i = 0; i < NMU; ++i) \
;         __builtin_amdgcn_global_load_lds((const unsigned*)((const char*)A + aoff[i] + (size_t)(kt) * 128), (PG8_LAS unsigned*)(MU_SA(buf) + wid * 1024 + i * 8192), 16, 0, 0); } while (0)
; template <int MODE>
; __device__ __forceinline__ void moe_unit(PG8_LAS unsigned char* lds, int e, int cb, int slot0  , int nv  , const bf16_t* A, const int* slot_tok,
;                                          const float* W0, const float* W1, bf16_t* OUT, const float* slot_rs  , const int* slot_dst) {
;     constexpr int K = MODE == 0 ? 4096 : 512, nt = K / 64, LDB = MODE == 0 ? 512 : 4096, RB = LDB * 4  ;
;     const int tid = threadIdx.x, wid = __builtin_amdgcn_readfirstlane(tid >> 6), lane = tid & 63, wr = wid >> 1, wc = wid & 1, fr = lane & 15, fq = lane >> 4;
;     unsigned aoff[NMU];
; #pragma unroll
;     for (int i = 0; i < NMU; ++i) { const int R = 8 * (wid + 8 * i) + (lane >> 3), C = 8 * ((lane & 7) ^ ((R >> 1) & 7)); const int w4 = R / RWU, r = 4 * (R - RWU * w4) + w4;
;         const unsigned row = r < nv ? (MODE == 0 ? (unsigned)slot_tok[slot0 + r] : (unsigned)(slot0 + r)) : (MODE == 0 ? 0u : (unsigned)slot0); aoff[i] = (row * (unsigned)K + (unsigned)C) * 2u; }
;     const int jj0 = 2 * (lane & 31), typ = lane >> 5;
;     const int R0 = MODE == 0 ? 64 * (jj0 >> 5) + 32 * typ + 16 * ((jj0 >> 2) & 1) + 4 * ((jj0 >> 3) & 3) + (jj0 & 3) : 2 * lane;
;     const char* Bb = MODE == 0 ? (const char*)((typ ? W1 : W0) + (size_t)e * K * LDB + 64 * cb + jj0) + (size_t)(8 * wid) * RB
;                                : (const char*)(W0 + (size_t)e * K * LDB + 128 * cb + 2 * lane) + (size_t)(8 * wid) * RB;
;     const unsigned bw0 = (unsigned)(R0 * 128 + ((wid ^ ((R0 >> 1) & 7)) * 16)), bw1 = bw0 + 128u;
;     const int nvw = (nv - wr + 3) >> 2, mcnt = nvw <= 0 ? 0 : (((nvw + 15) >> 4) > NMU ? NMU : ((nvw + 15) >> 4));
;     ...
;     f32x4 acc[NMU][4];
; #pragma unroll
;     for (int m = 0; m < NMU; ++m)
; #pragma unroll
;         for (int n = 0; n < 4; ++n) acc[m][n] = (f32x4){0.f, 0.f, 0.f, 0.f};
;     f32x2 s0[8], s1[8];
;     float g0[8];
;     MU_GLDS_A(0, 0); MU_B_ISSUE(s0, 0); MU_G_LOAD(g0, 0); MU_B_ISSUE(s1, 1);
.LBB0_699:
	s_or_b64 exec, exec, s[56:57]
	s_waitcnt vmcnt(0)
	v_lshlrev_b32_e32 v5, 13, v5
	v_lshlrev_b32_e32 v6, 13, v6
	v_lshlrev_b32_e32 v4, 13, v4
	v_lshlrev_b32_e32 v8, 13, v8
	v_lshlrev_b32_e32 v7, 13, v7
	s_lshr_b32 s33, s58, 7
	s_bfe_u32 s70, s58, 0x10006
	v_add_u32_e32 v166, s33, v176
	v_add_u32_e32 v166, v166, v94
	v_ashrrev_i32_e32 v167, 31, v166
	v_lshl_add_u64 v[166:167], v[166:167], 2, v[96:97]
	v_lshl_add_u64 v[166:167], v[166:167], 0, s[10:11]
	global_load_dword v178, v[166:167], off
	global_load_dword v179, v[166:167], off offset:256
	global_load_dword v180, v[166:167], off offset:512
	global_load_dword v181, v[166:167], off offset:768
	global_load_dword v182, v[166:167], off offset:1024
	v_bfe_u32 v166, v131, 1, 3
	v_xor_b32_e32 v166, v171, v166
	v_lshlrev_b32_e32 v166, 4, v166
	v_lshl_add_u32 v166, v170, 7, v166
	s_mul_i32 s56, s33, 0x2800
	v_add_u32_e32 v135, s56, v166
	v_xor_b32_e32 v137, 64, v135
	s_lshl_b32 s56, s70, 13
	s_add_i32 s56, s56, 0x1e000
	v_add_u32_e32 v139, s56, v166
	v_xor_b32_e32 v141, 64, v139
	v_xor_b32_e32 v1, s62, v177
	v_lshl_add_u32 v1, v1, 4, v172
	v_add_u32_e32 v1, 0x1e000, v1
	s_lshl_b32 s56, s62, 2
	v_add_u32_e32 v166, s56, v171
	v_xor_b32_e32 v166, v166, v131
	v_and_b32_e32 v166, 7, v166
	v_lshlrev_b32_e32 v166, 4, v166
	v_or_b32_e32 v86, v5, v166
	v_or_b32_e32 v134, v6, v166
	v_or_b32_e32 v136, v4, v166
	v_or_b32_e32 v138, v8, v166
	v_or_b32_e32 v140, v7, v166
	s_lshl_b64 s[56:57], s[54:55], 23
	s_lshl_b32 s59, s60, 8
	s_add_u32 s56, s56, s59
	s_addc_u32 s57, s57, 0
	s_lshl_b32 s59, s62, 14
	s_add_u32 s56, s56, s59
	s_addc_u32 s57, s57, 0
	v_mov_b32_e32 v91, 0
	v_lshl_add_u64 v[132:133], v[82:83], 0, s[56:57]
	v_lshl_add_u64 v[132:133], v[132:133], 0, v[90:91]
	s_lshl_b32 s54, s60, 6
	s_ashr_i32 s55, s54, 31
	v_readlane_b32 s28, v254, 9
	v_readlane_b32 s29, v254, 10
	s_lshl_b32 s56, s62, 5
	s_mov_b64 s[30:31], s[4:5]
	s_mov_b64 s[34:35], 0x1000
	s_mov_b64 s[36:37], 0x2000
	s_mov_b64 s[38:39], 0x3000
	s_mov_b64 s[40:41], 0x20000
	s_add_u32 s28, s28, s56
	s_addc_u32 s29, s29, 0
	s_mov_b32 s42, 0
	s_mov_b32 s43, 0xa000
	s_mov_b32 s44, 0x14000
	s_lshl_b32 s6, s62, 10
	s_load_dwordx8 s[12:19], s[28:29], 0x0
	s_load_dwordx8 s[20:27], s[28:29], 0x100
	s_add_u32 s28, s28, 0x200
	s_addc_u32 s29, s29, 0
	s_add_i32 m0, s6, 0x0
	s_nop 0
	global_load_lds_dwordx4 v86, s[30:31]
	s_add_i32 m0, s6, 0x2000
	s_nop 0
	global_load_lds_dwordx4 v134, s[30:31]
	s_add_i32 m0, s6, 0x4000
	s_nop 0
	global_load_lds_dwordx4 v136, s[30:31]
	s_add_i32 m0, s6, 0x6000
	s_nop 0
	global_load_lds_dwordx4 v138, s[30:31]
	s_add_i32 m0, s6, 0x8000
	s_nop 0
	global_load_lds_dwordx4 v140, s[30:31]
	s_add_u32 s30, s30, 0x80
	s_addc_u32 s31, s31, 0
	s_add_i32 m0, s6, 0xa000
	s_nop 0
	global_load_lds_dwordx4 v86, s[30:31]
	s_add_i32 m0, s6, 0xc000
	s_nop 0
	global_load_lds_dwordx4 v134, s[30:31]
	s_add_i32 m0, s6, 0xe000
	s_nop 0
	global_load_lds_dwordx4 v136, s[30:31]
	s_add_i32 m0, s6, 0x10000
	s_nop 0
	global_load_lds_dwordx4 v138, s[30:31]
	s_add_i32 m0, s6, 0x12000
	s_nop 0
	global_load_lds_dwordx4 v140, s[30:31]
	global_load_dwordx2 v[98:99], v[132:133], off
	global_load_dwordx2 v[100:101], v[132:133], off offset:2048
	v_lshl_add_u64 v[166:167], v[132:133], 0, s[34:35]
	global_load_dwordx2 v[102:103], v[166:167], off
	global_load_dwordx2 v[104:105], v[166:167], off offset:2048
	v_lshl_add_u64 v[166:167], v[132:133], 0, s[36:37]
	global_load_dwordx2 v[106:107], v[166:167], off
	global_load_dwordx2 v[108:109], v[166:167], off offset:2048
	v_lshl_add_u64 v[166:167], v[132:133], 0, s[38:39]
	global_load_dwordx2 v[110:111], v[166:167], off
	global_load_dwordx2 v[112:113], v[166:167], off offset:2048
	v_lshl_add_u64 v[132:133], v[132:133], 0, s[40:41]
	global_load_dwordx2 v[114:115], v[132:133], off
	global_load_dwordx2 v[116:117], v[132:133], off offset:2048
	v_lshl_add_u64 v[166:167], v[132:133], 0, s[34:35]
	global_load_dwordx2 v[118:119], v[166:167], off
	global_load_dwordx2 v[120:121], v[166:167], off offset:2048
	v_lshl_add_u64 v[166:167], v[132:133], 0, s[36:37]
	global_load_dwordx2 v[122:123], v[166:167], off
	global_load_dwordx2 v[124:125], v[166:167], off offset:2048
	v_lshl_add_u64 v[166:167], v[132:133], 0, s[38:39]
	global_load_dwordx2 v[126:127], v[166:167], off
	global_load_dwordx2 v[128:129], v[166:167], off offset:2048
	v_lshl_add_u64 v[132:133], v[132:133], 0, s[40:41]
	global_load_dwordx2 v[186:187], v[132:133], off
	global_load_dwordx2 v[188:189], v[132:133], off offset:2048
	v_lshl_add_u64 v[166:167], v[132:133], 0, s[34:35]
	global_load_dwordx2 v[190:191], v[166:167], off
	global_load_dwordx2 v[192:193], v[166:167], off offset:2048
	v_lshl_add_u64 v[166:167], v[132:133], 0, s[36:37]
	global_load_dwordx2 v[194:195], v[166:167], off
	global_load_dwordx2 v[196:197], v[166:167], off offset:2048
	v_lshl_add_u64 v[166:167], v[132:133], 0, s[38:39]
	global_load_dwordx2 v[198:199], v[166:167], off
	global_load_dwordx2 v[200:201], v[166:167], off offset:2048
	v_lshl_add_u64 v[132:133], v[132:133], 0, s[40:41]
	global_load_dwordx2 v[202:203], v[132:133], off
	global_load_dwordx2 v[204:205], v[132:133], off offset:2048
	v_lshl_add_u64 v[166:167], v[132:133], 0, s[34:35]
	global_load_dwordx2 v[206:207], v[166:167], off
	global_load_dwordx2 v[208:209], v[166:167], off offset:2048
	v_lshl_add_u64 v[166:167], v[132:133], 0, s[36:37]
	global_load_dwordx2 v[210:211], v[166:167], off
	global_load_dwordx2 v[212:213], v[166:167], off offset:2048
	v_lshl_add_u64 v[166:167], v[132:133], 0, s[38:39]
	global_load_dwordx2 v[214:215], v[166:167], off
	global_load_dwordx2 v[216:217], v[166:167], off offset:2048
	v_mov_b32_e32 v78, 0
; #define MU_GLDS_A(buf, kt) do { _Pragma("unroll") for (int i = 0; i < NMU; ++i) \
;         __builtin_amdgcn_global_load_lds((const unsigned*)((const char*)A + aoff[i] + (size_t)(kt) * 128), (PG8_LAS unsigned*)(MU_SA(buf) + wid * 1024 + i * 8192), 16, 0, 0); } while (0)
; #define MU_B_ISSUE(sb, kt) do { const char* kb_ = Bb + (size_t)(kt) * (64 * (size_t)RB); _Pragma("unroll") for (int j = 0; j < 8; ++j) { const char* p_ = kb_ + (size_t)j * RB; \
;         asm volatile("global_load_dwordx2 %0, %1, off" : "=&v"(sb[j]) : "v"(p_) : "memory"); } } while (0)
; #define MU_B_WAIT(sb, N) asm volatile("s_waitcnt vmcnt(%8)" : "+v"(sb[0]), "+v"(sb[1]), "+v"(sb[2]), "+v"(sb[3]), "+v"(sb[4]), "+v"(sb[5]), "+v"(sb[6]), "+v"(sb[7]) : "n"(N) : "memory")
; #define MU_COMPUTE(buf) MU_COMPUTE_N(buf, NMU)
; template <int MODE>
; __device__ __forceinline__ void moe_unit(PG8_LAS unsigned char* lds, int e, int cb, int slot0  , int nv  , const bf16_t* A, const int* slot_tok,
;                                          const float* W0, const float* W1, bf16_t* OUT, const float* slot_rs  , const int* slot_dst) {
;     ...
;     const int nvw = (nv - wr + 3) >> 2, mcnt = nvw <= 0 ? 0 : (((nvw + 15) >> 4) > NMU ? NMU : ((nvw + 15) >> 4));
;     ...
;     f32x4 acc[NMU][4];
; #pragma unroll
;     for (int m = 0; m < NMU; ++m)
; #pragma unroll
;         for (int n = 0; n < 4; ++n) acc[m][n] = (f32x4){0.f, 0.f, 0.f, 0.f};
;     f32x2 s0[8], s1[8];
;     float g0[8];
;     MU_GLDS_A(0, 0); MU_B_ISSUE(s0, 0); MU_G_LOAD(g0, 0); MU_B_ISSUE(s1, 1);
;     MU_B_WAIT(s0, 8); MU_B_WRITE(s0, 0, g0); __builtin_amdgcn_sched_barrier(0); MU_B_ISSUE(s0, 2);
;     asm volatile("s_waitcnt vmcnt(16)" ::: "memory");
;     asm volatile("s_waitcnt lgkmcnt(0)" ::: "memory"); __builtin_amdgcn_s_barrier(); asm volatile("" ::: "memory");
; #pragma unroll 1
;     for (int t = 0; t < nt; t += 2) {
;         if (t + 2 < nt) MU_B_WAIT(s1, 8); else MU_B_WAIT(s1, 0);
;         MU_G_LOAD(g0, t + 1); MU_B_WRITE(s1, 1, g0); __builtin_amdgcn_sched_barrier(0); MU_GLDS_A(1, t + 1); __builtin_amdgcn_sched_barrier(0);
;         if (t + 3 < nt) { MU_B_ISSUE(s1, t + 3); }
;         MU_COMPUTE(0);
;         MU_END(t + 3 >= nt);
	v_mov_b32_e32 v79, 0
	v_mov_b32_e32 v80, 0
	v_mov_b32_e32 v81, 0
	v_mov_b32_e32 v74, 0
	v_mov_b32_e32 v75, 0
	v_mov_b32_e32 v76, 0
	v_mov_b32_e32 v77, 0
	v_mov_b32_e32 v70, 0
	v_mov_b32_e32 v71, 0
	v_mov_b32_e32 v72, 0
	v_mov_b32_e32 v73, 0
	v_mov_b32_e32 v66, 0
	v_mov_b32_e32 v67, 0
	v_mov_b32_e32 v68, 0
	v_mov_b32_e32 v69, 0
	v_mov_b32_e32 v62, 0
	v_mov_b32_e32 v63, 0
	v_mov_b32_e32 v64, 0
	v_mov_b32_e32 v65, 0
	v_mov_b32_e32 v58, 0
	v_mov_b32_e32 v59, 0
	v_mov_b32_e32 v60, 0
	v_mov_b32_e32 v61, 0
	v_mov_b32_e32 v54, 0
	v_mov_b32_e32 v55, 0
	v_mov_b32_e32 v56, 0
	v_mov_b32_e32 v57, 0
	v_mov_b32_e32 v50, 0
	v_mov_b32_e32 v51, 0
	v_mov_b32_e32 v52, 0
	v_mov_b32_e32 v53, 0
	v_mov_b32_e32 v46, 0
	v_mov_b32_e32 v47, 0
	v_mov_b32_e32 v48, 0
	v_mov_b32_e32 v49, 0
	v_mov_b32_e32 v42, 0
	v_mov_b32_e32 v43, 0
	v_mov_b32_e32 v44, 0
	v_mov_b32_e32 v45, 0
	v_mov_b32_e32 v38, 0
	v_mov_b32_e32 v39, 0
	v_mov_b32_e32 v40, 0
	v_mov_b32_e32 v41, 0
	v_mov_b32_e32 v34, 0
	v_mov_b32_e32 v35, 0
	v_mov_b32_e32 v36, 0
	v_mov_b32_e32 v37, 0
	v_mov_b32_e32 v18, 0
	v_mov_b32_e32 v19, 0
	v_mov_b32_e32 v20, 0
	v_mov_b32_e32 v21, 0
	v_mov_b32_e32 v22, 0
	v_mov_b32_e32 v23, 0
	v_mov_b32_e32 v24, 0
	v_mov_b32_e32 v25, 0
	v_mov_b32_e32 v26, 0
	v_mov_b32_e32 v27, 0
	v_mov_b32_e32 v28, 0
	v_mov_b32_e32 v29, 0
	v_mov_b32_e32 v30, 0
	v_mov_b32_e32 v31, 0
	v_mov_b32_e32 v32, 0
	v_mov_b32_e32 v33, 0
	v_mov_b32_e32 v2, 0
	v_mov_b32_e32 v3, 0
	v_mov_b32_e32 v4, 0
	v_mov_b32_e32 v5, 0
	v_mov_b32_e32 v6, 0
	v_mov_b32_e32 v7, 0
	v_mov_b32_e32 v8, 0
	v_mov_b32_e32 v9, 0
	v_mov_b32_e32 v10, 0
	v_mov_b32_e32 v11, 0
	v_mov_b32_e32 v12, 0
	v_mov_b32_e32 v13, 0
	v_mov_b32_e32 v14, 0
	v_mov_b32_e32 v15, 0
	v_mov_b32_e32 v16, 0
	v_mov_b32_e32 v17, 0
	s_waitcnt vmcnt(24)
	s_waitcnt lgkmcnt(0)
	v_mul_f32_e32 v98, s12, v98
	v_mul_f32_e32 v99, s12, v99
	v_mul_f32_e32 v100, s13, v100
	v_mul_f32_e32 v101, s13, v101
	v_mul_f32_e32 v102, s14, v102
	v_mul_f32_e32 v103, s14, v103
	v_mul_f32_e32 v104, s15, v104
	v_mul_f32_e32 v105, s15, v105
	v_mul_f32_e32 v106, s16, v106
	v_mul_f32_e32 v107, s16, v107
	v_mul_f32_e32 v108, s17, v108
	v_mul_f32_e32 v109, s17, v109
	v_mul_f32_e32 v110, s18, v110
	v_mul_f32_e32 v111, s18, v111
	v_mul_f32_e32 v112, s19, v112
	v_mul_f32_e32 v113, s19, v113
	v_cvt_pk_bf16_f32 v158, v98, v100
	v_cvt_pk_bf16_f32 v159, v102, v104
	v_cvt_pk_bf16_f32 v160, v106, v108
	v_cvt_pk_bf16_f32 v161, v110, v112
	v_cvt_pk_bf16_f32 v162, v99, v101
	v_cvt_pk_bf16_f32 v163, v103, v105
	v_cvt_pk_bf16_f32 v164, v107, v109
	v_cvt_pk_bf16_f32 v165, v111, v113
	ds_write_b128 v1, v[158:161] offset:0
	ds_write_b128 v1, v[162:165] offset:128
	v_lshl_add_u64 v[132:133], v[132:133], 0, s[40:41]
	global_load_dwordx2 v[98:99], v[132:133], off
	global_load_dwordx2 v[100:101], v[132:133], off offset:2048
	v_lshl_add_u64 v[166:167], v[132:133], 0, s[34:35]
	global_load_dwordx2 v[102:103], v[166:167], off
	global_load_dwordx2 v[104:105], v[166:167], off offset:2048
	v_lshl_add_u64 v[166:167], v[132:133], 0, s[36:37]
	global_load_dwordx2 v[106:107], v[166:167], off
	global_load_dwordx2 v[108:109], v[166:167], off offset:2048
	v_lshl_add_u64 v[166:167], v[132:133], 0, s[38:39]
	global_load_dwordx2 v[110:111], v[166:167], off
	global_load_dwordx2 v[112:113], v[166:167], off offset:2048
	s_waitcnt lgkmcnt(0)
	s_barrier
	s_sub_i32 s56, s69, s33
	s_add_i32 s56, s56, 3
	s_ashr_i32 s56, s56, 2
	s_cmp_gt_i32 s56, 64
	s_cbranch_scc1 .Lmu_frag5
	s_cmp_gt_u32 s62, 3
	s_cbranch_scc1 .Lmu_grpY4
	s_waitcnt vmcnt(24)
	v_mul_f32_e32 v114, s20, v114
	v_mul_f32_e32 v115, s20, v115
	v_mul_f32_e32 v116, s21, v116
	v_mul_f32_e32 v117, s21, v117
	v_mul_f32_e32 v118, s22, v118
	v_mul_f32_e32 v119, s22, v119
	v_mul_f32_e32 v120, s23, v120
	v_mul_f32_e32 v121, s23, v121
	v_mul_f32_e32 v122, s24, v122
	v_mul_f32_e32 v123, s24, v123
	v_mul_f32_e32 v124, s25, v124
	v_mul_f32_e32 v125, s25, v125
	v_mul_f32_e32 v126, s26, v126
	v_mul_f32_e32 v127, s26, v127
	v_mul_f32_e32 v128, s27, v128
	v_mul_f32_e32 v129, s27, v129
	v_cvt_pk_bf16_f32 v158, v114, v116
	v_cvt_pk_bf16_f32 v159, v118, v120
	v_cvt_pk_bf16_f32 v160, v122, v124
	v_cvt_pk_bf16_f32 v161, v126, v128
	v_cvt_pk_bf16_f32 v162, v115, v117
	v_cvt_pk_bf16_f32 v163, v119, v121
	v_cvt_pk_bf16_f32 v164, v123, v125
	v_cvt_pk_bf16_f32 v165, v127, v129
	ds_write_b128 v1, v[158:161] offset:19456
	ds_write_b128 v1, v[162:165] offset:19584
	v_add_u32_e32 v91, s42, v135
	v_add_u32_e32 v93, s42, v137
	ds_read_b128 v[238:241], v139 offset:0
	ds_read_b128 v[242:245], v139 offset:2048
	ds_read_b128 v[246:249], v139 offset:4096
	ds_read_b128 v[250:253], v139 offset:6144
	ds_read_b128 v[218:221], v91 offset:0
	ds_read_b128 v[222:225], v91 offset:2048
	ds_read_b128 v[226:229], v91 offset:4096
	ds_read_b128 v[230:233], v91 offset:6144
	s_add_i32 s47, s44, s6
	s_add_u32 s30, s30, 0x80
	s_addc_u32 s31, s31, 0
	s_waitcnt lgkmcnt(0)
; #define MU_GLDS_A(buf, kt) do { _Pragma("unroll") for (int i = 0; i < NMU; ++i) \
;         __builtin_amdgcn_global_load_lds((const unsigned*)((const char*)A + aoff[i] + (size_t)(kt) * 128), (PG8_LAS unsigned*)(MU_SA(buf) + wid * 1024 + i * 8192), 16, 0, 0); } while (0)
; #define MU_B_ISSUE(sb, kt) do { const char* kb_ = Bb + (size_t)(kt) * (64 * (size_t)RB); _Pragma("unroll") for (int j = 0; j < 8; ++j) { const char* p_ = kb_ + (size_t)j * RB; \
;         asm volatile("global_load_dwordx2 %0, %1, off" : "=&v"(sb[j]) : "v"(p_) : "memory"); } } while (0)
; #define MU_B_WAIT(sb, N) asm volatile("s_waitcnt vmcnt(%8)" : "+v"(sb[0]), "+v"(sb[1]), "+v"(sb[2]), "+v"(sb[3]), "+v"(sb[4]), "+v"(sb[5]), "+v"(sb[6]), "+v"(sb[7]) : "n"(N) : "memory")
; #define MU_G_LOAD(ga, kt) do { const PG8_LAS f32x4* gk_ = (const PG8_LAS f32x4*)(lds + GAIN_OFF) + 16 * (kt) + 2 * wid; const f32x4 ga_ = gk_[0], gb_ = gk_[1]; \
;         ga[0] = ga_[0]; ga[1] = ga_[1]; ga[2] = ga_[2]; ga[3] = ga_[3]; ga[4] = gb_[0]; ga[5] = gb_[1]; ga[6] = gb_[2]; ga[7] = gb_[3]; } while (0)
; #define MU_COMPUTE(buf) MU_COMPUTE_N(buf, NMU)
; #define MU_END(last) do { if (last) asm volatile("s_waitcnt vmcnt(0)" ::: "memory"); else asm volatile("s_waitcnt vmcnt(8)" ::: "memory"); \
;         asm volatile("s_waitcnt lgkmcnt(0)" ::: "memory"); __builtin_amdgcn_s_barrier(); asm volatile("" ::: "memory"); } while (0)
; template <int MODE>
; __device__ __forceinline__ void moe_unit(PG8_LAS unsigned char* lds, int e, int cb, int slot0  , int nv  , const bf16_t* A, const int* slot_tok,
;                                          const float* W0, const float* W1, bf16_t* OUT, const float* slot_rs  , const int* slot_dst) {
;     ...
;     for (int t = 0; t < nt; t += 2) {
;         if (t + 2 < nt) MU_B_WAIT(s1, 8); else MU_B_WAIT(s1, 0);
;         MU_G_LOAD(g0, t + 1); MU_B_WRITE(s1, 1, g0); __builtin_amdgcn_sched_barrier(0); MU_GLDS_A(1, t + 1); __builtin_amdgcn_sched_barrier(0);
;         if (t + 3 < nt) { MU_B_ISSUE(s1, t + 3); }
;         MU_COMPUTE(0);
;         MU_END(t + 3 >= nt);
;         if (t + 2 < nt) { MU_B_WAIT(s0, 8); MU_G_LOAD(g0, t + 2); MU_B_WRITE(s0, 0, g0); __builtin_amdgcn_sched_barrier(0); MU_GLDS_A(0, t + 2); __builtin_amdgcn_sched_barrier(0); }
;         if (t + 4 < nt) { MU_B_ISSUE(s0, t + 4); }
;         MU_COMPUTE(1);
;         MU_END(t + 4 >= nt);
	v_mfma_f32_16x16x32_bf16 v[78:81], v[238:241], v[218:221], v[78:81]
	v_mfma_f32_16x16x32_bf16 v[74:77], v[242:245], v[218:221], v[74:77]
	v_mfma_f32_16x16x32_bf16 v[70:73], v[246:249], v[218:221], v[70:73]
	v_mfma_f32_16x16x32_bf16 v[66:69], v[250:253], v[218:221], v[66:69]
	ds_read_b128 v[218:221], v93 offset:0
	ds_read_b128 v[142:145], v141 offset:0
	s_mov_b32 m0, s47
	s_nop 0
	global_load_lds_dwordx4 v86, s[30:31]
	v_mfma_f32_16x16x32_bf16 v[62:65], v[238:241], v[222:225], v[62:65]
	v_mfma_f32_16x16x32_bf16 v[58:61], v[242:245], v[222:225], v[58:61]
	v_mfma_f32_16x16x32_bf16 v[54:57], v[246:249], v[222:225], v[54:57]
	v_mfma_f32_16x16x32_bf16 v[50:53], v[250:253], v[222:225], v[50:53]
	ds_read_b128 v[222:225], v93 offset:2048
	ds_read_b128 v[146:149], v141 offset:2048
	s_add_i32 m0, s47, 0x2000
	s_nop 0
	global_load_lds_dwordx4 v134, s[30:31]
	v_mfma_f32_16x16x32_bf16 v[46:49], v[238:241], v[226:229], v[46:49]
	v_mfma_f32_16x16x32_bf16 v[42:45], v[242:245], v[226:229], v[42:45]
	v_mfma_f32_16x16x32_bf16 v[38:41], v[246:249], v[226:229], v[38:41]
	v_mfma_f32_16x16x32_bf16 v[34:37], v[250:253], v[226:229], v[34:37]
	ds_read_b128 v[226:229], v93 offset:4096
	ds_read_b128 v[150:153], v141 offset:4096
	s_add_i32 m0, s47, 0x4000
	s_nop 0
	global_load_lds_dwordx4 v136, s[30:31]
	v_mfma_f32_16x16x32_bf16 v[18:21], v[238:241], v[230:233], v[18:21]
	v_mfma_f32_16x16x32_bf16 v[22:25], v[242:245], v[230:233], v[22:25]
	v_mfma_f32_16x16x32_bf16 v[26:29], v[246:249], v[230:233], v[26:29]
	v_mfma_f32_16x16x32_bf16 v[30:33], v[250:253], v[230:233], v[30:33]
	ds_read_b128 v[230:233], v93 offset:6144
	ds_read_b128 v[154:157], v141 offset:6144
	s_add_i32 m0, s47, 0x6000
	s_nop 0
	global_load_lds_dwordx4 v138, s[30:31]
	s_add_i32 m0, s47, 0x8000
	s_nop 0
	global_load_lds_dwordx4 v140, s[30:31]
	s_waitcnt lgkmcnt(0)
	s_load_dwordx8 s[12:19], s[28:29], 0x0
	s_add_u32 s28, s28, 0x100
	s_addc_u32 s29, s29, 0
	v_mfma_f32_16x16x32_bf16 v[78:81], v[142:145], v[218:221], v[78:81]
	v_mfma_f32_16x16x32_bf16 v[74:77], v[146:149], v[218:221], v[74:77]
	v_mfma_f32_16x16x32_bf16 v[70:73], v[150:153], v[218:221], v[70:73]
	v_mfma_f32_16x16x32_bf16 v[66:69], v[154:157], v[218:221], v[66:69]
	v_lshl_add_u64 v[132:133], v[132:133], 0, s[40:41]
	global_load_dwordx2 v[114:115], v[132:133], off
	global_load_dwordx2 v[116:117], v[132:133], off offset:2048
	v_mfma_f32_16x16x32_bf16 v[62:65], v[142:145], v[222:225], v[62:65]
	v_mfma_f32_16x16x32_bf16 v[58:61], v[146:149], v[222:225], v[58:61]
	v_mfma_f32_16x16x32_bf16 v[54:57], v[150:153], v[222:225], v[54:57]
	v_mfma_f32_16x16x32_bf16 v[50:53], v[154:157], v[222:225], v[50:53]
	v_lshl_add_u64 v[166:167], v[132:133], 0, s[34:35]
	global_load_dwordx2 v[118:119], v[166:167], off
	global_load_dwordx2 v[120:121], v[166:167], off offset:2048
	v_mfma_f32_16x16x32_bf16 v[46:49], v[142:145], v[226:229], v[46:49]
	v_mfma_f32_16x16x32_bf16 v[42:45], v[146:149], v[226:229], v[42:45]
	v_mfma_f32_16x16x32_bf16 v[38:41], v[150:153], v[226:229], v[38:41]
	v_mfma_f32_16x16x32_bf16 v[34:37], v[154:157], v[226:229], v[34:37]
	v_lshl_add_u64 v[166:167], v[132:133], 0, s[36:37]
	global_load_dwordx2 v[122:123], v[166:167], off
	global_load_dwordx2 v[124:125], v[166:167], off offset:2048
	v_mfma_f32_16x16x32_bf16 v[18:21], v[142:145], v[230:233], v[18:21]
	v_mfma_f32_16x16x32_bf16 v[22:25], v[146:149], v[230:233], v[22:25]
	v_mfma_f32_16x16x32_bf16 v[26:29], v[150:153], v[230:233], v[26:29]
	v_mfma_f32_16x16x32_bf16 v[30:33], v[154:157], v[230:233], v[30:33]
	v_lshl_add_u64 v[166:167], v[132:133], 0, s[38:39]
	global_load_dwordx2 v[126:127], v[166:167], off
	global_load_dwordx2 v[128:129], v[166:167], off offset:2048
	s_waitcnt lgkmcnt(0)
	s_barrier
	s_mov_b32 s47, s42
	s_mov_b32 s42, s43
	s_mov_b32 s43, s44
	s_mov_b32 s44, s47
	s_waitcnt vmcnt(29)
	v_mul_f32_e32 v186, s12, v186
	v_mul_f32_e32 v187, s12, v187
	v_mul_f32_e32 v188, s13, v188
	v_mul_f32_e32 v189, s13, v189
	v_mul_f32_e32 v190, s14, v190
	v_mul_f32_e32 v191, s14, v191
	v_mul_f32_e32 v192, s15, v192
	v_mul_f32_e32 v193, s15, v193
	v_mul_f32_e32 v194, s16, v194
	v_mul_f32_e32 v195, s16, v195
	v_mul_f32_e32 v196, s17, v196
	v_mul_f32_e32 v197, s17, v197
	v_mul_f32_e32 v198, s18, v198
	v_mul_f32_e32 v199, s18, v199
	v_mul_f32_e32 v200, s19, v200
	v_mul_f32_e32 v201, s19, v201
	v_cvt_pk_bf16_f32 v158, v186, v188
	v_cvt_pk_bf16_f32 v159, v190, v192
	v_cvt_pk_bf16_f32 v160, v194, v196
	v_cvt_pk_bf16_f32 v161, v198, v200
	v_cvt_pk_bf16_f32 v162, v187, v189
	v_cvt_pk_bf16_f32 v163, v191, v193
	v_cvt_pk_bf16_f32 v164, v195, v197
	v_cvt_pk_bf16_f32 v165, v199, v201
	ds_write_b128 v1, v[158:161] offset:0
	ds_write_b128 v1, v[162:165] offset:128
	v_add_u32_e32 v91, s42, v135
	v_add_u32_e32 v93, s42, v137
	ds_read_b128 v[238:241], v139 offset:19456
	ds_read_b128 v[242:245], v139 offset:21504
	ds_read_b128 v[246:249], v139 offset:23552
	ds_read_b128 v[250:253], v139 offset:25600
	ds_read_b128 v[218:221], v91 offset:0
	ds_read_b128 v[222:225], v91 offset:2048
	ds_read_b128 v[226:229], v91 offset:4096
	ds_read_b128 v[230:233], v91 offset:6144
	s_add_i32 s47, s44, s6
	s_add_u32 s30, s30, 0x80
	s_addc_u32 s31, s31, 0
	s_waitcnt lgkmcnt(0)
; #define MU_GLDS_A(buf, kt) do { _Pragma("unroll") for (int i = 0; i < NMU; ++i) \
;         __builtin_amdgcn_global_load_lds((const unsigned*)((const char*)A + aoff[i] + (size_t)(kt) * 128), (PG8_LAS unsigned*)(MU_SA(buf) + wid * 1024 + i * 8192), 16, 0, 0); } while (0)
; #define MU_B_ISSUE(sb, kt) do { const char* kb_ = Bb + (size_t)(kt) * (64 * (size_t)RB); _Pragma("unroll") for (int j = 0; j < 8; ++j) { const char* p_ = kb_ + (size_t)j * RB; \
;         asm volatile("global_load_dwordx2 %0, %1, off" : "=&v"(sb[j]) : "v"(p_) : "memory"); } } while (0)
; #define MU_B_WAIT(sb, N) asm volatile("s_waitcnt vmcnt(%8)" : "+v"(sb[0]), "+v"(sb[1]), "+v"(sb[2]), "+v"(sb[3]), "+v"(sb[4]), "+v"(sb[5]), "+v"(sb[6]), "+v"(sb[7]) : "n"(N) : "memory")
; #define MU_G_LOAD(ga, kt) do { const PG8_LAS f32x4* gk_ = (const PG8_LAS f32x4*)(lds + GAIN_OFF) + 16 * (kt) + 2 * wid; const f32x4 ga_ = gk_[0], gb_ = gk_[1]; \
;         ga[0] = ga_[0]; ga[1] = ga_[1]; ga[2] = ga_[2]; ga[3] = ga_[3]; ga[4] = gb_[0]; ga[5] = gb_[1]; ga[6] = gb_[2]; ga[7] = gb_[3]; } while (0)
; #define MU_COMPUTE(buf) MU_COMPUTE_N(buf, NMU)
; #define MU_END(last) do { if (last) asm volatile("s_waitcnt vmcnt(0)" ::: "memory"); else asm volatile("s_waitcnt vmcnt(8)" ::: "memory"); \
;         asm volatile("s_waitcnt lgkmcnt(0)" ::: "memory"); __builtin_amdgcn_s_barrier(); asm volatile("" ::: "memory"); } while (0)
; template <int MODE>
; __device__ __forceinline__ void moe_unit(PG8_LAS unsigned char* lds, int e, int cb, int slot0  , int nv  , const bf16_t* A, const int* slot_tok,
;                                          const float* W0, const float* W1, bf16_t* OUT, const float* slot_rs  , const int* slot_dst) {
;     ...
;     for (int t = 0; t < nt; t += 2) {
;         if (t + 2 < nt) MU_B_WAIT(s1, 8); else MU_B_WAIT(s1, 0);
;         MU_G_LOAD(g0, t + 1); MU_B_WRITE(s1, 1, g0); __builtin_amdgcn_sched_barrier(0); MU_GLDS_A(1, t + 1); __builtin_amdgcn_sched_barrier(0);
;         if (t + 3 < nt) { MU_B_ISSUE(s1, t + 3); }
;         MU_COMPUTE(0);
;         MU_END(t + 3 >= nt);
;         if (t + 2 < nt) { MU_B_WAIT(s0, 8); MU_G_LOAD(g0, t + 2); MU_B_WRITE(s0, 0, g0); __builtin_amdgcn_sched_barrier(0); MU_GLDS_A(0, t + 2); __builtin_amdgcn_sched_barrier(0); }
;         if (t + 4 < nt) { MU_B_ISSUE(s0, t + 4); }
;         MU_COMPUTE(1);
;         MU_END(t + 4 >= nt);
	v_mfma_f32_16x16x32_bf16 v[78:81], v[238:241], v[218:221], v[78:81]
	v_mfma_f32_16x16x32_bf16 v[74:77], v[242:245], v[218:221], v[74:77]
	v_mfma_f32_16x16x32_bf16 v[70:73], v[246:249], v[218:221], v[70:73]
	v_mfma_f32_16x16x32_bf16 v[66:69], v[250:253], v[218:221], v[66:69]
	ds_read_b128 v[218:221], v93 offset:0
	ds_read_b128 v[142:145], v141 offset:19456
	s_mov_b32 m0, s47
	s_nop 0
	global_load_lds_dwordx4 v86, s[30:31]
	v_mfma_f32_16x16x32_bf16 v[62:65], v[238:241], v[222:225], v[62:65]
	v_mfma_f32_16x16x32_bf16 v[58:61], v[242:245], v[222:225], v[58:61]
	v_mfma_f32_16x16x32_bf16 v[54:57], v[246:249], v[222:225], v[54:57]
	v_mfma_f32_16x16x32_bf16 v[50:53], v[250:253], v[222:225], v[50:53]
	ds_read_b128 v[222:225], v93 offset:2048
	ds_read_b128 v[146:149], v141 offset:21504
	s_add_i32 m0, s47, 0x2000
	s_nop 0
	global_load_lds_dwordx4 v134, s[30:31]
	v_mfma_f32_16x16x32_bf16 v[46:49], v[238:241], v[226:229], v[46:49]
	v_mfma_f32_16x16x32_bf16 v[42:45], v[242:245], v[226:229], v[42:45]
	v_mfma_f32_16x16x32_bf16 v[38:41], v[246:249], v[226:229], v[38:41]
	v_mfma_f32_16x16x32_bf16 v[34:37], v[250:253], v[226:229], v[34:37]
	ds_read_b128 v[226:229], v93 offset:4096
	ds_read_b128 v[150:153], v141 offset:23552
	s_add_i32 m0, s47, 0x4000
	s_nop 0
	global_load_lds_dwordx4 v136, s[30:31]
	v_mfma_f32_16x16x32_bf16 v[18:21], v[238:241], v[230:233], v[18:21]
	v_mfma_f32_16x16x32_bf16 v[22:25], v[242:245], v[230:233], v[22:25]
	v_mfma_f32_16x16x32_bf16 v[26:29], v[246:249], v[230:233], v[26:29]
	v_mfma_f32_16x16x32_bf16 v[30:33], v[250:253], v[230:233], v[30:33]
	ds_read_b128 v[230:233], v93 offset:6144
	ds_read_b128 v[154:157], v141 offset:25600
	s_add_i32 m0, s47, 0x6000
	s_nop 0
	global_load_lds_dwordx4 v138, s[30:31]
	s_add_i32 m0, s47, 0x8000
	s_nop 0
	global_load_lds_dwordx4 v140, s[30:31]
	s_waitcnt lgkmcnt(0)
	s_load_dwordx8 s[20:27], s[28:29], 0x0
	s_add_u32 s28, s28, 0x100
	s_addc_u32 s29, s29, 0
	v_mfma_f32_16x16x32_bf16 v[78:81], v[142:145], v[218:221], v[78:81]
	v_mfma_f32_16x16x32_bf16 v[74:77], v[146:149], v[218:221], v[74:77]
	v_mfma_f32_16x16x32_bf16 v[70:73], v[150:153], v[218:221], v[70:73]
	v_mfma_f32_16x16x32_bf16 v[66:69], v[154:157], v[218:221], v[66:69]
	v_lshl_add_u64 v[132:133], v[132:133], 0, s[40:41]
	global_load_dwordx2 v[186:187], v[132:133], off
	global_load_dwordx2 v[188:189], v[132:133], off offset:2048
	v_mfma_f32_16x16x32_bf16 v[62:65], v[142:145], v[222:225], v[62:65]
	v_mfma_f32_16x16x32_bf16 v[58:61], v[146:149], v[222:225], v[58:61]
	v_mfma_f32_16x16x32_bf16 v[54:57], v[150:153], v[222:225], v[54:57]
	v_mfma_f32_16x16x32_bf16 v[50:53], v[154:157], v[222:225], v[50:53]
	v_lshl_add_u64 v[166:167], v[132:133], 0, s[34:35]
	global_load_dwordx2 v[190:191], v[166:167], off
	global_load_dwordx2 v[192:193], v[166:167], off offset:2048
	v_mfma_f32_16x16x32_bf16 v[46:49], v[142:145], v[226:229], v[46:49]
	v_mfma_f32_16x16x32_bf16 v[42:45], v[146:149], v[226:229], v[42:45]
	v_mfma_f32_16x16x32_bf16 v[38:41], v[150:153], v[226:229], v[38:41]
	v_mfma_f32_16x16x32_bf16 v[34:37], v[154:157], v[226:229], v[34:37]
	v_lshl_add_u64 v[166:167], v[132:133], 0, s[36:37]
	global_load_dwordx2 v[194:195], v[166:167], off
	global_load_dwordx2 v[196:197], v[166:167], off offset:2048
	v_mfma_f32_16x16x32_bf16 v[18:21], v[142:145], v[230:233], v[18:21]
	v_mfma_f32_16x16x32_bf16 v[22:25], v[146:149], v[230:233], v[22:25]
	v_mfma_f32_16x16x32_bf16 v[26:29], v[150:153], v[230:233], v[26:29]
	v_mfma_f32_16x16x32_bf16 v[30:33], v[154:157], v[230:233], v[30:33]
	v_lshl_add_u64 v[166:167], v[132:133], 0, s[38:39]
	global_load_dwordx2 v[198:199], v[166:167], off
	global_load_dwordx2 v[200:201], v[166:167], off offset:2048
	s_waitcnt vmcnt(21)
	s_waitcnt lgkmcnt(0)
	s_barrier
	s_mov_b32 s47, s42
	s_mov_b32 s42, s43
	s_mov_b32 s43, s44
	s_mov_b32 s44, s47
	v_mul_f32_e32 v202, s20, v202
	v_mul_f32_e32 v203, s20, v203
	v_mul_f32_e32 v204, s21, v204
	v_mul_f32_e32 v205, s21, v205
	v_mul_f32_e32 v206, s22, v206
	v_mul_f32_e32 v207, s22, v207
	v_mul_f32_e32 v208, s23, v208
	v_mul_f32_e32 v209, s23, v209
	v_mul_f32_e32 v210, s24, v210
	v_mul_f32_e32 v211, s24, v211
	v_mul_f32_e32 v212, s25, v212
	v_mul_f32_e32 v213, s25, v213
	v_mul_f32_e32 v214, s26, v214
	v_mul_f32_e32 v215, s26, v215
	v_mul_f32_e32 v216, s27, v216
	v_mul_f32_e32 v217, s27, v217
	v_cvt_pk_bf16_f32 v158, v202, v204
	v_cvt_pk_bf16_f32 v159, v206, v208
	v_cvt_pk_bf16_f32 v160, v210, v212
	v_cvt_pk_bf16_f32 v161, v214, v216
	v_cvt_pk_bf16_f32 v162, v203, v205
	v_cvt_pk_bf16_f32 v163, v207, v209
	v_cvt_pk_bf16_f32 v164, v211, v213
	v_cvt_pk_bf16_f32 v165, v215, v217
	ds_write_b128 v1, v[158:161] offset:19456
	ds_write_b128 v1, v[162:165] offset:19584
	v_add_u32_e32 v91, s42, v135
	v_add_u32_e32 v93, s42, v137
	ds_read_b128 v[238:241], v139 offset:0
	ds_read_b128 v[242:245], v139 offset:2048
	ds_read_b128 v[246:249], v139 offset:4096
	ds_read_b128 v[250:253], v139 offset:6144
	ds_read_b128 v[218:221], v91 offset:0
	ds_read_b128 v[222:225], v91 offset:2048
	ds_read_b128 v[226:229], v91 offset:4096
	ds_read_b128 v[230:233], v91 offset:6144
	s_add_i32 s47, s44, s6
	s_add_u32 s30, s30, 0x80
	s_addc_u32 s31, s31, 0
	s_waitcnt lgkmcnt(0)
; #define MU_GLDS_A(buf, kt) do { _Pragma("unroll") for (int i = 0; i < NMU; ++i) \
;         __builtin_amdgcn_global_load_lds((const unsigned*)((const char*)A + aoff[i] + (size_t)(kt) * 128), (PG8_LAS unsigned*)(MU_SA(buf) + wid * 1024 + i * 8192), 16, 0, 0); } while (0)
; #define MU_B_ISSUE(sb, kt) do { const char* kb_ = Bb + (size_t)(kt) * (64 * (size_t)RB); _Pragma("unroll") for (int j = 0; j < 8; ++j) { const char* p_ = kb_ + (size_t)j * RB; \
;         asm volatile("global_load_dwordx2 %0, %1, off" : "=&v"(sb[j]) : "v"(p_) : "memory"); } } while (0)
; #define MU_B_WAIT(sb, N) asm volatile("s_waitcnt vmcnt(%8)" : "+v"(sb[0]), "+v"(sb[1]), "+v"(sb[2]), "+v"(sb[3]), "+v"(sb[4]), "+v"(sb[5]), "+v"(sb[6]), "+v"(sb[7]) : "n"(N) : "memory")
; #define MU_G_LOAD(ga, kt) do { const PG8_LAS f32x4* gk_ = (const PG8_LAS f32x4*)(lds + GAIN_OFF) + 16 * (kt) + 2 * wid; const f32x4 ga_ = gk_[0], gb_ = gk_[1]; \
;         ga[0] = ga_[0]; ga[1] = ga_[1]; ga[2] = ga_[2]; ga[3] = ga_[3]; ga[4] = gb_[0]; ga[5] = gb_[1]; ga[6] = gb_[2]; ga[7] = gb_[3]; } while (0)
; #define MU_COMPUTE(buf) MU_COMPUTE_N(buf, NMU)
; #define MU_END(last) do { if (last) asm volatile("s_waitcnt vmcnt(0)" ::: "memory"); else asm volatile("s_waitcnt vmcnt(8)" ::: "memory"); \
;         asm volatile("s_waitcnt lgkmcnt(0)" ::: "memory"); __builtin_amdgcn_s_barrier(); asm volatile("" ::: "memory"); } while (0)
; template <int MODE>
; __device__ __forceinline__ void moe_unit(PG8_LAS unsigned char* lds, int e, int cb, int slot0  , int nv  , const bf16_t* A, const int* slot_tok,
;                                          const float* W0, const float* W1, bf16_t* OUT, const float* slot_rs  , const int* slot_dst) {
;     ...
;     for (int t = 0; t < nt; t += 2) {
;         if (t + 2 < nt) MU_B_WAIT(s1, 8); else MU_B_WAIT(s1, 0);
;         MU_G_LOAD(g0, t + 1); MU_B_WRITE(s1, 1, g0); __builtin_amdgcn_sched_barrier(0); MU_GLDS_A(1, t + 1); __builtin_amdgcn_sched_barrier(0);
;         if (t + 3 < nt) { MU_B_ISSUE(s1, t + 3); }
;         MU_COMPUTE(0);
;         MU_END(t + 3 >= nt);
;         if (t + 2 < nt) { MU_B_WAIT(s0, 8); MU_G_LOAD(g0, t + 2); MU_B_WRITE(s0, 0, g0); __builtin_amdgcn_sched_barrier(0); MU_GLDS_A(0, t + 2); __builtin_amdgcn_sched_barrier(0); }
;         if (t + 4 < nt) { MU_B_ISSUE(s0, t + 4); }
;         MU_COMPUTE(1);
;         MU_END(t + 4 >= nt);
	v_mfma_f32_16x16x32_bf16 v[78:81], v[238:241], v[218:221], v[78:81]
	v_mfma_f32_16x16x32_bf16 v[74:77], v[242:245], v[218:221], v[74:77]
	v_mfma_f32_16x16x32_bf16 v[70:73], v[246:249], v[218:221], v[70:73]
	v_mfma_f32_16x16x32_bf16 v[66:69], v[250:253], v[218:221], v[66:69]
	ds_read_b128 v[218:221], v93 offset:0
	ds_read_b128 v[142:145], v141 offset:0
	s_mov_b32 m0, s47
	s_nop 0
	global_load_lds_dwordx4 v86, s[30:31]
	v_mfma_f32_16x16x32_bf16 v[62:65], v[238:241], v[222:225], v[62:65]
	v_mfma_f32_16x16x32_bf16 v[58:61], v[242:245], v[222:225], v[58:61]
	v_mfma_f32_16x16x32_bf16 v[54:57], v[246:249], v[222:225], v[54:57]
	v_mfma_f32_16x16x32_bf16 v[50:53], v[250:253], v[222:225], v[50:53]
	ds_read_b128 v[222:225], v93 offset:2048
	ds_read_b128 v[146:149], v141 offset:2048
	s_add_i32 m0, s47, 0x2000
	s_nop 0
	global_load_lds_dwordx4 v134, s[30:31]
	v_mfma_f32_16x16x32_bf16 v[46:49], v[238:241], v[226:229], v[46:49]
	v_mfma_f32_16x16x32_bf16 v[42:45], v[242:245], v[226:229], v[42:45]
	v_mfma_f32_16x16x32_bf16 v[38:41], v[246:249], v[226:229], v[38:41]
	v_mfma_f32_16x16x32_bf16 v[34:37], v[250:253], v[226:229], v[34:37]
	ds_read_b128 v[226:229], v93 offset:4096
	ds_read_b128 v[150:153], v141 offset:4096
	s_add_i32 m0, s47, 0x4000
	s_nop 0
	global_load_lds_dwordx4 v136, s[30:31]
	v_mfma_f32_16x16x32_bf16 v[18:21], v[238:241], v[230:233], v[18:21]
	v_mfma_f32_16x16x32_bf16 v[22:25], v[242:245], v[230:233], v[22:25]
	v_mfma_f32_16x16x32_bf16 v[26:29], v[246:249], v[230:233], v[26:29]
	v_mfma_f32_16x16x32_bf16 v[30:33], v[250:253], v[230:233], v[30:33]
	ds_read_b128 v[230:233], v93 offset:6144
	ds_read_b128 v[154:157], v141 offset:6144
	s_add_i32 m0, s47, 0x6000
	s_nop 0
	global_load_lds_dwordx4 v138, s[30:31]
	s_add_i32 m0, s47, 0x8000
	s_nop 0
	global_load_lds_dwordx4 v140, s[30:31]
	s_waitcnt lgkmcnt(0)
	s_load_dwordx8 s[12:19], s[28:29], 0x0
	s_add_u32 s28, s28, 0x100
	s_addc_u32 s29, s29, 0
	v_mfma_f32_16x16x32_bf16 v[78:81], v[142:145], v[218:221], v[78:81]
	v_mfma_f32_16x16x32_bf16 v[74:77], v[146:149], v[218:221], v[74:77]
	v_mfma_f32_16x16x32_bf16 v[70:73], v[150:153], v[218:221], v[70:73]
	v_mfma_f32_16x16x32_bf16 v[66:69], v[154:157], v[218:221], v[66:69]
	v_lshl_add_u64 v[132:133], v[132:133], 0, s[40:41]
	global_load_dwordx2 v[202:203], v[132:133], off
	global_load_dwordx2 v[204:205], v[132:133], off offset:2048
	v_mfma_f32_16x16x32_bf16 v[62:65], v[142:145], v[222:225], v[62:65]
	v_mfma_f32_16x16x32_bf16 v[58:61], v[146:149], v[222:225], v[58:61]
	v_mfma_f32_16x16x32_bf16 v[54:57], v[150:153], v[222:225], v[54:57]
	v_mfma_f32_16x16x32_bf16 v[50:53], v[154:157], v[222:225], v[50:53]
	v_lshl_add_u64 v[166:167], v[132:133], 0, s[34:35]
	global_load_dwordx2 v[206:207], v[166:167], off
	global_load_dwordx2 v[208:209], v[166:167], off offset:2048
	v_mfma_f32_16x16x32_bf16 v[46:49], v[142:145], v[226:229], v[46:49]
	v_mfma_f32_16x16x32_bf16 v[42:45], v[146:149], v[226:229], v[42:45]
	v_mfma_f32_16x16x32_bf16 v[38:41], v[150:153], v[226:229], v[38:41]
	v_mfma_f32_16x16x32_bf16 v[34:37], v[154:157], v[226:229], v[34:37]
	v_lshl_add_u64 v[166:167], v[132:133], 0, s[36:37]
	global_load_dwordx2 v[210:211], v[166:167], off
	global_load_dwordx2 v[212:213], v[166:167], off offset:2048
	v_mfma_f32_16x16x32_bf16 v[18:21], v[142:145], v[230:233], v[18:21]
	v_mfma_f32_16x16x32_bf16 v[22:25], v[146:149], v[230:233], v[22:25]
	v_mfma_f32_16x16x32_bf16 v[26:29], v[150:153], v[230:233], v[26:29]
	v_mfma_f32_16x16x32_bf16 v[30:33], v[154:157], v[230:233], v[30:33]
	v_lshl_add_u64 v[166:167], v[132:133], 0, s[38:39]
	global_load_dwordx2 v[214:215], v[166:167], off
	global_load_dwordx2 v[216:217], v[166:167], off offset:2048
	s_waitcnt vmcnt(21)
	s_waitcnt lgkmcnt(0)
	s_barrier
	s_mov_b32 s47, s42
	s_mov_b32 s42, s43
	s_mov_b32 s43, s44
	s_mov_b32 s44, s47
	v_mul_f32_e32 v98, s12, v98
	v_mul_f32_e32 v99, s12, v99
	v_mul_f32_e32 v100, s13, v100
	v_mul_f32_e32 v101, s13, v101
	v_mul_f32_e32 v102, s14, v102
	v_mul_f32_e32 v103, s14, v103
	v_mul_f32_e32 v104, s15, v104
	v_mul_f32_e32 v105, s15, v105
	v_mul_f32_e32 v106, s16, v106
	v_mul_f32_e32 v107, s16, v107
	v_mul_f32_e32 v108, s17, v108
	v_mul_f32_e32 v109, s17, v109
	v_mul_f32_e32 v110, s18, v110
	v_mul_f32_e32 v111, s18, v111
	v_mul_f32_e32 v112, s19, v112
	v_mul_f32_e32 v113, s19, v113
	v_cvt_pk_bf16_f32 v158, v98, v100
	v_cvt_pk_bf16_f32 v159, v102, v104
	v_cvt_pk_bf16_f32 v160, v106, v108
	v_cvt_pk_bf16_f32 v161, v110, v112
	v_cvt_pk_bf16_f32 v162, v99, v101
	v_cvt_pk_bf16_f32 v163, v103, v105
	v_cvt_pk_bf16_f32 v164, v107, v109
	v_cvt_pk_bf16_f32 v165, v111, v113
	ds_write_b128 v1, v[158:161] offset:0
	ds_write_b128 v1, v[162:165] offset:128
	v_add_u32_e32 v91, s42, v135
	v_add_u32_e32 v93, s42, v137
	ds_read_b128 v[238:241], v139 offset:19456
	ds_read_b128 v[242:245], v139 offset:21504
	ds_read_b128 v[246:249], v139 offset:23552
	ds_read_b128 v[250:253], v139 offset:25600
	ds_read_b128 v[218:221], v91 offset:0
	ds_read_b128 v[222:225], v91 offset:2048
	ds_read_b128 v[226:229], v91 offset:4096
	ds_read_b128 v[230:233], v91 offset:6144
	s_add_i32 s47, s44, s6
	s_add_u32 s30, s30, 0x80
	s_addc_u32 s31, s31, 0
	s_waitcnt lgkmcnt(0)
; #define MU_GLDS_A(buf, kt) do { _Pragma("unroll") for (int i = 0; i < NMU; ++i) \
;         __builtin_amdgcn_global_load_lds((const unsigned*)((const char*)A + aoff[i] + (size_t)(kt) * 128), (PG8_LAS unsigned*)(MU_SA(buf) + wid * 1024 + i * 8192), 16, 0, 0); } while (0)
; #define MU_B_ISSUE(sb, kt) do { const char* kb_ = Bb + (size_t)(kt) * (64 * (size_t)RB); _Pragma("unroll") for (int j = 0; j < 8; ++j) { const char* p_ = kb_ + (size_t)j * RB; \
;         asm volatile("global_load_dwordx2 %0, %1, off" : "=&v"(sb[j]) : "v"(p_) : "memory"); } } while (0)
; #define MU_B_WAIT(sb, N) asm volatile("s_waitcnt vmcnt(%8)" : "+v"(sb[0]), "+v"(sb[1]), "+v"(sb[2]), "+v"(sb[3]), "+v"(sb[4]), "+v"(sb[5]), "+v"(sb[6]), "+v"(sb[7]) : "n"(N) : "memory")
; #define MU_G_LOAD(ga, kt) do { const PG8_LAS f32x4* gk_ = (const PG8_LAS f32x4*)(lds + GAIN_OFF) + 16 * (kt) + 2 * wid; const f32x4 ga_ = gk_[0], gb_ = gk_[1]; \
;         ga[0] = ga_[0]; ga[1] = ga_[1]; ga[2] = ga_[2]; ga[3] = ga_[3]; ga[4] = gb_[0]; ga[5] = gb_[1]; ga[6] = gb_[2]; ga[7] = gb_[3]; } while (0)
; #define MU_COMPUTE(buf) MU_COMPUTE_N(buf, NMU)
; #define MU_END(last) do { if (last) asm volatile("s_waitcnt vmcnt(0)" ::: "memory"); else asm volatile("s_waitcnt vmcnt(8)" ::: "memory"); \
;         asm volatile("s_waitcnt lgkmcnt(0)" ::: "memory"); __builtin_amdgcn_s_barrier(); asm volatile("" ::: "memory"); } while (0)
; template <int MODE>
; __device__ __forceinline__ void moe_unit(PG8_LAS unsigned char* lds, int e, int cb, int slot0  , int nv  , const bf16_t* A, const int* slot_tok,
;                                          const float* W0, const float* W1, bf16_t* OUT, const float* slot_rs  , const int* slot_dst) {
;     ...
;     for (int t = 0; t < nt; t += 2) {
;         if (t + 2 < nt) MU_B_WAIT(s1, 8); else MU_B_WAIT(s1, 0);
;         MU_G_LOAD(g0, t + 1); MU_B_WRITE(s1, 1, g0); __builtin_amdgcn_sched_barrier(0); MU_GLDS_A(1, t + 1); __builtin_amdgcn_sched_barrier(0);
;         if (t + 3 < nt) { MU_B_ISSUE(s1, t + 3); }
;         MU_COMPUTE(0);
;         MU_END(t + 3 >= nt);
;         if (t + 2 < nt) { MU_B_WAIT(s0, 8); MU_G_LOAD(g0, t + 2); MU_B_WRITE(s0, 0, g0); __builtin_amdgcn_sched_barrier(0); MU_GLDS_A(0, t + 2); __builtin_amdgcn_sched_barrier(0); }
;         if (t + 4 < nt) { MU_B_ISSUE(s0, t + 4); }
;         MU_COMPUTE(1);
;         MU_END(t + 4 >= nt);
	v_mfma_f32_16x16x32_bf16 v[78:81], v[238:241], v[218:221], v[78:81]
	v_mfma_f32_16x16x32_bf16 v[74:77], v[242:245], v[218:221], v[74:77]
	v_mfma_f32_16x16x32_bf16 v[70:73], v[246:249], v[218:221], v[70:73]
	v_mfma_f32_16x16x32_bf16 v[66:69], v[250:253], v[218:221], v[66:69]
	ds_read_b128 v[218:221], v93 offset:0
	ds_read_b128 v[142:145], v141 offset:19456
	s_mov_b32 m0, s47
	s_nop 0
	global_load_lds_dwordx4 v86, s[30:31]
	v_mfma_f32_16x16x32_bf16 v[62:65], v[238:241], v[222:225], v[62:65]
	v_mfma_f32_16x16x32_bf16 v[58:61], v[242:245], v[222:225], v[58:61]
	v_mfma_f32_16x16x32_bf16 v[54:57], v[246:249], v[222:225], v[54:57]
	v_mfma_f32_16x16x32_bf16 v[50:53], v[250:253], v[222:225], v[50:53]
	ds_read_b128 v[222:225], v93 offset:2048
	ds_read_b128 v[146:149], v141 offset:21504
	s_add_i32 m0, s47, 0x2000
	s_nop 0
	global_load_lds_dwordx4 v134, s[30:31]
	v_mfma_f32_16x16x32_bf16 v[46:49], v[238:241], v[226:229], v[46:49]
	v_mfma_f32_16x16x32_bf16 v[42:45], v[242:245], v[226:229], v[42:45]
	v_mfma_f32_16x16x32_bf16 v[38:41], v[246:249], v[226:229], v[38:41]
	v_mfma_f32_16x16x32_bf16 v[34:37], v[250:253], v[226:229], v[34:37]
	ds_read_b128 v[226:229], v93 offset:4096
	ds_read_b128 v[150:153], v141 offset:23552
	s_add_i32 m0, s47, 0x4000
	s_nop 0
	global_load_lds_dwordx4 v136, s[30:31]
	v_mfma_f32_16x16x32_bf16 v[18:21], v[238:241], v[230:233], v[18:21]
	v_mfma_f32_16x16x32_bf16 v[22:25], v[242:245], v[230:233], v[22:25]
	v_mfma_f32_16x16x32_bf16 v[26:29], v[246:249], v[230:233], v[26:29]
	v_mfma_f32_16x16x32_bf16 v[30:33], v[250:253], v[230:233], v[30:33]
	ds_read_b128 v[230:233], v93 offset:6144
	ds_read_b128 v[154:157], v141 offset:25600
	s_add_i32 m0, s47, 0x6000
	s_nop 0
	global_load_lds_dwordx4 v138, s[30:31]
	s_add_i32 m0, s47, 0x8000
	s_nop 0
	global_load_lds_dwordx4 v140, s[30:31]
	s_waitcnt lgkmcnt(0)
	s_load_dwordx8 s[20:27], s[28:29], 0x0
	s_add_u32 s28, s28, 0x100
	s_addc_u32 s29, s29, 0
	v_mfma_f32_16x16x32_bf16 v[78:81], v[142:145], v[218:221], v[78:81]
	v_mfma_f32_16x16x32_bf16 v[74:77], v[146:149], v[218:221], v[74:77]
	v_mfma_f32_16x16x32_bf16 v[70:73], v[150:153], v[218:221], v[70:73]
	v_mfma_f32_16x16x32_bf16 v[66:69], v[154:157], v[218:221], v[66:69]
	v_lshl_add_u64 v[132:133], v[132:133], 0, s[40:41]
	global_load_dwordx2 v[98:99], v[132:133], off
	global_load_dwordx2 v[100:101], v[132:133], off offset:2048
	v_mfma_f32_16x16x32_bf16 v[62:65], v[142:145], v[222:225], v[62:65]
	v_mfma_f32_16x16x32_bf16 v[58:61], v[146:149], v[222:225], v[58:61]
	v_mfma_f32_16x16x32_bf16 v[54:57], v[150:153], v[222:225], v[54:57]
	v_mfma_f32_16x16x32_bf16 v[50:53], v[154:157], v[222:225], v[50:53]
	v_lshl_add_u64 v[166:167], v[132:133], 0, s[34:35]
	global_load_dwordx2 v[102:103], v[166:167], off
	global_load_dwordx2 v[104:105], v[166:167], off offset:2048
	v_mfma_f32_16x16x32_bf16 v[46:49], v[142:145], v[226:229], v[46:49]
	v_mfma_f32_16x16x32_bf16 v[42:45], v[146:149], v[226:229], v[42:45]
	v_mfma_f32_16x16x32_bf16 v[38:41], v[150:153], v[226:229], v[38:41]
	v_mfma_f32_16x16x32_bf16 v[34:37], v[154:157], v[226:229], v[34:37]
	v_lshl_add_u64 v[166:167], v[132:133], 0, s[36:37]
	global_load_dwordx2 v[106:107], v[166:167], off
	global_load_dwordx2 v[108:109], v[166:167], off offset:2048
	v_mfma_f32_16x16x32_bf16 v[18:21], v[142:145], v[230:233], v[18:21]
	v_mfma_f32_16x16x32_bf16 v[22:25], v[146:149], v[230:233], v[22:25]
	v_mfma_f32_16x16x32_bf16 v[26:29], v[150:153], v[230:233], v[26:29]
	v_mfma_f32_16x16x32_bf16 v[30:33], v[154:157], v[230:233], v[30:33]
	v_lshl_add_u64 v[166:167], v[132:133], 0, s[38:39]
	global_load_dwordx2 v[110:111], v[166:167], off
	global_load_dwordx2 v[112:113], v[166:167], off offset:2048
	s_waitcnt vmcnt(21)
	s_waitcnt lgkmcnt(0)
	s_barrier
	s_mov_b32 s47, s42
	s_mov_b32 s42, s43
	s_mov_b32 s43, s44
	s_mov_b32 s44, s47
	s_mov_b32 s46, 13
.Lmu_loop_X4:
	v_mul_f32_e32 v114, s20, v114
	v_mul_f32_e32 v115, s20, v115
	v_mul_f32_e32 v116, s21, v116
	v_mul_f32_e32 v117, s21, v117
	v_mul_f32_e32 v118, s22, v118
	v_mul_f32_e32 v119, s22, v119
	v_mul_f32_e32 v120, s23, v120
	v_mul_f32_e32 v121, s23, v121
	v_mul_f32_e32 v122, s24, v122
	v_mul_f32_e32 v123, s24, v123
	v_mul_f32_e32 v124, s25, v124
	v_mul_f32_e32 v125, s25, v125
	v_mul_f32_e32 v126, s26, v126
	v_mul_f32_e32 v127, s26, v127
	v_mul_f32_e32 v128, s27, v128
	v_mul_f32_e32 v129, s27, v129
	v_cvt_pk_bf16_f32 v158, v114, v116
	v_cvt_pk_bf16_f32 v159, v118, v120
	v_cvt_pk_bf16_f32 v160, v122, v124
	v_cvt_pk_bf16_f32 v161, v126, v128
	v_cvt_pk_bf16_f32 v162, v115, v117
	v_cvt_pk_bf16_f32 v163, v119, v121
	v_cvt_pk_bf16_f32 v164, v123, v125
	v_cvt_pk_bf16_f32 v165, v127, v129
	ds_write_b128 v1, v[158:161] offset:19456
	ds_write_b128 v1, v[162:165] offset:19584
	v_add_u32_e32 v91, s42, v135
	v_add_u32_e32 v93, s42, v137
	ds_read_b128 v[238:241], v139 offset:0
	ds_read_b128 v[242:245], v139 offset:2048
	ds_read_b128 v[246:249], v139 offset:4096
	ds_read_b128 v[250:253], v139 offset:6144
	ds_read_b128 v[218:221], v91 offset:0
	ds_read_b128 v[222:225], v91 offset:2048
	ds_read_b128 v[226:229], v91 offset:4096
	ds_read_b128 v[230:233], v91 offset:6144
	s_add_i32 s47, s44, s6
	s_add_u32 s30, s30, 0x80
	s_addc_u32 s31, s31, 0
	s_waitcnt lgkmcnt(0)
; #define MU_GLDS_A(buf, kt) do { _Pragma("unroll") for (int i = 0; i < NMU; ++i) \
;         __builtin_amdgcn_global_load_lds((const unsigned*)((const char*)A + aoff[i] + (size_t)(kt) * 128), (PG8_LAS unsigned*)(MU_SA(buf) + wid * 1024 + i * 8192), 16, 0, 0); } while (0)
; #define MU_B_ISSUE(sb, kt) do { const char* kb_ = Bb + (size_t)(kt) * (64 * (size_t)RB); _Pragma("unroll") for (int j = 0; j < 8; ++j) { const char* p_ = kb_ + (size_t)j * RB; \
;         asm volatile("global_load_dwordx2 %0, %1, off" : "=&v"(sb[j]) : "v"(p_) : "memory"); } } while (0)
; #define MU_B_WAIT(sb, N) asm volatile("s_waitcnt vmcnt(%8)" : "+v"(sb[0]), "+v"(sb[1]), "+v"(sb[2]), "+v"(sb[3]), "+v"(sb[4]), "+v"(sb[5]), "+v"(sb[6]), "+v"(sb[7]) : "n"(N) : "memory")
; #define MU_COMPUTE(buf) MU_COMPUTE_N(buf, NMU)
; template <int MODE>
; __device__ __forceinline__ void moe_unit(PG8_LAS unsigned char* lds, int e, int cb, int slot0  , int nv  , const bf16_t* A, const int* slot_tok,
;                                          const float* W0, const float* W1, bf16_t* OUT, const float* slot_rs  , const int* slot_dst) {
;     ...
;     f32x4 acc[NMU][4];
; #pragma unroll
;     for (int m = 0; m < NMU; ++m)
; #pragma unroll
;         for (int n = 0; n < 4; ++n) acc[m][n] = (f32x4){0.f, 0.f, 0.f, 0.f};
;     f32x2 s0[8], s1[8];
;     float g0[8];
;     MU_GLDS_A(0, 0); MU_B_ISSUE(s0, 0); MU_G_LOAD(g0, 0); MU_B_ISSUE(s1, 1);
;     MU_B_WAIT(s0, 8); MU_B_WRITE(s0, 0, g0); __builtin_amdgcn_sched_barrier(0); MU_B_ISSUE(s0, 2);
;     asm volatile("s_waitcnt vmcnt(16)" ::: "memory");
;     asm volatile("s_waitcnt lgkmcnt(0)" ::: "memory"); __builtin_amdgcn_s_barrier(); asm volatile("" ::: "memory");
; #pragma unroll 1
;     for (int t = 0; t < nt; t += 2) {
;         if (t + 2 < nt) MU_B_WAIT(s1, 8); else MU_B_WAIT(s1, 0);
;         MU_G_LOAD(g0, t + 1); MU_B_WRITE(s1, 1, g0); __builtin_amdgcn_sched_barrier(0); MU_GLDS_A(1, t + 1); __builtin_amdgcn_sched_barrier(0);
;         if (t + 3 < nt) { MU_B_ISSUE(s1, t + 3); }
;         MU_COMPUTE(0);
;         MU_END(t + 3 >= nt);
;         if (t + 2 < nt) { MU_B_WAIT(s0, 8); MU_G_LOAD(g0, t + 2); MU_B_WRITE(s0, 0, g0); __builtin_amdgcn_sched_barrier(0); MU_GLDS_A(0, t + 2); __builtin_amdgcn_sched_barrier(0); }
;         if (t + 4 < nt) { MU_B_ISSUE(s0, t + 4); }
;         MU_COMPUTE(1);
;         MU_END(t + 4 >= nt);
	v_mfma_f32_16x16x32_bf16 v[78:81], v[238:241], v[218:221], v[78:81]
	v_mfma_f32_16x16x32_bf16 v[74:77], v[242:245], v[218:221], v[74:77]
	v_mfma_f32_16x16x32_bf16 v[70:73], v[246:249], v[218:221], v[70:73]
	v_mfma_f32_16x16x32_bf16 v[66:69], v[250:253], v[218:221], v[66:69]
	ds_read_b128 v[218:221], v93 offset:0
	ds_read_b128 v[142:145], v141 offset:0
	s_mov_b32 m0, s47
	s_nop 0
	global_load_lds_dwordx4 v86, s[30:31]
	v_mfma_f32_16x16x32_bf16 v[62:65], v[238:241], v[222:225], v[62:65]
	v_mfma_f32_16x16x32_bf16 v[58:61], v[242:245], v[222:225], v[58:61]
	v_mfma_f32_16x16x32_bf16 v[54:57], v[246:249], v[222:225], v[54:57]
	v_mfma_f32_16x16x32_bf16 v[50:53], v[250:253], v[222:225], v[50:53]
	ds_read_b128 v[222:225], v93 offset:2048
	ds_read_b128 v[146:149], v141 offset:2048
	s_add_i32 m0, s47, 0x2000
	s_nop 0
	global_load_lds_dwordx4 v134, s[30:31]
	v_mfma_f32_16x16x32_bf16 v[46:49], v[238:241], v[226:229], v[46:49]
	v_mfma_f32_16x16x32_bf16 v[42:45], v[242:245], v[226:229], v[42:45]
	v_mfma_f32_16x16x32_bf16 v[38:41], v[246:249], v[226:229], v[38:41]
	v_mfma_f32_16x16x32_bf16 v[34:37], v[250:253], v[226:229], v[34:37]
	ds_read_b128 v[226:229], v93 offset:4096
	ds_read_b128 v[150:153], v141 offset:4096
	s_add_i32 m0, s47, 0x4000
	s_nop 0
	global_load_lds_dwordx4 v136, s[30:31]
	v_mfma_f32_16x16x32_bf16 v[18:21], v[238:241], v[230:233], v[18:21]
	v_mfma_f32_16x16x32_bf16 v[22:25], v[242:245], v[230:233], v[22:25]
	v_mfma_f32_16x16x32_bf16 v[26:29], v[246:249], v[230:233], v[26:29]
	v_mfma_f32_16x16x32_bf16 v[30:33], v[250:253], v[230:233], v[30:33]
	ds_read_b128 v[230:233], v93 offset:6144
	ds_read_b128 v[154:157], v141 offset:6144
	s_add_i32 m0, s47, 0x6000
	s_nop 0
	global_load_lds_dwordx4 v138, s[30:31]
	s_add_i32 m0, s47, 0x8000
	s_nop 0
	global_load_lds_dwordx4 v140, s[30:31]
	s_waitcnt lgkmcnt(0)
	s_load_dwordx8 s[12:19], s[28:29], 0x0
	s_add_u32 s28, s28, 0x100
	s_addc_u32 s29, s29, 0
	v_mfma_f32_16x16x32_bf16 v[78:81], v[142:145], v[218:221], v[78:81]
	v_mfma_f32_16x16x32_bf16 v[74:77], v[146:149], v[218:221], v[74:77]
	v_mfma_f32_16x16x32_bf16 v[70:73], v[150:153], v[218:221], v[70:73]
	v_mfma_f32_16x16x32_bf16 v[66:69], v[154:157], v[218:221], v[66:69]
	v_lshl_add_u64 v[132:133], v[132:133], 0, s[40:41]
	global_load_dwordx2 v[114:115], v[132:133], off
	global_load_dwordx2 v[116:117], v[132:133], off offset:2048
	v_mfma_f32_16x16x32_bf16 v[62:65], v[142:145], v[222:225], v[62:65]
	v_mfma_f32_16x16x32_bf16 v[58:61], v[146:149], v[222:225], v[58:61]
	v_mfma_f32_16x16x32_bf16 v[54:57], v[150:153], v[222:225], v[54:57]
	v_mfma_f32_16x16x32_bf16 v[50:53], v[154:157], v[222:225], v[50:53]
	v_lshl_add_u64 v[166:167], v[132:133], 0, s[34:35]
	global_load_dwordx2 v[118:119], v[166:167], off
	global_load_dwordx2 v[120:121], v[166:167], off offset:2048
	v_mfma_f32_16x16x32_bf16 v[46:49], v[142:145], v[226:229], v[46:49]
	v_mfma_f32_16x16x32_bf16 v[42:45], v[146:149], v[226:229], v[42:45]
	v_mfma_f32_16x16x32_bf16 v[38:41], v[150:153], v[226:229], v[38:41]
	v_mfma_f32_16x16x32_bf16 v[34:37], v[154:157], v[226:229], v[34:37]
	v_lshl_add_u64 v[166:167], v[132:133], 0, s[36:37]
	global_load_dwordx2 v[122:123], v[166:167], off
	global_load_dwordx2 v[124:125], v[166:167], off offset:2048
	v_mfma_f32_16x16x32_bf16 v[18:21], v[142:145], v[230:233], v[18:21]
	v_mfma_f32_16x16x32_bf16 v[22:25], v[146:149], v[230:233], v[22:25]
	v_mfma_f32_16x16x32_bf16 v[26:29], v[150:153], v[230:233], v[26:29]
	v_mfma_f32_16x16x32_bf16 v[30:33], v[154:157], v[230:233], v[30:33]
	v_lshl_add_u64 v[166:167], v[132:133], 0, s[38:39]
	global_load_dwordx2 v[126:127], v[166:167], off
	global_load_dwordx2 v[128:129], v[166:167], off offset:2048
	s_waitcnt vmcnt(21)
	s_waitcnt lgkmcnt(0)
	s_barrier
	s_mov_b32 s47, s42
	s_mov_b32 s42, s43
	s_mov_b32 s43, s44
	s_mov_b32 s44, s47
	v_mul_f32_e32 v186, s12, v186
	v_mul_f32_e32 v187, s12, v187
	v_mul_f32_e32 v188, s13, v188
	v_mul_f32_e32 v189, s13, v189
	v_mul_f32_e32 v190, s14, v190
	v_mul_f32_e32 v191, s14, v191
	v_mul_f32_e32 v192, s15, v192
	v_mul_f32_e32 v193, s15, v193
	v_mul_f32_e32 v194, s16, v194
	v_mul_f32_e32 v195, s16, v195
	v_mul_f32_e32 v196, s17, v196
	v_mul_f32_e32 v197, s17, v197
	v_mul_f32_e32 v198, s18, v198
	v_mul_f32_e32 v199, s18, v199
	v_mul_f32_e32 v200, s19, v200
	v_mul_f32_e32 v201, s19, v201
	v_cvt_pk_bf16_f32 v158, v186, v188
	v_cvt_pk_bf16_f32 v159, v190, v192
	v_cvt_pk_bf16_f32 v160, v194, v196
	v_cvt_pk_bf16_f32 v161, v198, v200
	v_cvt_pk_bf16_f32 v162, v187, v189
	v_cvt_pk_bf16_f32 v163, v191, v193
	v_cvt_pk_bf16_f32 v164, v195, v197
	v_cvt_pk_bf16_f32 v165, v199, v201
	ds_write_b128 v1, v[158:161] offset:0
	ds_write_b128 v1, v[162:165] offset:128
	v_add_u32_e32 v91, s42, v135
	v_add_u32_e32 v93, s42, v137
	ds_read_b128 v[238:241], v139 offset:19456
	ds_read_b128 v[242:245], v139 offset:21504
	ds_read_b128 v[246:249], v139 offset:23552
	ds_read_b128 v[250:253], v139 offset:25600
	ds_read_b128 v[218:221], v91 offset:0
	ds_read_b128 v[222:225], v91 offset:2048
	ds_read_b128 v[226:229], v91 offset:4096
	ds_read_b128 v[230:233], v91 offset:6144
	s_add_i32 s47, s44, s6
	s_add_u32 s30, s30, 0x80
	s_addc_u32 s31, s31, 0
	s_waitcnt lgkmcnt(0)
; #define MU_GLDS_A(buf, kt) do { _Pragma("unroll") for (int i = 0; i < NMU; ++i) \
;         __builtin_amdgcn_global_load_lds((const unsigned*)((const char*)A + aoff[i] + (size_t)(kt) * 128), (PG8_LAS unsigned*)(MU_SA(buf) + wid * 1024 + i * 8192), 16, 0, 0); } while (0)
; #define MU_B_ISSUE(sb, kt) do { const char* kb_ = Bb + (size_t)(kt) * (64 * (size_t)RB); _Pragma("unroll") for (int j = 0; j < 8; ++j) { const char* p_ = kb_ + (size_t)j * RB; \
;         asm volatile("global_load_dwordx2 %0, %1, off" : "=&v"(sb[j]) : "v"(p_) : "memory"); } } while (0)
; #define MU_B_WAIT(sb, N) asm volatile("s_waitcnt vmcnt(%8)" : "+v"(sb[0]), "+v"(sb[1]), "+v"(sb[2]), "+v"(sb[3]), "+v"(sb[4]), "+v"(sb[5]), "+v"(sb[6]), "+v"(sb[7]) : "n"(N) : "memory")
; #define MU_COMPUTE(buf) MU_COMPUTE_N(buf, NMU)
; template <int MODE>
; __device__ __forceinline__ void moe_unit(PG8_LAS unsigned char* lds, int e, int cb, int slot0  , int nv  , const bf16_t* A, const int* slot_tok,
;                                          const float* W0, const float* W1, bf16_t* OUT, const float* slot_rs  , const int* slot_dst) {
;     ...
;     f32x4 acc[NMU][4];
; #pragma unroll
;     for (int m = 0; m < NMU; ++m)
; #pragma unroll
;         for (int n = 0; n < 4; ++n) acc[m][n] = (f32x4){0.f, 0.f, 0.f, 0.f};
;     f32x2 s0[8], s1[8];
;     float g0[8];
;     MU_GLDS_A(0, 0); MU_B_ISSUE(s0, 0); MU_G_LOAD(g0, 0); MU_B_ISSUE(s1, 1);
;     MU_B_WAIT(s0, 8); MU_B_WRITE(s0, 0, g0); __builtin_amdgcn_sched_barrier(0); MU_B_ISSUE(s0, 2);
;     asm volatile("s_waitcnt vmcnt(16)" ::: "memory");
;     asm volatile("s_waitcnt lgkmcnt(0)" ::: "memory"); __builtin_amdgcn_s_barrier(); asm volatile("" ::: "memory");
; #pragma unroll 1
;     for (int t = 0; t < nt; t += 2) {
;         if (t + 2 < nt) MU_B_WAIT(s1, 8); else MU_B_WAIT(s1, 0);
;         MU_G_LOAD(g0, t + 1); MU_B_WRITE(s1, 1, g0); __builtin_amdgcn_sched_barrier(0); MU_GLDS_A(1, t + 1); __builtin_amdgcn_sched_barrier(0);
;         if (t + 3 < nt) { MU_B_ISSUE(s1, t + 3); }
;         MU_COMPUTE(0);
;         MU_END(t + 3 >= nt);
;         if (t + 2 < nt) { MU_B_WAIT(s0, 8); MU_G_LOAD(g0, t + 2); MU_B_WRITE(s0, 0, g0); __builtin_amdgcn_sched_barrier(0); MU_GLDS_A(0, t + 2); __builtin_amdgcn_sched_barrier(0); }
;         if (t + 4 < nt) { MU_B_ISSUE(s0, t + 4); }
;         MU_COMPUTE(1);
;         MU_END(t + 4 >= nt);
	v_mfma_f32_16x16x32_bf16 v[78:81], v[238:241], v[218:221], v[78:81]
	v_mfma_f32_16x16x32_bf16 v[74:77], v[242:245], v[218:221], v[74:77]
	v_mfma_f32_16x16x32_bf16 v[70:73], v[246:249], v[218:221], v[70:73]
	v_mfma_f32_16x16x32_bf16 v[66:69], v[250:253], v[218:221], v[66:69]
	ds_read_b128 v[218:221], v93 offset:0
	ds_read_b128 v[142:145], v141 offset:19456
	s_mov_b32 m0, s47
	s_nop 0
	global_load_lds_dwordx4 v86, s[30:31]
	v_mfma_f32_16x16x32_bf16 v[62:65], v[238:241], v[222:225], v[62:65]
	v_mfma_f32_16x16x32_bf16 v[58:61], v[242:245], v[222:225], v[58:61]
	v_mfma_f32_16x16x32_bf16 v[54:57], v[246:249], v[222:225], v[54:57]
	v_mfma_f32_16x16x32_bf16 v[50:53], v[250:253], v[222:225], v[50:53]
	ds_read_b128 v[222:225], v93 offset:2048
	ds_read_b128 v[146:149], v141 offset:21504
	s_add_i32 m0, s47, 0x2000
	s_nop 0
	global_load_lds_dwordx4 v134, s[30:31]
	v_mfma_f32_16x16x32_bf16 v[46:49], v[238:241], v[226:229], v[46:49]
	v_mfma_f32_16x16x32_bf16 v[42:45], v[242:245], v[226:229], v[42:45]
	v_mfma_f32_16x16x32_bf16 v[38:41], v[246:249], v[226:229], v[38:41]
	v_mfma_f32_16x16x32_bf16 v[34:37], v[250:253], v[226:229], v[34:37]
	ds_read_b128 v[226:229], v93 offset:4096
	ds_read_b128 v[150:153], v141 offset:23552
	s_add_i32 m0, s47, 0x4000
	s_nop 0
	global_load_lds_dwordx4 v136, s[30:31]
	v_mfma_f32_16x16x32_bf16 v[18:21], v[238:241], v[230:233], v[18:21]
	v_mfma_f32_16x16x32_bf16 v[22:25], v[242:245], v[230:233], v[22:25]
	v_mfma_f32_16x16x32_bf16 v[26:29], v[246:249], v[230:233], v[26:29]
	v_mfma_f32_16x16x32_bf16 v[30:33], v[250:253], v[230:233], v[30:33]
	ds_read_b128 v[230:233], v93 offset:6144
	ds_read_b128 v[154:157], v141 offset:25600
	s_add_i32 m0, s47, 0x6000
	s_nop 0
	global_load_lds_dwordx4 v138, s[30:31]
	s_add_i32 m0, s47, 0x8000
	s_nop 0
	global_load_lds_dwordx4 v140, s[30:31]
	s_waitcnt lgkmcnt(0)
	s_load_dwordx8 s[20:27], s[28:29], 0x0
	s_add_u32 s28, s28, 0x100
	s_addc_u32 s29, s29, 0
	v_mfma_f32_16x16x32_bf16 v[78:81], v[142:145], v[218:221], v[78:81]
	v_mfma_f32_16x16x32_bf16 v[74:77], v[146:149], v[218:221], v[74:77]
	v_mfma_f32_16x16x32_bf16 v[70:73], v[150:153], v[218:221], v[70:73]
	v_mfma_f32_16x16x32_bf16 v[66:69], v[154:157], v[218:221], v[66:69]
	v_lshl_add_u64 v[132:133], v[132:133], 0, s[40:41]
	global_load_dwordx2 v[186:187], v[132:133], off
	global_load_dwordx2 v[188:189], v[132:133], off offset:2048
	v_mfma_f32_16x16x32_bf16 v[62:65], v[142:145], v[222:225], v[62:65]
	v_mfma_f32_16x16x32_bf16 v[58:61], v[146:149], v[222:225], v[58:61]
	v_mfma_f32_16x16x32_bf16 v[54:57], v[150:153], v[222:225], v[54:57]
	v_mfma_f32_16x16x32_bf16 v[50:53], v[154:157], v[222:225], v[50:53]
	v_lshl_add_u64 v[166:167], v[132:133], 0, s[34:35]
	global_load_dwordx2 v[190:191], v[166:167], off
	global_load_dwordx2 v[192:193], v[166:167], off offset:2048
	v_mfma_f32_16x16x32_bf16 v[46:49], v[142:145], v[226:229], v[46:49]
	v_mfma_f32_16x16x32_bf16 v[42:45], v[146:149], v[226:229], v[42:45]
	v_mfma_f32_16x16x32_bf16 v[38:41], v[150:153], v[226:229], v[38:41]
	v_mfma_f32_16x16x32_bf16 v[34:37], v[154:157], v[226:229], v[34:37]
	v_lshl_add_u64 v[166:167], v[132:133], 0, s[36:37]
	global_load_dwordx2 v[194:195], v[166:167], off
	global_load_dwordx2 v[196:197], v[166:167], off offset:2048
	v_mfma_f32_16x16x32_bf16 v[18:21], v[142:145], v[230:233], v[18:21]
	v_mfma_f32_16x16x32_bf16 v[22:25], v[146:149], v[230:233], v[22:25]
	v_mfma_f32_16x16x32_bf16 v[26:29], v[150:153], v[230:233], v[26:29]
	v_mfma_f32_16x16x32_bf16 v[30:33], v[154:157], v[230:233], v[30:33]
	v_lshl_add_u64 v[166:167], v[132:133], 0, s[38:39]
	global_load_dwordx2 v[198:199], v[166:167], off
	global_load_dwordx2 v[200:201], v[166:167], off offset:2048
	s_waitcnt vmcnt(21)
	s_waitcnt lgkmcnt(0)
	s_barrier
	s_mov_b32 s47, s42
	s_mov_b32 s42, s43
	s_mov_b32 s43, s44
	s_mov_b32 s44, s47
	v_mul_f32_e32 v202, s20, v202
	v_mul_f32_e32 v203, s20, v203
	v_mul_f32_e32 v204, s21, v204
	v_mul_f32_e32 v205, s21, v205
	v_mul_f32_e32 v206, s22, v206
	v_mul_f32_e32 v207, s22, v207
	v_mul_f32_e32 v208, s23, v208
	v_mul_f32_e32 v209, s23, v209
	v_mul_f32_e32 v210, s24, v210
	v_mul_f32_e32 v211, s24, v211
	v_mul_f32_e32 v212, s25, v212
	v_mul_f32_e32 v213, s25, v213
	v_mul_f32_e32 v214, s26, v214
	v_mul_f32_e32 v215, s26, v215
	v_mul_f32_e32 v216, s27, v216
	v_mul_f32_e32 v217, s27, v217
	v_cvt_pk_bf16_f32 v158, v202, v204
	v_cvt_pk_bf16_f32 v159, v206, v208
	v_cvt_pk_bf16_f32 v160, v210, v212
	v_cvt_pk_bf16_f32 v161, v214, v216
	v_cvt_pk_bf16_f32 v162, v203, v205
	v_cvt_pk_bf16_f32 v163, v207, v209
	v_cvt_pk_bf16_f32 v164, v211, v213
	v_cvt_pk_bf16_f32 v165, v215, v217
	ds_write_b128 v1, v[158:161] offset:19456
	ds_write_b128 v1, v[162:165] offset:19584
	v_add_u32_e32 v91, s42, v135
	v_add_u32_e32 v93, s42, v137
	ds_read_b128 v[238:241], v139 offset:0
	ds_read_b128 v[242:245], v139 offset:2048
	ds_read_b128 v[246:249], v139 offset:4096
	ds_read_b128 v[250:253], v139 offset:6144
	ds_read_b128 v[218:221], v91 offset:0
	ds_read_b128 v[222:225], v91 offset:2048
	ds_read_b128 v[226:229], v91 offset:4096
	ds_read_b128 v[230:233], v91 offset:6144
	s_add_i32 s47, s44, s6
	s_add_u32 s30, s30, 0x80
	s_addc_u32 s31, s31, 0
	s_waitcnt lgkmcnt(0)
; #define MU_GLDS_A(buf, kt) do { _Pragma("unroll") for (int i = 0; i < NMU; ++i) \
;         __builtin_amdgcn_global_load_lds((const unsigned*)((const char*)A + aoff[i] + (size_t)(kt) * 128), (PG8_LAS unsigned*)(MU_SA(buf) + wid * 1024 + i * 8192), 16, 0, 0); } while (0)
; #define MU_B_ISSUE(sb, kt) do { const char* kb_ = Bb + (size_t)(kt) * (64 * (size_t)RB); _Pragma("unroll") for (int j = 0; j < 8; ++j) { const char* p_ = kb_ + (size_t)j * RB; \
;         asm volatile("global_load_dwordx2 %0, %1, off" : "=&v"(sb[j]) : "v"(p_) : "memory"); } } while (0)
; #define MU_B_WAIT(sb, N) asm volatile("s_waitcnt vmcnt(%8)" : "+v"(sb[0]), "+v"(sb[1]), "+v"(sb[2]), "+v"(sb[3]), "+v"(sb[4]), "+v"(sb[5]), "+v"(sb[6]), "+v"(sb[7]) : "n"(N) : "memory")
; #define MU_COMPUTE(buf) MU_COMPUTE_N(buf, NMU)
; template <int MODE>
; __device__ __forceinline__ void moe_unit(PG8_LAS unsigned char* lds, int e, int cb, int slot0  , int nv  , const bf16_t* A, const int* slot_tok,
;                                          const float* W0, const float* W1, bf16_t* OUT, const float* slot_rs  , const int* slot_dst) {
;     ...
;     f32x4 acc[NMU][4];
; #pragma unroll
;     for (int m = 0; m < NMU; ++m)
; #pragma unroll
;         for (int n = 0; n < 4; ++n) acc[m][n] = (f32x4){0.f, 0.f, 0.f, 0.f};
;     f32x2 s0[8], s1[8];
;     float g0[8];
;     MU_GLDS_A(0, 0); MU_B_ISSUE(s0, 0); MU_G_LOAD(g0, 0); MU_B_ISSUE(s1, 1);
;     MU_B_WAIT(s0, 8); MU_B_WRITE(s0, 0, g0); __builtin_amdgcn_sched_barrier(0); MU_B_ISSUE(s0, 2);
;     asm volatile("s_waitcnt vmcnt(16)" ::: "memory");
;     asm volatile("s_waitcnt lgkmcnt(0)" ::: "memory"); __builtin_amdgcn_s_barrier(); asm volatile("" ::: "memory");
; #pragma unroll 1
;     for (int t = 0; t < nt; t += 2) {
;         if (t + 2 < nt) MU_B_WAIT(s1, 8); else MU_B_WAIT(s1, 0);
;         MU_G_LOAD(g0, t + 1); MU_B_WRITE(s1, 1, g0); __builtin_amdgcn_sched_barrier(0); MU_GLDS_A(1, t + 1); __builtin_amdgcn_sched_barrier(0);
;         if (t + 3 < nt) { MU_B_ISSUE(s1, t + 3); }
;         MU_COMPUTE(0);
;         MU_END(t + 3 >= nt);
;         if (t + 2 < nt) { MU_B_WAIT(s0, 8); MU_G_LOAD(g0, t + 2); MU_B_WRITE(s0, 0, g0); __builtin_amdgcn_sched_barrier(0); MU_GLDS_A(0, t + 2); __builtin_amdgcn_sched_barrier(0); }
;         if (t + 4 < nt) { MU_B_ISSUE(s0, t + 4); }
;         MU_COMPUTE(1);
;         MU_END(t + 4 >= nt);
	v_mfma_f32_16x16x32_bf16 v[78:81], v[238:241], v[218:221], v[78:81]
	v_mfma_f32_16x16x32_bf16 v[74:77], v[242:245], v[218:221], v[74:77]
	v_mfma_f32_16x16x32_bf16 v[70:73], v[246:249], v[218:221], v[70:73]
	v_mfma_f32_16x16x32_bf16 v[66:69], v[250:253], v[218:221], v[66:69]
	ds_read_b128 v[218:221], v93 offset:0
	ds_read_b128 v[142:145], v141 offset:0
	s_mov_b32 m0, s47
	s_nop 0
	global_load_lds_dwordx4 v86, s[30:31]
	v_mfma_f32_16x16x32_bf16 v[62:65], v[238:241], v[222:225], v[62:65]
	v_mfma_f32_16x16x32_bf16 v[58:61], v[242:245], v[222:225], v[58:61]
	v_mfma_f32_16x16x32_bf16 v[54:57], v[246:249], v[222:225], v[54:57]
	v_mfma_f32_16x16x32_bf16 v[50:53], v[250:253], v[222:225], v[50:53]
	ds_read_b128 v[222:225], v93 offset:2048
	ds_read_b128 v[146:149], v141 offset:2048
	s_add_i32 m0, s47, 0x2000
	s_nop 0
	global_load_lds_dwordx4 v134, s[30:31]
	v_mfma_f32_16x16x32_bf16 v[46:49], v[238:241], v[226:229], v[46:49]
	v_mfma_f32_16x16x32_bf16 v[42:45], v[242:245], v[226:229], v[42:45]
	v_mfma_f32_16x16x32_bf16 v[38:41], v[246:249], v[226:229], v[38:41]
	v_mfma_f32_16x16x32_bf16 v[34:37], v[250:253], v[226:229], v[34:37]
	ds_read_b128 v[226:229], v93 offset:4096
	ds_read_b128 v[150:153], v141 offset:4096
	s_add_i32 m0, s47, 0x4000
	s_nop 0
	global_load_lds_dwordx4 v136, s[30:31]
	v_mfma_f32_16x16x32_bf16 v[18:21], v[238:241], v[230:233], v[18:21]
	v_mfma_f32_16x16x32_bf16 v[22:25], v[242:245], v[230:233], v[22:25]
	v_mfma_f32_16x16x32_bf16 v[26:29], v[246:249], v[230:233], v[26:29]
	v_mfma_f32_16x16x32_bf16 v[30:33], v[250:253], v[230:233], v[30:33]
	ds_read_b128 v[230:233], v93 offset:6144
	ds_read_b128 v[154:157], v141 offset:6144
	s_add_i32 m0, s47, 0x6000
	s_nop 0
	global_load_lds_dwordx4 v138, s[30:31]
	s_add_i32 m0, s47, 0x8000
	s_nop 0
	global_load_lds_dwordx4 v140, s[30:31]
	s_waitcnt lgkmcnt(0)
	s_load_dwordx8 s[12:19], s[28:29], 0x0
	s_add_u32 s28, s28, 0x100
	s_addc_u32 s29, s29, 0
	v_mfma_f32_16x16x32_bf16 v[78:81], v[142:145], v[218:221], v[78:81]
	v_mfma_f32_16x16x32_bf16 v[74:77], v[146:149], v[218:221], v[74:77]
	v_mfma_f32_16x16x32_bf16 v[70:73], v[150:153], v[218:221], v[70:73]
	v_mfma_f32_16x16x32_bf16 v[66:69], v[154:157], v[218:221], v[66:69]
	v_lshl_add_u64 v[132:133], v[132:133], 0, s[40:41]
	global_load_dwordx2 v[202:203], v[132:133], off
	global_load_dwordx2 v[204:205], v[132:133], off offset:2048
	v_mfma_f32_16x16x32_bf16 v[62:65], v[142:145], v[222:225], v[62:65]
	v_mfma_f32_16x16x32_bf16 v[58:61], v[146:149], v[222:225], v[58:61]
	v_mfma_f32_16x16x32_bf16 v[54:57], v[150:153], v[222:225], v[54:57]
	v_mfma_f32_16x16x32_bf16 v[50:53], v[154:157], v[222:225], v[50:53]
	v_lshl_add_u64 v[166:167], v[132:133], 0, s[34:35]
	global_load_dwordx2 v[206:207], v[166:167], off
	global_load_dwordx2 v[208:209], v[166:167], off offset:2048
	v_mfma_f32_16x16x32_bf16 v[46:49], v[142:145], v[226:229], v[46:49]
	v_mfma_f32_16x16x32_bf16 v[42:45], v[146:149], v[226:229], v[42:45]
	v_mfma_f32_16x16x32_bf16 v[38:41], v[150:153], v[226:229], v[38:41]
	v_mfma_f32_16x16x32_bf16 v[34:37], v[154:157], v[226:229], v[34:37]
	v_lshl_add_u64 v[166:167], v[132:133], 0, s[36:37]
	global_load_dwordx2 v[210:211], v[166:167], off
	global_load_dwordx2 v[212:213], v[166:167], off offset:2048
	v_mfma_f32_16x16x32_bf16 v[18:21], v[142:145], v[230:233], v[18:21]
	v_mfma_f32_16x16x32_bf16 v[22:25], v[146:149], v[230:233], v[22:25]
	v_mfma_f32_16x16x32_bf16 v[26:29], v[150:153], v[230:233], v[26:29]
	v_mfma_f32_16x16x32_bf16 v[30:33], v[154:157], v[230:233], v[30:33]
	v_lshl_add_u64 v[166:167], v[132:133], 0, s[38:39]
	global_load_dwordx2 v[214:215], v[166:167], off
	global_load_dwordx2 v[216:217], v[166:167], off offset:2048
	s_waitcnt vmcnt(21)
	s_waitcnt lgkmcnt(0)
	s_barrier
	s_mov_b32 s47, s42
	s_mov_b32 s42, s43
	s_mov_b32 s43, s44
	s_mov_b32 s44, s47
	v_mul_f32_e32 v98, s12, v98
	v_mul_f32_e32 v99, s12, v99
	v_mul_f32_e32 v100, s13, v100
	v_mul_f32_e32 v101, s13, v101
	v_mul_f32_e32 v102, s14, v102
	v_mul_f32_e32 v103, s14, v103
	v_mul_f32_e32 v104, s15, v104
	v_mul_f32_e32 v105, s15, v105
	v_mul_f32_e32 v106, s16, v106
	v_mul_f32_e32 v107, s16, v107
	v_mul_f32_e32 v108, s17, v108
	v_mul_f32_e32 v109, s17, v109
	v_mul_f32_e32 v110, s18, v110
	v_mul_f32_e32 v111, s18, v111
	v_mul_f32_e32 v112, s19, v112
	v_mul_f32_e32 v113, s19, v113
	v_cvt_pk_bf16_f32 v158, v98, v100
	v_cvt_pk_bf16_f32 v159, v102, v104
	v_cvt_pk_bf16_f32 v160, v106, v108
	v_cvt_pk_bf16_f32 v161, v110, v112
	v_cvt_pk_bf16_f32 v162, v99, v101
	v_cvt_pk_bf16_f32 v163, v103, v105
	v_cvt_pk_bf16_f32 v164, v107, v109
	v_cvt_pk_bf16_f32 v165, v111, v113
	ds_write_b128 v1, v[158:161] offset:0
	ds_write_b128 v1, v[162:165] offset:128
	v_add_u32_e32 v91, s42, v135
	v_add_u32_e32 v93, s42, v137
	ds_read_b128 v[238:241], v139 offset:19456
	ds_read_b128 v[242:245], v139 offset:21504
	ds_read_b128 v[246:249], v139 offset:23552
	ds_read_b128 v[250:253], v139 offset:25600
	ds_read_b128 v[218:221], v91 offset:0
	ds_read_b128 v[222:225], v91 offset:2048
	ds_read_b128 v[226:229], v91 offset:4096
	ds_read_b128 v[230:233], v91 offset:6144
	s_add_i32 s47, s44, s6
	s_add_u32 s30, s30, 0x80
	s_addc_u32 s31, s31, 0
	s_waitcnt lgkmcnt(0)
; #define MU_GLDS_A(buf, kt) do { _Pragma("unroll") for (int i = 0; i < NMU; ++i) \
;         __builtin_amdgcn_global_load_lds((const unsigned*)((const char*)A + aoff[i] + (size_t)(kt) * 128), (PG8_LAS unsigned*)(MU_SA(buf) + wid * 1024 + i * 8192), 16, 0, 0); } while (0)
; #define MU_B_ISSUE(sb, kt) do { const char* kb_ = Bb + (size_t)(kt) * (64 * (size_t)RB); _Pragma("unroll") for (int j = 0; j < 8; ++j) { const char* p_ = kb_ + (size_t)j * RB; \
;         asm volatile("global_load_dwordx2 %0, %1, off" : "=&v"(sb[j]) : "v"(p_) : "memory"); } } while (0)
; #define MU_B_WAIT(sb, N) asm volatile("s_waitcnt vmcnt(%8)" : "+v"(sb[0]), "+v"(sb[1]), "+v"(sb[2]), "+v"(sb[3]), "+v"(sb[4]), "+v"(sb[5]), "+v"(sb[6]), "+v"(sb[7]) : "n"(N) : "memory")
; #define MU_COMPUTE(buf) MU_COMPUTE_N(buf, NMU)
; template <int MODE>
; __device__ __forceinline__ void moe_unit(PG8_LAS unsigned char* lds, int e, int cb, int slot0  , int nv  , const bf16_t* A, const int* slot_tok,
;                                          const float* W0, const float* W1, bf16_t* OUT, const float* slot_rs  , const int* slot_dst) {
;     ...
;     f32x4 acc[NMU][4];
; #pragma unroll
;     for (int m = 0; m < NMU; ++m)
; #pragma unroll
;         for (int n = 0; n < 4; ++n) acc[m][n] = (f32x4){0.f, 0.f, 0.f, 0.f};
;     f32x2 s0[8], s1[8];
;     float g0[8];
;     MU_GLDS_A(0, 0); MU_B_ISSUE(s0, 0); MU_G_LOAD(g0, 0); MU_B_ISSUE(s1, 1);
;     MU_B_WAIT(s0, 8); MU_B_WRITE(s0, 0, g0); __builtin_amdgcn_sched_barrier(0); MU_B_ISSUE(s0, 2);
;     asm volatile("s_waitcnt vmcnt(16)" ::: "memory");
;     asm volatile("s_waitcnt lgkmcnt(0)" ::: "memory"); __builtin_amdgcn_s_barrier(); asm volatile("" ::: "memory");
; #pragma unroll 1
;     for (int t = 0; t < nt; t += 2) {
;         if (t + 2 < nt) MU_B_WAIT(s1, 8); else MU_B_WAIT(s1, 0);
;         MU_G_LOAD(g0, t + 1); MU_B_WRITE(s1, 1, g0); __builtin_amdgcn_sched_barrier(0); MU_GLDS_A(1, t + 1); __builtin_amdgcn_sched_barrier(0);
;         if (t + 3 < nt) { MU_B_ISSUE(s1, t + 3); }
;         MU_COMPUTE(0);
;         MU_END(t + 3 >= nt);
;         if (t + 2 < nt) { MU_B_WAIT(s0, 8); MU_G_LOAD(g0, t + 2); MU_B_WRITE(s0, 0, g0); __builtin_amdgcn_sched_barrier(0); MU_GLDS_A(0, t + 2); __builtin_amdgcn_sched_barrier(0); }
;         if (t + 4 < nt) { MU_B_ISSUE(s0, t + 4); }
;         MU_COMPUTE(1);
;         MU_END(t + 4 >= nt);
	v_mfma_f32_16x16x32_bf16 v[78:81], v[238:241], v[218:221], v[78:81]
	v_mfma_f32_16x16x32_bf16 v[74:77], v[242:245], v[218:221], v[74:77]
	v_mfma_f32_16x16x32_bf16 v[70:73], v[246:249], v[218:221], v[70:73]
	v_mfma_f32_16x16x32_bf16 v[66:69], v[250:253], v[218:221], v[66:69]
	ds_read_b128 v[218:221], v93 offset:0
	ds_read_b128 v[142:145], v141 offset:19456
	s_mov_b32 m0, s47
	s_nop 0
	global_load_lds_dwordx4 v86, s[30:31]
	v_mfma_f32_16x16x32_bf16 v[62:65], v[238:241], v[222:225], v[62:65]
	v_mfma_f32_16x16x32_bf16 v[58:61], v[242:245], v[222:225], v[58:61]
	v_mfma_f32_16x16x32_bf16 v[54:57], v[246:249], v[222:225], v[54:57]
	v_mfma_f32_16x16x32_bf16 v[50:53], v[250:253], v[222:225], v[50:53]
	ds_read_b128 v[222:225], v93 offset:2048
	ds_read_b128 v[146:149], v141 offset:21504
	s_add_i32 m0, s47, 0x2000
	s_nop 0
	global_load_lds_dwordx4 v134, s[30:31]
	v_mfma_f32_16x16x32_bf16 v[46:49], v[238:241], v[226:229], v[46:49]
	v_mfma_f32_16x16x32_bf16 v[42:45], v[242:245], v[226:229], v[42:45]
	v_mfma_f32_16x16x32_bf16 v[38:41], v[246:249], v[226:229], v[38:41]
	v_mfma_f32_16x16x32_bf16 v[34:37], v[250:253], v[226:229], v[34:37]
	ds_read_b128 v[226:229], v93 offset:4096
	ds_read_b128 v[150:153], v141 offset:23552
	s_add_i32 m0, s47, 0x4000
	s_nop 0
	global_load_lds_dwordx4 v136, s[30:31]
	v_mfma_f32_16x16x32_bf16 v[18:21], v[238:241], v[230:233], v[18:21]
	v_mfma_f32_16x16x32_bf16 v[22:25], v[242:245], v[230:233], v[22:25]
	v_mfma_f32_16x16x32_bf16 v[26:29], v[246:249], v[230:233], v[26:29]
	v_mfma_f32_16x16x32_bf16 v[30:33], v[250:253], v[230:233], v[30:33]
	ds_read_b128 v[230:233], v93 offset:6144
	ds_read_b128 v[154:157], v141 offset:25600
	s_add_i32 m0, s47, 0x6000
	s_nop 0
	global_load_lds_dwordx4 v138, s[30:31]
	s_add_i32 m0, s47, 0x8000
	s_nop 0
	global_load_lds_dwordx4 v140, s[30:31]
	s_waitcnt lgkmcnt(0)
	s_load_dwordx8 s[20:27], s[28:29], 0x0
	s_add_u32 s28, s28, 0x100
	s_addc_u32 s29, s29, 0
	v_mfma_f32_16x16x32_bf16 v[78:81], v[142:145], v[218:221], v[78:81]
	v_mfma_f32_16x16x32_bf16 v[74:77], v[146:149], v[218:221], v[74:77]
	v_mfma_f32_16x16x32_bf16 v[70:73], v[150:153], v[218:221], v[70:73]
	v_mfma_f32_16x16x32_bf16 v[66:69], v[154:157], v[218:221], v[66:69]
	v_lshl_add_u64 v[132:133], v[132:133], 0, s[40:41]
	global_load_dwordx2 v[98:99], v[132:133], off
	global_load_dwordx2 v[100:101], v[132:133], off offset:2048
	v_mfma_f32_16x16x32_bf16 v[62:65], v[142:145], v[222:225], v[62:65]
	v_mfma_f32_16x16x32_bf16 v[58:61], v[146:149], v[222:225], v[58:61]
	v_mfma_f32_16x16x32_bf16 v[54:57], v[150:153], v[222:225], v[54:57]
	v_mfma_f32_16x16x32_bf16 v[50:53], v[154:157], v[222:225], v[50:53]
	v_lshl_add_u64 v[166:167], v[132:133], 0, s[34:35]
	global_load_dwordx2 v[102:103], v[166:167], off
	global_load_dwordx2 v[104:105], v[166:167], off offset:2048
	v_mfma_f32_16x16x32_bf16 v[46:49], v[142:145], v[226:229], v[46:49]
	v_mfma_f32_16x16x32_bf16 v[42:45], v[146:149], v[226:229], v[42:45]
	v_mfma_f32_16x16x32_bf16 v[38:41], v[150:153], v[226:229], v[38:41]
	v_mfma_f32_16x16x32_bf16 v[34:37], v[154:157], v[226:229], v[34:37]
	v_lshl_add_u64 v[166:167], v[132:133], 0, s[36:37]
	global_load_dwordx2 v[106:107], v[166:167], off
	global_load_dwordx2 v[108:109], v[166:167], off offset:2048
	v_mfma_f32_16x16x32_bf16 v[18:21], v[142:145], v[230:233], v[18:21]
	v_mfma_f32_16x16x32_bf16 v[22:25], v[146:149], v[230:233], v[22:25]
	v_mfma_f32_16x16x32_bf16 v[26:29], v[150:153], v[230:233], v[26:29]
	v_mfma_f32_16x16x32_bf16 v[30:33], v[154:157], v[230:233], v[30:33]
	v_lshl_add_u64 v[166:167], v[132:133], 0, s[38:39]
	global_load_dwordx2 v[110:111], v[166:167], off
	global_load_dwordx2 v[112:113], v[166:167], off offset:2048
	s_waitcnt vmcnt(21)
	s_waitcnt lgkmcnt(0)
	s_barrier
	s_mov_b32 s47, s42
	s_mov_b32 s42, s43
	s_mov_b32 s43, s44
	s_mov_b32 s44, s47
	s_sub_u32 s46, s46, 1
	s_cmp_lg_u32 s46, 0
	s_cbranch_scc1 .Lmu_loop_X4
	v_mul_f32_e32 v114, s20, v114
	v_mul_f32_e32 v115, s20, v115
	v_mul_f32_e32 v116, s21, v116
	v_mul_f32_e32 v117, s21, v117
	v_mul_f32_e32 v118, s22, v118
	v_mul_f32_e32 v119, s22, v119
	v_mul_f32_e32 v120, s23, v120
	v_mul_f32_e32 v121, s23, v121
	v_mul_f32_e32 v122, s24, v122
	v_mul_f32_e32 v123, s24, v123
	v_mul_f32_e32 v124, s25, v124
	v_mul_f32_e32 v125, s25, v125
	v_mul_f32_e32 v126, s26, v126
	v_mul_f32_e32 v127, s26, v127
	v_mul_f32_e32 v128, s27, v128
	v_mul_f32_e32 v129, s27, v129
	v_cvt_pk_bf16_f32 v158, v114, v116
	v_cvt_pk_bf16_f32 v159, v118, v120
	v_cvt_pk_bf16_f32 v160, v122, v124
	v_cvt_pk_bf16_f32 v161, v126, v128
	v_cvt_pk_bf16_f32 v162, v115, v117
	v_cvt_pk_bf16_f32 v163, v119, v121
	v_cvt_pk_bf16_f32 v164, v123, v125
	v_cvt_pk_bf16_f32 v165, v127, v129
	ds_write_b128 v1, v[158:161] offset:19456
	ds_write_b128 v1, v[162:165] offset:19584
	v_add_u32_e32 v91, s42, v135
	v_add_u32_e32 v93, s42, v137
	ds_read_b128 v[238:241], v139 offset:0
	ds_read_b128 v[242:245], v139 offset:2048
	ds_read_b128 v[246:249], v139 offset:4096
	ds_read_b128 v[250:253], v139 offset:6144
	ds_read_b128 v[218:221], v91 offset:0
	ds_read_b128 v[222:225], v91 offset:2048
	ds_read_b128 v[226:229], v91 offset:4096
	ds_read_b128 v[230:233], v91 offset:6144
	s_add_i32 s47, s44, s6
	s_add_u32 s30, s30, 0x80
	s_addc_u32 s31, s31, 0
	s_waitcnt lgkmcnt(0)
; #define MU_GLDS_A(buf, kt) do { _Pragma("unroll") for (int i = 0; i < NMU; ++i) \
;         __builtin_amdgcn_global_load_lds((const unsigned*)((const char*)A + aoff[i] + (size_t)(kt) * 128), (PG8_LAS unsigned*)(MU_SA(buf) + wid * 1024 + i * 8192), 16, 0, 0); } while (0)
; #define MU_B_ISSUE(sb, kt) do { const char* kb_ = Bb + (size_t)(kt) * (64 * (size_t)RB); _Pragma("unroll") for (int j = 0; j < 8; ++j) { const char* p_ = kb_ + (size_t)j * RB; \
;         asm volatile("global_load_dwordx2 %0, %1, off" : "=&v"(sb[j]) : "v"(p_) : "memory"); } } while (0)
; #define MU_B_WAIT(sb, N) asm volatile("s_waitcnt vmcnt(%8)" : "+v"(sb[0]), "+v"(sb[1]), "+v"(sb[2]), "+v"(sb[3]), "+v"(sb[4]), "+v"(sb[5]), "+v"(sb[6]), "+v"(sb[7]) : "n"(N) : "memory")
; #define MU_COMPUTE(buf) MU_COMPUTE_N(buf, NMU)
; template <int MODE>
; __device__ __forceinline__ void moe_unit(PG8_LAS unsigned char* lds, int e, int cb, int slot0  , int nv  , const bf16_t* A, const int* slot_tok,
;                                          const float* W0, const float* W1, bf16_t* OUT, const float* slot_rs  , const int* slot_dst) {
;     ...
;     f32x4 acc[NMU][4];
; #pragma unroll
;     for (int m = 0; m < NMU; ++m)
; #pragma unroll
;         for (int n = 0; n < 4; ++n) acc[m][n] = (f32x4){0.f, 0.f, 0.f, 0.f};
;     f32x2 s0[8], s1[8];
;     float g0[8];
;     MU_GLDS_A(0, 0); MU_B_ISSUE(s0, 0); MU_G_LOAD(g0, 0); MU_B_ISSUE(s1, 1);
;     MU_B_WAIT(s0, 8); MU_B_WRITE(s0, 0, g0); __builtin_amdgcn_sched_barrier(0); MU_B_ISSUE(s0, 2);
;     asm volatile("s_waitcnt vmcnt(16)" ::: "memory");
;     asm volatile("s_waitcnt lgkmcnt(0)" ::: "memory"); __builtin_amdgcn_s_barrier(); asm volatile("" ::: "memory");
; #pragma unroll 1
;     for (int t = 0; t < nt; t += 2) {
;         if (t + 2 < nt) MU_B_WAIT(s1, 8); else MU_B_WAIT(s1, 0);
;         MU_G_LOAD(g0, t + 1); MU_B_WRITE(s1, 1, g0); __builtin_amdgcn_sched_barrier(0); MU_GLDS_A(1, t + 1); __builtin_amdgcn_sched_barrier(0);
;         if (t + 3 < nt) { MU_B_ISSUE(s1, t + 3); }
;         MU_COMPUTE(0);
;         MU_END(t + 3 >= nt);
;         if (t + 2 < nt) { MU_B_WAIT(s0, 8); MU_G_LOAD(g0, t + 2); MU_B_WRITE(s0, 0, g0); __builtin_amdgcn_sched_barrier(0); MU_GLDS_A(0, t + 2); __builtin_amdgcn_sched_barrier(0); }
;         if (t + 4 < nt) { MU_B_ISSUE(s0, t + 4); }
;         MU_COMPUTE(1);
;         MU_END(t + 4 >= nt);
	v_mfma_f32_16x16x32_bf16 v[78:81], v[238:241], v[218:221], v[78:81]
	v_mfma_f32_16x16x32_bf16 v[74:77], v[242:245], v[218:221], v[74:77]
	v_mfma_f32_16x16x32_bf16 v[70:73], v[246:249], v[218:221], v[70:73]
	v_mfma_f32_16x16x32_bf16 v[66:69], v[250:253], v[218:221], v[66:69]
	ds_read_b128 v[218:221], v93 offset:0
	ds_read_b128 v[142:145], v141 offset:0
	s_mov_b32 m0, s47
	s_nop 0
	global_load_lds_dwordx4 v86, s[30:31]
	v_mfma_f32_16x16x32_bf16 v[62:65], v[238:241], v[222:225], v[62:65]
	v_mfma_f32_16x16x32_bf16 v[58:61], v[242:245], v[222:225], v[58:61]
	v_mfma_f32_16x16x32_bf16 v[54:57], v[246:249], v[222:225], v[54:57]
	v_mfma_f32_16x16x32_bf16 v[50:53], v[250:253], v[222:225], v[50:53]
	ds_read_b128 v[222:225], v93 offset:2048
	ds_read_b128 v[146:149], v141 offset:2048
	s_add_i32 m0, s47, 0x2000
	s_nop 0
	global_load_lds_dwordx4 v134, s[30:31]
	v_mfma_f32_16x16x32_bf16 v[46:49], v[238:241], v[226:229], v[46:49]
	v_mfma_f32_16x16x32_bf16 v[42:45], v[242:245], v[226:229], v[42:45]
	v_mfma_f32_16x16x32_bf16 v[38:41], v[246:249], v[226:229], v[38:41]
	v_mfma_f32_16x16x32_bf16 v[34:37], v[250:253], v[226:229], v[34:37]
	ds_read_b128 v[226:229], v93 offset:4096
	ds_read_b128 v[150:153], v141 offset:4096
	s_add_i32 m0, s47, 0x4000
	s_nop 0
	global_load_lds_dwordx4 v136, s[30:31]
	v_mfma_f32_16x16x32_bf16 v[18:21], v[238:241], v[230:233], v[18:21]
	v_mfma_f32_16x16x32_bf16 v[22:25], v[242:245], v[230:233], v[22:25]
	v_mfma_f32_16x16x32_bf16 v[26:29], v[246:249], v[230:233], v[26:29]
	v_mfma_f32_16x16x32_bf16 v[30:33], v[250:253], v[230:233], v[30:33]
	ds_read_b128 v[230:233], v93 offset:6144
	ds_read_b128 v[154:157], v141 offset:6144
	s_add_i32 m0, s47, 0x6000
	s_nop 0
	global_load_lds_dwordx4 v138, s[30:31]
	s_add_i32 m0, s47, 0x8000
	s_nop 0
	global_load_lds_dwordx4 v140, s[30:31]
	s_waitcnt lgkmcnt(0)
	s_load_dwordx8 s[12:19], s[28:29], 0x0
	s_add_u32 s28, s28, 0x100
	s_addc_u32 s29, s29, 0
	v_mfma_f32_16x16x32_bf16 v[78:81], v[142:145], v[218:221], v[78:81]
	v_mfma_f32_16x16x32_bf16 v[74:77], v[146:149], v[218:221], v[74:77]
	v_mfma_f32_16x16x32_bf16 v[70:73], v[150:153], v[218:221], v[70:73]
	v_mfma_f32_16x16x32_bf16 v[66:69], v[154:157], v[218:221], v[66:69]
	v_lshl_add_u64 v[132:133], v[132:133], 0, s[40:41]
	global_load_dwordx2 v[114:115], v[132:133], off
	global_load_dwordx2 v[116:117], v[132:133], off offset:2048
	v_mfma_f32_16x16x32_bf16 v[62:65], v[142:145], v[222:225], v[62:65]
	v_mfma_f32_16x16x32_bf16 v[58:61], v[146:149], v[222:225], v[58:61]
	v_mfma_f32_16x16x32_bf16 v[54:57], v[150:153], v[222:225], v[54:57]
	v_mfma_f32_16x16x32_bf16 v[50:53], v[154:157], v[222:225], v[50:53]
	v_lshl_add_u64 v[166:167], v[132:133], 0, s[34:35]
	global_load_dwordx2 v[118:119], v[166:167], off
	global_load_dwordx2 v[120:121], v[166:167], off offset:2048
	v_mfma_f32_16x16x32_bf16 v[46:49], v[142:145], v[226:229], v[46:49]
	v_mfma_f32_16x16x32_bf16 v[42:45], v[146:149], v[226:229], v[42:45]
	v_mfma_f32_16x16x32_bf16 v[38:41], v[150:153], v[226:229], v[38:41]
	v_mfma_f32_16x16x32_bf16 v[34:37], v[154:157], v[226:229], v[34:37]
	v_lshl_add_u64 v[166:167], v[132:133], 0, s[36:37]
	global_load_dwordx2 v[122:123], v[166:167], off
	global_load_dwordx2 v[124:125], v[166:167], off offset:2048
	v_mfma_f32_16x16x32_bf16 v[18:21], v[142:145], v[230:233], v[18:21]
	v_mfma_f32_16x16x32_bf16 v[22:25], v[146:149], v[230:233], v[22:25]
	v_mfma_f32_16x16x32_bf16 v[26:29], v[150:153], v[230:233], v[26:29]
	v_mfma_f32_16x16x32_bf16 v[30:33], v[154:157], v[230:233], v[30:33]
	v_lshl_add_u64 v[166:167], v[132:133], 0, s[38:39]
	global_load_dwordx2 v[126:127], v[166:167], off
	global_load_dwordx2 v[128:129], v[166:167], off offset:2048
	s_waitcnt vmcnt(21)
	s_waitcnt lgkmcnt(0)
	s_barrier
	s_mov_b32 s47, s42
	s_mov_b32 s42, s43
	s_mov_b32 s43, s44
	s_mov_b32 s44, s47
	v_mul_f32_e32 v186, s12, v186
	v_mul_f32_e32 v187, s12, v187
	v_mul_f32_e32 v188, s13, v188
	v_mul_f32_e32 v189, s13, v189
	v_mul_f32_e32 v190, s14, v190
	v_mul_f32_e32 v191, s14, v191
	v_mul_f32_e32 v192, s15, v192
	v_mul_f32_e32 v193, s15, v193
	v_mul_f32_e32 v194, s16, v194
	v_mul_f32_e32 v195, s16, v195
	v_mul_f32_e32 v196, s17, v196
	v_mul_f32_e32 v197, s17, v197
	v_mul_f32_e32 v198, s18, v198
	v_mul_f32_e32 v199, s18, v199
	v_mul_f32_e32 v200, s19, v200
	v_mul_f32_e32 v201, s19, v201
	v_cvt_pk_bf16_f32 v158, v186, v188
	v_cvt_pk_bf16_f32 v159, v190, v192
	v_cvt_pk_bf16_f32 v160, v194, v196
	v_cvt_pk_bf16_f32 v161, v198, v200
	v_cvt_pk_bf16_f32 v162, v187, v189
	v_cvt_pk_bf16_f32 v163, v191, v193
	v_cvt_pk_bf16_f32 v164, v195, v197
	v_cvt_pk_bf16_f32 v165, v199, v201
	ds_write_b128 v1, v[158:161] offset:0
	ds_write_b128 v1, v[162:165] offset:128
	v_add_u32_e32 v91, s42, v135
	v_add_u32_e32 v93, s42, v137
	ds_read_b128 v[238:241], v139 offset:19456
	ds_read_b128 v[242:245], v139 offset:21504
	ds_read_b128 v[246:249], v139 offset:23552
	ds_read_b128 v[250:253], v139 offset:25600
	ds_read_b128 v[218:221], v91 offset:0
	ds_read_b128 v[222:225], v91 offset:2048
	ds_read_b128 v[226:229], v91 offset:4096
	ds_read_b128 v[230:233], v91 offset:6144
	s_add_i32 s47, s44, s6
	s_add_u32 s30, s30, 0x80
	s_addc_u32 s31, s31, 0
	s_waitcnt lgkmcnt(0)
; #define MU_GLDS_A(buf, kt) do { _Pragma("unroll") for (int i = 0; i < NMU; ++i) \
;         __builtin_amdgcn_global_load_lds((const unsigned*)((const char*)A + aoff[i] + (size_t)(kt) * 128), (PG8_LAS unsigned*)(MU_SA(buf) + wid * 1024 + i * 8192), 16, 0, 0); } while (0)
; #define MU_B_ISSUE(sb, kt) do { const char* kb_ = Bb + (size_t)(kt) * (64 * (size_t)RB); _Pragma("unroll") for (int j = 0; j < 8; ++j) { const char* p_ = kb_ + (size_t)j * RB; \
;         asm volatile("global_load_dwordx2 %0, %1, off" : "=&v"(sb[j]) : "v"(p_) : "memory"); } } while (0)
; #define MU_B_WAIT(sb, N) asm volatile("s_waitcnt vmcnt(%8)" : "+v"(sb[0]), "+v"(sb[1]), "+v"(sb[2]), "+v"(sb[3]), "+v"(sb[4]), "+v"(sb[5]), "+v"(sb[6]), "+v"(sb[7]) : "n"(N) : "memory")
; #define MU_COMPUTE(buf) MU_COMPUTE_N(buf, NMU)
; template <int MODE>
; __device__ __forceinline__ void moe_unit(PG8_LAS unsigned char* lds, int e, int cb, int slot0  , int nv  , const bf16_t* A, const int* slot_tok,
;                                          const float* W0, const float* W1, bf16_t* OUT, const float* slot_rs  , const int* slot_dst) {
;     ...
;     f32x4 acc[NMU][4];
; #pragma unroll
;     for (int m = 0; m < NMU; ++m)
; #pragma unroll
;         for (int n = 0; n < 4; ++n) acc[m][n] = (f32x4){0.f, 0.f, 0.f, 0.f};
;     f32x2 s0[8], s1[8];
;     float g0[8];
;     MU_GLDS_A(0, 0); MU_B_ISSUE(s0, 0); MU_G_LOAD(g0, 0); MU_B_ISSUE(s1, 1);
;     MU_B_WAIT(s0, 8); MU_B_WRITE(s0, 0, g0); __builtin_amdgcn_sched_barrier(0); MU_B_ISSUE(s0, 2);
;     asm volatile("s_waitcnt vmcnt(16)" ::: "memory");
;     asm volatile("s_waitcnt lgkmcnt(0)" ::: "memory"); __builtin_amdgcn_s_barrier(); asm volatile("" ::: "memory");
; #pragma unroll 1
;     for (int t = 0; t < nt; t += 2) {
;         if (t + 2 < nt) MU_B_WAIT(s1, 8); else MU_B_WAIT(s1, 0);
;         MU_G_LOAD(g0, t + 1); MU_B_WRITE(s1, 1, g0); __builtin_amdgcn_sched_barrier(0); MU_GLDS_A(1, t + 1); __builtin_amdgcn_sched_barrier(0);
;         if (t + 3 < nt) { MU_B_ISSUE(s1, t + 3); }
;         MU_COMPUTE(0);
;         MU_END(t + 3 >= nt);
;         if (t + 2 < nt) { MU_B_WAIT(s0, 8); MU_G_LOAD(g0, t + 2); MU_B_WRITE(s0, 0, g0); __builtin_amdgcn_sched_barrier(0); MU_GLDS_A(0, t + 2); __builtin_amdgcn_sched_barrier(0); }
;         if (t + 4 < nt) { MU_B_ISSUE(s0, t + 4); }
;         MU_COMPUTE(1);
;         MU_END(t + 4 >= nt);
	v_mfma_f32_16x16x32_bf16 v[78:81], v[238:241], v[218:221], v[78:81]
	v_mfma_f32_16x16x32_bf16 v[74:77], v[242:245], v[218:221], v[74:77]
	v_mfma_f32_16x16x32_bf16 v[70:73], v[246:249], v[218:221], v[70:73]
	v_mfma_f32_16x16x32_bf16 v[66:69], v[250:253], v[218:221], v[66:69]
	ds_read_b128 v[218:221], v93 offset:0
	ds_read_b128 v[142:145], v141 offset:19456
	s_mov_b32 m0, s47
	s_nop 0
	global_load_lds_dwordx4 v86, s[30:31]
	v_mfma_f32_16x16x32_bf16 v[62:65], v[238:241], v[222:225], v[62:65]
	v_mfma_f32_16x16x32_bf16 v[58:61], v[242:245], v[222:225], v[58:61]
	v_mfma_f32_16x16x32_bf16 v[54:57], v[246:249], v[222:225], v[54:57]
	v_mfma_f32_16x16x32_bf16 v[50:53], v[250:253], v[222:225], v[50:53]
	ds_read_b128 v[222:225], v93 offset:2048
	ds_read_b128 v[146:149], v141 offset:21504
	s_add_i32 m0, s47, 0x2000
	s_nop 0
	global_load_lds_dwordx4 v134, s[30:31]
	v_mfma_f32_16x16x32_bf16 v[46:49], v[238:241], v[226:229], v[46:49]
	v_mfma_f32_16x16x32_bf16 v[42:45], v[242:245], v[226:229], v[42:45]
	v_mfma_f32_16x16x32_bf16 v[38:41], v[246:249], v[226:229], v[38:41]
	v_mfma_f32_16x16x32_bf16 v[34:37], v[250:253], v[226:229], v[34:37]
	ds_read_b128 v[226:229], v93 offset:4096
	ds_read_b128 v[150:153], v141 offset:23552
	s_add_i32 m0, s47, 0x4000
	s_nop 0
	global_load_lds_dwordx4 v136, s[30:31]
	v_mfma_f32_16x16x32_bf16 v[18:21], v[238:241], v[230:233], v[18:21]
	v_mfma_f32_16x16x32_bf16 v[22:25], v[242:245], v[230:233], v[22:25]
	v_mfma_f32_16x16x32_bf16 v[26:29], v[246:249], v[230:233], v[26:29]
	v_mfma_f32_16x16x32_bf16 v[30:33], v[250:253], v[230:233], v[30:33]
	ds_read_b128 v[230:233], v93 offset:6144
	ds_read_b128 v[154:157], v141 offset:25600
	s_add_i32 m0, s47, 0x6000
	s_nop 0
	global_load_lds_dwordx4 v138, s[30:31]
	s_add_i32 m0, s47, 0x8000
	s_nop 0
	global_load_lds_dwordx4 v140, s[30:31]
	s_waitcnt lgkmcnt(0)
	s_load_dwordx8 s[20:27], s[28:29], 0x0
	s_add_u32 s28, s28, 0x100
	s_addc_u32 s29, s29, 0
	v_mfma_f32_16x16x32_bf16 v[78:81], v[142:145], v[218:221], v[78:81]
	v_mfma_f32_16x16x32_bf16 v[74:77], v[146:149], v[218:221], v[74:77]
	v_mfma_f32_16x16x32_bf16 v[70:73], v[150:153], v[218:221], v[70:73]
	v_mfma_f32_16x16x32_bf16 v[66:69], v[154:157], v[218:221], v[66:69]
	v_lshl_add_u64 v[132:133], v[132:133], 0, s[40:41]
	global_load_dwordx2 v[186:187], v[132:133], off
	global_load_dwordx2 v[188:189], v[132:133], off offset:2048
	v_mfma_f32_16x16x32_bf16 v[62:65], v[142:145], v[222:225], v[62:65]
	v_mfma_f32_16x16x32_bf16 v[58:61], v[146:149], v[222:225], v[58:61]
	v_mfma_f32_16x16x32_bf16 v[54:57], v[150:153], v[222:225], v[54:57]
	v_mfma_f32_16x16x32_bf16 v[50:53], v[154:157], v[222:225], v[50:53]
	v_lshl_add_u64 v[166:167], v[132:133], 0, s[34:35]
	global_load_dwordx2 v[190:191], v[166:167], off
	global_load_dwordx2 v[192:193], v[166:167], off offset:2048
	v_mfma_f32_16x16x32_bf16 v[46:49], v[142:145], v[226:229], v[46:49]
	v_mfma_f32_16x16x32_bf16 v[42:45], v[146:149], v[226:229], v[42:45]
	v_mfma_f32_16x16x32_bf16 v[38:41], v[150:153], v[226:229], v[38:41]
	v_mfma_f32_16x16x32_bf16 v[34:37], v[154:157], v[226:229], v[34:37]
	v_lshl_add_u64 v[166:167], v[132:133], 0, s[36:37]
	global_load_dwordx2 v[194:195], v[166:167], off
	global_load_dwordx2 v[196:197], v[166:167], off offset:2048
	v_mfma_f32_16x16x32_bf16 v[18:21], v[142:145], v[230:233], v[18:21]
	v_mfma_f32_16x16x32_bf16 v[22:25], v[146:149], v[230:233], v[22:25]
	v_mfma_f32_16x16x32_bf16 v[26:29], v[150:153], v[230:233], v[26:29]
	v_mfma_f32_16x16x32_bf16 v[30:33], v[154:157], v[230:233], v[30:33]
	v_lshl_add_u64 v[166:167], v[132:133], 0, s[38:39]
	global_load_dwordx2 v[198:199], v[166:167], off
	global_load_dwordx2 v[200:201], v[166:167], off offset:2048
	s_waitcnt vmcnt(21)
	s_waitcnt lgkmcnt(0)
	s_barrier
	s_mov_b32 s47, s42
	s_mov_b32 s42, s43
	s_mov_b32 s43, s44
	s_mov_b32 s44, s47
	v_mul_f32_e32 v202, s20, v202
	v_mul_f32_e32 v203, s20, v203
	v_mul_f32_e32 v204, s21, v204
	v_mul_f32_e32 v205, s21, v205
	v_mul_f32_e32 v206, s22, v206
	v_mul_f32_e32 v207, s22, v207
	v_mul_f32_e32 v208, s23, v208
	v_mul_f32_e32 v209, s23, v209
	v_mul_f32_e32 v210, s24, v210
	v_mul_f32_e32 v211, s24, v211
	v_mul_f32_e32 v212, s25, v212
	v_mul_f32_e32 v213, s25, v213
	v_mul_f32_e32 v214, s26, v214
	v_mul_f32_e32 v215, s26, v215
	v_mul_f32_e32 v216, s27, v216
	v_mul_f32_e32 v217, s27, v217
	v_cvt_pk_bf16_f32 v158, v202, v204
	v_cvt_pk_bf16_f32 v159, v206, v208
	v_cvt_pk_bf16_f32 v160, v210, v212
	v_cvt_pk_bf16_f32 v161, v214, v216
	v_cvt_pk_bf16_f32 v162, v203, v205
	v_cvt_pk_bf16_f32 v163, v207, v209
	v_cvt_pk_bf16_f32 v164, v211, v213
	v_cvt_pk_bf16_f32 v165, v215, v217
	ds_write_b128 v1, v[158:161] offset:19456
	ds_write_b128 v1, v[162:165] offset:19584
	v_add_u32_e32 v91, s42, v135
	v_add_u32_e32 v93, s42, v137
	ds_read_b128 v[238:241], v139 offset:0
	ds_read_b128 v[242:245], v139 offset:2048
	ds_read_b128 v[246:249], v139 offset:4096
	ds_read_b128 v[250:253], v139 offset:6144
	ds_read_b128 v[218:221], v91 offset:0
	ds_read_b128 v[222:225], v91 offset:2048
	ds_read_b128 v[226:229], v91 offset:4096
	ds_read_b128 v[230:233], v91 offset:6144
	s_add_i32 s47, s44, s6
	s_add_u32 s30, s30, 0x80
	s_addc_u32 s31, s31, 0
	s_waitcnt lgkmcnt(0)
; #define MU_GLDS_A(buf, kt) do { _Pragma("unroll") for (int i = 0; i < NMU; ++i) \
;         __builtin_amdgcn_global_load_lds((const unsigned*)((const char*)A + aoff[i] + (size_t)(kt) * 128), (PG8_LAS unsigned*)(MU_SA(buf) + wid * 1024 + i * 8192), 16, 0, 0); } while (0)
; #define MU_B_ISSUE(sb, kt) do { const char* kb_ = Bb + (size_t)(kt) * (64 * (size_t)RB); _Pragma("unroll") for (int j = 0; j < 8; ++j) { const char* p_ = kb_ + (size_t)j * RB; \
;         asm volatile("global_load_dwordx2 %0, %1, off" : "=&v"(sb[j]) : "v"(p_) : "memory"); } } while (0)
; #define MU_B_WAIT(sb, N) asm volatile("s_waitcnt vmcnt(%8)" : "+v"(sb[0]), "+v"(sb[1]), "+v"(sb[2]), "+v"(sb[3]), "+v"(sb[4]), "+v"(sb[5]), "+v"(sb[6]), "+v"(sb[7]) : "n"(N) : "memory")
; #define MU_COMPUTE(buf) MU_COMPUTE_N(buf, NMU)
; template <int MODE>
; __device__ __forceinline__ void moe_unit(PG8_LAS unsigned char* lds, int e, int cb, int slot0  , int nv  , const bf16_t* A, const int* slot_tok,
;                                          const float* W0, const float* W1, bf16_t* OUT, const float* slot_rs  , const int* slot_dst) {
;     ...
;     f32x4 acc[NMU][4];
; #pragma unroll
;     for (int m = 0; m < NMU; ++m)
; #pragma unroll
;         for (int n = 0; n < 4; ++n) acc[m][n] = (f32x4){0.f, 0.f, 0.f, 0.f};
;     f32x2 s0[8], s1[8];
;     float g0[8];
;     MU_GLDS_A(0, 0); MU_B_ISSUE(s0, 0); MU_G_LOAD(g0, 0); MU_B_ISSUE(s1, 1);
;     MU_B_WAIT(s0, 8); MU_B_WRITE(s0, 0, g0); __builtin_amdgcn_sched_barrier(0); MU_B_ISSUE(s0, 2);
;     asm volatile("s_waitcnt vmcnt(16)" ::: "memory");
;     asm volatile("s_waitcnt lgkmcnt(0)" ::: "memory"); __builtin_amdgcn_s_barrier(); asm volatile("" ::: "memory");
; #pragma unroll 1
;     for (int t = 0; t < nt; t += 2) {
;         if (t + 2 < nt) MU_B_WAIT(s1, 8); else MU_B_WAIT(s1, 0);
;         MU_G_LOAD(g0, t + 1); MU_B_WRITE(s1, 1, g0); __builtin_amdgcn_sched_barrier(0); MU_GLDS_A(1, t + 1); __builtin_amdgcn_sched_barrier(0);
;         if (t + 3 < nt) { MU_B_ISSUE(s1, t + 3); }
;         MU_COMPUTE(0);
;         MU_END(t + 3 >= nt);
;         if (t + 2 < nt) { MU_B_WAIT(s0, 8); MU_G_LOAD(g0, t + 2); MU_B_WRITE(s0, 0, g0); __builtin_amdgcn_sched_barrier(0); MU_GLDS_A(0, t + 2); __builtin_amdgcn_sched_barrier(0); }
;         if (t + 4 < nt) { MU_B_ISSUE(s0, t + 4); }
;         MU_COMPUTE(1);
;         MU_END(t + 4 >= nt);
	v_mfma_f32_16x16x32_bf16 v[78:81], v[238:241], v[218:221], v[78:81]
	v_mfma_f32_16x16x32_bf16 v[74:77], v[242:245], v[218:221], v[74:77]
	v_mfma_f32_16x16x32_bf16 v[70:73], v[246:249], v[218:221], v[70:73]
	v_mfma_f32_16x16x32_bf16 v[66:69], v[250:253], v[218:221], v[66:69]
	ds_read_b128 v[218:221], v93 offset:0
	ds_read_b128 v[142:145], v141 offset:0
	s_mov_b32 m0, s47
	s_nop 0
	global_load_lds_dwordx4 v86, s[30:31]
	v_mfma_f32_16x16x32_bf16 v[62:65], v[238:241], v[222:225], v[62:65]
	v_mfma_f32_16x16x32_bf16 v[58:61], v[242:245], v[222:225], v[58:61]
	v_mfma_f32_16x16x32_bf16 v[54:57], v[246:249], v[222:225], v[54:57]
	v_mfma_f32_16x16x32_bf16 v[50:53], v[250:253], v[222:225], v[50:53]
	ds_read_b128 v[222:225], v93 offset:2048
	ds_read_b128 v[146:149], v141 offset:2048
	s_add_i32 m0, s47, 0x2000
	s_nop 0
	global_load_lds_dwordx4 v134, s[30:31]
	v_mfma_f32_16x16x32_bf16 v[46:49], v[238:241], v[226:229], v[46:49]
	v_mfma_f32_16x16x32_bf16 v[42:45], v[242:245], v[226:229], v[42:45]
	v_mfma_f32_16x16x32_bf16 v[38:41], v[246:249], v[226:229], v[38:41]
	v_mfma_f32_16x16x32_bf16 v[34:37], v[250:253], v[226:229], v[34:37]
	ds_read_b128 v[226:229], v93 offset:4096
	ds_read_b128 v[150:153], v141 offset:4096
	s_add_i32 m0, s47, 0x4000
	s_nop 0
	global_load_lds_dwordx4 v136, s[30:31]
	v_mfma_f32_16x16x32_bf16 v[18:21], v[238:241], v[230:233], v[18:21]
	v_mfma_f32_16x16x32_bf16 v[22:25], v[242:245], v[230:233], v[22:25]
	v_mfma_f32_16x16x32_bf16 v[26:29], v[246:249], v[230:233], v[26:29]
	v_mfma_f32_16x16x32_bf16 v[30:33], v[250:253], v[230:233], v[30:33]
	ds_read_b128 v[230:233], v93 offset:6144
	ds_read_b128 v[154:157], v141 offset:6144
	s_add_i32 m0, s47, 0x6000
	s_nop 0
	global_load_lds_dwordx4 v138, s[30:31]
	s_add_i32 m0, s47, 0x8000
	s_nop 0
	global_load_lds_dwordx4 v140, s[30:31]
	s_waitcnt lgkmcnt(0)
	s_load_dwordx8 s[12:19], s[28:29], 0x0
	s_add_u32 s28, s28, 0x100
	s_addc_u32 s29, s29, 0
	v_mfma_f32_16x16x32_bf16 v[78:81], v[142:145], v[218:221], v[78:81]
	v_mfma_f32_16x16x32_bf16 v[74:77], v[146:149], v[218:221], v[74:77]
	v_mfma_f32_16x16x32_bf16 v[70:73], v[150:153], v[218:221], v[70:73]
	v_mfma_f32_16x16x32_bf16 v[66:69], v[154:157], v[218:221], v[66:69]
	v_lshl_add_u64 v[132:133], v[132:133], 0, s[40:41]
	global_load_dwordx2 v[202:203], v[132:133], off
	global_load_dwordx2 v[204:205], v[132:133], off offset:2048
	v_mfma_f32_16x16x32_bf16 v[62:65], v[142:145], v[222:225], v[62:65]
	v_mfma_f32_16x16x32_bf16 v[58:61], v[146:149], v[222:225], v[58:61]
	v_mfma_f32_16x16x32_bf16 v[54:57], v[150:153], v[222:225], v[54:57]
	v_mfma_f32_16x16x32_bf16 v[50:53], v[154:157], v[222:225], v[50:53]
	v_lshl_add_u64 v[166:167], v[132:133], 0, s[34:35]
	global_load_dwordx2 v[206:207], v[166:167], off
	global_load_dwordx2 v[208:209], v[166:167], off offset:2048
	v_mfma_f32_16x16x32_bf16 v[46:49], v[142:145], v[226:229], v[46:49]
	v_mfma_f32_16x16x32_bf16 v[42:45], v[146:149], v[226:229], v[42:45]
	v_mfma_f32_16x16x32_bf16 v[38:41], v[150:153], v[226:229], v[38:41]
	v_mfma_f32_16x16x32_bf16 v[34:37], v[154:157], v[226:229], v[34:37]
	v_lshl_add_u64 v[166:167], v[132:133], 0, s[36:37]
	global_load_dwordx2 v[210:211], v[166:167], off
	global_load_dwordx2 v[212:213], v[166:167], off offset:2048
	v_mfma_f32_16x16x32_bf16 v[18:21], v[142:145], v[230:233], v[18:21]
	v_mfma_f32_16x16x32_bf16 v[22:25], v[146:149], v[230:233], v[22:25]
	v_mfma_f32_16x16x32_bf16 v[26:29], v[150:153], v[230:233], v[26:29]
	v_mfma_f32_16x16x32_bf16 v[30:33], v[154:157], v[230:233], v[30:33]
	v_lshl_add_u64 v[166:167], v[132:133], 0, s[38:39]
	global_load_dwordx2 v[214:215], v[166:167], off
	global_load_dwordx2 v[216:217], v[166:167], off offset:2048
	s_waitcnt vmcnt(21)
	s_waitcnt lgkmcnt(0)
	s_barrier
	s_mov_b32 s47, s42
	s_mov_b32 s42, s43
	s_mov_b32 s43, s44
	s_mov_b32 s44, s47
	v_mul_f32_e32 v98, s12, v98
	v_mul_f32_e32 v99, s12, v99
	v_mul_f32_e32 v100, s13, v100
	v_mul_f32_e32 v101, s13, v101
	v_mul_f32_e32 v102, s14, v102
	v_mul_f32_e32 v103, s14, v103
	v_mul_f32_e32 v104, s15, v104
	v_mul_f32_e32 v105, s15, v105
	v_mul_f32_e32 v106, s16, v106
	v_mul_f32_e32 v107, s16, v107
	v_mul_f32_e32 v108, s17, v108
	v_mul_f32_e32 v109, s17, v109
	v_mul_f32_e32 v110, s18, v110
	v_mul_f32_e32 v111, s18, v111
	v_mul_f32_e32 v112, s19, v112
	v_mul_f32_e32 v113, s19, v113
	v_cvt_pk_bf16_f32 v158, v98, v100
	v_cvt_pk_bf16_f32 v159, v102, v104
	v_cvt_pk_bf16_f32 v160, v106, v108
	v_cvt_pk_bf16_f32 v161, v110, v112
	v_cvt_pk_bf16_f32 v162, v99, v101
	v_cvt_pk_bf16_f32 v163, v103, v105
	v_cvt_pk_bf16_f32 v164, v107, v109
	v_cvt_pk_bf16_f32 v165, v111, v113
	ds_write_b128 v1, v[158:161] offset:0
	ds_write_b128 v1, v[162:165] offset:128
	v_add_u32_e32 v91, s42, v135
	v_add_u32_e32 v93, s42, v137
	ds_read_b128 v[238:241], v139 offset:19456
	ds_read_b128 v[242:245], v139 offset:21504
	ds_read_b128 v[246:249], v139 offset:23552
	ds_read_b128 v[250:253], v139 offset:25600
	ds_read_b128 v[218:221], v91 offset:0
	ds_read_b128 v[222:225], v91 offset:2048
	ds_read_b128 v[226:229], v91 offset:4096
	ds_read_b128 v[230:233], v91 offset:6144
	s_add_i32 s47, s44, s6
	s_add_u32 s30, s30, 0x80
	s_addc_u32 s31, s31, 0
	s_waitcnt lgkmcnt(0)
; #define MU_GLDS_A(buf, kt) do { _Pragma("unroll") for (int i = 0; i < NMU; ++i) \
;         __builtin_amdgcn_global_load_lds((const unsigned*)((const char*)A + aoff[i] + (size_t)(kt) * 128), (PG8_LAS unsigned*)(MU_SA(buf) + wid * 1024 + i * 8192), 16, 0, 0); } while (0)
; #define MU_B_ISSUE(sb, kt) do { const char* kb_ = Bb + (size_t)(kt) * (64 * (size_t)RB); _Pragma("unroll") for (int j = 0; j < 8; ++j) { const char* p_ = kb_ + (size_t)j * RB; \
;         asm volatile("global_load_dwordx2 %0, %1, off" : "=&v"(sb[j]) : "v"(p_) : "memory"); } } while (0)
; #define MU_B_WAIT(sb, N) asm volatile("s_waitcnt vmcnt(%8)" : "+v"(sb[0]), "+v"(sb[1]), "+v"(sb[2]), "+v"(sb[3]), "+v"(sb[4]), "+v"(sb[5]), "+v"(sb[6]), "+v"(sb[7]) : "n"(N) : "memory")
; #define MU_COMPUTE(buf) MU_COMPUTE_N(buf, NMU)
; template <int MODE>
; __device__ __forceinline__ void moe_unit(PG8_LAS unsigned char* lds, int e, int cb, int slot0  , int nv  , const bf16_t* A, const int* slot_tok,
;                                          const float* W0, const float* W1, bf16_t* OUT, const float* slot_rs  , const int* slot_dst) {
;     ...
;     f32x4 acc[NMU][4];
; #pragma unroll
;     for (int m = 0; m < NMU; ++m)
; #pragma unroll
;         for (int n = 0; n < 4; ++n) acc[m][n] = (f32x4){0.f, 0.f, 0.f, 0.f};
;     f32x2 s0[8], s1[8];
;     float g0[8];
;     MU_GLDS_A(0, 0); MU_B_ISSUE(s0, 0); MU_G_LOAD(g0, 0); MU_B_ISSUE(s1, 1);
;     MU_B_WAIT(s0, 8); MU_B_WRITE(s0, 0, g0); __builtin_amdgcn_sched_barrier(0); MU_B_ISSUE(s0, 2);
;     asm volatile("s_waitcnt vmcnt(16)" ::: "memory");
;     asm volatile("s_waitcnt lgkmcnt(0)" ::: "memory"); __builtin_amdgcn_s_barrier(); asm volatile("" ::: "memory");
; #pragma unroll 1
;     for (int t = 0; t < nt; t += 2) {
;         if (t + 2 < nt) MU_B_WAIT(s1, 8); else MU_B_WAIT(s1, 0);
;         MU_G_LOAD(g0, t + 1); MU_B_WRITE(s1, 1, g0); __builtin_amdgcn_sched_barrier(0); MU_GLDS_A(1, t + 1); __builtin_amdgcn_sched_barrier(0);
;         if (t + 3 < nt) { MU_B_ISSUE(s1, t + 3); }
;         MU_COMPUTE(0);
;         MU_END(t + 3 >= nt);
;         if (t + 2 < nt) { MU_B_WAIT(s0, 8); MU_G_LOAD(g0, t + 2); MU_B_WRITE(s0, 0, g0); __builtin_amdgcn_sched_barrier(0); MU_GLDS_A(0, t + 2); __builtin_amdgcn_sched_barrier(0); }
;         if (t + 4 < nt) { MU_B_ISSUE(s0, t + 4); }
;         MU_COMPUTE(1);
;         MU_END(t + 4 >= nt);
	v_mfma_f32_16x16x32_bf16 v[78:81], v[238:241], v[218:221], v[78:81]
	v_mfma_f32_16x16x32_bf16 v[74:77], v[242:245], v[218:221], v[74:77]
	v_mfma_f32_16x16x32_bf16 v[70:73], v[246:249], v[218:221], v[70:73]
	v_mfma_f32_16x16x32_bf16 v[66:69], v[250:253], v[218:221], v[66:69]
	ds_read_b128 v[218:221], v93 offset:0
	ds_read_b128 v[142:145], v141 offset:19456
	s_mov_b32 m0, s47
	s_nop 0
	global_load_lds_dwordx4 v86, s[30:31]
	v_mfma_f32_16x16x32_bf16 v[62:65], v[238:241], v[222:225], v[62:65]
	v_mfma_f32_16x16x32_bf16 v[58:61], v[242:245], v[222:225], v[58:61]
	v_mfma_f32_16x16x32_bf16 v[54:57], v[246:249], v[222:225], v[54:57]
	v_mfma_f32_16x16x32_bf16 v[50:53], v[250:253], v[222:225], v[50:53]
	ds_read_b128 v[222:225], v93 offset:2048
	ds_read_b128 v[146:149], v141 offset:21504
	s_add_i32 m0, s47, 0x2000
	s_nop 0
	global_load_lds_dwordx4 v134, s[30:31]
	v_mfma_f32_16x16x32_bf16 v[46:49], v[238:241], v[226:229], v[46:49]
	v_mfma_f32_16x16x32_bf16 v[42:45], v[242:245], v[226:229], v[42:45]
	v_mfma_f32_16x16x32_bf16 v[38:41], v[246:249], v[226:229], v[38:41]
	v_mfma_f32_16x16x32_bf16 v[34:37], v[250:253], v[226:229], v[34:37]
	ds_read_b128 v[226:229], v93 offset:4096
	ds_read_b128 v[150:153], v141 offset:23552
	s_add_i32 m0, s47, 0x4000
	s_nop 0
	global_load_lds_dwordx4 v136, s[30:31]
	v_mfma_f32_16x16x32_bf16 v[18:21], v[238:241], v[230:233], v[18:21]
	v_mfma_f32_16x16x32_bf16 v[22:25], v[242:245], v[230:233], v[22:25]
	v_mfma_f32_16x16x32_bf16 v[26:29], v[246:249], v[230:233], v[26:29]
	v_mfma_f32_16x16x32_bf16 v[30:33], v[250:253], v[230:233], v[30:33]
	ds_read_b128 v[230:233], v93 offset:6144
	ds_read_b128 v[154:157], v141 offset:25600
	s_add_i32 m0, s47, 0x6000
	s_nop 0
	global_load_lds_dwordx4 v138, s[30:31]
	s_add_i32 m0, s47, 0x8000
	s_nop 0
	global_load_lds_dwordx4 v140, s[30:31]
	s_waitcnt lgkmcnt(0)
	s_load_dwordx8 s[20:27], s[28:29], 0x0
	s_add_u32 s28, s28, 0x100
	s_addc_u32 s29, s29, 0
	v_mfma_f32_16x16x32_bf16 v[78:81], v[142:145], v[218:221], v[78:81]
	v_mfma_f32_16x16x32_bf16 v[74:77], v[146:149], v[218:221], v[74:77]
	v_mfma_f32_16x16x32_bf16 v[70:73], v[150:153], v[218:221], v[70:73]
	v_mfma_f32_16x16x32_bf16 v[66:69], v[154:157], v[218:221], v[66:69]
	v_mfma_f32_16x16x32_bf16 v[62:65], v[142:145], v[222:225], v[62:65]
	v_mfma_f32_16x16x32_bf16 v[58:61], v[146:149], v[222:225], v[58:61]
	v_mfma_f32_16x16x32_bf16 v[54:57], v[150:153], v[222:225], v[54:57]
	v_mfma_f32_16x16x32_bf16 v[50:53], v[154:157], v[222:225], v[50:53]
	v_mfma_f32_16x16x32_bf16 v[46:49], v[142:145], v[226:229], v[46:49]
	v_mfma_f32_16x16x32_bf16 v[42:45], v[146:149], v[226:229], v[42:45]
	v_mfma_f32_16x16x32_bf16 v[38:41], v[150:153], v[226:229], v[38:41]
	v_mfma_f32_16x16x32_bf16 v[34:37], v[154:157], v[226:229], v[34:37]
	v_mfma_f32_16x16x32_bf16 v[18:21], v[142:145], v[230:233], v[18:21]
	v_mfma_f32_16x16x32_bf16 v[22:25], v[146:149], v[230:233], v[22:25]
	v_mfma_f32_16x16x32_bf16 v[26:29], v[150:153], v[230:233], v[26:29]
	v_mfma_f32_16x16x32_bf16 v[30:33], v[154:157], v[230:233], v[30:33]
	s_waitcnt vmcnt(13)
	s_waitcnt lgkmcnt(0)
	s_barrier
	s_mov_b32 s47, s42
	s_mov_b32 s42, s43
	s_mov_b32 s43, s44
	s_mov_b32 s44, s47
	v_mul_f32_e32 v114, s20, v114
	v_mul_f32_e32 v115, s20, v115
	v_mul_f32_e32 v116, s21, v116
	v_mul_f32_e32 v117, s21, v117
	v_mul_f32_e32 v118, s22, v118
	v_mul_f32_e32 v119, s22, v119
	v_mul_f32_e32 v120, s23, v120
	v_mul_f32_e32 v121, s23, v121
	v_mul_f32_e32 v122, s24, v122
	v_mul_f32_e32 v123, s24, v123
	v_mul_f32_e32 v124, s25, v124
	v_mul_f32_e32 v125, s25, v125
	v_mul_f32_e32 v126, s26, v126
	v_mul_f32_e32 v127, s26, v127
	v_mul_f32_e32 v128, s27, v128
	v_mul_f32_e32 v129, s27, v129
	v_cvt_pk_bf16_f32 v158, v114, v116
	v_cvt_pk_bf16_f32 v159, v118, v120
	v_cvt_pk_bf16_f32 v160, v122, v124
	v_cvt_pk_bf16_f32 v161, v126, v128
	v_cvt_pk_bf16_f32 v162, v115, v117
	v_cvt_pk_bf16_f32 v163, v119, v121
	v_cvt_pk_bf16_f32 v164, v123, v125
	v_cvt_pk_bf16_f32 v165, v127, v129
	ds_write_b128 v1, v[158:161] offset:19456
	ds_write_b128 v1, v[162:165] offset:19584
	v_add_u32_e32 v91, s42, v135
	v_add_u32_e32 v93, s42, v137
	ds_read_b128 v[238:241], v139 offset:0
	ds_read_b128 v[242:245], v139 offset:2048
	ds_read_b128 v[246:249], v139 offset:4096
	ds_read_b128 v[250:253], v139 offset:6144
	ds_read_b128 v[218:221], v91 offset:0
	ds_read_b128 v[222:225], v91 offset:2048
	ds_read_b128 v[226:229], v91 offset:4096
	ds_read_b128 v[230:233], v91 offset:6144
	s_add_i32 s47, s44, s6
	s_add_u32 s30, s30, 0x80
	s_addc_u32 s31, s31, 0
	s_waitcnt lgkmcnt(0)
	v_mfma_f32_16x16x32_bf16 v[78:81], v[238:241], v[218:221], v[78:81]
	v_mfma_f32_16x16x32_bf16 v[74:77], v[242:245], v[218:221], v[74:77]
	v_mfma_f32_16x16x32_bf16 v[70:73], v[246:249], v[218:221], v[70:73]
	v_mfma_f32_16x16x32_bf16 v[66:69], v[250:253], v[218:221], v[66:69]
	ds_read_b128 v[218:221], v93 offset:0
	ds_read_b128 v[142:145], v141 offset:0
	s_mov_b32 m0, s47
	s_nop 0
	global_load_lds_dwordx4 v86, s[30:31]
	v_mfma_f32_16x16x32_bf16 v[62:65], v[238:241], v[222:225], v[62:65]
	v_mfma_f32_16x16x32_bf16 v[58:61], v[242:245], v[222:225], v[58:61]
	v_mfma_f32_16x16x32_bf16 v[54:57], v[246:249], v[222:225], v[54:57]
	v_mfma_f32_16x16x32_bf16 v[50:53], v[250:253], v[222:225], v[50:53]
	ds_read_b128 v[222:225], v93 offset:2048
	ds_read_b128 v[146:149], v141 offset:2048
	s_add_i32 m0, s47, 0x2000
	s_nop 0
	global_load_lds_dwordx4 v134, s[30:31]
	v_mfma_f32_16x16x32_bf16 v[46:49], v[238:241], v[226:229], v[46:49]
	v_mfma_f32_16x16x32_bf16 v[42:45], v[242:245], v[226:229], v[42:45]
	v_mfma_f32_16x16x32_bf16 v[38:41], v[246:249], v[226:229], v[38:41]
	v_mfma_f32_16x16x32_bf16 v[34:37], v[250:253], v[226:229], v[34:37]
	ds_read_b128 v[226:229], v93 offset:4096
	ds_read_b128 v[150:153], v141 offset:4096
	s_add_i32 m0, s47, 0x4000
	s_nop 0
	global_load_lds_dwordx4 v136, s[30:31]
	v_mfma_f32_16x16x32_bf16 v[18:21], v[238:241], v[230:233], v[18:21]
	v_mfma_f32_16x16x32_bf16 v[22:25], v[242:245], v[230:233], v[22:25]
	v_mfma_f32_16x16x32_bf16 v[26:29], v[246:249], v[230:233], v[26:29]
	v_mfma_f32_16x16x32_bf16 v[30:33], v[250:253], v[230:233], v[30:33]
	ds_read_b128 v[230:233], v93 offset:6144
	ds_read_b128 v[154:157], v141 offset:6144
	s_add_i32 m0, s47, 0x6000
	s_nop 0
	global_load_lds_dwordx4 v138, s[30:31]
	s_add_i32 m0, s47, 0x8000
	s_nop 0
	global_load_lds_dwordx4 v140, s[30:31]
	s_waitcnt lgkmcnt(0)
; #define MU_GLDS_A(buf, kt) do { _Pragma("unroll") for (int i = 0; i < NMU; ++i) \
;         __builtin_amdgcn_global_load_lds((const unsigned*)((const char*)A + aoff[i] + (size_t)(kt) * 128), (PG8_LAS unsigned*)(MU_SA(buf) + wid * 1024 + i * 8192), 16, 0, 0); } while (0)
; #define MU_B_ISSUE(sb, kt) do { const char* kb_ = Bb + (size_t)(kt) * (64 * (size_t)RB); _Pragma("unroll") for (int j = 0; j < 8; ++j) { const char* p_ = kb_ + (size_t)j * RB; \
;         asm volatile("global_load_dwordx2 %0, %1, off" : "=&v"(sb[j]) : "v"(p_) : "memory"); } } while (0)
; #define MU_B_WAIT(sb, N) asm volatile("s_waitcnt vmcnt(%8)" : "+v"(sb[0]), "+v"(sb[1]), "+v"(sb[2]), "+v"(sb[3]), "+v"(sb[4]), "+v"(sb[5]), "+v"(sb[6]), "+v"(sb[7]) : "n"(N) : "memory")
; #define MU_COMPUTE(buf) MU_COMPUTE_N(buf, NMU)
; template <int MODE>
; __device__ __forceinline__ void moe_unit(PG8_LAS unsigned char* lds, int e, int cb, int slot0  , int nv  , const bf16_t* A, const int* slot_tok,
;                                          const float* W0, const float* W1, bf16_t* OUT, const float* slot_rs  , const int* slot_dst) {
;     ...
;     f32x4 acc[NMU][4];
; #pragma unroll
;     for (int m = 0; m < NMU; ++m)
; #pragma unroll
;         for (int n = 0; n < 4; ++n) acc[m][n] = (f32x4){0.f, 0.f, 0.f, 0.f};
;     f32x2 s0[8], s1[8];
;     float g0[8];
;     MU_GLDS_A(0, 0); MU_B_ISSUE(s0, 0); MU_G_LOAD(g0, 0); MU_B_ISSUE(s1, 1);
;     MU_B_WAIT(s0, 8); MU_B_WRITE(s0, 0, g0); __builtin_amdgcn_sched_barrier(0); MU_B_ISSUE(s0, 2);
;     asm volatile("s_waitcnt vmcnt(16)" ::: "memory");
;     asm volatile("s_waitcnt lgkmcnt(0)" ::: "memory"); __builtin_amdgcn_s_barrier(); asm volatile("" ::: "memory");
; #pragma unroll 1
;     for (int t = 0; t < nt; t += 2) {
;         if (t + 2 < nt) MU_B_WAIT(s1, 8); else MU_B_WAIT(s1, 0);
;         MU_G_LOAD(g0, t + 1); MU_B_WRITE(s1, 1, g0); __builtin_amdgcn_sched_barrier(0); MU_GLDS_A(1, t + 1); __builtin_amdgcn_sched_barrier(0);
;         if (t + 3 < nt) { MU_B_ISSUE(s1, t + 3); }
;         MU_COMPUTE(0);
;         MU_END(t + 3 >= nt);
;         if (t + 2 < nt) { MU_B_WAIT(s0, 8); MU_G_LOAD(g0, t + 2); MU_B_WRITE(s0, 0, g0); __builtin_amdgcn_sched_barrier(0); MU_GLDS_A(0, t + 2); __builtin_amdgcn_sched_barrier(0); }
;         if (t + 4 < nt) { MU_B_ISSUE(s0, t + 4); }
;         MU_COMPUTE(1);
;         MU_END(t + 4 >= nt);
	s_load_dwordx8 s[12:19], s[28:29], 0x0
	s_add_u32 s28, s28, 0x100
	s_addc_u32 s29, s29, 0
	v_mfma_f32_16x16x32_bf16 v[78:81], v[142:145], v[218:221], v[78:81]
	v_mfma_f32_16x16x32_bf16 v[74:77], v[146:149], v[218:221], v[74:77]
	v_mfma_f32_16x16x32_bf16 v[70:73], v[150:153], v[218:221], v[70:73]
	v_mfma_f32_16x16x32_bf16 v[66:69], v[154:157], v[218:221], v[66:69]
	v_mfma_f32_16x16x32_bf16 v[62:65], v[142:145], v[222:225], v[62:65]
	v_mfma_f32_16x16x32_bf16 v[58:61], v[146:149], v[222:225], v[58:61]
	v_mfma_f32_16x16x32_bf16 v[54:57], v[150:153], v[222:225], v[54:57]
	v_mfma_f32_16x16x32_bf16 v[50:53], v[154:157], v[222:225], v[50:53]
	v_mfma_f32_16x16x32_bf16 v[46:49], v[142:145], v[226:229], v[46:49]
	v_mfma_f32_16x16x32_bf16 v[42:45], v[146:149], v[226:229], v[42:45]
	v_mfma_f32_16x16x32_bf16 v[38:41], v[150:153], v[226:229], v[38:41]
	v_mfma_f32_16x16x32_bf16 v[34:37], v[154:157], v[226:229], v[34:37]
	v_mfma_f32_16x16x32_bf16 v[18:21], v[142:145], v[230:233], v[18:21]
	v_mfma_f32_16x16x32_bf16 v[22:25], v[146:149], v[230:233], v[22:25]
	v_mfma_f32_16x16x32_bf16 v[26:29], v[150:153], v[230:233], v[26:29]
	v_mfma_f32_16x16x32_bf16 v[30:33], v[154:157], v[230:233], v[30:33]
	s_waitcnt vmcnt(5)
	s_waitcnt lgkmcnt(0)
	s_barrier
	s_mov_b32 s47, s42
	s_mov_b32 s42, s43
	s_mov_b32 s43, s44
	s_mov_b32 s44, s47
	v_mul_f32_e32 v186, s12, v186
	v_mul_f32_e32 v187, s12, v187
	v_mul_f32_e32 v188, s13, v188
	v_mul_f32_e32 v189, s13, v189
	v_mul_f32_e32 v190, s14, v190
	v_mul_f32_e32 v191, s14, v191
	v_mul_f32_e32 v192, s15, v192
	v_mul_f32_e32 v193, s15, v193
	v_mul_f32_e32 v194, s16, v194
	v_mul_f32_e32 v195, s16, v195
	v_mul_f32_e32 v196, s17, v196
	v_mul_f32_e32 v197, s17, v197
	v_mul_f32_e32 v198, s18, v198
	v_mul_f32_e32 v199, s18, v199
	v_mul_f32_e32 v200, s19, v200
	v_mul_f32_e32 v201, s19, v201
	v_cvt_pk_bf16_f32 v158, v186, v188
	v_cvt_pk_bf16_f32 v159, v190, v192
	v_cvt_pk_bf16_f32 v160, v194, v196
	v_cvt_pk_bf16_f32 v161, v198, v200
	v_cvt_pk_bf16_f32 v162, v187, v189
	v_cvt_pk_bf16_f32 v163, v191, v193
	v_cvt_pk_bf16_f32 v164, v195, v197
	v_cvt_pk_bf16_f32 v165, v199, v201
	ds_write_b128 v1, v[158:161] offset:0
	ds_write_b128 v1, v[162:165] offset:128
	v_add_u32_e32 v91, s42, v135
	v_add_u32_e32 v93, s42, v137
	ds_read_b128 v[238:241], v139 offset:19456
	ds_read_b128 v[242:245], v139 offset:21504
	ds_read_b128 v[246:249], v139 offset:23552
	ds_read_b128 v[250:253], v139 offset:25600
	ds_read_b128 v[218:221], v91 offset:0
	ds_read_b128 v[222:225], v91 offset:2048
	ds_read_b128 v[226:229], v91 offset:4096
	ds_read_b128 v[230:233], v91 offset:6144
	s_add_i32 s47, s44, s6
	s_add_u32 s30, s30, 0x80
	s_addc_u32 s31, s31, 0
	s_waitcnt lgkmcnt(0)
	v_mfma_f32_16x16x32_bf16 v[78:81], v[238:241], v[218:221], v[78:81]
	v_mfma_f32_16x16x32_bf16 v[74:77], v[242:245], v[218:221], v[74:77]
	v_mfma_f32_16x16x32_bf16 v[70:73], v[246:249], v[218:221], v[70:73]
	v_mfma_f32_16x16x32_bf16 v[66:69], v[250:253], v[218:221], v[66:69]
	ds_read_b128 v[218:221], v93 offset:0
	ds_read_b128 v[142:145], v141 offset:19456
	s_mov_b32 m0, s47
	s_nop 0
	global_load_lds_dwordx4 v86, s[30:31]
	v_mfma_f32_16x16x32_bf16 v[62:65], v[238:241], v[222:225], v[62:65]
	v_mfma_f32_16x16x32_bf16 v[58:61], v[242:245], v[222:225], v[58:61]
	v_mfma_f32_16x16x32_bf16 v[54:57], v[246:249], v[222:225], v[54:57]
	v_mfma_f32_16x16x32_bf16 v[50:53], v[250:253], v[222:225], v[50:53]
	ds_read_b128 v[222:225], v93 offset:2048
	ds_read_b128 v[146:149], v141 offset:21504
	s_add_i32 m0, s47, 0x2000
	s_nop 0
	global_load_lds_dwordx4 v134, s[30:31]
	v_mfma_f32_16x16x32_bf16 v[46:49], v[238:241], v[226:229], v[46:49]
	v_mfma_f32_16x16x32_bf16 v[42:45], v[242:245], v[226:229], v[42:45]
	v_mfma_f32_16x16x32_bf16 v[38:41], v[246:249], v[226:229], v[38:41]
	v_mfma_f32_16x16x32_bf16 v[34:37], v[250:253], v[226:229], v[34:37]
	ds_read_b128 v[226:229], v93 offset:4096
	ds_read_b128 v[150:153], v141 offset:23552
	s_add_i32 m0, s47, 0x4000
	s_nop 0
	global_load_lds_dwordx4 v136, s[30:31]
	v_mfma_f32_16x16x32_bf16 v[18:21], v[238:241], v[230:233], v[18:21]
	v_mfma_f32_16x16x32_bf16 v[22:25], v[242:245], v[230:233], v[22:25]
	v_mfma_f32_16x16x32_bf16 v[26:29], v[246:249], v[230:233], v[26:29]
	v_mfma_f32_16x16x32_bf16 v[30:33], v[250:253], v[230:233], v[30:33]
	ds_read_b128 v[230:233], v93 offset:6144
	ds_read_b128 v[154:157], v141 offset:25600
	s_add_i32 m0, s47, 0x6000
	s_nop 0
	global_load_lds_dwordx4 v138, s[30:31]
	s_add_i32 m0, s47, 0x8000
	s_nop 0
	global_load_lds_dwordx4 v140, s[30:31]
	s_waitcnt lgkmcnt(0)
	s_load_dwordx8 s[20:27], s[28:29], 0x0
	s_add_u32 s28, s28, 0x100
	s_addc_u32 s29, s29, 0
	v_mfma_f32_16x16x32_bf16 v[78:81], v[142:145], v[218:221], v[78:81]
	v_mfma_f32_16x16x32_bf16 v[74:77], v[146:149], v[218:221], v[74:77]
	v_mfma_f32_16x16x32_bf16 v[70:73], v[150:153], v[218:221], v[70:73]
	v_mfma_f32_16x16x32_bf16 v[66:69], v[154:157], v[218:221], v[66:69]
	v_mfma_f32_16x16x32_bf16 v[62:65], v[142:145], v[222:225], v[62:65]
	v_mfma_f32_16x16x32_bf16 v[58:61], v[146:149], v[222:225], v[58:61]
	v_mfma_f32_16x16x32_bf16 v[54:57], v[150:153], v[222:225], v[54:57]
	v_mfma_f32_16x16x32_bf16 v[50:53], v[154:157], v[222:225], v[50:53]
	v_mfma_f32_16x16x32_bf16 v[46:49], v[142:145], v[226:229], v[46:49]
	v_mfma_f32_16x16x32_bf16 v[42:45], v[146:149], v[226:229], v[42:45]
	v_mfma_f32_16x16x32_bf16 v[38:41], v[150:153], v[226:229], v[38:41]
	v_mfma_f32_16x16x32_bf16 v[34:37], v[154:157], v[226:229], v[34:37]
	v_mfma_f32_16x16x32_bf16 v[18:21], v[142:145], v[230:233], v[18:21]
	v_mfma_f32_16x16x32_bf16 v[22:25], v[146:149], v[230:233], v[22:25]
	v_mfma_f32_16x16x32_bf16 v[26:29], v[150:153], v[230:233], v[26:29]
	v_mfma_f32_16x16x32_bf16 v[30:33], v[154:157], v[230:233], v[30:33]
	s_waitcnt vmcnt(5)
	s_waitcnt lgkmcnt(0)
	s_barrier
; #define MU_GLDS_A(buf, kt) do { _Pragma("unroll") for (int i = 0; i < NMU; ++i) \
;         __builtin_amdgcn_global_load_lds((const unsigned*)((const char*)A + aoff[i] + (size_t)(kt) * 128), (PG8_LAS unsigned*)(MU_SA(buf) + wid * 1024 + i * 8192), 16, 0, 0); } while (0)
; #define MU_B_ISSUE(sb, kt) do { const char* kb_ = Bb + (size_t)(kt) * (64 * (size_t)RB); _Pragma("unroll") for (int j = 0; j < 8; ++j) { const char* p_ = kb_ + (size_t)j * RB; \
;         asm volatile("global_load_dwordx2 %0, %1, off" : "=&v"(sb[j]) : "v"(p_) : "memory"); } } while (0)
; #define MU_B_WAIT(sb, N) asm volatile("s_waitcnt vmcnt(%8)" : "+v"(sb[0]), "+v"(sb[1]), "+v"(sb[2]), "+v"(sb[3]), "+v"(sb[4]), "+v"(sb[5]), "+v"(sb[6]), "+v"(sb[7]) : "n"(N) : "memory")
; #define MU_COMPUTE(buf) MU_COMPUTE_N(buf, NMU)
; template <int MODE>
; __device__ __forceinline__ void moe_unit(PG8_LAS unsigned char* lds, int e, int cb, int slot0  , int nv  , const bf16_t* A, const int* slot_tok,
;                                          const float* W0, const float* W1, bf16_t* OUT, const float* slot_rs  , const int* slot_dst) {
;     ...
;     f32x4 acc[NMU][4];
; #pragma unroll
;     for (int m = 0; m < NMU; ++m)
; #pragma unroll
;         for (int n = 0; n < 4; ++n) acc[m][n] = (f32x4){0.f, 0.f, 0.f, 0.f};
;     f32x2 s0[8], s1[8];
;     float g0[8];
;     MU_GLDS_A(0, 0); MU_B_ISSUE(s0, 0); MU_G_LOAD(g0, 0); MU_B_ISSUE(s1, 1);
;     MU_B_WAIT(s0, 8); MU_B_WRITE(s0, 0, g0); __builtin_amdgcn_sched_barrier(0); MU_B_ISSUE(s0, 2);
;     asm volatile("s_waitcnt vmcnt(16)" ::: "memory");
;     asm volatile("s_waitcnt lgkmcnt(0)" ::: "memory"); __builtin_amdgcn_s_barrier(); asm volatile("" ::: "memory");
; #pragma unroll 1
;     for (int t = 0; t < nt; t += 2) {
;         if (t + 2 < nt) MU_B_WAIT(s1, 8); else MU_B_WAIT(s1, 0);
;         MU_G_LOAD(g0, t + 1); MU_B_WRITE(s1, 1, g0); __builtin_amdgcn_sched_barrier(0); MU_GLDS_A(1, t + 1); __builtin_amdgcn_sched_barrier(0);
;         if (t + 3 < nt) { MU_B_ISSUE(s1, t + 3); }
;         MU_COMPUTE(0);
;         MU_END(t + 3 >= nt);
;         if (t + 2 < nt) { MU_B_WAIT(s0, 8); MU_G_LOAD(g0, t + 2); MU_B_WRITE(s0, 0, g0); __builtin_amdgcn_sched_barrier(0); MU_GLDS_A(0, t + 2); __builtin_amdgcn_sched_barrier(0); }
;         if (t + 4 < nt) { MU_B_ISSUE(s0, t + 4); }
;         MU_COMPUTE(1);
;         MU_END(t + 4 >= nt);
	s_mov_b32 s47, s42
	s_mov_b32 s42, s43
	s_mov_b32 s43, s44
	s_mov_b32 s44, s47
	v_mul_f32_e32 v202, s20, v202
	v_mul_f32_e32 v203, s20, v203
	v_mul_f32_e32 v204, s21, v204
	v_mul_f32_e32 v205, s21, v205
	v_mul_f32_e32 v206, s22, v206
	v_mul_f32_e32 v207, s22, v207
	v_mul_f32_e32 v208, s23, v208
	v_mul_f32_e32 v209, s23, v209
	v_mul_f32_e32 v210, s24, v210
	v_mul_f32_e32 v211, s24, v211
	v_mul_f32_e32 v212, s25, v212
	v_mul_f32_e32 v213, s25, v213
	v_mul_f32_e32 v214, s26, v214
	v_mul_f32_e32 v215, s26, v215
	v_mul_f32_e32 v216, s27, v216
	v_mul_f32_e32 v217, s27, v217
	v_cvt_pk_bf16_f32 v158, v202, v204
	v_cvt_pk_bf16_f32 v159, v206, v208
	v_cvt_pk_bf16_f32 v160, v210, v212
	v_cvt_pk_bf16_f32 v161, v214, v216
	v_cvt_pk_bf16_f32 v162, v203, v205
	v_cvt_pk_bf16_f32 v163, v207, v209
	v_cvt_pk_bf16_f32 v164, v211, v213
	v_cvt_pk_bf16_f32 v165, v215, v217
	ds_write_b128 v1, v[158:161] offset:19456
	ds_write_b128 v1, v[162:165] offset:19584
	v_add_u32_e32 v91, s42, v135
	v_add_u32_e32 v93, s42, v137
	ds_read_b128 v[238:241], v139 offset:0
	ds_read_b128 v[242:245], v139 offset:2048
	ds_read_b128 v[246:249], v139 offset:4096
	ds_read_b128 v[250:253], v139 offset:6144
	ds_read_b128 v[218:221], v91 offset:0
	ds_read_b128 v[222:225], v91 offset:2048
	ds_read_b128 v[226:229], v91 offset:4096
	ds_read_b128 v[230:233], v91 offset:6144
	s_waitcnt lgkmcnt(0)
	v_mfma_f32_16x16x32_bf16 v[78:81], v[238:241], v[218:221], v[78:81]
	v_mfma_f32_16x16x32_bf16 v[74:77], v[242:245], v[218:221], v[74:77]
	v_mfma_f32_16x16x32_bf16 v[70:73], v[246:249], v[218:221], v[70:73]
	v_mfma_f32_16x16x32_bf16 v[66:69], v[250:253], v[218:221], v[66:69]
	ds_read_b128 v[218:221], v93 offset:0
	ds_read_b128 v[142:145], v141 offset:0
	v_mfma_f32_16x16x32_bf16 v[62:65], v[238:241], v[222:225], v[62:65]
	v_mfma_f32_16x16x32_bf16 v[58:61], v[242:245], v[222:225], v[58:61]
	v_mfma_f32_16x16x32_bf16 v[54:57], v[246:249], v[222:225], v[54:57]
	v_mfma_f32_16x16x32_bf16 v[50:53], v[250:253], v[222:225], v[50:53]
	ds_read_b128 v[222:225], v93 offset:2048
	ds_read_b128 v[146:149], v141 offset:2048
	v_mfma_f32_16x16x32_bf16 v[46:49], v[238:241], v[226:229], v[46:49]
	v_mfma_f32_16x16x32_bf16 v[42:45], v[242:245], v[226:229], v[42:45]
	v_mfma_f32_16x16x32_bf16 v[38:41], v[246:249], v[226:229], v[38:41]
	v_mfma_f32_16x16x32_bf16 v[34:37], v[250:253], v[226:229], v[34:37]
	ds_read_b128 v[226:229], v93 offset:4096
	ds_read_b128 v[150:153], v141 offset:4096
	v_mfma_f32_16x16x32_bf16 v[18:21], v[238:241], v[230:233], v[18:21]
	v_mfma_f32_16x16x32_bf16 v[22:25], v[242:245], v[230:233], v[22:25]
	v_mfma_f32_16x16x32_bf16 v[26:29], v[246:249], v[230:233], v[26:29]
	v_mfma_f32_16x16x32_bf16 v[30:33], v[250:253], v[230:233], v[30:33]
	ds_read_b128 v[230:233], v93 offset:6144
	ds_read_b128 v[154:157], v141 offset:6144
	s_waitcnt lgkmcnt(0)
	v_mfma_f32_16x16x32_bf16 v[78:81], v[142:145], v[218:221], v[78:81]
	v_mfma_f32_16x16x32_bf16 v[74:77], v[146:149], v[218:221], v[74:77]
	v_mfma_f32_16x16x32_bf16 v[70:73], v[150:153], v[218:221], v[70:73]
	v_mfma_f32_16x16x32_bf16 v[66:69], v[154:157], v[218:221], v[66:69]
	v_mfma_f32_16x16x32_bf16 v[62:65], v[142:145], v[222:225], v[62:65]
	v_mfma_f32_16x16x32_bf16 v[58:61], v[146:149], v[222:225], v[58:61]
	v_mfma_f32_16x16x32_bf16 v[54:57], v[150:153], v[222:225], v[54:57]
	v_mfma_f32_16x16x32_bf16 v[50:53], v[154:157], v[222:225], v[50:53]
	v_mfma_f32_16x16x32_bf16 v[46:49], v[142:145], v[226:229], v[46:49]
	v_mfma_f32_16x16x32_bf16 v[42:45], v[146:149], v[226:229], v[42:45]
	v_mfma_f32_16x16x32_bf16 v[38:41], v[150:153], v[226:229], v[38:41]
	v_mfma_f32_16x16x32_bf16 v[34:37], v[154:157], v[226:229], v[34:37]
	v_mfma_f32_16x16x32_bf16 v[18:21], v[142:145], v[230:233], v[18:21]
	v_mfma_f32_16x16x32_bf16 v[22:25], v[146:149], v[230:233], v[22:25]
	v_mfma_f32_16x16x32_bf16 v[26:29], v[150:153], v[230:233], v[26:29]
	v_mfma_f32_16x16x32_bf16 v[30:33], v[154:157], v[230:233], v[30:33]
	s_waitcnt vmcnt(0)
	s_waitcnt lgkmcnt(0)
	s_barrier
	s_mov_b32 s47, s42
	s_mov_b32 s42, s43
	s_mov_b32 s43, s44
	s_mov_b32 s44, s47
	v_add_u32_e32 v91, s42, v135
	v_add_u32_e32 v93, s42, v137
	ds_read_b128 v[238:241], v139 offset:19456
	ds_read_b128 v[242:245], v139 offset:21504
	ds_read_b128 v[246:249], v139 offset:23552
	ds_read_b128 v[250:253], v139 offset:25600
	ds_read_b128 v[218:221], v91 offset:0
	ds_read_b128 v[222:225], v91 offset:2048
	ds_read_b128 v[226:229], v91 offset:4096
	ds_read_b128 v[230:233], v91 offset:6144
	s_waitcnt lgkmcnt(0)
	v_mfma_f32_16x16x32_bf16 v[78:81], v[238:241], v[218:221], v[78:81]
	v_mfma_f32_16x16x32_bf16 v[74:77], v[242:245], v[218:221], v[74:77]
	v_mfma_f32_16x16x32_bf16 v[70:73], v[246:249], v[218:221], v[70:73]
	v_mfma_f32_16x16x32_bf16 v[66:69], v[250:253], v[218:221], v[66:69]
	ds_read_b128 v[218:221], v93 offset:0
	ds_read_b128 v[142:145], v141 offset:19456
	v_mfma_f32_16x16x32_bf16 v[62:65], v[238:241], v[222:225], v[62:65]
	v_mfma_f32_16x16x32_bf16 v[58:61], v[242:245], v[222:225], v[58:61]
	v_mfma_f32_16x16x32_bf16 v[54:57], v[246:249], v[222:225], v[54:57]
	v_mfma_f32_16x16x32_bf16 v[50:53], v[250:253], v[222:225], v[50:53]
	ds_read_b128 v[222:225], v93 offset:2048
	ds_read_b128 v[146:149], v141 offset:21504
	v_mfma_f32_16x16x32_bf16 v[46:49], v[238:241], v[226:229], v[46:49]
	v_mfma_f32_16x16x32_bf16 v[42:45], v[242:245], v[226:229], v[42:45]
	v_mfma_f32_16x16x32_bf16 v[38:41], v[246:249], v[226:229], v[38:41]
	v_mfma_f32_16x16x32_bf16 v[34:37], v[250:253], v[226:229], v[34:37]
	ds_read_b128 v[226:229], v93 offset:4096
	ds_read_b128 v[150:153], v141 offset:23552
	v_mfma_f32_16x16x32_bf16 v[18:21], v[238:241], v[230:233], v[18:21]
	v_mfma_f32_16x16x32_bf16 v[22:25], v[242:245], v[230:233], v[22:25]
	v_mfma_f32_16x16x32_bf16 v[26:29], v[246:249], v[230:233], v[26:29]
	v_mfma_f32_16x16x32_bf16 v[30:33], v[250:253], v[230:233], v[30:33]
	ds_read_b128 v[230:233], v93 offset:6144
	ds_read_b128 v[154:157], v141 offset:25600
	s_waitcnt lgkmcnt(0)
; #define MU_GLDS_A(buf, kt) do { _Pragma("unroll") for (int i = 0; i < NMU; ++i) \
;         __builtin_amdgcn_global_load_lds((const unsigned*)((const char*)A + aoff[i] + (size_t)(kt) * 128), (PG8_LAS unsigned*)(MU_SA(buf) + wid * 1024 + i * 8192), 16, 0, 0); } while (0)
; #define MU_B_ISSUE(sb, kt) do { const char* kb_ = Bb + (size_t)(kt) * (64 * (size_t)RB); _Pragma("unroll") for (int j = 0; j < 8; ++j) { const char* p_ = kb_ + (size_t)j * RB; \
;         asm volatile("global_load_dwordx2 %0, %1, off" : "=&v"(sb[j]) : "v"(p_) : "memory"); } } while (0)
; #define MU_B_WAIT(sb, N) asm volatile("s_waitcnt vmcnt(%8)" : "+v"(sb[0]), "+v"(sb[1]), "+v"(sb[2]), "+v"(sb[3]), "+v"(sb[4]), "+v"(sb[5]), "+v"(sb[6]), "+v"(sb[7]) : "n"(N) : "memory")
; #define MU_COMPUTE(buf) MU_COMPUTE_N(buf, NMU)
; template <int MODE>
; __device__ __forceinline__ void moe_unit(PG8_LAS unsigned char* lds, int e, int cb, int slot0  , int nv  , const bf16_t* A, const int* slot_tok,
;                                          const float* W0, const float* W1, bf16_t* OUT, const float* slot_rs  , const int* slot_dst) {
;     ...
;     f32x4 acc[NMU][4];
; #pragma unroll
;     for (int m = 0; m < NMU; ++m)
; #pragma unroll
;         for (int n = 0; n < 4; ++n) acc[m][n] = (f32x4){0.f, 0.f, 0.f, 0.f};
;     f32x2 s0[8], s1[8];
;     float g0[8];
;     MU_GLDS_A(0, 0); MU_B_ISSUE(s0, 0); MU_G_LOAD(g0, 0); MU_B_ISSUE(s1, 1);
;     MU_B_WAIT(s0, 8); MU_B_WRITE(s0, 0, g0); __builtin_amdgcn_sched_barrier(0); MU_B_ISSUE(s0, 2);
;     asm volatile("s_waitcnt vmcnt(16)" ::: "memory");
;     asm volatile("s_waitcnt lgkmcnt(0)" ::: "memory"); __builtin_amdgcn_s_barrier(); asm volatile("" ::: "memory");
; #pragma unroll 1
;     for (int t = 0; t < nt; t += 2) {
;         if (t + 2 < nt) MU_B_WAIT(s1, 8); else MU_B_WAIT(s1, 0);
;         MU_G_LOAD(g0, t + 1); MU_B_WRITE(s1, 1, g0); __builtin_amdgcn_sched_barrier(0); MU_GLDS_A(1, t + 1); __builtin_amdgcn_sched_barrier(0);
;         if (t + 3 < nt) { MU_B_ISSUE(s1, t + 3); }
;         MU_COMPUTE(0);
;         MU_END(t + 3 >= nt);
;         if (t + 2 < nt) { MU_B_WAIT(s0, 8); MU_G_LOAD(g0, t + 2); MU_B_WRITE(s0, 0, g0); __builtin_amdgcn_sched_barrier(0); MU_GLDS_A(0, t + 2); __builtin_amdgcn_sched_barrier(0); }
;         if (t + 4 < nt) { MU_B_ISSUE(s0, t + 4); }
;         MU_COMPUTE(1);
;         MU_END(t + 4 >= nt);
	v_mfma_f32_16x16x32_bf16 v[78:81], v[142:145], v[218:221], v[78:81]
	v_mfma_f32_16x16x32_bf16 v[74:77], v[146:149], v[218:221], v[74:77]
	v_mfma_f32_16x16x32_bf16 v[70:73], v[150:153], v[218:221], v[70:73]
	v_mfma_f32_16x16x32_bf16 v[66:69], v[154:157], v[218:221], v[66:69]
	v_mfma_f32_16x16x32_bf16 v[62:65], v[142:145], v[222:225], v[62:65]
	v_mfma_f32_16x16x32_bf16 v[58:61], v[146:149], v[222:225], v[58:61]
	v_mfma_f32_16x16x32_bf16 v[54:57], v[150:153], v[222:225], v[54:57]
	v_mfma_f32_16x16x32_bf16 v[50:53], v[154:157], v[222:225], v[50:53]
	v_mfma_f32_16x16x32_bf16 v[46:49], v[142:145], v[226:229], v[46:49]
	v_mfma_f32_16x16x32_bf16 v[42:45], v[146:149], v[226:229], v[42:45]
	v_mfma_f32_16x16x32_bf16 v[38:41], v[150:153], v[226:229], v[38:41]
	v_mfma_f32_16x16x32_bf16 v[34:37], v[154:157], v[226:229], v[34:37]
	v_mfma_f32_16x16x32_bf16 v[18:21], v[142:145], v[230:233], v[18:21]
	v_mfma_f32_16x16x32_bf16 v[22:25], v[146:149], v[230:233], v[22:25]
	v_mfma_f32_16x16x32_bf16 v[26:29], v[150:153], v[230:233], v[26:29]
	v_mfma_f32_16x16x32_bf16 v[30:33], v[154:157], v[230:233], v[30:33]
	s_waitcnt lgkmcnt(0)
	s_barrier
	s_mov_b32 s47, s42
	s_mov_b32 s42, s43
	s_mov_b32 s43, s44
	s_mov_b32 s44, s47
	s_branch .Lmu_done
.Lmu_grpY4:
	s_add_i32 s47, s44, s6
	s_add_u32 s30, s30, 0x80
	s_addc_u32 s31, s31, 0
	s_mov_b32 m0, s47
	s_nop 0
	global_load_lds_dwordx4 v86, s[30:31]
	s_add_i32 m0, s47, 0x2000
	s_nop 0
	global_load_lds_dwordx4 v134, s[30:31]
	s_add_i32 m0, s47, 0x4000
	s_nop 0
	global_load_lds_dwordx4 v136, s[30:31]
	s_add_i32 m0, s47, 0x6000
	s_nop 0
	global_load_lds_dwordx4 v138, s[30:31]
	s_add_i32 m0, s47, 0x8000
	s_nop 0
	global_load_lds_dwordx4 v140, s[30:31]
	s_waitcnt vmcnt(29)
	v_mul_f32_e32 v114, s20, v114
	v_mul_f32_e32 v115, s20, v115
	v_mul_f32_e32 v116, s21, v116
	v_mul_f32_e32 v117, s21, v117
	v_mul_f32_e32 v118, s22, v118
	v_mul_f32_e32 v119, s22, v119
	v_mul_f32_e32 v120, s23, v120
	v_mul_f32_e32 v121, s23, v121
	v_mul_f32_e32 v122, s24, v122
	v_mul_f32_e32 v123, s24, v123
	v_mul_f32_e32 v124, s25, v124
	v_mul_f32_e32 v125, s25, v125
	v_mul_f32_e32 v126, s26, v126
	v_mul_f32_e32 v127, s26, v127
	v_mul_f32_e32 v128, s27, v128
	v_mul_f32_e32 v129, s27, v129
	v_cvt_pk_bf16_f32 v158, v114, v116
	v_cvt_pk_bf16_f32 v159, v118, v120
	v_cvt_pk_bf16_f32 v160, v122, v124
	v_cvt_pk_bf16_f32 v161, v126, v128
	v_cvt_pk_bf16_f32 v162, v115, v117
	v_cvt_pk_bf16_f32 v163, v119, v121
	v_cvt_pk_bf16_f32 v164, v123, v125
	v_cvt_pk_bf16_f32 v165, v127, v129
	ds_write_b128 v1, v[158:161] offset:19456
	ds_write_b128 v1, v[162:165] offset:19584
	v_add_u32_e32 v91, s42, v135
	v_add_u32_e32 v93, s42, v137
	ds_read_b128 v[238:241], v139 offset:0
	ds_read_b128 v[242:245], v139 offset:2048
	ds_read_b128 v[246:249], v139 offset:4096
	ds_read_b128 v[250:253], v139 offset:6144
	ds_read_b128 v[218:221], v91 offset:0
	ds_read_b128 v[222:225], v91 offset:2048
	ds_read_b128 v[226:229], v91 offset:4096
	ds_read_b128 v[230:233], v91 offset:6144
	s_waitcnt lgkmcnt(0)
	s_load_dwordx8 s[12:19], s[28:29], 0x0
	s_add_u32 s28, s28, 0x100
	s_addc_u32 s29, s29, 0
	v_mfma_f32_16x16x32_bf16 v[78:81], v[238:241], v[218:221], v[78:81]
	v_mfma_f32_16x16x32_bf16 v[74:77], v[242:245], v[218:221], v[74:77]
	v_mfma_f32_16x16x32_bf16 v[70:73], v[246:249], v[218:221], v[70:73]
	v_mfma_f32_16x16x32_bf16 v[66:69], v[250:253], v[218:221], v[66:69]
	ds_read_b128 v[218:221], v93 offset:0
	ds_read_b128 v[142:145], v141 offset:0
	v_lshl_add_u64 v[132:133], v[132:133], 0, s[40:41]
	global_load_dwordx2 v[114:115], v[132:133], off
	global_load_dwordx2 v[116:117], v[132:133], off offset:2048
	v_mfma_f32_16x16x32_bf16 v[62:65], v[238:241], v[222:225], v[62:65]
	v_mfma_f32_16x16x32_bf16 v[58:61], v[242:245], v[222:225], v[58:61]
	v_mfma_f32_16x16x32_bf16 v[54:57], v[246:249], v[222:225], v[54:57]
	v_mfma_f32_16x16x32_bf16 v[50:53], v[250:253], v[222:225], v[50:53]
	ds_read_b128 v[222:225], v93 offset:2048
	ds_read_b128 v[146:149], v141 offset:2048
	v_lshl_add_u64 v[166:167], v[132:133], 0, s[34:35]
	global_load_dwordx2 v[118:119], v[166:167], off
	global_load_dwordx2 v[120:121], v[166:167], off offset:2048
	v_mfma_f32_16x16x32_bf16 v[46:49], v[238:241], v[226:229], v[46:49]
	v_mfma_f32_16x16x32_bf16 v[42:45], v[242:245], v[226:229], v[42:45]
	v_mfma_f32_16x16x32_bf16 v[38:41], v[246:249], v[226:229], v[38:41]
	v_mfma_f32_16x16x32_bf16 v[34:37], v[250:253], v[226:229], v[34:37]
	ds_read_b128 v[226:229], v93 offset:4096
	ds_read_b128 v[150:153], v141 offset:4096
	v_lshl_add_u64 v[166:167], v[132:133], 0, s[36:37]
	global_load_dwordx2 v[122:123], v[166:167], off
	global_load_dwordx2 v[124:125], v[166:167], off offset:2048
	v_mfma_f32_16x16x32_bf16 v[18:21], v[238:241], v[230:233], v[18:21]
	v_mfma_f32_16x16x32_bf16 v[22:25], v[242:245], v[230:233], v[22:25]
	v_mfma_f32_16x16x32_bf16 v[26:29], v[246:249], v[230:233], v[26:29]
	v_mfma_f32_16x16x32_bf16 v[30:33], v[250:253], v[230:233], v[30:33]
	ds_read_b128 v[230:233], v93 offset:6144
	ds_read_b128 v[154:157], v141 offset:6144
	v_lshl_add_u64 v[166:167], v[132:133], 0, s[38:39]
	global_load_dwordx2 v[126:127], v[166:167], off
	global_load_dwordx2 v[128:129], v[166:167], off offset:2048
	s_waitcnt lgkmcnt(0)
	s_barrier
; #define MU_GLDS_A(buf, kt) do { _Pragma("unroll") for (int i = 0; i < NMU; ++i) \
;         __builtin_amdgcn_global_load_lds((const unsigned*)((const char*)A + aoff[i] + (size_t)(kt) * 128), (PG8_LAS unsigned*)(MU_SA(buf) + wid * 1024 + i * 8192), 16, 0, 0); } while (0)
; #define MU_B_ISSUE(sb, kt) do { const char* kb_ = Bb + (size_t)(kt) * (64 * (size_t)RB); _Pragma("unroll") for (int j = 0; j < 8; ++j) { const char* p_ = kb_ + (size_t)j * RB; \
;         asm volatile("global_load_dwordx2 %0, %1, off" : "=&v"(sb[j]) : "v"(p_) : "memory"); } } while (0)
; #define MU_B_WAIT(sb, N) asm volatile("s_waitcnt vmcnt(%8)" : "+v"(sb[0]), "+v"(sb[1]), "+v"(sb[2]), "+v"(sb[3]), "+v"(sb[4]), "+v"(sb[5]), "+v"(sb[6]), "+v"(sb[7]) : "n"(N) : "memory")
; #define MU_COMPUTE(buf) MU_COMPUTE_N(buf, NMU)
; template <int MODE>
; __device__ __forceinline__ void moe_unit(PG8_LAS unsigned char* lds, int e, int cb, int slot0  , int nv  , const bf16_t* A, const int* slot_tok,
;                                          const float* W0, const float* W1, bf16_t* OUT, const float* slot_rs  , const int* slot_dst) {
;     ...
;     f32x4 acc[NMU][4];
; #pragma unroll
;     for (int m = 0; m < NMU; ++m)
; #pragma unroll
;         for (int n = 0; n < 4; ++n) acc[m][n] = (f32x4){0.f, 0.f, 0.f, 0.f};
;     f32x2 s0[8], s1[8];
;     float g0[8];
;     MU_GLDS_A(0, 0); MU_B_ISSUE(s0, 0); MU_G_LOAD(g0, 0); MU_B_ISSUE(s1, 1);
;     MU_B_WAIT(s0, 8); MU_B_WRITE(s0, 0, g0); __builtin_amdgcn_sched_barrier(0); MU_B_ISSUE(s0, 2);
;     asm volatile("s_waitcnt vmcnt(16)" ::: "memory");
;     asm volatile("s_waitcnt lgkmcnt(0)" ::: "memory"); __builtin_amdgcn_s_barrier(); asm volatile("" ::: "memory");
; #pragma unroll 1
;     for (int t = 0; t < nt; t += 2) {
;         if (t + 2 < nt) MU_B_WAIT(s1, 8); else MU_B_WAIT(s1, 0);
;         MU_G_LOAD(g0, t + 1); MU_B_WRITE(s1, 1, g0); __builtin_amdgcn_sched_barrier(0); MU_GLDS_A(1, t + 1); __builtin_amdgcn_sched_barrier(0);
;         if (t + 3 < nt) { MU_B_ISSUE(s1, t + 3); }
;         MU_COMPUTE(0);
;         MU_END(t + 3 >= nt);
;         if (t + 2 < nt) { MU_B_WAIT(s0, 8); MU_G_LOAD(g0, t + 2); MU_B_WRITE(s0, 0, g0); __builtin_amdgcn_sched_barrier(0); MU_GLDS_A(0, t + 2); __builtin_amdgcn_sched_barrier(0); }
;         if (t + 4 < nt) { MU_B_ISSUE(s0, t + 4); }
;         MU_COMPUTE(1);
;         MU_END(t + 4 >= nt);
	s_mov_b32 s47, s42
	s_mov_b32 s42, s43
	s_mov_b32 s43, s44
	s_mov_b32 s44, s47
	s_add_i32 s47, s44, s6
	s_add_u32 s30, s30, 0x80
	s_addc_u32 s31, s31, 0
	v_mfma_f32_16x16x32_bf16 v[78:81], v[142:145], v[218:221], v[78:81]
	v_mfma_f32_16x16x32_bf16 v[74:77], v[146:149], v[218:221], v[74:77]
	v_mfma_f32_16x16x32_bf16 v[70:73], v[150:153], v[218:221], v[70:73]
	v_mfma_f32_16x16x32_bf16 v[66:69], v[154:157], v[218:221], v[66:69]
	s_mov_b32 m0, s47
	s_nop 0
	global_load_lds_dwordx4 v86, s[30:31]
	v_mfma_f32_16x16x32_bf16 v[62:65], v[142:145], v[222:225], v[62:65]
	v_mfma_f32_16x16x32_bf16 v[58:61], v[146:149], v[222:225], v[58:61]
	v_mfma_f32_16x16x32_bf16 v[54:57], v[150:153], v[222:225], v[54:57]
	v_mfma_f32_16x16x32_bf16 v[50:53], v[154:157], v[222:225], v[50:53]
	s_add_i32 m0, s47, 0x2000
	s_nop 0
	global_load_lds_dwordx4 v134, s[30:31]
	v_mfma_f32_16x16x32_bf16 v[46:49], v[142:145], v[226:229], v[46:49]
	v_mfma_f32_16x16x32_bf16 v[42:45], v[146:149], v[226:229], v[42:45]
	v_mfma_f32_16x16x32_bf16 v[38:41], v[150:153], v[226:229], v[38:41]
	v_mfma_f32_16x16x32_bf16 v[34:37], v[154:157], v[226:229], v[34:37]
	s_add_i32 m0, s47, 0x4000
	s_nop 0
	global_load_lds_dwordx4 v136, s[30:31]
	v_mfma_f32_16x16x32_bf16 v[18:21], v[142:145], v[230:233], v[18:21]
	v_mfma_f32_16x16x32_bf16 v[22:25], v[146:149], v[230:233], v[22:25]
	v_mfma_f32_16x16x32_bf16 v[26:29], v[150:153], v[230:233], v[26:29]
	v_mfma_f32_16x16x32_bf16 v[30:33], v[154:157], v[230:233], v[30:33]
	s_add_i32 m0, s47, 0x6000
	s_nop 0
	global_load_lds_dwordx4 v138, s[30:31]
	s_add_i32 m0, s47, 0x8000
	s_nop 0
	global_load_lds_dwordx4 v140, s[30:31]
	s_waitcnt vmcnt(34)
	v_mul_f32_e32 v186, s12, v186
	v_mul_f32_e32 v187, s12, v187
	v_mul_f32_e32 v188, s13, v188
	v_mul_f32_e32 v189, s13, v189
	v_mul_f32_e32 v190, s14, v190
	v_mul_f32_e32 v191, s14, v191
	v_mul_f32_e32 v192, s15, v192
	v_mul_f32_e32 v193, s15, v193
	v_mul_f32_e32 v194, s16, v194
	v_mul_f32_e32 v195, s16, v195
	v_mul_f32_e32 v196, s17, v196
	v_mul_f32_e32 v197, s17, v197
	v_mul_f32_e32 v198, s18, v198
	v_mul_f32_e32 v199, s18, v199
	v_mul_f32_e32 v200, s19, v200
	v_mul_f32_e32 v201, s19, v201
	v_cvt_pk_bf16_f32 v158, v186, v188
	v_cvt_pk_bf16_f32 v159, v190, v192
	v_cvt_pk_bf16_f32 v160, v194, v196
	v_cvt_pk_bf16_f32 v161, v198, v200
	v_cvt_pk_bf16_f32 v162, v187, v189
	v_cvt_pk_bf16_f32 v163, v191, v193
	v_cvt_pk_bf16_f32 v164, v195, v197
	v_cvt_pk_bf16_f32 v165, v199, v201
	ds_write_b128 v1, v[158:161] offset:0
	ds_write_b128 v1, v[162:165] offset:128
	v_add_u32_e32 v91, s42, v135
	v_add_u32_e32 v93, s42, v137
	ds_read_b128 v[238:241], v139 offset:19456
	ds_read_b128 v[242:245], v139 offset:21504
	ds_read_b128 v[246:249], v139 offset:23552
	ds_read_b128 v[250:253], v139 offset:25600
	ds_read_b128 v[218:221], v91 offset:0
	ds_read_b128 v[222:225], v91 offset:2048
	ds_read_b128 v[226:229], v91 offset:4096
	ds_read_b128 v[230:233], v91 offset:6144
	s_waitcnt lgkmcnt(0)
	s_load_dwordx8 s[20:27], s[28:29], 0x0
	s_add_u32 s28, s28, 0x100
	s_addc_u32 s29, s29, 0
	v_mfma_f32_16x16x32_bf16 v[78:81], v[238:241], v[218:221], v[78:81]
	v_mfma_f32_16x16x32_bf16 v[74:77], v[242:245], v[218:221], v[74:77]
	v_mfma_f32_16x16x32_bf16 v[70:73], v[246:249], v[218:221], v[70:73]
	v_mfma_f32_16x16x32_bf16 v[66:69], v[250:253], v[218:221], v[66:69]
	ds_read_b128 v[218:221], v93 offset:0
	ds_read_b128 v[142:145], v141 offset:19456
	v_lshl_add_u64 v[132:133], v[132:133], 0, s[40:41]
	global_load_dwordx2 v[186:187], v[132:133], off
	global_load_dwordx2 v[188:189], v[132:133], off offset:2048
	v_mfma_f32_16x16x32_bf16 v[62:65], v[238:241], v[222:225], v[62:65]
	v_mfma_f32_16x16x32_bf16 v[58:61], v[242:245], v[222:225], v[58:61]
	v_mfma_f32_16x16x32_bf16 v[54:57], v[246:249], v[222:225], v[54:57]
	v_mfma_f32_16x16x32_bf16 v[50:53], v[250:253], v[222:225], v[50:53]
	ds_read_b128 v[222:225], v93 offset:2048
	ds_read_b128 v[146:149], v141 offset:21504
	v_lshl_add_u64 v[166:167], v[132:133], 0, s[34:35]
	global_load_dwordx2 v[190:191], v[166:167], off
	global_load_dwordx2 v[192:193], v[166:167], off offset:2048
	v_mfma_f32_16x16x32_bf16 v[46:49], v[238:241], v[226:229], v[46:49]
	v_mfma_f32_16x16x32_bf16 v[42:45], v[242:245], v[226:229], v[42:45]
	v_mfma_f32_16x16x32_bf16 v[38:41], v[246:249], v[226:229], v[38:41]
	v_mfma_f32_16x16x32_bf16 v[34:37], v[250:253], v[226:229], v[34:37]
	ds_read_b128 v[226:229], v93 offset:4096
	ds_read_b128 v[150:153], v141 offset:23552
	v_lshl_add_u64 v[166:167], v[132:133], 0, s[36:37]
	global_load_dwordx2 v[194:195], v[166:167], off
	global_load_dwordx2 v[196:197], v[166:167], off offset:2048
	v_mfma_f32_16x16x32_bf16 v[18:21], v[238:241], v[230:233], v[18:21]
	v_mfma_f32_16x16x32_bf16 v[22:25], v[242:245], v[230:233], v[22:25]
	v_mfma_f32_16x16x32_bf16 v[26:29], v[246:249], v[230:233], v[26:29]
	v_mfma_f32_16x16x32_bf16 v[30:33], v[250:253], v[230:233], v[30:33]
	ds_read_b128 v[230:233], v93 offset:6144
	ds_read_b128 v[154:157], v141 offset:25600
	v_lshl_add_u64 v[166:167], v[132:133], 0, s[38:39]
	global_load_dwordx2 v[198:199], v[166:167], off
	global_load_dwordx2 v[200:201], v[166:167], off offset:2048
	s_waitcnt vmcnt(21)
	s_waitcnt lgkmcnt(0)
	s_barrier
; #define MU_GLDS_A(buf, kt) do { _Pragma("unroll") for (int i = 0; i < NMU; ++i) \
;         __builtin_amdgcn_global_load_lds((const unsigned*)((const char*)A + aoff[i] + (size_t)(kt) * 128), (PG8_LAS unsigned*)(MU_SA(buf) + wid * 1024 + i * 8192), 16, 0, 0); } while (0)
; #define MU_B_ISSUE(sb, kt) do { const char* kb_ = Bb + (size_t)(kt) * (64 * (size_t)RB); _Pragma("unroll") for (int j = 0; j < 8; ++j) { const char* p_ = kb_ + (size_t)j * RB; \
;         asm volatile("global_load_dwordx2 %0, %1, off" : "=&v"(sb[j]) : "v"(p_) : "memory"); } } while (0)
; #define MU_B_WAIT(sb, N) asm volatile("s_waitcnt vmcnt(%8)" : "+v"(sb[0]), "+v"(sb[1]), "+v"(sb[2]), "+v"(sb[3]), "+v"(sb[4]), "+v"(sb[5]), "+v"(sb[6]), "+v"(sb[7]) : "n"(N) : "memory")
; #define MU_COMPUTE(buf) MU_COMPUTE_N(buf, NMU)
; template <int MODE>
; __device__ __forceinline__ void moe_unit(PG8_LAS unsigned char* lds, int e, int cb, int slot0  , int nv  , const bf16_t* A, const int* slot_tok,
;                                          const float* W0, const float* W1, bf16_t* OUT, const float* slot_rs  , const int* slot_dst) {
;     ...
;     f32x4 acc[NMU][4];
; #pragma unroll
;     for (int m = 0; m < NMU; ++m)
; #pragma unroll
;         for (int n = 0; n < 4; ++n) acc[m][n] = (f32x4){0.f, 0.f, 0.f, 0.f};
;     f32x2 s0[8], s1[8];
;     float g0[8];
;     MU_GLDS_A(0, 0); MU_B_ISSUE(s0, 0); MU_G_LOAD(g0, 0); MU_B_ISSUE(s1, 1);
;     MU_B_WAIT(s0, 8); MU_B_WRITE(s0, 0, g0); __builtin_amdgcn_sched_barrier(0); MU_B_ISSUE(s0, 2);
;     asm volatile("s_waitcnt vmcnt(16)" ::: "memory");
;     asm volatile("s_waitcnt lgkmcnt(0)" ::: "memory"); __builtin_amdgcn_s_barrier(); asm volatile("" ::: "memory");
; #pragma unroll 1
;     for (int t = 0; t < nt; t += 2) {
;         if (t + 2 < nt) MU_B_WAIT(s1, 8); else MU_B_WAIT(s1, 0);
;         MU_G_LOAD(g0, t + 1); MU_B_WRITE(s1, 1, g0); __builtin_amdgcn_sched_barrier(0); MU_GLDS_A(1, t + 1); __builtin_amdgcn_sched_barrier(0);
;         if (t + 3 < nt) { MU_B_ISSUE(s1, t + 3); }
;         MU_COMPUTE(0);
;         MU_END(t + 3 >= nt);
;         if (t + 2 < nt) { MU_B_WAIT(s0, 8); MU_G_LOAD(g0, t + 2); MU_B_WRITE(s0, 0, g0); __builtin_amdgcn_sched_barrier(0); MU_GLDS_A(0, t + 2); __builtin_amdgcn_sched_barrier(0); }
;         if (t + 4 < nt) { MU_B_ISSUE(s0, t + 4); }
;         MU_COMPUTE(1);
;         MU_END(t + 4 >= nt);
	s_mov_b32 s47, s42
	s_mov_b32 s42, s43
	s_mov_b32 s43, s44
	s_mov_b32 s44, s47
	s_add_i32 s47, s44, s6
	s_add_u32 s30, s30, 0x80
	s_addc_u32 s31, s31, 0
	v_mfma_f32_16x16x32_bf16 v[78:81], v[142:145], v[218:221], v[78:81]
	v_mfma_f32_16x16x32_bf16 v[74:77], v[146:149], v[218:221], v[74:77]
	v_mfma_f32_16x16x32_bf16 v[70:73], v[150:153], v[218:221], v[70:73]
	v_mfma_f32_16x16x32_bf16 v[66:69], v[154:157], v[218:221], v[66:69]
	s_mov_b32 m0, s47
	s_nop 0
	global_load_lds_dwordx4 v86, s[30:31]
	v_mfma_f32_16x16x32_bf16 v[62:65], v[142:145], v[222:225], v[62:65]
	v_mfma_f32_16x16x32_bf16 v[58:61], v[146:149], v[222:225], v[58:61]
	v_mfma_f32_16x16x32_bf16 v[54:57], v[150:153], v[222:225], v[54:57]
	v_mfma_f32_16x16x32_bf16 v[50:53], v[154:157], v[222:225], v[50:53]
	s_add_i32 m0, s47, 0x2000
	s_nop 0
	global_load_lds_dwordx4 v134, s[30:31]
	v_mfma_f32_16x16x32_bf16 v[46:49], v[142:145], v[226:229], v[46:49]
	v_mfma_f32_16x16x32_bf16 v[42:45], v[146:149], v[226:229], v[42:45]
	v_mfma_f32_16x16x32_bf16 v[38:41], v[150:153], v[226:229], v[38:41]
	v_mfma_f32_16x16x32_bf16 v[34:37], v[154:157], v[226:229], v[34:37]
	s_add_i32 m0, s47, 0x4000
	s_nop 0
	global_load_lds_dwordx4 v136, s[30:31]
	v_mfma_f32_16x16x32_bf16 v[18:21], v[142:145], v[230:233], v[18:21]
	v_mfma_f32_16x16x32_bf16 v[22:25], v[146:149], v[230:233], v[22:25]
	v_mfma_f32_16x16x32_bf16 v[26:29], v[150:153], v[230:233], v[26:29]
	v_mfma_f32_16x16x32_bf16 v[30:33], v[154:157], v[230:233], v[30:33]
	s_add_i32 m0, s47, 0x6000
	s_nop 0
	global_load_lds_dwordx4 v138, s[30:31]
	s_add_i32 m0, s47, 0x8000
	s_nop 0
	global_load_lds_dwordx4 v140, s[30:31]
	v_mul_f32_e32 v202, s20, v202
	v_mul_f32_e32 v203, s20, v203
	v_mul_f32_e32 v204, s21, v204
	v_mul_f32_e32 v205, s21, v205
	v_mul_f32_e32 v206, s22, v206
	v_mul_f32_e32 v207, s22, v207
	v_mul_f32_e32 v208, s23, v208
	v_mul_f32_e32 v209, s23, v209
	v_mul_f32_e32 v210, s24, v210
	v_mul_f32_e32 v211, s24, v211
	v_mul_f32_e32 v212, s25, v212
	v_mul_f32_e32 v213, s25, v213
	v_mul_f32_e32 v214, s26, v214
	v_mul_f32_e32 v215, s26, v215
	v_mul_f32_e32 v216, s27, v216
	v_mul_f32_e32 v217, s27, v217
	v_cvt_pk_bf16_f32 v158, v202, v204
	v_cvt_pk_bf16_f32 v159, v206, v208
	v_cvt_pk_bf16_f32 v160, v210, v212
	v_cvt_pk_bf16_f32 v161, v214, v216
	v_cvt_pk_bf16_f32 v162, v203, v205
	v_cvt_pk_bf16_f32 v163, v207, v209
	v_cvt_pk_bf16_f32 v164, v211, v213
	v_cvt_pk_bf16_f32 v165, v215, v217
	ds_write_b128 v1, v[158:161] offset:19456
	ds_write_b128 v1, v[162:165] offset:19584
	v_add_u32_e32 v91, s42, v135
	v_add_u32_e32 v93, s42, v137
	ds_read_b128 v[238:241], v139 offset:0
	ds_read_b128 v[242:245], v139 offset:2048
	ds_read_b128 v[246:249], v139 offset:4096
	ds_read_b128 v[250:253], v139 offset:6144
	ds_read_b128 v[218:221], v91 offset:0
	ds_read_b128 v[222:225], v91 offset:2048
	ds_read_b128 v[226:229], v91 offset:4096
	ds_read_b128 v[230:233], v91 offset:6144
	s_waitcnt lgkmcnt(0)
	s_load_dwordx8 s[12:19], s[28:29], 0x0
	s_add_u32 s28, s28, 0x100
	s_addc_u32 s29, s29, 0
	v_mfma_f32_16x16x32_bf16 v[78:81], v[238:241], v[218:221], v[78:81]
	v_mfma_f32_16x16x32_bf16 v[74:77], v[242:245], v[218:221], v[74:77]
	v_mfma_f32_16x16x32_bf16 v[70:73], v[246:249], v[218:221], v[70:73]
	v_mfma_f32_16x16x32_bf16 v[66:69], v[250:253], v[218:221], v[66:69]
	ds_read_b128 v[218:221], v93 offset:0
	ds_read_b128 v[142:145], v141 offset:0
	v_lshl_add_u64 v[132:133], v[132:133], 0, s[40:41]
	global_load_dwordx2 v[202:203], v[132:133], off
	global_load_dwordx2 v[204:205], v[132:133], off offset:2048
	v_mfma_f32_16x16x32_bf16 v[62:65], v[238:241], v[222:225], v[62:65]
	v_mfma_f32_16x16x32_bf16 v[58:61], v[242:245], v[222:225], v[58:61]
	v_mfma_f32_16x16x32_bf16 v[54:57], v[246:249], v[222:225], v[54:57]
	v_mfma_f32_16x16x32_bf16 v[50:53], v[250:253], v[222:225], v[50:53]
	ds_read_b128 v[222:225], v93 offset:2048
	ds_read_b128 v[146:149], v141 offset:2048
	v_lshl_add_u64 v[166:167], v[132:133], 0, s[34:35]
	global_load_dwordx2 v[206:207], v[166:167], off
	global_load_dwordx2 v[208:209], v[166:167], off offset:2048
	v_mfma_f32_16x16x32_bf16 v[46:49], v[238:241], v[226:229], v[46:49]
	v_mfma_f32_16x16x32_bf16 v[42:45], v[242:245], v[226:229], v[42:45]
	v_mfma_f32_16x16x32_bf16 v[38:41], v[246:249], v[226:229], v[38:41]
	v_mfma_f32_16x16x32_bf16 v[34:37], v[250:253], v[226:229], v[34:37]
	ds_read_b128 v[226:229], v93 offset:4096
	ds_read_b128 v[150:153], v141 offset:4096
	v_lshl_add_u64 v[166:167], v[132:133], 0, s[36:37]
	global_load_dwordx2 v[210:211], v[166:167], off
	global_load_dwordx2 v[212:213], v[166:167], off offset:2048
	v_mfma_f32_16x16x32_bf16 v[18:21], v[238:241], v[230:233], v[18:21]
	v_mfma_f32_16x16x32_bf16 v[22:25], v[242:245], v[230:233], v[22:25]
	v_mfma_f32_16x16x32_bf16 v[26:29], v[246:249], v[230:233], v[26:29]
	v_mfma_f32_16x16x32_bf16 v[30:33], v[250:253], v[230:233], v[30:33]
	ds_read_b128 v[230:233], v93 offset:6144
	ds_read_b128 v[154:157], v141 offset:6144
	v_lshl_add_u64 v[166:167], v[132:133], 0, s[38:39]
	global_load_dwordx2 v[214:215], v[166:167], off
	global_load_dwordx2 v[216:217], v[166:167], off offset:2048
	s_waitcnt vmcnt(21)
	s_waitcnt lgkmcnt(0)
	s_barrier
; #define MU_GLDS_A(buf, kt) do { _Pragma("unroll") for (int i = 0; i < NMU; ++i) \
;         __builtin_amdgcn_global_load_lds((const unsigned*)((const char*)A + aoff[i] + (size_t)(kt) * 128), (PG8_LAS unsigned*)(MU_SA(buf) + wid * 1024 + i * 8192), 16, 0, 0); } while (0)
; #define MU_B_ISSUE(sb, kt) do { const char* kb_ = Bb + (size_t)(kt) * (64 * (size_t)RB); _Pragma("unroll") for (int j = 0; j < 8; ++j) { const char* p_ = kb_ + (size_t)j * RB; \
;         asm volatile("global_load_dwordx2 %0, %1, off" : "=&v"(sb[j]) : "v"(p_) : "memory"); } } while (0)
; #define MU_B_WAIT(sb, N) asm volatile("s_waitcnt vmcnt(%8)" : "+v"(sb[0]), "+v"(sb[1]), "+v"(sb[2]), "+v"(sb[3]), "+v"(sb[4]), "+v"(sb[5]), "+v"(sb[6]), "+v"(sb[7]) : "n"(N) : "memory")
; #define MU_COMPUTE(buf) MU_COMPUTE_N(buf, NMU)
; template <int MODE>
; __device__ __forceinline__ void moe_unit(PG8_LAS unsigned char* lds, int e, int cb, int slot0  , int nv  , const bf16_t* A, const int* slot_tok,
;                                          const float* W0, const float* W1, bf16_t* OUT, const float* slot_rs  , const int* slot_dst) {
;     ...
;     f32x4 acc[NMU][4];
; #pragma unroll
;     for (int m = 0; m < NMU; ++m)
; #pragma unroll
;         for (int n = 0; n < 4; ++n) acc[m][n] = (f32x4){0.f, 0.f, 0.f, 0.f};
;     f32x2 s0[8], s1[8];
;     float g0[8];
;     MU_GLDS_A(0, 0); MU_B_ISSUE(s0, 0); MU_G_LOAD(g0, 0); MU_B_ISSUE(s1, 1);
;     MU_B_WAIT(s0, 8); MU_B_WRITE(s0, 0, g0); __builtin_amdgcn_sched_barrier(0); MU_B_ISSUE(s0, 2);
;     asm volatile("s_waitcnt vmcnt(16)" ::: "memory");
;     asm volatile("s_waitcnt lgkmcnt(0)" ::: "memory"); __builtin_amdgcn_s_barrier(); asm volatile("" ::: "memory");
; #pragma unroll 1
;     for (int t = 0; t < nt; t += 2) {
;         if (t + 2 < nt) MU_B_WAIT(s1, 8); else MU_B_WAIT(s1, 0);
;         MU_G_LOAD(g0, t + 1); MU_B_WRITE(s1, 1, g0); __builtin_amdgcn_sched_barrier(0); MU_GLDS_A(1, t + 1); __builtin_amdgcn_sched_barrier(0);
;         if (t + 3 < nt) { MU_B_ISSUE(s1, t + 3); }
;         MU_COMPUTE(0);
;         MU_END(t + 3 >= nt);
;         if (t + 2 < nt) { MU_B_WAIT(s0, 8); MU_G_LOAD(g0, t + 2); MU_B_WRITE(s0, 0, g0); __builtin_amdgcn_sched_barrier(0); MU_GLDS_A(0, t + 2); __builtin_amdgcn_sched_barrier(0); }
;         if (t + 4 < nt) { MU_B_ISSUE(s0, t + 4); }
;         MU_COMPUTE(1);
;         MU_END(t + 4 >= nt);
	s_mov_b32 s47, s42
	s_mov_b32 s42, s43
	s_mov_b32 s43, s44
	s_mov_b32 s44, s47
	s_add_i32 s47, s44, s6
	s_add_u32 s30, s30, 0x80
	s_addc_u32 s31, s31, 0
	v_mfma_f32_16x16x32_bf16 v[78:81], v[142:145], v[218:221], v[78:81]
	v_mfma_f32_16x16x32_bf16 v[74:77], v[146:149], v[218:221], v[74:77]
	v_mfma_f32_16x16x32_bf16 v[70:73], v[150:153], v[218:221], v[70:73]
	v_mfma_f32_16x16x32_bf16 v[66:69], v[154:157], v[218:221], v[66:69]
	s_mov_b32 m0, s47
	s_nop 0
	global_load_lds_dwordx4 v86, s[30:31]
	v_mfma_f32_16x16x32_bf16 v[62:65], v[142:145], v[222:225], v[62:65]
	v_mfma_f32_16x16x32_bf16 v[58:61], v[146:149], v[222:225], v[58:61]
	v_mfma_f32_16x16x32_bf16 v[54:57], v[150:153], v[222:225], v[54:57]
	v_mfma_f32_16x16x32_bf16 v[50:53], v[154:157], v[222:225], v[50:53]
	s_add_i32 m0, s47, 0x2000
	s_nop 0
	global_load_lds_dwordx4 v134, s[30:31]
	v_mfma_f32_16x16x32_bf16 v[46:49], v[142:145], v[226:229], v[46:49]
	v_mfma_f32_16x16x32_bf16 v[42:45], v[146:149], v[226:229], v[42:45]
	v_mfma_f32_16x16x32_bf16 v[38:41], v[150:153], v[226:229], v[38:41]
	v_mfma_f32_16x16x32_bf16 v[34:37], v[154:157], v[226:229], v[34:37]
	s_add_i32 m0, s47, 0x4000
	s_nop 0
	global_load_lds_dwordx4 v136, s[30:31]
	v_mfma_f32_16x16x32_bf16 v[18:21], v[142:145], v[230:233], v[18:21]
	v_mfma_f32_16x16x32_bf16 v[22:25], v[146:149], v[230:233], v[22:25]
	v_mfma_f32_16x16x32_bf16 v[26:29], v[150:153], v[230:233], v[26:29]
	v_mfma_f32_16x16x32_bf16 v[30:33], v[154:157], v[230:233], v[30:33]
	s_add_i32 m0, s47, 0x6000
	s_nop 0
	global_load_lds_dwordx4 v138, s[30:31]
	s_add_i32 m0, s47, 0x8000
	s_nop 0
	global_load_lds_dwordx4 v140, s[30:31]
	v_mul_f32_e32 v98, s12, v98
	v_mul_f32_e32 v99, s12, v99
	v_mul_f32_e32 v100, s13, v100
	v_mul_f32_e32 v101, s13, v101
	v_mul_f32_e32 v102, s14, v102
	v_mul_f32_e32 v103, s14, v103
	v_mul_f32_e32 v104, s15, v104
	v_mul_f32_e32 v105, s15, v105
	v_mul_f32_e32 v106, s16, v106
	v_mul_f32_e32 v107, s16, v107
	v_mul_f32_e32 v108, s17, v108
	v_mul_f32_e32 v109, s17, v109
	v_mul_f32_e32 v110, s18, v110
	v_mul_f32_e32 v111, s18, v111
	v_mul_f32_e32 v112, s19, v112
	v_mul_f32_e32 v113, s19, v113
	v_cvt_pk_bf16_f32 v158, v98, v100
	v_cvt_pk_bf16_f32 v159, v102, v104
	v_cvt_pk_bf16_f32 v160, v106, v108
	v_cvt_pk_bf16_f32 v161, v110, v112
	v_cvt_pk_bf16_f32 v162, v99, v101
	v_cvt_pk_bf16_f32 v163, v103, v105
	v_cvt_pk_bf16_f32 v164, v107, v109
	v_cvt_pk_bf16_f32 v165, v111, v113
	ds_write_b128 v1, v[158:161] offset:0
	ds_write_b128 v1, v[162:165] offset:128
	v_add_u32_e32 v91, s42, v135
	v_add_u32_e32 v93, s42, v137
	ds_read_b128 v[238:241], v139 offset:19456
	ds_read_b128 v[242:245], v139 offset:21504
	ds_read_b128 v[246:249], v139 offset:23552
	ds_read_b128 v[250:253], v139 offset:25600
	ds_read_b128 v[218:221], v91 offset:0
	ds_read_b128 v[222:225], v91 offset:2048
	ds_read_b128 v[226:229], v91 offset:4096
	ds_read_b128 v[230:233], v91 offset:6144
	s_waitcnt lgkmcnt(0)
	s_load_dwordx8 s[20:27], s[28:29], 0x0
	s_add_u32 s28, s28, 0x100
	s_addc_u32 s29, s29, 0
	v_mfma_f32_16x16x32_bf16 v[78:81], v[238:241], v[218:221], v[78:81]
	v_mfma_f32_16x16x32_bf16 v[74:77], v[242:245], v[218:221], v[74:77]
	v_mfma_f32_16x16x32_bf16 v[70:73], v[246:249], v[218:221], v[70:73]
	v_mfma_f32_16x16x32_bf16 v[66:69], v[250:253], v[218:221], v[66:69]
	ds_read_b128 v[218:221], v93 offset:0
	ds_read_b128 v[142:145], v141 offset:19456
	v_lshl_add_u64 v[132:133], v[132:133], 0, s[40:41]
	global_load_dwordx2 v[98:99], v[132:133], off
	global_load_dwordx2 v[100:101], v[132:133], off offset:2048
	v_mfma_f32_16x16x32_bf16 v[62:65], v[238:241], v[222:225], v[62:65]
	v_mfma_f32_16x16x32_bf16 v[58:61], v[242:245], v[222:225], v[58:61]
	v_mfma_f32_16x16x32_bf16 v[54:57], v[246:249], v[222:225], v[54:57]
	v_mfma_f32_16x16x32_bf16 v[50:53], v[250:253], v[222:225], v[50:53]
	ds_read_b128 v[222:225], v93 offset:2048
	ds_read_b128 v[146:149], v141 offset:21504
	v_lshl_add_u64 v[166:167], v[132:133], 0, s[34:35]
	global_load_dwordx2 v[102:103], v[166:167], off
	global_load_dwordx2 v[104:105], v[166:167], off offset:2048
	v_mfma_f32_16x16x32_bf16 v[46:49], v[238:241], v[226:229], v[46:49]
	v_mfma_f32_16x16x32_bf16 v[42:45], v[242:245], v[226:229], v[42:45]
	v_mfma_f32_16x16x32_bf16 v[38:41], v[246:249], v[226:229], v[38:41]
	v_mfma_f32_16x16x32_bf16 v[34:37], v[250:253], v[226:229], v[34:37]
	ds_read_b128 v[226:229], v93 offset:4096
	ds_read_b128 v[150:153], v141 offset:23552
	v_lshl_add_u64 v[166:167], v[132:133], 0, s[36:37]
	global_load_dwordx2 v[106:107], v[166:167], off
	global_load_dwordx2 v[108:109], v[166:167], off offset:2048
	v_mfma_f32_16x16x32_bf16 v[18:21], v[238:241], v[230:233], v[18:21]
	v_mfma_f32_16x16x32_bf16 v[22:25], v[242:245], v[230:233], v[22:25]
	v_mfma_f32_16x16x32_bf16 v[26:29], v[246:249], v[230:233], v[26:29]
	v_mfma_f32_16x16x32_bf16 v[30:33], v[250:253], v[230:233], v[30:33]
	ds_read_b128 v[230:233], v93 offset:6144
	ds_read_b128 v[154:157], v141 offset:25600
	v_lshl_add_u64 v[166:167], v[132:133], 0, s[38:39]
	global_load_dwordx2 v[110:111], v[166:167], off
	global_load_dwordx2 v[112:113], v[166:167], off offset:2048
	s_waitcnt vmcnt(21)
	s_waitcnt lgkmcnt(0)
	s_barrier
	s_mov_b32 s47, s42
	s_mov_b32 s42, s43
	s_mov_b32 s43, s44
	s_mov_b32 s44, s47
	s_mov_b32 s46, 13
; #define MU_GLDS_A(buf, kt) do { _Pragma("unroll") for (int i = 0; i < NMU; ++i) \
;         __builtin_amdgcn_global_load_lds((const unsigned*)((const char*)A + aoff[i] + (size_t)(kt) * 128), (PG8_LAS unsigned*)(MU_SA(buf) + wid * 1024 + i * 8192), 16, 0, 0); } while (0)
; #define MU_B_ISSUE(sb, kt) do { const char* kb_ = Bb + (size_t)(kt) * (64 * (size_t)RB); _Pragma("unroll") for (int j = 0; j < 8; ++j) { const char* p_ = kb_ + (size_t)j * RB; \
;         asm volatile("global_load_dwordx2 %0, %1, off" : "=&v"(sb[j]) : "v"(p_) : "memory"); } } while (0)
; #define MU_B_WAIT(sb, N) asm volatile("s_waitcnt vmcnt(%8)" : "+v"(sb[0]), "+v"(sb[1]), "+v"(sb[2]), "+v"(sb[3]), "+v"(sb[4]), "+v"(sb[5]), "+v"(sb[6]), "+v"(sb[7]) : "n"(N) : "memory")
; #define MU_COMPUTE(buf) MU_COMPUTE_N(buf, NMU)
; template <int MODE>
; __device__ __forceinline__ void moe_unit(PG8_LAS unsigned char* lds, int e, int cb, int slot0  , int nv  , const bf16_t* A, const int* slot_tok,
;                                          const float* W0, const float* W1, bf16_t* OUT, const float* slot_rs  , const int* slot_dst) {
;     ...
;     f32x4 acc[NMU][4];
; #pragma unroll
;     for (int m = 0; m < NMU; ++m)
; #pragma unroll
;         for (int n = 0; n < 4; ++n) acc[m][n] = (f32x4){0.f, 0.f, 0.f, 0.f};
;     f32x2 s0[8], s1[8];
;     float g0[8];
;     MU_GLDS_A(0, 0); MU_B_ISSUE(s0, 0); MU_G_LOAD(g0, 0); MU_B_ISSUE(s1, 1);
;     MU_B_WAIT(s0, 8); MU_B_WRITE(s0, 0, g0); __builtin_amdgcn_sched_barrier(0); MU_B_ISSUE(s0, 2);
;     asm volatile("s_waitcnt vmcnt(16)" ::: "memory");
;     asm volatile("s_waitcnt lgkmcnt(0)" ::: "memory"); __builtin_amdgcn_s_barrier(); asm volatile("" ::: "memory");
; #pragma unroll 1
;     for (int t = 0; t < nt; t += 2) {
;         if (t + 2 < nt) MU_B_WAIT(s1, 8); else MU_B_WAIT(s1, 0);
;         MU_G_LOAD(g0, t + 1); MU_B_WRITE(s1, 1, g0); __builtin_amdgcn_sched_barrier(0); MU_GLDS_A(1, t + 1); __builtin_amdgcn_sched_barrier(0);
;         if (t + 3 < nt) { MU_B_ISSUE(s1, t + 3); }
;         MU_COMPUTE(0);
;         MU_END(t + 3 >= nt);
;         if (t + 2 < nt) { MU_B_WAIT(s0, 8); MU_G_LOAD(g0, t + 2); MU_B_WRITE(s0, 0, g0); __builtin_amdgcn_sched_barrier(0); MU_GLDS_A(0, t + 2); __builtin_amdgcn_sched_barrier(0); }
;         if (t + 4 < nt) { MU_B_ISSUE(s0, t + 4); }
;         MU_COMPUTE(1);
;         MU_END(t + 4 >= nt);
.Lmu_loop_Y4:
	s_add_i32 s47, s44, s6
	s_add_u32 s30, s30, 0x80
	s_addc_u32 s31, s31, 0
	v_mfma_f32_16x16x32_bf16 v[78:81], v[142:145], v[218:221], v[78:81]
	v_mfma_f32_16x16x32_bf16 v[74:77], v[146:149], v[218:221], v[74:77]
	v_mfma_f32_16x16x32_bf16 v[70:73], v[150:153], v[218:221], v[70:73]
	v_mfma_f32_16x16x32_bf16 v[66:69], v[154:157], v[218:221], v[66:69]
	s_mov_b32 m0, s47
	s_nop 0
	global_load_lds_dwordx4 v86, s[30:31]
	v_mfma_f32_16x16x32_bf16 v[62:65], v[142:145], v[222:225], v[62:65]
	v_mfma_f32_16x16x32_bf16 v[58:61], v[146:149], v[222:225], v[58:61]
	v_mfma_f32_16x16x32_bf16 v[54:57], v[150:153], v[222:225], v[54:57]
	v_mfma_f32_16x16x32_bf16 v[50:53], v[154:157], v[222:225], v[50:53]
	s_add_i32 m0, s47, 0x2000
	s_nop 0
	global_load_lds_dwordx4 v134, s[30:31]
	v_mfma_f32_16x16x32_bf16 v[46:49], v[142:145], v[226:229], v[46:49]
	v_mfma_f32_16x16x32_bf16 v[42:45], v[146:149], v[226:229], v[42:45]
	v_mfma_f32_16x16x32_bf16 v[38:41], v[150:153], v[226:229], v[38:41]
	v_mfma_f32_16x16x32_bf16 v[34:37], v[154:157], v[226:229], v[34:37]
	s_add_i32 m0, s47, 0x4000
	s_nop 0
	global_load_lds_dwordx4 v136, s[30:31]
	v_mfma_f32_16x16x32_bf16 v[18:21], v[142:145], v[230:233], v[18:21]
	v_mfma_f32_16x16x32_bf16 v[22:25], v[146:149], v[230:233], v[22:25]
	v_mfma_f32_16x16x32_bf16 v[26:29], v[150:153], v[230:233], v[26:29]
	v_mfma_f32_16x16x32_bf16 v[30:33], v[154:157], v[230:233], v[30:33]
	s_add_i32 m0, s47, 0x6000
	s_nop 0
	global_load_lds_dwordx4 v138, s[30:31]
	s_add_i32 m0, s47, 0x8000
	s_nop 0
	global_load_lds_dwordx4 v140, s[30:31]
	v_mul_f32_e32 v114, s20, v114
	v_mul_f32_e32 v115, s20, v115
	v_mul_f32_e32 v116, s21, v116
	v_mul_f32_e32 v117, s21, v117
	v_mul_f32_e32 v118, s22, v118
	v_mul_f32_e32 v119, s22, v119
	v_mul_f32_e32 v120, s23, v120
	v_mul_f32_e32 v121, s23, v121
	v_mul_f32_e32 v122, s24, v122
	v_mul_f32_e32 v123, s24, v123
	v_mul_f32_e32 v124, s25, v124
	v_mul_f32_e32 v125, s25, v125
	v_mul_f32_e32 v126, s26, v126
	v_mul_f32_e32 v127, s26, v127
	v_mul_f32_e32 v128, s27, v128
	v_mul_f32_e32 v129, s27, v129
	v_cvt_pk_bf16_f32 v158, v114, v116
	v_cvt_pk_bf16_f32 v159, v118, v120
	v_cvt_pk_bf16_f32 v160, v122, v124
	v_cvt_pk_bf16_f32 v161, v126, v128
	v_cvt_pk_bf16_f32 v162, v115, v117
	v_cvt_pk_bf16_f32 v163, v119, v121
	v_cvt_pk_bf16_f32 v164, v123, v125
	v_cvt_pk_bf16_f32 v165, v127, v129
	ds_write_b128 v1, v[158:161] offset:19456
	ds_write_b128 v1, v[162:165] offset:19584
	v_add_u32_e32 v91, s42, v135
	v_add_u32_e32 v93, s42, v137
	ds_read_b128 v[238:241], v139 offset:0
	ds_read_b128 v[242:245], v139 offset:2048
	ds_read_b128 v[246:249], v139 offset:4096
	ds_read_b128 v[250:253], v139 offset:6144
	ds_read_b128 v[218:221], v91 offset:0
	ds_read_b128 v[222:225], v91 offset:2048
	ds_read_b128 v[226:229], v91 offset:4096
	ds_read_b128 v[230:233], v91 offset:6144
	s_waitcnt lgkmcnt(0)
	s_load_dwordx8 s[12:19], s[28:29], 0x0
	s_add_u32 s28, s28, 0x100
	s_addc_u32 s29, s29, 0
	v_mfma_f32_16x16x32_bf16 v[78:81], v[238:241], v[218:221], v[78:81]
	v_mfma_f32_16x16x32_bf16 v[74:77], v[242:245], v[218:221], v[74:77]
	v_mfma_f32_16x16x32_bf16 v[70:73], v[246:249], v[218:221], v[70:73]
	v_mfma_f32_16x16x32_bf16 v[66:69], v[250:253], v[218:221], v[66:69]
	ds_read_b128 v[218:221], v93 offset:0
	ds_read_b128 v[142:145], v141 offset:0
	v_lshl_add_u64 v[132:133], v[132:133], 0, s[40:41]
	global_load_dwordx2 v[114:115], v[132:133], off
	global_load_dwordx2 v[116:117], v[132:133], off offset:2048
	v_mfma_f32_16x16x32_bf16 v[62:65], v[238:241], v[222:225], v[62:65]
	v_mfma_f32_16x16x32_bf16 v[58:61], v[242:245], v[222:225], v[58:61]
	v_mfma_f32_16x16x32_bf16 v[54:57], v[246:249], v[222:225], v[54:57]
	v_mfma_f32_16x16x32_bf16 v[50:53], v[250:253], v[222:225], v[50:53]
	ds_read_b128 v[222:225], v93 offset:2048
	ds_read_b128 v[146:149], v141 offset:2048
	v_lshl_add_u64 v[166:167], v[132:133], 0, s[34:35]
	global_load_dwordx2 v[118:119], v[166:167], off
	global_load_dwordx2 v[120:121], v[166:167], off offset:2048
	v_mfma_f32_16x16x32_bf16 v[46:49], v[238:241], v[226:229], v[46:49]
	v_mfma_f32_16x16x32_bf16 v[42:45], v[242:245], v[226:229], v[42:45]
	v_mfma_f32_16x16x32_bf16 v[38:41], v[246:249], v[226:229], v[38:41]
	v_mfma_f32_16x16x32_bf16 v[34:37], v[250:253], v[226:229], v[34:37]
	ds_read_b128 v[226:229], v93 offset:4096
	ds_read_b128 v[150:153], v141 offset:4096
	v_lshl_add_u64 v[166:167], v[132:133], 0, s[36:37]
	global_load_dwordx2 v[122:123], v[166:167], off
	global_load_dwordx2 v[124:125], v[166:167], off offset:2048
	v_mfma_f32_16x16x32_bf16 v[18:21], v[238:241], v[230:233], v[18:21]
	v_mfma_f32_16x16x32_bf16 v[22:25], v[242:245], v[230:233], v[22:25]
	v_mfma_f32_16x16x32_bf16 v[26:29], v[246:249], v[230:233], v[26:29]
	v_mfma_f32_16x16x32_bf16 v[30:33], v[250:253], v[230:233], v[30:33]
	ds_read_b128 v[230:233], v93 offset:6144
	ds_read_b128 v[154:157], v141 offset:6144
	v_lshl_add_u64 v[166:167], v[132:133], 0, s[38:39]
	global_load_dwordx2 v[126:127], v[166:167], off
	global_load_dwordx2 v[128:129], v[166:167], off offset:2048
	s_waitcnt vmcnt(21)
	s_waitcnt lgkmcnt(0)
	s_barrier
; #define MU_GLDS_A(buf, kt) do { _Pragma("unroll") for (int i = 0; i < NMU; ++i) \
;         __builtin_amdgcn_global_load_lds((const unsigned*)((const char*)A + aoff[i] + (size_t)(kt) * 128), (PG8_LAS unsigned*)(MU_SA(buf) + wid * 1024 + i * 8192), 16, 0, 0); } while (0)
; #define MU_B_ISSUE(sb, kt) do { const char* kb_ = Bb + (size_t)(kt) * (64 * (size_t)RB); _Pragma("unroll") for (int j = 0; j < 8; ++j) { const char* p_ = kb_ + (size_t)j * RB; \
;         asm volatile("global_load_dwordx2 %0, %1, off" : "=&v"(sb[j]) : "v"(p_) : "memory"); } } while (0)
; #define MU_B_WAIT(sb, N) asm volatile("s_waitcnt vmcnt(%8)" : "+v"(sb[0]), "+v"(sb[1]), "+v"(sb[2]), "+v"(sb[3]), "+v"(sb[4]), "+v"(sb[5]), "+v"(sb[6]), "+v"(sb[7]) : "n"(N) : "memory")
; #define MU_COMPUTE(buf) MU_COMPUTE_N(buf, NMU)
; template <int MODE>
; __device__ __forceinline__ void moe_unit(PG8_LAS unsigned char* lds, int e, int cb, int slot0  , int nv  , const bf16_t* A, const int* slot_tok,
;                                          const float* W0, const float* W1, bf16_t* OUT, const float* slot_rs  , const int* slot_dst) {
;     ...
;     f32x4 acc[NMU][4];
; #pragma unroll
;     for (int m = 0; m < NMU; ++m)
; #pragma unroll
;         for (int n = 0; n < 4; ++n) acc[m][n] = (f32x4){0.f, 0.f, 0.f, 0.f};
;     f32x2 s0[8], s1[8];
;     float g0[8];
;     MU_GLDS_A(0, 0); MU_B_ISSUE(s0, 0); MU_G_LOAD(g0, 0); MU_B_ISSUE(s1, 1);
;     MU_B_WAIT(s0, 8); MU_B_WRITE(s0, 0, g0); __builtin_amdgcn_sched_barrier(0); MU_B_ISSUE(s0, 2);
;     asm volatile("s_waitcnt vmcnt(16)" ::: "memory");
;     asm volatile("s_waitcnt lgkmcnt(0)" ::: "memory"); __builtin_amdgcn_s_barrier(); asm volatile("" ::: "memory");
; #pragma unroll 1
;     for (int t = 0; t < nt; t += 2) {
;         if (t + 2 < nt) MU_B_WAIT(s1, 8); else MU_B_WAIT(s1, 0);
;         MU_G_LOAD(g0, t + 1); MU_B_WRITE(s1, 1, g0); __builtin_amdgcn_sched_barrier(0); MU_GLDS_A(1, t + 1); __builtin_amdgcn_sched_barrier(0);
;         if (t + 3 < nt) { MU_B_ISSUE(s1, t + 3); }
;         MU_COMPUTE(0);
;         MU_END(t + 3 >= nt);
;         if (t + 2 < nt) { MU_B_WAIT(s0, 8); MU_G_LOAD(g0, t + 2); MU_B_WRITE(s0, 0, g0); __builtin_amdgcn_sched_barrier(0); MU_GLDS_A(0, t + 2); __builtin_amdgcn_sched_barrier(0); }
;         if (t + 4 < nt) { MU_B_ISSUE(s0, t + 4); }
;         MU_COMPUTE(1);
;         MU_END(t + 4 >= nt);
	s_mov_b32 s47, s42
	s_mov_b32 s42, s43
	s_mov_b32 s43, s44
	s_mov_b32 s44, s47
	s_add_i32 s47, s44, s6
	s_add_u32 s30, s30, 0x80
	s_addc_u32 s31, s31, 0
	v_mfma_f32_16x16x32_bf16 v[78:81], v[142:145], v[218:221], v[78:81]
	v_mfma_f32_16x16x32_bf16 v[74:77], v[146:149], v[218:221], v[74:77]
	v_mfma_f32_16x16x32_bf16 v[70:73], v[150:153], v[218:221], v[70:73]
	v_mfma_f32_16x16x32_bf16 v[66:69], v[154:157], v[218:221], v[66:69]
	s_mov_b32 m0, s47
	s_nop 0
	global_load_lds_dwordx4 v86, s[30:31]
	v_mfma_f32_16x16x32_bf16 v[62:65], v[142:145], v[222:225], v[62:65]
	v_mfma_f32_16x16x32_bf16 v[58:61], v[146:149], v[222:225], v[58:61]
	v_mfma_f32_16x16x32_bf16 v[54:57], v[150:153], v[222:225], v[54:57]
	v_mfma_f32_16x16x32_bf16 v[50:53], v[154:157], v[222:225], v[50:53]
	s_add_i32 m0, s47, 0x2000
	s_nop 0
	global_load_lds_dwordx4 v134, s[30:31]
	v_mfma_f32_16x16x32_bf16 v[46:49], v[142:145], v[226:229], v[46:49]
	v_mfma_f32_16x16x32_bf16 v[42:45], v[146:149], v[226:229], v[42:45]
	v_mfma_f32_16x16x32_bf16 v[38:41], v[150:153], v[226:229], v[38:41]
	v_mfma_f32_16x16x32_bf16 v[34:37], v[154:157], v[226:229], v[34:37]
	s_add_i32 m0, s47, 0x4000
	s_nop 0
	global_load_lds_dwordx4 v136, s[30:31]
	v_mfma_f32_16x16x32_bf16 v[18:21], v[142:145], v[230:233], v[18:21]
	v_mfma_f32_16x16x32_bf16 v[22:25], v[146:149], v[230:233], v[22:25]
	v_mfma_f32_16x16x32_bf16 v[26:29], v[150:153], v[230:233], v[26:29]
	v_mfma_f32_16x16x32_bf16 v[30:33], v[154:157], v[230:233], v[30:33]
	s_add_i32 m0, s47, 0x6000
	s_nop 0
	global_load_lds_dwordx4 v138, s[30:31]
	s_add_i32 m0, s47, 0x8000
	s_nop 0
	global_load_lds_dwordx4 v140, s[30:31]
	v_mul_f32_e32 v186, s12, v186
	v_mul_f32_e32 v187, s12, v187
	v_mul_f32_e32 v188, s13, v188
	v_mul_f32_e32 v189, s13, v189
	v_mul_f32_e32 v190, s14, v190
	v_mul_f32_e32 v191, s14, v191
	v_mul_f32_e32 v192, s15, v192
	v_mul_f32_e32 v193, s15, v193
	v_mul_f32_e32 v194, s16, v194
	v_mul_f32_e32 v195, s16, v195
	v_mul_f32_e32 v196, s17, v196
	v_mul_f32_e32 v197, s17, v197
	v_mul_f32_e32 v198, s18, v198
	v_mul_f32_e32 v199, s18, v199
	v_mul_f32_e32 v200, s19, v200
	v_mul_f32_e32 v201, s19, v201
	v_cvt_pk_bf16_f32 v158, v186, v188
	v_cvt_pk_bf16_f32 v159, v190, v192
	v_cvt_pk_bf16_f32 v160, v194, v196
	v_cvt_pk_bf16_f32 v161, v198, v200
	v_cvt_pk_bf16_f32 v162, v187, v189
	v_cvt_pk_bf16_f32 v163, v191, v193
	v_cvt_pk_bf16_f32 v164, v195, v197
	v_cvt_pk_bf16_f32 v165, v199, v201
	ds_write_b128 v1, v[158:161] offset:0
	ds_write_b128 v1, v[162:165] offset:128
	v_add_u32_e32 v91, s42, v135
	v_add_u32_e32 v93, s42, v137
	ds_read_b128 v[238:241], v139 offset:19456
	ds_read_b128 v[242:245], v139 offset:21504
	ds_read_b128 v[246:249], v139 offset:23552
	ds_read_b128 v[250:253], v139 offset:25600
	ds_read_b128 v[218:221], v91 offset:0
	ds_read_b128 v[222:225], v91 offset:2048
	ds_read_b128 v[226:229], v91 offset:4096
	ds_read_b128 v[230:233], v91 offset:6144
	s_waitcnt lgkmcnt(0)
	s_load_dwordx8 s[20:27], s[28:29], 0x0
	s_add_u32 s28, s28, 0x100
	s_addc_u32 s29, s29, 0
	v_mfma_f32_16x16x32_bf16 v[78:81], v[238:241], v[218:221], v[78:81]
	v_mfma_f32_16x16x32_bf16 v[74:77], v[242:245], v[218:221], v[74:77]
	v_mfma_f32_16x16x32_bf16 v[70:73], v[246:249], v[218:221], v[70:73]
	v_mfma_f32_16x16x32_bf16 v[66:69], v[250:253], v[218:221], v[66:69]
	ds_read_b128 v[218:221], v93 offset:0
	ds_read_b128 v[142:145], v141 offset:19456
	v_lshl_add_u64 v[132:133], v[132:133], 0, s[40:41]
	global_load_dwordx2 v[186:187], v[132:133], off
	global_load_dwordx2 v[188:189], v[132:133], off offset:2048
	v_mfma_f32_16x16x32_bf16 v[62:65], v[238:241], v[222:225], v[62:65]
	v_mfma_f32_16x16x32_bf16 v[58:61], v[242:245], v[222:225], v[58:61]
	v_mfma_f32_16x16x32_bf16 v[54:57], v[246:249], v[222:225], v[54:57]
	v_mfma_f32_16x16x32_bf16 v[50:53], v[250:253], v[222:225], v[50:53]
	ds_read_b128 v[222:225], v93 offset:2048
	ds_read_b128 v[146:149], v141 offset:21504
	v_lshl_add_u64 v[166:167], v[132:133], 0, s[34:35]
	global_load_dwordx2 v[190:191], v[166:167], off
	global_load_dwordx2 v[192:193], v[166:167], off offset:2048
	v_mfma_f32_16x16x32_bf16 v[46:49], v[238:241], v[226:229], v[46:49]
	v_mfma_f32_16x16x32_bf16 v[42:45], v[242:245], v[226:229], v[42:45]
	v_mfma_f32_16x16x32_bf16 v[38:41], v[246:249], v[226:229], v[38:41]
	v_mfma_f32_16x16x32_bf16 v[34:37], v[250:253], v[226:229], v[34:37]
	ds_read_b128 v[226:229], v93 offset:4096
	ds_read_b128 v[150:153], v141 offset:23552
	v_lshl_add_u64 v[166:167], v[132:133], 0, s[36:37]
	global_load_dwordx2 v[194:195], v[166:167], off
	global_load_dwordx2 v[196:197], v[166:167], off offset:2048
	v_mfma_f32_16x16x32_bf16 v[18:21], v[238:241], v[230:233], v[18:21]
	v_mfma_f32_16x16x32_bf16 v[22:25], v[242:245], v[230:233], v[22:25]
	v_mfma_f32_16x16x32_bf16 v[26:29], v[246:249], v[230:233], v[26:29]
	v_mfma_f32_16x16x32_bf16 v[30:33], v[250:253], v[230:233], v[30:33]
	ds_read_b128 v[230:233], v93 offset:6144
	ds_read_b128 v[154:157], v141 offset:25600
	v_lshl_add_u64 v[166:167], v[132:133], 0, s[38:39]
	global_load_dwordx2 v[198:199], v[166:167], off
	global_load_dwordx2 v[200:201], v[166:167], off offset:2048
	s_waitcnt vmcnt(21)
	s_waitcnt lgkmcnt(0)
	s_barrier
; #define MU_GLDS_A(buf, kt) do { _Pragma("unroll") for (int i = 0; i < NMU; ++i) \
;         __builtin_amdgcn_global_load_lds((const unsigned*)((const char*)A + aoff[i] + (size_t)(kt) * 128), (PG8_LAS unsigned*)(MU_SA(buf) + wid * 1024 + i * 8192), 16, 0, 0); } while (0)
; #define MU_B_ISSUE(sb, kt) do { const char* kb_ = Bb + (size_t)(kt) * (64 * (size_t)RB); _Pragma("unroll") for (int j = 0; j < 8; ++j) { const char* p_ = kb_ + (size_t)j * RB; \
;         asm volatile("global_load_dwordx2 %0, %1, off" : "=&v"(sb[j]) : "v"(p_) : "memory"); } } while (0)
; #define MU_B_WAIT(sb, N) asm volatile("s_waitcnt vmcnt(%8)" : "+v"(sb[0]), "+v"(sb[1]), "+v"(sb[2]), "+v"(sb[3]), "+v"(sb[4]), "+v"(sb[5]), "+v"(sb[6]), "+v"(sb[7]) : "n"(N) : "memory")
; #define MU_COMPUTE(buf) MU_COMPUTE_N(buf, NMU)
; template <int MODE>
; __device__ __forceinline__ void moe_unit(PG8_LAS unsigned char* lds, int e, int cb, int slot0  , int nv  , const bf16_t* A, const int* slot_tok,
;                                          const float* W0, const float* W1, bf16_t* OUT, const float* slot_rs  , const int* slot_dst) {
;     ...
;     f32x4 acc[NMU][4];
; #pragma unroll
;     for (int m = 0; m < NMU; ++m)
; #pragma unroll
;         for (int n = 0; n < 4; ++n) acc[m][n] = (f32x4){0.f, 0.f, 0.f, 0.f};
;     f32x2 s0[8], s1[8];
;     float g0[8];
;     MU_GLDS_A(0, 0); MU_B_ISSUE(s0, 0); MU_G_LOAD(g0, 0); MU_B_ISSUE(s1, 1);
;     MU_B_WAIT(s0, 8); MU_B_WRITE(s0, 0, g0); __builtin_amdgcn_sched_barrier(0); MU_B_ISSUE(s0, 2);
;     asm volatile("s_waitcnt vmcnt(16)" ::: "memory");
;     asm volatile("s_waitcnt lgkmcnt(0)" ::: "memory"); __builtin_amdgcn_s_barrier(); asm volatile("" ::: "memory");
; #pragma unroll 1
;     for (int t = 0; t < nt; t += 2) {
;         if (t + 2 < nt) MU_B_WAIT(s1, 8); else MU_B_WAIT(s1, 0);
;         MU_G_LOAD(g0, t + 1); MU_B_WRITE(s1, 1, g0); __builtin_amdgcn_sched_barrier(0); MU_GLDS_A(1, t + 1); __builtin_amdgcn_sched_barrier(0);
;         if (t + 3 < nt) { MU_B_ISSUE(s1, t + 3); }
;         MU_COMPUTE(0);
;         MU_END(t + 3 >= nt);
;         if (t + 2 < nt) { MU_B_WAIT(s0, 8); MU_G_LOAD(g0, t + 2); MU_B_WRITE(s0, 0, g0); __builtin_amdgcn_sched_barrier(0); MU_GLDS_A(0, t + 2); __builtin_amdgcn_sched_barrier(0); }
;         if (t + 4 < nt) { MU_B_ISSUE(s0, t + 4); }
;         MU_COMPUTE(1);
;         MU_END(t + 4 >= nt);
	s_mov_b32 s47, s42
	s_mov_b32 s42, s43
	s_mov_b32 s43, s44
	s_mov_b32 s44, s47
	s_add_i32 s47, s44, s6
	s_add_u32 s30, s30, 0x80
	s_addc_u32 s31, s31, 0
	v_mfma_f32_16x16x32_bf16 v[78:81], v[142:145], v[218:221], v[78:81]
	v_mfma_f32_16x16x32_bf16 v[74:77], v[146:149], v[218:221], v[74:77]
	v_mfma_f32_16x16x32_bf16 v[70:73], v[150:153], v[218:221], v[70:73]
	v_mfma_f32_16x16x32_bf16 v[66:69], v[154:157], v[218:221], v[66:69]
	s_mov_b32 m0, s47
	s_nop 0
	global_load_lds_dwordx4 v86, s[30:31]
	v_mfma_f32_16x16x32_bf16 v[62:65], v[142:145], v[222:225], v[62:65]
	v_mfma_f32_16x16x32_bf16 v[58:61], v[146:149], v[222:225], v[58:61]
	v_mfma_f32_16x16x32_bf16 v[54:57], v[150:153], v[222:225], v[54:57]
	v_mfma_f32_16x16x32_bf16 v[50:53], v[154:157], v[222:225], v[50:53]
	s_add_i32 m0, s47, 0x2000
	s_nop 0
	global_load_lds_dwordx4 v134, s[30:31]
	v_mfma_f32_16x16x32_bf16 v[46:49], v[142:145], v[226:229], v[46:49]
	v_mfma_f32_16x16x32_bf16 v[42:45], v[146:149], v[226:229], v[42:45]
	v_mfma_f32_16x16x32_bf16 v[38:41], v[150:153], v[226:229], v[38:41]
	v_mfma_f32_16x16x32_bf16 v[34:37], v[154:157], v[226:229], v[34:37]
	s_add_i32 m0, s47, 0x4000
	s_nop 0
	global_load_lds_dwordx4 v136, s[30:31]
	v_mfma_f32_16x16x32_bf16 v[18:21], v[142:145], v[230:233], v[18:21]
	v_mfma_f32_16x16x32_bf16 v[22:25], v[146:149], v[230:233], v[22:25]
	v_mfma_f32_16x16x32_bf16 v[26:29], v[150:153], v[230:233], v[26:29]
	v_mfma_f32_16x16x32_bf16 v[30:33], v[154:157], v[230:233], v[30:33]
	s_add_i32 m0, s47, 0x6000
	s_nop 0
	global_load_lds_dwordx4 v138, s[30:31]
	s_add_i32 m0, s47, 0x8000
	s_nop 0
	global_load_lds_dwordx4 v140, s[30:31]
	v_mul_f32_e32 v202, s20, v202
	v_mul_f32_e32 v203, s20, v203
	v_mul_f32_e32 v204, s21, v204
	v_mul_f32_e32 v205, s21, v205
	v_mul_f32_e32 v206, s22, v206
	v_mul_f32_e32 v207, s22, v207
	v_mul_f32_e32 v208, s23, v208
	v_mul_f32_e32 v209, s23, v209
	v_mul_f32_e32 v210, s24, v210
	v_mul_f32_e32 v211, s24, v211
	v_mul_f32_e32 v212, s25, v212
	v_mul_f32_e32 v213, s25, v213
	v_mul_f32_e32 v214, s26, v214
	v_mul_f32_e32 v215, s26, v215
	v_mul_f32_e32 v216, s27, v216
	v_mul_f32_e32 v217, s27, v217
	v_cvt_pk_bf16_f32 v158, v202, v204
	v_cvt_pk_bf16_f32 v159, v206, v208
	v_cvt_pk_bf16_f32 v160, v210, v212
	v_cvt_pk_bf16_f32 v161, v214, v216
	v_cvt_pk_bf16_f32 v162, v203, v205
	v_cvt_pk_bf16_f32 v163, v207, v209
	v_cvt_pk_bf16_f32 v164, v211, v213
	v_cvt_pk_bf16_f32 v165, v215, v217
	ds_write_b128 v1, v[158:161] offset:19456
	ds_write_b128 v1, v[162:165] offset:19584
	v_add_u32_e32 v91, s42, v135
	v_add_u32_e32 v93, s42, v137
	ds_read_b128 v[238:241], v139 offset:0
	ds_read_b128 v[242:245], v139 offset:2048
	ds_read_b128 v[246:249], v139 offset:4096
	ds_read_b128 v[250:253], v139 offset:6144
	ds_read_b128 v[218:221], v91 offset:0
	ds_read_b128 v[222:225], v91 offset:2048
	ds_read_b128 v[226:229], v91 offset:4096
	ds_read_b128 v[230:233], v91 offset:6144
	s_waitcnt lgkmcnt(0)
	s_load_dwordx8 s[12:19], s[28:29], 0x0
	s_add_u32 s28, s28, 0x100
	s_addc_u32 s29, s29, 0
	v_mfma_f32_16x16x32_bf16 v[78:81], v[238:241], v[218:221], v[78:81]
	v_mfma_f32_16x16x32_bf16 v[74:77], v[242:245], v[218:221], v[74:77]
	v_mfma_f32_16x16x32_bf16 v[70:73], v[246:249], v[218:221], v[70:73]
	v_mfma_f32_16x16x32_bf16 v[66:69], v[250:253], v[218:221], v[66:69]
	ds_read_b128 v[218:221], v93 offset:0
	ds_read_b128 v[142:145], v141 offset:0
	v_lshl_add_u64 v[132:133], v[132:133], 0, s[40:41]
	global_load_dwordx2 v[202:203], v[132:133], off
	global_load_dwordx2 v[204:205], v[132:133], off offset:2048
	v_mfma_f32_16x16x32_bf16 v[62:65], v[238:241], v[222:225], v[62:65]
	v_mfma_f32_16x16x32_bf16 v[58:61], v[242:245], v[222:225], v[58:61]
	v_mfma_f32_16x16x32_bf16 v[54:57], v[246:249], v[222:225], v[54:57]
	v_mfma_f32_16x16x32_bf16 v[50:53], v[250:253], v[222:225], v[50:53]
	ds_read_b128 v[222:225], v93 offset:2048
	ds_read_b128 v[146:149], v141 offset:2048
	v_lshl_add_u64 v[166:167], v[132:133], 0, s[34:35]
	global_load_dwordx2 v[206:207], v[166:167], off
	global_load_dwordx2 v[208:209], v[166:167], off offset:2048
	v_mfma_f32_16x16x32_bf16 v[46:49], v[238:241], v[226:229], v[46:49]
	v_mfma_f32_16x16x32_bf16 v[42:45], v[242:245], v[226:229], v[42:45]
	v_mfma_f32_16x16x32_bf16 v[38:41], v[246:249], v[226:229], v[38:41]
	v_mfma_f32_16x16x32_bf16 v[34:37], v[250:253], v[226:229], v[34:37]
	ds_read_b128 v[226:229], v93 offset:4096
	ds_read_b128 v[150:153], v141 offset:4096
	v_lshl_add_u64 v[166:167], v[132:133], 0, s[36:37]
	global_load_dwordx2 v[210:211], v[166:167], off
	global_load_dwordx2 v[212:213], v[166:167], off offset:2048
	v_mfma_f32_16x16x32_bf16 v[18:21], v[238:241], v[230:233], v[18:21]
	v_mfma_f32_16x16x32_bf16 v[22:25], v[242:245], v[230:233], v[22:25]
	v_mfma_f32_16x16x32_bf16 v[26:29], v[246:249], v[230:233], v[26:29]
	v_mfma_f32_16x16x32_bf16 v[30:33], v[250:253], v[230:233], v[30:33]
	ds_read_b128 v[230:233], v93 offset:6144
	ds_read_b128 v[154:157], v141 offset:6144
	v_lshl_add_u64 v[166:167], v[132:133], 0, s[38:39]
	global_load_dwordx2 v[214:215], v[166:167], off
	global_load_dwordx2 v[216:217], v[166:167], off offset:2048
	s_waitcnt vmcnt(21)
	s_waitcnt lgkmcnt(0)
	s_barrier
; #define MU_GLDS_A(buf, kt) do { _Pragma("unroll") for (int i = 0; i < NMU; ++i) \
;         __builtin_amdgcn_global_load_lds((const unsigned*)((const char*)A + aoff[i] + (size_t)(kt) * 128), (PG8_LAS unsigned*)(MU_SA(buf) + wid * 1024 + i * 8192), 16, 0, 0); } while (0)
; #define MU_B_ISSUE(sb, kt) do { const char* kb_ = Bb + (size_t)(kt) * (64 * (size_t)RB); _Pragma("unroll") for (int j = 0; j < 8; ++j) { const char* p_ = kb_ + (size_t)j * RB; \
;         asm volatile("global_load_dwordx2 %0, %1, off" : "=&v"(sb[j]) : "v"(p_) : "memory"); } } while (0)
; #define MU_B_WAIT(sb, N) asm volatile("s_waitcnt vmcnt(%8)" : "+v"(sb[0]), "+v"(sb[1]), "+v"(sb[2]), "+v"(sb[3]), "+v"(sb[4]), "+v"(sb[5]), "+v"(sb[6]), "+v"(sb[7]) : "n"(N) : "memory")
; #define MU_COMPUTE(buf) MU_COMPUTE_N(buf, NMU)
; template <int MODE>
; __device__ __forceinline__ void moe_unit(PG8_LAS unsigned char* lds, int e, int cb, int slot0  , int nv  , const bf16_t* A, const int* slot_tok,
;                                          const float* W0, const float* W1, bf16_t* OUT, const float* slot_rs  , const int* slot_dst) {
;     ...
;     f32x4 acc[NMU][4];
; #pragma unroll
;     for (int m = 0; m < NMU; ++m)
; #pragma unroll
;         for (int n = 0; n < 4; ++n) acc[m][n] = (f32x4){0.f, 0.f, 0.f, 0.f};
;     f32x2 s0[8], s1[8];
;     float g0[8];
;     MU_GLDS_A(0, 0); MU_B_ISSUE(s0, 0); MU_G_LOAD(g0, 0); MU_B_ISSUE(s1, 1);
;     MU_B_WAIT(s0, 8); MU_B_WRITE(s0, 0, g0); __builtin_amdgcn_sched_barrier(0); MU_B_ISSUE(s0, 2);
;     asm volatile("s_waitcnt vmcnt(16)" ::: "memory");
;     asm volatile("s_waitcnt lgkmcnt(0)" ::: "memory"); __builtin_amdgcn_s_barrier(); asm volatile("" ::: "memory");
; #pragma unroll 1
;     for (int t = 0; t < nt; t += 2) {
;         if (t + 2 < nt) MU_B_WAIT(s1, 8); else MU_B_WAIT(s1, 0);
;         MU_G_LOAD(g0, t + 1); MU_B_WRITE(s1, 1, g0); __builtin_amdgcn_sched_barrier(0); MU_GLDS_A(1, t + 1); __builtin_amdgcn_sched_barrier(0);
;         if (t + 3 < nt) { MU_B_ISSUE(s1, t + 3); }
;         MU_COMPUTE(0);
;         MU_END(t + 3 >= nt);
;         if (t + 2 < nt) { MU_B_WAIT(s0, 8); MU_G_LOAD(g0, t + 2); MU_B_WRITE(s0, 0, g0); __builtin_amdgcn_sched_barrier(0); MU_GLDS_A(0, t + 2); __builtin_amdgcn_sched_barrier(0); }
;         if (t + 4 < nt) { MU_B_ISSUE(s0, t + 4); }
;         MU_COMPUTE(1);
;         MU_END(t + 4 >= nt);
	s_mov_b32 s47, s42
	s_mov_b32 s42, s43
	s_mov_b32 s43, s44
	s_mov_b32 s44, s47
	s_add_i32 s47, s44, s6
	s_add_u32 s30, s30, 0x80
	s_addc_u32 s31, s31, 0
	v_mfma_f32_16x16x32_bf16 v[78:81], v[142:145], v[218:221], v[78:81]
	v_mfma_f32_16x16x32_bf16 v[74:77], v[146:149], v[218:221], v[74:77]
	v_mfma_f32_16x16x32_bf16 v[70:73], v[150:153], v[218:221], v[70:73]
	v_mfma_f32_16x16x32_bf16 v[66:69], v[154:157], v[218:221], v[66:69]
	s_mov_b32 m0, s47
	s_nop 0
	global_load_lds_dwordx4 v86, s[30:31]
	v_mfma_f32_16x16x32_bf16 v[62:65], v[142:145], v[222:225], v[62:65]
	v_mfma_f32_16x16x32_bf16 v[58:61], v[146:149], v[222:225], v[58:61]
	v_mfma_f32_16x16x32_bf16 v[54:57], v[150:153], v[222:225], v[54:57]
	v_mfma_f32_16x16x32_bf16 v[50:53], v[154:157], v[222:225], v[50:53]
	s_add_i32 m0, s47, 0x2000
	s_nop 0
	global_load_lds_dwordx4 v134, s[30:31]
	v_mfma_f32_16x16x32_bf16 v[46:49], v[142:145], v[226:229], v[46:49]
	v_mfma_f32_16x16x32_bf16 v[42:45], v[146:149], v[226:229], v[42:45]
	v_mfma_f32_16x16x32_bf16 v[38:41], v[150:153], v[226:229], v[38:41]
	v_mfma_f32_16x16x32_bf16 v[34:37], v[154:157], v[226:229], v[34:37]
	s_add_i32 m0, s47, 0x4000
	s_nop 0
	global_load_lds_dwordx4 v136, s[30:31]
	v_mfma_f32_16x16x32_bf16 v[18:21], v[142:145], v[230:233], v[18:21]
	v_mfma_f32_16x16x32_bf16 v[22:25], v[146:149], v[230:233], v[22:25]
	v_mfma_f32_16x16x32_bf16 v[26:29], v[150:153], v[230:233], v[26:29]
	v_mfma_f32_16x16x32_bf16 v[30:33], v[154:157], v[230:233], v[30:33]
	s_add_i32 m0, s47, 0x6000
	s_nop 0
	global_load_lds_dwordx4 v138, s[30:31]
	s_add_i32 m0, s47, 0x8000
	s_nop 0
	global_load_lds_dwordx4 v140, s[30:31]
	v_mul_f32_e32 v98, s12, v98
	v_mul_f32_e32 v99, s12, v99
	v_mul_f32_e32 v100, s13, v100
	v_mul_f32_e32 v101, s13, v101
	v_mul_f32_e32 v102, s14, v102
	v_mul_f32_e32 v103, s14, v103
	v_mul_f32_e32 v104, s15, v104
	v_mul_f32_e32 v105, s15, v105
	v_mul_f32_e32 v106, s16, v106
	v_mul_f32_e32 v107, s16, v107
	v_mul_f32_e32 v108, s17, v108
	v_mul_f32_e32 v109, s17, v109
	v_mul_f32_e32 v110, s18, v110
	v_mul_f32_e32 v111, s18, v111
	v_mul_f32_e32 v112, s19, v112
	v_mul_f32_e32 v113, s19, v113
	v_cvt_pk_bf16_f32 v158, v98, v100
	v_cvt_pk_bf16_f32 v159, v102, v104
	v_cvt_pk_bf16_f32 v160, v106, v108
	v_cvt_pk_bf16_f32 v161, v110, v112
	v_cvt_pk_bf16_f32 v162, v99, v101
	v_cvt_pk_bf16_f32 v163, v103, v105
	v_cvt_pk_bf16_f32 v164, v107, v109
	v_cvt_pk_bf16_f32 v165, v111, v113
	ds_write_b128 v1, v[158:161] offset:0
	ds_write_b128 v1, v[162:165] offset:128
	v_add_u32_e32 v91, s42, v135
	v_add_u32_e32 v93, s42, v137
	ds_read_b128 v[238:241], v139 offset:19456
	ds_read_b128 v[242:245], v139 offset:21504
	ds_read_b128 v[246:249], v139 offset:23552
	ds_read_b128 v[250:253], v139 offset:25600
	ds_read_b128 v[218:221], v91 offset:0
	ds_read_b128 v[222:225], v91 offset:2048
	ds_read_b128 v[226:229], v91 offset:4096
	ds_read_b128 v[230:233], v91 offset:6144
	s_waitcnt lgkmcnt(0)
	s_load_dwordx8 s[20:27], s[28:29], 0x0
	s_add_u32 s28, s28, 0x100
	s_addc_u32 s29, s29, 0
	v_mfma_f32_16x16x32_bf16 v[78:81], v[238:241], v[218:221], v[78:81]
	v_mfma_f32_16x16x32_bf16 v[74:77], v[242:245], v[218:221], v[74:77]
	v_mfma_f32_16x16x32_bf16 v[70:73], v[246:249], v[218:221], v[70:73]
	v_mfma_f32_16x16x32_bf16 v[66:69], v[250:253], v[218:221], v[66:69]
	ds_read_b128 v[218:221], v93 offset:0
	ds_read_b128 v[142:145], v141 offset:19456
	v_lshl_add_u64 v[132:133], v[132:133], 0, s[40:41]
	global_load_dwordx2 v[98:99], v[132:133], off
	global_load_dwordx2 v[100:101], v[132:133], off offset:2048
	v_mfma_f32_16x16x32_bf16 v[62:65], v[238:241], v[222:225], v[62:65]
	v_mfma_f32_16x16x32_bf16 v[58:61], v[242:245], v[222:225], v[58:61]
	v_mfma_f32_16x16x32_bf16 v[54:57], v[246:249], v[222:225], v[54:57]
	v_mfma_f32_16x16x32_bf16 v[50:53], v[250:253], v[222:225], v[50:53]
	ds_read_b128 v[222:225], v93 offset:2048
	ds_read_b128 v[146:149], v141 offset:21504
	v_lshl_add_u64 v[166:167], v[132:133], 0, s[34:35]
	global_load_dwordx2 v[102:103], v[166:167], off
	global_load_dwordx2 v[104:105], v[166:167], off offset:2048
	v_mfma_f32_16x16x32_bf16 v[46:49], v[238:241], v[226:229], v[46:49]
	v_mfma_f32_16x16x32_bf16 v[42:45], v[242:245], v[226:229], v[42:45]
	v_mfma_f32_16x16x32_bf16 v[38:41], v[246:249], v[226:229], v[38:41]
	v_mfma_f32_16x16x32_bf16 v[34:37], v[250:253], v[226:229], v[34:37]
	ds_read_b128 v[226:229], v93 offset:4096
	ds_read_b128 v[150:153], v141 offset:23552
	v_lshl_add_u64 v[166:167], v[132:133], 0, s[36:37]
	global_load_dwordx2 v[106:107], v[166:167], off
	global_load_dwordx2 v[108:109], v[166:167], off offset:2048
	v_mfma_f32_16x16x32_bf16 v[18:21], v[238:241], v[230:233], v[18:21]
	v_mfma_f32_16x16x32_bf16 v[22:25], v[242:245], v[230:233], v[22:25]
	v_mfma_f32_16x16x32_bf16 v[26:29], v[246:249], v[230:233], v[26:29]
	v_mfma_f32_16x16x32_bf16 v[30:33], v[250:253], v[230:233], v[30:33]
	ds_read_b128 v[230:233], v93 offset:6144
	ds_read_b128 v[154:157], v141 offset:25600
	v_lshl_add_u64 v[166:167], v[132:133], 0, s[38:39]
	global_load_dwordx2 v[110:111], v[166:167], off
	global_load_dwordx2 v[112:113], v[166:167], off offset:2048
	s_waitcnt vmcnt(21)
	s_waitcnt lgkmcnt(0)
	s_barrier
	s_mov_b32 s47, s42
	s_mov_b32 s42, s43
	s_mov_b32 s43, s44
	s_mov_b32 s44, s47
	s_sub_u32 s46, s46, 1
	s_cmp_lg_u32 s46, 0
	s_cbranch_scc1 .Lmu_loop_Y4
; #define MU_GLDS_A(buf, kt) do { _Pragma("unroll") for (int i = 0; i < NMU; ++i) \
;         __builtin_amdgcn_global_load_lds((const unsigned*)((const char*)A + aoff[i] + (size_t)(kt) * 128), (PG8_LAS unsigned*)(MU_SA(buf) + wid * 1024 + i * 8192), 16, 0, 0); } while (0)
; #define MU_B_ISSUE(sb, kt) do { const char* kb_ = Bb + (size_t)(kt) * (64 * (size_t)RB); _Pragma("unroll") for (int j = 0; j < 8; ++j) { const char* p_ = kb_ + (size_t)j * RB; \
;         asm volatile("global_load_dwordx2 %0, %1, off" : "=&v"(sb[j]) : "v"(p_) : "memory"); } } while (0)
; #define MU_B_WAIT(sb, N) asm volatile("s_waitcnt vmcnt(%8)" : "+v"(sb[0]), "+v"(sb[1]), "+v"(sb[2]), "+v"(sb[3]), "+v"(sb[4]), "+v"(sb[5]), "+v"(sb[6]), "+v"(sb[7]) : "n"(N) : "memory")
; #define MU_COMPUTE(buf) MU_COMPUTE_N(buf, NMU)
; template <int MODE>
; __device__ __forceinline__ void moe_unit(PG8_LAS unsigned char* lds, int e, int cb, int slot0  , int nv  , const bf16_t* A, const int* slot_tok,
;                                          const float* W0, const float* W1, bf16_t* OUT, const float* slot_rs  , const int* slot_dst) {
;     ...
;     f32x4 acc[NMU][4];
; #pragma unroll
;     for (int m = 0; m < NMU; ++m)
; #pragma unroll
;         for (int n = 0; n < 4; ++n) acc[m][n] = (f32x4){0.f, 0.f, 0.f, 0.f};
;     f32x2 s0[8], s1[8];
;     float g0[8];
;     MU_GLDS_A(0, 0); MU_B_ISSUE(s0, 0); MU_G_LOAD(g0, 0); MU_B_ISSUE(s1, 1);
;     MU_B_WAIT(s0, 8); MU_B_WRITE(s0, 0, g0); __builtin_amdgcn_sched_barrier(0); MU_B_ISSUE(s0, 2);
;     asm volatile("s_waitcnt vmcnt(16)" ::: "memory");
;     asm volatile("s_waitcnt lgkmcnt(0)" ::: "memory"); __builtin_amdgcn_s_barrier(); asm volatile("" ::: "memory");
; #pragma unroll 1
;     for (int t = 0; t < nt; t += 2) {
;         if (t + 2 < nt) MU_B_WAIT(s1, 8); else MU_B_WAIT(s1, 0);
;         MU_G_LOAD(g0, t + 1); MU_B_WRITE(s1, 1, g0); __builtin_amdgcn_sched_barrier(0); MU_GLDS_A(1, t + 1); __builtin_amdgcn_sched_barrier(0);
;         if (t + 3 < nt) { MU_B_ISSUE(s1, t + 3); }
;         MU_COMPUTE(0);
;         MU_END(t + 3 >= nt);
;         if (t + 2 < nt) { MU_B_WAIT(s0, 8); MU_G_LOAD(g0, t + 2); MU_B_WRITE(s0, 0, g0); __builtin_amdgcn_sched_barrier(0); MU_GLDS_A(0, t + 2); __builtin_amdgcn_sched_barrier(0); }
;         if (t + 4 < nt) { MU_B_ISSUE(s0, t + 4); }
;         MU_COMPUTE(1);
;         MU_END(t + 4 >= nt);
	s_add_i32 s47, s44, s6
	s_add_u32 s30, s30, 0x80
	s_addc_u32 s31, s31, 0
	v_mfma_f32_16x16x32_bf16 v[78:81], v[142:145], v[218:221], v[78:81]
	v_mfma_f32_16x16x32_bf16 v[74:77], v[146:149], v[218:221], v[74:77]
	v_mfma_f32_16x16x32_bf16 v[70:73], v[150:153], v[218:221], v[70:73]
	v_mfma_f32_16x16x32_bf16 v[66:69], v[154:157], v[218:221], v[66:69]
	s_mov_b32 m0, s47
	s_nop 0
	global_load_lds_dwordx4 v86, s[30:31]
	v_mfma_f32_16x16x32_bf16 v[62:65], v[142:145], v[222:225], v[62:65]
	v_mfma_f32_16x16x32_bf16 v[58:61], v[146:149], v[222:225], v[58:61]
	v_mfma_f32_16x16x32_bf16 v[54:57], v[150:153], v[222:225], v[54:57]
	v_mfma_f32_16x16x32_bf16 v[50:53], v[154:157], v[222:225], v[50:53]
	s_add_i32 m0, s47, 0x2000
	s_nop 0
	global_load_lds_dwordx4 v134, s[30:31]
	v_mfma_f32_16x16x32_bf16 v[46:49], v[142:145], v[226:229], v[46:49]
	v_mfma_f32_16x16x32_bf16 v[42:45], v[146:149], v[226:229], v[42:45]
	v_mfma_f32_16x16x32_bf16 v[38:41], v[150:153], v[226:229], v[38:41]
	v_mfma_f32_16x16x32_bf16 v[34:37], v[154:157], v[226:229], v[34:37]
	s_add_i32 m0, s47, 0x4000
	s_nop 0
	global_load_lds_dwordx4 v136, s[30:31]
	v_mfma_f32_16x16x32_bf16 v[18:21], v[142:145], v[230:233], v[18:21]
	v_mfma_f32_16x16x32_bf16 v[22:25], v[146:149], v[230:233], v[22:25]
	v_mfma_f32_16x16x32_bf16 v[26:29], v[150:153], v[230:233], v[26:29]
	v_mfma_f32_16x16x32_bf16 v[30:33], v[154:157], v[230:233], v[30:33]
	s_add_i32 m0, s47, 0x6000
	s_nop 0
	global_load_lds_dwordx4 v138, s[30:31]
	s_add_i32 m0, s47, 0x8000
	s_nop 0
	global_load_lds_dwordx4 v140, s[30:31]
	v_mul_f32_e32 v114, s20, v114
	v_mul_f32_e32 v115, s20, v115
	v_mul_f32_e32 v116, s21, v116
	v_mul_f32_e32 v117, s21, v117
	v_mul_f32_e32 v118, s22, v118
	v_mul_f32_e32 v119, s22, v119
	v_mul_f32_e32 v120, s23, v120
	v_mul_f32_e32 v121, s23, v121
	v_mul_f32_e32 v122, s24, v122
	v_mul_f32_e32 v123, s24, v123
	v_mul_f32_e32 v124, s25, v124
	v_mul_f32_e32 v125, s25, v125
	v_mul_f32_e32 v126, s26, v126
	v_mul_f32_e32 v127, s26, v127
	v_mul_f32_e32 v128, s27, v128
	v_mul_f32_e32 v129, s27, v129
	v_cvt_pk_bf16_f32 v158, v114, v116
	v_cvt_pk_bf16_f32 v159, v118, v120
	v_cvt_pk_bf16_f32 v160, v122, v124
	v_cvt_pk_bf16_f32 v161, v126, v128
	v_cvt_pk_bf16_f32 v162, v115, v117
	v_cvt_pk_bf16_f32 v163, v119, v121
	v_cvt_pk_bf16_f32 v164, v123, v125
	v_cvt_pk_bf16_f32 v165, v127, v129
	ds_write_b128 v1, v[158:161] offset:19456
	ds_write_b128 v1, v[162:165] offset:19584
	v_add_u32_e32 v91, s42, v135
	v_add_u32_e32 v93, s42, v137
	ds_read_b128 v[238:241], v139 offset:0
	ds_read_b128 v[242:245], v139 offset:2048
	ds_read_b128 v[246:249], v139 offset:4096
	ds_read_b128 v[250:253], v139 offset:6144
	ds_read_b128 v[218:221], v91 offset:0
	ds_read_b128 v[222:225], v91 offset:2048
	ds_read_b128 v[226:229], v91 offset:4096
	ds_read_b128 v[230:233], v91 offset:6144
	s_waitcnt lgkmcnt(0)
	s_load_dwordx8 s[12:19], s[28:29], 0x0
	s_add_u32 s28, s28, 0x100
	s_addc_u32 s29, s29, 0
	v_mfma_f32_16x16x32_bf16 v[78:81], v[238:241], v[218:221], v[78:81]
	v_mfma_f32_16x16x32_bf16 v[74:77], v[242:245], v[218:221], v[74:77]
	v_mfma_f32_16x16x32_bf16 v[70:73], v[246:249], v[218:221], v[70:73]
	v_mfma_f32_16x16x32_bf16 v[66:69], v[250:253], v[218:221], v[66:69]
	ds_read_b128 v[218:221], v93 offset:0
	ds_read_b128 v[142:145], v141 offset:0
	v_lshl_add_u64 v[132:133], v[132:133], 0, s[40:41]
	global_load_dwordx2 v[114:115], v[132:133], off
	global_load_dwordx2 v[116:117], v[132:133], off offset:2048
	v_mfma_f32_16x16x32_bf16 v[62:65], v[238:241], v[222:225], v[62:65]
	v_mfma_f32_16x16x32_bf16 v[58:61], v[242:245], v[222:225], v[58:61]
	v_mfma_f32_16x16x32_bf16 v[54:57], v[246:249], v[222:225], v[54:57]
	v_mfma_f32_16x16x32_bf16 v[50:53], v[250:253], v[222:225], v[50:53]
	ds_read_b128 v[222:225], v93 offset:2048
	ds_read_b128 v[146:149], v141 offset:2048
	v_lshl_add_u64 v[166:167], v[132:133], 0, s[34:35]
	global_load_dwordx2 v[118:119], v[166:167], off
	global_load_dwordx2 v[120:121], v[166:167], off offset:2048
	v_mfma_f32_16x16x32_bf16 v[46:49], v[238:241], v[226:229], v[46:49]
	v_mfma_f32_16x16x32_bf16 v[42:45], v[242:245], v[226:229], v[42:45]
	v_mfma_f32_16x16x32_bf16 v[38:41], v[246:249], v[226:229], v[38:41]
	v_mfma_f32_16x16x32_bf16 v[34:37], v[250:253], v[226:229], v[34:37]
	ds_read_b128 v[226:229], v93 offset:4096
	ds_read_b128 v[150:153], v141 offset:4096
	v_lshl_add_u64 v[166:167], v[132:133], 0, s[36:37]
	global_load_dwordx2 v[122:123], v[166:167], off
	global_load_dwordx2 v[124:125], v[166:167], off offset:2048
	v_mfma_f32_16x16x32_bf16 v[18:21], v[238:241], v[230:233], v[18:21]
	v_mfma_f32_16x16x32_bf16 v[22:25], v[242:245], v[230:233], v[22:25]
	v_mfma_f32_16x16x32_bf16 v[26:29], v[246:249], v[230:233], v[26:29]
	v_mfma_f32_16x16x32_bf16 v[30:33], v[250:253], v[230:233], v[30:33]
	ds_read_b128 v[230:233], v93 offset:6144
	ds_read_b128 v[154:157], v141 offset:6144
	v_lshl_add_u64 v[166:167], v[132:133], 0, s[38:39]
	global_load_dwordx2 v[126:127], v[166:167], off
	global_load_dwordx2 v[128:129], v[166:167], off offset:2048
	s_waitcnt vmcnt(21)
	s_waitcnt lgkmcnt(0)
	s_barrier
; #define MU_GLDS_A(buf, kt) do { _Pragma("unroll") for (int i = 0; i < NMU; ++i) \
;         __builtin_amdgcn_global_load_lds((const unsigned*)((const char*)A + aoff[i] + (size_t)(kt) * 128), (PG8_LAS unsigned*)(MU_SA(buf) + wid * 1024 + i * 8192), 16, 0, 0); } while (0)
; #define MU_B_ISSUE(sb, kt) do { const char* kb_ = Bb + (size_t)(kt) * (64 * (size_t)RB); _Pragma("unroll") for (int j = 0; j < 8; ++j) { const char* p_ = kb_ + (size_t)j * RB; \
;         asm volatile("global_load_dwordx2 %0, %1, off" : "=&v"(sb[j]) : "v"(p_) : "memory"); } } while (0)
; #define MU_B_WAIT(sb, N) asm volatile("s_waitcnt vmcnt(%8)" : "+v"(sb[0]), "+v"(sb[1]), "+v"(sb[2]), "+v"(sb[3]), "+v"(sb[4]), "+v"(sb[5]), "+v"(sb[6]), "+v"(sb[7]) : "n"(N) : "memory")
; #define MU_COMPUTE(buf) MU_COMPUTE_N(buf, NMU)
; template <int MODE>
; __device__ __forceinline__ void moe_unit(PG8_LAS unsigned char* lds, int e, int cb, int slot0  , int nv  , const bf16_t* A, const int* slot_tok,
;                                          const float* W0, const float* W1, bf16_t* OUT, const float* slot_rs  , const int* slot_dst) {
;     ...
;     f32x4 acc[NMU][4];
; #pragma unroll
;     for (int m = 0; m < NMU; ++m)
; #pragma unroll
;         for (int n = 0; n < 4; ++n) acc[m][n] = (f32x4){0.f, 0.f, 0.f, 0.f};
;     f32x2 s0[8], s1[8];
;     float g0[8];
;     MU_GLDS_A(0, 0); MU_B_ISSUE(s0, 0); MU_G_LOAD(g0, 0); MU_B_ISSUE(s1, 1);
;     MU_B_WAIT(s0, 8); MU_B_WRITE(s0, 0, g0); __builtin_amdgcn_sched_barrier(0); MU_B_ISSUE(s0, 2);
;     asm volatile("s_waitcnt vmcnt(16)" ::: "memory");
;     asm volatile("s_waitcnt lgkmcnt(0)" ::: "memory"); __builtin_amdgcn_s_barrier(); asm volatile("" ::: "memory");
; #pragma unroll 1
;     for (int t = 0; t < nt; t += 2) {
;         if (t + 2 < nt) MU_B_WAIT(s1, 8); else MU_B_WAIT(s1, 0);
;         MU_G_LOAD(g0, t + 1); MU_B_WRITE(s1, 1, g0); __builtin_amdgcn_sched_barrier(0); MU_GLDS_A(1, t + 1); __builtin_amdgcn_sched_barrier(0);
;         if (t + 3 < nt) { MU_B_ISSUE(s1, t + 3); }
;         MU_COMPUTE(0);
;         MU_END(t + 3 >= nt);
;         if (t + 2 < nt) { MU_B_WAIT(s0, 8); MU_G_LOAD(g0, t + 2); MU_B_WRITE(s0, 0, g0); __builtin_amdgcn_sched_barrier(0); MU_GLDS_A(0, t + 2); __builtin_amdgcn_sched_barrier(0); }
;         if (t + 4 < nt) { MU_B_ISSUE(s0, t + 4); }
;         MU_COMPUTE(1);
;         MU_END(t + 4 >= nt);
	s_mov_b32 s47, s42
	s_mov_b32 s42, s43
	s_mov_b32 s43, s44
	s_mov_b32 s44, s47
	s_add_i32 s47, s44, s6
	s_add_u32 s30, s30, 0x80
	s_addc_u32 s31, s31, 0
	v_mfma_f32_16x16x32_bf16 v[78:81], v[142:145], v[218:221], v[78:81]
	v_mfma_f32_16x16x32_bf16 v[74:77], v[146:149], v[218:221], v[74:77]
	v_mfma_f32_16x16x32_bf16 v[70:73], v[150:153], v[218:221], v[70:73]
	v_mfma_f32_16x16x32_bf16 v[66:69], v[154:157], v[218:221], v[66:69]
	s_mov_b32 m0, s47
	s_nop 0
	global_load_lds_dwordx4 v86, s[30:31]
	v_mfma_f32_16x16x32_bf16 v[62:65], v[142:145], v[222:225], v[62:65]
	v_mfma_f32_16x16x32_bf16 v[58:61], v[146:149], v[222:225], v[58:61]
	v_mfma_f32_16x16x32_bf16 v[54:57], v[150:153], v[222:225], v[54:57]
	v_mfma_f32_16x16x32_bf16 v[50:53], v[154:157], v[222:225], v[50:53]
	s_add_i32 m0, s47, 0x2000
	s_nop 0
	global_load_lds_dwordx4 v134, s[30:31]
	v_mfma_f32_16x16x32_bf16 v[46:49], v[142:145], v[226:229], v[46:49]
	v_mfma_f32_16x16x32_bf16 v[42:45], v[146:149], v[226:229], v[42:45]
	v_mfma_f32_16x16x32_bf16 v[38:41], v[150:153], v[226:229], v[38:41]
	v_mfma_f32_16x16x32_bf16 v[34:37], v[154:157], v[226:229], v[34:37]
	s_add_i32 m0, s47, 0x4000
	s_nop 0
	global_load_lds_dwordx4 v136, s[30:31]
	v_mfma_f32_16x16x32_bf16 v[18:21], v[142:145], v[230:233], v[18:21]
	v_mfma_f32_16x16x32_bf16 v[22:25], v[146:149], v[230:233], v[22:25]
	v_mfma_f32_16x16x32_bf16 v[26:29], v[150:153], v[230:233], v[26:29]
	v_mfma_f32_16x16x32_bf16 v[30:33], v[154:157], v[230:233], v[30:33]
	s_add_i32 m0, s47, 0x6000
	s_nop 0
	global_load_lds_dwordx4 v138, s[30:31]
	s_add_i32 m0, s47, 0x8000
	s_nop 0
	global_load_lds_dwordx4 v140, s[30:31]
	v_mul_f32_e32 v186, s12, v186
	v_mul_f32_e32 v187, s12, v187
	v_mul_f32_e32 v188, s13, v188
	v_mul_f32_e32 v189, s13, v189
	v_mul_f32_e32 v190, s14, v190
	v_mul_f32_e32 v191, s14, v191
	v_mul_f32_e32 v192, s15, v192
	v_mul_f32_e32 v193, s15, v193
	v_mul_f32_e32 v194, s16, v194
	v_mul_f32_e32 v195, s16, v195
	v_mul_f32_e32 v196, s17, v196
	v_mul_f32_e32 v197, s17, v197
	v_mul_f32_e32 v198, s18, v198
	v_mul_f32_e32 v199, s18, v199
	v_mul_f32_e32 v200, s19, v200
	v_mul_f32_e32 v201, s19, v201
	v_cvt_pk_bf16_f32 v158, v186, v188
	v_cvt_pk_bf16_f32 v159, v190, v192
	v_cvt_pk_bf16_f32 v160, v194, v196
	v_cvt_pk_bf16_f32 v161, v198, v200
	v_cvt_pk_bf16_f32 v162, v187, v189
	v_cvt_pk_bf16_f32 v163, v191, v193
	v_cvt_pk_bf16_f32 v164, v195, v197
	v_cvt_pk_bf16_f32 v165, v199, v201
	ds_write_b128 v1, v[158:161] offset:0
	ds_write_b128 v1, v[162:165] offset:128
	v_add_u32_e32 v91, s42, v135
	v_add_u32_e32 v93, s42, v137
	ds_read_b128 v[238:241], v139 offset:19456
	ds_read_b128 v[242:245], v139 offset:21504
	ds_read_b128 v[246:249], v139 offset:23552
	ds_read_b128 v[250:253], v139 offset:25600
	ds_read_b128 v[218:221], v91 offset:0
	ds_read_b128 v[222:225], v91 offset:2048
	ds_read_b128 v[226:229], v91 offset:4096
	ds_read_b128 v[230:233], v91 offset:6144
	s_waitcnt lgkmcnt(0)
	s_load_dwordx8 s[20:27], s[28:29], 0x0
	s_add_u32 s28, s28, 0x100
	s_addc_u32 s29, s29, 0
	v_mfma_f32_16x16x32_bf16 v[78:81], v[238:241], v[218:221], v[78:81]
	v_mfma_f32_16x16x32_bf16 v[74:77], v[242:245], v[218:221], v[74:77]
	v_mfma_f32_16x16x32_bf16 v[70:73], v[246:249], v[218:221], v[70:73]
	v_mfma_f32_16x16x32_bf16 v[66:69], v[250:253], v[218:221], v[66:69]
	ds_read_b128 v[218:221], v93 offset:0
	ds_read_b128 v[142:145], v141 offset:19456
	v_lshl_add_u64 v[132:133], v[132:133], 0, s[40:41]
	global_load_dwordx2 v[186:187], v[132:133], off
	global_load_dwordx2 v[188:189], v[132:133], off offset:2048
	v_mfma_f32_16x16x32_bf16 v[62:65], v[238:241], v[222:225], v[62:65]
	v_mfma_f32_16x16x32_bf16 v[58:61], v[242:245], v[222:225], v[58:61]
	v_mfma_f32_16x16x32_bf16 v[54:57], v[246:249], v[222:225], v[54:57]
	v_mfma_f32_16x16x32_bf16 v[50:53], v[250:253], v[222:225], v[50:53]
	ds_read_b128 v[222:225], v93 offset:2048
	ds_read_b128 v[146:149], v141 offset:21504
	v_lshl_add_u64 v[166:167], v[132:133], 0, s[34:35]
	global_load_dwordx2 v[190:191], v[166:167], off
	global_load_dwordx2 v[192:193], v[166:167], off offset:2048
	v_mfma_f32_16x16x32_bf16 v[46:49], v[238:241], v[226:229], v[46:49]
	v_mfma_f32_16x16x32_bf16 v[42:45], v[242:245], v[226:229], v[42:45]
	v_mfma_f32_16x16x32_bf16 v[38:41], v[246:249], v[226:229], v[38:41]
	v_mfma_f32_16x16x32_bf16 v[34:37], v[250:253], v[226:229], v[34:37]
	ds_read_b128 v[226:229], v93 offset:4096
	ds_read_b128 v[150:153], v141 offset:23552
	v_lshl_add_u64 v[166:167], v[132:133], 0, s[36:37]
	global_load_dwordx2 v[194:195], v[166:167], off
	global_load_dwordx2 v[196:197], v[166:167], off offset:2048
	v_mfma_f32_16x16x32_bf16 v[18:21], v[238:241], v[230:233], v[18:21]
	v_mfma_f32_16x16x32_bf16 v[22:25], v[242:245], v[230:233], v[22:25]
	v_mfma_f32_16x16x32_bf16 v[26:29], v[246:249], v[230:233], v[26:29]
	v_mfma_f32_16x16x32_bf16 v[30:33], v[250:253], v[230:233], v[30:33]
	ds_read_b128 v[230:233], v93 offset:6144
	ds_read_b128 v[154:157], v141 offset:25600
	v_lshl_add_u64 v[166:167], v[132:133], 0, s[38:39]
	global_load_dwordx2 v[198:199], v[166:167], off
	global_load_dwordx2 v[200:201], v[166:167], off offset:2048
	s_waitcnt vmcnt(21)
	s_waitcnt lgkmcnt(0)
	s_barrier
; #define MU_GLDS_A(buf, kt) do { _Pragma("unroll") for (int i = 0; i < NMU; ++i) \
;         __builtin_amdgcn_global_load_lds((const unsigned*)((const char*)A + aoff[i] + (size_t)(kt) * 128), (PG8_LAS unsigned*)(MU_SA(buf) + wid * 1024 + i * 8192), 16, 0, 0); } while (0)
; #define MU_B_ISSUE(sb, kt) do { const char* kb_ = Bb + (size_t)(kt) * (64 * (size_t)RB); _Pragma("unroll") for (int j = 0; j < 8; ++j) { const char* p_ = kb_ + (size_t)j * RB; \
;         asm volatile("global_load_dwordx2 %0, %1, off" : "=&v"(sb[j]) : "v"(p_) : "memory"); } } while (0)
; #define MU_B_WAIT(sb, N) asm volatile("s_waitcnt vmcnt(%8)" : "+v"(sb[0]), "+v"(sb[1]), "+v"(sb[2]), "+v"(sb[3]), "+v"(sb[4]), "+v"(sb[5]), "+v"(sb[6]), "+v"(sb[7]) : "n"(N) : "memory")
; #define MU_COMPUTE(buf) MU_COMPUTE_N(buf, NMU)
; template <int MODE>
; __device__ __forceinline__ void moe_unit(PG8_LAS unsigned char* lds, int e, int cb, int slot0  , int nv  , const bf16_t* A, const int* slot_tok,
;                                          const float* W0, const float* W1, bf16_t* OUT, const float* slot_rs  , const int* slot_dst) {
;     ...
;     f32x4 acc[NMU][4];
; #pragma unroll
;     for (int m = 0; m < NMU; ++m)
; #pragma unroll
;         for (int n = 0; n < 4; ++n) acc[m][n] = (f32x4){0.f, 0.f, 0.f, 0.f};
;     f32x2 s0[8], s1[8];
;     float g0[8];
;     MU_GLDS_A(0, 0); MU_B_ISSUE(s0, 0); MU_G_LOAD(g0, 0); MU_B_ISSUE(s1, 1);
;     MU_B_WAIT(s0, 8); MU_B_WRITE(s0, 0, g0); __builtin_amdgcn_sched_barrier(0); MU_B_ISSUE(s0, 2);
;     asm volatile("s_waitcnt vmcnt(16)" ::: "memory");
;     asm volatile("s_waitcnt lgkmcnt(0)" ::: "memory"); __builtin_amdgcn_s_barrier(); asm volatile("" ::: "memory");
; #pragma unroll 1
;     for (int t = 0; t < nt; t += 2) {
;         if (t + 2 < nt) MU_B_WAIT(s1, 8); else MU_B_WAIT(s1, 0);
;         MU_G_LOAD(g0, t + 1); MU_B_WRITE(s1, 1, g0); __builtin_amdgcn_sched_barrier(0); MU_GLDS_A(1, t + 1); __builtin_amdgcn_sched_barrier(0);
;         if (t + 3 < nt) { MU_B_ISSUE(s1, t + 3); }
;         MU_COMPUTE(0);
;         MU_END(t + 3 >= nt);
;         if (t + 2 < nt) { MU_B_WAIT(s0, 8); MU_G_LOAD(g0, t + 2); MU_B_WRITE(s0, 0, g0); __builtin_amdgcn_sched_barrier(0); MU_GLDS_A(0, t + 2); __builtin_amdgcn_sched_barrier(0); }
;         if (t + 4 < nt) { MU_B_ISSUE(s0, t + 4); }
;         MU_COMPUTE(1);
;         MU_END(t + 4 >= nt);
	s_mov_b32 s47, s42
	s_mov_b32 s42, s43
	s_mov_b32 s43, s44
	s_mov_b32 s44, s47
	s_add_i32 s47, s44, s6
	s_add_u32 s30, s30, 0x80
	s_addc_u32 s31, s31, 0
	v_mfma_f32_16x16x32_bf16 v[78:81], v[142:145], v[218:221], v[78:81]
	v_mfma_f32_16x16x32_bf16 v[74:77], v[146:149], v[218:221], v[74:77]
	v_mfma_f32_16x16x32_bf16 v[70:73], v[150:153], v[218:221], v[70:73]
	v_mfma_f32_16x16x32_bf16 v[66:69], v[154:157], v[218:221], v[66:69]
	s_mov_b32 m0, s47
	s_nop 0
	global_load_lds_dwordx4 v86, s[30:31]
	v_mfma_f32_16x16x32_bf16 v[62:65], v[142:145], v[222:225], v[62:65]
	v_mfma_f32_16x16x32_bf16 v[58:61], v[146:149], v[222:225], v[58:61]
	v_mfma_f32_16x16x32_bf16 v[54:57], v[150:153], v[222:225], v[54:57]
	v_mfma_f32_16x16x32_bf16 v[50:53], v[154:157], v[222:225], v[50:53]
	s_add_i32 m0, s47, 0x2000
	s_nop 0
	global_load_lds_dwordx4 v134, s[30:31]
	v_mfma_f32_16x16x32_bf16 v[46:49], v[142:145], v[226:229], v[46:49]
	v_mfma_f32_16x16x32_bf16 v[42:45], v[146:149], v[226:229], v[42:45]
	v_mfma_f32_16x16x32_bf16 v[38:41], v[150:153], v[226:229], v[38:41]
	v_mfma_f32_16x16x32_bf16 v[34:37], v[154:157], v[226:229], v[34:37]
	s_add_i32 m0, s47, 0x4000
	s_nop 0
	global_load_lds_dwordx4 v136, s[30:31]
	v_mfma_f32_16x16x32_bf16 v[18:21], v[142:145], v[230:233], v[18:21]
	v_mfma_f32_16x16x32_bf16 v[22:25], v[146:149], v[230:233], v[22:25]
	v_mfma_f32_16x16x32_bf16 v[26:29], v[150:153], v[230:233], v[26:29]
	v_mfma_f32_16x16x32_bf16 v[30:33], v[154:157], v[230:233], v[30:33]
	s_add_i32 m0, s47, 0x6000
	s_nop 0
	global_load_lds_dwordx4 v138, s[30:31]
	s_add_i32 m0, s47, 0x8000
	s_nop 0
	global_load_lds_dwordx4 v140, s[30:31]
	v_mul_f32_e32 v202, s20, v202
	v_mul_f32_e32 v203, s20, v203
	v_mul_f32_e32 v204, s21, v204
	v_mul_f32_e32 v205, s21, v205
	v_mul_f32_e32 v206, s22, v206
	v_mul_f32_e32 v207, s22, v207
	v_mul_f32_e32 v208, s23, v208
	v_mul_f32_e32 v209, s23, v209
	v_mul_f32_e32 v210, s24, v210
	v_mul_f32_e32 v211, s24, v211
	v_mul_f32_e32 v212, s25, v212
	v_mul_f32_e32 v213, s25, v213
	v_mul_f32_e32 v214, s26, v214
	v_mul_f32_e32 v215, s26, v215
	v_mul_f32_e32 v216, s27, v216
	v_mul_f32_e32 v217, s27, v217
	v_cvt_pk_bf16_f32 v158, v202, v204
	v_cvt_pk_bf16_f32 v159, v206, v208
	v_cvt_pk_bf16_f32 v160, v210, v212
	v_cvt_pk_bf16_f32 v161, v214, v216
	v_cvt_pk_bf16_f32 v162, v203, v205
	v_cvt_pk_bf16_f32 v163, v207, v209
	v_cvt_pk_bf16_f32 v164, v211, v213
	v_cvt_pk_bf16_f32 v165, v215, v217
	ds_write_b128 v1, v[158:161] offset:19456
	ds_write_b128 v1, v[162:165] offset:19584
	v_add_u32_e32 v91, s42, v135
	v_add_u32_e32 v93, s42, v137
	ds_read_b128 v[238:241], v139 offset:0
	ds_read_b128 v[242:245], v139 offset:2048
	ds_read_b128 v[246:249], v139 offset:4096
	ds_read_b128 v[250:253], v139 offset:6144
	ds_read_b128 v[218:221], v91 offset:0
	ds_read_b128 v[222:225], v91 offset:2048
	ds_read_b128 v[226:229], v91 offset:4096
	ds_read_b128 v[230:233], v91 offset:6144
	s_waitcnt lgkmcnt(0)
	s_load_dwordx8 s[12:19], s[28:29], 0x0
	s_add_u32 s28, s28, 0x100
	s_addc_u32 s29, s29, 0
	v_mfma_f32_16x16x32_bf16 v[78:81], v[238:241], v[218:221], v[78:81]
	v_mfma_f32_16x16x32_bf16 v[74:77], v[242:245], v[218:221], v[74:77]
	v_mfma_f32_16x16x32_bf16 v[70:73], v[246:249], v[218:221], v[70:73]
	v_mfma_f32_16x16x32_bf16 v[66:69], v[250:253], v[218:221], v[66:69]
	ds_read_b128 v[218:221], v93 offset:0
	ds_read_b128 v[142:145], v141 offset:0
	v_lshl_add_u64 v[132:133], v[132:133], 0, s[40:41]
	global_load_dwordx2 v[202:203], v[132:133], off
	global_load_dwordx2 v[204:205], v[132:133], off offset:2048
	v_mfma_f32_16x16x32_bf16 v[62:65], v[238:241], v[222:225], v[62:65]
	v_mfma_f32_16x16x32_bf16 v[58:61], v[242:245], v[222:225], v[58:61]
	v_mfma_f32_16x16x32_bf16 v[54:57], v[246:249], v[222:225], v[54:57]
	v_mfma_f32_16x16x32_bf16 v[50:53], v[250:253], v[222:225], v[50:53]
	ds_read_b128 v[222:225], v93 offset:2048
	ds_read_b128 v[146:149], v141 offset:2048
	v_lshl_add_u64 v[166:167], v[132:133], 0, s[34:35]
	global_load_dwordx2 v[206:207], v[166:167], off
	global_load_dwordx2 v[208:209], v[166:167], off offset:2048
	v_mfma_f32_16x16x32_bf16 v[46:49], v[238:241], v[226:229], v[46:49]
	v_mfma_f32_16x16x32_bf16 v[42:45], v[242:245], v[226:229], v[42:45]
	v_mfma_f32_16x16x32_bf16 v[38:41], v[246:249], v[226:229], v[38:41]
	v_mfma_f32_16x16x32_bf16 v[34:37], v[250:253], v[226:229], v[34:37]
	ds_read_b128 v[226:229], v93 offset:4096
	ds_read_b128 v[150:153], v141 offset:4096
	v_lshl_add_u64 v[166:167], v[132:133], 0, s[36:37]
	global_load_dwordx2 v[210:211], v[166:167], off
	global_load_dwordx2 v[212:213], v[166:167], off offset:2048
	v_mfma_f32_16x16x32_bf16 v[18:21], v[238:241], v[230:233], v[18:21]
	v_mfma_f32_16x16x32_bf16 v[22:25], v[242:245], v[230:233], v[22:25]
	v_mfma_f32_16x16x32_bf16 v[26:29], v[246:249], v[230:233], v[26:29]
	v_mfma_f32_16x16x32_bf16 v[30:33], v[250:253], v[230:233], v[30:33]
	ds_read_b128 v[230:233], v93 offset:6144
	ds_read_b128 v[154:157], v141 offset:6144
	v_lshl_add_u64 v[166:167], v[132:133], 0, s[38:39]
	global_load_dwordx2 v[214:215], v[166:167], off
	global_load_dwordx2 v[216:217], v[166:167], off offset:2048
	s_waitcnt vmcnt(21)
	s_waitcnt lgkmcnt(0)
	s_barrier
; #define MU_GLDS_A(buf, kt) do { _Pragma("unroll") for (int i = 0; i < NMU; ++i) \
;         __builtin_amdgcn_global_load_lds((const unsigned*)((const char*)A + aoff[i] + (size_t)(kt) * 128), (PG8_LAS unsigned*)(MU_SA(buf) + wid * 1024 + i * 8192), 16, 0, 0); } while (0)
; #define MU_B_ISSUE(sb, kt) do { const char* kb_ = Bb + (size_t)(kt) * (64 * (size_t)RB); _Pragma("unroll") for (int j = 0; j < 8; ++j) { const char* p_ = kb_ + (size_t)j * RB; \
;         asm volatile("global_load_dwordx2 %0, %1, off" : "=&v"(sb[j]) : "v"(p_) : "memory"); } } while (0)
; #define MU_B_WAIT(sb, N) asm volatile("s_waitcnt vmcnt(%8)" : "+v"(sb[0]), "+v"(sb[1]), "+v"(sb[2]), "+v"(sb[3]), "+v"(sb[4]), "+v"(sb[5]), "+v"(sb[6]), "+v"(sb[7]) : "n"(N) : "memory")
; #define MU_COMPUTE(buf) MU_COMPUTE_N(buf, NMU)
; template <int MODE>
; __device__ __forceinline__ void moe_unit(PG8_LAS unsigned char* lds, int e, int cb, int slot0  , int nv  , const bf16_t* A, const int* slot_tok,
;                                          const float* W0, const float* W1, bf16_t* OUT, const float* slot_rs  , const int* slot_dst) {
;     ...
;     f32x4 acc[NMU][4];
; #pragma unroll
;     for (int m = 0; m < NMU; ++m)
; #pragma unroll
;         for (int n = 0; n < 4; ++n) acc[m][n] = (f32x4){0.f, 0.f, 0.f, 0.f};
;     f32x2 s0[8], s1[8];
;     float g0[8];
;     MU_GLDS_A(0, 0); MU_B_ISSUE(s0, 0); MU_G_LOAD(g0, 0); MU_B_ISSUE(s1, 1);
;     MU_B_WAIT(s0, 8); MU_B_WRITE(s0, 0, g0); __builtin_amdgcn_sched_barrier(0); MU_B_ISSUE(s0, 2);
;     asm volatile("s_waitcnt vmcnt(16)" ::: "memory");
;     asm volatile("s_waitcnt lgkmcnt(0)" ::: "memory"); __builtin_amdgcn_s_barrier(); asm volatile("" ::: "memory");
; #pragma unroll 1
;     for (int t = 0; t < nt; t += 2) {
;         if (t + 2 < nt) MU_B_WAIT(s1, 8); else MU_B_WAIT(s1, 0);
;         MU_G_LOAD(g0, t + 1); MU_B_WRITE(s1, 1, g0); __builtin_amdgcn_sched_barrier(0); MU_GLDS_A(1, t + 1); __builtin_amdgcn_sched_barrier(0);
;         if (t + 3 < nt) { MU_B_ISSUE(s1, t + 3); }
;         MU_COMPUTE(0);
;         MU_END(t + 3 >= nt);
;         if (t + 2 < nt) { MU_B_WAIT(s0, 8); MU_G_LOAD(g0, t + 2); MU_B_WRITE(s0, 0, g0); __builtin_amdgcn_sched_barrier(0); MU_GLDS_A(0, t + 2); __builtin_amdgcn_sched_barrier(0); }
;         if (t + 4 < nt) { MU_B_ISSUE(s0, t + 4); }
;         MU_COMPUTE(1);
;         MU_END(t + 4 >= nt);
	s_mov_b32 s47, s42
	s_mov_b32 s42, s43
	s_mov_b32 s43, s44
	s_mov_b32 s44, s47
	s_add_i32 s47, s44, s6
	s_add_u32 s30, s30, 0x80
	s_addc_u32 s31, s31, 0
	v_mfma_f32_16x16x32_bf16 v[78:81], v[142:145], v[218:221], v[78:81]
	v_mfma_f32_16x16x32_bf16 v[74:77], v[146:149], v[218:221], v[74:77]
	v_mfma_f32_16x16x32_bf16 v[70:73], v[150:153], v[218:221], v[70:73]
	v_mfma_f32_16x16x32_bf16 v[66:69], v[154:157], v[218:221], v[66:69]
	s_mov_b32 m0, s47
	s_nop 0
	global_load_lds_dwordx4 v86, s[30:31]
	v_mfma_f32_16x16x32_bf16 v[62:65], v[142:145], v[222:225], v[62:65]
	v_mfma_f32_16x16x32_bf16 v[58:61], v[146:149], v[222:225], v[58:61]
	v_mfma_f32_16x16x32_bf16 v[54:57], v[150:153], v[222:225], v[54:57]
	v_mfma_f32_16x16x32_bf16 v[50:53], v[154:157], v[222:225], v[50:53]
	s_add_i32 m0, s47, 0x2000
	s_nop 0
	global_load_lds_dwordx4 v134, s[30:31]
	v_mfma_f32_16x16x32_bf16 v[46:49], v[142:145], v[226:229], v[46:49]
	v_mfma_f32_16x16x32_bf16 v[42:45], v[146:149], v[226:229], v[42:45]
	v_mfma_f32_16x16x32_bf16 v[38:41], v[150:153], v[226:229], v[38:41]
	v_mfma_f32_16x16x32_bf16 v[34:37], v[154:157], v[226:229], v[34:37]
	s_add_i32 m0, s47, 0x4000
	s_nop 0
	global_load_lds_dwordx4 v136, s[30:31]
	v_mfma_f32_16x16x32_bf16 v[18:21], v[142:145], v[230:233], v[18:21]
	v_mfma_f32_16x16x32_bf16 v[22:25], v[146:149], v[230:233], v[22:25]
	v_mfma_f32_16x16x32_bf16 v[26:29], v[150:153], v[230:233], v[26:29]
	v_mfma_f32_16x16x32_bf16 v[30:33], v[154:157], v[230:233], v[30:33]
	s_add_i32 m0, s47, 0x6000
	s_nop 0
	global_load_lds_dwordx4 v138, s[30:31]
	s_add_i32 m0, s47, 0x8000
	s_nop 0
	global_load_lds_dwordx4 v140, s[30:31]
	v_mul_f32_e32 v98, s12, v98
	v_mul_f32_e32 v99, s12, v99
	v_mul_f32_e32 v100, s13, v100
	v_mul_f32_e32 v101, s13, v101
	v_mul_f32_e32 v102, s14, v102
	v_mul_f32_e32 v103, s14, v103
	v_mul_f32_e32 v104, s15, v104
	v_mul_f32_e32 v105, s15, v105
	v_mul_f32_e32 v106, s16, v106
	v_mul_f32_e32 v107, s16, v107
	v_mul_f32_e32 v108, s17, v108
	v_mul_f32_e32 v109, s17, v109
	v_mul_f32_e32 v110, s18, v110
	v_mul_f32_e32 v111, s18, v111
	v_mul_f32_e32 v112, s19, v112
	v_mul_f32_e32 v113, s19, v113
	v_cvt_pk_bf16_f32 v158, v98, v100
	v_cvt_pk_bf16_f32 v159, v102, v104
	v_cvt_pk_bf16_f32 v160, v106, v108
	v_cvt_pk_bf16_f32 v161, v110, v112
	v_cvt_pk_bf16_f32 v162, v99, v101
	v_cvt_pk_bf16_f32 v163, v103, v105
	v_cvt_pk_bf16_f32 v164, v107, v109
	v_cvt_pk_bf16_f32 v165, v111, v113
	ds_write_b128 v1, v[158:161] offset:0
	ds_write_b128 v1, v[162:165] offset:128
	v_add_u32_e32 v91, s42, v135
	v_add_u32_e32 v93, s42, v137
	ds_read_b128 v[238:241], v139 offset:19456
	ds_read_b128 v[242:245], v139 offset:21504
	ds_read_b128 v[246:249], v139 offset:23552
	ds_read_b128 v[250:253], v139 offset:25600
	ds_read_b128 v[218:221], v91 offset:0
	ds_read_b128 v[222:225], v91 offset:2048
	ds_read_b128 v[226:229], v91 offset:4096
	ds_read_b128 v[230:233], v91 offset:6144
	s_waitcnt lgkmcnt(0)
	s_load_dwordx8 s[20:27], s[28:29], 0x0
	s_add_u32 s28, s28, 0x100
	s_addc_u32 s29, s29, 0
	v_mfma_f32_16x16x32_bf16 v[78:81], v[238:241], v[218:221], v[78:81]
	v_mfma_f32_16x16x32_bf16 v[74:77], v[242:245], v[218:221], v[74:77]
	v_mfma_f32_16x16x32_bf16 v[70:73], v[246:249], v[218:221], v[70:73]
	v_mfma_f32_16x16x32_bf16 v[66:69], v[250:253], v[218:221], v[66:69]
	ds_read_b128 v[218:221], v93 offset:0
	ds_read_b128 v[142:145], v141 offset:19456
	v_mfma_f32_16x16x32_bf16 v[62:65], v[238:241], v[222:225], v[62:65]
	v_mfma_f32_16x16x32_bf16 v[58:61], v[242:245], v[222:225], v[58:61]
	v_mfma_f32_16x16x32_bf16 v[54:57], v[246:249], v[222:225], v[54:57]
	v_mfma_f32_16x16x32_bf16 v[50:53], v[250:253], v[222:225], v[50:53]
	ds_read_b128 v[222:225], v93 offset:2048
	ds_read_b128 v[146:149], v141 offset:21504
	v_mfma_f32_16x16x32_bf16 v[46:49], v[238:241], v[226:229], v[46:49]
	v_mfma_f32_16x16x32_bf16 v[42:45], v[242:245], v[226:229], v[42:45]
	v_mfma_f32_16x16x32_bf16 v[38:41], v[246:249], v[226:229], v[38:41]
	v_mfma_f32_16x16x32_bf16 v[34:37], v[250:253], v[226:229], v[34:37]
	ds_read_b128 v[226:229], v93 offset:4096
	ds_read_b128 v[150:153], v141 offset:23552
	v_mfma_f32_16x16x32_bf16 v[18:21], v[238:241], v[230:233], v[18:21]
	v_mfma_f32_16x16x32_bf16 v[22:25], v[242:245], v[230:233], v[22:25]
	v_mfma_f32_16x16x32_bf16 v[26:29], v[246:249], v[230:233], v[26:29]
	v_mfma_f32_16x16x32_bf16 v[30:33], v[250:253], v[230:233], v[30:33]
	ds_read_b128 v[230:233], v93 offset:6144
	ds_read_b128 v[154:157], v141 offset:25600
	s_waitcnt vmcnt(13)
	s_waitcnt lgkmcnt(0)
	s_barrier
; #define MU_GLDS_A(buf, kt) do { _Pragma("unroll") for (int i = 0; i < NMU; ++i) \
;         __builtin_amdgcn_global_load_lds((const unsigned*)((const char*)A + aoff[i] + (size_t)(kt) * 128), (PG8_LAS unsigned*)(MU_SA(buf) + wid * 1024 + i * 8192), 16, 0, 0); } while (0)
; #define MU_B_ISSUE(sb, kt) do { const char* kb_ = Bb + (size_t)(kt) * (64 * (size_t)RB); _Pragma("unroll") for (int j = 0; j < 8; ++j) { const char* p_ = kb_ + (size_t)j * RB; \
;         asm volatile("global_load_dwordx2 %0, %1, off" : "=&v"(sb[j]) : "v"(p_) : "memory"); } } while (0)
; #define MU_B_WAIT(sb, N) asm volatile("s_waitcnt vmcnt(%8)" : "+v"(sb[0]), "+v"(sb[1]), "+v"(sb[2]), "+v"(sb[3]), "+v"(sb[4]), "+v"(sb[5]), "+v"(sb[6]), "+v"(sb[7]) : "n"(N) : "memory")
; #define MU_COMPUTE(buf) MU_COMPUTE_N(buf, NMU)
; template <int MODE>
; __device__ __forceinline__ void moe_unit(PG8_LAS unsigned char* lds, int e, int cb, int slot0  , int nv  , const bf16_t* A, const int* slot_tok,
;                                          const float* W0, const float* W1, bf16_t* OUT, const float* slot_rs  , const int* slot_dst) {
;     ...
;     f32x4 acc[NMU][4];
; #pragma unroll
;     for (int m = 0; m < NMU; ++m)
; #pragma unroll
;         for (int n = 0; n < 4; ++n) acc[m][n] = (f32x4){0.f, 0.f, 0.f, 0.f};
;     f32x2 s0[8], s1[8];
;     float g0[8];
;     MU_GLDS_A(0, 0); MU_B_ISSUE(s0, 0); MU_G_LOAD(g0, 0); MU_B_ISSUE(s1, 1);
;     MU_B_WAIT(s0, 8); MU_B_WRITE(s0, 0, g0); __builtin_amdgcn_sched_barrier(0); MU_B_ISSUE(s0, 2);
;     asm volatile("s_waitcnt vmcnt(16)" ::: "memory");
;     asm volatile("s_waitcnt lgkmcnt(0)" ::: "memory"); __builtin_amdgcn_s_barrier(); asm volatile("" ::: "memory");
; #pragma unroll 1
;     for (int t = 0; t < nt; t += 2) {
;         if (t + 2 < nt) MU_B_WAIT(s1, 8); else MU_B_WAIT(s1, 0);
;         MU_G_LOAD(g0, t + 1); MU_B_WRITE(s1, 1, g0); __builtin_amdgcn_sched_barrier(0); MU_GLDS_A(1, t + 1); __builtin_amdgcn_sched_barrier(0);
;         if (t + 3 < nt) { MU_B_ISSUE(s1, t + 3); }
;         MU_COMPUTE(0);
;         MU_END(t + 3 >= nt);
;         if (t + 2 < nt) { MU_B_WAIT(s0, 8); MU_G_LOAD(g0, t + 2); MU_B_WRITE(s0, 0, g0); __builtin_amdgcn_sched_barrier(0); MU_GLDS_A(0, t + 2); __builtin_amdgcn_sched_barrier(0); }
;         if (t + 4 < nt) { MU_B_ISSUE(s0, t + 4); }
;         MU_COMPUTE(1);
;         MU_END(t + 4 >= nt);
	s_mov_b32 s47, s42
	s_mov_b32 s42, s43
	s_mov_b32 s43, s44
	s_mov_b32 s44, s47
	s_add_i32 s47, s44, s6
	s_add_u32 s30, s30, 0x80
	s_addc_u32 s31, s31, 0
	v_mfma_f32_16x16x32_bf16 v[78:81], v[142:145], v[218:221], v[78:81]
	v_mfma_f32_16x16x32_bf16 v[74:77], v[146:149], v[218:221], v[74:77]
	v_mfma_f32_16x16x32_bf16 v[70:73], v[150:153], v[218:221], v[70:73]
	v_mfma_f32_16x16x32_bf16 v[66:69], v[154:157], v[218:221], v[66:69]
	s_mov_b32 m0, s47
	s_nop 0
	global_load_lds_dwordx4 v86, s[30:31]
	v_mfma_f32_16x16x32_bf16 v[62:65], v[142:145], v[222:225], v[62:65]
	v_mfma_f32_16x16x32_bf16 v[58:61], v[146:149], v[222:225], v[58:61]
	v_mfma_f32_16x16x32_bf16 v[54:57], v[150:153], v[222:225], v[54:57]
	v_mfma_f32_16x16x32_bf16 v[50:53], v[154:157], v[222:225], v[50:53]
	s_add_i32 m0, s47, 0x2000
	s_nop 0
	global_load_lds_dwordx4 v134, s[30:31]
	v_mfma_f32_16x16x32_bf16 v[46:49], v[142:145], v[226:229], v[46:49]
	v_mfma_f32_16x16x32_bf16 v[42:45], v[146:149], v[226:229], v[42:45]
	v_mfma_f32_16x16x32_bf16 v[38:41], v[150:153], v[226:229], v[38:41]
	v_mfma_f32_16x16x32_bf16 v[34:37], v[154:157], v[226:229], v[34:37]
	s_add_i32 m0, s47, 0x4000
	s_nop 0
	global_load_lds_dwordx4 v136, s[30:31]
	v_mfma_f32_16x16x32_bf16 v[18:21], v[142:145], v[230:233], v[18:21]
	v_mfma_f32_16x16x32_bf16 v[22:25], v[146:149], v[230:233], v[22:25]
	v_mfma_f32_16x16x32_bf16 v[26:29], v[150:153], v[230:233], v[26:29]
	v_mfma_f32_16x16x32_bf16 v[30:33], v[154:157], v[230:233], v[30:33]
	s_add_i32 m0, s47, 0x6000
	s_nop 0
	global_load_lds_dwordx4 v138, s[30:31]
	s_add_i32 m0, s47, 0x8000
	s_nop 0
	global_load_lds_dwordx4 v140, s[30:31]
	v_mul_f32_e32 v114, s20, v114
	v_mul_f32_e32 v115, s20, v115
	v_mul_f32_e32 v116, s21, v116
	v_mul_f32_e32 v117, s21, v117
	v_mul_f32_e32 v118, s22, v118
	v_mul_f32_e32 v119, s22, v119
	v_mul_f32_e32 v120, s23, v120
	v_mul_f32_e32 v121, s23, v121
	v_mul_f32_e32 v122, s24, v122
	v_mul_f32_e32 v123, s24, v123
	v_mul_f32_e32 v124, s25, v124
	v_mul_f32_e32 v125, s25, v125
	v_mul_f32_e32 v126, s26, v126
	v_mul_f32_e32 v127, s26, v127
	v_mul_f32_e32 v128, s27, v128
	v_mul_f32_e32 v129, s27, v129
	v_cvt_pk_bf16_f32 v158, v114, v116
	v_cvt_pk_bf16_f32 v159, v118, v120
	v_cvt_pk_bf16_f32 v160, v122, v124
	v_cvt_pk_bf16_f32 v161, v126, v128
	v_cvt_pk_bf16_f32 v162, v115, v117
	v_cvt_pk_bf16_f32 v163, v119, v121
	v_cvt_pk_bf16_f32 v164, v123, v125
	v_cvt_pk_bf16_f32 v165, v127, v129
	ds_write_b128 v1, v[158:161] offset:19456
	ds_write_b128 v1, v[162:165] offset:19584
	v_add_u32_e32 v91, s42, v135
	v_add_u32_e32 v93, s42, v137
	ds_read_b128 v[238:241], v139 offset:0
	ds_read_b128 v[242:245], v139 offset:2048
	ds_read_b128 v[246:249], v139 offset:4096
	ds_read_b128 v[250:253], v139 offset:6144
	ds_read_b128 v[218:221], v91 offset:0
	ds_read_b128 v[222:225], v91 offset:2048
	ds_read_b128 v[226:229], v91 offset:4096
	ds_read_b128 v[230:233], v91 offset:6144
	s_waitcnt lgkmcnt(0)
	s_load_dwordx8 s[12:19], s[28:29], 0x0
	s_add_u32 s28, s28, 0x100
	s_addc_u32 s29, s29, 0
	v_mfma_f32_16x16x32_bf16 v[78:81], v[238:241], v[218:221], v[78:81]
	v_mfma_f32_16x16x32_bf16 v[74:77], v[242:245], v[218:221], v[74:77]
	v_mfma_f32_16x16x32_bf16 v[70:73], v[246:249], v[218:221], v[70:73]
	v_mfma_f32_16x16x32_bf16 v[66:69], v[250:253], v[218:221], v[66:69]
	ds_read_b128 v[218:221], v93 offset:0
	ds_read_b128 v[142:145], v141 offset:0
	v_mfma_f32_16x16x32_bf16 v[62:65], v[238:241], v[222:225], v[62:65]
	v_mfma_f32_16x16x32_bf16 v[58:61], v[242:245], v[222:225], v[58:61]
	v_mfma_f32_16x16x32_bf16 v[54:57], v[246:249], v[222:225], v[54:57]
	v_mfma_f32_16x16x32_bf16 v[50:53], v[250:253], v[222:225], v[50:53]
	ds_read_b128 v[222:225], v93 offset:2048
	ds_read_b128 v[146:149], v141 offset:2048
	v_mfma_f32_16x16x32_bf16 v[46:49], v[238:241], v[226:229], v[46:49]
	v_mfma_f32_16x16x32_bf16 v[42:45], v[242:245], v[226:229], v[42:45]
	v_mfma_f32_16x16x32_bf16 v[38:41], v[246:249], v[226:229], v[38:41]
	v_mfma_f32_16x16x32_bf16 v[34:37], v[250:253], v[226:229], v[34:37]
	ds_read_b128 v[226:229], v93 offset:4096
	ds_read_b128 v[150:153], v141 offset:4096
	v_mfma_f32_16x16x32_bf16 v[18:21], v[238:241], v[230:233], v[18:21]
	v_mfma_f32_16x16x32_bf16 v[22:25], v[242:245], v[230:233], v[22:25]
	v_mfma_f32_16x16x32_bf16 v[26:29], v[246:249], v[230:233], v[26:29]
	v_mfma_f32_16x16x32_bf16 v[30:33], v[250:253], v[230:233], v[30:33]
	ds_read_b128 v[230:233], v93 offset:6144
	ds_read_b128 v[154:157], v141 offset:6144
	s_waitcnt vmcnt(5)
	s_waitcnt lgkmcnt(0)
	s_barrier
; #define MU_GLDS_A(buf, kt) do { _Pragma("unroll") for (int i = 0; i < NMU; ++i) \
;         __builtin_amdgcn_global_load_lds((const unsigned*)((const char*)A + aoff[i] + (size_t)(kt) * 128), (PG8_LAS unsigned*)(MU_SA(buf) + wid * 1024 + i * 8192), 16, 0, 0); } while (0)
; #define MU_B_ISSUE(sb, kt) do { const char* kb_ = Bb + (size_t)(kt) * (64 * (size_t)RB); _Pragma("unroll") for (int j = 0; j < 8; ++j) { const char* p_ = kb_ + (size_t)j * RB; \
;         asm volatile("global_load_dwordx2 %0, %1, off" : "=&v"(sb[j]) : "v"(p_) : "memory"); } } while (0)
; #define MU_B_WAIT(sb, N) asm volatile("s_waitcnt vmcnt(%8)" : "+v"(sb[0]), "+v"(sb[1]), "+v"(sb[2]), "+v"(sb[3]), "+v"(sb[4]), "+v"(sb[5]), "+v"(sb[6]), "+v"(sb[7]) : "n"(N) : "memory")
; #define MU_COMPUTE(buf) MU_COMPUTE_N(buf, NMU)
; template <int MODE>
; __device__ __forceinline__ void moe_unit(PG8_LAS unsigned char* lds, int e, int cb, int slot0  , int nv  , const bf16_t* A, const int* slot_tok,
;                                          const float* W0, const float* W1, bf16_t* OUT, const float* slot_rs  , const int* slot_dst) {
;     ...
;     f32x4 acc[NMU][4];
; #pragma unroll
;     for (int m = 0; m < NMU; ++m)
; #pragma unroll
;         for (int n = 0; n < 4; ++n) acc[m][n] = (f32x4){0.f, 0.f, 0.f, 0.f};
;     f32x2 s0[8], s1[8];
;     float g0[8];
;     MU_GLDS_A(0, 0); MU_B_ISSUE(s0, 0); MU_G_LOAD(g0, 0); MU_B_ISSUE(s1, 1);
;     MU_B_WAIT(s0, 8); MU_B_WRITE(s0, 0, g0); __builtin_amdgcn_sched_barrier(0); MU_B_ISSUE(s0, 2);
;     asm volatile("s_waitcnt vmcnt(16)" ::: "memory");
;     asm volatile("s_waitcnt lgkmcnt(0)" ::: "memory"); __builtin_amdgcn_s_barrier(); asm volatile("" ::: "memory");
; #pragma unroll 1
;     for (int t = 0; t < nt; t += 2) {
;         if (t + 2 < nt) MU_B_WAIT(s1, 8); else MU_B_WAIT(s1, 0);
;         MU_G_LOAD(g0, t + 1); MU_B_WRITE(s1, 1, g0); __builtin_amdgcn_sched_barrier(0); MU_GLDS_A(1, t + 1); __builtin_amdgcn_sched_barrier(0);
;         if (t + 3 < nt) { MU_B_ISSUE(s1, t + 3); }
;         MU_COMPUTE(0);
;         MU_END(t + 3 >= nt);
;         if (t + 2 < nt) { MU_B_WAIT(s0, 8); MU_G_LOAD(g0, t + 2); MU_B_WRITE(s0, 0, g0); __builtin_amdgcn_sched_barrier(0); MU_GLDS_A(0, t + 2); __builtin_amdgcn_sched_barrier(0); }
;         if (t + 4 < nt) { MU_B_ISSUE(s0, t + 4); }
;         MU_COMPUTE(1);
;         MU_END(t + 4 >= nt);
	s_mov_b32 s47, s42
	s_mov_b32 s42, s43
	s_mov_b32 s43, s44
	s_mov_b32 s44, s47
	s_add_i32 s47, s44, s6
	s_add_u32 s30, s30, 0x80
	s_addc_u32 s31, s31, 0
	v_mfma_f32_16x16x32_bf16 v[78:81], v[142:145], v[218:221], v[78:81]
	v_mfma_f32_16x16x32_bf16 v[74:77], v[146:149], v[218:221], v[74:77]
	v_mfma_f32_16x16x32_bf16 v[70:73], v[150:153], v[218:221], v[70:73]
	v_mfma_f32_16x16x32_bf16 v[66:69], v[154:157], v[218:221], v[66:69]
	s_mov_b32 m0, s47
	s_nop 0
	global_load_lds_dwordx4 v86, s[30:31]
	v_mfma_f32_16x16x32_bf16 v[62:65], v[142:145], v[222:225], v[62:65]
	v_mfma_f32_16x16x32_bf16 v[58:61], v[146:149], v[222:225], v[58:61]
	v_mfma_f32_16x16x32_bf16 v[54:57], v[150:153], v[222:225], v[54:57]
	v_mfma_f32_16x16x32_bf16 v[50:53], v[154:157], v[222:225], v[50:53]
	s_add_i32 m0, s47, 0x2000
	s_nop 0
	global_load_lds_dwordx4 v134, s[30:31]
	v_mfma_f32_16x16x32_bf16 v[46:49], v[142:145], v[226:229], v[46:49]
	v_mfma_f32_16x16x32_bf16 v[42:45], v[146:149], v[226:229], v[42:45]
	v_mfma_f32_16x16x32_bf16 v[38:41], v[150:153], v[226:229], v[38:41]
	v_mfma_f32_16x16x32_bf16 v[34:37], v[154:157], v[226:229], v[34:37]
	s_add_i32 m0, s47, 0x4000
	s_nop 0
	global_load_lds_dwordx4 v136, s[30:31]
	v_mfma_f32_16x16x32_bf16 v[18:21], v[142:145], v[230:233], v[18:21]
	v_mfma_f32_16x16x32_bf16 v[22:25], v[146:149], v[230:233], v[22:25]
	v_mfma_f32_16x16x32_bf16 v[26:29], v[150:153], v[230:233], v[26:29]
	v_mfma_f32_16x16x32_bf16 v[30:33], v[154:157], v[230:233], v[30:33]
	s_add_i32 m0, s47, 0x6000
	s_nop 0
	global_load_lds_dwordx4 v138, s[30:31]
	s_add_i32 m0, s47, 0x8000
	s_nop 0
	global_load_lds_dwordx4 v140, s[30:31]
	v_mul_f32_e32 v186, s12, v186
	v_mul_f32_e32 v187, s12, v187
	v_mul_f32_e32 v188, s13, v188
	v_mul_f32_e32 v189, s13, v189
	v_mul_f32_e32 v190, s14, v190
	v_mul_f32_e32 v191, s14, v191
	v_mul_f32_e32 v192, s15, v192
	v_mul_f32_e32 v193, s15, v193
	v_mul_f32_e32 v194, s16, v194
	v_mul_f32_e32 v195, s16, v195
	v_mul_f32_e32 v196, s17, v196
	v_mul_f32_e32 v197, s17, v197
	v_mul_f32_e32 v198, s18, v198
	v_mul_f32_e32 v199, s18, v199
	v_mul_f32_e32 v200, s19, v200
	v_mul_f32_e32 v201, s19, v201
	v_cvt_pk_bf16_f32 v158, v186, v188
	v_cvt_pk_bf16_f32 v159, v190, v192
	v_cvt_pk_bf16_f32 v160, v194, v196
	v_cvt_pk_bf16_f32 v161, v198, v200
	v_cvt_pk_bf16_f32 v162, v187, v189
	v_cvt_pk_bf16_f32 v163, v191, v193
	v_cvt_pk_bf16_f32 v164, v195, v197
	v_cvt_pk_bf16_f32 v165, v199, v201
	ds_write_b128 v1, v[158:161] offset:0
	ds_write_b128 v1, v[162:165] offset:128
	v_add_u32_e32 v91, s42, v135
	v_add_u32_e32 v93, s42, v137
	ds_read_b128 v[238:241], v139 offset:19456
	ds_read_b128 v[242:245], v139 offset:21504
	ds_read_b128 v[246:249], v139 offset:23552
	ds_read_b128 v[250:253], v139 offset:25600
	ds_read_b128 v[218:221], v91 offset:0
	ds_read_b128 v[222:225], v91 offset:2048
	ds_read_b128 v[226:229], v91 offset:4096
	ds_read_b128 v[230:233], v91 offset:6144
	s_waitcnt lgkmcnt(0)
	s_load_dwordx8 s[20:27], s[28:29], 0x0
	s_add_u32 s28, s28, 0x100
	s_addc_u32 s29, s29, 0
	v_mfma_f32_16x16x32_bf16 v[78:81], v[238:241], v[218:221], v[78:81]
	v_mfma_f32_16x16x32_bf16 v[74:77], v[242:245], v[218:221], v[74:77]
	v_mfma_f32_16x16x32_bf16 v[70:73], v[246:249], v[218:221], v[70:73]
	v_mfma_f32_16x16x32_bf16 v[66:69], v[250:253], v[218:221], v[66:69]
	ds_read_b128 v[218:221], v93 offset:0
	ds_read_b128 v[142:145], v141 offset:19456
	v_mfma_f32_16x16x32_bf16 v[62:65], v[238:241], v[222:225], v[62:65]
	v_mfma_f32_16x16x32_bf16 v[58:61], v[242:245], v[222:225], v[58:61]
	v_mfma_f32_16x16x32_bf16 v[54:57], v[246:249], v[222:225], v[54:57]
	v_mfma_f32_16x16x32_bf16 v[50:53], v[250:253], v[222:225], v[50:53]
	ds_read_b128 v[222:225], v93 offset:2048
	ds_read_b128 v[146:149], v141 offset:21504
	v_mfma_f32_16x16x32_bf16 v[46:49], v[238:241], v[226:229], v[46:49]
	v_mfma_f32_16x16x32_bf16 v[42:45], v[242:245], v[226:229], v[42:45]
	v_mfma_f32_16x16x32_bf16 v[38:41], v[246:249], v[226:229], v[38:41]
	v_mfma_f32_16x16x32_bf16 v[34:37], v[250:253], v[226:229], v[34:37]
	ds_read_b128 v[226:229], v93 offset:4096
	ds_read_b128 v[150:153], v141 offset:23552
	v_mfma_f32_16x16x32_bf16 v[18:21], v[238:241], v[230:233], v[18:21]
	v_mfma_f32_16x16x32_bf16 v[22:25], v[242:245], v[230:233], v[22:25]
	v_mfma_f32_16x16x32_bf16 v[26:29], v[246:249], v[230:233], v[26:29]
	v_mfma_f32_16x16x32_bf16 v[30:33], v[250:253], v[230:233], v[30:33]
	ds_read_b128 v[230:233], v93 offset:6144
	ds_read_b128 v[154:157], v141 offset:25600
	s_waitcnt vmcnt(5)
	s_waitcnt lgkmcnt(0)
	s_barrier
; #define MU_GLDS_A(buf, kt) do { _Pragma("unroll") for (int i = 0; i < NMU; ++i) \
;         __builtin_amdgcn_global_load_lds((const unsigned*)((const char*)A + aoff[i] + (size_t)(kt) * 128), (PG8_LAS unsigned*)(MU_SA(buf) + wid * 1024 + i * 8192), 16, 0, 0); } while (0)
; #define MU_B_ISSUE(sb, kt) do { const char* kb_ = Bb + (size_t)(kt) * (64 * (size_t)RB); _Pragma("unroll") for (int j = 0; j < 8; ++j) { const char* p_ = kb_ + (size_t)j * RB; \
;         asm volatile("global_load_dwordx2 %0, %1, off" : "=&v"(sb[j]) : "v"(p_) : "memory"); } } while (0)
; #define MU_B_WAIT(sb, N) asm volatile("s_waitcnt vmcnt(%8)" : "+v"(sb[0]), "+v"(sb[1]), "+v"(sb[2]), "+v"(sb[3]), "+v"(sb[4]), "+v"(sb[5]), "+v"(sb[6]), "+v"(sb[7]) : "n"(N) : "memory")
; #define MU_COMPUTE(buf) MU_COMPUTE_N(buf, NMU)
; template <int MODE>
; __device__ __forceinline__ void moe_unit(PG8_LAS unsigned char* lds, int e, int cb, int slot0  , int nv  , const bf16_t* A, const int* slot_tok,
;                                          const float* W0, const float* W1, bf16_t* OUT, const float* slot_rs  , const int* slot_dst) {
;     ...
;     f32x4 acc[NMU][4];
; #pragma unroll
;     for (int m = 0; m < NMU; ++m)
; #pragma unroll
;         for (int n = 0; n < 4; ++n) acc[m][n] = (f32x4){0.f, 0.f, 0.f, 0.f};
;     f32x2 s0[8], s1[8];
;     float g0[8];
;     MU_GLDS_A(0, 0); MU_B_ISSUE(s0, 0); MU_G_LOAD(g0, 0); MU_B_ISSUE(s1, 1);
;     MU_B_WAIT(s0, 8); MU_B_WRITE(s0, 0, g0); __builtin_amdgcn_sched_barrier(0); MU_B_ISSUE(s0, 2);
;     asm volatile("s_waitcnt vmcnt(16)" ::: "memory");
;     asm volatile("s_waitcnt lgkmcnt(0)" ::: "memory"); __builtin_amdgcn_s_barrier(); asm volatile("" ::: "memory");
; #pragma unroll 1
;     for (int t = 0; t < nt; t += 2) {
;         if (t + 2 < nt) MU_B_WAIT(s1, 8); else MU_B_WAIT(s1, 0);
;         MU_G_LOAD(g0, t + 1); MU_B_WRITE(s1, 1, g0); __builtin_amdgcn_sched_barrier(0); MU_GLDS_A(1, t + 1); __builtin_amdgcn_sched_barrier(0);
;         if (t + 3 < nt) { MU_B_ISSUE(s1, t + 3); }
;         MU_COMPUTE(0);
;         MU_END(t + 3 >= nt);
;         if (t + 2 < nt) { MU_B_WAIT(s0, 8); MU_G_LOAD(g0, t + 2); MU_B_WRITE(s0, 0, g0); __builtin_amdgcn_sched_barrier(0); MU_GLDS_A(0, t + 2); __builtin_amdgcn_sched_barrier(0); }
;         if (t + 4 < nt) { MU_B_ISSUE(s0, t + 4); }
;         MU_COMPUTE(1);
;         MU_END(t + 4 >= nt);
	s_mov_b32 s47, s42
	s_mov_b32 s42, s43
	s_mov_b32 s43, s44
	s_mov_b32 s44, s47
	v_mfma_f32_16x16x32_bf16 v[78:81], v[142:145], v[218:221], v[78:81]
	v_mfma_f32_16x16x32_bf16 v[74:77], v[146:149], v[218:221], v[74:77]
	v_mfma_f32_16x16x32_bf16 v[70:73], v[150:153], v[218:221], v[70:73]
	v_mfma_f32_16x16x32_bf16 v[66:69], v[154:157], v[218:221], v[66:69]
	v_mfma_f32_16x16x32_bf16 v[62:65], v[142:145], v[222:225], v[62:65]
	v_mfma_f32_16x16x32_bf16 v[58:61], v[146:149], v[222:225], v[58:61]
	v_mfma_f32_16x16x32_bf16 v[54:57], v[150:153], v[222:225], v[54:57]
	v_mfma_f32_16x16x32_bf16 v[50:53], v[154:157], v[222:225], v[50:53]
	v_mfma_f32_16x16x32_bf16 v[46:49], v[142:145], v[226:229], v[46:49]
	v_mfma_f32_16x16x32_bf16 v[42:45], v[146:149], v[226:229], v[42:45]
	v_mfma_f32_16x16x32_bf16 v[38:41], v[150:153], v[226:229], v[38:41]
	v_mfma_f32_16x16x32_bf16 v[34:37], v[154:157], v[226:229], v[34:37]
	v_mfma_f32_16x16x32_bf16 v[18:21], v[142:145], v[230:233], v[18:21]
	v_mfma_f32_16x16x32_bf16 v[22:25], v[146:149], v[230:233], v[22:25]
	v_mfma_f32_16x16x32_bf16 v[26:29], v[150:153], v[230:233], v[26:29]
	v_mfma_f32_16x16x32_bf16 v[30:33], v[154:157], v[230:233], v[30:33]
	v_mul_f32_e32 v202, s20, v202
	v_mul_f32_e32 v203, s20, v203
	v_mul_f32_e32 v204, s21, v204
	v_mul_f32_e32 v205, s21, v205
	v_mul_f32_e32 v206, s22, v206
	v_mul_f32_e32 v207, s22, v207
	v_mul_f32_e32 v208, s23, v208
	v_mul_f32_e32 v209, s23, v209
	v_mul_f32_e32 v210, s24, v210
	v_mul_f32_e32 v211, s24, v211
	v_mul_f32_e32 v212, s25, v212
	v_mul_f32_e32 v213, s25, v213
	v_mul_f32_e32 v214, s26, v214
	v_mul_f32_e32 v215, s26, v215
	v_mul_f32_e32 v216, s27, v216
	v_mul_f32_e32 v217, s27, v217
	v_cvt_pk_bf16_f32 v158, v202, v204
	v_cvt_pk_bf16_f32 v159, v206, v208
	v_cvt_pk_bf16_f32 v160, v210, v212
	v_cvt_pk_bf16_f32 v161, v214, v216
	v_cvt_pk_bf16_f32 v162, v203, v205
	v_cvt_pk_bf16_f32 v163, v207, v209
	v_cvt_pk_bf16_f32 v164, v211, v213
	v_cvt_pk_bf16_f32 v165, v215, v217
	ds_write_b128 v1, v[158:161] offset:19456
	ds_write_b128 v1, v[162:165] offset:19584
	v_add_u32_e32 v91, s42, v135
	v_add_u32_e32 v93, s42, v137
	ds_read_b128 v[238:241], v139 offset:0
	ds_read_b128 v[242:245], v139 offset:2048
	ds_read_b128 v[246:249], v139 offset:4096
	ds_read_b128 v[250:253], v139 offset:6144
	ds_read_b128 v[218:221], v91 offset:0
	ds_read_b128 v[222:225], v91 offset:2048
	ds_read_b128 v[226:229], v91 offset:4096
	ds_read_b128 v[230:233], v91 offset:6144
	s_waitcnt lgkmcnt(0)
	v_mfma_f32_16x16x32_bf16 v[78:81], v[238:241], v[218:221], v[78:81]
	v_mfma_f32_16x16x32_bf16 v[74:77], v[242:245], v[218:221], v[74:77]
	v_mfma_f32_16x16x32_bf16 v[70:73], v[246:249], v[218:221], v[70:73]
	v_mfma_f32_16x16x32_bf16 v[66:69], v[250:253], v[218:221], v[66:69]
	ds_read_b128 v[218:221], v93 offset:0
	ds_read_b128 v[142:145], v141 offset:0
	v_mfma_f32_16x16x32_bf16 v[62:65], v[238:241], v[222:225], v[62:65]
	v_mfma_f32_16x16x32_bf16 v[58:61], v[242:245], v[222:225], v[58:61]
	v_mfma_f32_16x16x32_bf16 v[54:57], v[246:249], v[222:225], v[54:57]
	v_mfma_f32_16x16x32_bf16 v[50:53], v[250:253], v[222:225], v[50:53]
	ds_read_b128 v[222:225], v93 offset:2048
	ds_read_b128 v[146:149], v141 offset:2048
	v_mfma_f32_16x16x32_bf16 v[46:49], v[238:241], v[226:229], v[46:49]
	v_mfma_f32_16x16x32_bf16 v[42:45], v[242:245], v[226:229], v[42:45]
	v_mfma_f32_16x16x32_bf16 v[38:41], v[246:249], v[226:229], v[38:41]
	v_mfma_f32_16x16x32_bf16 v[34:37], v[250:253], v[226:229], v[34:37]
	ds_read_b128 v[226:229], v93 offset:4096
	ds_read_b128 v[150:153], v141 offset:4096
	v_mfma_f32_16x16x32_bf16 v[18:21], v[238:241], v[230:233], v[18:21]
	v_mfma_f32_16x16x32_bf16 v[22:25], v[242:245], v[230:233], v[22:25]
	v_mfma_f32_16x16x32_bf16 v[26:29], v[246:249], v[230:233], v[26:29]
	v_mfma_f32_16x16x32_bf16 v[30:33], v[250:253], v[230:233], v[30:33]
	ds_read_b128 v[230:233], v93 offset:6144
	ds_read_b128 v[154:157], v141 offset:6144
	s_waitcnt vmcnt(0)
	s_waitcnt lgkmcnt(0)
	s_barrier
	s_mov_b32 s47, s42
	s_mov_b32 s42, s43
	s_mov_b32 s43, s44
	s_mov_b32 s44, s47
	v_mfma_f32_16x16x32_bf16 v[78:81], v[142:145], v[218:221], v[78:81]
	v_mfma_f32_16x16x32_bf16 v[74:77], v[146:149], v[218:221], v[74:77]
	v_mfma_f32_16x16x32_bf16 v[70:73], v[150:153], v[218:221], v[70:73]
	v_mfma_f32_16x16x32_bf16 v[66:69], v[154:157], v[218:221], v[66:69]
	v_mfma_f32_16x16x32_bf16 v[62:65], v[142:145], v[222:225], v[62:65]
	v_mfma_f32_16x16x32_bf16 v[58:61], v[146:149], v[222:225], v[58:61]
	v_mfma_f32_16x16x32_bf16 v[54:57], v[150:153], v[222:225], v[54:57]
	v_mfma_f32_16x16x32_bf16 v[50:53], v[154:157], v[222:225], v[50:53]
	v_mfma_f32_16x16x32_bf16 v[46:49], v[142:145], v[226:229], v[46:49]
	v_mfma_f32_16x16x32_bf16 v[42:45], v[146:149], v[226:229], v[42:45]
	v_mfma_f32_16x16x32_bf16 v[38:41], v[150:153], v[226:229], v[38:41]
	v_mfma_f32_16x16x32_bf16 v[34:37], v[154:157], v[226:229], v[34:37]
	v_mfma_f32_16x16x32_bf16 v[18:21], v[142:145], v[230:233], v[18:21]
	v_mfma_f32_16x16x32_bf16 v[22:25], v[146:149], v[230:233], v[22:25]
	v_mfma_f32_16x16x32_bf16 v[26:29], v[150:153], v[230:233], v[26:29]
	v_mfma_f32_16x16x32_bf16 v[30:33], v[154:157], v[230:233], v[30:33]
	v_add_u32_e32 v91, s42, v135
	v_add_u32_e32 v93, s42, v137
	ds_read_b128 v[238:241], v139 offset:19456
	ds_read_b128 v[242:245], v139 offset:21504
	ds_read_b128 v[246:249], v139 offset:23552
	ds_read_b128 v[250:253], v139 offset:25600
	ds_read_b128 v[218:221], v91 offset:0
	ds_read_b128 v[222:225], v91 offset:2048
	ds_read_b128 v[226:229], v91 offset:4096
	ds_read_b128 v[230:233], v91 offset:6144
	s_waitcnt lgkmcnt(0)
	v_mfma_f32_16x16x32_bf16 v[78:81], v[238:241], v[218:221], v[78:81]
	v_mfma_f32_16x16x32_bf16 v[74:77], v[242:245], v[218:221], v[74:77]
	v_mfma_f32_16x16x32_bf16 v[70:73], v[246:249], v[218:221], v[70:73]
	v_mfma_f32_16x16x32_bf16 v[66:69], v[250:253], v[218:221], v[66:69]
	ds_read_b128 v[218:221], v93 offset:0
	ds_read_b128 v[142:145], v141 offset:19456
	v_mfma_f32_16x16x32_bf16 v[62:65], v[238:241], v[222:225], v[62:65]
	v_mfma_f32_16x16x32_bf16 v[58:61], v[242:245], v[222:225], v[58:61]
	v_mfma_f32_16x16x32_bf16 v[54:57], v[246:249], v[222:225], v[54:57]
	v_mfma_f32_16x16x32_bf16 v[50:53], v[250:253], v[222:225], v[50:53]
	ds_read_b128 v[222:225], v93 offset:2048
	ds_read_b128 v[146:149], v141 offset:21504
	v_mfma_f32_16x16x32_bf16 v[46:49], v[238:241], v[226:229], v[46:49]
	v_mfma_f32_16x16x32_bf16 v[42:45], v[242:245], v[226:229], v[42:45]
	v_mfma_f32_16x16x32_bf16 v[38:41], v[246:249], v[226:229], v[38:41]
	v_mfma_f32_16x16x32_bf16 v[34:37], v[250:253], v[226:229], v[34:37]
	ds_read_b128 v[226:229], v93 offset:4096
	ds_read_b128 v[150:153], v141 offset:23552
	v_mfma_f32_16x16x32_bf16 v[18:21], v[238:241], v[230:233], v[18:21]
	v_mfma_f32_16x16x32_bf16 v[22:25], v[242:245], v[230:233], v[22:25]
	v_mfma_f32_16x16x32_bf16 v[26:29], v[246:249], v[230:233], v[26:29]
	v_mfma_f32_16x16x32_bf16 v[30:33], v[250:253], v[230:233], v[30:33]
	ds_read_b128 v[230:233], v93 offset:6144
	ds_read_b128 v[154:157], v141 offset:25600
	s_waitcnt lgkmcnt(0)
	s_barrier
; #define MU_GLDS_A(buf, kt) do { _Pragma("unroll") for (int i = 0; i < NMU; ++i) \
;         __builtin_amdgcn_global_load_lds((const unsigned*)((const char*)A + aoff[i] + (size_t)(kt) * 128), (PG8_LAS unsigned*)(MU_SA(buf) + wid * 1024 + i * 8192), 16, 0, 0); } while (0)
; #define MU_B_ISSUE(sb, kt) do { const char* kb_ = Bb + (size_t)(kt) * (64 * (size_t)RB); _Pragma("unroll") for (int j = 0; j < 8; ++j) { const char* p_ = kb_ + (size_t)j * RB; \
;         asm volatile("global_load_dwordx2 %0, %1, off" : "=&v"(sb[j]) : "v"(p_) : "memory"); } } while (0)
; #define MU_B_WAIT(sb, N) asm volatile("s_waitcnt vmcnt(%8)" : "+v"(sb[0]), "+v"(sb[1]), "+v"(sb[2]), "+v"(sb[3]), "+v"(sb[4]), "+v"(sb[5]), "+v"(sb[6]), "+v"(sb[7]) : "n"(N) : "memory")
; #define MU_COMPUTE(buf) MU_COMPUTE_N(buf, NMU)
; template <int MODE>
; __device__ __forceinline__ void moe_unit(PG8_LAS unsigned char* lds, int e, int cb, int slot0  , int nv  , const bf16_t* A, const int* slot_tok,
;                                          const float* W0, const float* W1, bf16_t* OUT, const float* slot_rs  , const int* slot_dst) {
;     ...
;     f32x4 acc[NMU][4];
; #pragma unroll
;     for (int m = 0; m < NMU; ++m)
; #pragma unroll
;         for (int n = 0; n < 4; ++n) acc[m][n] = (f32x4){0.f, 0.f, 0.f, 0.f};
;     f32x2 s0[8], s1[8];
;     float g0[8];
;     MU_GLDS_A(0, 0); MU_B_ISSUE(s0, 0); MU_G_LOAD(g0, 0); MU_B_ISSUE(s1, 1);
;     MU_B_WAIT(s0, 8); MU_B_WRITE(s0, 0, g0); __builtin_amdgcn_sched_barrier(0); MU_B_ISSUE(s0, 2);
;     asm volatile("s_waitcnt vmcnt(16)" ::: "memory");
;     asm volatile("s_waitcnt lgkmcnt(0)" ::: "memory"); __builtin_amdgcn_s_barrier(); asm volatile("" ::: "memory");
; #pragma unroll 1
;     for (int t = 0; t < nt; t += 2) {
;         if (t + 2 < nt) MU_B_WAIT(s1, 8); else MU_B_WAIT(s1, 0);
;         MU_G_LOAD(g0, t + 1); MU_B_WRITE(s1, 1, g0); __builtin_amdgcn_sched_barrier(0); MU_GLDS_A(1, t + 1); __builtin_amdgcn_sched_barrier(0);
;         if (t + 3 < nt) { MU_B_ISSUE(s1, t + 3); }
;         MU_COMPUTE(0);
;         MU_END(t + 3 >= nt);
;         if (t + 2 < nt) { MU_B_WAIT(s0, 8); MU_G_LOAD(g0, t + 2); MU_B_WRITE(s0, 0, g0); __builtin_amdgcn_sched_barrier(0); MU_GLDS_A(0, t + 2); __builtin_amdgcn_sched_barrier(0); }
;         if (t + 4 < nt) { MU_B_ISSUE(s0, t + 4); }
;         MU_COMPUTE(1);
;         MU_END(t + 4 >= nt);
	s_mov_b32 s47, s42
	s_mov_b32 s42, s43
	s_mov_b32 s43, s44
	s_mov_b32 s44, s47
	v_mfma_f32_16x16x32_bf16 v[78:81], v[142:145], v[218:221], v[78:81]
	v_mfma_f32_16x16x32_bf16 v[74:77], v[146:149], v[218:221], v[74:77]
	v_mfma_f32_16x16x32_bf16 v[70:73], v[150:153], v[218:221], v[70:73]
	v_mfma_f32_16x16x32_bf16 v[66:69], v[154:157], v[218:221], v[66:69]
	v_mfma_f32_16x16x32_bf16 v[62:65], v[142:145], v[222:225], v[62:65]
	v_mfma_f32_16x16x32_bf16 v[58:61], v[146:149], v[222:225], v[58:61]
	v_mfma_f32_16x16x32_bf16 v[54:57], v[150:153], v[222:225], v[54:57]
	v_mfma_f32_16x16x32_bf16 v[50:53], v[154:157], v[222:225], v[50:53]
	v_mfma_f32_16x16x32_bf16 v[46:49], v[142:145], v[226:229], v[46:49]
	v_mfma_f32_16x16x32_bf16 v[42:45], v[146:149], v[226:229], v[42:45]
	v_mfma_f32_16x16x32_bf16 v[38:41], v[150:153], v[226:229], v[38:41]
	v_mfma_f32_16x16x32_bf16 v[34:37], v[154:157], v[226:229], v[34:37]
	v_mfma_f32_16x16x32_bf16 v[18:21], v[142:145], v[230:233], v[18:21]
	v_mfma_f32_16x16x32_bf16 v[22:25], v[146:149], v[230:233], v[22:25]
	v_mfma_f32_16x16x32_bf16 v[26:29], v[150:153], v[230:233], v[26:29]
	v_mfma_f32_16x16x32_bf16 v[30:33], v[154:157], v[230:233], v[30:33]
	s_branch .Lmu_done
.Lmu_frag5:
	s_cmp_gt_u32 s62, 3
	s_cbranch_scc1 .Lmu_grpY5
	s_waitcnt vmcnt(24)
	v_mul_f32_e32 v114, s20, v114
	v_mul_f32_e32 v115, s20, v115
	v_mul_f32_e32 v116, s21, v116
	v_mul_f32_e32 v117, s21, v117
	v_mul_f32_e32 v118, s22, v118
	v_mul_f32_e32 v119, s22, v119
	v_mul_f32_e32 v120, s23, v120
	v_mul_f32_e32 v121, s23, v121
	v_mul_f32_e32 v122, s24, v122
	v_mul_f32_e32 v123, s24, v123
	v_mul_f32_e32 v124, s25, v124
	v_mul_f32_e32 v125, s25, v125
	v_mul_f32_e32 v126, s26, v126
	v_mul_f32_e32 v127, s26, v127
	v_mul_f32_e32 v128, s27, v128
	v_mul_f32_e32 v129, s27, v129
	v_cvt_pk_bf16_f32 v158, v114, v116
	v_cvt_pk_bf16_f32 v159, v118, v120
	v_cvt_pk_bf16_f32 v160, v122, v124
	v_cvt_pk_bf16_f32 v161, v126, v128
	v_cvt_pk_bf16_f32 v162, v115, v117
	v_cvt_pk_bf16_f32 v163, v119, v121
	v_cvt_pk_bf16_f32 v164, v123, v125
	v_cvt_pk_bf16_f32 v165, v127, v129
	ds_write_b128 v1, v[158:161] offset:19456
	ds_write_b128 v1, v[162:165] offset:19584
	v_add_u32_e32 v91, s42, v135
	v_add_u32_e32 v93, s42, v137
	ds_read_b128 v[238:241], v139 offset:0
	ds_read_b128 v[242:245], v139 offset:2048
	ds_read_b128 v[246:249], v139 offset:4096
	ds_read_b128 v[250:253], v139 offset:6144
	ds_read_b128 v[218:221], v91 offset:0
	ds_read_b128 v[222:225], v91 offset:2048
	ds_read_b128 v[226:229], v91 offset:4096
	ds_read_b128 v[230:233], v91 offset:6144
	ds_read_b128 v[234:237], v91 offset:8192
	s_add_i32 s47, s44, s6
	s_add_u32 s30, s30, 0x80
	s_addc_u32 s31, s31, 0
	s_waitcnt lgkmcnt(0)
	v_mfma_f32_16x16x32_bf16 v[78:81], v[238:241], v[218:221], v[78:81]
	v_mfma_f32_16x16x32_bf16 v[74:77], v[242:245], v[218:221], v[74:77]
	v_mfma_f32_16x16x32_bf16 v[70:73], v[246:249], v[218:221], v[70:73]
	v_mfma_f32_16x16x32_bf16 v[66:69], v[250:253], v[218:221], v[66:69]
	ds_read_b128 v[218:221], v93 offset:0
	ds_read_b128 v[142:145], v141 offset:0
	s_mov_b32 m0, s47
	s_nop 0
	global_load_lds_dwordx4 v86, s[30:31]
	v_mfma_f32_16x16x32_bf16 v[62:65], v[238:241], v[222:225], v[62:65]
	v_mfma_f32_16x16x32_bf16 v[58:61], v[242:245], v[222:225], v[58:61]
	v_mfma_f32_16x16x32_bf16 v[54:57], v[246:249], v[222:225], v[54:57]
	v_mfma_f32_16x16x32_bf16 v[50:53], v[250:253], v[222:225], v[50:53]
	ds_read_b128 v[222:225], v93 offset:2048
	ds_read_b128 v[146:149], v141 offset:2048
	s_add_i32 m0, s47, 0x2000
	s_nop 0
	global_load_lds_dwordx4 v134, s[30:31]
	v_mfma_f32_16x16x32_bf16 v[46:49], v[238:241], v[226:229], v[46:49]
	v_mfma_f32_16x16x32_bf16 v[42:45], v[242:245], v[226:229], v[42:45]
	v_mfma_f32_16x16x32_bf16 v[38:41], v[246:249], v[226:229], v[38:41]
	v_mfma_f32_16x16x32_bf16 v[34:37], v[250:253], v[226:229], v[34:37]
	ds_read_b128 v[226:229], v93 offset:4096
	ds_read_b128 v[150:153], v141 offset:4096
	s_add_i32 m0, s47, 0x4000
	s_nop 0
	global_load_lds_dwordx4 v136, s[30:31]
	v_mfma_f32_16x16x32_bf16 v[18:21], v[238:241], v[230:233], v[18:21]
	v_mfma_f32_16x16x32_bf16 v[22:25], v[242:245], v[230:233], v[22:25]
	v_mfma_f32_16x16x32_bf16 v[26:29], v[246:249], v[230:233], v[26:29]
	v_mfma_f32_16x16x32_bf16 v[30:33], v[250:253], v[230:233], v[30:33]
	ds_read_b128 v[230:233], v93 offset:6144
	ds_read_b128 v[154:157], v141 offset:6144
	s_add_i32 m0, s47, 0x6000
	s_nop 0
	global_load_lds_dwordx4 v138, s[30:31]
	v_mfma_f32_16x16x32_bf16 v[2:5], v[238:241], v[234:237], v[2:5]
	v_mfma_f32_16x16x32_bf16 v[6:9], v[242:245], v[234:237], v[6:9]
	v_mfma_f32_16x16x32_bf16 v[10:13], v[246:249], v[234:237], v[10:13]
	v_mfma_f32_16x16x32_bf16 v[14:17], v[250:253], v[234:237], v[14:17]
	ds_read_b128 v[234:237], v93 offset:8192
	s_add_i32 m0, s47, 0x8000
	s_nop 0
	global_load_lds_dwordx4 v140, s[30:31]
	s_waitcnt lgkmcnt(0)
	s_load_dwordx8 s[12:19], s[28:29], 0x0
	s_add_u32 s28, s28, 0x100
	s_addc_u32 s29, s29, 0
	v_mfma_f32_16x16x32_bf16 v[78:81], v[142:145], v[218:221], v[78:81]
	v_mfma_f32_16x16x32_bf16 v[74:77], v[146:149], v[218:221], v[74:77]
	v_mfma_f32_16x16x32_bf16 v[70:73], v[150:153], v[218:221], v[70:73]
	v_mfma_f32_16x16x32_bf16 v[66:69], v[154:157], v[218:221], v[66:69]
	v_lshl_add_u64 v[132:133], v[132:133], 0, s[40:41]
	global_load_dwordx2 v[114:115], v[132:133], off
	global_load_dwordx2 v[116:117], v[132:133], off offset:2048
	v_mfma_f32_16x16x32_bf16 v[62:65], v[142:145], v[222:225], v[62:65]
	v_mfma_f32_16x16x32_bf16 v[58:61], v[146:149], v[222:225], v[58:61]
	v_mfma_f32_16x16x32_bf16 v[54:57], v[150:153], v[222:225], v[54:57]
	v_mfma_f32_16x16x32_bf16 v[50:53], v[154:157], v[222:225], v[50:53]
	v_lshl_add_u64 v[166:167], v[132:133], 0, s[34:35]
	global_load_dwordx2 v[118:119], v[166:167], off
	global_load_dwordx2 v[120:121], v[166:167], off offset:2048
	v_mfma_f32_16x16x32_bf16 v[46:49], v[142:145], v[226:229], v[46:49]
	v_mfma_f32_16x16x32_bf16 v[42:45], v[146:149], v[226:229], v[42:45]
	v_mfma_f32_16x16x32_bf16 v[38:41], v[150:153], v[226:229], v[38:41]
	v_mfma_f32_16x16x32_bf16 v[34:37], v[154:157], v[226:229], v[34:37]
	v_lshl_add_u64 v[166:167], v[132:133], 0, s[36:37]
	global_load_dwordx2 v[122:123], v[166:167], off
	global_load_dwordx2 v[124:125], v[166:167], off offset:2048
	v_mfma_f32_16x16x32_bf16 v[18:21], v[142:145], v[230:233], v[18:21]
	v_mfma_f32_16x16x32_bf16 v[22:25], v[146:149], v[230:233], v[22:25]
	v_mfma_f32_16x16x32_bf16 v[26:29], v[150:153], v[230:233], v[26:29]
	v_mfma_f32_16x16x32_bf16 v[30:33], v[154:157], v[230:233], v[30:33]
	v_lshl_add_u64 v[166:167], v[132:133], 0, s[38:39]
	global_load_dwordx2 v[126:127], v[166:167], off
	global_load_dwordx2 v[128:129], v[166:167], off offset:2048
	v_mfma_f32_16x16x32_bf16 v[2:5], v[142:145], v[234:237], v[2:5]
	v_mfma_f32_16x16x32_bf16 v[6:9], v[146:149], v[234:237], v[6:9]
	v_mfma_f32_16x16x32_bf16 v[10:13], v[150:153], v[234:237], v[10:13]
	v_mfma_f32_16x16x32_bf16 v[14:17], v[154:157], v[234:237], v[14:17]
	s_waitcnt lgkmcnt(0)
	s_barrier
; #define MU_GLDS_A(buf, kt) do { _Pragma("unroll") for (int i = 0; i < NMU; ++i) \
;         __builtin_amdgcn_global_load_lds((const unsigned*)((const char*)A + aoff[i] + (size_t)(kt) * 128), (PG8_LAS unsigned*)(MU_SA(buf) + wid * 1024 + i * 8192), 16, 0, 0); } while (0)
; #define MU_B_ISSUE(sb, kt) do { const char* kb_ = Bb + (size_t)(kt) * (64 * (size_t)RB); _Pragma("unroll") for (int j = 0; j < 8; ++j) { const char* p_ = kb_ + (size_t)j * RB; \
;         asm volatile("global_load_dwordx2 %0, %1, off" : "=&v"(sb[j]) : "v"(p_) : "memory"); } } while (0)
; #define MU_B_WAIT(sb, N) asm volatile("s_waitcnt vmcnt(%8)" : "+v"(sb[0]), "+v"(sb[1]), "+v"(sb[2]), "+v"(sb[3]), "+v"(sb[4]), "+v"(sb[5]), "+v"(sb[6]), "+v"(sb[7]) : "n"(N) : "memory")
; #define MU_COMPUTE(buf) MU_COMPUTE_N(buf, NMU)
; template <int MODE>
; __device__ __forceinline__ void moe_unit(PG8_LAS unsigned char* lds, int e, int cb, int slot0  , int nv  , const bf16_t* A, const int* slot_tok,
;                                          const float* W0, const float* W1, bf16_t* OUT, const float* slot_rs  , const int* slot_dst) {
;     ...
;     f32x4 acc[NMU][4];
; #pragma unroll
;     for (int m = 0; m < NMU; ++m)
; #pragma unroll
;         for (int n = 0; n < 4; ++n) acc[m][n] = (f32x4){0.f, 0.f, 0.f, 0.f};
;     f32x2 s0[8], s1[8];
;     float g0[8];
;     MU_GLDS_A(0, 0); MU_B_ISSUE(s0, 0); MU_G_LOAD(g0, 0); MU_B_ISSUE(s1, 1);
;     MU_B_WAIT(s0, 8); MU_B_WRITE(s0, 0, g0); __builtin_amdgcn_sched_barrier(0); MU_B_ISSUE(s0, 2);
;     asm volatile("s_waitcnt vmcnt(16)" ::: "memory");
;     asm volatile("s_waitcnt lgkmcnt(0)" ::: "memory"); __builtin_amdgcn_s_barrier(); asm volatile("" ::: "memory");
; #pragma unroll 1
;     for (int t = 0; t < nt; t += 2) {
;         if (t + 2 < nt) MU_B_WAIT(s1, 8); else MU_B_WAIT(s1, 0);
;         MU_G_LOAD(g0, t + 1); MU_B_WRITE(s1, 1, g0); __builtin_amdgcn_sched_barrier(0); MU_GLDS_A(1, t + 1); __builtin_amdgcn_sched_barrier(0);
;         if (t + 3 < nt) { MU_B_ISSUE(s1, t + 3); }
;         MU_COMPUTE(0);
;         MU_END(t + 3 >= nt);
;         if (t + 2 < nt) { MU_B_WAIT(s0, 8); MU_G_LOAD(g0, t + 2); MU_B_WRITE(s0, 0, g0); __builtin_amdgcn_sched_barrier(0); MU_GLDS_A(0, t + 2); __builtin_amdgcn_sched_barrier(0); }
;         if (t + 4 < nt) { MU_B_ISSUE(s0, t + 4); }
;         MU_COMPUTE(1);
;         MU_END(t + 4 >= nt);
	s_mov_b32 s47, s42
	s_mov_b32 s42, s43
	s_mov_b32 s43, s44
	s_mov_b32 s44, s47
	s_waitcnt vmcnt(29)
	v_mul_f32_e32 v186, s12, v186
	v_mul_f32_e32 v187, s12, v187
	v_mul_f32_e32 v188, s13, v188
	v_mul_f32_e32 v189, s13, v189
	v_mul_f32_e32 v190, s14, v190
	v_mul_f32_e32 v191, s14, v191
	v_mul_f32_e32 v192, s15, v192
	v_mul_f32_e32 v193, s15, v193
	v_mul_f32_e32 v194, s16, v194
	v_mul_f32_e32 v195, s16, v195
	v_mul_f32_e32 v196, s17, v196
	v_mul_f32_e32 v197, s17, v197
	v_mul_f32_e32 v198, s18, v198
	v_mul_f32_e32 v199, s18, v199
	v_mul_f32_e32 v200, s19, v200
	v_mul_f32_e32 v201, s19, v201
	v_cvt_pk_bf16_f32 v158, v186, v188
	v_cvt_pk_bf16_f32 v159, v190, v192
	v_cvt_pk_bf16_f32 v160, v194, v196
	v_cvt_pk_bf16_f32 v161, v198, v200
	v_cvt_pk_bf16_f32 v162, v187, v189
	v_cvt_pk_bf16_f32 v163, v191, v193
	v_cvt_pk_bf16_f32 v164, v195, v197
	v_cvt_pk_bf16_f32 v165, v199, v201
	ds_write_b128 v1, v[158:161] offset:0
	ds_write_b128 v1, v[162:165] offset:128
	v_add_u32_e32 v91, s42, v135
	v_add_u32_e32 v93, s42, v137
	ds_read_b128 v[238:241], v139 offset:19456
	ds_read_b128 v[242:245], v139 offset:21504
	ds_read_b128 v[246:249], v139 offset:23552
	ds_read_b128 v[250:253], v139 offset:25600
	ds_read_b128 v[218:221], v91 offset:0
	ds_read_b128 v[222:225], v91 offset:2048
	ds_read_b128 v[226:229], v91 offset:4096
	ds_read_b128 v[230:233], v91 offset:6144
	ds_read_b128 v[234:237], v91 offset:8192
	s_add_i32 s47, s44, s6
	s_add_u32 s30, s30, 0x80
	s_addc_u32 s31, s31, 0
	s_waitcnt lgkmcnt(0)
	v_mfma_f32_16x16x32_bf16 v[78:81], v[238:241], v[218:221], v[78:81]
	v_mfma_f32_16x16x32_bf16 v[74:77], v[242:245], v[218:221], v[74:77]
	v_mfma_f32_16x16x32_bf16 v[70:73], v[246:249], v[218:221], v[70:73]
	v_mfma_f32_16x16x32_bf16 v[66:69], v[250:253], v[218:221], v[66:69]
	ds_read_b128 v[218:221], v93 offset:0
	ds_read_b128 v[142:145], v141 offset:19456
	s_mov_b32 m0, s47
	s_nop 0
	global_load_lds_dwordx4 v86, s[30:31]
	v_mfma_f32_16x16x32_bf16 v[62:65], v[238:241], v[222:225], v[62:65]
	v_mfma_f32_16x16x32_bf16 v[58:61], v[242:245], v[222:225], v[58:61]
	v_mfma_f32_16x16x32_bf16 v[54:57], v[246:249], v[222:225], v[54:57]
	v_mfma_f32_16x16x32_bf16 v[50:53], v[250:253], v[222:225], v[50:53]
	ds_read_b128 v[222:225], v93 offset:2048
	ds_read_b128 v[146:149], v141 offset:21504
	s_add_i32 m0, s47, 0x2000
	s_nop 0
	global_load_lds_dwordx4 v134, s[30:31]
	v_mfma_f32_16x16x32_bf16 v[46:49], v[238:241], v[226:229], v[46:49]
	v_mfma_f32_16x16x32_bf16 v[42:45], v[242:245], v[226:229], v[42:45]
	v_mfma_f32_16x16x32_bf16 v[38:41], v[246:249], v[226:229], v[38:41]
	v_mfma_f32_16x16x32_bf16 v[34:37], v[250:253], v[226:229], v[34:37]
	ds_read_b128 v[226:229], v93 offset:4096
	ds_read_b128 v[150:153], v141 offset:23552
	s_add_i32 m0, s47, 0x4000
	s_nop 0
	global_load_lds_dwordx4 v136, s[30:31]
	v_mfma_f32_16x16x32_bf16 v[18:21], v[238:241], v[230:233], v[18:21]
	v_mfma_f32_16x16x32_bf16 v[22:25], v[242:245], v[230:233], v[22:25]
	v_mfma_f32_16x16x32_bf16 v[26:29], v[246:249], v[230:233], v[26:29]
	v_mfma_f32_16x16x32_bf16 v[30:33], v[250:253], v[230:233], v[30:33]
	ds_read_b128 v[230:233], v93 offset:6144
	ds_read_b128 v[154:157], v141 offset:25600
	s_add_i32 m0, s47, 0x6000
	s_nop 0
	global_load_lds_dwordx4 v138, s[30:31]
	v_mfma_f32_16x16x32_bf16 v[2:5], v[238:241], v[234:237], v[2:5]
	v_mfma_f32_16x16x32_bf16 v[6:9], v[242:245], v[234:237], v[6:9]
	v_mfma_f32_16x16x32_bf16 v[10:13], v[246:249], v[234:237], v[10:13]
	v_mfma_f32_16x16x32_bf16 v[14:17], v[250:253], v[234:237], v[14:17]
	ds_read_b128 v[234:237], v93 offset:8192
	s_add_i32 m0, s47, 0x8000
	s_nop 0
	global_load_lds_dwordx4 v140, s[30:31]
	s_waitcnt lgkmcnt(0)
	s_load_dwordx8 s[20:27], s[28:29], 0x0
	s_add_u32 s28, s28, 0x100
	s_addc_u32 s29, s29, 0
	v_mfma_f32_16x16x32_bf16 v[78:81], v[142:145], v[218:221], v[78:81]
	v_mfma_f32_16x16x32_bf16 v[74:77], v[146:149], v[218:221], v[74:77]
	v_mfma_f32_16x16x32_bf16 v[70:73], v[150:153], v[218:221], v[70:73]
	v_mfma_f32_16x16x32_bf16 v[66:69], v[154:157], v[218:221], v[66:69]
	v_lshl_add_u64 v[132:133], v[132:133], 0, s[40:41]
	global_load_dwordx2 v[186:187], v[132:133], off
	global_load_dwordx2 v[188:189], v[132:133], off offset:2048
	v_mfma_f32_16x16x32_bf16 v[62:65], v[142:145], v[222:225], v[62:65]
	v_mfma_f32_16x16x32_bf16 v[58:61], v[146:149], v[222:225], v[58:61]
	v_mfma_f32_16x16x32_bf16 v[54:57], v[150:153], v[222:225], v[54:57]
	v_mfma_f32_16x16x32_bf16 v[50:53], v[154:157], v[222:225], v[50:53]
	v_lshl_add_u64 v[166:167], v[132:133], 0, s[34:35]
	global_load_dwordx2 v[190:191], v[166:167], off
	global_load_dwordx2 v[192:193], v[166:167], off offset:2048
	v_mfma_f32_16x16x32_bf16 v[46:49], v[142:145], v[226:229], v[46:49]
	v_mfma_f32_16x16x32_bf16 v[42:45], v[146:149], v[226:229], v[42:45]
	v_mfma_f32_16x16x32_bf16 v[38:41], v[150:153], v[226:229], v[38:41]
	v_mfma_f32_16x16x32_bf16 v[34:37], v[154:157], v[226:229], v[34:37]
	v_lshl_add_u64 v[166:167], v[132:133], 0, s[36:37]
	global_load_dwordx2 v[194:195], v[166:167], off
	global_load_dwordx2 v[196:197], v[166:167], off offset:2048
	v_mfma_f32_16x16x32_bf16 v[18:21], v[142:145], v[230:233], v[18:21]
	v_mfma_f32_16x16x32_bf16 v[22:25], v[146:149], v[230:233], v[22:25]
	v_mfma_f32_16x16x32_bf16 v[26:29], v[150:153], v[230:233], v[26:29]
	v_mfma_f32_16x16x32_bf16 v[30:33], v[154:157], v[230:233], v[30:33]
	v_lshl_add_u64 v[166:167], v[132:133], 0, s[38:39]
	global_load_dwordx2 v[198:199], v[166:167], off
	global_load_dwordx2 v[200:201], v[166:167], off offset:2048
	v_mfma_f32_16x16x32_bf16 v[2:5], v[142:145], v[234:237], v[2:5]
	v_mfma_f32_16x16x32_bf16 v[6:9], v[146:149], v[234:237], v[6:9]
	v_mfma_f32_16x16x32_bf16 v[10:13], v[150:153], v[234:237], v[10:13]
	v_mfma_f32_16x16x32_bf16 v[14:17], v[154:157], v[234:237], v[14:17]
	s_waitcnt vmcnt(21)
	s_waitcnt lgkmcnt(0)
	s_barrier
; #define MU_GLDS_A(buf, kt) do { _Pragma("unroll") for (int i = 0; i < NMU; ++i) \
;         __builtin_amdgcn_global_load_lds((const unsigned*)((const char*)A + aoff[i] + (size_t)(kt) * 128), (PG8_LAS unsigned*)(MU_SA(buf) + wid * 1024 + i * 8192), 16, 0, 0); } while (0)
; #define MU_B_ISSUE(sb, kt) do { const char* kb_ = Bb + (size_t)(kt) * (64 * (size_t)RB); _Pragma("unroll") for (int j = 0; j < 8; ++j) { const char* p_ = kb_ + (size_t)j * RB; \
;         asm volatile("global_load_dwordx2 %0, %1, off" : "=&v"(sb[j]) : "v"(p_) : "memory"); } } while (0)
; #define MU_B_WAIT(sb, N) asm volatile("s_waitcnt vmcnt(%8)" : "+v"(sb[0]), "+v"(sb[1]), "+v"(sb[2]), "+v"(sb[3]), "+v"(sb[4]), "+v"(sb[5]), "+v"(sb[6]), "+v"(sb[7]) : "n"(N) : "memory")
; #define MU_COMPUTE(buf) MU_COMPUTE_N(buf, NMU)
; template <int MODE>
; __device__ __forceinline__ void moe_unit(PG8_LAS unsigned char* lds, int e, int cb, int slot0  , int nv  , const bf16_t* A, const int* slot_tok,
;                                          const float* W0, const float* W1, bf16_t* OUT, const float* slot_rs  , const int* slot_dst) {
;     ...
;     f32x4 acc[NMU][4];
; #pragma unroll
;     for (int m = 0; m < NMU; ++m)
; #pragma unroll
;         for (int n = 0; n < 4; ++n) acc[m][n] = (f32x4){0.f, 0.f, 0.f, 0.f};
;     f32x2 s0[8], s1[8];
;     float g0[8];
;     MU_GLDS_A(0, 0); MU_B_ISSUE(s0, 0); MU_G_LOAD(g0, 0); MU_B_ISSUE(s1, 1);
;     MU_B_WAIT(s0, 8); MU_B_WRITE(s0, 0, g0); __builtin_amdgcn_sched_barrier(0); MU_B_ISSUE(s0, 2);
;     asm volatile("s_waitcnt vmcnt(16)" ::: "memory");
;     asm volatile("s_waitcnt lgkmcnt(0)" ::: "memory"); __builtin_amdgcn_s_barrier(); asm volatile("" ::: "memory");
; #pragma unroll 1
;     for (int t = 0; t < nt; t += 2) {
;         if (t + 2 < nt) MU_B_WAIT(s1, 8); else MU_B_WAIT(s1, 0);
;         MU_G_LOAD(g0, t + 1); MU_B_WRITE(s1, 1, g0); __builtin_amdgcn_sched_barrier(0); MU_GLDS_A(1, t + 1); __builtin_amdgcn_sched_barrier(0);
;         if (t + 3 < nt) { MU_B_ISSUE(s1, t + 3); }
;         MU_COMPUTE(0);
;         MU_END(t + 3 >= nt);
;         if (t + 2 < nt) { MU_B_WAIT(s0, 8); MU_G_LOAD(g0, t + 2); MU_B_WRITE(s0, 0, g0); __builtin_amdgcn_sched_barrier(0); MU_GLDS_A(0, t + 2); __builtin_amdgcn_sched_barrier(0); }
;         if (t + 4 < nt) { MU_B_ISSUE(s0, t + 4); }
;         MU_COMPUTE(1);
;         MU_END(t + 4 >= nt);
	s_mov_b32 s47, s42
	s_mov_b32 s42, s43
	s_mov_b32 s43, s44
	s_mov_b32 s44, s47
	v_mul_f32_e32 v202, s20, v202
	v_mul_f32_e32 v203, s20, v203
	v_mul_f32_e32 v204, s21, v204
	v_mul_f32_e32 v205, s21, v205
	v_mul_f32_e32 v206, s22, v206
	v_mul_f32_e32 v207, s22, v207
	v_mul_f32_e32 v208, s23, v208
	v_mul_f32_e32 v209, s23, v209
	v_mul_f32_e32 v210, s24, v210
	v_mul_f32_e32 v211, s24, v211
	v_mul_f32_e32 v212, s25, v212
	v_mul_f32_e32 v213, s25, v213
	v_mul_f32_e32 v214, s26, v214
	v_mul_f32_e32 v215, s26, v215
	v_mul_f32_e32 v216, s27, v216
	v_mul_f32_e32 v217, s27, v217
	v_cvt_pk_bf16_f32 v158, v202, v204
	v_cvt_pk_bf16_f32 v159, v206, v208
	v_cvt_pk_bf16_f32 v160, v210, v212
	v_cvt_pk_bf16_f32 v161, v214, v216
	v_cvt_pk_bf16_f32 v162, v203, v205
	v_cvt_pk_bf16_f32 v163, v207, v209
	v_cvt_pk_bf16_f32 v164, v211, v213
	v_cvt_pk_bf16_f32 v165, v215, v217
	ds_write_b128 v1, v[158:161] offset:19456
	ds_write_b128 v1, v[162:165] offset:19584
	v_add_u32_e32 v91, s42, v135
	v_add_u32_e32 v93, s42, v137
	ds_read_b128 v[238:241], v139 offset:0
	ds_read_b128 v[242:245], v139 offset:2048
	ds_read_b128 v[246:249], v139 offset:4096
	ds_read_b128 v[250:253], v139 offset:6144
	ds_read_b128 v[218:221], v91 offset:0
	ds_read_b128 v[222:225], v91 offset:2048
	ds_read_b128 v[226:229], v91 offset:4096
	ds_read_b128 v[230:233], v91 offset:6144
	ds_read_b128 v[234:237], v91 offset:8192
	s_add_i32 s47, s44, s6
	s_add_u32 s30, s30, 0x80
	s_addc_u32 s31, s31, 0
	s_waitcnt lgkmcnt(0)
	v_mfma_f32_16x16x32_bf16 v[78:81], v[238:241], v[218:221], v[78:81]
	v_mfma_f32_16x16x32_bf16 v[74:77], v[242:245], v[218:221], v[74:77]
	v_mfma_f32_16x16x32_bf16 v[70:73], v[246:249], v[218:221], v[70:73]
	v_mfma_f32_16x16x32_bf16 v[66:69], v[250:253], v[218:221], v[66:69]
	ds_read_b128 v[218:221], v93 offset:0
	ds_read_b128 v[142:145], v141 offset:0
	s_mov_b32 m0, s47
	s_nop 0
	global_load_lds_dwordx4 v86, s[30:31]
	v_mfma_f32_16x16x32_bf16 v[62:65], v[238:241], v[222:225], v[62:65]
	v_mfma_f32_16x16x32_bf16 v[58:61], v[242:245], v[222:225], v[58:61]
	v_mfma_f32_16x16x32_bf16 v[54:57], v[246:249], v[222:225], v[54:57]
	v_mfma_f32_16x16x32_bf16 v[50:53], v[250:253], v[222:225], v[50:53]
	ds_read_b128 v[222:225], v93 offset:2048
	ds_read_b128 v[146:149], v141 offset:2048
	s_add_i32 m0, s47, 0x2000
	s_nop 0
	global_load_lds_dwordx4 v134, s[30:31]
	v_mfma_f32_16x16x32_bf16 v[46:49], v[238:241], v[226:229], v[46:49]
	v_mfma_f32_16x16x32_bf16 v[42:45], v[242:245], v[226:229], v[42:45]
	v_mfma_f32_16x16x32_bf16 v[38:41], v[246:249], v[226:229], v[38:41]
	v_mfma_f32_16x16x32_bf16 v[34:37], v[250:253], v[226:229], v[34:37]
	ds_read_b128 v[226:229], v93 offset:4096
	ds_read_b128 v[150:153], v141 offset:4096
	s_add_i32 m0, s47, 0x4000
	s_nop 0
	global_load_lds_dwordx4 v136, s[30:31]
	v_mfma_f32_16x16x32_bf16 v[18:21], v[238:241], v[230:233], v[18:21]
	v_mfma_f32_16x16x32_bf16 v[22:25], v[242:245], v[230:233], v[22:25]
	v_mfma_f32_16x16x32_bf16 v[26:29], v[246:249], v[230:233], v[26:29]
	v_mfma_f32_16x16x32_bf16 v[30:33], v[250:253], v[230:233], v[30:33]
	ds_read_b128 v[230:233], v93 offset:6144
	ds_read_b128 v[154:157], v141 offset:6144
	s_add_i32 m0, s47, 0x6000
	s_nop 0
	global_load_lds_dwordx4 v138, s[30:31]
	v_mfma_f32_16x16x32_bf16 v[2:5], v[238:241], v[234:237], v[2:5]
	v_mfma_f32_16x16x32_bf16 v[6:9], v[242:245], v[234:237], v[6:9]
	v_mfma_f32_16x16x32_bf16 v[10:13], v[246:249], v[234:237], v[10:13]
	v_mfma_f32_16x16x32_bf16 v[14:17], v[250:253], v[234:237], v[14:17]
	ds_read_b128 v[234:237], v93 offset:8192
	s_add_i32 m0, s47, 0x8000
	s_nop 0
	global_load_lds_dwordx4 v140, s[30:31]
	s_waitcnt lgkmcnt(0)
	s_load_dwordx8 s[12:19], s[28:29], 0x0
	s_add_u32 s28, s28, 0x100
	s_addc_u32 s29, s29, 0
	v_mfma_f32_16x16x32_bf16 v[78:81], v[142:145], v[218:221], v[78:81]
	v_mfma_f32_16x16x32_bf16 v[74:77], v[146:149], v[218:221], v[74:77]
	v_mfma_f32_16x16x32_bf16 v[70:73], v[150:153], v[218:221], v[70:73]
	v_mfma_f32_16x16x32_bf16 v[66:69], v[154:157], v[218:221], v[66:69]
	v_lshl_add_u64 v[132:133], v[132:133], 0, s[40:41]
	global_load_dwordx2 v[202:203], v[132:133], off
	global_load_dwordx2 v[204:205], v[132:133], off offset:2048
	v_mfma_f32_16x16x32_bf16 v[62:65], v[142:145], v[222:225], v[62:65]
	v_mfma_f32_16x16x32_bf16 v[58:61], v[146:149], v[222:225], v[58:61]
	v_mfma_f32_16x16x32_bf16 v[54:57], v[150:153], v[222:225], v[54:57]
	v_mfma_f32_16x16x32_bf16 v[50:53], v[154:157], v[222:225], v[50:53]
	v_lshl_add_u64 v[166:167], v[132:133], 0, s[34:35]
	global_load_dwordx2 v[206:207], v[166:167], off
	global_load_dwordx2 v[208:209], v[166:167], off offset:2048
	v_mfma_f32_16x16x32_bf16 v[46:49], v[142:145], v[226:229], v[46:49]
	v_mfma_f32_16x16x32_bf16 v[42:45], v[146:149], v[226:229], v[42:45]
	v_mfma_f32_16x16x32_bf16 v[38:41], v[150:153], v[226:229], v[38:41]
	v_mfma_f32_16x16x32_bf16 v[34:37], v[154:157], v[226:229], v[34:37]
	v_lshl_add_u64 v[166:167], v[132:133], 0, s[36:37]
	global_load_dwordx2 v[210:211], v[166:167], off
	global_load_dwordx2 v[212:213], v[166:167], off offset:2048
	v_mfma_f32_16x16x32_bf16 v[18:21], v[142:145], v[230:233], v[18:21]
	v_mfma_f32_16x16x32_bf16 v[22:25], v[146:149], v[230:233], v[22:25]
	v_mfma_f32_16x16x32_bf16 v[26:29], v[150:153], v[230:233], v[26:29]
	v_mfma_f32_16x16x32_bf16 v[30:33], v[154:157], v[230:233], v[30:33]
	v_lshl_add_u64 v[166:167], v[132:133], 0, s[38:39]
	global_load_dwordx2 v[214:215], v[166:167], off
	global_load_dwordx2 v[216:217], v[166:167], off offset:2048
	v_mfma_f32_16x16x32_bf16 v[2:5], v[142:145], v[234:237], v[2:5]
	v_mfma_f32_16x16x32_bf16 v[6:9], v[146:149], v[234:237], v[6:9]
	v_mfma_f32_16x16x32_bf16 v[10:13], v[150:153], v[234:237], v[10:13]
	v_mfma_f32_16x16x32_bf16 v[14:17], v[154:157], v[234:237], v[14:17]
	s_waitcnt vmcnt(21)
	s_waitcnt lgkmcnt(0)
	s_barrier
; #define MU_GLDS_A(buf, kt) do { _Pragma("unroll") for (int i = 0; i < NMU; ++i) \
;         __builtin_amdgcn_global_load_lds((const unsigned*)((const char*)A + aoff[i] + (size_t)(kt) * 128), (PG8_LAS unsigned*)(MU_SA(buf) + wid * 1024 + i * 8192), 16, 0, 0); } while (0)
; #define MU_B_ISSUE(sb, kt) do { const char* kb_ = Bb + (size_t)(kt) * (64 * (size_t)RB); _Pragma("unroll") for (int j = 0; j < 8; ++j) { const char* p_ = kb_ + (size_t)j * RB; \
;         asm volatile("global_load_dwordx2 %0, %1, off" : "=&v"(sb[j]) : "v"(p_) : "memory"); } } while (0)
; #define MU_B_WAIT(sb, N) asm volatile("s_waitcnt vmcnt(%8)" : "+v"(sb[0]), "+v"(sb[1]), "+v"(sb[2]), "+v"(sb[3]), "+v"(sb[4]), "+v"(sb[5]), "+v"(sb[6]), "+v"(sb[7]) : "n"(N) : "memory")
; #define MU_COMPUTE(buf) MU_COMPUTE_N(buf, NMU)
; template <int MODE>
; __device__ __forceinline__ void moe_unit(PG8_LAS unsigned char* lds, int e, int cb, int slot0  , int nv  , const bf16_t* A, const int* slot_tok,
;                                          const float* W0, const float* W1, bf16_t* OUT, const float* slot_rs  , const int* slot_dst) {
;     ...
;     f32x4 acc[NMU][4];
; #pragma unroll
;     for (int m = 0; m < NMU; ++m)
; #pragma unroll
;         for (int n = 0; n < 4; ++n) acc[m][n] = (f32x4){0.f, 0.f, 0.f, 0.f};
;     f32x2 s0[8], s1[8];
;     float g0[8];
;     MU_GLDS_A(0, 0); MU_B_ISSUE(s0, 0); MU_G_LOAD(g0, 0); MU_B_ISSUE(s1, 1);
;     MU_B_WAIT(s0, 8); MU_B_WRITE(s0, 0, g0); __builtin_amdgcn_sched_barrier(0); MU_B_ISSUE(s0, 2);
;     asm volatile("s_waitcnt vmcnt(16)" ::: "memory");
;     asm volatile("s_waitcnt lgkmcnt(0)" ::: "memory"); __builtin_amdgcn_s_barrier(); asm volatile("" ::: "memory");
; #pragma unroll 1
;     for (int t = 0; t < nt; t += 2) {
;         if (t + 2 < nt) MU_B_WAIT(s1, 8); else MU_B_WAIT(s1, 0);
;         MU_G_LOAD(g0, t + 1); MU_B_WRITE(s1, 1, g0); __builtin_amdgcn_sched_barrier(0); MU_GLDS_A(1, t + 1); __builtin_amdgcn_sched_barrier(0);
;         if (t + 3 < nt) { MU_B_ISSUE(s1, t + 3); }
;         MU_COMPUTE(0);
;         MU_END(t + 3 >= nt);
;         if (t + 2 < nt) { MU_B_WAIT(s0, 8); MU_G_LOAD(g0, t + 2); MU_B_WRITE(s0, 0, g0); __builtin_amdgcn_sched_barrier(0); MU_GLDS_A(0, t + 2); __builtin_amdgcn_sched_barrier(0); }
;         if (t + 4 < nt) { MU_B_ISSUE(s0, t + 4); }
;         MU_COMPUTE(1);
;         MU_END(t + 4 >= nt);
	s_mov_b32 s47, s42
	s_mov_b32 s42, s43
	s_mov_b32 s43, s44
	s_mov_b32 s44, s47
	v_mul_f32_e32 v98, s12, v98
	v_mul_f32_e32 v99, s12, v99
	v_mul_f32_e32 v100, s13, v100
	v_mul_f32_e32 v101, s13, v101
	v_mul_f32_e32 v102, s14, v102
	v_mul_f32_e32 v103, s14, v103
	v_mul_f32_e32 v104, s15, v104
	v_mul_f32_e32 v105, s15, v105
	v_mul_f32_e32 v106, s16, v106
	v_mul_f32_e32 v107, s16, v107
	v_mul_f32_e32 v108, s17, v108
	v_mul_f32_e32 v109, s17, v109
	v_mul_f32_e32 v110, s18, v110
	v_mul_f32_e32 v111, s18, v111
	v_mul_f32_e32 v112, s19, v112
	v_mul_f32_e32 v113, s19, v113
	v_cvt_pk_bf16_f32 v158, v98, v100
	v_cvt_pk_bf16_f32 v159, v102, v104
	v_cvt_pk_bf16_f32 v160, v106, v108
	v_cvt_pk_bf16_f32 v161, v110, v112
	v_cvt_pk_bf16_f32 v162, v99, v101
	v_cvt_pk_bf16_f32 v163, v103, v105
	v_cvt_pk_bf16_f32 v164, v107, v109
	v_cvt_pk_bf16_f32 v165, v111, v113
	ds_write_b128 v1, v[158:161] offset:0
	ds_write_b128 v1, v[162:165] offset:128
	v_add_u32_e32 v91, s42, v135
	v_add_u32_e32 v93, s42, v137
	ds_read_b128 v[238:241], v139 offset:19456
	ds_read_b128 v[242:245], v139 offset:21504
	ds_read_b128 v[246:249], v139 offset:23552
	ds_read_b128 v[250:253], v139 offset:25600
	ds_read_b128 v[218:221], v91 offset:0
	ds_read_b128 v[222:225], v91 offset:2048
	ds_read_b128 v[226:229], v91 offset:4096
	ds_read_b128 v[230:233], v91 offset:6144
	ds_read_b128 v[234:237], v91 offset:8192
	s_add_i32 s47, s44, s6
	s_add_u32 s30, s30, 0x80
	s_addc_u32 s31, s31, 0
	s_waitcnt lgkmcnt(0)
	v_mfma_f32_16x16x32_bf16 v[78:81], v[238:241], v[218:221], v[78:81]
	v_mfma_f32_16x16x32_bf16 v[74:77], v[242:245], v[218:221], v[74:77]
	v_mfma_f32_16x16x32_bf16 v[70:73], v[246:249], v[218:221], v[70:73]
	v_mfma_f32_16x16x32_bf16 v[66:69], v[250:253], v[218:221], v[66:69]
	ds_read_b128 v[218:221], v93 offset:0
	ds_read_b128 v[142:145], v141 offset:19456
	s_mov_b32 m0, s47
	s_nop 0
	global_load_lds_dwordx4 v86, s[30:31]
	v_mfma_f32_16x16x32_bf16 v[62:65], v[238:241], v[222:225], v[62:65]
	v_mfma_f32_16x16x32_bf16 v[58:61], v[242:245], v[222:225], v[58:61]
	v_mfma_f32_16x16x32_bf16 v[54:57], v[246:249], v[222:225], v[54:57]
	v_mfma_f32_16x16x32_bf16 v[50:53], v[250:253], v[222:225], v[50:53]
	ds_read_b128 v[222:225], v93 offset:2048
	ds_read_b128 v[146:149], v141 offset:21504
	s_add_i32 m0, s47, 0x2000
	s_nop 0
	global_load_lds_dwordx4 v134, s[30:31]
	v_mfma_f32_16x16x32_bf16 v[46:49], v[238:241], v[226:229], v[46:49]
	v_mfma_f32_16x16x32_bf16 v[42:45], v[242:245], v[226:229], v[42:45]
	v_mfma_f32_16x16x32_bf16 v[38:41], v[246:249], v[226:229], v[38:41]
	v_mfma_f32_16x16x32_bf16 v[34:37], v[250:253], v[226:229], v[34:37]
	ds_read_b128 v[226:229], v93 offset:4096
	ds_read_b128 v[150:153], v141 offset:23552
	s_add_i32 m0, s47, 0x4000
	s_nop 0
	global_load_lds_dwordx4 v136, s[30:31]
	v_mfma_f32_16x16x32_bf16 v[18:21], v[238:241], v[230:233], v[18:21]
	v_mfma_f32_16x16x32_bf16 v[22:25], v[242:245], v[230:233], v[22:25]
	v_mfma_f32_16x16x32_bf16 v[26:29], v[246:249], v[230:233], v[26:29]
	v_mfma_f32_16x16x32_bf16 v[30:33], v[250:253], v[230:233], v[30:33]
	ds_read_b128 v[230:233], v93 offset:6144
	ds_read_b128 v[154:157], v141 offset:25600
	s_add_i32 m0, s47, 0x6000
	s_nop 0
	global_load_lds_dwordx4 v138, s[30:31]
	v_mfma_f32_16x16x32_bf16 v[2:5], v[238:241], v[234:237], v[2:5]
	v_mfma_f32_16x16x32_bf16 v[6:9], v[242:245], v[234:237], v[6:9]
	v_mfma_f32_16x16x32_bf16 v[10:13], v[246:249], v[234:237], v[10:13]
	v_mfma_f32_16x16x32_bf16 v[14:17], v[250:253], v[234:237], v[14:17]
	ds_read_b128 v[234:237], v93 offset:8192
	s_add_i32 m0, s47, 0x8000
	s_nop 0
	global_load_lds_dwordx4 v140, s[30:31]
	s_waitcnt lgkmcnt(0)
	s_load_dwordx8 s[20:27], s[28:29], 0x0
	s_add_u32 s28, s28, 0x100
	s_addc_u32 s29, s29, 0
	v_mfma_f32_16x16x32_bf16 v[78:81], v[142:145], v[218:221], v[78:81]
	v_mfma_f32_16x16x32_bf16 v[74:77], v[146:149], v[218:221], v[74:77]
	v_mfma_f32_16x16x32_bf16 v[70:73], v[150:153], v[218:221], v[70:73]
	v_mfma_f32_16x16x32_bf16 v[66:69], v[154:157], v[218:221], v[66:69]
	v_lshl_add_u64 v[132:133], v[132:133], 0, s[40:41]
	global_load_dwordx2 v[98:99], v[132:133], off
	global_load_dwordx2 v[100:101], v[132:133], off offset:2048
	v_mfma_f32_16x16x32_bf16 v[62:65], v[142:145], v[222:225], v[62:65]
	v_mfma_f32_16x16x32_bf16 v[58:61], v[146:149], v[222:225], v[58:61]
	v_mfma_f32_16x16x32_bf16 v[54:57], v[150:153], v[222:225], v[54:57]
	v_mfma_f32_16x16x32_bf16 v[50:53], v[154:157], v[222:225], v[50:53]
	v_lshl_add_u64 v[166:167], v[132:133], 0, s[34:35]
	global_load_dwordx2 v[102:103], v[166:167], off
	global_load_dwordx2 v[104:105], v[166:167], off offset:2048
	v_mfma_f32_16x16x32_bf16 v[46:49], v[142:145], v[226:229], v[46:49]
	v_mfma_f32_16x16x32_bf16 v[42:45], v[146:149], v[226:229], v[42:45]
	v_mfma_f32_16x16x32_bf16 v[38:41], v[150:153], v[226:229], v[38:41]
	v_mfma_f32_16x16x32_bf16 v[34:37], v[154:157], v[226:229], v[34:37]
	v_lshl_add_u64 v[166:167], v[132:133], 0, s[36:37]
	global_load_dwordx2 v[106:107], v[166:167], off
	global_load_dwordx2 v[108:109], v[166:167], off offset:2048
	v_mfma_f32_16x16x32_bf16 v[18:21], v[142:145], v[230:233], v[18:21]
	v_mfma_f32_16x16x32_bf16 v[22:25], v[146:149], v[230:233], v[22:25]
	v_mfma_f32_16x16x32_bf16 v[26:29], v[150:153], v[230:233], v[26:29]
	v_mfma_f32_16x16x32_bf16 v[30:33], v[154:157], v[230:233], v[30:33]
	v_lshl_add_u64 v[166:167], v[132:133], 0, s[38:39]
	global_load_dwordx2 v[110:111], v[166:167], off
	global_load_dwordx2 v[112:113], v[166:167], off offset:2048
	v_mfma_f32_16x16x32_bf16 v[2:5], v[142:145], v[234:237], v[2:5]
	v_mfma_f32_16x16x32_bf16 v[6:9], v[146:149], v[234:237], v[6:9]
	v_mfma_f32_16x16x32_bf16 v[10:13], v[150:153], v[234:237], v[10:13]
	v_mfma_f32_16x16x32_bf16 v[14:17], v[154:157], v[234:237], v[14:17]
	s_waitcnt vmcnt(21)
	s_waitcnt lgkmcnt(0)
	s_barrier
	s_mov_b32 s47, s42
	s_mov_b32 s42, s43
	s_mov_b32 s43, s44
	s_mov_b32 s44, s47
	s_mov_b32 s46, 13

; __device__ __forceinline__ void moe_down_stream(PG8_LAS unsigned char* lds, int e, int cb0, int slot0, int nv, const bf16_t* HIDp, const float* Wd, bf16_t* Y, const float* slot_w, const int* slot_dst) {
;     constexpr int K = 512, NT = 8 * DCB, RB = 4096 * 4;
;     const int tid = threadIdx.x, wid = __builtin_amdgcn_readfirstlane(tid >> 6), lane = tid & 63, wr = wid >> 1, wc = wid & 1, fr = lane & 15, fq = lane >> 4;
;     unsigned aoff[5];
; #pragma unroll
;     for (int i = 0; i < 5; ++i) { const int R = 8 * (wid + 8 * i) + (lane >> 3), C = 8 * ((lane & 7) ^ ((R >> 1) & 7)); const int w4 = R / DRW; int r = 4 * (R - DRW * w4) + w4; r = r < nv ? r : r % nv;
;         aoff[i] = ((unsigned)(slot0 + r) * (unsigned)K + (unsigned)C) * 2u; }
;     const int c0_ = 2 * lane, R0 = 64 * (c0_ >> 6) + 16 * (2 * ((c0_ >> 5) & 1) + ((c0_ >> 2) & 1)) + 4 * ((c0_ >> 3) & 3) + (c0_ & 3);
;     const char* Bb = (const char*)(Wd + (size_t)e * K * 4096 + 128 * cb0 + 2 * lane) + (size_t)(8 * wid) * RB;
;     const unsigned bw0 = (unsigned)(R0 * 128 + ((wid ^ ((R0 >> 1) & 7)) * 16)), bw1 = bw0 + 128u;
;     const int nvw = (nv - wr + 3) >> 2, mcnt = nvw <= 0 ? 0 : (((nvw + 15) >> 4) > DNM ? DNM : ((nvw + 15) >> 4));
;     unsigned amask = 0u;
; #pragma unroll
;     for (int i = 0; i < 5; ++i) { const int grp = 4 * i + (wid >> 1), w4 = grp / DNM, mf = grp % DNM, nv4 = (nv - w4 + 3) >> 2, mc4 = nv4 <= 0 ? 0 : ((nv4 + 15) >> 4); if (mf < mc4) amask |= 1u << i; }
;     LAS int* ldst = (LAS int*)(lds + MD_TAB_OFF); LAS float* lw = (LAS float*)(ldst + DR);
;     PG8_LAS unsigned char* stg = lds + MD_STG_OFF + wid * 2048;
;     __syncthreads();
;     for (int r = tid; r < DR; r += 512) { const bool ok = r < nv; ldst[r] = ok ? slot_dst[slot0 + r] : -1; lw[r] = ok ? slot_w[slot0 + r] : 0.f; }
;     asm volatile("s_waitcnt vmcnt(0)" ::: "memory");
;     ...
;     f32x4 acc[DNM][4];
; #pragma unroll
;     for (int m = 0; m < DNM; ++m)
; #pragma unroll
;         for (int n = 0; n < 4; ++n) acc[m][n] = (f32x4){0.f, 0.f, 0.f, 0.f};
;     f32x2 s0[8], s1[8];
;     MD_GLDS_A(0, 0); MD_B_ISSUE(s0, 0); MD_B_ISSUE(s1, 1);
;     MD_B_WAIT(s0, 8); MD_B_WRITE(s0, 0); __builtin_amdgcn_sched_barrier(0); MD_B_ISSUE(s0, 2);
;     asm volatile("s_waitcnt vmcnt(16)" ::: "memory");
;     asm volatile("s_waitcnt lgkmcnt(0)" ::: "memory"); __builtin_amdgcn_s_barrier(); asm volatile("" ::: "memory");
.Lmd_used_4:
	v_bfe_u32 v180, v131, 1, 3
	v_xor_b32_e32 v180, v171, v180
	v_lshlrev_b32_e32 v180, 4, v180
	v_lshl_add_u32 v180, v170, 7, v180
	s_mul_i32 s57, s67, 0x2800
	v_add_u32_e32 v135, s57, v180
	v_xor_b32_e32 v137, 64, v135
	s_lshl_b32 s57, s10, 13
	s_add_i32 s57, s57, 0x1e000
	v_add_u32_e32 v139, s57, v180
	v_xor_b32_e32 v141, 64, v139
	v_lshrrev_b32_e32 v164, 4, v131
	v_lshlrev_b32_e32 v95, 5, v164
	v_bfe_u32 v164, v131, 1, 1
	v_lshl_or_b32 v95, v164, 4, v95
	v_bfe_u32 v164, v131, 2, 2
	v_lshl_or_b32 v95, v164, 2, v95
	v_and_b32_e32 v165, 1, v131
	v_lshl_or_b32 v95, v165, 1, v95
	v_lshl_or_b32 v164, v164, 1, v165
	v_xor_b32_e32 v164, s66, v164
	v_lshlrev_b32_e32 v95, 7, v95
	v_lshl_or_b32 v95, v164, 4, v95
	v_add_u32_e32 v95, 0x1e000, v95
	s_lshl_b32 s57, s67, 2
	v_lshl_add_u32 v82, v170, 4, s57
	v_add_u32_e32 v82, 0x27340, v82
	v_lshl_add_u32 v83, v130, 4, s57
	v_add_u32_e32 v83, 0x26e40, v83
	v_and_b32_e32 v164, 7, v170
	v_xor_b32_e32 v165, v171, v164
	v_lshlrev_b32_e32 v165, 4, v165
	v_lshl_or_b32 v84, v164, 7, v165
	v_lshrrev_b32_e32 v164, 3, v170
	v_lshl_or_b32 v84, v164, 13, v84
	v_and_b32_e32 v164, 7, v131
	v_xor_b32_e32 v165, v130, v164
	v_and_b32_e32 v165, 7, v165
	v_lshlrev_b32_e32 v165, 4, v165
	v_lshl_or_b32 v85, v130, 7, v165
	s_lshl_b32 s57, s14, 8
	s_lshl_b32 s58, s10, 7
	s_add_i32 s57, s57, s58
	s_add_u32 s58, s96, s57
	s_addc_u32 s59, s97, 0
	v_lshlrev_b32_e32 v164, 4, v164
	v_mov_b32_e32 v165, 0
	v_lshl_add_u64 v[86:87], v[164:165], 0, s[58:59]
	v_readlane_b32 s58, v254, 25
	v_readlane_b32 s59, v254, 26
	s_lshl_b64 s[60:61], s[6:7], 23
	s_add_u32 s58, s58, s60
	s_addc_u32 s59, s59, s61
	s_lshl_b32 s60, s14, 9
	s_add_u32 s58, s58, s60
	s_addc_u32 s59, s59, 0
	s_lshl_b32 s60, s66, 17
	s_add_u32 s58, s58, s60
	s_addc_u32 s59, s59, 0
	v_lshlrev_b32_e32 v164, 3, v131
	v_mov_b32_e32 v165, 0
	v_lshl_add_u64 v[132:133], v[164:165], 0, s[58:59]
	s_mov_b64 s[24:25], 0x4000
	s_mov_b64 s[26:27], 0x8000
	s_mov_b64 s[28:29], 0xc000
	s_mov_b64 s[36:37], 0x10000
	s_mov_b64 s[38:39], 0x14000
	s_mov_b64 s[40:41], 0x18000
	s_mov_b64 s[42:43], 0x1c000
	s_mov_b32 s34, 0xff901000
	s_mov_b32 s35, 0x100000
	s_mov_b32 s53, 0xfffffc80
	s_mov_b32 s32, 0x80
	v_readlane_b32 s58, v254, 31
	v_readlane_b32 s59, v254, 32
	s_add_u32 s58, s58, 0x4b000000
	s_addc_u32 s59, s59, 0
	v_lshlrev_b32_e32 v164, 4, v131
	v_mov_b32_e32 v165, 0
	v_lshl_add_u64 v[168:169], v[164:165], 0, s[58:59]
	s_mov_b64 s[30:31], s[16:17]
	s_mov_b32 s46, 0
	s_mov_b32 s47, 0xa000
	s_mov_b32 s48, 0x14000
	s_mov_b32 s51, 4
	s_mov_b32 s50, 0
	s_mov_b32 s52, 1
	s_add_i32 m0, s74, 0x0
	s_nop 0
	global_load_lds_dwordx4 v88, s[30:31]
	s_add_i32 m0, s74, 0x2000
	s_nop 0
	global_load_lds_dwordx4 v90, s[30:31]
	s_add_i32 m0, s74, 0x4000
	s_nop 0
	global_load_lds_dwordx4 v92, s[30:31]
	s_add_i32 m0, s74, 0x6000
	s_nop 0
	global_load_lds_dwordx4 v94, s[30:31]
	s_add_i32 m0, s74, 0x8000
	s_nop 0
	global_load_lds_dwordx4 v96, s[30:31]
	s_add_u32 s30, s30, 0x80
	s_addc_u32 s31, s31, 0
	s_add_i32 m0, s74, 0xa000
	s_nop 0
	global_load_lds_dwordx4 v88, s[30:31]
	s_add_i32 m0, s74, 0xc000
	s_nop 0
	global_load_lds_dwordx4 v90, s[30:31]
	s_add_i32 m0, s74, 0xe000
	s_nop 0
	global_load_lds_dwordx4 v92, s[30:31]
	s_add_i32 m0, s74, 0x10000
	s_nop 0
	global_load_lds_dwordx4 v94, s[30:31]
	s_add_i32 m0, s74, 0x12000
	s_nop 0
	global_load_lds_dwordx4 v96, s[30:31]
	s_mov_b32 s44, 0x100000
	s_mov_b32 s45, 0
	global_load_dwordx2 v[98:99], v[132:133], off
	v_lshl_add_u64 v[180:181], v[132:133], 0, s[24:25]
	global_load_dwordx2 v[100:101], v[180:181], off
	v_lshl_add_u64 v[180:181], v[132:133], 0, s[26:27]
	global_load_dwordx2 v[102:103], v[180:181], off
	v_lshl_add_u64 v[180:181], v[132:133], 0, s[28:29]
	global_load_dwordx2 v[104:105], v[180:181], off
	v_lshl_add_u64 v[180:181], v[132:133], 0, s[36:37]
	global_load_dwordx2 v[106:107], v[180:181], off
	v_lshl_add_u64 v[180:181], v[132:133], 0, s[38:39]
	global_load_dwordx2 v[108:109], v[180:181], off
	v_lshl_add_u64 v[180:181], v[132:133], 0, s[40:41]
	global_load_dwordx2 v[110:111], v[180:181], off
	v_lshl_add_u64 v[180:181], v[132:133], 0, s[42:43]
	global_load_dwordx2 v[112:113], v[180:181], off
	v_lshl_add_u64 v[132:133], v[132:133], 0, s[44:45]
	global_load_dwordx2 v[114:115], v[132:133], off
	v_lshl_add_u64 v[180:181], v[132:133], 0, s[24:25]
	global_load_dwordx2 v[116:117], v[180:181], off
	v_lshl_add_u64 v[180:181], v[132:133], 0, s[26:27]
	global_load_dwordx2 v[118:119], v[180:181], off
	v_lshl_add_u64 v[180:181], v[132:133], 0, s[28:29]
	global_load_dwordx2 v[120:121], v[180:181], off
	v_lshl_add_u64 v[180:181], v[132:133], 0, s[36:37]
	global_load_dwordx2 v[122:123], v[180:181], off
	v_lshl_add_u64 v[180:181], v[132:133], 0, s[38:39]
	global_load_dwordx2 v[124:125], v[180:181], off
	v_lshl_add_u64 v[180:181], v[132:133], 0, s[40:41]
	global_load_dwordx2 v[126:127], v[180:181], off
	v_lshl_add_u64 v[180:181], v[132:133], 0, s[42:43]
	global_load_dwordx2 v[128:129], v[180:181], off
	v_lshl_add_u64 v[132:133], v[132:133], 0, s[44:45]
	global_load_dwordx2 v[186:187], v[132:133], off
	v_lshl_add_u64 v[180:181], v[132:133], 0, s[24:25]
	global_load_dwordx2 v[188:189], v[180:181], off
	v_lshl_add_u64 v[180:181], v[132:133], 0, s[26:27]
	global_load_dwordx2 v[190:191], v[180:181], off
	v_lshl_add_u64 v[180:181], v[132:133], 0, s[28:29]
	global_load_dwordx2 v[192:193], v[180:181], off
	v_lshl_add_u64 v[180:181], v[132:133], 0, s[36:37]
	global_load_dwordx2 v[194:195], v[180:181], off
	v_lshl_add_u64 v[180:181], v[132:133], 0, s[38:39]
	global_load_dwordx2 v[196:197], v[180:181], off
	v_lshl_add_u64 v[180:181], v[132:133], 0, s[40:41]
; #define MD_GLDS_A(buf, tau) do { _Pragma("unroll") for (int i = 0; i < 5; ++i) if (amask & (1u << i)) \
;         __builtin_amdgcn_global_load_lds((const unsigned*)((const char*)HIDp + aoff[i] + (size_t)((tau) & 7) * 128), (PG8_LAS unsigned*)(MD_SA(buf) + wid * 1024 + i * 8192), 16, 0, 0); } while (0)
; #define MD_B_ISSUE(sb, tau) do { const char* kb_ = Bb + (size_t)((tau) >> 3) * 512 + (size_t)((tau) & 7) * (64 * (size_t)RB); _Pragma("unroll") for (int j = 0; j < 8; ++j) { const char* p_ = kb_ + (size_t)j * RB; \
;         asm volatile("global_load_dwordx2 %0, %1, off" : "=&v"(sb[j]) : "v"(p_) : "memory"); } } while (0)
; #define MD_B_WAIT(sb, N) asm volatile("s_waitcnt vmcnt(%8)" : "+v"(sb[0]), "+v"(sb[1]), "+v"(sb[2]), "+v"(sb[3]), "+v"(sb[4]), "+v"(sb[5]), "+v"(sb[6]), "+v"(sb[7]) : "n"(N) : "memory")
; __device__ __forceinline__ void moe_down_stream(PG8_LAS unsigned char* lds, int e, int cb0, int slot0, int nv, const bf16_t* HIDp, const float* Wd, bf16_t* Y, const float* slot_w, const int* slot_dst) {
;     ...
;     f32x4 acc[DNM][4];
; #pragma unroll
;     for (int m = 0; m < DNM; ++m)
; #pragma unroll
;         for (int n = 0; n < 4; ++n) acc[m][n] = (f32x4){0.f, 0.f, 0.f, 0.f};
;     f32x2 s0[8], s1[8];
;     MD_GLDS_A(0, 0); MD_B_ISSUE(s0, 0); MD_B_ISSUE(s1, 1);
;     MD_B_WAIT(s0, 8); MD_B_WRITE(s0, 0); __builtin_amdgcn_sched_barrier(0); MD_B_ISSUE(s0, 2);
;     asm volatile("s_waitcnt vmcnt(16)" ::: "memory");
;     asm volatile("s_waitcnt lgkmcnt(0)" ::: "memory"); __builtin_amdgcn_s_barrier(); asm volatile("" ::: "memory");
; #pragma unroll 1
;     for (int t = 0; t < NT; t += 2) {
;         if (t + 2 < NT) MD_B_WAIT(s1, 8); else MD_B_WAIT(s1, 0);
;         MD_B_WRITE(s1, 1); __builtin_amdgcn_sched_barrier(0); MD_GLDS_A(1, t + 1); __builtin_amdgcn_sched_barrier(0);
;         if (t + 3 < NT) MD_B_ISSUE(s1, t + 3);
;         MD_COMPUTE(0);
	global_load_dwordx2 v[198:199], v[180:181], off
	v_lshl_add_u64 v[180:181], v[132:133], 0, s[42:43]
	global_load_dwordx2 v[200:201], v[180:181], off
	v_lshl_add_u64 v[132:133], v[132:133], 0, s[44:45]
	global_load_dwordx2 v[202:203], v[132:133], off
	v_lshl_add_u64 v[180:181], v[132:133], 0, s[24:25]
	global_load_dwordx2 v[204:205], v[180:181], off
	v_lshl_add_u64 v[180:181], v[132:133], 0, s[26:27]
	global_load_dwordx2 v[206:207], v[180:181], off
	v_lshl_add_u64 v[180:181], v[132:133], 0, s[28:29]
	global_load_dwordx2 v[208:209], v[180:181], off
	v_lshl_add_u64 v[180:181], v[132:133], 0, s[36:37]
	global_load_dwordx2 v[210:211], v[180:181], off
	v_lshl_add_u64 v[180:181], v[132:133], 0, s[38:39]
	global_load_dwordx2 v[212:213], v[180:181], off
	v_lshl_add_u64 v[180:181], v[132:133], 0, s[40:41]
	global_load_dwordx2 v[214:215], v[180:181], off
	v_lshl_add_u64 v[180:181], v[132:133], 0, s[42:43]
	global_load_dwordx2 v[216:217], v[180:181], off
	v_mov_b32_e32 v78, 0
	v_mov_b32_e32 v79, 0
	v_mov_b32_e32 v80, 0
	v_mov_b32_e32 v81, 0
	v_mov_b32_e32 v74, 0
	v_mov_b32_e32 v75, 0
	v_mov_b32_e32 v76, 0
	v_mov_b32_e32 v77, 0
	v_mov_b32_e32 v70, 0
	v_mov_b32_e32 v71, 0
	v_mov_b32_e32 v72, 0
	v_mov_b32_e32 v73, 0
	v_mov_b32_e32 v66, 0
	v_mov_b32_e32 v67, 0
	v_mov_b32_e32 v68, 0
	v_mov_b32_e32 v69, 0
	v_mov_b32_e32 v62, 0
	v_mov_b32_e32 v63, 0
	v_mov_b32_e32 v64, 0
	v_mov_b32_e32 v65, 0
	v_mov_b32_e32 v58, 0
	v_mov_b32_e32 v59, 0
	v_mov_b32_e32 v60, 0
	v_mov_b32_e32 v61, 0
	v_mov_b32_e32 v54, 0
	v_mov_b32_e32 v55, 0
	v_mov_b32_e32 v56, 0
	v_mov_b32_e32 v57, 0
	v_mov_b32_e32 v50, 0
	v_mov_b32_e32 v51, 0
	v_mov_b32_e32 v52, 0
	v_mov_b32_e32 v53, 0
	v_mov_b32_e32 v46, 0
	v_mov_b32_e32 v47, 0
	v_mov_b32_e32 v48, 0
	v_mov_b32_e32 v49, 0
	v_mov_b32_e32 v42, 0
	v_mov_b32_e32 v43, 0
	v_mov_b32_e32 v44, 0
	v_mov_b32_e32 v45, 0
	v_mov_b32_e32 v38, 0
	v_mov_b32_e32 v39, 0
	v_mov_b32_e32 v40, 0
	v_mov_b32_e32 v41, 0
	v_mov_b32_e32 v34, 0
	v_mov_b32_e32 v35, 0
	v_mov_b32_e32 v36, 0
	v_mov_b32_e32 v37, 0
	v_mov_b32_e32 v18, 0
	v_mov_b32_e32 v19, 0
	v_mov_b32_e32 v20, 0
	v_mov_b32_e32 v21, 0
	v_mov_b32_e32 v22, 0
	v_mov_b32_e32 v23, 0
	v_mov_b32_e32 v24, 0
	v_mov_b32_e32 v25, 0
	v_mov_b32_e32 v26, 0
	v_mov_b32_e32 v27, 0
	v_mov_b32_e32 v28, 0
	v_mov_b32_e32 v29, 0
	v_mov_b32_e32 v30, 0
	v_mov_b32_e32 v31, 0
	v_mov_b32_e32 v32, 0
	v_mov_b32_e32 v33, 0
	v_mov_b32_e32 v2, 0
	v_mov_b32_e32 v3, 0
	v_mov_b32_e32 v4, 0
	v_mov_b32_e32 v5, 0
	v_mov_b32_e32 v6, 0
	v_mov_b32_e32 v7, 0
	v_mov_b32_e32 v8, 0
	v_mov_b32_e32 v9, 0
	v_mov_b32_e32 v10, 0
	v_mov_b32_e32 v11, 0
	v_mov_b32_e32 v12, 0
	v_mov_b32_e32 v13, 0
	v_mov_b32_e32 v14, 0
	v_mov_b32_e32 v15, 0
	v_mov_b32_e32 v16, 0
	v_mov_b32_e32 v17, 0
	s_waitcnt vmcnt(24)
	v_cvt_pk_bf16_f32 v172, v98, v100
	v_cvt_pk_bf16_f32 v173, v102, v104
	v_cvt_pk_bf16_f32 v174, v106, v108
	v_cvt_pk_bf16_f32 v175, v110, v112
	v_cvt_pk_bf16_f32 v176, v99, v101
	v_cvt_pk_bf16_f32 v177, v103, v105
	v_cvt_pk_bf16_f32 v178, v107, v109
	v_cvt_pk_bf16_f32 v179, v111, v113
	ds_write_b128 v95, v[172:175] offset:0
	ds_write_b128 v95, v[176:179] offset:128
	v_lshl_add_u64 v[132:133], v[132:133], 0, s[44:45]
	global_load_dwordx2 v[98:99], v[132:133], off
	v_lshl_add_u64 v[180:181], v[132:133], 0, s[24:25]
	global_load_dwordx2 v[100:101], v[180:181], off
	v_lshl_add_u64 v[180:181], v[132:133], 0, s[26:27]
	global_load_dwordx2 v[102:103], v[180:181], off
	v_lshl_add_u64 v[180:181], v[132:133], 0, s[28:29]
	global_load_dwordx2 v[104:105], v[180:181], off
	v_lshl_add_u64 v[180:181], v[132:133], 0, s[36:37]
	global_load_dwordx2 v[106:107], v[180:181], off
	v_lshl_add_u64 v[180:181], v[132:133], 0, s[38:39]
	global_load_dwordx2 v[108:109], v[180:181], off
	v_lshl_add_u64 v[180:181], v[132:133], 0, s[40:41]
	global_load_dwordx2 v[110:111], v[180:181], off
	v_lshl_add_u64 v[180:181], v[132:133], 0, s[42:43]
	global_load_dwordx2 v[112:113], v[180:181], off
	s_waitcnt lgkmcnt(0)
	s_barrier
	s_cmp_gt_u32 s66, 3
	s_cbranch_scc1 .Lmd_grpY
	s_waitcnt vmcnt(24)
	v_cvt_pk_bf16_f32 v172, v114, v116
	v_cvt_pk_bf16_f32 v173, v118, v120
	v_cvt_pk_bf16_f32 v174, v122, v124
	v_cvt_pk_bf16_f32 v175, v126, v128
	v_cvt_pk_bf16_f32 v176, v115, v117
	v_cvt_pk_bf16_f32 v177, v119, v121
	v_cvt_pk_bf16_f32 v178, v123, v125
	v_cvt_pk_bf16_f32 v179, v127, v129
	ds_write_b128 v95, v[172:175] offset:19456
	ds_write_b128 v95, v[176:179] offset:19584
	v_add_u32_e32 v91, s46, v135
	v_add_u32_e32 v93, s46, v137
	ds_read_b128 v[238:241], v139 offset:0
	ds_read_b128 v[242:245], v139 offset:2048
	ds_read_b128 v[246:249], v139 offset:4096
	ds_read_b128 v[250:253], v139 offset:6144
	ds_read_b128 v[218:221], v91 offset:0
	ds_read_b128 v[222:225], v91 offset:2048
	ds_read_b128 v[226:229], v91 offset:4096
	ds_read_b128 v[230:233], v91 offset:6144
	ds_read_b128 v[234:237], v91 offset:8192
	s_add_i32 s49, s48, s74
	s_add_i32 s52, s52, 1
	s_and_b32 s54, s52, 7
	s_cmp_eq_u32 s54, 0
	s_cselect_b32 s54, s53, s32
	s_cselect_b32 s55, -1, 0
	s_add_u32 s30, s30, s54
	s_addc_u32 s31, s31, s55
	s_waitcnt lgkmcnt(0)
	v_mfma_f32_16x16x32_bf16 v[78:81], v[238:241], v[218:221], v[78:81]
	v_mfma_f32_16x16x32_bf16 v[74:77], v[242:245], v[218:221], v[74:77]
	v_mfma_f32_16x16x32_bf16 v[70:73], v[246:249], v[218:221], v[70:73]
	v_mfma_f32_16x16x32_bf16 v[66:69], v[250:253], v[218:221], v[66:69]
	ds_read_b128 v[218:221], v93 offset:0
	ds_read_b128 v[142:145], v141 offset:0
	s_mov_b32 m0, s49
	s_nop 0
	global_load_lds_dwordx4 v88, s[30:31]
	v_mfma_f32_16x16x32_bf16 v[62:65], v[238:241], v[222:225], v[62:65]
	v_mfma_f32_16x16x32_bf16 v[58:61], v[242:245], v[222:225], v[58:61]
	v_mfma_f32_16x16x32_bf16 v[54:57], v[246:249], v[222:225], v[54:57]
	v_mfma_f32_16x16x32_bf16 v[50:53], v[250:253], v[222:225], v[50:53]
	ds_read_b128 v[222:225], v93 offset:2048
	ds_read_b128 v[146:149], v141 offset:2048
	s_add_i32 m0, s49, 0x2000
	s_nop 0
	global_load_lds_dwordx4 v90, s[30:31]
	v_mfma_f32_16x16x32_bf16 v[46:49], v[238:241], v[226:229], v[46:49]
	v_mfma_f32_16x16x32_bf16 v[42:45], v[242:245], v[226:229], v[42:45]
	v_mfma_f32_16x16x32_bf16 v[38:41], v[246:249], v[226:229], v[38:41]
	v_mfma_f32_16x16x32_bf16 v[34:37], v[250:253], v[226:229], v[34:37]
	ds_read_b128 v[226:229], v93 offset:4096
	ds_read_b128 v[156:159], v141 offset:4096
	s_add_i32 m0, s49, 0x4000
	s_nop 0
	global_load_lds_dwordx4 v92, s[30:31]
	v_mfma_f32_16x16x32_bf16 v[18:21], v[238:241], v[230:233], v[18:21]
	v_mfma_f32_16x16x32_bf16 v[22:25], v[242:245], v[230:233], v[22:25]
	v_mfma_f32_16x16x32_bf16 v[26:29], v[246:249], v[230:233], v[26:29]
	v_mfma_f32_16x16x32_bf16 v[30:33], v[250:253], v[230:233], v[30:33]
	ds_read_b128 v[230:233], v93 offset:6144
	ds_read_b128 v[160:163], v141 offset:6144
	s_add_i32 m0, s49, 0x6000
	s_nop 0
	global_load_lds_dwordx4 v94, s[30:31]
	v_mfma_f32_16x16x32_bf16 v[2:5], v[238:241], v[234:237], v[2:5]
	v_mfma_f32_16x16x32_bf16 v[6:9], v[242:245], v[234:237], v[6:9]
	v_mfma_f32_16x16x32_bf16 v[10:13], v[246:249], v[234:237], v[10:13]
	v_mfma_f32_16x16x32_bf16 v[14:17], v[250:253], v[234:237], v[14:17]
	ds_read_b128 v[234:237], v93 offset:8192
	s_add_i32 m0, s49, 0x8000
	s_nop 0
	global_load_lds_dwordx4 v96, s[30:31]
	s_waitcnt lgkmcnt(0)
	v_mfma_f32_16x16x32_bf16 v[78:81], v[142:145], v[218:221], v[78:81]
	v_mfma_f32_16x16x32_bf16 v[74:77], v[146:149], v[218:221], v[74:77]
	v_mfma_f32_16x16x32_bf16 v[70:73], v[156:159], v[218:221], v[70:73]
	v_mfma_f32_16x16x32_bf16 v[66:69], v[160:163], v[218:221], v[66:69]
	s_add_i32 s51, s51, 1
	s_and_b32 s54, s51, 7
	s_cmp_eq_u32 s54, 0
	s_cselect_b32 s44, s34, s35
	s_cselect_b32 s45, -1, 0
	v_lshl_add_u64 v[132:133], v[132:133], 0, s[44:45]
	global_load_dwordx2 v[114:115], v[132:133], off
	v_lshl_add_u64 v[180:181], v[132:133], 0, s[24:25]
	global_load_dwordx2 v[116:117], v[180:181], off
	v_mfma_f32_16x16x32_bf16 v[62:65], v[142:145], v[222:225], v[62:65]
	v_mfma_f32_16x16x32_bf16 v[58:61], v[146:149], v[222:225], v[58:61]
	v_mfma_f32_16x16x32_bf16 v[54:57], v[156:159], v[222:225], v[54:57]
	v_mfma_f32_16x16x32_bf16 v[50:53], v[160:163], v[222:225], v[50:53]
	v_lshl_add_u64 v[180:181], v[132:133], 0, s[26:27]
	global_load_dwordx2 v[118:119], v[180:181], off
	v_lshl_add_u64 v[180:181], v[132:133], 0, s[28:29]
	global_load_dwordx2 v[120:121], v[180:181], off
	v_mfma_f32_16x16x32_bf16 v[46:49], v[142:145], v[226:229], v[46:49]
	v_mfma_f32_16x16x32_bf16 v[42:45], v[146:149], v[226:229], v[42:45]
	v_mfma_f32_16x16x32_bf16 v[38:41], v[156:159], v[226:229], v[38:41]
	v_mfma_f32_16x16x32_bf16 v[34:37], v[160:163], v[226:229], v[34:37]
	v_lshl_add_u64 v[180:181], v[132:133], 0, s[36:37]
	global_load_dwordx2 v[122:123], v[180:181], off
	v_lshl_add_u64 v[180:181], v[132:133], 0, s[38:39]
	global_load_dwordx2 v[124:125], v[180:181], off
	v_mfma_f32_16x16x32_bf16 v[18:21], v[142:145], v[230:233], v[18:21]
	v_mfma_f32_16x16x32_bf16 v[22:25], v[146:149], v[230:233], v[22:25]
	v_mfma_f32_16x16x32_bf16 v[26:29], v[156:159], v[230:233], v[26:29]
	v_mfma_f32_16x16x32_bf16 v[30:33], v[160:163], v[230:233], v[30:33]
	v_lshl_add_u64 v[180:181], v[132:133], 0, s[40:41]
	global_load_dwordx2 v[126:127], v[180:181], off
	v_lshl_add_u64 v[180:181], v[132:133], 0, s[42:43]
	global_load_dwordx2 v[128:129], v[180:181], off
	v_mfma_f32_16x16x32_bf16 v[2:5], v[142:145], v[234:237], v[2:5]
	v_mfma_f32_16x16x32_bf16 v[6:9], v[146:149], v[234:237], v[6:9]
	v_mfma_f32_16x16x32_bf16 v[10:13], v[156:159], v[234:237], v[10:13]
	v_mfma_f32_16x16x32_bf16 v[14:17], v[160:163], v[234:237], v[14:17]
	s_waitcnt lgkmcnt(0)
	s_barrier
; #define MD_GLDS_A(buf, tau) do { _Pragma("unroll") for (int i = 0; i < 5; ++i) if (amask & (1u << i)) \
;         __builtin_amdgcn_global_load_lds((const unsigned*)((const char*)HIDp + aoff[i] + (size_t)((tau) & 7) * 128), (PG8_LAS unsigned*)(MD_SA(buf) + wid * 1024 + i * 8192), 16, 0, 0); } while (0)
; #define MD_B_ISSUE(sb, tau) do { const char* kb_ = Bb + (size_t)((tau) >> 3) * 512 + (size_t)((tau) & 7) * (64 * (size_t)RB); _Pragma("unroll") for (int j = 0; j < 8; ++j) { const char* p_ = kb_ + (size_t)j * RB; \
;         asm volatile("global_load_dwordx2 %0, %1, off" : "=&v"(sb[j]) : "v"(p_) : "memory"); } } while (0)
; #define MD_B_WAIT(sb, N) asm volatile("s_waitcnt vmcnt(%8)" : "+v"(sb[0]), "+v"(sb[1]), "+v"(sb[2]), "+v"(sb[3]), "+v"(sb[4]), "+v"(sb[5]), "+v"(sb[6]), "+v"(sb[7]) : "n"(N) : "memory")
; __device__ __forceinline__ void moe_down_stream(PG8_LAS unsigned char* lds, int e, int cb0, int slot0, int nv, const bf16_t* HIDp, const float* Wd, bf16_t* Y, const float* slot_w, const int* slot_dst) {
;     ...
;     f32x4 acc[DNM][4];
; #pragma unroll
;     for (int m = 0; m < DNM; ++m)
; #pragma unroll
;         for (int n = 0; n < 4; ++n) acc[m][n] = (f32x4){0.f, 0.f, 0.f, 0.f};
;     f32x2 s0[8], s1[8];
;     MD_GLDS_A(0, 0); MD_B_ISSUE(s0, 0); MD_B_ISSUE(s1, 1);
;     MD_B_WAIT(s0, 8); MD_B_WRITE(s0, 0); __builtin_amdgcn_sched_barrier(0); MD_B_ISSUE(s0, 2);
;     asm volatile("s_waitcnt vmcnt(16)" ::: "memory");
;     asm volatile("s_waitcnt lgkmcnt(0)" ::: "memory"); __builtin_amdgcn_s_barrier(); asm volatile("" ::: "memory");
; #pragma unroll 1
;     for (int t = 0; t < NT; t += 2) {
;         if (t + 2 < NT) MD_B_WAIT(s1, 8); else MD_B_WAIT(s1, 0);
;         MD_B_WRITE(s1, 1); __builtin_amdgcn_sched_barrier(0); MD_GLDS_A(1, t + 1); __builtin_amdgcn_sched_barrier(0);
;         if (t + 3 < NT) MD_B_ISSUE(s1, t + 3);
;         MD_COMPUTE(0);
;         MD_END(t + 3 >= NT);
;         if (t + 2 < NT) { MD_B_WAIT(s0, 8); MD_B_WRITE(s0, 0); __builtin_amdgcn_sched_barrier(0); MD_GLDS_A(0, t + 2); __builtin_amdgcn_sched_barrier(0); }
;         if (t + 4 < NT) MD_B_ISSUE(s0, t + 4);
;         MD_COMPUTE(1);
;         MD_END(t + 4 >= NT);
	s_mov_b32 s49, s46
	s_mov_b32 s46, s47
	s_mov_b32 s47, s48
	s_mov_b32 s48, s49
	s_add_i32 s50, s50, 1
	s_waitcnt vmcnt(29)
	v_cvt_pk_bf16_f32 v172, v186, v188
	v_cvt_pk_bf16_f32 v173, v190, v192
	v_cvt_pk_bf16_f32 v174, v194, v196
	v_cvt_pk_bf16_f32 v175, v198, v200
	v_cvt_pk_bf16_f32 v176, v187, v189
	v_cvt_pk_bf16_f32 v177, v191, v193
	v_cvt_pk_bf16_f32 v178, v195, v197
	v_cvt_pk_bf16_f32 v179, v199, v201
	ds_write_b128 v95, v[172:175] offset:0
	ds_write_b128 v95, v[176:179] offset:128
	v_add_u32_e32 v91, s46, v135
	v_add_u32_e32 v93, s46, v137
	ds_read_b128 v[238:241], v139 offset:19456
	ds_read_b128 v[242:245], v139 offset:21504
	ds_read_b128 v[246:249], v139 offset:23552
	ds_read_b128 v[250:253], v139 offset:25600
	ds_read_b128 v[218:221], v91 offset:0
	ds_read_b128 v[222:225], v91 offset:2048
	ds_read_b128 v[226:229], v91 offset:4096
	ds_read_b128 v[230:233], v91 offset:6144
	ds_read_b128 v[234:237], v91 offset:8192
	s_add_i32 s49, s48, s74
	s_add_i32 s52, s52, 1
	s_and_b32 s54, s52, 7
	s_cmp_eq_u32 s54, 0
	s_cselect_b32 s54, s53, s32
	s_cselect_b32 s55, -1, 0
	s_add_u32 s30, s30, s54
	s_addc_u32 s31, s31, s55
	s_waitcnt lgkmcnt(0)
	v_mfma_f32_16x16x32_bf16 v[78:81], v[238:241], v[218:221], v[78:81]
	v_mfma_f32_16x16x32_bf16 v[74:77], v[242:245], v[218:221], v[74:77]
	v_mfma_f32_16x16x32_bf16 v[70:73], v[246:249], v[218:221], v[70:73]
	v_mfma_f32_16x16x32_bf16 v[66:69], v[250:253], v[218:221], v[66:69]
	ds_read_b128 v[218:221], v93 offset:0
	ds_read_b128 v[142:145], v141 offset:19456
	s_mov_b32 m0, s49
	s_nop 0
	global_load_lds_dwordx4 v88, s[30:31]
	v_mfma_f32_16x16x32_bf16 v[62:65], v[238:241], v[222:225], v[62:65]
	v_mfma_f32_16x16x32_bf16 v[58:61], v[242:245], v[222:225], v[58:61]
	v_mfma_f32_16x16x32_bf16 v[54:57], v[246:249], v[222:225], v[54:57]
	v_mfma_f32_16x16x32_bf16 v[50:53], v[250:253], v[222:225], v[50:53]
	ds_read_b128 v[222:225], v93 offset:2048
	ds_read_b128 v[146:149], v141 offset:21504
	s_add_i32 m0, s49, 0x2000
	s_nop 0
	global_load_lds_dwordx4 v90, s[30:31]
	v_mfma_f32_16x16x32_bf16 v[46:49], v[238:241], v[226:229], v[46:49]
	v_mfma_f32_16x16x32_bf16 v[42:45], v[242:245], v[226:229], v[42:45]
	v_mfma_f32_16x16x32_bf16 v[38:41], v[246:249], v[226:229], v[38:41]
	v_mfma_f32_16x16x32_bf16 v[34:37], v[250:253], v[226:229], v[34:37]
	ds_read_b128 v[226:229], v93 offset:4096
	ds_read_b128 v[156:159], v141 offset:23552
	s_add_i32 m0, s49, 0x4000
	s_nop 0
	global_load_lds_dwordx4 v92, s[30:31]
	v_mfma_f32_16x16x32_bf16 v[18:21], v[238:241], v[230:233], v[18:21]
	v_mfma_f32_16x16x32_bf16 v[22:25], v[242:245], v[230:233], v[22:25]
	v_mfma_f32_16x16x32_bf16 v[26:29], v[246:249], v[230:233], v[26:29]
	v_mfma_f32_16x16x32_bf16 v[30:33], v[250:253], v[230:233], v[30:33]
	ds_read_b128 v[230:233], v93 offset:6144
	ds_read_b128 v[160:163], v141 offset:25600
	s_add_i32 m0, s49, 0x6000
	s_nop 0
	global_load_lds_dwordx4 v94, s[30:31]
	v_mfma_f32_16x16x32_bf16 v[2:5], v[238:241], v[234:237], v[2:5]
	v_mfma_f32_16x16x32_bf16 v[6:9], v[242:245], v[234:237], v[6:9]
	v_mfma_f32_16x16x32_bf16 v[10:13], v[246:249], v[234:237], v[10:13]
	v_mfma_f32_16x16x32_bf16 v[14:17], v[250:253], v[234:237], v[14:17]
	ds_read_b128 v[234:237], v93 offset:8192
	s_add_i32 m0, s49, 0x8000
	s_nop 0
	global_load_lds_dwordx4 v96, s[30:31]
	s_waitcnt lgkmcnt(0)
	v_mfma_f32_16x16x32_bf16 v[78:81], v[142:145], v[218:221], v[78:81]
	v_mfma_f32_16x16x32_bf16 v[74:77], v[146:149], v[218:221], v[74:77]
	v_mfma_f32_16x16x32_bf16 v[70:73], v[156:159], v[218:221], v[70:73]
	v_mfma_f32_16x16x32_bf16 v[66:69], v[160:163], v[218:221], v[66:69]
	s_add_i32 s51, s51, 1
	s_and_b32 s54, s51, 7
	s_cmp_eq_u32 s54, 0
	s_cselect_b32 s44, s34, s35
	s_cselect_b32 s45, -1, 0
	v_lshl_add_u64 v[132:133], v[132:133], 0, s[44:45]
	global_load_dwordx2 v[186:187], v[132:133], off
	v_lshl_add_u64 v[180:181], v[132:133], 0, s[24:25]
	global_load_dwordx2 v[188:189], v[180:181], off
	v_mfma_f32_16x16x32_bf16 v[62:65], v[142:145], v[222:225], v[62:65]
	v_mfma_f32_16x16x32_bf16 v[58:61], v[146:149], v[222:225], v[58:61]
	v_mfma_f32_16x16x32_bf16 v[54:57], v[156:159], v[222:225], v[54:57]
	v_mfma_f32_16x16x32_bf16 v[50:53], v[160:163], v[222:225], v[50:53]
	v_lshl_add_u64 v[180:181], v[132:133], 0, s[26:27]
	global_load_dwordx2 v[190:191], v[180:181], off
	v_lshl_add_u64 v[180:181], v[132:133], 0, s[28:29]
	global_load_dwordx2 v[192:193], v[180:181], off
	v_mfma_f32_16x16x32_bf16 v[46:49], v[142:145], v[226:229], v[46:49]
	v_mfma_f32_16x16x32_bf16 v[42:45], v[146:149], v[226:229], v[42:45]
	v_mfma_f32_16x16x32_bf16 v[38:41], v[156:159], v[226:229], v[38:41]
	v_mfma_f32_16x16x32_bf16 v[34:37], v[160:163], v[226:229], v[34:37]
	v_lshl_add_u64 v[180:181], v[132:133], 0, s[36:37]
	global_load_dwordx2 v[194:195], v[180:181], off
	v_lshl_add_u64 v[180:181], v[132:133], 0, s[38:39]
	global_load_dwordx2 v[196:197], v[180:181], off
	v_mfma_f32_16x16x32_bf16 v[18:21], v[142:145], v[230:233], v[18:21]
	v_mfma_f32_16x16x32_bf16 v[22:25], v[146:149], v[230:233], v[22:25]
	v_mfma_f32_16x16x32_bf16 v[26:29], v[156:159], v[230:233], v[26:29]
	v_mfma_f32_16x16x32_bf16 v[30:33], v[160:163], v[230:233], v[30:33]
	v_lshl_add_u64 v[180:181], v[132:133], 0, s[40:41]
	global_load_dwordx2 v[198:199], v[180:181], off
	v_lshl_add_u64 v[180:181], v[132:133], 0, s[42:43]
	global_load_dwordx2 v[200:201], v[180:181], off
	v_mfma_f32_16x16x32_bf16 v[2:5], v[142:145], v[234:237], v[2:5]
	v_mfma_f32_16x16x32_bf16 v[6:9], v[146:149], v[234:237], v[6:9]
	v_mfma_f32_16x16x32_bf16 v[10:13], v[156:159], v[234:237], v[10:13]
	v_mfma_f32_16x16x32_bf16 v[14:17], v[160:163], v[234:237], v[14:17]
	s_waitcnt vmcnt(21)
	s_waitcnt lgkmcnt(0)
	s_barrier
; #define MD_GLDS_A(buf, tau) do { _Pragma("unroll") for (int i = 0; i < 5; ++i) if (amask & (1u << i)) \
;         __builtin_amdgcn_global_load_lds((const unsigned*)((const char*)HIDp + aoff[i] + (size_t)((tau) & 7) * 128), (PG8_LAS unsigned*)(MD_SA(buf) + wid * 1024 + i * 8192), 16, 0, 0); } while (0)
; #define MD_B_ISSUE(sb, tau) do { const char* kb_ = Bb + (size_t)((tau) >> 3) * 512 + (size_t)((tau) & 7) * (64 * (size_t)RB); _Pragma("unroll") for (int j = 0; j < 8; ++j) { const char* p_ = kb_ + (size_t)j * RB; \
;         asm volatile("global_load_dwordx2 %0, %1, off" : "=&v"(sb[j]) : "v"(p_) : "memory"); } } while (0)
; #define MD_B_WAIT(sb, N) asm volatile("s_waitcnt vmcnt(%8)" : "+v"(sb[0]), "+v"(sb[1]), "+v"(sb[2]), "+v"(sb[3]), "+v"(sb[4]), "+v"(sb[5]), "+v"(sb[6]), "+v"(sb[7]) : "n"(N) : "memory")
; __device__ __forceinline__ void moe_down_stream(PG8_LAS unsigned char* lds, int e, int cb0, int slot0, int nv, const bf16_t* HIDp, const float* Wd, bf16_t* Y, const float* slot_w, const int* slot_dst) {
;     ...
;     f32x4 acc[DNM][4];
; #pragma unroll
;     for (int m = 0; m < DNM; ++m)
; #pragma unroll
;         for (int n = 0; n < 4; ++n) acc[m][n] = (f32x4){0.f, 0.f, 0.f, 0.f};
;     f32x2 s0[8], s1[8];
;     MD_GLDS_A(0, 0); MD_B_ISSUE(s0, 0); MD_B_ISSUE(s1, 1);
;     MD_B_WAIT(s0, 8); MD_B_WRITE(s0, 0); __builtin_amdgcn_sched_barrier(0); MD_B_ISSUE(s0, 2);
;     asm volatile("s_waitcnt vmcnt(16)" ::: "memory");
;     asm volatile("s_waitcnt lgkmcnt(0)" ::: "memory"); __builtin_amdgcn_s_barrier(); asm volatile("" ::: "memory");
; #pragma unroll 1
;     for (int t = 0; t < NT; t += 2) {
;         if (t + 2 < NT) MD_B_WAIT(s1, 8); else MD_B_WAIT(s1, 0);
;         MD_B_WRITE(s1, 1); __builtin_amdgcn_sched_barrier(0); MD_GLDS_A(1, t + 1); __builtin_amdgcn_sched_barrier(0);
;         if (t + 3 < NT) MD_B_ISSUE(s1, t + 3);
;         MD_COMPUTE(0);
;         MD_END(t + 3 >= NT);
;         if (t + 2 < NT) { MD_B_WAIT(s0, 8); MD_B_WRITE(s0, 0); __builtin_amdgcn_sched_barrier(0); MD_GLDS_A(0, t + 2); __builtin_amdgcn_sched_barrier(0); }
;         if (t + 4 < NT) MD_B_ISSUE(s0, t + 4);
;         MD_COMPUTE(1);
;         MD_END(t + 4 >= NT);
	s_mov_b32 s49, s46
	s_mov_b32 s46, s47
	s_mov_b32 s47, s48
	s_mov_b32 s48, s49
	s_add_i32 s50, s50, 1
	v_cvt_pk_bf16_f32 v172, v202, v204
	v_cvt_pk_bf16_f32 v173, v206, v208
	v_cvt_pk_bf16_f32 v174, v210, v212
	v_cvt_pk_bf16_f32 v175, v214, v216
	v_cvt_pk_bf16_f32 v176, v203, v205
	v_cvt_pk_bf16_f32 v177, v207, v209
	v_cvt_pk_bf16_f32 v178, v211, v213
	v_cvt_pk_bf16_f32 v179, v215, v217
	ds_write_b128 v95, v[172:175] offset:19456
	ds_write_b128 v95, v[176:179] offset:19584
	v_add_u32_e32 v91, s46, v135
	v_add_u32_e32 v93, s46, v137
	ds_read_b128 v[238:241], v139 offset:0
	ds_read_b128 v[242:245], v139 offset:2048
	ds_read_b128 v[246:249], v139 offset:4096
	ds_read_b128 v[250:253], v139 offset:6144
	ds_read_b128 v[218:221], v91 offset:0
	ds_read_b128 v[222:225], v91 offset:2048
	ds_read_b128 v[226:229], v91 offset:4096
	ds_read_b128 v[230:233], v91 offset:6144
	ds_read_b128 v[234:237], v91 offset:8192
	s_add_i32 s49, s48, s74
	s_add_i32 s52, s52, 1
	s_and_b32 s54, s52, 7
	s_cmp_eq_u32 s54, 0
	s_cselect_b32 s54, s53, s32
	s_cselect_b32 s55, -1, 0
	s_add_u32 s30, s30, s54
	s_addc_u32 s31, s31, s55
	s_waitcnt lgkmcnt(0)
	v_mfma_f32_16x16x32_bf16 v[78:81], v[238:241], v[218:221], v[78:81]
	v_mfma_f32_16x16x32_bf16 v[74:77], v[242:245], v[218:221], v[74:77]
	v_mfma_f32_16x16x32_bf16 v[70:73], v[246:249], v[218:221], v[70:73]
	v_mfma_f32_16x16x32_bf16 v[66:69], v[250:253], v[218:221], v[66:69]
	ds_read_b128 v[218:221], v93 offset:0
	ds_read_b128 v[142:145], v141 offset:0
	s_mov_b32 m0, s49
	s_nop 0
	global_load_lds_dwordx4 v88, s[30:31]
	v_mfma_f32_16x16x32_bf16 v[62:65], v[238:241], v[222:225], v[62:65]
	v_mfma_f32_16x16x32_bf16 v[58:61], v[242:245], v[222:225], v[58:61]
	v_mfma_f32_16x16x32_bf16 v[54:57], v[246:249], v[222:225], v[54:57]
	v_mfma_f32_16x16x32_bf16 v[50:53], v[250:253], v[222:225], v[50:53]
	ds_read_b128 v[222:225], v93 offset:2048
	ds_read_b128 v[146:149], v141 offset:2048
	s_add_i32 m0, s49, 0x2000
	s_nop 0
	global_load_lds_dwordx4 v90, s[30:31]
	v_mfma_f32_16x16x32_bf16 v[46:49], v[238:241], v[226:229], v[46:49]
	v_mfma_f32_16x16x32_bf16 v[42:45], v[242:245], v[226:229], v[42:45]
	v_mfma_f32_16x16x32_bf16 v[38:41], v[246:249], v[226:229], v[38:41]
	v_mfma_f32_16x16x32_bf16 v[34:37], v[250:253], v[226:229], v[34:37]
	ds_read_b128 v[226:229], v93 offset:4096
	ds_read_b128 v[156:159], v141 offset:4096
	s_add_i32 m0, s49, 0x4000
	s_nop 0
	global_load_lds_dwordx4 v92, s[30:31]
	v_mfma_f32_16x16x32_bf16 v[18:21], v[238:241], v[230:233], v[18:21]
	v_mfma_f32_16x16x32_bf16 v[22:25], v[242:245], v[230:233], v[22:25]
	v_mfma_f32_16x16x32_bf16 v[26:29], v[246:249], v[230:233], v[26:29]
	v_mfma_f32_16x16x32_bf16 v[30:33], v[250:253], v[230:233], v[30:33]
	ds_read_b128 v[230:233], v93 offset:6144
	ds_read_b128 v[160:163], v141 offset:6144
	s_add_i32 m0, s49, 0x6000
	s_nop 0
	global_load_lds_dwordx4 v94, s[30:31]
	v_mfma_f32_16x16x32_bf16 v[2:5], v[238:241], v[234:237], v[2:5]
	v_mfma_f32_16x16x32_bf16 v[6:9], v[242:245], v[234:237], v[6:9]
	v_mfma_f32_16x16x32_bf16 v[10:13], v[246:249], v[234:237], v[10:13]
	v_mfma_f32_16x16x32_bf16 v[14:17], v[250:253], v[234:237], v[14:17]
	ds_read_b128 v[234:237], v93 offset:8192
	s_add_i32 m0, s49, 0x8000
	s_nop 0
	global_load_lds_dwordx4 v96, s[30:31]
	s_waitcnt lgkmcnt(0)
	v_mfma_f32_16x16x32_bf16 v[78:81], v[142:145], v[218:221], v[78:81]
	v_mfma_f32_16x16x32_bf16 v[74:77], v[146:149], v[218:221], v[74:77]
	v_mfma_f32_16x16x32_bf16 v[70:73], v[156:159], v[218:221], v[70:73]
	v_mfma_f32_16x16x32_bf16 v[66:69], v[160:163], v[218:221], v[66:69]
	s_add_i32 s51, s51, 1
	s_and_b32 s54, s51, 7
	s_cmp_eq_u32 s54, 0
	s_cselect_b32 s44, s34, s35
	s_cselect_b32 s45, -1, 0
	v_lshl_add_u64 v[132:133], v[132:133], 0, s[44:45]
	global_load_dwordx2 v[202:203], v[132:133], off
	v_lshl_add_u64 v[180:181], v[132:133], 0, s[24:25]
	global_load_dwordx2 v[204:205], v[180:181], off
	v_mfma_f32_16x16x32_bf16 v[62:65], v[142:145], v[222:225], v[62:65]
	v_mfma_f32_16x16x32_bf16 v[58:61], v[146:149], v[222:225], v[58:61]
	v_mfma_f32_16x16x32_bf16 v[54:57], v[156:159], v[222:225], v[54:57]
	v_mfma_f32_16x16x32_bf16 v[50:53], v[160:163], v[222:225], v[50:53]
	v_lshl_add_u64 v[180:181], v[132:133], 0, s[26:27]
	global_load_dwordx2 v[206:207], v[180:181], off
	v_lshl_add_u64 v[180:181], v[132:133], 0, s[28:29]
	global_load_dwordx2 v[208:209], v[180:181], off
	v_mfma_f32_16x16x32_bf16 v[46:49], v[142:145], v[226:229], v[46:49]
	v_mfma_f32_16x16x32_bf16 v[42:45], v[146:149], v[226:229], v[42:45]
	v_mfma_f32_16x16x32_bf16 v[38:41], v[156:159], v[226:229], v[38:41]
	v_mfma_f32_16x16x32_bf16 v[34:37], v[160:163], v[226:229], v[34:37]
	v_lshl_add_u64 v[180:181], v[132:133], 0, s[36:37]
	global_load_dwordx2 v[210:211], v[180:181], off
	v_lshl_add_u64 v[180:181], v[132:133], 0, s[38:39]
	global_load_dwordx2 v[212:213], v[180:181], off
	v_mfma_f32_16x16x32_bf16 v[18:21], v[142:145], v[230:233], v[18:21]
	v_mfma_f32_16x16x32_bf16 v[22:25], v[146:149], v[230:233], v[22:25]
	v_mfma_f32_16x16x32_bf16 v[26:29], v[156:159], v[230:233], v[26:29]
	v_mfma_f32_16x16x32_bf16 v[30:33], v[160:163], v[230:233], v[30:33]
	v_lshl_add_u64 v[180:181], v[132:133], 0, s[40:41]
	global_load_dwordx2 v[214:215], v[180:181], off
	v_lshl_add_u64 v[180:181], v[132:133], 0, s[42:43]
	global_load_dwordx2 v[216:217], v[180:181], off
	v_mfma_f32_16x16x32_bf16 v[2:5], v[142:145], v[234:237], v[2:5]
	v_mfma_f32_16x16x32_bf16 v[6:9], v[146:149], v[234:237], v[6:9]
	v_mfma_f32_16x16x32_bf16 v[10:13], v[156:159], v[234:237], v[10:13]
	v_mfma_f32_16x16x32_bf16 v[14:17], v[160:163], v[234:237], v[14:17]
	s_waitcnt vmcnt(21)
	s_waitcnt lgkmcnt(0)
	s_barrier
; #define MD_GLDS_A(buf, tau) do { _Pragma("unroll") for (int i = 0; i < 5; ++i) if (amask & (1u << i)) \
;         __builtin_amdgcn_global_load_lds((const unsigned*)((const char*)HIDp + aoff[i] + (size_t)((tau) & 7) * 128), (PG8_LAS unsigned*)(MD_SA(buf) + wid * 1024 + i * 8192), 16, 0, 0); } while (0)
; #define MD_B_ISSUE(sb, tau) do { const char* kb_ = Bb + (size_t)((tau) >> 3) * 512 + (size_t)((tau) & 7) * (64 * (size_t)RB); _Pragma("unroll") for (int j = 0; j < 8; ++j) { const char* p_ = kb_ + (size_t)j * RB; \
;         asm volatile("global_load_dwordx2 %0, %1, off" : "=&v"(sb[j]) : "v"(p_) : "memory"); } } while (0)
; #define MD_B_WAIT(sb, N) asm volatile("s_waitcnt vmcnt(%8)" : "+v"(sb[0]), "+v"(sb[1]), "+v"(sb[2]), "+v"(sb[3]), "+v"(sb[4]), "+v"(sb[5]), "+v"(sb[6]), "+v"(sb[7]) : "n"(N) : "memory")
; __device__ __forceinline__ void moe_down_stream(PG8_LAS unsigned char* lds, int e, int cb0, int slot0, int nv, const bf16_t* HIDp, const float* Wd, bf16_t* Y, const float* slot_w, const int* slot_dst) {
;     ...
;     f32x4 acc[DNM][4];
; #pragma unroll
;     for (int m = 0; m < DNM; ++m)
; #pragma unroll
;         for (int n = 0; n < 4; ++n) acc[m][n] = (f32x4){0.f, 0.f, 0.f, 0.f};
;     f32x2 s0[8], s1[8];
;     MD_GLDS_A(0, 0); MD_B_ISSUE(s0, 0); MD_B_ISSUE(s1, 1);
;     MD_B_WAIT(s0, 8); MD_B_WRITE(s0, 0); __builtin_amdgcn_sched_barrier(0); MD_B_ISSUE(s0, 2);
;     asm volatile("s_waitcnt vmcnt(16)" ::: "memory");
;     asm volatile("s_waitcnt lgkmcnt(0)" ::: "memory"); __builtin_amdgcn_s_barrier(); asm volatile("" ::: "memory");
; #pragma unroll 1
;     for (int t = 0; t < NT; t += 2) {
;         if (t + 2 < NT) MD_B_WAIT(s1, 8); else MD_B_WAIT(s1, 0);
;         MD_B_WRITE(s1, 1); __builtin_amdgcn_sched_barrier(0); MD_GLDS_A(1, t + 1); __builtin_amdgcn_sched_barrier(0);
;         if (t + 3 < NT) MD_B_ISSUE(s1, t + 3);
;         MD_COMPUTE(0);
;         MD_END(t + 3 >= NT);
;         if (t + 2 < NT) { MD_B_WAIT(s0, 8); MD_B_WRITE(s0, 0); __builtin_amdgcn_sched_barrier(0); MD_GLDS_A(0, t + 2); __builtin_amdgcn_sched_barrier(0); }
;         if (t + 4 < NT) MD_B_ISSUE(s0, t + 4);
;         MD_COMPUTE(1);
;         MD_END(t + 4 >= NT);
	s_mov_b32 s49, s46
	s_mov_b32 s46, s47
	s_mov_b32 s47, s48
	s_mov_b32 s48, s49
	s_add_i32 s50, s50, 1
	v_cvt_pk_bf16_f32 v172, v98, v100
	v_cvt_pk_bf16_f32 v173, v102, v104
	v_cvt_pk_bf16_f32 v174, v106, v108
	v_cvt_pk_bf16_f32 v175, v110, v112
	v_cvt_pk_bf16_f32 v176, v99, v101
	v_cvt_pk_bf16_f32 v177, v103, v105
	v_cvt_pk_bf16_f32 v178, v107, v109
	v_cvt_pk_bf16_f32 v179, v111, v113
	ds_write_b128 v95, v[172:175] offset:0
	ds_write_b128 v95, v[176:179] offset:128
	v_add_u32_e32 v91, s46, v135
	v_add_u32_e32 v93, s46, v137
	ds_read_b128 v[238:241], v139 offset:19456
	ds_read_b128 v[242:245], v139 offset:21504
	ds_read_b128 v[246:249], v139 offset:23552
	ds_read_b128 v[250:253], v139 offset:25600
	ds_read_b128 v[218:221], v91 offset:0
	ds_read_b128 v[222:225], v91 offset:2048
	ds_read_b128 v[226:229], v91 offset:4096
	ds_read_b128 v[230:233], v91 offset:6144
	ds_read_b128 v[234:237], v91 offset:8192
	s_add_i32 s49, s48, s74
	s_add_i32 s52, s52, 1
	s_and_b32 s54, s52, 7
	s_cmp_eq_u32 s54, 0
	s_cselect_b32 s54, s53, s32
	s_cselect_b32 s55, -1, 0
	s_add_u32 s30, s30, s54
	s_addc_u32 s31, s31, s55
	s_waitcnt lgkmcnt(0)
	v_mfma_f32_16x16x32_bf16 v[78:81], v[238:241], v[218:221], v[78:81]
	v_mfma_f32_16x16x32_bf16 v[74:77], v[242:245], v[218:221], v[74:77]
	v_mfma_f32_16x16x32_bf16 v[70:73], v[246:249], v[218:221], v[70:73]
	v_mfma_f32_16x16x32_bf16 v[66:69], v[250:253], v[218:221], v[66:69]
	ds_read_b128 v[218:221], v93 offset:0
	ds_read_b128 v[142:145], v141 offset:19456
	s_mov_b32 m0, s49
	s_nop 0
	global_load_lds_dwordx4 v88, s[30:31]
	v_mfma_f32_16x16x32_bf16 v[62:65], v[238:241], v[222:225], v[62:65]
	v_mfma_f32_16x16x32_bf16 v[58:61], v[242:245], v[222:225], v[58:61]
	v_mfma_f32_16x16x32_bf16 v[54:57], v[246:249], v[222:225], v[54:57]
	v_mfma_f32_16x16x32_bf16 v[50:53], v[250:253], v[222:225], v[50:53]
	ds_read_b128 v[222:225], v93 offset:2048
	ds_read_b128 v[146:149], v141 offset:21504
	s_add_i32 m0, s49, 0x2000
	s_nop 0
	global_load_lds_dwordx4 v90, s[30:31]
	v_mfma_f32_16x16x32_bf16 v[46:49], v[238:241], v[226:229], v[46:49]
	v_mfma_f32_16x16x32_bf16 v[42:45], v[242:245], v[226:229], v[42:45]
	v_mfma_f32_16x16x32_bf16 v[38:41], v[246:249], v[226:229], v[38:41]
	v_mfma_f32_16x16x32_bf16 v[34:37], v[250:253], v[226:229], v[34:37]
	ds_read_b128 v[226:229], v93 offset:4096
	ds_read_b128 v[156:159], v141 offset:23552
	s_add_i32 m0, s49, 0x4000
	s_nop 0
	global_load_lds_dwordx4 v92, s[30:31]
	v_mfma_f32_16x16x32_bf16 v[18:21], v[238:241], v[230:233], v[18:21]
	v_mfma_f32_16x16x32_bf16 v[22:25], v[242:245], v[230:233], v[22:25]
	v_mfma_f32_16x16x32_bf16 v[26:29], v[246:249], v[230:233], v[26:29]
	v_mfma_f32_16x16x32_bf16 v[30:33], v[250:253], v[230:233], v[30:33]
	ds_read_b128 v[230:233], v93 offset:6144
	ds_read_b128 v[160:163], v141 offset:25600
	s_add_i32 m0, s49, 0x6000
	s_nop 0
	global_load_lds_dwordx4 v94, s[30:31]
	v_mfma_f32_16x16x32_bf16 v[2:5], v[238:241], v[234:237], v[2:5]
	v_mfma_f32_16x16x32_bf16 v[6:9], v[242:245], v[234:237], v[6:9]
	v_mfma_f32_16x16x32_bf16 v[10:13], v[246:249], v[234:237], v[10:13]
	v_mfma_f32_16x16x32_bf16 v[14:17], v[250:253], v[234:237], v[14:17]
	ds_read_b128 v[234:237], v93 offset:8192
	s_add_i32 m0, s49, 0x8000
	s_nop 0
	global_load_lds_dwordx4 v96, s[30:31]
	s_waitcnt lgkmcnt(0)
	v_mfma_f32_16x16x32_bf16 v[78:81], v[142:145], v[218:221], v[78:81]
	v_mfma_f32_16x16x32_bf16 v[74:77], v[146:149], v[218:221], v[74:77]
	v_mfma_f32_16x16x32_bf16 v[70:73], v[156:159], v[218:221], v[70:73]
	v_mfma_f32_16x16x32_bf16 v[66:69], v[160:163], v[218:221], v[66:69]
	s_add_i32 s51, s51, 1
	s_and_b32 s54, s51, 7
	s_cmp_eq_u32 s54, 0
	s_cselect_b32 s44, s34, s35
	s_cselect_b32 s45, -1, 0
	v_lshl_add_u64 v[132:133], v[132:133], 0, s[44:45]
	global_load_dwordx2 v[98:99], v[132:133], off
	v_lshl_add_u64 v[180:181], v[132:133], 0, s[24:25]
	global_load_dwordx2 v[100:101], v[180:181], off
	v_mfma_f32_16x16x32_bf16 v[62:65], v[142:145], v[222:225], v[62:65]
	v_mfma_f32_16x16x32_bf16 v[58:61], v[146:149], v[222:225], v[58:61]
	v_mfma_f32_16x16x32_bf16 v[54:57], v[156:159], v[222:225], v[54:57]
	v_mfma_f32_16x16x32_bf16 v[50:53], v[160:163], v[222:225], v[50:53]
	v_lshl_add_u64 v[180:181], v[132:133], 0, s[26:27]
	global_load_dwordx2 v[102:103], v[180:181], off
	v_lshl_add_u64 v[180:181], v[132:133], 0, s[28:29]
	global_load_dwordx2 v[104:105], v[180:181], off
	v_mfma_f32_16x16x32_bf16 v[46:49], v[142:145], v[226:229], v[46:49]
	v_mfma_f32_16x16x32_bf16 v[42:45], v[146:149], v[226:229], v[42:45]
	v_mfma_f32_16x16x32_bf16 v[38:41], v[156:159], v[226:229], v[38:41]
	v_mfma_f32_16x16x32_bf16 v[34:37], v[160:163], v[226:229], v[34:37]
	v_lshl_add_u64 v[180:181], v[132:133], 0, s[36:37]
	global_load_dwordx2 v[106:107], v[180:181], off
	v_lshl_add_u64 v[180:181], v[132:133], 0, s[38:39]
	global_load_dwordx2 v[108:109], v[180:181], off
	v_mfma_f32_16x16x32_bf16 v[18:21], v[142:145], v[230:233], v[18:21]
	v_mfma_f32_16x16x32_bf16 v[22:25], v[146:149], v[230:233], v[22:25]
	v_mfma_f32_16x16x32_bf16 v[26:29], v[156:159], v[230:233], v[26:29]
	v_mfma_f32_16x16x32_bf16 v[30:33], v[160:163], v[230:233], v[30:33]
	v_lshl_add_u64 v[180:181], v[132:133], 0, s[40:41]
	global_load_dwordx2 v[110:111], v[180:181], off
	v_lshl_add_u64 v[180:181], v[132:133], 0, s[42:43]
	global_load_dwordx2 v[112:113], v[180:181], off
	v_mfma_f32_16x16x32_bf16 v[2:5], v[142:145], v[234:237], v[2:5]
	v_mfma_f32_16x16x32_bf16 v[6:9], v[146:149], v[234:237], v[6:9]
	v_mfma_f32_16x16x32_bf16 v[10:13], v[156:159], v[234:237], v[10:13]
	v_mfma_f32_16x16x32_bf16 v[14:17], v[160:163], v[234:237], v[14:17]
	s_waitcnt vmcnt(21)
	s_waitcnt lgkmcnt(0)
	s_barrier
	s_mov_b32 s49, s46
	s_mov_b32 s46, s47
	s_mov_b32 s47, s48
	s_mov_b32 s48, s49
	s_add_i32 s50, s50, 1
	s_mov_b32 s56, 5
; #define MD_GLDS_A(buf, tau) do { _Pragma("unroll") for (int i = 0; i < 5; ++i) if (amask & (1u << i)) \
;         __builtin_amdgcn_global_load_lds((const unsigned*)((const char*)HIDp + aoff[i] + (size_t)((tau) & 7) * 128), (PG8_LAS unsigned*)(MD_SA(buf) + wid * 1024 + i * 8192), 16, 0, 0); } while (0)
; #define MD_B_ISSUE(sb, tau) do { const char* kb_ = Bb + (size_t)((tau) >> 3) * 512 + (size_t)((tau) & 7) * (64 * (size_t)RB); _Pragma("unroll") for (int j = 0; j < 8; ++j) { const char* p_ = kb_ + (size_t)j * RB; \
;         asm volatile("global_load_dwordx2 %0, %1, off" : "=&v"(sb[j]) : "v"(p_) : "memory"); } } while (0)
; #define MD_B_WAIT(sb, N) asm volatile("s_waitcnt vmcnt(%8)" : "+v"(sb[0]), "+v"(sb[1]), "+v"(sb[2]), "+v"(sb[3]), "+v"(sb[4]), "+v"(sb[5]), "+v"(sb[6]), "+v"(sb[7]) : "n"(N) : "memory")
; #define MD_END(last) do { if (last) asm volatile("s_waitcnt vmcnt(0)" ::: "memory"); else asm volatile("s_waitcnt vmcnt(8)" ::: "memory"); \
;         asm volatile("s_waitcnt lgkmcnt(0)" ::: "memory"); __builtin_amdgcn_s_barrier(); asm volatile("" ::: "memory"); } while (0)
; __device__ __forceinline__ void moe_down_stream(PG8_LAS unsigned char* lds, int e, int cb0, int slot0, int nv, const bf16_t* HIDp, const float* Wd, bf16_t* Y, const float* slot_w, const int* slot_dst) {
;     ...
;     for (int t = 0; t < NT; t += 2) {
;         if (t + 2 < NT) MD_B_WAIT(s1, 8); else MD_B_WAIT(s1, 0);
;         MD_B_WRITE(s1, 1); __builtin_amdgcn_sched_barrier(0); MD_GLDS_A(1, t + 1); __builtin_amdgcn_sched_barrier(0);
;         if (t + 3 < NT) MD_B_ISSUE(s1, t + 3);
;         MD_COMPUTE(0);
;         MD_END(t + 3 >= NT);
;         if (t + 2 < NT) { MD_B_WAIT(s0, 8); MD_B_WRITE(s0, 0); __builtin_amdgcn_sched_barrier(0); MD_GLDS_A(0, t + 2); __builtin_amdgcn_sched_barrier(0); }
;         if (t + 4 < NT) MD_B_ISSUE(s0, t + 4);
;         MD_COMPUTE(1);
;         MD_END(t + 4 >= NT);
.Lmd_loop_X:
	v_cvt_pk_bf16_f32 v172, v114, v116
	v_cvt_pk_bf16_f32 v173, v118, v120
	v_cvt_pk_bf16_f32 v174, v122, v124
	v_cvt_pk_bf16_f32 v175, v126, v128
	v_cvt_pk_bf16_f32 v176, v115, v117
	v_cvt_pk_bf16_f32 v177, v119, v121
	v_cvt_pk_bf16_f32 v178, v123, v125
	v_cvt_pk_bf16_f32 v179, v127, v129
	ds_write_b128 v95, v[172:175] offset:19456
	ds_write_b128 v95, v[176:179] offset:19584
	v_add_u32_e32 v91, s46, v135
	v_add_u32_e32 v93, s46, v137
	ds_read_b128 v[238:241], v139 offset:0
	ds_read_b128 v[242:245], v139 offset:2048
	ds_read_b128 v[246:249], v139 offset:4096
	ds_read_b128 v[250:253], v139 offset:6144
	ds_read_b128 v[218:221], v91 offset:0
	ds_read_b128 v[222:225], v91 offset:2048
	ds_read_b128 v[226:229], v91 offset:4096
	ds_read_b128 v[230:233], v91 offset:6144
	ds_read_b128 v[234:237], v91 offset:8192
	s_add_i32 s49, s48, s74
	s_add_i32 s52, s52, 1
	s_and_b32 s54, s52, 7
	s_cmp_eq_u32 s54, 0
	s_cselect_b32 s54, s53, s32
	s_cselect_b32 s55, -1, 0
	s_add_u32 s30, s30, s54
	s_addc_u32 s31, s31, s55
	s_waitcnt lgkmcnt(0)
	v_mfma_f32_16x16x32_bf16 v[78:81], v[238:241], v[218:221], v[78:81]
	v_mfma_f32_16x16x32_bf16 v[74:77], v[242:245], v[218:221], v[74:77]
	v_mfma_f32_16x16x32_bf16 v[70:73], v[246:249], v[218:221], v[70:73]
	v_mfma_f32_16x16x32_bf16 v[66:69], v[250:253], v[218:221], v[66:69]
	ds_read_b128 v[218:221], v93 offset:0
	ds_read_b128 v[142:145], v141 offset:0
	s_mov_b32 m0, s49
	s_nop 0
	global_load_lds_dwordx4 v88, s[30:31]
	v_mfma_f32_16x16x32_bf16 v[62:65], v[238:241], v[222:225], v[62:65]
	v_mfma_f32_16x16x32_bf16 v[58:61], v[242:245], v[222:225], v[58:61]
	v_mfma_f32_16x16x32_bf16 v[54:57], v[246:249], v[222:225], v[54:57]
	v_mfma_f32_16x16x32_bf16 v[50:53], v[250:253], v[222:225], v[50:53]
	ds_read_b128 v[222:225], v93 offset:2048
	ds_read_b128 v[146:149], v141 offset:2048
	s_add_i32 m0, s49, 0x2000
	s_nop 0
	global_load_lds_dwordx4 v90, s[30:31]
	v_mfma_f32_16x16x32_bf16 v[46:49], v[238:241], v[226:229], v[46:49]
	v_mfma_f32_16x16x32_bf16 v[42:45], v[242:245], v[226:229], v[42:45]
	v_mfma_f32_16x16x32_bf16 v[38:41], v[246:249], v[226:229], v[38:41]
	v_mfma_f32_16x16x32_bf16 v[34:37], v[250:253], v[226:229], v[34:37]
	ds_read_b128 v[226:229], v93 offset:4096
	ds_read_b128 v[156:159], v141 offset:4096
	s_add_i32 m0, s49, 0x4000
	s_nop 0
	global_load_lds_dwordx4 v92, s[30:31]
	v_mfma_f32_16x16x32_bf16 v[18:21], v[238:241], v[230:233], v[18:21]
	v_mfma_f32_16x16x32_bf16 v[22:25], v[242:245], v[230:233], v[22:25]
	v_mfma_f32_16x16x32_bf16 v[26:29], v[246:249], v[230:233], v[26:29]
	v_mfma_f32_16x16x32_bf16 v[30:33], v[250:253], v[230:233], v[30:33]
	ds_read_b128 v[230:233], v93 offset:6144
	ds_read_b128 v[160:163], v141 offset:6144
	s_add_i32 m0, s49, 0x6000
	s_nop 0
	global_load_lds_dwordx4 v94, s[30:31]
	v_mfma_f32_16x16x32_bf16 v[2:5], v[238:241], v[234:237], v[2:5]
	v_mfma_f32_16x16x32_bf16 v[6:9], v[242:245], v[234:237], v[6:9]
	v_mfma_f32_16x16x32_bf16 v[10:13], v[246:249], v[234:237], v[10:13]
	v_mfma_f32_16x16x32_bf16 v[14:17], v[250:253], v[234:237], v[14:17]
	ds_read_b128 v[234:237], v93 offset:8192
	s_add_i32 m0, s49, 0x8000
	s_nop 0
	global_load_lds_dwordx4 v96, s[30:31]
	s_waitcnt lgkmcnt(0)
	v_mfma_f32_16x16x32_bf16 v[78:81], v[142:145], v[218:221], v[78:81]
	v_mfma_f32_16x16x32_bf16 v[74:77], v[146:149], v[218:221], v[74:77]
	v_mfma_f32_16x16x32_bf16 v[70:73], v[156:159], v[218:221], v[70:73]
	v_mfma_f32_16x16x32_bf16 v[66:69], v[160:163], v[218:221], v[66:69]
	s_add_i32 s51, s51, 1
	s_and_b32 s54, s51, 7
	s_cmp_eq_u32 s54, 0
	s_cselect_b32 s44, s34, s35
	s_cselect_b32 s45, -1, 0
	v_lshl_add_u64 v[132:133], v[132:133], 0, s[44:45]
	global_load_dwordx2 v[114:115], v[132:133], off
	v_lshl_add_u64 v[180:181], v[132:133], 0, s[24:25]
	global_load_dwordx2 v[116:117], v[180:181], off
	v_mfma_f32_16x16x32_bf16 v[62:65], v[142:145], v[222:225], v[62:65]
	v_mfma_f32_16x16x32_bf16 v[58:61], v[146:149], v[222:225], v[58:61]
	v_mfma_f32_16x16x32_bf16 v[54:57], v[156:159], v[222:225], v[54:57]
	v_mfma_f32_16x16x32_bf16 v[50:53], v[160:163], v[222:225], v[50:53]
	v_lshl_add_u64 v[180:181], v[132:133], 0, s[26:27]
	global_load_dwordx2 v[118:119], v[180:181], off
	v_lshl_add_u64 v[180:181], v[132:133], 0, s[28:29]
	global_load_dwordx2 v[120:121], v[180:181], off
	v_mfma_f32_16x16x32_bf16 v[46:49], v[142:145], v[226:229], v[46:49]
	v_mfma_f32_16x16x32_bf16 v[42:45], v[146:149], v[226:229], v[42:45]
	v_mfma_f32_16x16x32_bf16 v[38:41], v[156:159], v[226:229], v[38:41]
	v_mfma_f32_16x16x32_bf16 v[34:37], v[160:163], v[226:229], v[34:37]
	v_lshl_add_u64 v[180:181], v[132:133], 0, s[36:37]
	global_load_dwordx2 v[122:123], v[180:181], off
	v_lshl_add_u64 v[180:181], v[132:133], 0, s[38:39]
	global_load_dwordx2 v[124:125], v[180:181], off
	v_mfma_f32_16x16x32_bf16 v[18:21], v[142:145], v[230:233], v[18:21]
	v_mfma_f32_16x16x32_bf16 v[22:25], v[146:149], v[230:233], v[22:25]
	v_mfma_f32_16x16x32_bf16 v[26:29], v[156:159], v[230:233], v[26:29]
	v_mfma_f32_16x16x32_bf16 v[30:33], v[160:163], v[230:233], v[30:33]
	v_lshl_add_u64 v[180:181], v[132:133], 0, s[40:41]
	global_load_dwordx2 v[126:127], v[180:181], off
	v_lshl_add_u64 v[180:181], v[132:133], 0, s[42:43]
	global_load_dwordx2 v[128:129], v[180:181], off
	v_mfma_f32_16x16x32_bf16 v[2:5], v[142:145], v[234:237], v[2:5]
	v_mfma_f32_16x16x32_bf16 v[6:9], v[146:149], v[234:237], v[6:9]
	v_mfma_f32_16x16x32_bf16 v[10:13], v[156:159], v[234:237], v[10:13]
	v_mfma_f32_16x16x32_bf16 v[14:17], v[160:163], v[234:237], v[14:17]
	s_waitcnt vmcnt(21)
	s_waitcnt lgkmcnt(0)
	s_barrier
; #define MD_GLDS_A(buf, tau) do { _Pragma("unroll") for (int i = 0; i < 5; ++i) if (amask & (1u << i)) \
;         __builtin_amdgcn_global_load_lds((const unsigned*)((const char*)HIDp + aoff[i] + (size_t)((tau) & 7) * 128), (PG8_LAS unsigned*)(MD_SA(buf) + wid * 1024 + i * 8192), 16, 0, 0); } while (0)
; #define MD_B_ISSUE(sb, tau) do { const char* kb_ = Bb + (size_t)((tau) >> 3) * 512 + (size_t)((tau) & 7) * (64 * (size_t)RB); _Pragma("unroll") for (int j = 0; j < 8; ++j) { const char* p_ = kb_ + (size_t)j * RB; \
;         asm volatile("global_load_dwordx2 %0, %1, off" : "=&v"(sb[j]) : "v"(p_) : "memory"); } } while (0)
; #define MD_B_WAIT(sb, N) asm volatile("s_waitcnt vmcnt(%8)" : "+v"(sb[0]), "+v"(sb[1]), "+v"(sb[2]), "+v"(sb[3]), "+v"(sb[4]), "+v"(sb[5]), "+v"(sb[6]), "+v"(sb[7]) : "n"(N) : "memory")
; #define MD_END(last) do { if (last) asm volatile("s_waitcnt vmcnt(0)" ::: "memory"); else asm volatile("s_waitcnt vmcnt(8)" ::: "memory"); \
;         asm volatile("s_waitcnt lgkmcnt(0)" ::: "memory"); __builtin_amdgcn_s_barrier(); asm volatile("" ::: "memory"); } while (0)
; __device__ __forceinline__ void moe_down_stream(PG8_LAS unsigned char* lds, int e, int cb0, int slot0, int nv, const bf16_t* HIDp, const float* Wd, bf16_t* Y, const float* slot_w, const int* slot_dst) {
;     ...
;     for (int t = 0; t < NT; t += 2) {
;         if (t + 2 < NT) MD_B_WAIT(s1, 8); else MD_B_WAIT(s1, 0);
;         MD_B_WRITE(s1, 1); __builtin_amdgcn_sched_barrier(0); MD_GLDS_A(1, t + 1); __builtin_amdgcn_sched_barrier(0);
;         if (t + 3 < NT) MD_B_ISSUE(s1, t + 3);
;         MD_COMPUTE(0);
;         MD_END(t + 3 >= NT);
;         if (t + 2 < NT) { MD_B_WAIT(s0, 8); MD_B_WRITE(s0, 0); __builtin_amdgcn_sched_barrier(0); MD_GLDS_A(0, t + 2); __builtin_amdgcn_sched_barrier(0); }
;         if (t + 4 < NT) MD_B_ISSUE(s0, t + 4);
;         MD_COMPUTE(1);
;         MD_END(t + 4 >= NT);
	s_mov_b32 s49, s46
	s_mov_b32 s46, s47
	s_mov_b32 s47, s48
	s_mov_b32 s48, s49
	s_add_i32 s50, s50, 1
	v_cvt_pk_bf16_f32 v172, v186, v188
	v_cvt_pk_bf16_f32 v173, v190, v192
	v_cvt_pk_bf16_f32 v174, v194, v196
	v_cvt_pk_bf16_f32 v175, v198, v200
	v_cvt_pk_bf16_f32 v176, v187, v189
	v_cvt_pk_bf16_f32 v177, v191, v193
	v_cvt_pk_bf16_f32 v178, v195, v197
	v_cvt_pk_bf16_f32 v179, v199, v201
	ds_write_b128 v95, v[172:175] offset:0
	ds_write_b128 v95, v[176:179] offset:128
	v_add_u32_e32 v91, s46, v135
	v_add_u32_e32 v93, s46, v137
	ds_read_b128 v[238:241], v139 offset:19456
	ds_read_b128 v[242:245], v139 offset:21504
	ds_read_b128 v[246:249], v139 offset:23552
	ds_read_b128 v[250:253], v139 offset:25600
	ds_read_b128 v[218:221], v91 offset:0
	ds_read_b128 v[222:225], v91 offset:2048
	ds_read_b128 v[226:229], v91 offset:4096
	ds_read_b128 v[230:233], v91 offset:6144
	ds_read_b128 v[234:237], v91 offset:8192
	s_add_i32 s49, s48, s74
	s_add_i32 s52, s52, 1
	s_and_b32 s54, s52, 7
	s_cmp_eq_u32 s54, 0
	s_cselect_b32 s54, s53, s32
	s_cselect_b32 s55, -1, 0
	s_add_u32 s30, s30, s54
	s_addc_u32 s31, s31, s55
	s_waitcnt lgkmcnt(0)
	v_mfma_f32_16x16x32_bf16 v[78:81], v[238:241], v[218:221], v[78:81]
	v_mfma_f32_16x16x32_bf16 v[74:77], v[242:245], v[218:221], v[74:77]
	v_mfma_f32_16x16x32_bf16 v[70:73], v[246:249], v[218:221], v[70:73]
	v_mfma_f32_16x16x32_bf16 v[66:69], v[250:253], v[218:221], v[66:69]
	ds_read_b128 v[218:221], v93 offset:0
	ds_read_b128 v[142:145], v141 offset:19456
	s_mov_b32 m0, s49
	s_nop 0
	global_load_lds_dwordx4 v88, s[30:31]
	v_mfma_f32_16x16x32_bf16 v[62:65], v[238:241], v[222:225], v[62:65]
	v_mfma_f32_16x16x32_bf16 v[58:61], v[242:245], v[222:225], v[58:61]
	v_mfma_f32_16x16x32_bf16 v[54:57], v[246:249], v[222:225], v[54:57]
	v_mfma_f32_16x16x32_bf16 v[50:53], v[250:253], v[222:225], v[50:53]
	ds_read_b128 v[222:225], v93 offset:2048
	ds_read_b128 v[146:149], v141 offset:21504
	s_add_i32 m0, s49, 0x2000
	s_nop 0
	global_load_lds_dwordx4 v90, s[30:31]
	v_mfma_f32_16x16x32_bf16 v[46:49], v[238:241], v[226:229], v[46:49]
	v_mfma_f32_16x16x32_bf16 v[42:45], v[242:245], v[226:229], v[42:45]
	v_mfma_f32_16x16x32_bf16 v[38:41], v[246:249], v[226:229], v[38:41]
	v_mfma_f32_16x16x32_bf16 v[34:37], v[250:253], v[226:229], v[34:37]
	ds_read_b128 v[226:229], v93 offset:4096
	ds_read_b128 v[156:159], v141 offset:23552
	s_add_i32 m0, s49, 0x4000
	s_nop 0
	global_load_lds_dwordx4 v92, s[30:31]
	v_mfma_f32_16x16x32_bf16 v[18:21], v[238:241], v[230:233], v[18:21]
	v_mfma_f32_16x16x32_bf16 v[22:25], v[242:245], v[230:233], v[22:25]
	v_mfma_f32_16x16x32_bf16 v[26:29], v[246:249], v[230:233], v[26:29]
	v_mfma_f32_16x16x32_bf16 v[30:33], v[250:253], v[230:233], v[30:33]
	ds_read_b128 v[230:233], v93 offset:6144
	ds_read_b128 v[160:163], v141 offset:25600
	s_add_i32 m0, s49, 0x6000
	s_nop 0
	global_load_lds_dwordx4 v94, s[30:31]
	v_mfma_f32_16x16x32_bf16 v[2:5], v[238:241], v[234:237], v[2:5]
	v_mfma_f32_16x16x32_bf16 v[6:9], v[242:245], v[234:237], v[6:9]
	v_mfma_f32_16x16x32_bf16 v[10:13], v[246:249], v[234:237], v[10:13]
	v_mfma_f32_16x16x32_bf16 v[14:17], v[250:253], v[234:237], v[14:17]
	ds_read_b128 v[234:237], v93 offset:8192
	s_add_i32 m0, s49, 0x8000
	s_nop 0
	global_load_lds_dwordx4 v96, s[30:31]
	s_waitcnt lgkmcnt(0)
	v_mfma_f32_16x16x32_bf16 v[78:81], v[142:145], v[218:221], v[78:81]
	v_mfma_f32_16x16x32_bf16 v[74:77], v[146:149], v[218:221], v[74:77]
	v_mfma_f32_16x16x32_bf16 v[70:73], v[156:159], v[218:221], v[70:73]
	v_mfma_f32_16x16x32_bf16 v[66:69], v[160:163], v[218:221], v[66:69]
	s_add_i32 s51, s51, 1
	s_and_b32 s54, s51, 7
	s_cmp_eq_u32 s54, 0
	s_cselect_b32 s44, s34, s35
	s_cselect_b32 s45, -1, 0
	v_lshl_add_u64 v[132:133], v[132:133], 0, s[44:45]
	global_load_dwordx2 v[186:187], v[132:133], off
	v_lshl_add_u64 v[180:181], v[132:133], 0, s[24:25]
	global_load_dwordx2 v[188:189], v[180:181], off
	v_mfma_f32_16x16x32_bf16 v[62:65], v[142:145], v[222:225], v[62:65]
	v_mfma_f32_16x16x32_bf16 v[58:61], v[146:149], v[222:225], v[58:61]
	v_mfma_f32_16x16x32_bf16 v[54:57], v[156:159], v[222:225], v[54:57]
	v_mfma_f32_16x16x32_bf16 v[50:53], v[160:163], v[222:225], v[50:53]
	v_lshl_add_u64 v[180:181], v[132:133], 0, s[26:27]
	global_load_dwordx2 v[190:191], v[180:181], off
	v_lshl_add_u64 v[180:181], v[132:133], 0, s[28:29]
	global_load_dwordx2 v[192:193], v[180:181], off
	v_mfma_f32_16x16x32_bf16 v[46:49], v[142:145], v[226:229], v[46:49]
	v_mfma_f32_16x16x32_bf16 v[42:45], v[146:149], v[226:229], v[42:45]
	v_mfma_f32_16x16x32_bf16 v[38:41], v[156:159], v[226:229], v[38:41]
	v_mfma_f32_16x16x32_bf16 v[34:37], v[160:163], v[226:229], v[34:37]
	v_lshl_add_u64 v[180:181], v[132:133], 0, s[36:37]
	global_load_dwordx2 v[194:195], v[180:181], off
	v_lshl_add_u64 v[180:181], v[132:133], 0, s[38:39]
	global_load_dwordx2 v[196:197], v[180:181], off
	v_mfma_f32_16x16x32_bf16 v[18:21], v[142:145], v[230:233], v[18:21]
	v_mfma_f32_16x16x32_bf16 v[22:25], v[146:149], v[230:233], v[22:25]
	v_mfma_f32_16x16x32_bf16 v[26:29], v[156:159], v[230:233], v[26:29]
	v_mfma_f32_16x16x32_bf16 v[30:33], v[160:163], v[230:233], v[30:33]
	v_lshl_add_u64 v[180:181], v[132:133], 0, s[40:41]
	global_load_dwordx2 v[198:199], v[180:181], off
	v_lshl_add_u64 v[180:181], v[132:133], 0, s[42:43]
	global_load_dwordx2 v[200:201], v[180:181], off
	v_mfma_f32_16x16x32_bf16 v[2:5], v[142:145], v[234:237], v[2:5]
	v_mfma_f32_16x16x32_bf16 v[6:9], v[146:149], v[234:237], v[6:9]
	v_mfma_f32_16x16x32_bf16 v[10:13], v[156:159], v[234:237], v[10:13]
	v_mfma_f32_16x16x32_bf16 v[14:17], v[160:163], v[234:237], v[14:17]
	s_waitcnt vmcnt(21)
	s_waitcnt lgkmcnt(0)
	s_barrier
; #define MD_GLDS_A(buf, tau) do { _Pragma("unroll") for (int i = 0; i < 5; ++i) if (amask & (1u << i)) \
;         __builtin_amdgcn_global_load_lds((const unsigned*)((const char*)HIDp + aoff[i] + (size_t)((tau) & 7) * 128), (PG8_LAS unsigned*)(MD_SA(buf) + wid * 1024 + i * 8192), 16, 0, 0); } while (0)
; #define MD_B_ISSUE(sb, tau) do { const char* kb_ = Bb + (size_t)((tau) >> 3) * 512 + (size_t)((tau) & 7) * (64 * (size_t)RB); _Pragma("unroll") for (int j = 0; j < 8; ++j) { const char* p_ = kb_ + (size_t)j * RB; \
;         asm volatile("global_load_dwordx2 %0, %1, off" : "=&v"(sb[j]) : "v"(p_) : "memory"); } } while (0)
; #define MD_B_WAIT(sb, N) asm volatile("s_waitcnt vmcnt(%8)" : "+v"(sb[0]), "+v"(sb[1]), "+v"(sb[2]), "+v"(sb[3]), "+v"(sb[4]), "+v"(sb[5]), "+v"(sb[6]), "+v"(sb[7]) : "n"(N) : "memory")
; #define MD_END(last) do { if (last) asm volatile("s_waitcnt vmcnt(0)" ::: "memory"); else asm volatile("s_waitcnt vmcnt(8)" ::: "memory"); \
;         asm volatile("s_waitcnt lgkmcnt(0)" ::: "memory"); __builtin_amdgcn_s_barrier(); asm volatile("" ::: "memory"); } while (0)
; __device__ __forceinline__ void moe_down_stream(PG8_LAS unsigned char* lds, int e, int cb0, int slot0, int nv, const bf16_t* HIDp, const float* Wd, bf16_t* Y, const float* slot_w, const int* slot_dst) {
;     ...
;     for (int t = 0; t < NT; t += 2) {
;         if (t + 2 < NT) MD_B_WAIT(s1, 8); else MD_B_WAIT(s1, 0);
;         MD_B_WRITE(s1, 1); __builtin_amdgcn_sched_barrier(0); MD_GLDS_A(1, t + 1); __builtin_amdgcn_sched_barrier(0);
;         if (t + 3 < NT) MD_B_ISSUE(s1, t + 3);
;         MD_COMPUTE(0);
;         MD_END(t + 3 >= NT);
;         if (t + 2 < NT) { MD_B_WAIT(s0, 8); MD_B_WRITE(s0, 0); __builtin_amdgcn_sched_barrier(0); MD_GLDS_A(0, t + 2); __builtin_amdgcn_sched_barrier(0); }
;         if (t + 4 < NT) MD_B_ISSUE(s0, t + 4);
;         MD_COMPUTE(1);
;         MD_END(t + 4 >= NT);
	s_mov_b32 s49, s46
	s_mov_b32 s46, s47
	s_mov_b32 s47, s48
	s_mov_b32 s48, s49
	s_add_i32 s50, s50, 1
	v_cvt_pk_bf16_f32 v172, v202, v204
	v_cvt_pk_bf16_f32 v173, v206, v208
	v_cvt_pk_bf16_f32 v174, v210, v212
	v_cvt_pk_bf16_f32 v175, v214, v216
	v_cvt_pk_bf16_f32 v176, v203, v205
	v_cvt_pk_bf16_f32 v177, v207, v209
	v_cvt_pk_bf16_f32 v178, v211, v213
	v_cvt_pk_bf16_f32 v179, v215, v217
	ds_write_b128 v95, v[172:175] offset:19456
	ds_write_b128 v95, v[176:179] offset:19584
	v_add_u32_e32 v91, s46, v135
	v_add_u32_e32 v93, s46, v137
	ds_read_b128 v[238:241], v139 offset:0
	ds_read_b128 v[242:245], v139 offset:2048
	ds_read_b128 v[246:249], v139 offset:4096
	ds_read_b128 v[250:253], v139 offset:6144
	ds_read_b128 v[218:221], v91 offset:0
	ds_read_b128 v[222:225], v91 offset:2048
	ds_read_b128 v[226:229], v91 offset:4096
	ds_read_b128 v[230:233], v91 offset:6144
	ds_read_b128 v[234:237], v91 offset:8192
	s_add_i32 s49, s48, s74
	s_add_i32 s52, s52, 1
	s_and_b32 s54, s52, 7
	s_cmp_eq_u32 s54, 0
	s_cselect_b32 s54, s53, s32
	s_cselect_b32 s55, -1, 0
	s_add_u32 s30, s30, s54
	s_addc_u32 s31, s31, s55
	s_waitcnt lgkmcnt(0)
	v_mfma_f32_16x16x32_bf16 v[78:81], v[238:241], v[218:221], v[78:81]
	v_mfma_f32_16x16x32_bf16 v[74:77], v[242:245], v[218:221], v[74:77]
	v_mfma_f32_16x16x32_bf16 v[70:73], v[246:249], v[218:221], v[70:73]
	v_mfma_f32_16x16x32_bf16 v[66:69], v[250:253], v[218:221], v[66:69]
	ds_read_b128 v[218:221], v93 offset:0
	ds_read_b128 v[142:145], v141 offset:0
	s_mov_b32 m0, s49
	s_nop 0
	global_load_lds_dwordx4 v88, s[30:31]
	v_mfma_f32_16x16x32_bf16 v[62:65], v[238:241], v[222:225], v[62:65]
	v_mfma_f32_16x16x32_bf16 v[58:61], v[242:245], v[222:225], v[58:61]
	v_mfma_f32_16x16x32_bf16 v[54:57], v[246:249], v[222:225], v[54:57]
	v_mfma_f32_16x16x32_bf16 v[50:53], v[250:253], v[222:225], v[50:53]
	ds_read_b128 v[222:225], v93 offset:2048
	ds_read_b128 v[146:149], v141 offset:2048
	s_add_i32 m0, s49, 0x2000
	s_nop 0
	global_load_lds_dwordx4 v90, s[30:31]
	v_mfma_f32_16x16x32_bf16 v[46:49], v[238:241], v[226:229], v[46:49]
	v_mfma_f32_16x16x32_bf16 v[42:45], v[242:245], v[226:229], v[42:45]
	v_mfma_f32_16x16x32_bf16 v[38:41], v[246:249], v[226:229], v[38:41]
	v_mfma_f32_16x16x32_bf16 v[34:37], v[250:253], v[226:229], v[34:37]
	ds_read_b128 v[226:229], v93 offset:4096
	ds_read_b128 v[156:159], v141 offset:4096
	s_add_i32 m0, s49, 0x4000
	s_nop 0
	global_load_lds_dwordx4 v92, s[30:31]
	v_mfma_f32_16x16x32_bf16 v[18:21], v[238:241], v[230:233], v[18:21]
	v_mfma_f32_16x16x32_bf16 v[22:25], v[242:245], v[230:233], v[22:25]
	v_mfma_f32_16x16x32_bf16 v[26:29], v[246:249], v[230:233], v[26:29]
	v_mfma_f32_16x16x32_bf16 v[30:33], v[250:253], v[230:233], v[30:33]
	ds_read_b128 v[230:233], v93 offset:6144
	ds_read_b128 v[160:163], v141 offset:6144
	s_add_i32 m0, s49, 0x6000
	s_nop 0
	global_load_lds_dwordx4 v94, s[30:31]
	v_mfma_f32_16x16x32_bf16 v[2:5], v[238:241], v[234:237], v[2:5]
	v_mfma_f32_16x16x32_bf16 v[6:9], v[242:245], v[234:237], v[6:9]
	v_mfma_f32_16x16x32_bf16 v[10:13], v[246:249], v[234:237], v[10:13]
	v_mfma_f32_16x16x32_bf16 v[14:17], v[250:253], v[234:237], v[14:17]
	ds_read_b128 v[234:237], v93 offset:8192
	s_add_i32 m0, s49, 0x8000
	s_nop 0
	global_load_lds_dwordx4 v96, s[30:31]
	s_waitcnt lgkmcnt(0)
	v_mfma_f32_16x16x32_bf16 v[78:81], v[142:145], v[218:221], v[78:81]
	v_mfma_f32_16x16x32_bf16 v[74:77], v[146:149], v[218:221], v[74:77]
	v_mfma_f32_16x16x32_bf16 v[70:73], v[156:159], v[218:221], v[70:73]
	v_mfma_f32_16x16x32_bf16 v[66:69], v[160:163], v[218:221], v[66:69]
	s_add_i32 s51, s51, 1
	s_and_b32 s54, s51, 7
	s_cmp_eq_u32 s54, 0
	s_cselect_b32 s44, s34, s35
	s_cselect_b32 s45, -1, 0
	v_lshl_add_u64 v[132:133], v[132:133], 0, s[44:45]
	global_load_dwordx2 v[202:203], v[132:133], off
	v_lshl_add_u64 v[180:181], v[132:133], 0, s[24:25]
	global_load_dwordx2 v[204:205], v[180:181], off
	v_mfma_f32_16x16x32_bf16 v[62:65], v[142:145], v[222:225], v[62:65]
	v_mfma_f32_16x16x32_bf16 v[58:61], v[146:149], v[222:225], v[58:61]
	v_mfma_f32_16x16x32_bf16 v[54:57], v[156:159], v[222:225], v[54:57]
	v_mfma_f32_16x16x32_bf16 v[50:53], v[160:163], v[222:225], v[50:53]
	v_lshl_add_u64 v[180:181], v[132:133], 0, s[26:27]
	global_load_dwordx2 v[206:207], v[180:181], off
	v_lshl_add_u64 v[180:181], v[132:133], 0, s[28:29]
	global_load_dwordx2 v[208:209], v[180:181], off
	v_mfma_f32_16x16x32_bf16 v[46:49], v[142:145], v[226:229], v[46:49]
	v_mfma_f32_16x16x32_bf16 v[42:45], v[146:149], v[226:229], v[42:45]
	v_mfma_f32_16x16x32_bf16 v[38:41], v[156:159], v[226:229], v[38:41]
	v_mfma_f32_16x16x32_bf16 v[34:37], v[160:163], v[226:229], v[34:37]
	v_lshl_add_u64 v[180:181], v[132:133], 0, s[36:37]
	global_load_dwordx2 v[210:211], v[180:181], off
	v_lshl_add_u64 v[180:181], v[132:133], 0, s[38:39]
	global_load_dwordx2 v[212:213], v[180:181], off
	v_mfma_f32_16x16x32_bf16 v[18:21], v[142:145], v[230:233], v[18:21]
	v_mfma_f32_16x16x32_bf16 v[22:25], v[146:149], v[230:233], v[22:25]
	v_mfma_f32_16x16x32_bf16 v[26:29], v[156:159], v[230:233], v[26:29]
	v_mfma_f32_16x16x32_bf16 v[30:33], v[160:163], v[230:233], v[30:33]
	v_lshl_add_u64 v[180:181], v[132:133], 0, s[40:41]
	global_load_dwordx2 v[214:215], v[180:181], off
	v_lshl_add_u64 v[180:181], v[132:133], 0, s[42:43]
	global_load_dwordx2 v[216:217], v[180:181], off
	v_mfma_f32_16x16x32_bf16 v[2:5], v[142:145], v[234:237], v[2:5]
	v_mfma_f32_16x16x32_bf16 v[6:9], v[146:149], v[234:237], v[6:9]
	v_mfma_f32_16x16x32_bf16 v[10:13], v[156:159], v[234:237], v[10:13]
	v_mfma_f32_16x16x32_bf16 v[14:17], v[160:163], v[234:237], v[14:17]
	s_waitcnt vmcnt(21)
	s_waitcnt lgkmcnt(0)
	s_barrier
; #define MD_GLDS_A(buf, tau) do { _Pragma("unroll") for (int i = 0; i < 5; ++i) if (amask & (1u << i)) \
;         __builtin_amdgcn_global_load_lds((const unsigned*)((const char*)HIDp + aoff[i] + (size_t)((tau) & 7) * 128), (PG8_LAS unsigned*)(MD_SA(buf) + wid * 1024 + i * 8192), 16, 0, 0); } while (0)
; #define MD_B_ISSUE(sb, tau) do { const char* kb_ = Bb + (size_t)((tau) >> 3) * 512 + (size_t)((tau) & 7) * (64 * (size_t)RB); _Pragma("unroll") for (int j = 0; j < 8; ++j) { const char* p_ = kb_ + (size_t)j * RB; \
;         asm volatile("global_load_dwordx2 %0, %1, off" : "=&v"(sb[j]) : "v"(p_) : "memory"); } } while (0)
; #define MD_B_WAIT(sb, N) asm volatile("s_waitcnt vmcnt(%8)" : "+v"(sb[0]), "+v"(sb[1]), "+v"(sb[2]), "+v"(sb[3]), "+v"(sb[4]), "+v"(sb[5]), "+v"(sb[6]), "+v"(sb[7]) : "n"(N) : "memory")
; #define MD_END(last) do { if (last) asm volatile("s_waitcnt vmcnt(0)" ::: "memory"); else asm volatile("s_waitcnt vmcnt(8)" ::: "memory"); \
;         asm volatile("s_waitcnt lgkmcnt(0)" ::: "memory"); __builtin_amdgcn_s_barrier(); asm volatile("" ::: "memory"); } while (0)
; __device__ __forceinline__ void moe_down_stream(PG8_LAS unsigned char* lds, int e, int cb0, int slot0, int nv, const bf16_t* HIDp, const float* Wd, bf16_t* Y, const float* slot_w, const int* slot_dst) {
;     ...
;     for (int t = 0; t < NT; t += 2) {
;         if (t + 2 < NT) MD_B_WAIT(s1, 8); else MD_B_WAIT(s1, 0);
;         MD_B_WRITE(s1, 1); __builtin_amdgcn_sched_barrier(0); MD_GLDS_A(1, t + 1); __builtin_amdgcn_sched_barrier(0);
;         if (t + 3 < NT) MD_B_ISSUE(s1, t + 3);
;         MD_COMPUTE(0);
;         MD_END(t + 3 >= NT);
;         if (t + 2 < NT) { MD_B_WAIT(s0, 8); MD_B_WRITE(s0, 0); __builtin_amdgcn_sched_barrier(0); MD_GLDS_A(0, t + 2); __builtin_amdgcn_sched_barrier(0); }
;         if (t + 4 < NT) MD_B_ISSUE(s0, t + 4);
;         MD_COMPUTE(1);
;         MD_END(t + 4 >= NT);
	s_mov_b32 s49, s46
	s_mov_b32 s46, s47
	s_mov_b32 s47, s48
	s_mov_b32 s48, s49
	s_add_i32 s50, s50, 1
	v_cvt_pk_bf16_f32 v172, v98, v100
	v_cvt_pk_bf16_f32 v173, v102, v104
	v_cvt_pk_bf16_f32 v174, v106, v108
	v_cvt_pk_bf16_f32 v175, v110, v112
	v_cvt_pk_bf16_f32 v176, v99, v101
	v_cvt_pk_bf16_f32 v177, v103, v105
	v_cvt_pk_bf16_f32 v178, v107, v109
	v_cvt_pk_bf16_f32 v179, v111, v113
	ds_write_b128 v95, v[172:175] offset:0
	ds_write_b128 v95, v[176:179] offset:128
	v_add_u32_e32 v91, s46, v135
	v_add_u32_e32 v93, s46, v137
	ds_read_b128 v[238:241], v139 offset:19456
	ds_read_b128 v[242:245], v139 offset:21504
	ds_read_b128 v[246:249], v139 offset:23552
	ds_read_b128 v[250:253], v139 offset:25600
	ds_read_b128 v[218:221], v91 offset:0
	ds_read_b128 v[222:225], v91 offset:2048
	ds_read_b128 v[226:229], v91 offset:4096
	ds_read_b128 v[230:233], v91 offset:6144
	ds_read_b128 v[234:237], v91 offset:8192
	s_add_i32 s49, s48, s74
	s_add_i32 s52, s52, 1
	s_and_b32 s54, s52, 7
	s_cmp_eq_u32 s54, 0
	s_cselect_b32 s54, s53, s32
	s_cselect_b32 s55, -1, 0
	s_add_u32 s30, s30, s54
	s_addc_u32 s31, s31, s55
	s_waitcnt lgkmcnt(0)
	v_mfma_f32_16x16x32_bf16 v[78:81], v[238:241], v[218:221], v[78:81]
	v_mfma_f32_16x16x32_bf16 v[74:77], v[242:245], v[218:221], v[74:77]
	v_mfma_f32_16x16x32_bf16 v[70:73], v[246:249], v[218:221], v[70:73]
	v_mfma_f32_16x16x32_bf16 v[66:69], v[250:253], v[218:221], v[66:69]
	ds_read_b128 v[218:221], v93 offset:0
	ds_read_b128 v[142:145], v141 offset:19456
	s_mov_b32 m0, s49
	s_nop 0
	global_load_lds_dwordx4 v88, s[30:31]
	v_mfma_f32_16x16x32_bf16 v[62:65], v[238:241], v[222:225], v[62:65]
	v_mfma_f32_16x16x32_bf16 v[58:61], v[242:245], v[222:225], v[58:61]
	v_mfma_f32_16x16x32_bf16 v[54:57], v[246:249], v[222:225], v[54:57]
	v_mfma_f32_16x16x32_bf16 v[50:53], v[250:253], v[222:225], v[50:53]
	ds_read_b128 v[222:225], v93 offset:2048
	ds_read_b128 v[146:149], v141 offset:21504
	s_add_i32 m0, s49, 0x2000
	s_nop 0
	global_load_lds_dwordx4 v90, s[30:31]
	v_mfma_f32_16x16x32_bf16 v[46:49], v[238:241], v[226:229], v[46:49]
	v_mfma_f32_16x16x32_bf16 v[42:45], v[242:245], v[226:229], v[42:45]
	v_mfma_f32_16x16x32_bf16 v[38:41], v[246:249], v[226:229], v[38:41]
	v_mfma_f32_16x16x32_bf16 v[34:37], v[250:253], v[226:229], v[34:37]
	ds_read_b128 v[226:229], v93 offset:4096
	ds_read_b128 v[156:159], v141 offset:23552
	s_add_i32 m0, s49, 0x4000
	s_nop 0
	global_load_lds_dwordx4 v92, s[30:31]
	v_mfma_f32_16x16x32_bf16 v[18:21], v[238:241], v[230:233], v[18:21]
	v_mfma_f32_16x16x32_bf16 v[22:25], v[242:245], v[230:233], v[22:25]
	v_mfma_f32_16x16x32_bf16 v[26:29], v[246:249], v[230:233], v[26:29]
	v_mfma_f32_16x16x32_bf16 v[30:33], v[250:253], v[230:233], v[30:33]
	ds_read_b128 v[230:233], v93 offset:6144
	ds_read_b128 v[160:163], v141 offset:25600
	s_add_i32 m0, s49, 0x6000
	s_nop 0
	global_load_lds_dwordx4 v94, s[30:31]
	v_mfma_f32_16x16x32_bf16 v[2:5], v[238:241], v[234:237], v[2:5]
	v_mfma_f32_16x16x32_bf16 v[6:9], v[242:245], v[234:237], v[6:9]
	v_mfma_f32_16x16x32_bf16 v[10:13], v[246:249], v[234:237], v[10:13]
	v_mfma_f32_16x16x32_bf16 v[14:17], v[250:253], v[234:237], v[14:17]
	ds_read_b128 v[234:237], v93 offset:8192
	s_add_i32 m0, s49, 0x8000
	s_nop 0
	global_load_lds_dwordx4 v96, s[30:31]
	s_waitcnt lgkmcnt(0)
	v_mfma_f32_16x16x32_bf16 v[78:81], v[142:145], v[218:221], v[78:81]
	v_mfma_f32_16x16x32_bf16 v[74:77], v[146:149], v[218:221], v[74:77]
	v_mfma_f32_16x16x32_bf16 v[70:73], v[156:159], v[218:221], v[70:73]
	v_mfma_f32_16x16x32_bf16 v[66:69], v[160:163], v[218:221], v[66:69]
	s_add_i32 s51, s51, 1
	s_and_b32 s54, s51, 7
	s_cmp_eq_u32 s54, 0
	s_cselect_b32 s44, s34, s35
	s_cselect_b32 s45, -1, 0
	v_lshl_add_u64 v[132:133], v[132:133], 0, s[44:45]
	global_load_dwordx2 v[98:99], v[132:133], off
	v_lshl_add_u64 v[180:181], v[132:133], 0, s[24:25]
	global_load_dwordx2 v[100:101], v[180:181], off
	v_mfma_f32_16x16x32_bf16 v[62:65], v[142:145], v[222:225], v[62:65]
	v_mfma_f32_16x16x32_bf16 v[58:61], v[146:149], v[222:225], v[58:61]
	v_mfma_f32_16x16x32_bf16 v[54:57], v[156:159], v[222:225], v[54:57]
	v_mfma_f32_16x16x32_bf16 v[50:53], v[160:163], v[222:225], v[50:53]
	v_lshl_add_u64 v[180:181], v[132:133], 0, s[26:27]
	global_load_dwordx2 v[102:103], v[180:181], off
	v_lshl_add_u64 v[180:181], v[132:133], 0, s[28:29]
	global_load_dwordx2 v[104:105], v[180:181], off
	v_mfma_f32_16x16x32_bf16 v[46:49], v[142:145], v[226:229], v[46:49]
	v_mfma_f32_16x16x32_bf16 v[42:45], v[146:149], v[226:229], v[42:45]
	v_mfma_f32_16x16x32_bf16 v[38:41], v[156:159], v[226:229], v[38:41]
	v_mfma_f32_16x16x32_bf16 v[34:37], v[160:163], v[226:229], v[34:37]
	v_lshl_add_u64 v[180:181], v[132:133], 0, s[36:37]
	global_load_dwordx2 v[106:107], v[180:181], off
	v_lshl_add_u64 v[180:181], v[132:133], 0, s[38:39]
	global_load_dwordx2 v[108:109], v[180:181], off
	v_mfma_f32_16x16x32_bf16 v[18:21], v[142:145], v[230:233], v[18:21]
	v_mfma_f32_16x16x32_bf16 v[22:25], v[146:149], v[230:233], v[22:25]
	v_mfma_f32_16x16x32_bf16 v[26:29], v[156:159], v[230:233], v[26:29]
	v_mfma_f32_16x16x32_bf16 v[30:33], v[160:163], v[230:233], v[30:33]
	v_lshl_add_u64 v[180:181], v[132:133], 0, s[40:41]
	global_load_dwordx2 v[110:111], v[180:181], off
	v_lshl_add_u64 v[180:181], v[132:133], 0, s[42:43]
	global_load_dwordx2 v[112:113], v[180:181], off
	v_mfma_f32_16x16x32_bf16 v[2:5], v[142:145], v[234:237], v[2:5]
	v_mfma_f32_16x16x32_bf16 v[6:9], v[146:149], v[234:237], v[6:9]
	v_mfma_f32_16x16x32_bf16 v[10:13], v[156:159], v[234:237], v[10:13]
	v_mfma_f32_16x16x32_bf16 v[14:17], v[160:163], v[234:237], v[14:17]
	s_waitcnt vmcnt(21)
	s_waitcnt lgkmcnt(0)
	s_barrier
; #define PG8_LAS __attribute__((address_space(3)))
; __device__ __forceinline__ unsigned cvtpk(float lo, float hi) { f32x2 v = {lo, hi}; bf16x2_t b = __builtin_convertvector(v, bf16x2_t); return __builtin_bit_cast(unsigned, b); }
; __device__ __forceinline__ void moe_down_stream(PG8_LAS unsigned char* lds, int e, int cb0, int slot0, int nv, const bf16_t* HIDp, const float* Wd, bf16_t* Y, const float* slot_w, const int* slot_dst) {
;     ...
;         if (((t + 1) & 7) == 7) {
;             const int cb = cb0 + ((t + 1) >> 3);
; #pragma unroll
;             for (int m = 0; m < DNM; ++m) {
;                 const float w_ = lw[4 * (16 * m + fr) + wr];
; #pragma unroll
;                 for (int p = 0; p < 2; ++p) { const f32x4 v0 = acc[m][2 * p] * w_, v1 = acc[m][2 * p + 1] * w_; u32x4 w; w.x = cvtpk(v0[0], v0[1]); w.y = cvtpk(v0[2], v0[3]); w.z = cvtpk(v1[0], v1[1]); w.w = cvtpk(v1[2], v1[3]);
;                     *(PG8_LAS u32x4*)(stg + fr * 128 + (((4 * p + fq) ^ (fr & 7)) * 16)) = w; }
; #pragma unroll
;                 for (int hh = 0; hh < 2; ++hh) { const int r = (lane >> 3) + 8 * hh, cc = lane & 7; const u32x4 d = *(const PG8_LAS u32x4*)(stg + r * 128 + ((cc ^ (r & 7)) * 16)); const int dst_ = ldst[4 * (16 * m + r) + wr];
;                     if (dst_ >= 0) *(u32x4*)(Y + (size_t)dst_ * D + 128 * cb + 64 * wc + 8 * cc) = d; }
; #pragma unroll
;                 for (int n = 0; n < 4; ++n) acc[m][n] = (f32x4){0.f, 0.f, 0.f, 0.f}; } }
	s_mov_b32 s49, s46
	s_mov_b32 s46, s47
	s_mov_b32 s47, s48
	s_mov_b32 s48, s49
	s_add_i32 s50, s50, 1
	s_and_b32 s54, s50, 7
	s_cmp_lg_u32 s54, 0
	s_cbranch_scc1 .Lmd_noepi_X
	s_add_i32 s54, s48, s74
	v_add_u32_e32 v164, s54, v84
	v_add_u32_e32 v165, s54, v85
	ds_read_b32 v150, v82 offset:0
	ds_read_b32 v151, v83 offset:0
	ds_read_b32 v166, v83 offset:128
	s_waitcnt lgkmcnt(2)
	v_mul_f32_e32 v78, v150, v78
	v_mul_f32_e32 v79, v150, v79
	v_mul_f32_e32 v80, v150, v80
	v_mul_f32_e32 v81, v150, v81
	v_mul_f32_e32 v74, v150, v74
	v_mul_f32_e32 v75, v150, v75
	v_mul_f32_e32 v76, v150, v76
	v_mul_f32_e32 v77, v150, v77
	v_cvt_pk_bf16_f32 v182, v78, v79
	v_cvt_pk_bf16_f32 v183, v80, v81
	v_cvt_pk_bf16_f32 v184, v74, v75
	v_cvt_pk_bf16_f32 v185, v76, v77
	ds_write_b128 v164, v[182:185]
	v_mul_f32_e32 v70, v150, v70
	v_mul_f32_e32 v71, v150, v71
	v_mul_f32_e32 v72, v150, v72
	v_mul_f32_e32 v73, v150, v73
	v_mul_f32_e32 v66, v150, v66
	v_mul_f32_e32 v67, v150, v67
	v_mul_f32_e32 v68, v150, v68
	v_mul_f32_e32 v69, v150, v69
	v_cvt_pk_bf16_f32 v182, v70, v71
	v_cvt_pk_bf16_f32 v183, v72, v73
	v_cvt_pk_bf16_f32 v184, v66, v67
	v_cvt_pk_bf16_f32 v185, v68, v69
	v_xor_b32_e32 v167, 64, v164
	ds_write_b128 v167, v[182:185]
	v_mov_b32_e32 v78, 0
	v_mov_b32_e32 v74, 0
	v_mov_b32_e32 v70, 0
	v_mov_b32_e32 v66, 0
	v_mov_b32_e32 v79, 0
	v_mov_b32_e32 v75, 0
	v_mov_b32_e32 v71, 0
	v_mov_b32_e32 v67, 0
	v_mov_b32_e32 v80, 0
	v_mov_b32_e32 v76, 0
	v_mov_b32_e32 v72, 0
	v_mov_b32_e32 v68, 0
	v_mov_b32_e32 v81, 0
	v_mov_b32_e32 v77, 0
	v_mov_b32_e32 v73, 0
	v_mov_b32_e32 v69, 0
	ds_read_b128 v[182:185], v165 offset:0
	v_cmp_lt_i32_e32 vcc, -1, v151
	v_lshlrev_b32_e32 v148, 13, v151
	v_mov_b32_e32 v149, 0
	v_lshl_add_u64 v[148:149], v[148:149], 0, v[86:87]
	v_cndmask_b32_e32 v148, v168, v148, vcc
	v_cndmask_b32_e32 v149, v169, v149, vcc
	s_waitcnt lgkmcnt(0)
	global_store_dwordx4 v[148:149], v[182:185], off
	ds_read_b128 v[182:185], v165 offset:8192
	v_cmp_lt_i32_e32 vcc, -1, v166
	v_lshlrev_b32_e32 v148, 13, v166
	v_mov_b32_e32 v149, 0
	v_lshl_add_u64 v[148:149], v[148:149], 0, v[86:87]
	v_cndmask_b32_e32 v148, v168, v148, vcc
	v_cndmask_b32_e32 v149, v169, v149, vcc
	s_waitcnt lgkmcnt(0)
	global_store_dwordx4 v[148:149], v[182:185], off
	ds_read_b32 v150, v82 offset:256
	ds_read_b32 v151, v83 offset:256
	ds_read_b32 v166, v83 offset:384
	s_waitcnt lgkmcnt(2)
	v_mul_f32_e32 v62, v150, v62
	v_mul_f32_e32 v63, v150, v63
	v_mul_f32_e32 v64, v150, v64
	v_mul_f32_e32 v65, v150, v65
	v_mul_f32_e32 v58, v150, v58
	v_mul_f32_e32 v59, v150, v59
	v_mul_f32_e32 v60, v150, v60
	v_mul_f32_e32 v61, v150, v61
	v_cvt_pk_bf16_f32 v182, v62, v63
	v_cvt_pk_bf16_f32 v183, v64, v65
	v_cvt_pk_bf16_f32 v184, v58, v59
	v_cvt_pk_bf16_f32 v185, v60, v61
	ds_write_b128 v164, v[182:185]
	v_mul_f32_e32 v54, v150, v54
	v_mul_f32_e32 v55, v150, v55
	v_mul_f32_e32 v56, v150, v56
	v_mul_f32_e32 v57, v150, v57
	v_mul_f32_e32 v50, v150, v50
	v_mul_f32_e32 v51, v150, v51
	v_mul_f32_e32 v52, v150, v52
	v_mul_f32_e32 v53, v150, v53
	v_cvt_pk_bf16_f32 v182, v54, v55
	v_cvt_pk_bf16_f32 v183, v56, v57
	v_cvt_pk_bf16_f32 v184, v50, v51
	v_cvt_pk_bf16_f32 v185, v52, v53
	v_xor_b32_e32 v167, 64, v164
	ds_write_b128 v167, v[182:185]
	v_mov_b32_e32 v62, 0
	v_mov_b32_e32 v58, 0
	v_mov_b32_e32 v54, 0
	v_mov_b32_e32 v50, 0
	v_mov_b32_e32 v63, 0
	v_mov_b32_e32 v59, 0
	v_mov_b32_e32 v55, 0
	v_mov_b32_e32 v51, 0
	v_mov_b32_e32 v64, 0
	v_mov_b32_e32 v60, 0
	v_mov_b32_e32 v56, 0
	v_mov_b32_e32 v52, 0
	v_mov_b32_e32 v65, 0
	v_mov_b32_e32 v61, 0
	v_mov_b32_e32 v57, 0
	v_mov_b32_e32 v53, 0
	ds_read_b128 v[182:185], v165 offset:0
	v_cmp_lt_i32_e32 vcc, -1, v151
	v_lshlrev_b32_e32 v148, 13, v151
	v_mov_b32_e32 v149, 0
	v_lshl_add_u64 v[148:149], v[148:149], 0, v[86:87]
	v_cndmask_b32_e32 v148, v168, v148, vcc
	v_cndmask_b32_e32 v149, v169, v149, vcc
	s_waitcnt lgkmcnt(0)
	global_store_dwordx4 v[148:149], v[182:185], off
	ds_read_b128 v[182:185], v165 offset:8192
	v_cmp_lt_i32_e32 vcc, -1, v166
	v_lshlrev_b32_e32 v148, 13, v166
	v_mov_b32_e32 v149, 0
	v_lshl_add_u64 v[148:149], v[148:149], 0, v[86:87]
	v_cndmask_b32_e32 v148, v168, v148, vcc
	v_cndmask_b32_e32 v149, v169, v149, vcc
	s_waitcnt lgkmcnt(0)
	global_store_dwordx4 v[148:149], v[182:185], off
	ds_read_b32 v150, v82 offset:512
	ds_read_b32 v151, v83 offset:512
	ds_read_b32 v166, v83 offset:640
	s_waitcnt lgkmcnt(2)
	v_mul_f32_e32 v46, v150, v46
	v_mul_f32_e32 v47, v150, v47
	v_mul_f32_e32 v48, v150, v48
	v_mul_f32_e32 v49, v150, v49
	v_mul_f32_e32 v42, v150, v42
	v_mul_f32_e32 v43, v150, v43
	v_mul_f32_e32 v44, v150, v44
	v_mul_f32_e32 v45, v150, v45
	v_cvt_pk_bf16_f32 v182, v46, v47
	v_cvt_pk_bf16_f32 v183, v48, v49
	v_cvt_pk_bf16_f32 v184, v42, v43
	v_cvt_pk_bf16_f32 v185, v44, v45
	ds_write_b128 v164, v[182:185]
	v_mul_f32_e32 v38, v150, v38
	v_mul_f32_e32 v39, v150, v39
	v_mul_f32_e32 v40, v150, v40
	v_mul_f32_e32 v41, v150, v41
	v_mul_f32_e32 v34, v150, v34
	v_mul_f32_e32 v35, v150, v35
	v_mul_f32_e32 v36, v150, v36
	v_mul_f32_e32 v37, v150, v37
	v_cvt_pk_bf16_f32 v182, v38, v39
	v_cvt_pk_bf16_f32 v183, v40, v41
	v_cvt_pk_bf16_f32 v184, v34, v35
	v_cvt_pk_bf16_f32 v185, v36, v37
	v_xor_b32_e32 v167, 64, v164
	ds_write_b128 v167, v[182:185]
	v_mov_b32_e32 v46, 0
	v_mov_b32_e32 v42, 0
	v_mov_b32_e32 v38, 0
	v_mov_b32_e32 v34, 0
	v_mov_b32_e32 v47, 0
	v_mov_b32_e32 v43, 0
	v_mov_b32_e32 v39, 0
	v_mov_b32_e32 v35, 0
	v_mov_b32_e32 v48, 0
	v_mov_b32_e32 v44, 0
	v_mov_b32_e32 v40, 0
	v_mov_b32_e32 v36, 0
	v_mov_b32_e32 v49, 0
	v_mov_b32_e32 v45, 0
	v_mov_b32_e32 v41, 0
	v_mov_b32_e32 v37, 0
	ds_read_b128 v[182:185], v165 offset:0
	v_cmp_lt_i32_e32 vcc, -1, v151
	v_lshlrev_b32_e32 v148, 13, v151
	v_mov_b32_e32 v149, 0
	v_lshl_add_u64 v[148:149], v[148:149], 0, v[86:87]
	v_cndmask_b32_e32 v148, v168, v148, vcc
	v_cndmask_b32_e32 v149, v169, v149, vcc
	s_waitcnt lgkmcnt(0)
; #define PG8_LAS __attribute__((address_space(3)))
; __device__ __forceinline__ unsigned cvtpk(float lo, float hi) { f32x2 v = {lo, hi}; bf16x2_t b = __builtin_convertvector(v, bf16x2_t); return __builtin_bit_cast(unsigned, b); }
; __device__ __forceinline__ void moe_down_stream(PG8_LAS unsigned char* lds, int e, int cb0, int slot0, int nv, const bf16_t* HIDp, const float* Wd, bf16_t* Y, const float* slot_w, const int* slot_dst) {
;     ...
;         if (((t + 1) & 7) == 7) {
;             const int cb = cb0 + ((t + 1) >> 3);
; #pragma unroll
;             for (int m = 0; m < DNM; ++m) {
;                 const float w_ = lw[4 * (16 * m + fr) + wr];
; #pragma unroll
;                 for (int p = 0; p < 2; ++p) { const f32x4 v0 = acc[m][2 * p] * w_, v1 = acc[m][2 * p + 1] * w_; u32x4 w; w.x = cvtpk(v0[0], v0[1]); w.y = cvtpk(v0[2], v0[3]); w.z = cvtpk(v1[0], v1[1]); w.w = cvtpk(v1[2], v1[3]);
;                     *(PG8_LAS u32x4*)(stg + fr * 128 + (((4 * p + fq) ^ (fr & 7)) * 16)) = w; }
; #pragma unroll
;                 for (int hh = 0; hh < 2; ++hh) { const int r = (lane >> 3) + 8 * hh, cc = lane & 7; const u32x4 d = *(const PG8_LAS u32x4*)(stg + r * 128 + ((cc ^ (r & 7)) * 16)); const int dst_ = ldst[4 * (16 * m + r) + wr];
;                     if (dst_ >= 0) *(u32x4*)(Y + (size_t)dst_ * D + 128 * cb + 64 * wc + 8 * cc) = d; }
; #pragma unroll
;                 for (int n = 0; n < 4; ++n) acc[m][n] = (f32x4){0.f, 0.f, 0.f, 0.f}; } }
	global_store_dwordx4 v[148:149], v[182:185], off
	ds_read_b128 v[182:185], v165 offset:8192
	v_cmp_lt_i32_e32 vcc, -1, v166
	v_lshlrev_b32_e32 v148, 13, v166
	v_mov_b32_e32 v149, 0
	v_lshl_add_u64 v[148:149], v[148:149], 0, v[86:87]
	v_cndmask_b32_e32 v148, v168, v148, vcc
	v_cndmask_b32_e32 v149, v169, v149, vcc
	s_waitcnt lgkmcnt(0)
	global_store_dwordx4 v[148:149], v[182:185], off
	ds_read_b32 v150, v82 offset:768
	ds_read_b32 v151, v83 offset:768
	ds_read_b32 v166, v83 offset:896
	s_waitcnt lgkmcnt(2)
	v_mul_f32_e32 v18, v150, v18
	v_mul_f32_e32 v19, v150, v19
	v_mul_f32_e32 v20, v150, v20
	v_mul_f32_e32 v21, v150, v21
	v_mul_f32_e32 v22, v150, v22
	v_mul_f32_e32 v23, v150, v23
	v_mul_f32_e32 v24, v150, v24
	v_mul_f32_e32 v25, v150, v25
	v_cvt_pk_bf16_f32 v182, v18, v19
	v_cvt_pk_bf16_f32 v183, v20, v21
	v_cvt_pk_bf16_f32 v184, v22, v23
	v_cvt_pk_bf16_f32 v185, v24, v25
	ds_write_b128 v164, v[182:185]
	v_mul_f32_e32 v26, v150, v26
	v_mul_f32_e32 v27, v150, v27
	v_mul_f32_e32 v28, v150, v28
	v_mul_f32_e32 v29, v150, v29
	v_mul_f32_e32 v30, v150, v30
	v_mul_f32_e32 v31, v150, v31
	v_mul_f32_e32 v32, v150, v32
	v_mul_f32_e32 v33, v150, v33
	v_cvt_pk_bf16_f32 v182, v26, v27
	v_cvt_pk_bf16_f32 v183, v28, v29
	v_cvt_pk_bf16_f32 v184, v30, v31
	v_cvt_pk_bf16_f32 v185, v32, v33
	v_xor_b32_e32 v167, 64, v164
	ds_write_b128 v167, v[182:185]
	v_mov_b32_e32 v18, 0
	v_mov_b32_e32 v22, 0
	v_mov_b32_e32 v26, 0
	v_mov_b32_e32 v30, 0
	v_mov_b32_e32 v19, 0
	v_mov_b32_e32 v23, 0
	v_mov_b32_e32 v27, 0
	v_mov_b32_e32 v31, 0
	v_mov_b32_e32 v20, 0
	v_mov_b32_e32 v24, 0
	v_mov_b32_e32 v28, 0
	v_mov_b32_e32 v32, 0
	v_mov_b32_e32 v21, 0
	v_mov_b32_e32 v25, 0
	v_mov_b32_e32 v29, 0
	v_mov_b32_e32 v33, 0
	ds_read_b128 v[182:185], v165 offset:0
	v_cmp_lt_i32_e32 vcc, -1, v151
	v_lshlrev_b32_e32 v148, 13, v151
	v_mov_b32_e32 v149, 0
	v_lshl_add_u64 v[148:149], v[148:149], 0, v[86:87]
	v_cndmask_b32_e32 v148, v168, v148, vcc
	v_cndmask_b32_e32 v149, v169, v149, vcc
	s_waitcnt lgkmcnt(0)
	global_store_dwordx4 v[148:149], v[182:185], off
	ds_read_b128 v[182:185], v165 offset:8192
	v_cmp_lt_i32_e32 vcc, -1, v166
	v_lshlrev_b32_e32 v148, 13, v166
	v_mov_b32_e32 v149, 0
	v_lshl_add_u64 v[148:149], v[148:149], 0, v[86:87]
	v_cndmask_b32_e32 v148, v168, v148, vcc
	v_cndmask_b32_e32 v149, v169, v149, vcc
	s_waitcnt lgkmcnt(0)
	global_store_dwordx4 v[148:149], v[182:185], off
	ds_read_b32 v150, v82 offset:1024
	ds_read_b32 v151, v83 offset:1024
	ds_read_b32 v166, v83 offset:1152
	s_waitcnt lgkmcnt(2)
	v_mul_f32_e32 v2, v150, v2
	v_mul_f32_e32 v3, v150, v3
	v_mul_f32_e32 v4, v150, v4
	v_mul_f32_e32 v5, v150, v5
	v_mul_f32_e32 v6, v150, v6
	v_mul_f32_e32 v7, v150, v7
	v_mul_f32_e32 v8, v150, v8
	v_mul_f32_e32 v9, v150, v9
	v_cvt_pk_bf16_f32 v182, v2, v3
	v_cvt_pk_bf16_f32 v183, v4, v5
	v_cvt_pk_bf16_f32 v184, v6, v7
	v_cvt_pk_bf16_f32 v185, v8, v9
	ds_write_b128 v164, v[182:185]
	v_mul_f32_e32 v10, v150, v10
	v_mul_f32_e32 v11, v150, v11
	v_mul_f32_e32 v12, v150, v12
	v_mul_f32_e32 v13, v150, v13
	v_mul_f32_e32 v14, v150, v14
	v_mul_f32_e32 v15, v150, v15
	v_mul_f32_e32 v16, v150, v16
	v_mul_f32_e32 v17, v150, v17
	v_cvt_pk_bf16_f32 v182, v10, v11
	v_cvt_pk_bf16_f32 v183, v12, v13
	v_cvt_pk_bf16_f32 v184, v14, v15
	v_cvt_pk_bf16_f32 v185, v16, v17
	v_xor_b32_e32 v167, 64, v164
	ds_write_b128 v167, v[182:185]
	v_mov_b32_e32 v2, 0
	v_mov_b32_e32 v6, 0
	v_mov_b32_e32 v10, 0
	v_mov_b32_e32 v14, 0
	v_mov_b32_e32 v3, 0
	v_mov_b32_e32 v7, 0
	v_mov_b32_e32 v11, 0
	v_mov_b32_e32 v15, 0
	v_mov_b32_e32 v4, 0
	v_mov_b32_e32 v8, 0
	v_mov_b32_e32 v12, 0
	v_mov_b32_e32 v16, 0
	v_mov_b32_e32 v5, 0
	v_mov_b32_e32 v9, 0
	v_mov_b32_e32 v13, 0
	v_mov_b32_e32 v17, 0
	ds_read_b128 v[182:185], v165 offset:0
	v_cmp_lt_i32_e32 vcc, -1, v151
	v_lshlrev_b32_e32 v148, 13, v151
	v_mov_b32_e32 v149, 0
	v_lshl_add_u64 v[148:149], v[148:149], 0, v[86:87]
	v_cndmask_b32_e32 v148, v168, v148, vcc
	v_cndmask_b32_e32 v149, v169, v149, vcc
	s_waitcnt lgkmcnt(0)
	global_store_dwordx4 v[148:149], v[182:185], off
	ds_read_b128 v[182:185], v165 offset:8192
	v_cmp_lt_i32_e32 vcc, -1, v166
	v_lshlrev_b32_e32 v148, 13, v166
	v_mov_b32_e32 v149, 0
	v_lshl_add_u64 v[148:149], v[148:149], 0, v[86:87]
	v_cndmask_b32_e32 v148, v168, v148, vcc
	v_cndmask_b32_e32 v149, v169, v149, vcc
	s_waitcnt lgkmcnt(0)
	global_store_dwordx4 v[148:149], v[182:185], off
	v_add_co_u32_e32 v86, vcc, 0x800, v86
	s_nop 1
	v_addc_co_u32_e32 v87, vcc, 0, v87, vcc
	s_waitcnt lgkmcnt(0)
; #define MD_GLDS_A(buf, tau) do { _Pragma("unroll") for (int i = 0; i < 5; ++i) if (amask & (1u << i)) \
;         __builtin_amdgcn_global_load_lds((const unsigned*)((const char*)HIDp + aoff[i] + (size_t)((tau) & 7) * 128), (PG8_LAS unsigned*)(MD_SA(buf) + wid * 1024 + i * 8192), 16, 0, 0); } while (0)
; #define MD_B_ISSUE(sb, tau) do { const char* kb_ = Bb + (size_t)((tau) >> 3) * 512 + (size_t)((tau) & 7) * (64 * (size_t)RB); _Pragma("unroll") for (int j = 0; j < 8; ++j) { const char* p_ = kb_ + (size_t)j * RB; \
;         asm volatile("global_load_dwordx2 %0, %1, off" : "=&v"(sb[j]) : "v"(p_) : "memory"); } } while (0)
; #define MD_B_WAIT(sb, N) asm volatile("s_waitcnt vmcnt(%8)" : "+v"(sb[0]), "+v"(sb[1]), "+v"(sb[2]), "+v"(sb[3]), "+v"(sb[4]), "+v"(sb[5]), "+v"(sb[6]), "+v"(sb[7]) : "n"(N) : "memory")
; #define MD_END(last) do { if (last) asm volatile("s_waitcnt vmcnt(0)" ::: "memory"); else asm volatile("s_waitcnt vmcnt(8)" ::: "memory"); \
;         asm volatile("s_waitcnt lgkmcnt(0)" ::: "memory"); __builtin_amdgcn_s_barrier(); asm volatile("" ::: "memory"); } while (0)
; __device__ __forceinline__ void moe_down_stream(PG8_LAS unsigned char* lds, int e, int cb0, int slot0, int nv, const bf16_t* HIDp, const float* Wd, bf16_t* Y, const float* slot_w, const int* slot_dst) {
;     ...
;     for (int t = 0; t < NT; t += 2) {
;         if (t + 2 < NT) MD_B_WAIT(s1, 8); else MD_B_WAIT(s1, 0);
;         MD_B_WRITE(s1, 1); __builtin_amdgcn_sched_barrier(0); MD_GLDS_A(1, t + 1); __builtin_amdgcn_sched_barrier(0);
;         if (t + 3 < NT) MD_B_ISSUE(s1, t + 3);
;         MD_COMPUTE(0);
;         MD_END(t + 3 >= NT);
;         if (t + 2 < NT) { MD_B_WAIT(s0, 8); MD_B_WRITE(s0, 0); __builtin_amdgcn_sched_barrier(0); MD_GLDS_A(0, t + 2); __builtin_amdgcn_sched_barrier(0); }
;         if (t + 4 < NT) MD_B_ISSUE(s0, t + 4);
;         MD_COMPUTE(1);
;         MD_END(t + 4 >= NT);
.Lmd_noepi_X:
	s_sub_u32 s56, s56, 1
	s_cmp_lg_u32 s56, 0
	s_cbranch_scc1 .Lmd_loop_X
	v_cvt_pk_bf16_f32 v172, v114, v116
	v_cvt_pk_bf16_f32 v173, v118, v120
	v_cvt_pk_bf16_f32 v174, v122, v124
	v_cvt_pk_bf16_f32 v175, v126, v128
	v_cvt_pk_bf16_f32 v176, v115, v117
	v_cvt_pk_bf16_f32 v177, v119, v121
	v_cvt_pk_bf16_f32 v178, v123, v125
	v_cvt_pk_bf16_f32 v179, v127, v129
	ds_write_b128 v95, v[172:175] offset:19456
	ds_write_b128 v95, v[176:179] offset:19584
	v_add_u32_e32 v91, s46, v135
	v_add_u32_e32 v93, s46, v137
	ds_read_b128 v[238:241], v139 offset:0
	ds_read_b128 v[242:245], v139 offset:2048
	ds_read_b128 v[246:249], v139 offset:4096
	ds_read_b128 v[250:253], v139 offset:6144
	ds_read_b128 v[218:221], v91 offset:0
	ds_read_b128 v[222:225], v91 offset:2048
	ds_read_b128 v[226:229], v91 offset:4096
	ds_read_b128 v[230:233], v91 offset:6144
	ds_read_b128 v[234:237], v91 offset:8192
	s_add_i32 s49, s48, s74
	s_add_i32 s52, s52, 1
	s_and_b32 s54, s52, 7
	s_cmp_eq_u32 s54, 0
	s_cselect_b32 s54, s53, s32
	s_cselect_b32 s55, -1, 0
	s_add_u32 s30, s30, s54
	s_addc_u32 s31, s31, s55
	s_waitcnt lgkmcnt(0)
	v_mfma_f32_16x16x32_bf16 v[78:81], v[238:241], v[218:221], v[78:81]
	v_mfma_f32_16x16x32_bf16 v[74:77], v[242:245], v[218:221], v[74:77]
	v_mfma_f32_16x16x32_bf16 v[70:73], v[246:249], v[218:221], v[70:73]
	v_mfma_f32_16x16x32_bf16 v[66:69], v[250:253], v[218:221], v[66:69]
	ds_read_b128 v[218:221], v93 offset:0
	ds_read_b128 v[142:145], v141 offset:0
	s_mov_b32 m0, s49
	s_nop 0
	global_load_lds_dwordx4 v88, s[30:31]
	v_mfma_f32_16x16x32_bf16 v[62:65], v[238:241], v[222:225], v[62:65]
	v_mfma_f32_16x16x32_bf16 v[58:61], v[242:245], v[222:225], v[58:61]
	v_mfma_f32_16x16x32_bf16 v[54:57], v[246:249], v[222:225], v[54:57]
	v_mfma_f32_16x16x32_bf16 v[50:53], v[250:253], v[222:225], v[50:53]
	ds_read_b128 v[222:225], v93 offset:2048
	ds_read_b128 v[146:149], v141 offset:2048
	s_add_i32 m0, s49, 0x2000
	s_nop 0
	global_load_lds_dwordx4 v90, s[30:31]
	v_mfma_f32_16x16x32_bf16 v[46:49], v[238:241], v[226:229], v[46:49]
	v_mfma_f32_16x16x32_bf16 v[42:45], v[242:245], v[226:229], v[42:45]
	v_mfma_f32_16x16x32_bf16 v[38:41], v[246:249], v[226:229], v[38:41]
	v_mfma_f32_16x16x32_bf16 v[34:37], v[250:253], v[226:229], v[34:37]
	ds_read_b128 v[226:229], v93 offset:4096
	ds_read_b128 v[156:159], v141 offset:4096
	s_add_i32 m0, s49, 0x4000
	s_nop 0
	global_load_lds_dwordx4 v92, s[30:31]
	v_mfma_f32_16x16x32_bf16 v[18:21], v[238:241], v[230:233], v[18:21]
	v_mfma_f32_16x16x32_bf16 v[22:25], v[242:245], v[230:233], v[22:25]
	v_mfma_f32_16x16x32_bf16 v[26:29], v[246:249], v[230:233], v[26:29]
	v_mfma_f32_16x16x32_bf16 v[30:33], v[250:253], v[230:233], v[30:33]
	ds_read_b128 v[230:233], v93 offset:6144
	ds_read_b128 v[160:163], v141 offset:6144
	s_add_i32 m0, s49, 0x6000
	s_nop 0
	global_load_lds_dwordx4 v94, s[30:31]
	v_mfma_f32_16x16x32_bf16 v[2:5], v[238:241], v[234:237], v[2:5]
	v_mfma_f32_16x16x32_bf16 v[6:9], v[242:245], v[234:237], v[6:9]
	v_mfma_f32_16x16x32_bf16 v[10:13], v[246:249], v[234:237], v[10:13]
	v_mfma_f32_16x16x32_bf16 v[14:17], v[250:253], v[234:237], v[14:17]
	ds_read_b128 v[234:237], v93 offset:8192
	s_add_i32 m0, s49, 0x8000
	s_nop 0
	global_load_lds_dwordx4 v96, s[30:31]
	s_waitcnt lgkmcnt(0)
	v_mfma_f32_16x16x32_bf16 v[78:81], v[142:145], v[218:221], v[78:81]
	v_mfma_f32_16x16x32_bf16 v[74:77], v[146:149], v[218:221], v[74:77]
	v_mfma_f32_16x16x32_bf16 v[70:73], v[156:159], v[218:221], v[70:73]
	v_mfma_f32_16x16x32_bf16 v[66:69], v[160:163], v[218:221], v[66:69]
	s_add_i32 s51, s51, 1
	s_and_b32 s54, s51, 7
	s_cmp_eq_u32 s54, 0
	s_cselect_b32 s44, s34, s35
	s_cselect_b32 s45, -1, 0
	v_lshl_add_u64 v[132:133], v[132:133], 0, s[44:45]
	global_load_dwordx2 v[114:115], v[132:133], off
	v_lshl_add_u64 v[180:181], v[132:133], 0, s[24:25]
	global_load_dwordx2 v[116:117], v[180:181], off
	v_mfma_f32_16x16x32_bf16 v[62:65], v[142:145], v[222:225], v[62:65]
	v_mfma_f32_16x16x32_bf16 v[58:61], v[146:149], v[222:225], v[58:61]
	v_mfma_f32_16x16x32_bf16 v[54:57], v[156:159], v[222:225], v[54:57]
	v_mfma_f32_16x16x32_bf16 v[50:53], v[160:163], v[222:225], v[50:53]
	v_lshl_add_u64 v[180:181], v[132:133], 0, s[26:27]
	global_load_dwordx2 v[118:119], v[180:181], off
	v_lshl_add_u64 v[180:181], v[132:133], 0, s[28:29]
	global_load_dwordx2 v[120:121], v[180:181], off
	v_mfma_f32_16x16x32_bf16 v[46:49], v[142:145], v[226:229], v[46:49]
	v_mfma_f32_16x16x32_bf16 v[42:45], v[146:149], v[226:229], v[42:45]
	v_mfma_f32_16x16x32_bf16 v[38:41], v[156:159], v[226:229], v[38:41]
	v_mfma_f32_16x16x32_bf16 v[34:37], v[160:163], v[226:229], v[34:37]
	v_lshl_add_u64 v[180:181], v[132:133], 0, s[36:37]
	global_load_dwordx2 v[122:123], v[180:181], off
	v_lshl_add_u64 v[180:181], v[132:133], 0, s[38:39]
	global_load_dwordx2 v[124:125], v[180:181], off
	v_mfma_f32_16x16x32_bf16 v[18:21], v[142:145], v[230:233], v[18:21]
	v_mfma_f32_16x16x32_bf16 v[22:25], v[146:149], v[230:233], v[22:25]
	v_mfma_f32_16x16x32_bf16 v[26:29], v[156:159], v[230:233], v[26:29]
	v_mfma_f32_16x16x32_bf16 v[30:33], v[160:163], v[230:233], v[30:33]
	v_lshl_add_u64 v[180:181], v[132:133], 0, s[40:41]
	global_load_dwordx2 v[126:127], v[180:181], off
	v_lshl_add_u64 v[180:181], v[132:133], 0, s[42:43]
	global_load_dwordx2 v[128:129], v[180:181], off
	v_mfma_f32_16x16x32_bf16 v[2:5], v[142:145], v[234:237], v[2:5]
	v_mfma_f32_16x16x32_bf16 v[6:9], v[146:149], v[234:237], v[6:9]
	v_mfma_f32_16x16x32_bf16 v[10:13], v[156:159], v[234:237], v[10:13]
	v_mfma_f32_16x16x32_bf16 v[14:17], v[160:163], v[234:237], v[14:17]
	s_waitcnt vmcnt(21)
	s_waitcnt lgkmcnt(0)
	s_barrier
; #define MD_GLDS_A(buf, tau) do { _Pragma("unroll") for (int i = 0; i < 5; ++i) if (amask & (1u << i)) \
;         __builtin_amdgcn_global_load_lds((const unsigned*)((const char*)HIDp + aoff[i] + (size_t)((tau) & 7) * 128), (PG8_LAS unsigned*)(MD_SA(buf) + wid * 1024 + i * 8192), 16, 0, 0); } while (0)
; #define MD_B_ISSUE(sb, tau) do { const char* kb_ = Bb + (size_t)((tau) >> 3) * 512 + (size_t)((tau) & 7) * (64 * (size_t)RB); _Pragma("unroll") for (int j = 0; j < 8; ++j) { const char* p_ = kb_ + (size_t)j * RB; \
;         asm volatile("global_load_dwordx2 %0, %1, off" : "=&v"(sb[j]) : "v"(p_) : "memory"); } } while (0)
; #define MD_B_WAIT(sb, N) asm volatile("s_waitcnt vmcnt(%8)" : "+v"(sb[0]), "+v"(sb[1]), "+v"(sb[2]), "+v"(sb[3]), "+v"(sb[4]), "+v"(sb[5]), "+v"(sb[6]), "+v"(sb[7]) : "n"(N) : "memory")
; #define MD_END(last) do { if (last) asm volatile("s_waitcnt vmcnt(0)" ::: "memory"); else asm volatile("s_waitcnt vmcnt(8)" ::: "memory"); \
;         asm volatile("s_waitcnt lgkmcnt(0)" ::: "memory"); __builtin_amdgcn_s_barrier(); asm volatile("" ::: "memory"); } while (0)
; __device__ __forceinline__ void moe_down_stream(PG8_LAS unsigned char* lds, int e, int cb0, int slot0, int nv, const bf16_t* HIDp, const float* Wd, bf16_t* Y, const float* slot_w, const int* slot_dst) {
;     ...
;     for (int t = 0; t < NT; t += 2) {
;         if (t + 2 < NT) MD_B_WAIT(s1, 8); else MD_B_WAIT(s1, 0);
;         MD_B_WRITE(s1, 1); __builtin_amdgcn_sched_barrier(0); MD_GLDS_A(1, t + 1); __builtin_amdgcn_sched_barrier(0);
;         if (t + 3 < NT) MD_B_ISSUE(s1, t + 3);
;         MD_COMPUTE(0);
;         MD_END(t + 3 >= NT);
;         if (t + 2 < NT) { MD_B_WAIT(s0, 8); MD_B_WRITE(s0, 0); __builtin_amdgcn_sched_barrier(0); MD_GLDS_A(0, t + 2); __builtin_amdgcn_sched_barrier(0); }
;         if (t + 4 < NT) MD_B_ISSUE(s0, t + 4);
;         MD_COMPUTE(1);
;         MD_END(t + 4 >= NT);
	s_mov_b32 s49, s46
	s_mov_b32 s46, s47
	s_mov_b32 s47, s48
	s_mov_b32 s48, s49
	s_add_i32 s50, s50, 1
	v_cvt_pk_bf16_f32 v172, v186, v188
	v_cvt_pk_bf16_f32 v173, v190, v192
	v_cvt_pk_bf16_f32 v174, v194, v196
	v_cvt_pk_bf16_f32 v175, v198, v200
	v_cvt_pk_bf16_f32 v176, v187, v189
	v_cvt_pk_bf16_f32 v177, v191, v193
	v_cvt_pk_bf16_f32 v178, v195, v197
	v_cvt_pk_bf16_f32 v179, v199, v201
	ds_write_b128 v95, v[172:175] offset:0
	ds_write_b128 v95, v[176:179] offset:128
	v_add_u32_e32 v91, s46, v135
	v_add_u32_e32 v93, s46, v137
	ds_read_b128 v[238:241], v139 offset:19456
	ds_read_b128 v[242:245], v139 offset:21504
	ds_read_b128 v[246:249], v139 offset:23552
	ds_read_b128 v[250:253], v139 offset:25600
	ds_read_b128 v[218:221], v91 offset:0
	ds_read_b128 v[222:225], v91 offset:2048
	ds_read_b128 v[226:229], v91 offset:4096
	ds_read_b128 v[230:233], v91 offset:6144
	ds_read_b128 v[234:237], v91 offset:8192
	s_add_i32 s49, s48, s74
	s_add_i32 s52, s52, 1
	s_and_b32 s54, s52, 7
	s_cmp_eq_u32 s54, 0
	s_cselect_b32 s54, s53, s32
	s_cselect_b32 s55, -1, 0
	s_add_u32 s30, s30, s54
	s_addc_u32 s31, s31, s55
	s_waitcnt lgkmcnt(0)
	v_mfma_f32_16x16x32_bf16 v[78:81], v[238:241], v[218:221], v[78:81]
	v_mfma_f32_16x16x32_bf16 v[74:77], v[242:245], v[218:221], v[74:77]
	v_mfma_f32_16x16x32_bf16 v[70:73], v[246:249], v[218:221], v[70:73]
	v_mfma_f32_16x16x32_bf16 v[66:69], v[250:253], v[218:221], v[66:69]
	ds_read_b128 v[218:221], v93 offset:0
	ds_read_b128 v[142:145], v141 offset:19456
	s_mov_b32 m0, s49
	s_nop 0
	global_load_lds_dwordx4 v88, s[30:31]
	v_mfma_f32_16x16x32_bf16 v[62:65], v[238:241], v[222:225], v[62:65]
	v_mfma_f32_16x16x32_bf16 v[58:61], v[242:245], v[222:225], v[58:61]
	v_mfma_f32_16x16x32_bf16 v[54:57], v[246:249], v[222:225], v[54:57]
	v_mfma_f32_16x16x32_bf16 v[50:53], v[250:253], v[222:225], v[50:53]
	ds_read_b128 v[222:225], v93 offset:2048
	ds_read_b128 v[146:149], v141 offset:21504
	s_add_i32 m0, s49, 0x2000
	s_nop 0
	global_load_lds_dwordx4 v90, s[30:31]
	v_mfma_f32_16x16x32_bf16 v[46:49], v[238:241], v[226:229], v[46:49]
	v_mfma_f32_16x16x32_bf16 v[42:45], v[242:245], v[226:229], v[42:45]
	v_mfma_f32_16x16x32_bf16 v[38:41], v[246:249], v[226:229], v[38:41]
	v_mfma_f32_16x16x32_bf16 v[34:37], v[250:253], v[226:229], v[34:37]
	ds_read_b128 v[226:229], v93 offset:4096
	ds_read_b128 v[156:159], v141 offset:23552
	s_add_i32 m0, s49, 0x4000
	s_nop 0
	global_load_lds_dwordx4 v92, s[30:31]
	v_mfma_f32_16x16x32_bf16 v[18:21], v[238:241], v[230:233], v[18:21]
	v_mfma_f32_16x16x32_bf16 v[22:25], v[242:245], v[230:233], v[22:25]
	v_mfma_f32_16x16x32_bf16 v[26:29], v[246:249], v[230:233], v[26:29]
	v_mfma_f32_16x16x32_bf16 v[30:33], v[250:253], v[230:233], v[30:33]
	ds_read_b128 v[230:233], v93 offset:6144
	ds_read_b128 v[160:163], v141 offset:25600
	s_add_i32 m0, s49, 0x6000
	s_nop 0
	global_load_lds_dwordx4 v94, s[30:31]
	v_mfma_f32_16x16x32_bf16 v[2:5], v[238:241], v[234:237], v[2:5]
	v_mfma_f32_16x16x32_bf16 v[6:9], v[242:245], v[234:237], v[6:9]
	v_mfma_f32_16x16x32_bf16 v[10:13], v[246:249], v[234:237], v[10:13]
	v_mfma_f32_16x16x32_bf16 v[14:17], v[250:253], v[234:237], v[14:17]
	ds_read_b128 v[234:237], v93 offset:8192
	s_add_i32 m0, s49, 0x8000
	s_nop 0
	global_load_lds_dwordx4 v96, s[30:31]
	s_waitcnt lgkmcnt(0)
	v_mfma_f32_16x16x32_bf16 v[78:81], v[142:145], v[218:221], v[78:81]
	v_mfma_f32_16x16x32_bf16 v[74:77], v[146:149], v[218:221], v[74:77]
	v_mfma_f32_16x16x32_bf16 v[70:73], v[156:159], v[218:221], v[70:73]
	v_mfma_f32_16x16x32_bf16 v[66:69], v[160:163], v[218:221], v[66:69]
	s_add_i32 s51, s51, 1
	s_and_b32 s54, s51, 7
	s_cmp_eq_u32 s54, 0
	s_cselect_b32 s44, s34, s35
	s_cselect_b32 s45, -1, 0
	v_lshl_add_u64 v[132:133], v[132:133], 0, s[44:45]
	global_load_dwordx2 v[186:187], v[132:133], off
	v_lshl_add_u64 v[180:181], v[132:133], 0, s[24:25]
	global_load_dwordx2 v[188:189], v[180:181], off
	v_mfma_f32_16x16x32_bf16 v[62:65], v[142:145], v[222:225], v[62:65]
	v_mfma_f32_16x16x32_bf16 v[58:61], v[146:149], v[222:225], v[58:61]
	v_mfma_f32_16x16x32_bf16 v[54:57], v[156:159], v[222:225], v[54:57]
	v_mfma_f32_16x16x32_bf16 v[50:53], v[160:163], v[222:225], v[50:53]
	v_lshl_add_u64 v[180:181], v[132:133], 0, s[26:27]
	global_load_dwordx2 v[190:191], v[180:181], off
	v_lshl_add_u64 v[180:181], v[132:133], 0, s[28:29]
	global_load_dwordx2 v[192:193], v[180:181], off
	v_mfma_f32_16x16x32_bf16 v[46:49], v[142:145], v[226:229], v[46:49]
	v_mfma_f32_16x16x32_bf16 v[42:45], v[146:149], v[226:229], v[42:45]
	v_mfma_f32_16x16x32_bf16 v[38:41], v[156:159], v[226:229], v[38:41]
	v_mfma_f32_16x16x32_bf16 v[34:37], v[160:163], v[226:229], v[34:37]
	v_lshl_add_u64 v[180:181], v[132:133], 0, s[36:37]
	global_load_dwordx2 v[194:195], v[180:181], off
	v_lshl_add_u64 v[180:181], v[132:133], 0, s[38:39]
	global_load_dwordx2 v[196:197], v[180:181], off
	v_mfma_f32_16x16x32_bf16 v[18:21], v[142:145], v[230:233], v[18:21]
	v_mfma_f32_16x16x32_bf16 v[22:25], v[146:149], v[230:233], v[22:25]
	v_mfma_f32_16x16x32_bf16 v[26:29], v[156:159], v[230:233], v[26:29]
	v_mfma_f32_16x16x32_bf16 v[30:33], v[160:163], v[230:233], v[30:33]
	v_lshl_add_u64 v[180:181], v[132:133], 0, s[40:41]
	global_load_dwordx2 v[198:199], v[180:181], off
	v_lshl_add_u64 v[180:181], v[132:133], 0, s[42:43]
	global_load_dwordx2 v[200:201], v[180:181], off
	v_mfma_f32_16x16x32_bf16 v[2:5], v[142:145], v[234:237], v[2:5]
	v_mfma_f32_16x16x32_bf16 v[6:9], v[146:149], v[234:237], v[6:9]
	v_mfma_f32_16x16x32_bf16 v[10:13], v[156:159], v[234:237], v[10:13]
	v_mfma_f32_16x16x32_bf16 v[14:17], v[160:163], v[234:237], v[14:17]
	s_waitcnt vmcnt(21)
	s_waitcnt lgkmcnt(0)
	s_barrier
; #define MD_GLDS_A(buf, tau) do { _Pragma("unroll") for (int i = 0; i < 5; ++i) if (amask & (1u << i)) \
;         __builtin_amdgcn_global_load_lds((const unsigned*)((const char*)HIDp + aoff[i] + (size_t)((tau) & 7) * 128), (PG8_LAS unsigned*)(MD_SA(buf) + wid * 1024 + i * 8192), 16, 0, 0); } while (0)
; #define MD_B_ISSUE(sb, tau) do { const char* kb_ = Bb + (size_t)((tau) >> 3) * 512 + (size_t)((tau) & 7) * (64 * (size_t)RB); _Pragma("unroll") for (int j = 0; j < 8; ++j) { const char* p_ = kb_ + (size_t)j * RB; \
;         asm volatile("global_load_dwordx2 %0, %1, off" : "=&v"(sb[j]) : "v"(p_) : "memory"); } } while (0)
; #define MD_B_WAIT(sb, N) asm volatile("s_waitcnt vmcnt(%8)" : "+v"(sb[0]), "+v"(sb[1]), "+v"(sb[2]), "+v"(sb[3]), "+v"(sb[4]), "+v"(sb[5]), "+v"(sb[6]), "+v"(sb[7]) : "n"(N) : "memory")
; #define MD_END(last) do { if (last) asm volatile("s_waitcnt vmcnt(0)" ::: "memory"); else asm volatile("s_waitcnt vmcnt(8)" ::: "memory"); \
;         asm volatile("s_waitcnt lgkmcnt(0)" ::: "memory"); __builtin_amdgcn_s_barrier(); asm volatile("" ::: "memory"); } while (0)
; __device__ __forceinline__ void moe_down_stream(PG8_LAS unsigned char* lds, int e, int cb0, int slot0, int nv, const bf16_t* HIDp, const float* Wd, bf16_t* Y, const float* slot_w, const int* slot_dst) {
;     ...
;     for (int t = 0; t < NT; t += 2) {
;         if (t + 2 < NT) MD_B_WAIT(s1, 8); else MD_B_WAIT(s1, 0);
;         MD_B_WRITE(s1, 1); __builtin_amdgcn_sched_barrier(0); MD_GLDS_A(1, t + 1); __builtin_amdgcn_sched_barrier(0);
;         if (t + 3 < NT) MD_B_ISSUE(s1, t + 3);
;         MD_COMPUTE(0);
;         MD_END(t + 3 >= NT);
;         if (t + 2 < NT) { MD_B_WAIT(s0, 8); MD_B_WRITE(s0, 0); __builtin_amdgcn_sched_barrier(0); MD_GLDS_A(0, t + 2); __builtin_amdgcn_sched_barrier(0); }
;         if (t + 4 < NT) MD_B_ISSUE(s0, t + 4);
;         MD_COMPUTE(1);
;         MD_END(t + 4 >= NT);
	s_mov_b32 s49, s46
	s_mov_b32 s46, s47
	s_mov_b32 s47, s48
	s_mov_b32 s48, s49
	s_add_i32 s50, s50, 1
	v_cvt_pk_bf16_f32 v172, v202, v204
	v_cvt_pk_bf16_f32 v173, v206, v208
	v_cvt_pk_bf16_f32 v174, v210, v212
	v_cvt_pk_bf16_f32 v175, v214, v216
	v_cvt_pk_bf16_f32 v176, v203, v205
	v_cvt_pk_bf16_f32 v177, v207, v209
	v_cvt_pk_bf16_f32 v178, v211, v213
	v_cvt_pk_bf16_f32 v179, v215, v217
	ds_write_b128 v95, v[172:175] offset:19456
	ds_write_b128 v95, v[176:179] offset:19584
	v_add_u32_e32 v91, s46, v135
	v_add_u32_e32 v93, s46, v137
	ds_read_b128 v[238:241], v139 offset:0
	ds_read_b128 v[242:245], v139 offset:2048
	ds_read_b128 v[246:249], v139 offset:4096
	ds_read_b128 v[250:253], v139 offset:6144
	ds_read_b128 v[218:221], v91 offset:0
	ds_read_b128 v[222:225], v91 offset:2048
	ds_read_b128 v[226:229], v91 offset:4096
	ds_read_b128 v[230:233], v91 offset:6144
	ds_read_b128 v[234:237], v91 offset:8192
	s_add_i32 s49, s48, s74
	s_add_i32 s52, s52, 1
	s_and_b32 s54, s52, 7
	s_cmp_eq_u32 s54, 0
	s_cselect_b32 s54, s53, s32
	s_cselect_b32 s55, -1, 0
	s_add_u32 s30, s30, s54
	s_addc_u32 s31, s31, s55
	s_waitcnt lgkmcnt(0)
	v_mfma_f32_16x16x32_bf16 v[78:81], v[238:241], v[218:221], v[78:81]
	v_mfma_f32_16x16x32_bf16 v[74:77], v[242:245], v[218:221], v[74:77]
	v_mfma_f32_16x16x32_bf16 v[70:73], v[246:249], v[218:221], v[70:73]
	v_mfma_f32_16x16x32_bf16 v[66:69], v[250:253], v[218:221], v[66:69]
	ds_read_b128 v[218:221], v93 offset:0
	ds_read_b128 v[142:145], v141 offset:0
	s_mov_b32 m0, s49
	s_nop 0
	global_load_lds_dwordx4 v88, s[30:31]
	v_mfma_f32_16x16x32_bf16 v[62:65], v[238:241], v[222:225], v[62:65]
	v_mfma_f32_16x16x32_bf16 v[58:61], v[242:245], v[222:225], v[58:61]
	v_mfma_f32_16x16x32_bf16 v[54:57], v[246:249], v[222:225], v[54:57]
	v_mfma_f32_16x16x32_bf16 v[50:53], v[250:253], v[222:225], v[50:53]
	ds_read_b128 v[222:225], v93 offset:2048
	ds_read_b128 v[146:149], v141 offset:2048
	s_add_i32 m0, s49, 0x2000
	s_nop 0
	global_load_lds_dwordx4 v90, s[30:31]
	v_mfma_f32_16x16x32_bf16 v[46:49], v[238:241], v[226:229], v[46:49]
	v_mfma_f32_16x16x32_bf16 v[42:45], v[242:245], v[226:229], v[42:45]
	v_mfma_f32_16x16x32_bf16 v[38:41], v[246:249], v[226:229], v[38:41]
	v_mfma_f32_16x16x32_bf16 v[34:37], v[250:253], v[226:229], v[34:37]
	ds_read_b128 v[226:229], v93 offset:4096
	ds_read_b128 v[156:159], v141 offset:4096
	s_add_i32 m0, s49, 0x4000
	s_nop 0
	global_load_lds_dwordx4 v92, s[30:31]
	v_mfma_f32_16x16x32_bf16 v[18:21], v[238:241], v[230:233], v[18:21]
	v_mfma_f32_16x16x32_bf16 v[22:25], v[242:245], v[230:233], v[22:25]
	v_mfma_f32_16x16x32_bf16 v[26:29], v[246:249], v[230:233], v[26:29]
	v_mfma_f32_16x16x32_bf16 v[30:33], v[250:253], v[230:233], v[30:33]
	ds_read_b128 v[230:233], v93 offset:6144
	ds_read_b128 v[160:163], v141 offset:6144
	s_add_i32 m0, s49, 0x6000
	s_nop 0
	global_load_lds_dwordx4 v94, s[30:31]
	v_mfma_f32_16x16x32_bf16 v[2:5], v[238:241], v[234:237], v[2:5]
	v_mfma_f32_16x16x32_bf16 v[6:9], v[242:245], v[234:237], v[6:9]
	v_mfma_f32_16x16x32_bf16 v[10:13], v[246:249], v[234:237], v[10:13]
	v_mfma_f32_16x16x32_bf16 v[14:17], v[250:253], v[234:237], v[14:17]
	ds_read_b128 v[234:237], v93 offset:8192
	s_add_i32 m0, s49, 0x8000
	s_nop 0
	global_load_lds_dwordx4 v96, s[30:31]
	s_waitcnt lgkmcnt(0)
	v_mfma_f32_16x16x32_bf16 v[78:81], v[142:145], v[218:221], v[78:81]
	v_mfma_f32_16x16x32_bf16 v[74:77], v[146:149], v[218:221], v[74:77]
	v_mfma_f32_16x16x32_bf16 v[70:73], v[156:159], v[218:221], v[70:73]
	v_mfma_f32_16x16x32_bf16 v[66:69], v[160:163], v[218:221], v[66:69]
	s_add_i32 s51, s51, 1
	s_and_b32 s54, s51, 7
	s_cmp_eq_u32 s54, 0
	s_cselect_b32 s44, s34, s35
	s_cselect_b32 s45, -1, 0
	v_lshl_add_u64 v[132:133], v[132:133], 0, s[44:45]
	global_load_dwordx2 v[202:203], v[132:133], off
	v_lshl_add_u64 v[180:181], v[132:133], 0, s[24:25]
	global_load_dwordx2 v[204:205], v[180:181], off
	v_mfma_f32_16x16x32_bf16 v[62:65], v[142:145], v[222:225], v[62:65]
	v_mfma_f32_16x16x32_bf16 v[58:61], v[146:149], v[222:225], v[58:61]
	v_mfma_f32_16x16x32_bf16 v[54:57], v[156:159], v[222:225], v[54:57]
	v_mfma_f32_16x16x32_bf16 v[50:53], v[160:163], v[222:225], v[50:53]
	v_lshl_add_u64 v[180:181], v[132:133], 0, s[26:27]
	global_load_dwordx2 v[206:207], v[180:181], off
	v_lshl_add_u64 v[180:181], v[132:133], 0, s[28:29]
	global_load_dwordx2 v[208:209], v[180:181], off
	v_mfma_f32_16x16x32_bf16 v[46:49], v[142:145], v[226:229], v[46:49]
	v_mfma_f32_16x16x32_bf16 v[42:45], v[146:149], v[226:229], v[42:45]
	v_mfma_f32_16x16x32_bf16 v[38:41], v[156:159], v[226:229], v[38:41]
	v_mfma_f32_16x16x32_bf16 v[34:37], v[160:163], v[226:229], v[34:37]
	v_lshl_add_u64 v[180:181], v[132:133], 0, s[36:37]
	global_load_dwordx2 v[210:211], v[180:181], off
	v_lshl_add_u64 v[180:181], v[132:133], 0, s[38:39]
	global_load_dwordx2 v[212:213], v[180:181], off
	v_mfma_f32_16x16x32_bf16 v[18:21], v[142:145], v[230:233], v[18:21]
	v_mfma_f32_16x16x32_bf16 v[22:25], v[146:149], v[230:233], v[22:25]
	v_mfma_f32_16x16x32_bf16 v[26:29], v[156:159], v[230:233], v[26:29]
	v_mfma_f32_16x16x32_bf16 v[30:33], v[160:163], v[230:233], v[30:33]
	v_lshl_add_u64 v[180:181], v[132:133], 0, s[40:41]
	global_load_dwordx2 v[214:215], v[180:181], off
	v_lshl_add_u64 v[180:181], v[132:133], 0, s[42:43]
	global_load_dwordx2 v[216:217], v[180:181], off
	v_mfma_f32_16x16x32_bf16 v[2:5], v[142:145], v[234:237], v[2:5]
	v_mfma_f32_16x16x32_bf16 v[6:9], v[146:149], v[234:237], v[6:9]
	v_mfma_f32_16x16x32_bf16 v[10:13], v[156:159], v[234:237], v[10:13]
	v_mfma_f32_16x16x32_bf16 v[14:17], v[160:163], v[234:237], v[14:17]
	s_waitcnt vmcnt(21)
	s_waitcnt lgkmcnt(0)
	s_barrier
; #define MD_GLDS_A(buf, tau) do { _Pragma("unroll") for (int i = 0; i < 5; ++i) if (amask & (1u << i)) \
;         __builtin_amdgcn_global_load_lds((const unsigned*)((const char*)HIDp + aoff[i] + (size_t)((tau) & 7) * 128), (PG8_LAS unsigned*)(MD_SA(buf) + wid * 1024 + i * 8192), 16, 0, 0); } while (0)
; #define MD_B_ISSUE(sb, tau) do { const char* kb_ = Bb + (size_t)((tau) >> 3) * 512 + (size_t)((tau) & 7) * (64 * (size_t)RB); _Pragma("unroll") for (int j = 0; j < 8; ++j) { const char* p_ = kb_ + (size_t)j * RB; \
;         asm volatile("global_load_dwordx2 %0, %1, off" : "=&v"(sb[j]) : "v"(p_) : "memory"); } } while (0)
; #define MD_B_WAIT(sb, N) asm volatile("s_waitcnt vmcnt(%8)" : "+v"(sb[0]), "+v"(sb[1]), "+v"(sb[2]), "+v"(sb[3]), "+v"(sb[4]), "+v"(sb[5]), "+v"(sb[6]), "+v"(sb[7]) : "n"(N) : "memory")
; #define MD_END(last) do { if (last) asm volatile("s_waitcnt vmcnt(0)" ::: "memory"); else asm volatile("s_waitcnt vmcnt(8)" ::: "memory"); \
;         asm volatile("s_waitcnt lgkmcnt(0)" ::: "memory"); __builtin_amdgcn_s_barrier(); asm volatile("" ::: "memory"); } while (0)
; __device__ __forceinline__ void moe_down_stream(PG8_LAS unsigned char* lds, int e, int cb0, int slot0, int nv, const bf16_t* HIDp, const float* Wd, bf16_t* Y, const float* slot_w, const int* slot_dst) {
;     ...
;     for (int t = 0; t < NT; t += 2) {
;         if (t + 2 < NT) MD_B_WAIT(s1, 8); else MD_B_WAIT(s1, 0);
;         MD_B_WRITE(s1, 1); __builtin_amdgcn_sched_barrier(0); MD_GLDS_A(1, t + 1); __builtin_amdgcn_sched_barrier(0);
;         if (t + 3 < NT) MD_B_ISSUE(s1, t + 3);
;         MD_COMPUTE(0);
;         MD_END(t + 3 >= NT);
;         if (t + 2 < NT) { MD_B_WAIT(s0, 8); MD_B_WRITE(s0, 0); __builtin_amdgcn_sched_barrier(0); MD_GLDS_A(0, t + 2); __builtin_amdgcn_sched_barrier(0); }
;         if (t + 4 < NT) MD_B_ISSUE(s0, t + 4);
;         MD_COMPUTE(1);
;         MD_END(t + 4 >= NT);
	s_mov_b32 s49, s46
	s_mov_b32 s46, s47
	s_mov_b32 s47, s48
	s_mov_b32 s48, s49
	s_add_i32 s50, s50, 1
	v_cvt_pk_bf16_f32 v172, v98, v100
	v_cvt_pk_bf16_f32 v173, v102, v104
	v_cvt_pk_bf16_f32 v174, v106, v108
	v_cvt_pk_bf16_f32 v175, v110, v112
	v_cvt_pk_bf16_f32 v176, v99, v101
	v_cvt_pk_bf16_f32 v177, v103, v105
	v_cvt_pk_bf16_f32 v178, v107, v109
	v_cvt_pk_bf16_f32 v179, v111, v113
	ds_write_b128 v95, v[172:175] offset:0
	ds_write_b128 v95, v[176:179] offset:128
	v_add_u32_e32 v91, s46, v135
	v_add_u32_e32 v93, s46, v137
	ds_read_b128 v[238:241], v139 offset:19456
	ds_read_b128 v[242:245], v139 offset:21504
	ds_read_b128 v[246:249], v139 offset:23552
	ds_read_b128 v[250:253], v139 offset:25600
	ds_read_b128 v[218:221], v91 offset:0
	ds_read_b128 v[222:225], v91 offset:2048
	ds_read_b128 v[226:229], v91 offset:4096
	ds_read_b128 v[230:233], v91 offset:6144
	ds_read_b128 v[234:237], v91 offset:8192
	s_add_i32 s49, s48, s74
	s_add_i32 s52, s52, 1
	s_and_b32 s54, s52, 7
	s_cmp_eq_u32 s54, 0
	s_cselect_b32 s54, s53, s32
	s_cselect_b32 s55, -1, 0
	s_add_u32 s30, s30, s54
	s_addc_u32 s31, s31, s55
	s_waitcnt lgkmcnt(0)
	v_mfma_f32_16x16x32_bf16 v[78:81], v[238:241], v[218:221], v[78:81]
	v_mfma_f32_16x16x32_bf16 v[74:77], v[242:245], v[218:221], v[74:77]
	v_mfma_f32_16x16x32_bf16 v[70:73], v[246:249], v[218:221], v[70:73]
	v_mfma_f32_16x16x32_bf16 v[66:69], v[250:253], v[218:221], v[66:69]
	ds_read_b128 v[218:221], v93 offset:0
	ds_read_b128 v[142:145], v141 offset:19456
	s_mov_b32 m0, s49
	s_nop 0
	global_load_lds_dwordx4 v88, s[30:31]
	v_mfma_f32_16x16x32_bf16 v[62:65], v[238:241], v[222:225], v[62:65]
	v_mfma_f32_16x16x32_bf16 v[58:61], v[242:245], v[222:225], v[58:61]
	v_mfma_f32_16x16x32_bf16 v[54:57], v[246:249], v[222:225], v[54:57]
	v_mfma_f32_16x16x32_bf16 v[50:53], v[250:253], v[222:225], v[50:53]
	ds_read_b128 v[222:225], v93 offset:2048
	ds_read_b128 v[146:149], v141 offset:21504
	s_add_i32 m0, s49, 0x2000
	s_nop 0
	global_load_lds_dwordx4 v90, s[30:31]
	v_mfma_f32_16x16x32_bf16 v[46:49], v[238:241], v[226:229], v[46:49]
	v_mfma_f32_16x16x32_bf16 v[42:45], v[242:245], v[226:229], v[42:45]
	v_mfma_f32_16x16x32_bf16 v[38:41], v[246:249], v[226:229], v[38:41]
	v_mfma_f32_16x16x32_bf16 v[34:37], v[250:253], v[226:229], v[34:37]
	ds_read_b128 v[226:229], v93 offset:4096
	ds_read_b128 v[156:159], v141 offset:23552
	s_add_i32 m0, s49, 0x4000
	s_nop 0
	global_load_lds_dwordx4 v92, s[30:31]
	v_mfma_f32_16x16x32_bf16 v[18:21], v[238:241], v[230:233], v[18:21]
	v_mfma_f32_16x16x32_bf16 v[22:25], v[242:245], v[230:233], v[22:25]
	v_mfma_f32_16x16x32_bf16 v[26:29], v[246:249], v[230:233], v[26:29]
	v_mfma_f32_16x16x32_bf16 v[30:33], v[250:253], v[230:233], v[30:33]
	ds_read_b128 v[230:233], v93 offset:6144
	ds_read_b128 v[160:163], v141 offset:25600
	s_add_i32 m0, s49, 0x6000
	s_nop 0
	global_load_lds_dwordx4 v94, s[30:31]
	v_mfma_f32_16x16x32_bf16 v[2:5], v[238:241], v[234:237], v[2:5]
	v_mfma_f32_16x16x32_bf16 v[6:9], v[242:245], v[234:237], v[6:9]
	v_mfma_f32_16x16x32_bf16 v[10:13], v[246:249], v[234:237], v[10:13]
	v_mfma_f32_16x16x32_bf16 v[14:17], v[250:253], v[234:237], v[14:17]
	ds_read_b128 v[234:237], v93 offset:8192
	s_add_i32 m0, s49, 0x8000
	s_nop 0
	global_load_lds_dwordx4 v96, s[30:31]
	s_waitcnt lgkmcnt(0)
	v_mfma_f32_16x16x32_bf16 v[78:81], v[142:145], v[218:221], v[78:81]
	v_mfma_f32_16x16x32_bf16 v[74:77], v[146:149], v[218:221], v[74:77]
	v_mfma_f32_16x16x32_bf16 v[70:73], v[156:159], v[218:221], v[70:73]
	v_mfma_f32_16x16x32_bf16 v[66:69], v[160:163], v[218:221], v[66:69]
	v_mfma_f32_16x16x32_bf16 v[62:65], v[142:145], v[222:225], v[62:65]
	v_mfma_f32_16x16x32_bf16 v[58:61], v[146:149], v[222:225], v[58:61]
	v_mfma_f32_16x16x32_bf16 v[54:57], v[156:159], v[222:225], v[54:57]
	v_mfma_f32_16x16x32_bf16 v[50:53], v[160:163], v[222:225], v[50:53]
	v_mfma_f32_16x16x32_bf16 v[46:49], v[142:145], v[226:229], v[46:49]
	v_mfma_f32_16x16x32_bf16 v[42:45], v[146:149], v[226:229], v[42:45]
	v_mfma_f32_16x16x32_bf16 v[38:41], v[156:159], v[226:229], v[38:41]
	v_mfma_f32_16x16x32_bf16 v[34:37], v[160:163], v[226:229], v[34:37]
	v_mfma_f32_16x16x32_bf16 v[18:21], v[142:145], v[230:233], v[18:21]
	v_mfma_f32_16x16x32_bf16 v[22:25], v[146:149], v[230:233], v[22:25]
	v_mfma_f32_16x16x32_bf16 v[26:29], v[156:159], v[230:233], v[26:29]
	v_mfma_f32_16x16x32_bf16 v[30:33], v[160:163], v[230:233], v[30:33]
	v_mfma_f32_16x16x32_bf16 v[2:5], v[142:145], v[234:237], v[2:5]
	v_mfma_f32_16x16x32_bf16 v[6:9], v[146:149], v[234:237], v[6:9]
	v_mfma_f32_16x16x32_bf16 v[10:13], v[156:159], v[234:237], v[10:13]
	v_mfma_f32_16x16x32_bf16 v[14:17], v[160:163], v[234:237], v[14:17]
	s_waitcnt vmcnt(13)
	s_waitcnt lgkmcnt(0)
	s_barrier
; #define MD_GLDS_A(buf, tau) do { _Pragma("unroll") for (int i = 0; i < 5; ++i) if (amask & (1u << i)) \
;         __builtin_amdgcn_global_load_lds((const unsigned*)((const char*)HIDp + aoff[i] + (size_t)((tau) & 7) * 128), (PG8_LAS unsigned*)(MD_SA(buf) + wid * 1024 + i * 8192), 16, 0, 0); } while (0)
; #define MD_B_ISSUE(sb, tau) do { const char* kb_ = Bb + (size_t)((tau) >> 3) * 512 + (size_t)((tau) & 7) * (64 * (size_t)RB); _Pragma("unroll") for (int j = 0; j < 8; ++j) { const char* p_ = kb_ + (size_t)j * RB; \
;         asm volatile("global_load_dwordx2 %0, %1, off" : "=&v"(sb[j]) : "v"(p_) : "memory"); } } while (0)
; #define MD_B_WAIT(sb, N) asm volatile("s_waitcnt vmcnt(%8)" : "+v"(sb[0]), "+v"(sb[1]), "+v"(sb[2]), "+v"(sb[3]), "+v"(sb[4]), "+v"(sb[5]), "+v"(sb[6]), "+v"(sb[7]) : "n"(N) : "memory")
; __device__ __forceinline__ void moe_down_stream(PG8_LAS unsigned char* lds, int e, int cb0, int slot0, int nv, const bf16_t* HIDp, const float* Wd, bf16_t* Y, const float* slot_w, const int* slot_dst) {
;     ...
;     f32x4 acc[DNM][4];
; #pragma unroll
;     for (int m = 0; m < DNM; ++m)
; #pragma unroll
;         for (int n = 0; n < 4; ++n) acc[m][n] = (f32x4){0.f, 0.f, 0.f, 0.f};
;     f32x2 s0[8], s1[8];
;     MD_GLDS_A(0, 0); MD_B_ISSUE(s0, 0); MD_B_ISSUE(s1, 1);
;     MD_B_WAIT(s0, 8); MD_B_WRITE(s0, 0); __builtin_amdgcn_sched_barrier(0); MD_B_ISSUE(s0, 2);
;     asm volatile("s_waitcnt vmcnt(16)" ::: "memory");
;     asm volatile("s_waitcnt lgkmcnt(0)" ::: "memory"); __builtin_amdgcn_s_barrier(); asm volatile("" ::: "memory");
; #pragma unroll 1
;     for (int t = 0; t < NT; t += 2) {
;         if (t + 2 < NT) MD_B_WAIT(s1, 8); else MD_B_WAIT(s1, 0);
;         MD_B_WRITE(s1, 1); __builtin_amdgcn_sched_barrier(0); MD_GLDS_A(1, t + 1); __builtin_amdgcn_sched_barrier(0);
;         if (t + 3 < NT) MD_B_ISSUE(s1, t + 3);
;         MD_COMPUTE(0);
;         MD_END(t + 3 >= NT);
;         if (t + 2 < NT) { MD_B_WAIT(s0, 8); MD_B_WRITE(s0, 0); __builtin_amdgcn_sched_barrier(0); MD_GLDS_A(0, t + 2); __builtin_amdgcn_sched_barrier(0); }
;         if (t + 4 < NT) MD_B_ISSUE(s0, t + 4);
;         MD_COMPUTE(1);
;         MD_END(t + 4 >= NT);
	s_mov_b32 s49, s46
	s_mov_b32 s46, s47
	s_mov_b32 s47, s48
	s_mov_b32 s48, s49
	s_add_i32 s50, s50, 1
	v_cvt_pk_bf16_f32 v172, v114, v116
	v_cvt_pk_bf16_f32 v173, v118, v120
	v_cvt_pk_bf16_f32 v174, v122, v124
	v_cvt_pk_bf16_f32 v175, v126, v128
	v_cvt_pk_bf16_f32 v176, v115, v117
	v_cvt_pk_bf16_f32 v177, v119, v121
	v_cvt_pk_bf16_f32 v178, v123, v125
	v_cvt_pk_bf16_f32 v179, v127, v129
	ds_write_b128 v95, v[172:175] offset:19456
	ds_write_b128 v95, v[176:179] offset:19584
	v_add_u32_e32 v91, s46, v135
	v_add_u32_e32 v93, s46, v137
	ds_read_b128 v[238:241], v139 offset:0
	ds_read_b128 v[242:245], v139 offset:2048
	ds_read_b128 v[246:249], v139 offset:4096
	ds_read_b128 v[250:253], v139 offset:6144
	ds_read_b128 v[218:221], v91 offset:0
	ds_read_b128 v[222:225], v91 offset:2048
	ds_read_b128 v[226:229], v91 offset:4096
	ds_read_b128 v[230:233], v91 offset:6144
	ds_read_b128 v[234:237], v91 offset:8192
	s_add_i32 s49, s48, s74
	s_add_i32 s52, s52, 1
	s_and_b32 s54, s52, 7
	s_cmp_eq_u32 s54, 0
	s_cselect_b32 s54, s53, s32
	s_cselect_b32 s55, -1, 0
	s_add_u32 s30, s30, s54
	s_addc_u32 s31, s31, s55
	s_waitcnt lgkmcnt(0)
	v_mfma_f32_16x16x32_bf16 v[78:81], v[238:241], v[218:221], v[78:81]
	v_mfma_f32_16x16x32_bf16 v[74:77], v[242:245], v[218:221], v[74:77]
	v_mfma_f32_16x16x32_bf16 v[70:73], v[246:249], v[218:221], v[70:73]
	v_mfma_f32_16x16x32_bf16 v[66:69], v[250:253], v[218:221], v[66:69]
	ds_read_b128 v[218:221], v93 offset:0
	ds_read_b128 v[142:145], v141 offset:0
	s_mov_b32 m0, s49
	s_nop 0
	global_load_lds_dwordx4 v88, s[30:31]
	v_mfma_f32_16x16x32_bf16 v[62:65], v[238:241], v[222:225], v[62:65]
	v_mfma_f32_16x16x32_bf16 v[58:61], v[242:245], v[222:225], v[58:61]
	v_mfma_f32_16x16x32_bf16 v[54:57], v[246:249], v[222:225], v[54:57]
	v_mfma_f32_16x16x32_bf16 v[50:53], v[250:253], v[222:225], v[50:53]
	ds_read_b128 v[222:225], v93 offset:2048
	ds_read_b128 v[146:149], v141 offset:2048
	s_add_i32 m0, s49, 0x2000
	s_nop 0
	global_load_lds_dwordx4 v90, s[30:31]
	v_mfma_f32_16x16x32_bf16 v[46:49], v[238:241], v[226:229], v[46:49]
	v_mfma_f32_16x16x32_bf16 v[42:45], v[242:245], v[226:229], v[42:45]
	v_mfma_f32_16x16x32_bf16 v[38:41], v[246:249], v[226:229], v[38:41]
	v_mfma_f32_16x16x32_bf16 v[34:37], v[250:253], v[226:229], v[34:37]
	ds_read_b128 v[226:229], v93 offset:4096
	ds_read_b128 v[156:159], v141 offset:4096
	s_add_i32 m0, s49, 0x4000
	s_nop 0
	global_load_lds_dwordx4 v92, s[30:31]
	v_mfma_f32_16x16x32_bf16 v[18:21], v[238:241], v[230:233], v[18:21]
	v_mfma_f32_16x16x32_bf16 v[22:25], v[242:245], v[230:233], v[22:25]
	v_mfma_f32_16x16x32_bf16 v[26:29], v[246:249], v[230:233], v[26:29]
	v_mfma_f32_16x16x32_bf16 v[30:33], v[250:253], v[230:233], v[30:33]
	ds_read_b128 v[230:233], v93 offset:6144
	ds_read_b128 v[160:163], v141 offset:6144
	s_add_i32 m0, s49, 0x6000
	s_nop 0
	global_load_lds_dwordx4 v94, s[30:31]
	v_mfma_f32_16x16x32_bf16 v[2:5], v[238:241], v[234:237], v[2:5]
	v_mfma_f32_16x16x32_bf16 v[6:9], v[242:245], v[234:237], v[6:9]
	v_mfma_f32_16x16x32_bf16 v[10:13], v[246:249], v[234:237], v[10:13]
	v_mfma_f32_16x16x32_bf16 v[14:17], v[250:253], v[234:237], v[14:17]
	ds_read_b128 v[234:237], v93 offset:8192
	s_add_i32 m0, s49, 0x8000
	s_nop 0
	global_load_lds_dwordx4 v96, s[30:31]
	s_waitcnt lgkmcnt(0)
	v_mfma_f32_16x16x32_bf16 v[78:81], v[142:145], v[218:221], v[78:81]
	v_mfma_f32_16x16x32_bf16 v[74:77], v[146:149], v[218:221], v[74:77]
	v_mfma_f32_16x16x32_bf16 v[70:73], v[156:159], v[218:221], v[70:73]
	v_mfma_f32_16x16x32_bf16 v[66:69], v[160:163], v[218:221], v[66:69]
	v_mfma_f32_16x16x32_bf16 v[62:65], v[142:145], v[222:225], v[62:65]
	v_mfma_f32_16x16x32_bf16 v[58:61], v[146:149], v[222:225], v[58:61]
	v_mfma_f32_16x16x32_bf16 v[54:57], v[156:159], v[222:225], v[54:57]
	v_mfma_f32_16x16x32_bf16 v[50:53], v[160:163], v[222:225], v[50:53]
	v_mfma_f32_16x16x32_bf16 v[46:49], v[142:145], v[226:229], v[46:49]
	v_mfma_f32_16x16x32_bf16 v[42:45], v[146:149], v[226:229], v[42:45]
	v_mfma_f32_16x16x32_bf16 v[38:41], v[156:159], v[226:229], v[38:41]
	v_mfma_f32_16x16x32_bf16 v[34:37], v[160:163], v[226:229], v[34:37]
	v_mfma_f32_16x16x32_bf16 v[18:21], v[142:145], v[230:233], v[18:21]
	v_mfma_f32_16x16x32_bf16 v[22:25], v[146:149], v[230:233], v[22:25]
	v_mfma_f32_16x16x32_bf16 v[26:29], v[156:159], v[230:233], v[26:29]
	v_mfma_f32_16x16x32_bf16 v[30:33], v[160:163], v[230:233], v[30:33]
	v_mfma_f32_16x16x32_bf16 v[2:5], v[142:145], v[234:237], v[2:5]
	v_mfma_f32_16x16x32_bf16 v[6:9], v[146:149], v[234:237], v[6:9]
	v_mfma_f32_16x16x32_bf16 v[10:13], v[156:159], v[234:237], v[10:13]
	v_mfma_f32_16x16x32_bf16 v[14:17], v[160:163], v[234:237], v[14:17]
	s_waitcnt vmcnt(5)
	s_waitcnt lgkmcnt(0)
	s_barrier
; #define MD_GLDS_A(buf, tau) do { _Pragma("unroll") for (int i = 0; i < 5; ++i) if (amask & (1u << i)) \
;         __builtin_amdgcn_global_load_lds((const unsigned*)((const char*)HIDp + aoff[i] + (size_t)((tau) & 7) * 128), (PG8_LAS unsigned*)(MD_SA(buf) + wid * 1024 + i * 8192), 16, 0, 0); } while (0)
; #define MD_B_ISSUE(sb, tau) do { const char* kb_ = Bb + (size_t)((tau) >> 3) * 512 + (size_t)((tau) & 7) * (64 * (size_t)RB); _Pragma("unroll") for (int j = 0; j < 8; ++j) { const char* p_ = kb_ + (size_t)j * RB; \
;         asm volatile("global_load_dwordx2 %0, %1, off" : "=&v"(sb[j]) : "v"(p_) : "memory"); } } while (0)
; #define MD_B_WAIT(sb, N) asm volatile("s_waitcnt vmcnt(%8)" : "+v"(sb[0]), "+v"(sb[1]), "+v"(sb[2]), "+v"(sb[3]), "+v"(sb[4]), "+v"(sb[5]), "+v"(sb[6]), "+v"(sb[7]) : "n"(N) : "memory")
; __device__ __forceinline__ void moe_down_stream(PG8_LAS unsigned char* lds, int e, int cb0, int slot0, int nv, const bf16_t* HIDp, const float* Wd, bf16_t* Y, const float* slot_w, const int* slot_dst) {
;     ...
;     f32x4 acc[DNM][4];
; #pragma unroll
;     for (int m = 0; m < DNM; ++m)
; #pragma unroll
;         for (int n = 0; n < 4; ++n) acc[m][n] = (f32x4){0.f, 0.f, 0.f, 0.f};
;     f32x2 s0[8], s1[8];
;     MD_GLDS_A(0, 0); MD_B_ISSUE(s0, 0); MD_B_ISSUE(s1, 1);
;     MD_B_WAIT(s0, 8); MD_B_WRITE(s0, 0); __builtin_amdgcn_sched_barrier(0); MD_B_ISSUE(s0, 2);
;     asm volatile("s_waitcnt vmcnt(16)" ::: "memory");
;     asm volatile("s_waitcnt lgkmcnt(0)" ::: "memory"); __builtin_amdgcn_s_barrier(); asm volatile("" ::: "memory");
; #pragma unroll 1
;     for (int t = 0; t < NT; t += 2) {
;         if (t + 2 < NT) MD_B_WAIT(s1, 8); else MD_B_WAIT(s1, 0);
;         MD_B_WRITE(s1, 1); __builtin_amdgcn_sched_barrier(0); MD_GLDS_A(1, t + 1); __builtin_amdgcn_sched_barrier(0);
;         if (t + 3 < NT) MD_B_ISSUE(s1, t + 3);
;         MD_COMPUTE(0);
;         MD_END(t + 3 >= NT);
;         if (t + 2 < NT) { MD_B_WAIT(s0, 8); MD_B_WRITE(s0, 0); __builtin_amdgcn_sched_barrier(0); MD_GLDS_A(0, t + 2); __builtin_amdgcn_sched_barrier(0); }
;         if (t + 4 < NT) MD_B_ISSUE(s0, t + 4);
;         MD_COMPUTE(1);
;         MD_END(t + 4 >= NT);
	s_mov_b32 s49, s46
	s_mov_b32 s46, s47
	s_mov_b32 s47, s48
	s_mov_b32 s48, s49
	s_add_i32 s50, s50, 1
	v_cvt_pk_bf16_f32 v172, v186, v188
	v_cvt_pk_bf16_f32 v173, v190, v192
	v_cvt_pk_bf16_f32 v174, v194, v196
	v_cvt_pk_bf16_f32 v175, v198, v200
	v_cvt_pk_bf16_f32 v176, v187, v189
	v_cvt_pk_bf16_f32 v177, v191, v193
	v_cvt_pk_bf16_f32 v178, v195, v197
	v_cvt_pk_bf16_f32 v179, v199, v201
	ds_write_b128 v95, v[172:175] offset:0
	ds_write_b128 v95, v[176:179] offset:128
	v_add_u32_e32 v91, s46, v135
	v_add_u32_e32 v93, s46, v137
	ds_read_b128 v[238:241], v139 offset:19456
	ds_read_b128 v[242:245], v139 offset:21504
	ds_read_b128 v[246:249], v139 offset:23552
	ds_read_b128 v[250:253], v139 offset:25600
	ds_read_b128 v[218:221], v91 offset:0
	ds_read_b128 v[222:225], v91 offset:2048
	ds_read_b128 v[226:229], v91 offset:4096
	ds_read_b128 v[230:233], v91 offset:6144
	ds_read_b128 v[234:237], v91 offset:8192
	s_add_i32 s49, s48, s74
	s_add_i32 s52, s52, 1
	s_and_b32 s54, s52, 7
	s_cmp_eq_u32 s54, 0
	s_cselect_b32 s54, s53, s32
	s_cselect_b32 s55, -1, 0
	s_add_u32 s30, s30, s54
	s_addc_u32 s31, s31, s55
	s_waitcnt lgkmcnt(0)
	v_mfma_f32_16x16x32_bf16 v[78:81], v[238:241], v[218:221], v[78:81]
	v_mfma_f32_16x16x32_bf16 v[74:77], v[242:245], v[218:221], v[74:77]
	v_mfma_f32_16x16x32_bf16 v[70:73], v[246:249], v[218:221], v[70:73]
	v_mfma_f32_16x16x32_bf16 v[66:69], v[250:253], v[218:221], v[66:69]
	ds_read_b128 v[218:221], v93 offset:0
	ds_read_b128 v[142:145], v141 offset:19456
	s_mov_b32 m0, s49
	s_nop 0
	global_load_lds_dwordx4 v88, s[30:31]
	v_mfma_f32_16x16x32_bf16 v[62:65], v[238:241], v[222:225], v[62:65]
	v_mfma_f32_16x16x32_bf16 v[58:61], v[242:245], v[222:225], v[58:61]
	v_mfma_f32_16x16x32_bf16 v[54:57], v[246:249], v[222:225], v[54:57]
	v_mfma_f32_16x16x32_bf16 v[50:53], v[250:253], v[222:225], v[50:53]
	ds_read_b128 v[222:225], v93 offset:2048
	ds_read_b128 v[146:149], v141 offset:21504
	s_add_i32 m0, s49, 0x2000
	s_nop 0
	global_load_lds_dwordx4 v90, s[30:31]
	v_mfma_f32_16x16x32_bf16 v[46:49], v[238:241], v[226:229], v[46:49]
	v_mfma_f32_16x16x32_bf16 v[42:45], v[242:245], v[226:229], v[42:45]
	v_mfma_f32_16x16x32_bf16 v[38:41], v[246:249], v[226:229], v[38:41]
	v_mfma_f32_16x16x32_bf16 v[34:37], v[250:253], v[226:229], v[34:37]
	ds_read_b128 v[226:229], v93 offset:4096
	ds_read_b128 v[156:159], v141 offset:23552
	s_add_i32 m0, s49, 0x4000
	s_nop 0
	global_load_lds_dwordx4 v92, s[30:31]
	v_mfma_f32_16x16x32_bf16 v[18:21], v[238:241], v[230:233], v[18:21]
	v_mfma_f32_16x16x32_bf16 v[22:25], v[242:245], v[230:233], v[22:25]
	v_mfma_f32_16x16x32_bf16 v[26:29], v[246:249], v[230:233], v[26:29]
	v_mfma_f32_16x16x32_bf16 v[30:33], v[250:253], v[230:233], v[30:33]
	ds_read_b128 v[230:233], v93 offset:6144
	ds_read_b128 v[160:163], v141 offset:25600
	s_add_i32 m0, s49, 0x6000
	s_nop 0
	global_load_lds_dwordx4 v94, s[30:31]
	v_mfma_f32_16x16x32_bf16 v[2:5], v[238:241], v[234:237], v[2:5]
	v_mfma_f32_16x16x32_bf16 v[6:9], v[242:245], v[234:237], v[6:9]
	v_mfma_f32_16x16x32_bf16 v[10:13], v[246:249], v[234:237], v[10:13]
	v_mfma_f32_16x16x32_bf16 v[14:17], v[250:253], v[234:237], v[14:17]
	ds_read_b128 v[234:237], v93 offset:8192
	s_add_i32 m0, s49, 0x8000
	s_nop 0
	global_load_lds_dwordx4 v96, s[30:31]
	s_waitcnt lgkmcnt(0)
	v_mfma_f32_16x16x32_bf16 v[78:81], v[142:145], v[218:221], v[78:81]
	v_mfma_f32_16x16x32_bf16 v[74:77], v[146:149], v[218:221], v[74:77]
	v_mfma_f32_16x16x32_bf16 v[70:73], v[156:159], v[218:221], v[70:73]
	v_mfma_f32_16x16x32_bf16 v[66:69], v[160:163], v[218:221], v[66:69]
	v_mfma_f32_16x16x32_bf16 v[62:65], v[142:145], v[222:225], v[62:65]
	v_mfma_f32_16x16x32_bf16 v[58:61], v[146:149], v[222:225], v[58:61]
	v_mfma_f32_16x16x32_bf16 v[54:57], v[156:159], v[222:225], v[54:57]
	v_mfma_f32_16x16x32_bf16 v[50:53], v[160:163], v[222:225], v[50:53]
	v_mfma_f32_16x16x32_bf16 v[46:49], v[142:145], v[226:229], v[46:49]
	v_mfma_f32_16x16x32_bf16 v[42:45], v[146:149], v[226:229], v[42:45]
	v_mfma_f32_16x16x32_bf16 v[38:41], v[156:159], v[226:229], v[38:41]
	v_mfma_f32_16x16x32_bf16 v[34:37], v[160:163], v[226:229], v[34:37]
	v_mfma_f32_16x16x32_bf16 v[18:21], v[142:145], v[230:233], v[18:21]
	v_mfma_f32_16x16x32_bf16 v[22:25], v[146:149], v[230:233], v[22:25]
	v_mfma_f32_16x16x32_bf16 v[26:29], v[156:159], v[230:233], v[26:29]
	v_mfma_f32_16x16x32_bf16 v[30:33], v[160:163], v[230:233], v[30:33]
	v_mfma_f32_16x16x32_bf16 v[2:5], v[142:145], v[234:237], v[2:5]
	v_mfma_f32_16x16x32_bf16 v[6:9], v[146:149], v[234:237], v[6:9]
	v_mfma_f32_16x16x32_bf16 v[10:13], v[156:159], v[234:237], v[10:13]
	v_mfma_f32_16x16x32_bf16 v[14:17], v[160:163], v[234:237], v[14:17]
	s_waitcnt vmcnt(5)
	s_waitcnt lgkmcnt(0)
	s_barrier
; #define MD_GLDS_A(buf, tau) do { _Pragma("unroll") for (int i = 0; i < 5; ++i) if (amask & (1u << i)) \
;         __builtin_amdgcn_global_load_lds((const unsigned*)((const char*)HIDp + aoff[i] + (size_t)((tau) & 7) * 128), (PG8_LAS unsigned*)(MD_SA(buf) + wid * 1024 + i * 8192), 16, 0, 0); } while (0)
; #define MD_B_ISSUE(sb, tau) do { const char* kb_ = Bb + (size_t)((tau) >> 3) * 512 + (size_t)((tau) & 7) * (64 * (size_t)RB); _Pragma("unroll") for (int j = 0; j < 8; ++j) { const char* p_ = kb_ + (size_t)j * RB; \
;         asm volatile("global_load_dwordx2 %0, %1, off" : "=&v"(sb[j]) : "v"(p_) : "memory"); } } while (0)
; #define MD_B_WAIT(sb, N) asm volatile("s_waitcnt vmcnt(%8)" : "+v"(sb[0]), "+v"(sb[1]), "+v"(sb[2]), "+v"(sb[3]), "+v"(sb[4]), "+v"(sb[5]), "+v"(sb[6]), "+v"(sb[7]) : "n"(N) : "memory")
; __device__ __forceinline__ void moe_down_stream(PG8_LAS unsigned char* lds, int e, int cb0, int slot0, int nv, const bf16_t* HIDp, const float* Wd, bf16_t* Y, const float* slot_w, const int* slot_dst) {
;     ...
;     f32x4 acc[DNM][4];
; #pragma unroll
;     for (int m = 0; m < DNM; ++m)
; #pragma unroll
;         for (int n = 0; n < 4; ++n) acc[m][n] = (f32x4){0.f, 0.f, 0.f, 0.f};
;     f32x2 s0[8], s1[8];
;     MD_GLDS_A(0, 0); MD_B_ISSUE(s0, 0); MD_B_ISSUE(s1, 1);
;     MD_B_WAIT(s0, 8); MD_B_WRITE(s0, 0); __builtin_amdgcn_sched_barrier(0); MD_B_ISSUE(s0, 2);
;     asm volatile("s_waitcnt vmcnt(16)" ::: "memory");
;     asm volatile("s_waitcnt lgkmcnt(0)" ::: "memory"); __builtin_amdgcn_s_barrier(); asm volatile("" ::: "memory");
; #pragma unroll 1
;     for (int t = 0; t < NT; t += 2) {
;         if (t + 2 < NT) MD_B_WAIT(s1, 8); else MD_B_WAIT(s1, 0);
;         MD_B_WRITE(s1, 1); __builtin_amdgcn_sched_barrier(0); MD_GLDS_A(1, t + 1); __builtin_amdgcn_sched_barrier(0);
;         if (t + 3 < NT) MD_B_ISSUE(s1, t + 3);
;         MD_COMPUTE(0);
;         MD_END(t + 3 >= NT);
;         if (t + 2 < NT) { MD_B_WAIT(s0, 8); MD_B_WRITE(s0, 0); __builtin_amdgcn_sched_barrier(0); MD_GLDS_A(0, t + 2); __builtin_amdgcn_sched_barrier(0); }
;         if (t + 4 < NT) MD_B_ISSUE(s0, t + 4);
;         MD_COMPUTE(1);
;         MD_END(t + 4 >= NT);
	s_mov_b32 s49, s46
	s_mov_b32 s46, s47
	s_mov_b32 s47, s48
	s_mov_b32 s48, s49
	s_add_i32 s50, s50, 1
	v_cvt_pk_bf16_f32 v172, v202, v204
	v_cvt_pk_bf16_f32 v173, v206, v208
	v_cvt_pk_bf16_f32 v174, v210, v212
	v_cvt_pk_bf16_f32 v175, v214, v216
	v_cvt_pk_bf16_f32 v176, v203, v205
	v_cvt_pk_bf16_f32 v177, v207, v209
	v_cvt_pk_bf16_f32 v178, v211, v213
	v_cvt_pk_bf16_f32 v179, v215, v217
	ds_write_b128 v95, v[172:175] offset:19456
	ds_write_b128 v95, v[176:179] offset:19584
	v_add_u32_e32 v91, s46, v135
	v_add_u32_e32 v93, s46, v137
	ds_read_b128 v[238:241], v139 offset:0
	ds_read_b128 v[242:245], v139 offset:2048
	ds_read_b128 v[246:249], v139 offset:4096
	ds_read_b128 v[250:253], v139 offset:6144
	ds_read_b128 v[218:221], v91 offset:0
	ds_read_b128 v[222:225], v91 offset:2048
	ds_read_b128 v[226:229], v91 offset:4096
	ds_read_b128 v[230:233], v91 offset:6144
	ds_read_b128 v[234:237], v91 offset:8192
	s_waitcnt lgkmcnt(0)
	v_mfma_f32_16x16x32_bf16 v[78:81], v[238:241], v[218:221], v[78:81]
	v_mfma_f32_16x16x32_bf16 v[74:77], v[242:245], v[218:221], v[74:77]
	v_mfma_f32_16x16x32_bf16 v[70:73], v[246:249], v[218:221], v[70:73]
	v_mfma_f32_16x16x32_bf16 v[66:69], v[250:253], v[218:221], v[66:69]
	ds_read_b128 v[218:221], v93 offset:0
	ds_read_b128 v[142:145], v141 offset:0
	v_mfma_f32_16x16x32_bf16 v[62:65], v[238:241], v[222:225], v[62:65]
	v_mfma_f32_16x16x32_bf16 v[58:61], v[242:245], v[222:225], v[58:61]
	v_mfma_f32_16x16x32_bf16 v[54:57], v[246:249], v[222:225], v[54:57]
	v_mfma_f32_16x16x32_bf16 v[50:53], v[250:253], v[222:225], v[50:53]
	ds_read_b128 v[222:225], v93 offset:2048
	ds_read_b128 v[146:149], v141 offset:2048
	v_mfma_f32_16x16x32_bf16 v[46:49], v[238:241], v[226:229], v[46:49]
	v_mfma_f32_16x16x32_bf16 v[42:45], v[242:245], v[226:229], v[42:45]
	v_mfma_f32_16x16x32_bf16 v[38:41], v[246:249], v[226:229], v[38:41]
	v_mfma_f32_16x16x32_bf16 v[34:37], v[250:253], v[226:229], v[34:37]
	ds_read_b128 v[226:229], v93 offset:4096
	ds_read_b128 v[156:159], v141 offset:4096
	v_mfma_f32_16x16x32_bf16 v[18:21], v[238:241], v[230:233], v[18:21]
	v_mfma_f32_16x16x32_bf16 v[22:25], v[242:245], v[230:233], v[22:25]
	v_mfma_f32_16x16x32_bf16 v[26:29], v[246:249], v[230:233], v[26:29]
	v_mfma_f32_16x16x32_bf16 v[30:33], v[250:253], v[230:233], v[30:33]
	ds_read_b128 v[230:233], v93 offset:6144
	ds_read_b128 v[160:163], v141 offset:6144
	v_mfma_f32_16x16x32_bf16 v[2:5], v[238:241], v[234:237], v[2:5]
	v_mfma_f32_16x16x32_bf16 v[6:9], v[242:245], v[234:237], v[6:9]
	v_mfma_f32_16x16x32_bf16 v[10:13], v[246:249], v[234:237], v[10:13]
	v_mfma_f32_16x16x32_bf16 v[14:17], v[250:253], v[234:237], v[14:17]
	ds_read_b128 v[234:237], v93 offset:8192
	s_waitcnt lgkmcnt(0)
	v_mfma_f32_16x16x32_bf16 v[78:81], v[142:145], v[218:221], v[78:81]
	v_mfma_f32_16x16x32_bf16 v[74:77], v[146:149], v[218:221], v[74:77]
	v_mfma_f32_16x16x32_bf16 v[70:73], v[156:159], v[218:221], v[70:73]
	v_mfma_f32_16x16x32_bf16 v[66:69], v[160:163], v[218:221], v[66:69]
	v_mfma_f32_16x16x32_bf16 v[62:65], v[142:145], v[222:225], v[62:65]
	v_mfma_f32_16x16x32_bf16 v[58:61], v[146:149], v[222:225], v[58:61]
	v_mfma_f32_16x16x32_bf16 v[54:57], v[156:159], v[222:225], v[54:57]
	v_mfma_f32_16x16x32_bf16 v[50:53], v[160:163], v[222:225], v[50:53]
	v_mfma_f32_16x16x32_bf16 v[46:49], v[142:145], v[226:229], v[46:49]
	v_mfma_f32_16x16x32_bf16 v[42:45], v[146:149], v[226:229], v[42:45]
	v_mfma_f32_16x16x32_bf16 v[38:41], v[156:159], v[226:229], v[38:41]
	v_mfma_f32_16x16x32_bf16 v[34:37], v[160:163], v[226:229], v[34:37]
	v_mfma_f32_16x16x32_bf16 v[18:21], v[142:145], v[230:233], v[18:21]
	v_mfma_f32_16x16x32_bf16 v[22:25], v[146:149], v[230:233], v[22:25]
	v_mfma_f32_16x16x32_bf16 v[26:29], v[156:159], v[230:233], v[26:29]
	v_mfma_f32_16x16x32_bf16 v[30:33], v[160:163], v[230:233], v[30:33]
	v_mfma_f32_16x16x32_bf16 v[2:5], v[142:145], v[234:237], v[2:5]
	v_mfma_f32_16x16x32_bf16 v[6:9], v[146:149], v[234:237], v[6:9]
	v_mfma_f32_16x16x32_bf16 v[10:13], v[156:159], v[234:237], v[10:13]
	v_mfma_f32_16x16x32_bf16 v[14:17], v[160:163], v[234:237], v[14:17]
	s_waitcnt vmcnt(0)
	s_waitcnt lgkmcnt(0)
	s_barrier
	s_mov_b32 s49, s46
	s_mov_b32 s46, s47
	s_mov_b32 s47, s48
	s_mov_b32 s48, s49
	s_add_i32 s50, s50, 1
	v_add_u32_e32 v91, s46, v135
	v_add_u32_e32 v93, s46, v137
	ds_read_b128 v[238:241], v139 offset:19456
	ds_read_b128 v[242:245], v139 offset:21504
	ds_read_b128 v[246:249], v139 offset:23552
	ds_read_b128 v[250:253], v139 offset:25600
	ds_read_b128 v[218:221], v91 offset:0
	ds_read_b128 v[222:225], v91 offset:2048
	ds_read_b128 v[226:229], v91 offset:4096
	ds_read_b128 v[230:233], v91 offset:6144
	ds_read_b128 v[234:237], v91 offset:8192
	s_waitcnt lgkmcnt(0)
	v_mfma_f32_16x16x32_bf16 v[78:81], v[238:241], v[218:221], v[78:81]
	v_mfma_f32_16x16x32_bf16 v[74:77], v[242:245], v[218:221], v[74:77]
	v_mfma_f32_16x16x32_bf16 v[70:73], v[246:249], v[218:221], v[70:73]
	v_mfma_f32_16x16x32_bf16 v[66:69], v[250:253], v[218:221], v[66:69]
	ds_read_b128 v[218:221], v93 offset:0
	ds_read_b128 v[142:145], v141 offset:19456
	v_mfma_f32_16x16x32_bf16 v[62:65], v[238:241], v[222:225], v[62:65]
	v_mfma_f32_16x16x32_bf16 v[58:61], v[242:245], v[222:225], v[58:61]
	v_mfma_f32_16x16x32_bf16 v[54:57], v[246:249], v[222:225], v[54:57]
	v_mfma_f32_16x16x32_bf16 v[50:53], v[250:253], v[222:225], v[50:53]
	ds_read_b128 v[222:225], v93 offset:2048
	ds_read_b128 v[146:149], v141 offset:21504
	v_mfma_f32_16x16x32_bf16 v[46:49], v[238:241], v[226:229], v[46:49]
	v_mfma_f32_16x16x32_bf16 v[42:45], v[242:245], v[226:229], v[42:45]
	v_mfma_f32_16x16x32_bf16 v[38:41], v[246:249], v[226:229], v[38:41]
	v_mfma_f32_16x16x32_bf16 v[34:37], v[250:253], v[226:229], v[34:37]
	ds_read_b128 v[226:229], v93 offset:4096
	ds_read_b128 v[156:159], v141 offset:23552
	v_mfma_f32_16x16x32_bf16 v[18:21], v[238:241], v[230:233], v[18:21]
	v_mfma_f32_16x16x32_bf16 v[22:25], v[242:245], v[230:233], v[22:25]
	v_mfma_f32_16x16x32_bf16 v[26:29], v[246:249], v[230:233], v[26:29]
	v_mfma_f32_16x16x32_bf16 v[30:33], v[250:253], v[230:233], v[30:33]
	ds_read_b128 v[230:233], v93 offset:6144
	ds_read_b128 v[160:163], v141 offset:25600
	v_mfma_f32_16x16x32_bf16 v[2:5], v[238:241], v[234:237], v[2:5]
	v_mfma_f32_16x16x32_bf16 v[6:9], v[242:245], v[234:237], v[6:9]
	v_mfma_f32_16x16x32_bf16 v[10:13], v[246:249], v[234:237], v[10:13]
	v_mfma_f32_16x16x32_bf16 v[14:17], v[250:253], v[234:237], v[14:17]
	ds_read_b128 v[234:237], v93 offset:8192
	s_waitcnt lgkmcnt(0)
; #define PG8_LAS __attribute__((address_space(3)))
; __device__ __forceinline__ unsigned cvtpk(float lo, float hi) { f32x2 v = {lo, hi}; bf16x2_t b = __builtin_convertvector(v, bf16x2_t); return __builtin_bit_cast(unsigned, b); }
; __device__ __forceinline__ void moe_down_stream(PG8_LAS unsigned char* lds, int e, int cb0, int slot0, int nv, const bf16_t* HIDp, const float* Wd, bf16_t* Y, const float* slot_w, const int* slot_dst) {
;     ...
;         if (((t + 1) & 7) == 7) {
;             const int cb = cb0 + ((t + 1) >> 3);
; #pragma unroll
;             for (int m = 0; m < DNM; ++m) {
;                 const float w_ = lw[4 * (16 * m + fr) + wr];
; #pragma unroll
;                 for (int p = 0; p < 2; ++p) { const f32x4 v0 = acc[m][2 * p] * w_, v1 = acc[m][2 * p + 1] * w_; u32x4 w; w.x = cvtpk(v0[0], v0[1]); w.y = cvtpk(v0[2], v0[3]); w.z = cvtpk(v1[0], v1[1]); w.w = cvtpk(v1[2], v1[3]);
;                     *(PG8_LAS u32x4*)(stg + fr * 128 + (((4 * p + fq) ^ (fr & 7)) * 16)) = w; }
; #pragma unroll
;                 for (int hh = 0; hh < 2; ++hh) { const int r = (lane >> 3) + 8 * hh, cc = lane & 7; const u32x4 d = *(const PG8_LAS u32x4*)(stg + r * 128 + ((cc ^ (r & 7)) * 16)); const int dst_ = ldst[4 * (16 * m + r) + wr];
;                     if (dst_ >= 0) *(u32x4*)(Y + (size_t)dst_ * D + 128 * cb + 64 * wc + 8 * cc) = d; }
; #pragma unroll
;                 for (int n = 0; n < 4; ++n) acc[m][n] = (f32x4){0.f, 0.f, 0.f, 0.f}; } }
	v_mfma_f32_16x16x32_bf16 v[78:81], v[142:145], v[218:221], v[78:81]
	v_mfma_f32_16x16x32_bf16 v[74:77], v[146:149], v[218:221], v[74:77]
	v_mfma_f32_16x16x32_bf16 v[70:73], v[156:159], v[218:221], v[70:73]
	v_mfma_f32_16x16x32_bf16 v[66:69], v[160:163], v[218:221], v[66:69]
	v_mfma_f32_16x16x32_bf16 v[62:65], v[142:145], v[222:225], v[62:65]
	v_mfma_f32_16x16x32_bf16 v[58:61], v[146:149], v[222:225], v[58:61]
	v_mfma_f32_16x16x32_bf16 v[54:57], v[156:159], v[222:225], v[54:57]
	v_mfma_f32_16x16x32_bf16 v[50:53], v[160:163], v[222:225], v[50:53]
	v_mfma_f32_16x16x32_bf16 v[46:49], v[142:145], v[226:229], v[46:49]
	v_mfma_f32_16x16x32_bf16 v[42:45], v[146:149], v[226:229], v[42:45]
	v_mfma_f32_16x16x32_bf16 v[38:41], v[156:159], v[226:229], v[38:41]
	v_mfma_f32_16x16x32_bf16 v[34:37], v[160:163], v[226:229], v[34:37]
	v_mfma_f32_16x16x32_bf16 v[18:21], v[142:145], v[230:233], v[18:21]
	v_mfma_f32_16x16x32_bf16 v[22:25], v[146:149], v[230:233], v[22:25]
	v_mfma_f32_16x16x32_bf16 v[26:29], v[156:159], v[230:233], v[26:29]
	v_mfma_f32_16x16x32_bf16 v[30:33], v[160:163], v[230:233], v[30:33]
	v_mfma_f32_16x16x32_bf16 v[2:5], v[142:145], v[234:237], v[2:5]
	v_mfma_f32_16x16x32_bf16 v[6:9], v[146:149], v[234:237], v[6:9]
	v_mfma_f32_16x16x32_bf16 v[10:13], v[156:159], v[234:237], v[10:13]
	v_mfma_f32_16x16x32_bf16 v[14:17], v[160:163], v[234:237], v[14:17]
	s_waitcnt lgkmcnt(0)
	s_barrier
	s_mov_b32 s49, s46
	s_mov_b32 s46, s47
	s_mov_b32 s47, s48
	s_mov_b32 s48, s49
	s_add_i32 s50, s50, 1
	s_add_i32 s54, s48, s74
	v_add_u32_e32 v164, s54, v84
	v_add_u32_e32 v165, s54, v85
	ds_read_b32 v150, v82 offset:0
	ds_read_b32 v151, v83 offset:0
	ds_read_b32 v166, v83 offset:128
	s_waitcnt lgkmcnt(2)
	v_mul_f32_e32 v78, v150, v78
	v_mul_f32_e32 v79, v150, v79
	v_mul_f32_e32 v80, v150, v80
	v_mul_f32_e32 v81, v150, v81
	v_mul_f32_e32 v74, v150, v74
	v_mul_f32_e32 v75, v150, v75
	v_mul_f32_e32 v76, v150, v76
	v_mul_f32_e32 v77, v150, v77
	v_cvt_pk_bf16_f32 v182, v78, v79
	v_cvt_pk_bf16_f32 v183, v80, v81
	v_cvt_pk_bf16_f32 v184, v74, v75
	v_cvt_pk_bf16_f32 v185, v76, v77
	ds_write_b128 v164, v[182:185]
	v_mul_f32_e32 v70, v150, v70
	v_mul_f32_e32 v71, v150, v71
	v_mul_f32_e32 v72, v150, v72
	v_mul_f32_e32 v73, v150, v73
	v_mul_f32_e32 v66, v150, v66
	v_mul_f32_e32 v67, v150, v67
	v_mul_f32_e32 v68, v150, v68
	v_mul_f32_e32 v69, v150, v69
	v_cvt_pk_bf16_f32 v182, v70, v71
	v_cvt_pk_bf16_f32 v183, v72, v73
	v_cvt_pk_bf16_f32 v184, v66, v67
	v_cvt_pk_bf16_f32 v185, v68, v69
	v_xor_b32_e32 v167, 64, v164
	ds_write_b128 v167, v[182:185]
	v_mov_b32_e32 v78, 0
	v_mov_b32_e32 v74, 0
	v_mov_b32_e32 v70, 0
	v_mov_b32_e32 v66, 0
	v_mov_b32_e32 v79, 0
	v_mov_b32_e32 v75, 0
	v_mov_b32_e32 v71, 0
	v_mov_b32_e32 v67, 0
	v_mov_b32_e32 v80, 0
	v_mov_b32_e32 v76, 0
	v_mov_b32_e32 v72, 0
	v_mov_b32_e32 v68, 0
	v_mov_b32_e32 v81, 0
	v_mov_b32_e32 v77, 0
	v_mov_b32_e32 v73, 0
	v_mov_b32_e32 v69, 0
	ds_read_b128 v[182:185], v165 offset:0
	v_cmp_lt_i32_e32 vcc, -1, v151
	v_lshlrev_b32_e32 v148, 13, v151
	v_mov_b32_e32 v149, 0
	v_lshl_add_u64 v[148:149], v[148:149], 0, v[86:87]
	v_cndmask_b32_e32 v148, v168, v148, vcc
	v_cndmask_b32_e32 v149, v169, v149, vcc
	s_waitcnt lgkmcnt(0)
	global_store_dwordx4 v[148:149], v[182:185], off
	ds_read_b128 v[182:185], v165 offset:8192
	v_cmp_lt_i32_e32 vcc, -1, v166
	v_lshlrev_b32_e32 v148, 13, v166
	v_mov_b32_e32 v149, 0
	v_lshl_add_u64 v[148:149], v[148:149], 0, v[86:87]
	v_cndmask_b32_e32 v148, v168, v148, vcc
	v_cndmask_b32_e32 v149, v169, v149, vcc
	s_waitcnt lgkmcnt(0)
	global_store_dwordx4 v[148:149], v[182:185], off
	ds_read_b32 v150, v82 offset:256
	ds_read_b32 v151, v83 offset:256
	ds_read_b32 v166, v83 offset:384
	s_waitcnt lgkmcnt(2)
	v_mul_f32_e32 v62, v150, v62
	v_mul_f32_e32 v63, v150, v63
	v_mul_f32_e32 v64, v150, v64
	v_mul_f32_e32 v65, v150, v65
	v_mul_f32_e32 v58, v150, v58
	v_mul_f32_e32 v59, v150, v59
	v_mul_f32_e32 v60, v150, v60
	v_mul_f32_e32 v61, v150, v61
	v_cvt_pk_bf16_f32 v182, v62, v63
	v_cvt_pk_bf16_f32 v183, v64, v65
	v_cvt_pk_bf16_f32 v184, v58, v59
	v_cvt_pk_bf16_f32 v185, v60, v61
	ds_write_b128 v164, v[182:185]
	v_mul_f32_e32 v54, v150, v54
	v_mul_f32_e32 v55, v150, v55
	v_mul_f32_e32 v56, v150, v56
	v_mul_f32_e32 v57, v150, v57
	v_mul_f32_e32 v50, v150, v50
	v_mul_f32_e32 v51, v150, v51
	v_mul_f32_e32 v52, v150, v52
	v_mul_f32_e32 v53, v150, v53
	v_cvt_pk_bf16_f32 v182, v54, v55
	v_cvt_pk_bf16_f32 v183, v56, v57
	v_cvt_pk_bf16_f32 v184, v50, v51
	v_cvt_pk_bf16_f32 v185, v52, v53
	v_xor_b32_e32 v167, 64, v164
	ds_write_b128 v167, v[182:185]
	v_mov_b32_e32 v62, 0
	v_mov_b32_e32 v58, 0
	v_mov_b32_e32 v54, 0
	v_mov_b32_e32 v50, 0
	v_mov_b32_e32 v63, 0
	v_mov_b32_e32 v59, 0
	v_mov_b32_e32 v55, 0
	v_mov_b32_e32 v51, 0
	v_mov_b32_e32 v64, 0
	v_mov_b32_e32 v60, 0
	v_mov_b32_e32 v56, 0
	v_mov_b32_e32 v52, 0
	v_mov_b32_e32 v65, 0
	v_mov_b32_e32 v61, 0
	v_mov_b32_e32 v57, 0
	v_mov_b32_e32 v53, 0
	ds_read_b128 v[182:185], v165 offset:0
	v_cmp_lt_i32_e32 vcc, -1, v151
	v_lshlrev_b32_e32 v148, 13, v151
	v_mov_b32_e32 v149, 0
	v_lshl_add_u64 v[148:149], v[148:149], 0, v[86:87]
	v_cndmask_b32_e32 v148, v168, v148, vcc
	v_cndmask_b32_e32 v149, v169, v149, vcc
	s_waitcnt lgkmcnt(0)
	global_store_dwordx4 v[148:149], v[182:185], off
	ds_read_b128 v[182:185], v165 offset:8192
	v_cmp_lt_i32_e32 vcc, -1, v166
	v_lshlrev_b32_e32 v148, 13, v166
	v_mov_b32_e32 v149, 0
	v_lshl_add_u64 v[148:149], v[148:149], 0, v[86:87]
	v_cndmask_b32_e32 v148, v168, v148, vcc
	v_cndmask_b32_e32 v149, v169, v149, vcc
	s_waitcnt lgkmcnt(0)
	global_store_dwordx4 v[148:149], v[182:185], off
	ds_read_b32 v150, v82 offset:512
	ds_read_b32 v151, v83 offset:512
	ds_read_b32 v166, v83 offset:640
	s_waitcnt lgkmcnt(2)
; #define PG8_LAS __attribute__((address_space(3)))
; __device__ __forceinline__ unsigned cvtpk(float lo, float hi) { f32x2 v = {lo, hi}; bf16x2_t b = __builtin_convertvector(v, bf16x2_t); return __builtin_bit_cast(unsigned, b); }
; __device__ __forceinline__ void moe_down_stream(PG8_LAS unsigned char* lds, int e, int cb0, int slot0, int nv, const bf16_t* HIDp, const float* Wd, bf16_t* Y, const float* slot_w, const int* slot_dst) {
;     ...
;         if (((t + 1) & 7) == 7) {
;             const int cb = cb0 + ((t + 1) >> 3);
; #pragma unroll
;             for (int m = 0; m < DNM; ++m) {
;                 const float w_ = lw[4 * (16 * m + fr) + wr];
; #pragma unroll
;                 for (int p = 0; p < 2; ++p) { const f32x4 v0 = acc[m][2 * p] * w_, v1 = acc[m][2 * p + 1] * w_; u32x4 w; w.x = cvtpk(v0[0], v0[1]); w.y = cvtpk(v0[2], v0[3]); w.z = cvtpk(v1[0], v1[1]); w.w = cvtpk(v1[2], v1[3]);
;                     *(PG8_LAS u32x4*)(stg + fr * 128 + (((4 * p + fq) ^ (fr & 7)) * 16)) = w; }
; #pragma unroll
;                 for (int hh = 0; hh < 2; ++hh) { const int r = (lane >> 3) + 8 * hh, cc = lane & 7; const u32x4 d = *(const PG8_LAS u32x4*)(stg + r * 128 + ((cc ^ (r & 7)) * 16)); const int dst_ = ldst[4 * (16 * m + r) + wr];
;                     if (dst_ >= 0) *(u32x4*)(Y + (size_t)dst_ * D + 128 * cb + 64 * wc + 8 * cc) = d; }
; #pragma unroll
;                 for (int n = 0; n < 4; ++n) acc[m][n] = (f32x4){0.f, 0.f, 0.f, 0.f}; } }
	v_mul_f32_e32 v46, v150, v46
	v_mul_f32_e32 v47, v150, v47
	v_mul_f32_e32 v48, v150, v48
	v_mul_f32_e32 v49, v150, v49
	v_mul_f32_e32 v42, v150, v42
	v_mul_f32_e32 v43, v150, v43
	v_mul_f32_e32 v44, v150, v44
	v_mul_f32_e32 v45, v150, v45
	v_cvt_pk_bf16_f32 v182, v46, v47
	v_cvt_pk_bf16_f32 v183, v48, v49
	v_cvt_pk_bf16_f32 v184, v42, v43
	v_cvt_pk_bf16_f32 v185, v44, v45
	ds_write_b128 v164, v[182:185]
	v_mul_f32_e32 v38, v150, v38
	v_mul_f32_e32 v39, v150, v39
	v_mul_f32_e32 v40, v150, v40
	v_mul_f32_e32 v41, v150, v41
	v_mul_f32_e32 v34, v150, v34
	v_mul_f32_e32 v35, v150, v35
	v_mul_f32_e32 v36, v150, v36
	v_mul_f32_e32 v37, v150, v37
	v_cvt_pk_bf16_f32 v182, v38, v39
	v_cvt_pk_bf16_f32 v183, v40, v41
	v_cvt_pk_bf16_f32 v184, v34, v35
	v_cvt_pk_bf16_f32 v185, v36, v37
	v_xor_b32_e32 v167, 64, v164
	ds_write_b128 v167, v[182:185]
	v_mov_b32_e32 v46, 0
	v_mov_b32_e32 v42, 0
	v_mov_b32_e32 v38, 0
	v_mov_b32_e32 v34, 0
	v_mov_b32_e32 v47, 0
	v_mov_b32_e32 v43, 0
	v_mov_b32_e32 v39, 0
	v_mov_b32_e32 v35, 0
	v_mov_b32_e32 v48, 0
	v_mov_b32_e32 v44, 0
	v_mov_b32_e32 v40, 0
	v_mov_b32_e32 v36, 0
	v_mov_b32_e32 v49, 0
	v_mov_b32_e32 v45, 0
	v_mov_b32_e32 v41, 0
	v_mov_b32_e32 v37, 0
	ds_read_b128 v[182:185], v165 offset:0
	v_cmp_lt_i32_e32 vcc, -1, v151
	v_lshlrev_b32_e32 v148, 13, v151
	v_mov_b32_e32 v149, 0
	v_lshl_add_u64 v[148:149], v[148:149], 0, v[86:87]
	v_cndmask_b32_e32 v148, v168, v148, vcc
	v_cndmask_b32_e32 v149, v169, v149, vcc
	s_waitcnt lgkmcnt(0)
	global_store_dwordx4 v[148:149], v[182:185], off
	ds_read_b128 v[182:185], v165 offset:8192
	v_cmp_lt_i32_e32 vcc, -1, v166
	v_lshlrev_b32_e32 v148, 13, v166
	v_mov_b32_e32 v149, 0
	v_lshl_add_u64 v[148:149], v[148:149], 0, v[86:87]
	v_cndmask_b32_e32 v148, v168, v148, vcc
	v_cndmask_b32_e32 v149, v169, v149, vcc
	s_waitcnt lgkmcnt(0)
	global_store_dwordx4 v[148:149], v[182:185], off
	ds_read_b32 v150, v82 offset:768
	ds_read_b32 v151, v83 offset:768
	ds_read_b32 v166, v83 offset:896
	s_waitcnt lgkmcnt(2)
	v_mul_f32_e32 v18, v150, v18
	v_mul_f32_e32 v19, v150, v19
	v_mul_f32_e32 v20, v150, v20
	v_mul_f32_e32 v21, v150, v21
	v_mul_f32_e32 v22, v150, v22
	v_mul_f32_e32 v23, v150, v23
	v_mul_f32_e32 v24, v150, v24
	v_mul_f32_e32 v25, v150, v25
	v_cvt_pk_bf16_f32 v182, v18, v19
	v_cvt_pk_bf16_f32 v183, v20, v21
	v_cvt_pk_bf16_f32 v184, v22, v23
	v_cvt_pk_bf16_f32 v185, v24, v25
	ds_write_b128 v164, v[182:185]
	v_mul_f32_e32 v26, v150, v26
	v_mul_f32_e32 v27, v150, v27
	v_mul_f32_e32 v28, v150, v28
	v_mul_f32_e32 v29, v150, v29
	v_mul_f32_e32 v30, v150, v30
	v_mul_f32_e32 v31, v150, v31
	v_mul_f32_e32 v32, v150, v32
	v_mul_f32_e32 v33, v150, v33
	v_cvt_pk_bf16_f32 v182, v26, v27
	v_cvt_pk_bf16_f32 v183, v28, v29
	v_cvt_pk_bf16_f32 v184, v30, v31
	v_cvt_pk_bf16_f32 v185, v32, v33
	v_xor_b32_e32 v167, 64, v164
	ds_write_b128 v167, v[182:185]
	v_mov_b32_e32 v18, 0
	v_mov_b32_e32 v22, 0
	v_mov_b32_e32 v26, 0
	v_mov_b32_e32 v30, 0
	v_mov_b32_e32 v19, 0
	v_mov_b32_e32 v23, 0
	v_mov_b32_e32 v27, 0
	v_mov_b32_e32 v31, 0
	v_mov_b32_e32 v20, 0
	v_mov_b32_e32 v24, 0
	v_mov_b32_e32 v28, 0
	v_mov_b32_e32 v32, 0
	v_mov_b32_e32 v21, 0
	v_mov_b32_e32 v25, 0
	v_mov_b32_e32 v29, 0
	v_mov_b32_e32 v33, 0
	ds_read_b128 v[182:185], v165 offset:0
	v_cmp_lt_i32_e32 vcc, -1, v151
	v_lshlrev_b32_e32 v148, 13, v151
	v_mov_b32_e32 v149, 0
	v_lshl_add_u64 v[148:149], v[148:149], 0, v[86:87]
	v_cndmask_b32_e32 v148, v168, v148, vcc
	v_cndmask_b32_e32 v149, v169, v149, vcc
	s_waitcnt lgkmcnt(0)
	global_store_dwordx4 v[148:149], v[182:185], off
	ds_read_b128 v[182:185], v165 offset:8192
	v_cmp_lt_i32_e32 vcc, -1, v166
	v_lshlrev_b32_e32 v148, 13, v166
	v_mov_b32_e32 v149, 0
	v_lshl_add_u64 v[148:149], v[148:149], 0, v[86:87]
	v_cndmask_b32_e32 v148, v168, v148, vcc
	v_cndmask_b32_e32 v149, v169, v149, vcc
	s_waitcnt lgkmcnt(0)
	global_store_dwordx4 v[148:149], v[182:185], off
	ds_read_b32 v150, v82 offset:1024
	ds_read_b32 v151, v83 offset:1024
	ds_read_b32 v166, v83 offset:1152
	s_waitcnt lgkmcnt(2)
	v_mul_f32_e32 v2, v150, v2
	v_mul_f32_e32 v3, v150, v3
	v_mul_f32_e32 v4, v150, v4
	v_mul_f32_e32 v5, v150, v5
	v_mul_f32_e32 v6, v150, v6
	v_mul_f32_e32 v7, v150, v7
	v_mul_f32_e32 v8, v150, v8
	v_mul_f32_e32 v9, v150, v9
	v_cvt_pk_bf16_f32 v182, v2, v3
	v_cvt_pk_bf16_f32 v183, v4, v5
	v_cvt_pk_bf16_f32 v184, v6, v7
	v_cvt_pk_bf16_f32 v185, v8, v9
	ds_write_b128 v164, v[182:185]
	v_mul_f32_e32 v10, v150, v10
	v_mul_f32_e32 v11, v150, v11
	v_mul_f32_e32 v12, v150, v12
	v_mul_f32_e32 v13, v150, v13
	v_mul_f32_e32 v14, v150, v14
	v_mul_f32_e32 v15, v150, v15
	v_mul_f32_e32 v16, v150, v16
	v_mul_f32_e32 v17, v150, v17
	v_cvt_pk_bf16_f32 v182, v10, v11
	v_cvt_pk_bf16_f32 v183, v12, v13
	v_cvt_pk_bf16_f32 v184, v14, v15
	v_cvt_pk_bf16_f32 v185, v16, v17
	v_xor_b32_e32 v167, 64, v164
	ds_write_b128 v167, v[182:185]
	v_mov_b32_e32 v2, 0
	v_mov_b32_e32 v6, 0
	v_mov_b32_e32 v10, 0
	v_mov_b32_e32 v14, 0
	v_mov_b32_e32 v3, 0
	v_mov_b32_e32 v7, 0
	v_mov_b32_e32 v11, 0
	v_mov_b32_e32 v15, 0
	v_mov_b32_e32 v4, 0
	v_mov_b32_e32 v8, 0
	v_mov_b32_e32 v12, 0
	v_mov_b32_e32 v16, 0
	v_mov_b32_e32 v5, 0
	v_mov_b32_e32 v9, 0
	v_mov_b32_e32 v13, 0
	v_mov_b32_e32 v17, 0
	ds_read_b128 v[182:185], v165 offset:0
	v_cmp_lt_i32_e32 vcc, -1, v151
	v_lshlrev_b32_e32 v148, 13, v151
	v_mov_b32_e32 v149, 0
	v_lshl_add_u64 v[148:149], v[148:149], 0, v[86:87]
	v_cndmask_b32_e32 v148, v168, v148, vcc
	v_cndmask_b32_e32 v149, v169, v149, vcc
	s_waitcnt lgkmcnt(0)
	global_store_dwordx4 v[148:149], v[182:185], off
	ds_read_b128 v[182:185], v165 offset:8192
	v_cmp_lt_i32_e32 vcc, -1, v166
	v_lshlrev_b32_e32 v148, 13, v166
	v_mov_b32_e32 v149, 0
	v_lshl_add_u64 v[148:149], v[148:149], 0, v[86:87]
	v_cndmask_b32_e32 v148, v168, v148, vcc
	v_cndmask_b32_e32 v149, v169, v149, vcc
	s_waitcnt lgkmcnt(0)
	global_store_dwordx4 v[148:149], v[182:185], off
	v_add_co_u32_e32 v86, vcc, 0x800, v86
	s_nop 1
	v_addc_co_u32_e32 v87, vcc, 0, v87, vcc
	s_waitcnt lgkmcnt(0)
	s_branch .Lmd_done
; #define MD_GLDS_A(buf, tau) do { _Pragma("unroll") for (int i = 0; i < 5; ++i) if (amask & (1u << i)) \
;         __builtin_amdgcn_global_load_lds((const unsigned*)((const char*)HIDp + aoff[i] + (size_t)((tau) & 7) * 128), (PG8_LAS unsigned*)(MD_SA(buf) + wid * 1024 + i * 8192), 16, 0, 0); } while (0)
; #define MD_B_ISSUE(sb, tau) do { const char* kb_ = Bb + (size_t)((tau) >> 3) * 512 + (size_t)((tau) & 7) * (64 * (size_t)RB); _Pragma("unroll") for (int j = 0; j < 8; ++j) { const char* p_ = kb_ + (size_t)j * RB; \
;         asm volatile("global_load_dwordx2 %0, %1, off" : "=&v"(sb[j]) : "v"(p_) : "memory"); } } while (0)
; #define MD_B_WAIT(sb, N) asm volatile("s_waitcnt vmcnt(%8)" : "+v"(sb[0]), "+v"(sb[1]), "+v"(sb[2]), "+v"(sb[3]), "+v"(sb[4]), "+v"(sb[5]), "+v"(sb[6]), "+v"(sb[7]) : "n"(N) : "memory")
; __device__ __forceinline__ void moe_down_stream(PG8_LAS unsigned char* lds, int e, int cb0, int slot0, int nv, const bf16_t* HIDp, const float* Wd, bf16_t* Y, const float* slot_w, const int* slot_dst) {
;     ...
;     f32x4 acc[DNM][4];
; #pragma unroll
;     for (int m = 0; m < DNM; ++m)
; #pragma unroll
;         for (int n = 0; n < 4; ++n) acc[m][n] = (f32x4){0.f, 0.f, 0.f, 0.f};
;     f32x2 s0[8], s1[8];
;     MD_GLDS_A(0, 0); MD_B_ISSUE(s0, 0); MD_B_ISSUE(s1, 1);
;     MD_B_WAIT(s0, 8); MD_B_WRITE(s0, 0); __builtin_amdgcn_sched_barrier(0); MD_B_ISSUE(s0, 2);
;     asm volatile("s_waitcnt vmcnt(16)" ::: "memory");
;     asm volatile("s_waitcnt lgkmcnt(0)" ::: "memory"); __builtin_amdgcn_s_barrier(); asm volatile("" ::: "memory");
; #pragma unroll 1
;     for (int t = 0; t < NT; t += 2) {
;         if (t + 2 < NT) MD_B_WAIT(s1, 8); else MD_B_WAIT(s1, 0);
;         MD_B_WRITE(s1, 1); __builtin_amdgcn_sched_barrier(0); MD_GLDS_A(1, t + 1); __builtin_amdgcn_sched_barrier(0);
;         if (t + 3 < NT) MD_B_ISSUE(s1, t + 3);
;         MD_COMPUTE(0);
;         MD_END(t + 3 >= NT);
;         if (t + 2 < NT) { MD_B_WAIT(s0, 8); MD_B_WRITE(s0, 0); __builtin_amdgcn_sched_barrier(0); MD_GLDS_A(0, t + 2); __builtin_amdgcn_sched_barrier(0); }
;         if (t + 4 < NT) MD_B_ISSUE(s0, t + 4);
;         MD_COMPUTE(1);
;         MD_END(t + 4 >= NT);
.Lmd_grpY:
	s_add_i32 s49, s48, s74
	s_add_i32 s52, s52, 1
	s_and_b32 s54, s52, 7
	s_cmp_eq_u32 s54, 0
	s_cselect_b32 s54, s53, s32
	s_cselect_b32 s55, -1, 0
	s_add_u32 s30, s30, s54
	s_addc_u32 s31, s31, s55
	s_mov_b32 m0, s49
	s_nop 0
	global_load_lds_dwordx4 v88, s[30:31]
	s_add_i32 m0, s49, 0x2000
	s_nop 0
	global_load_lds_dwordx4 v90, s[30:31]
	s_add_i32 m0, s49, 0x4000
	s_nop 0
	global_load_lds_dwordx4 v92, s[30:31]
	s_add_i32 m0, s49, 0x6000
	s_nop 0
	global_load_lds_dwordx4 v94, s[30:31]
	s_add_i32 m0, s49, 0x8000
	s_nop 0
	global_load_lds_dwordx4 v96, s[30:31]
	s_waitcnt vmcnt(29)
	v_cvt_pk_bf16_f32 v172, v114, v116
	v_cvt_pk_bf16_f32 v173, v118, v120
	v_cvt_pk_bf16_f32 v174, v122, v124
	v_cvt_pk_bf16_f32 v175, v126, v128
	v_cvt_pk_bf16_f32 v176, v115, v117
	v_cvt_pk_bf16_f32 v177, v119, v121
	v_cvt_pk_bf16_f32 v178, v123, v125
	v_cvt_pk_bf16_f32 v179, v127, v129
	ds_write_b128 v95, v[172:175] offset:19456
	ds_write_b128 v95, v[176:179] offset:19584
	v_add_u32_e32 v91, s46, v135
	v_add_u32_e32 v93, s46, v137
	ds_read_b128 v[238:241], v139 offset:0
	ds_read_b128 v[242:245], v139 offset:2048
	ds_read_b128 v[246:249], v139 offset:4096
	ds_read_b128 v[250:253], v139 offset:6144
	ds_read_b128 v[218:221], v91 offset:0
	ds_read_b128 v[222:225], v91 offset:2048
	ds_read_b128 v[226:229], v91 offset:4096
	ds_read_b128 v[230:233], v91 offset:6144
	ds_read_b128 v[234:237], v91 offset:8192
	s_waitcnt lgkmcnt(0)
	v_mfma_f32_16x16x32_bf16 v[78:81], v[238:241], v[218:221], v[78:81]
	v_mfma_f32_16x16x32_bf16 v[74:77], v[242:245], v[218:221], v[74:77]
	v_mfma_f32_16x16x32_bf16 v[70:73], v[246:249], v[218:221], v[70:73]
	v_mfma_f32_16x16x32_bf16 v[66:69], v[250:253], v[218:221], v[66:69]
	ds_read_b128 v[218:221], v93 offset:0
	ds_read_b128 v[142:145], v141 offset:0
	s_add_i32 s51, s51, 1
	s_and_b32 s54, s51, 7
	s_cmp_eq_u32 s54, 0
	s_cselect_b32 s44, s34, s35
	s_cselect_b32 s45, -1, 0
	v_lshl_add_u64 v[132:133], v[132:133], 0, s[44:45]
	global_load_dwordx2 v[114:115], v[132:133], off
	v_lshl_add_u64 v[180:181], v[132:133], 0, s[24:25]
	global_load_dwordx2 v[116:117], v[180:181], off
	v_mfma_f32_16x16x32_bf16 v[62:65], v[238:241], v[222:225], v[62:65]
	v_mfma_f32_16x16x32_bf16 v[58:61], v[242:245], v[222:225], v[58:61]
	v_mfma_f32_16x16x32_bf16 v[54:57], v[246:249], v[222:225], v[54:57]
	v_mfma_f32_16x16x32_bf16 v[50:53], v[250:253], v[222:225], v[50:53]
	ds_read_b128 v[222:225], v93 offset:2048
	ds_read_b128 v[146:149], v141 offset:2048
	v_lshl_add_u64 v[180:181], v[132:133], 0, s[26:27]
	global_load_dwordx2 v[118:119], v[180:181], off
	v_lshl_add_u64 v[180:181], v[132:133], 0, s[28:29]
	global_load_dwordx2 v[120:121], v[180:181], off
	v_mfma_f32_16x16x32_bf16 v[46:49], v[238:241], v[226:229], v[46:49]
	v_mfma_f32_16x16x32_bf16 v[42:45], v[242:245], v[226:229], v[42:45]
	v_mfma_f32_16x16x32_bf16 v[38:41], v[246:249], v[226:229], v[38:41]
	v_mfma_f32_16x16x32_bf16 v[34:37], v[250:253], v[226:229], v[34:37]
	ds_read_b128 v[226:229], v93 offset:4096
	ds_read_b128 v[156:159], v141 offset:4096
	v_lshl_add_u64 v[180:181], v[132:133], 0, s[36:37]
	global_load_dwordx2 v[122:123], v[180:181], off
	v_lshl_add_u64 v[180:181], v[132:133], 0, s[38:39]
	global_load_dwordx2 v[124:125], v[180:181], off
	v_mfma_f32_16x16x32_bf16 v[18:21], v[238:241], v[230:233], v[18:21]
	v_mfma_f32_16x16x32_bf16 v[22:25], v[242:245], v[230:233], v[22:25]
	v_mfma_f32_16x16x32_bf16 v[26:29], v[246:249], v[230:233], v[26:29]
	v_mfma_f32_16x16x32_bf16 v[30:33], v[250:253], v[230:233], v[30:33]
	ds_read_b128 v[230:233], v93 offset:6144
	ds_read_b128 v[160:163], v141 offset:6144
	v_lshl_add_u64 v[180:181], v[132:133], 0, s[40:41]
	global_load_dwordx2 v[126:127], v[180:181], off
	v_lshl_add_u64 v[180:181], v[132:133], 0, s[42:43]
	global_load_dwordx2 v[128:129], v[180:181], off
	v_mfma_f32_16x16x32_bf16 v[2:5], v[238:241], v[234:237], v[2:5]
	v_mfma_f32_16x16x32_bf16 v[6:9], v[242:245], v[234:237], v[6:9]
	v_mfma_f32_16x16x32_bf16 v[10:13], v[246:249], v[234:237], v[10:13]
	v_mfma_f32_16x16x32_bf16 v[14:17], v[250:253], v[234:237], v[14:17]
	ds_read_b128 v[234:237], v93 offset:8192
	s_waitcnt lgkmcnt(0)
	s_barrier
	s_mov_b32 s49, s46
	s_mov_b32 s46, s47
	s_mov_b32 s47, s48
	s_mov_b32 s48, s49
	s_add_i32 s50, s50, 1
	s_add_i32 s49, s48, s74
	s_add_i32 s52, s52, 1
	s_and_b32 s54, s52, 7
	s_cmp_eq_u32 s54, 0
	s_cselect_b32 s54, s53, s32
	s_cselect_b32 s55, -1, 0
	s_add_u32 s30, s30, s54
	s_addc_u32 s31, s31, s55
	v_mfma_f32_16x16x32_bf16 v[78:81], v[142:145], v[218:221], v[78:81]
	v_mfma_f32_16x16x32_bf16 v[74:77], v[146:149], v[218:221], v[74:77]
	v_mfma_f32_16x16x32_bf16 v[70:73], v[156:159], v[218:221], v[70:73]
	v_mfma_f32_16x16x32_bf16 v[66:69], v[160:163], v[218:221], v[66:69]
	s_mov_b32 m0, s49
	s_nop 0
	global_load_lds_dwordx4 v88, s[30:31]
	v_mfma_f32_16x16x32_bf16 v[62:65], v[142:145], v[222:225], v[62:65]
	v_mfma_f32_16x16x32_bf16 v[58:61], v[146:149], v[222:225], v[58:61]
	v_mfma_f32_16x16x32_bf16 v[54:57], v[156:159], v[222:225], v[54:57]
	v_mfma_f32_16x16x32_bf16 v[50:53], v[160:163], v[222:225], v[50:53]
	s_add_i32 m0, s49, 0x2000
	s_nop 0
	global_load_lds_dwordx4 v90, s[30:31]
	v_mfma_f32_16x16x32_bf16 v[46:49], v[142:145], v[226:229], v[46:49]
	v_mfma_f32_16x16x32_bf16 v[42:45], v[146:149], v[226:229], v[42:45]
	v_mfma_f32_16x16x32_bf16 v[38:41], v[156:159], v[226:229], v[38:41]
	v_mfma_f32_16x16x32_bf16 v[34:37], v[160:163], v[226:229], v[34:37]
	s_add_i32 m0, s49, 0x4000
	s_nop 0
	global_load_lds_dwordx4 v92, s[30:31]
	v_mfma_f32_16x16x32_bf16 v[18:21], v[142:145], v[230:233], v[18:21]
	v_mfma_f32_16x16x32_bf16 v[22:25], v[146:149], v[230:233], v[22:25]
	v_mfma_f32_16x16x32_bf16 v[26:29], v[156:159], v[230:233], v[26:29]
	v_mfma_f32_16x16x32_bf16 v[30:33], v[160:163], v[230:233], v[30:33]
	s_add_i32 m0, s49, 0x6000
	s_nop 0
	global_load_lds_dwordx4 v94, s[30:31]
	v_mfma_f32_16x16x32_bf16 v[2:5], v[142:145], v[234:237], v[2:5]
	v_mfma_f32_16x16x32_bf16 v[6:9], v[146:149], v[234:237], v[6:9]
	v_mfma_f32_16x16x32_bf16 v[10:13], v[156:159], v[234:237], v[10:13]
	v_mfma_f32_16x16x32_bf16 v[14:17], v[160:163], v[234:237], v[14:17]
	s_add_i32 m0, s49, 0x8000
	s_nop 0
	global_load_lds_dwordx4 v96, s[30:31]
	s_waitcnt vmcnt(34)
; #define MD_GLDS_A(buf, tau) do { _Pragma("unroll") for (int i = 0; i < 5; ++i) if (amask & (1u << i)) \
;         __builtin_amdgcn_global_load_lds((const unsigned*)((const char*)HIDp + aoff[i] + (size_t)((tau) & 7) * 128), (PG8_LAS unsigned*)(MD_SA(buf) + wid * 1024 + i * 8192), 16, 0, 0); } while (0)
; #define MD_B_ISSUE(sb, tau) do { const char* kb_ = Bb + (size_t)((tau) >> 3) * 512 + (size_t)((tau) & 7) * (64 * (size_t)RB); _Pragma("unroll") for (int j = 0; j < 8; ++j) { const char* p_ = kb_ + (size_t)j * RB; \
;         asm volatile("global_load_dwordx2 %0, %1, off" : "=&v"(sb[j]) : "v"(p_) : "memory"); } } while (0)
; #define MD_B_WAIT(sb, N) asm volatile("s_waitcnt vmcnt(%8)" : "+v"(sb[0]), "+v"(sb[1]), "+v"(sb[2]), "+v"(sb[3]), "+v"(sb[4]), "+v"(sb[5]), "+v"(sb[6]), "+v"(sb[7]) : "n"(N) : "memory")
; __device__ __forceinline__ void moe_down_stream(PG8_LAS unsigned char* lds, int e, int cb0, int slot0, int nv, const bf16_t* HIDp, const float* Wd, bf16_t* Y, const float* slot_w, const int* slot_dst) {
;     ...
;     f32x4 acc[DNM][4];
; #pragma unroll
;     for (int m = 0; m < DNM; ++m)
; #pragma unroll
;         for (int n = 0; n < 4; ++n) acc[m][n] = (f32x4){0.f, 0.f, 0.f, 0.f};
;     f32x2 s0[8], s1[8];
;     MD_GLDS_A(0, 0); MD_B_ISSUE(s0, 0); MD_B_ISSUE(s1, 1);
;     MD_B_WAIT(s0, 8); MD_B_WRITE(s0, 0); __builtin_amdgcn_sched_barrier(0); MD_B_ISSUE(s0, 2);
;     asm volatile("s_waitcnt vmcnt(16)" ::: "memory");
;     asm volatile("s_waitcnt lgkmcnt(0)" ::: "memory"); __builtin_amdgcn_s_barrier(); asm volatile("" ::: "memory");
; #pragma unroll 1
;     for (int t = 0; t < NT; t += 2) {
;         if (t + 2 < NT) MD_B_WAIT(s1, 8); else MD_B_WAIT(s1, 0);
;         MD_B_WRITE(s1, 1); __builtin_amdgcn_sched_barrier(0); MD_GLDS_A(1, t + 1); __builtin_amdgcn_sched_barrier(0);
;         if (t + 3 < NT) MD_B_ISSUE(s1, t + 3);
;         MD_COMPUTE(0);
;         MD_END(t + 3 >= NT);
;         if (t + 2 < NT) { MD_B_WAIT(s0, 8); MD_B_WRITE(s0, 0); __builtin_amdgcn_sched_barrier(0); MD_GLDS_A(0, t + 2); __builtin_amdgcn_sched_barrier(0); }
;         if (t + 4 < NT) MD_B_ISSUE(s0, t + 4);
;         MD_COMPUTE(1);
;         MD_END(t + 4 >= NT);
	v_cvt_pk_bf16_f32 v172, v186, v188
	v_cvt_pk_bf16_f32 v173, v190, v192
	v_cvt_pk_bf16_f32 v174, v194, v196
	v_cvt_pk_bf16_f32 v175, v198, v200
	v_cvt_pk_bf16_f32 v176, v187, v189
	v_cvt_pk_bf16_f32 v177, v191, v193
	v_cvt_pk_bf16_f32 v178, v195, v197
	v_cvt_pk_bf16_f32 v179, v199, v201
	ds_write_b128 v95, v[172:175] offset:0
	ds_write_b128 v95, v[176:179] offset:128
	v_add_u32_e32 v91, s46, v135
	v_add_u32_e32 v93, s46, v137
	ds_read_b128 v[238:241], v139 offset:19456
	ds_read_b128 v[242:245], v139 offset:21504
	ds_read_b128 v[246:249], v139 offset:23552
	ds_read_b128 v[250:253], v139 offset:25600
	ds_read_b128 v[218:221], v91 offset:0
	ds_read_b128 v[222:225], v91 offset:2048
	ds_read_b128 v[226:229], v91 offset:4096
	ds_read_b128 v[230:233], v91 offset:6144
	ds_read_b128 v[234:237], v91 offset:8192
	s_waitcnt lgkmcnt(0)
	v_mfma_f32_16x16x32_bf16 v[78:81], v[238:241], v[218:221], v[78:81]
	v_mfma_f32_16x16x32_bf16 v[74:77], v[242:245], v[218:221], v[74:77]
	v_mfma_f32_16x16x32_bf16 v[70:73], v[246:249], v[218:221], v[70:73]
	v_mfma_f32_16x16x32_bf16 v[66:69], v[250:253], v[218:221], v[66:69]
	ds_read_b128 v[218:221], v93 offset:0
	ds_read_b128 v[142:145], v141 offset:19456
	s_add_i32 s51, s51, 1
	s_and_b32 s54, s51, 7
	s_cmp_eq_u32 s54, 0
	s_cselect_b32 s44, s34, s35
	s_cselect_b32 s45, -1, 0
	v_lshl_add_u64 v[132:133], v[132:133], 0, s[44:45]
	global_load_dwordx2 v[186:187], v[132:133], off
	v_lshl_add_u64 v[180:181], v[132:133], 0, s[24:25]
	global_load_dwordx2 v[188:189], v[180:181], off
	v_mfma_f32_16x16x32_bf16 v[62:65], v[238:241], v[222:225], v[62:65]
	v_mfma_f32_16x16x32_bf16 v[58:61], v[242:245], v[222:225], v[58:61]
	v_mfma_f32_16x16x32_bf16 v[54:57], v[246:249], v[222:225], v[54:57]
	v_mfma_f32_16x16x32_bf16 v[50:53], v[250:253], v[222:225], v[50:53]
	ds_read_b128 v[222:225], v93 offset:2048
	ds_read_b128 v[146:149], v141 offset:21504
	v_lshl_add_u64 v[180:181], v[132:133], 0, s[26:27]
	global_load_dwordx2 v[190:191], v[180:181], off
	v_lshl_add_u64 v[180:181], v[132:133], 0, s[28:29]
	global_load_dwordx2 v[192:193], v[180:181], off
	v_mfma_f32_16x16x32_bf16 v[46:49], v[238:241], v[226:229], v[46:49]
	v_mfma_f32_16x16x32_bf16 v[42:45], v[242:245], v[226:229], v[42:45]
	v_mfma_f32_16x16x32_bf16 v[38:41], v[246:249], v[226:229], v[38:41]
	v_mfma_f32_16x16x32_bf16 v[34:37], v[250:253], v[226:229], v[34:37]
	ds_read_b128 v[226:229], v93 offset:4096
	ds_read_b128 v[156:159], v141 offset:23552
	v_lshl_add_u64 v[180:181], v[132:133], 0, s[36:37]
	global_load_dwordx2 v[194:195], v[180:181], off
	v_lshl_add_u64 v[180:181], v[132:133], 0, s[38:39]
	global_load_dwordx2 v[196:197], v[180:181], off
	v_mfma_f32_16x16x32_bf16 v[18:21], v[238:241], v[230:233], v[18:21]
	v_mfma_f32_16x16x32_bf16 v[22:25], v[242:245], v[230:233], v[22:25]
	v_mfma_f32_16x16x32_bf16 v[26:29], v[246:249], v[230:233], v[26:29]
	v_mfma_f32_16x16x32_bf16 v[30:33], v[250:253], v[230:233], v[30:33]
	ds_read_b128 v[230:233], v93 offset:6144
	ds_read_b128 v[160:163], v141 offset:25600
	v_lshl_add_u64 v[180:181], v[132:133], 0, s[40:41]
	global_load_dwordx2 v[198:199], v[180:181], off
	v_lshl_add_u64 v[180:181], v[132:133], 0, s[42:43]
	global_load_dwordx2 v[200:201], v[180:181], off
	v_mfma_f32_16x16x32_bf16 v[2:5], v[238:241], v[234:237], v[2:5]
	v_mfma_f32_16x16x32_bf16 v[6:9], v[242:245], v[234:237], v[6:9]
	v_mfma_f32_16x16x32_bf16 v[10:13], v[246:249], v[234:237], v[10:13]
	v_mfma_f32_16x16x32_bf16 v[14:17], v[250:253], v[234:237], v[14:17]
	ds_read_b128 v[234:237], v93 offset:8192
	s_waitcnt vmcnt(21)
	s_waitcnt lgkmcnt(0)
	s_barrier
	s_mov_b32 s49, s46
	s_mov_b32 s46, s47
	s_mov_b32 s47, s48
	s_mov_b32 s48, s49
	s_add_i32 s50, s50, 1
	s_add_i32 s49, s48, s74
	s_add_i32 s52, s52, 1
	s_and_b32 s54, s52, 7
	s_cmp_eq_u32 s54, 0
	s_cselect_b32 s54, s53, s32
	s_cselect_b32 s55, -1, 0
	s_add_u32 s30, s30, s54
	s_addc_u32 s31, s31, s55
	v_mfma_f32_16x16x32_bf16 v[78:81], v[142:145], v[218:221], v[78:81]
	v_mfma_f32_16x16x32_bf16 v[74:77], v[146:149], v[218:221], v[74:77]
	v_mfma_f32_16x16x32_bf16 v[70:73], v[156:159], v[218:221], v[70:73]
	v_mfma_f32_16x16x32_bf16 v[66:69], v[160:163], v[218:221], v[66:69]
	s_mov_b32 m0, s49
	s_nop 0
	global_load_lds_dwordx4 v88, s[30:31]
	v_mfma_f32_16x16x32_bf16 v[62:65], v[142:145], v[222:225], v[62:65]
	v_mfma_f32_16x16x32_bf16 v[58:61], v[146:149], v[222:225], v[58:61]
	v_mfma_f32_16x16x32_bf16 v[54:57], v[156:159], v[222:225], v[54:57]
	v_mfma_f32_16x16x32_bf16 v[50:53], v[160:163], v[222:225], v[50:53]
	s_add_i32 m0, s49, 0x2000
	s_nop 0
	global_load_lds_dwordx4 v90, s[30:31]
	v_mfma_f32_16x16x32_bf16 v[46:49], v[142:145], v[226:229], v[46:49]
	v_mfma_f32_16x16x32_bf16 v[42:45], v[146:149], v[226:229], v[42:45]
	v_mfma_f32_16x16x32_bf16 v[38:41], v[156:159], v[226:229], v[38:41]
	v_mfma_f32_16x16x32_bf16 v[34:37], v[160:163], v[226:229], v[34:37]
	s_add_i32 m0, s49, 0x4000
	s_nop 0
	global_load_lds_dwordx4 v92, s[30:31]
	v_mfma_f32_16x16x32_bf16 v[18:21], v[142:145], v[230:233], v[18:21]
	v_mfma_f32_16x16x32_bf16 v[22:25], v[146:149], v[230:233], v[22:25]
	v_mfma_f32_16x16x32_bf16 v[26:29], v[156:159], v[230:233], v[26:29]
	v_mfma_f32_16x16x32_bf16 v[30:33], v[160:163], v[230:233], v[30:33]
	s_add_i32 m0, s49, 0x6000
	s_nop 0
	global_load_lds_dwordx4 v94, s[30:31]
	v_mfma_f32_16x16x32_bf16 v[2:5], v[142:145], v[234:237], v[2:5]
	v_mfma_f32_16x16x32_bf16 v[6:9], v[146:149], v[234:237], v[6:9]
	v_mfma_f32_16x16x32_bf16 v[10:13], v[156:159], v[234:237], v[10:13]
	v_mfma_f32_16x16x32_bf16 v[14:17], v[160:163], v[234:237], v[14:17]
	s_add_i32 m0, s49, 0x8000
	s_nop 0
	global_load_lds_dwordx4 v96, s[30:31]
	v_cvt_pk_bf16_f32 v172, v202, v204
	v_cvt_pk_bf16_f32 v173, v206, v208
	v_cvt_pk_bf16_f32 v174, v210, v212
	v_cvt_pk_bf16_f32 v175, v214, v216
	v_cvt_pk_bf16_f32 v176, v203, v205
	v_cvt_pk_bf16_f32 v177, v207, v209
	v_cvt_pk_bf16_f32 v178, v211, v213
	v_cvt_pk_bf16_f32 v179, v215, v217
	ds_write_b128 v95, v[172:175] offset:19456
	ds_write_b128 v95, v[176:179] offset:19584
	v_add_u32_e32 v91, s46, v135
	v_add_u32_e32 v93, s46, v137
	ds_read_b128 v[238:241], v139 offset:0
	ds_read_b128 v[242:245], v139 offset:2048
	ds_read_b128 v[246:249], v139 offset:4096
	ds_read_b128 v[250:253], v139 offset:6144
	ds_read_b128 v[218:221], v91 offset:0
	ds_read_b128 v[222:225], v91 offset:2048
	ds_read_b128 v[226:229], v91 offset:4096
	ds_read_b128 v[230:233], v91 offset:6144
	ds_read_b128 v[234:237], v91 offset:8192
	s_waitcnt lgkmcnt(0)
; #define MD_GLDS_A(buf, tau) do { _Pragma("unroll") for (int i = 0; i < 5; ++i) if (amask & (1u << i)) \
;         __builtin_amdgcn_global_load_lds((const unsigned*)((const char*)HIDp + aoff[i] + (size_t)((tau) & 7) * 128), (PG8_LAS unsigned*)(MD_SA(buf) + wid * 1024 + i * 8192), 16, 0, 0); } while (0)
; #define MD_B_ISSUE(sb, tau) do { const char* kb_ = Bb + (size_t)((tau) >> 3) * 512 + (size_t)((tau) & 7) * (64 * (size_t)RB); _Pragma("unroll") for (int j = 0; j < 8; ++j) { const char* p_ = kb_ + (size_t)j * RB; \
;         asm volatile("global_load_dwordx2 %0, %1, off" : "=&v"(sb[j]) : "v"(p_) : "memory"); } } while (0)
; #define MD_B_WAIT(sb, N) asm volatile("s_waitcnt vmcnt(%8)" : "+v"(sb[0]), "+v"(sb[1]), "+v"(sb[2]), "+v"(sb[3]), "+v"(sb[4]), "+v"(sb[5]), "+v"(sb[6]), "+v"(sb[7]) : "n"(N) : "memory")
; __device__ __forceinline__ void moe_down_stream(PG8_LAS unsigned char* lds, int e, int cb0, int slot0, int nv, const bf16_t* HIDp, const float* Wd, bf16_t* Y, const float* slot_w, const int* slot_dst) {
;     ...
;     f32x4 acc[DNM][4];
; #pragma unroll
;     for (int m = 0; m < DNM; ++m)
; #pragma unroll
;         for (int n = 0; n < 4; ++n) acc[m][n] = (f32x4){0.f, 0.f, 0.f, 0.f};
;     f32x2 s0[8], s1[8];
;     MD_GLDS_A(0, 0); MD_B_ISSUE(s0, 0); MD_B_ISSUE(s1, 1);
;     MD_B_WAIT(s0, 8); MD_B_WRITE(s0, 0); __builtin_amdgcn_sched_barrier(0); MD_B_ISSUE(s0, 2);
;     asm volatile("s_waitcnt vmcnt(16)" ::: "memory");
;     asm volatile("s_waitcnt lgkmcnt(0)" ::: "memory"); __builtin_amdgcn_s_barrier(); asm volatile("" ::: "memory");
; #pragma unroll 1
;     for (int t = 0; t < NT; t += 2) {
;         if (t + 2 < NT) MD_B_WAIT(s1, 8); else MD_B_WAIT(s1, 0);
;         MD_B_WRITE(s1, 1); __builtin_amdgcn_sched_barrier(0); MD_GLDS_A(1, t + 1); __builtin_amdgcn_sched_barrier(0);
;         if (t + 3 < NT) MD_B_ISSUE(s1, t + 3);
;         MD_COMPUTE(0);
;         MD_END(t + 3 >= NT);
;         if (t + 2 < NT) { MD_B_WAIT(s0, 8); MD_B_WRITE(s0, 0); __builtin_amdgcn_sched_barrier(0); MD_GLDS_A(0, t + 2); __builtin_amdgcn_sched_barrier(0); }
;         if (t + 4 < NT) MD_B_ISSUE(s0, t + 4);
;         MD_COMPUTE(1);
;         MD_END(t + 4 >= NT);
	v_mfma_f32_16x16x32_bf16 v[78:81], v[238:241], v[218:221], v[78:81]
	v_mfma_f32_16x16x32_bf16 v[74:77], v[242:245], v[218:221], v[74:77]
	v_mfma_f32_16x16x32_bf16 v[70:73], v[246:249], v[218:221], v[70:73]
	v_mfma_f32_16x16x32_bf16 v[66:69], v[250:253], v[218:221], v[66:69]
	ds_read_b128 v[218:221], v93 offset:0
	ds_read_b128 v[142:145], v141 offset:0
	s_add_i32 s51, s51, 1
	s_and_b32 s54, s51, 7
	s_cmp_eq_u32 s54, 0
	s_cselect_b32 s44, s34, s35
	s_cselect_b32 s45, -1, 0
	v_lshl_add_u64 v[132:133], v[132:133], 0, s[44:45]
	global_load_dwordx2 v[202:203], v[132:133], off
	v_lshl_add_u64 v[180:181], v[132:133], 0, s[24:25]
	global_load_dwordx2 v[204:205], v[180:181], off
	v_mfma_f32_16x16x32_bf16 v[62:65], v[238:241], v[222:225], v[62:65]
	v_mfma_f32_16x16x32_bf16 v[58:61], v[242:245], v[222:225], v[58:61]
	v_mfma_f32_16x16x32_bf16 v[54:57], v[246:249], v[222:225], v[54:57]
	v_mfma_f32_16x16x32_bf16 v[50:53], v[250:253], v[222:225], v[50:53]
	ds_read_b128 v[222:225], v93 offset:2048
	ds_read_b128 v[146:149], v141 offset:2048
	v_lshl_add_u64 v[180:181], v[132:133], 0, s[26:27]
	global_load_dwordx2 v[206:207], v[180:181], off
	v_lshl_add_u64 v[180:181], v[132:133], 0, s[28:29]
	global_load_dwordx2 v[208:209], v[180:181], off
	v_mfma_f32_16x16x32_bf16 v[46:49], v[238:241], v[226:229], v[46:49]
	v_mfma_f32_16x16x32_bf16 v[42:45], v[242:245], v[226:229], v[42:45]
	v_mfma_f32_16x16x32_bf16 v[38:41], v[246:249], v[226:229], v[38:41]
	v_mfma_f32_16x16x32_bf16 v[34:37], v[250:253], v[226:229], v[34:37]
	ds_read_b128 v[226:229], v93 offset:4096
	ds_read_b128 v[156:159], v141 offset:4096
	v_lshl_add_u64 v[180:181], v[132:133], 0, s[36:37]
	global_load_dwordx2 v[210:211], v[180:181], off
	v_lshl_add_u64 v[180:181], v[132:133], 0, s[38:39]
	global_load_dwordx2 v[212:213], v[180:181], off
	v_mfma_f32_16x16x32_bf16 v[18:21], v[238:241], v[230:233], v[18:21]
	v_mfma_f32_16x16x32_bf16 v[22:25], v[242:245], v[230:233], v[22:25]
	v_mfma_f32_16x16x32_bf16 v[26:29], v[246:249], v[230:233], v[26:29]
	v_mfma_f32_16x16x32_bf16 v[30:33], v[250:253], v[230:233], v[30:33]
	ds_read_b128 v[230:233], v93 offset:6144
	ds_read_b128 v[160:163], v141 offset:6144
	v_lshl_add_u64 v[180:181], v[132:133], 0, s[40:41]
	global_load_dwordx2 v[214:215], v[180:181], off
	v_lshl_add_u64 v[180:181], v[132:133], 0, s[42:43]
	global_load_dwordx2 v[216:217], v[180:181], off
	v_mfma_f32_16x16x32_bf16 v[2:5], v[238:241], v[234:237], v[2:5]
	v_mfma_f32_16x16x32_bf16 v[6:9], v[242:245], v[234:237], v[6:9]
	v_mfma_f32_16x16x32_bf16 v[10:13], v[246:249], v[234:237], v[10:13]
	v_mfma_f32_16x16x32_bf16 v[14:17], v[250:253], v[234:237], v[14:17]
	ds_read_b128 v[234:237], v93 offset:8192
	s_waitcnt vmcnt(21)
	s_waitcnt lgkmcnt(0)
	s_barrier
	s_mov_b32 s49, s46
	s_mov_b32 s46, s47
	s_mov_b32 s47, s48
	s_mov_b32 s48, s49
	s_add_i32 s50, s50, 1
	s_add_i32 s49, s48, s74
	s_add_i32 s52, s52, 1
	s_and_b32 s54, s52, 7
	s_cmp_eq_u32 s54, 0
	s_cselect_b32 s54, s53, s32
	s_cselect_b32 s55, -1, 0
	s_add_u32 s30, s30, s54
	s_addc_u32 s31, s31, s55
	v_mfma_f32_16x16x32_bf16 v[78:81], v[142:145], v[218:221], v[78:81]
	v_mfma_f32_16x16x32_bf16 v[74:77], v[146:149], v[218:221], v[74:77]
	v_mfma_f32_16x16x32_bf16 v[70:73], v[156:159], v[218:221], v[70:73]
	v_mfma_f32_16x16x32_bf16 v[66:69], v[160:163], v[218:221], v[66:69]
	s_mov_b32 m0, s49
	s_nop 0
	global_load_lds_dwordx4 v88, s[30:31]
	v_mfma_f32_16x16x32_bf16 v[62:65], v[142:145], v[222:225], v[62:65]
	v_mfma_f32_16x16x32_bf16 v[58:61], v[146:149], v[222:225], v[58:61]
	v_mfma_f32_16x16x32_bf16 v[54:57], v[156:159], v[222:225], v[54:57]
	v_mfma_f32_16x16x32_bf16 v[50:53], v[160:163], v[222:225], v[50:53]
	s_add_i32 m0, s49, 0x2000
	s_nop 0
	global_load_lds_dwordx4 v90, s[30:31]
	v_mfma_f32_16x16x32_bf16 v[46:49], v[142:145], v[226:229], v[46:49]
	v_mfma_f32_16x16x32_bf16 v[42:45], v[146:149], v[226:229], v[42:45]
	v_mfma_f32_16x16x32_bf16 v[38:41], v[156:159], v[226:229], v[38:41]
	v_mfma_f32_16x16x32_bf16 v[34:37], v[160:163], v[226:229], v[34:37]
	s_add_i32 m0, s49, 0x4000
	s_nop 0
	global_load_lds_dwordx4 v92, s[30:31]
	v_mfma_f32_16x16x32_bf16 v[18:21], v[142:145], v[230:233], v[18:21]
	v_mfma_f32_16x16x32_bf16 v[22:25], v[146:149], v[230:233], v[22:25]
	v_mfma_f32_16x16x32_bf16 v[26:29], v[156:159], v[230:233], v[26:29]
	v_mfma_f32_16x16x32_bf16 v[30:33], v[160:163], v[230:233], v[30:33]
	s_add_i32 m0, s49, 0x6000
	s_nop 0
	global_load_lds_dwordx4 v94, s[30:31]
	v_mfma_f32_16x16x32_bf16 v[2:5], v[142:145], v[234:237], v[2:5]
	v_mfma_f32_16x16x32_bf16 v[6:9], v[146:149], v[234:237], v[6:9]
	v_mfma_f32_16x16x32_bf16 v[10:13], v[156:159], v[234:237], v[10:13]
	v_mfma_f32_16x16x32_bf16 v[14:17], v[160:163], v[234:237], v[14:17]
	s_add_i32 m0, s49, 0x8000
	s_nop 0
	global_load_lds_dwordx4 v96, s[30:31]
	v_cvt_pk_bf16_f32 v172, v98, v100
	v_cvt_pk_bf16_f32 v173, v102, v104
	v_cvt_pk_bf16_f32 v174, v106, v108
	v_cvt_pk_bf16_f32 v175, v110, v112
	v_cvt_pk_bf16_f32 v176, v99, v101
	v_cvt_pk_bf16_f32 v177, v103, v105
	v_cvt_pk_bf16_f32 v178, v107, v109
	v_cvt_pk_bf16_f32 v179, v111, v113
	ds_write_b128 v95, v[172:175] offset:0
	ds_write_b128 v95, v[176:179] offset:128
	v_add_u32_e32 v91, s46, v135
	v_add_u32_e32 v93, s46, v137
	ds_read_b128 v[238:241], v139 offset:19456
	ds_read_b128 v[242:245], v139 offset:21504
	ds_read_b128 v[246:249], v139 offset:23552
	ds_read_b128 v[250:253], v139 offset:25600
	ds_read_b128 v[218:221], v91 offset:0
	ds_read_b128 v[222:225], v91 offset:2048
	ds_read_b128 v[226:229], v91 offset:4096
	ds_read_b128 v[230:233], v91 offset:6144
	ds_read_b128 v[234:237], v91 offset:8192
	s_waitcnt lgkmcnt(0)
; #define MD_GLDS_A(buf, tau) do { _Pragma("unroll") for (int i = 0; i < 5; ++i) if (amask & (1u << i)) \
;         __builtin_amdgcn_global_load_lds((const unsigned*)((const char*)HIDp + aoff[i] + (size_t)((tau) & 7) * 128), (PG8_LAS unsigned*)(MD_SA(buf) + wid * 1024 + i * 8192), 16, 0, 0); } while (0)
; #define MD_B_ISSUE(sb, tau) do { const char* kb_ = Bb + (size_t)((tau) >> 3) * 512 + (size_t)((tau) & 7) * (64 * (size_t)RB); _Pragma("unroll") for (int j = 0; j < 8; ++j) { const char* p_ = kb_ + (size_t)j * RB; \
;         asm volatile("global_load_dwordx2 %0, %1, off" : "=&v"(sb[j]) : "v"(p_) : "memory"); } } while (0)
; #define MD_B_WAIT(sb, N) asm volatile("s_waitcnt vmcnt(%8)" : "+v"(sb[0]), "+v"(sb[1]), "+v"(sb[2]), "+v"(sb[3]), "+v"(sb[4]), "+v"(sb[5]), "+v"(sb[6]), "+v"(sb[7]) : "n"(N) : "memory")
; #define MD_END(last) do { if (last) asm volatile("s_waitcnt vmcnt(0)" ::: "memory"); else asm volatile("s_waitcnt vmcnt(8)" ::: "memory"); \
;         asm volatile("s_waitcnt lgkmcnt(0)" ::: "memory"); __builtin_amdgcn_s_barrier(); asm volatile("" ::: "memory"); } while (0)
; __device__ __forceinline__ void moe_down_stream(PG8_LAS unsigned char* lds, int e, int cb0, int slot0, int nv, const bf16_t* HIDp, const float* Wd, bf16_t* Y, const float* slot_w, const int* slot_dst) {
;     ...
;     for (int t = 0; t < NT; t += 2) {
;         if (t + 2 < NT) MD_B_WAIT(s1, 8); else MD_B_WAIT(s1, 0);
;         MD_B_WRITE(s1, 1); __builtin_amdgcn_sched_barrier(0); MD_GLDS_A(1, t + 1); __builtin_amdgcn_sched_barrier(0);
;         if (t + 3 < NT) MD_B_ISSUE(s1, t + 3);
;         MD_COMPUTE(0);
;         MD_END(t + 3 >= NT);
;         if (t + 2 < NT) { MD_B_WAIT(s0, 8); MD_B_WRITE(s0, 0); __builtin_amdgcn_sched_barrier(0); MD_GLDS_A(0, t + 2); __builtin_amdgcn_sched_barrier(0); }
;         if (t + 4 < NT) MD_B_ISSUE(s0, t + 4);
;         MD_COMPUTE(1);
;         MD_END(t + 4 >= NT);
	v_mfma_f32_16x16x32_bf16 v[78:81], v[238:241], v[218:221], v[78:81]
	v_mfma_f32_16x16x32_bf16 v[74:77], v[242:245], v[218:221], v[74:77]
	v_mfma_f32_16x16x32_bf16 v[70:73], v[246:249], v[218:221], v[70:73]
	v_mfma_f32_16x16x32_bf16 v[66:69], v[250:253], v[218:221], v[66:69]
	ds_read_b128 v[218:221], v93 offset:0
	ds_read_b128 v[142:145], v141 offset:19456
	s_add_i32 s51, s51, 1
	s_and_b32 s54, s51, 7
	s_cmp_eq_u32 s54, 0
	s_cselect_b32 s44, s34, s35
	s_cselect_b32 s45, -1, 0
	v_lshl_add_u64 v[132:133], v[132:133], 0, s[44:45]
	global_load_dwordx2 v[98:99], v[132:133], off
	v_lshl_add_u64 v[180:181], v[132:133], 0, s[24:25]
	global_load_dwordx2 v[100:101], v[180:181], off
	v_mfma_f32_16x16x32_bf16 v[62:65], v[238:241], v[222:225], v[62:65]
	v_mfma_f32_16x16x32_bf16 v[58:61], v[242:245], v[222:225], v[58:61]
	v_mfma_f32_16x16x32_bf16 v[54:57], v[246:249], v[222:225], v[54:57]
	v_mfma_f32_16x16x32_bf16 v[50:53], v[250:253], v[222:225], v[50:53]
	ds_read_b128 v[222:225], v93 offset:2048
	ds_read_b128 v[146:149], v141 offset:21504
	v_lshl_add_u64 v[180:181], v[132:133], 0, s[26:27]
	global_load_dwordx2 v[102:103], v[180:181], off
	v_lshl_add_u64 v[180:181], v[132:133], 0, s[28:29]
	global_load_dwordx2 v[104:105], v[180:181], off
	v_mfma_f32_16x16x32_bf16 v[46:49], v[238:241], v[226:229], v[46:49]
	v_mfma_f32_16x16x32_bf16 v[42:45], v[242:245], v[226:229], v[42:45]
	v_mfma_f32_16x16x32_bf16 v[38:41], v[246:249], v[226:229], v[38:41]
	v_mfma_f32_16x16x32_bf16 v[34:37], v[250:253], v[226:229], v[34:37]
	ds_read_b128 v[226:229], v93 offset:4096
	ds_read_b128 v[156:159], v141 offset:23552
	v_lshl_add_u64 v[180:181], v[132:133], 0, s[36:37]
	global_load_dwordx2 v[106:107], v[180:181], off
	v_lshl_add_u64 v[180:181], v[132:133], 0, s[38:39]
	global_load_dwordx2 v[108:109], v[180:181], off
	v_mfma_f32_16x16x32_bf16 v[18:21], v[238:241], v[230:233], v[18:21]
	v_mfma_f32_16x16x32_bf16 v[22:25], v[242:245], v[230:233], v[22:25]
	v_mfma_f32_16x16x32_bf16 v[26:29], v[246:249], v[230:233], v[26:29]
	v_mfma_f32_16x16x32_bf16 v[30:33], v[250:253], v[230:233], v[30:33]
	ds_read_b128 v[230:233], v93 offset:6144
	ds_read_b128 v[160:163], v141 offset:25600
	v_lshl_add_u64 v[180:181], v[132:133], 0, s[40:41]
	global_load_dwordx2 v[110:111], v[180:181], off
	v_lshl_add_u64 v[180:181], v[132:133], 0, s[42:43]
	global_load_dwordx2 v[112:113], v[180:181], off
	v_mfma_f32_16x16x32_bf16 v[2:5], v[238:241], v[234:237], v[2:5]
	v_mfma_f32_16x16x32_bf16 v[6:9], v[242:245], v[234:237], v[6:9]
	v_mfma_f32_16x16x32_bf16 v[10:13], v[246:249], v[234:237], v[10:13]
	v_mfma_f32_16x16x32_bf16 v[14:17], v[250:253], v[234:237], v[14:17]
	ds_read_b128 v[234:237], v93 offset:8192
	s_waitcnt vmcnt(21)
	s_waitcnt lgkmcnt(0)
	s_barrier
	s_mov_b32 s49, s46
	s_mov_b32 s46, s47
	s_mov_b32 s47, s48
	s_mov_b32 s48, s49
	s_add_i32 s50, s50, 1
	s_mov_b32 s56, 5
.Lmd_loop_Y:
	v_mfma_f32_16x16x32_bf16 v[78:81], v[142:145], v[218:221], v[78:81]
	v_mfma_f32_16x16x32_bf16 v[74:77], v[146:149], v[218:221], v[74:77]
	v_mfma_f32_16x16x32_bf16 v[70:73], v[156:159], v[218:221], v[70:73]
	v_mfma_f32_16x16x32_bf16 v[66:69], v[160:163], v[218:221], v[66:69]
	v_mfma_f32_16x16x32_bf16 v[62:65], v[142:145], v[222:225], v[62:65]
	v_mfma_f32_16x16x32_bf16 v[58:61], v[146:149], v[222:225], v[58:61]
	v_mfma_f32_16x16x32_bf16 v[54:57], v[156:159], v[222:225], v[54:57]
	v_mfma_f32_16x16x32_bf16 v[50:53], v[160:163], v[222:225], v[50:53]
	v_mfma_f32_16x16x32_bf16 v[46:49], v[142:145], v[226:229], v[46:49]
	v_mfma_f32_16x16x32_bf16 v[42:45], v[146:149], v[226:229], v[42:45]
	v_mfma_f32_16x16x32_bf16 v[38:41], v[156:159], v[226:229], v[38:41]
	v_mfma_f32_16x16x32_bf16 v[34:37], v[160:163], v[226:229], v[34:37]
	v_mfma_f32_16x16x32_bf16 v[18:21], v[142:145], v[230:233], v[18:21]
	v_mfma_f32_16x16x32_bf16 v[22:25], v[146:149], v[230:233], v[22:25]
	v_mfma_f32_16x16x32_bf16 v[26:29], v[156:159], v[230:233], v[26:29]
	v_mfma_f32_16x16x32_bf16 v[30:33], v[160:163], v[230:233], v[30:33]
	v_mfma_f32_16x16x32_bf16 v[2:5], v[142:145], v[234:237], v[2:5]
	v_mfma_f32_16x16x32_bf16 v[6:9], v[146:149], v[234:237], v[6:9]
	v_mfma_f32_16x16x32_bf16 v[10:13], v[156:159], v[234:237], v[10:13]
	v_mfma_f32_16x16x32_bf16 v[14:17], v[160:163], v[234:237], v[14:17]
	s_and_b32 s54, s50, 7
	s_cmp_lg_u32 s54, 0
	s_cbranch_scc1 .Lmd_noepi_Y
; #define PG8_LAS __attribute__((address_space(3)))
; __device__ __forceinline__ unsigned cvtpk(float lo, float hi) { f32x2 v = {lo, hi}; bf16x2_t b = __builtin_convertvector(v, bf16x2_t); return __builtin_bit_cast(unsigned, b); }
; __device__ __forceinline__ void moe_down_stream(PG8_LAS unsigned char* lds, int e, int cb0, int slot0, int nv, const bf16_t* HIDp, const float* Wd, bf16_t* Y, const float* slot_w, const int* slot_dst) {
;     ...
;         if (((t + 1) & 7) == 7) {
;             const int cb = cb0 + ((t + 1) >> 3);
; #pragma unroll
;             for (int m = 0; m < DNM; ++m) {
;                 const float w_ = lw[4 * (16 * m + fr) + wr];
; #pragma unroll
;                 for (int p = 0; p < 2; ++p) { const f32x4 v0 = acc[m][2 * p] * w_, v1 = acc[m][2 * p + 1] * w_; u32x4 w; w.x = cvtpk(v0[0], v0[1]); w.y = cvtpk(v0[2], v0[3]); w.z = cvtpk(v1[0], v1[1]); w.w = cvtpk(v1[2], v1[3]);
;                     *(PG8_LAS u32x4*)(stg + fr * 128 + (((4 * p + fq) ^ (fr & 7)) * 16)) = w; }
; #pragma unroll
;                 for (int hh = 0; hh < 2; ++hh) { const int r = (lane >> 3) + 8 * hh, cc = lane & 7; const u32x4 d = *(const PG8_LAS u32x4*)(stg + r * 128 + ((cc ^ (r & 7)) * 16)); const int dst_ = ldst[4 * (16 * m + r) + wr];
;                     if (dst_ >= 0) *(u32x4*)(Y + (size_t)dst_ * D + 128 * cb + 64 * wc + 8 * cc) = d; }
; #pragma unroll
;                 for (int n = 0; n < 4; ++n) acc[m][n] = (f32x4){0.f, 0.f, 0.f, 0.f}; } }
	s_add_i32 s54, s48, s74
	v_add_u32_e32 v164, s54, v84
	v_add_u32_e32 v165, s54, v85
	ds_read_b32 v150, v82 offset:0
	ds_read_b32 v151, v83 offset:0
	ds_read_b32 v166, v83 offset:128
	s_waitcnt lgkmcnt(2)
	v_mul_f32_e32 v78, v150, v78
	v_mul_f32_e32 v79, v150, v79
	v_mul_f32_e32 v80, v150, v80
	v_mul_f32_e32 v81, v150, v81
	v_mul_f32_e32 v74, v150, v74
	v_mul_f32_e32 v75, v150, v75
	v_mul_f32_e32 v76, v150, v76
	v_mul_f32_e32 v77, v150, v77
	v_cvt_pk_bf16_f32 v182, v78, v79
	v_cvt_pk_bf16_f32 v183, v80, v81
	v_cvt_pk_bf16_f32 v184, v74, v75
	v_cvt_pk_bf16_f32 v185, v76, v77
	ds_write_b128 v164, v[182:185]
	v_mul_f32_e32 v70, v150, v70
	v_mul_f32_e32 v71, v150, v71
	v_mul_f32_e32 v72, v150, v72
	v_mul_f32_e32 v73, v150, v73
	v_mul_f32_e32 v66, v150, v66
	v_mul_f32_e32 v67, v150, v67
	v_mul_f32_e32 v68, v150, v68
	v_mul_f32_e32 v69, v150, v69
	v_cvt_pk_bf16_f32 v182, v70, v71
	v_cvt_pk_bf16_f32 v183, v72, v73
	v_cvt_pk_bf16_f32 v184, v66, v67
	v_cvt_pk_bf16_f32 v185, v68, v69
	v_xor_b32_e32 v167, 64, v164
	ds_write_b128 v167, v[182:185]
	v_mov_b32_e32 v78, 0
	v_mov_b32_e32 v74, 0
	v_mov_b32_e32 v70, 0
	v_mov_b32_e32 v66, 0
	v_mov_b32_e32 v79, 0
	v_mov_b32_e32 v75, 0
	v_mov_b32_e32 v71, 0
	v_mov_b32_e32 v67, 0
	v_mov_b32_e32 v80, 0
	v_mov_b32_e32 v76, 0
	v_mov_b32_e32 v72, 0
	v_mov_b32_e32 v68, 0
	v_mov_b32_e32 v81, 0
	v_mov_b32_e32 v77, 0
	v_mov_b32_e32 v73, 0
	v_mov_b32_e32 v69, 0
	ds_read_b128 v[182:185], v165 offset:0
	v_cmp_lt_i32_e32 vcc, -1, v151
	v_lshlrev_b32_e32 v148, 13, v151
	v_mov_b32_e32 v149, 0
	v_lshl_add_u64 v[148:149], v[148:149], 0, v[86:87]
	v_cndmask_b32_e32 v148, v168, v148, vcc
	v_cndmask_b32_e32 v149, v169, v149, vcc
	s_waitcnt lgkmcnt(0)
	global_store_dwordx4 v[148:149], v[182:185], off
	ds_read_b128 v[182:185], v165 offset:8192
	v_cmp_lt_i32_e32 vcc, -1, v166
	v_lshlrev_b32_e32 v148, 13, v166
	v_mov_b32_e32 v149, 0
	v_lshl_add_u64 v[148:149], v[148:149], 0, v[86:87]
	v_cndmask_b32_e32 v148, v168, v148, vcc
	v_cndmask_b32_e32 v149, v169, v149, vcc
	s_waitcnt lgkmcnt(0)
	global_store_dwordx4 v[148:149], v[182:185], off
	ds_read_b32 v150, v82 offset:256
	ds_read_b32 v151, v83 offset:256
	ds_read_b32 v166, v83 offset:384
	s_waitcnt lgkmcnt(2)
	v_mul_f32_e32 v62, v150, v62
	v_mul_f32_e32 v63, v150, v63
	v_mul_f32_e32 v64, v150, v64
	v_mul_f32_e32 v65, v150, v65
	v_mul_f32_e32 v58, v150, v58
	v_mul_f32_e32 v59, v150, v59
	v_mul_f32_e32 v60, v150, v60
	v_mul_f32_e32 v61, v150, v61
	v_cvt_pk_bf16_f32 v182, v62, v63
	v_cvt_pk_bf16_f32 v183, v64, v65
	v_cvt_pk_bf16_f32 v184, v58, v59
	v_cvt_pk_bf16_f32 v185, v60, v61
	ds_write_b128 v164, v[182:185]
	v_mul_f32_e32 v54, v150, v54
	v_mul_f32_e32 v55, v150, v55
	v_mul_f32_e32 v56, v150, v56
	v_mul_f32_e32 v57, v150, v57
	v_mul_f32_e32 v50, v150, v50
	v_mul_f32_e32 v51, v150, v51
	v_mul_f32_e32 v52, v150, v52
	v_mul_f32_e32 v53, v150, v53
	v_cvt_pk_bf16_f32 v182, v54, v55
	v_cvt_pk_bf16_f32 v183, v56, v57
	v_cvt_pk_bf16_f32 v184, v50, v51
	v_cvt_pk_bf16_f32 v185, v52, v53
	v_xor_b32_e32 v167, 64, v164
	ds_write_b128 v167, v[182:185]
	v_mov_b32_e32 v62, 0
	v_mov_b32_e32 v58, 0
	v_mov_b32_e32 v54, 0
	v_mov_b32_e32 v50, 0
	v_mov_b32_e32 v63, 0
	v_mov_b32_e32 v59, 0
	v_mov_b32_e32 v55, 0
	v_mov_b32_e32 v51, 0
	v_mov_b32_e32 v64, 0
	v_mov_b32_e32 v60, 0
	v_mov_b32_e32 v56, 0
	v_mov_b32_e32 v52, 0
	v_mov_b32_e32 v65, 0
	v_mov_b32_e32 v61, 0
	v_mov_b32_e32 v57, 0
	v_mov_b32_e32 v53, 0
	ds_read_b128 v[182:185], v165 offset:0
	v_cmp_lt_i32_e32 vcc, -1, v151
	v_lshlrev_b32_e32 v148, 13, v151
	v_mov_b32_e32 v149, 0
	v_lshl_add_u64 v[148:149], v[148:149], 0, v[86:87]
	v_cndmask_b32_e32 v148, v168, v148, vcc
	v_cndmask_b32_e32 v149, v169, v149, vcc
	s_waitcnt lgkmcnt(0)
	global_store_dwordx4 v[148:149], v[182:185], off
	ds_read_b128 v[182:185], v165 offset:8192
	v_cmp_lt_i32_e32 vcc, -1, v166
	v_lshlrev_b32_e32 v148, 13, v166
	v_mov_b32_e32 v149, 0
	v_lshl_add_u64 v[148:149], v[148:149], 0, v[86:87]
	v_cndmask_b32_e32 v148, v168, v148, vcc
	v_cndmask_b32_e32 v149, v169, v149, vcc
	s_waitcnt lgkmcnt(0)
	global_store_dwordx4 v[148:149], v[182:185], off
	ds_read_b32 v150, v82 offset:512
	ds_read_b32 v151, v83 offset:512
	ds_read_b32 v166, v83 offset:640
	s_waitcnt lgkmcnt(2)
	v_mul_f32_e32 v46, v150, v46
	v_mul_f32_e32 v47, v150, v47
	v_mul_f32_e32 v48, v150, v48
	v_mul_f32_e32 v49, v150, v49
	v_mul_f32_e32 v42, v150, v42
	v_mul_f32_e32 v43, v150, v43
	v_mul_f32_e32 v44, v150, v44
	v_mul_f32_e32 v45, v150, v45
	v_cvt_pk_bf16_f32 v182, v46, v47
	v_cvt_pk_bf16_f32 v183, v48, v49
	v_cvt_pk_bf16_f32 v184, v42, v43
	v_cvt_pk_bf16_f32 v185, v44, v45
	ds_write_b128 v164, v[182:185]
	v_mul_f32_e32 v38, v150, v38
	v_mul_f32_e32 v39, v150, v39
	v_mul_f32_e32 v40, v150, v40
	v_mul_f32_e32 v41, v150, v41
	v_mul_f32_e32 v34, v150, v34
	v_mul_f32_e32 v35, v150, v35
	v_mul_f32_e32 v36, v150, v36
	v_mul_f32_e32 v37, v150, v37
	v_cvt_pk_bf16_f32 v182, v38, v39
	v_cvt_pk_bf16_f32 v183, v40, v41
	v_cvt_pk_bf16_f32 v184, v34, v35
	v_cvt_pk_bf16_f32 v185, v36, v37
	v_xor_b32_e32 v167, 64, v164
	ds_write_b128 v167, v[182:185]
	v_mov_b32_e32 v46, 0
	v_mov_b32_e32 v42, 0
	v_mov_b32_e32 v38, 0
	v_mov_b32_e32 v34, 0
	v_mov_b32_e32 v47, 0
	v_mov_b32_e32 v43, 0
	v_mov_b32_e32 v39, 0
	v_mov_b32_e32 v35, 0
	v_mov_b32_e32 v48, 0
	v_mov_b32_e32 v44, 0
	v_mov_b32_e32 v40, 0
	v_mov_b32_e32 v36, 0
	v_mov_b32_e32 v49, 0
	v_mov_b32_e32 v45, 0
	v_mov_b32_e32 v41, 0
	v_mov_b32_e32 v37, 0
	ds_read_b128 v[182:185], v165 offset:0
	v_cmp_lt_i32_e32 vcc, -1, v151
	v_lshlrev_b32_e32 v148, 13, v151
	v_mov_b32_e32 v149, 0
	v_lshl_add_u64 v[148:149], v[148:149], 0, v[86:87]
	v_cndmask_b32_e32 v148, v168, v148, vcc
	v_cndmask_b32_e32 v149, v169, v149, vcc
	s_waitcnt lgkmcnt(0)
; #define PG8_LAS __attribute__((address_space(3)))
; __device__ __forceinline__ unsigned cvtpk(float lo, float hi) { f32x2 v = {lo, hi}; bf16x2_t b = __builtin_convertvector(v, bf16x2_t); return __builtin_bit_cast(unsigned, b); }
; __device__ __forceinline__ void moe_down_stream(PG8_LAS unsigned char* lds, int e, int cb0, int slot0, int nv, const bf16_t* HIDp, const float* Wd, bf16_t* Y, const float* slot_w, const int* slot_dst) {
;     ...
;         if (((t + 1) & 7) == 7) {
;             const int cb = cb0 + ((t + 1) >> 3);
; #pragma unroll
;             for (int m = 0; m < DNM; ++m) {
;                 const float w_ = lw[4 * (16 * m + fr) + wr];
; #pragma unroll
;                 for (int p = 0; p < 2; ++p) { const f32x4 v0 = acc[m][2 * p] * w_, v1 = acc[m][2 * p + 1] * w_; u32x4 w; w.x = cvtpk(v0[0], v0[1]); w.y = cvtpk(v0[2], v0[3]); w.z = cvtpk(v1[0], v1[1]); w.w = cvtpk(v1[2], v1[3]);
;                     *(PG8_LAS u32x4*)(stg + fr * 128 + (((4 * p + fq) ^ (fr & 7)) * 16)) = w; }
; #pragma unroll
;                 for (int hh = 0; hh < 2; ++hh) { const int r = (lane >> 3) + 8 * hh, cc = lane & 7; const u32x4 d = *(const PG8_LAS u32x4*)(stg + r * 128 + ((cc ^ (r & 7)) * 16)); const int dst_ = ldst[4 * (16 * m + r) + wr];
;                     if (dst_ >= 0) *(u32x4*)(Y + (size_t)dst_ * D + 128 * cb + 64 * wc + 8 * cc) = d; }
; #pragma unroll
;                 for (int n = 0; n < 4; ++n) acc[m][n] = (f32x4){0.f, 0.f, 0.f, 0.f}; } }
	global_store_dwordx4 v[148:149], v[182:185], off
	ds_read_b128 v[182:185], v165 offset:8192
	v_cmp_lt_i32_e32 vcc, -1, v166
	v_lshlrev_b32_e32 v148, 13, v166
	v_mov_b32_e32 v149, 0
	v_lshl_add_u64 v[148:149], v[148:149], 0, v[86:87]
	v_cndmask_b32_e32 v148, v168, v148, vcc
	v_cndmask_b32_e32 v149, v169, v149, vcc
	s_waitcnt lgkmcnt(0)
	global_store_dwordx4 v[148:149], v[182:185], off
	ds_read_b32 v150, v82 offset:768
	ds_read_b32 v151, v83 offset:768
	ds_read_b32 v166, v83 offset:896
	s_waitcnt lgkmcnt(2)
	v_mul_f32_e32 v18, v150, v18
	v_mul_f32_e32 v19, v150, v19
	v_mul_f32_e32 v20, v150, v20
	v_mul_f32_e32 v21, v150, v21
	v_mul_f32_e32 v22, v150, v22
	v_mul_f32_e32 v23, v150, v23
	v_mul_f32_e32 v24, v150, v24
	v_mul_f32_e32 v25, v150, v25
	v_cvt_pk_bf16_f32 v182, v18, v19
	v_cvt_pk_bf16_f32 v183, v20, v21
	v_cvt_pk_bf16_f32 v184, v22, v23
	v_cvt_pk_bf16_f32 v185, v24, v25
	ds_write_b128 v164, v[182:185]
	v_mul_f32_e32 v26, v150, v26
	v_mul_f32_e32 v27, v150, v27
	v_mul_f32_e32 v28, v150, v28
	v_mul_f32_e32 v29, v150, v29
	v_mul_f32_e32 v30, v150, v30
	v_mul_f32_e32 v31, v150, v31
	v_mul_f32_e32 v32, v150, v32
	v_mul_f32_e32 v33, v150, v33
	v_cvt_pk_bf16_f32 v182, v26, v27
	v_cvt_pk_bf16_f32 v183, v28, v29
	v_cvt_pk_bf16_f32 v184, v30, v31
	v_cvt_pk_bf16_f32 v185, v32, v33
	v_xor_b32_e32 v167, 64, v164
	ds_write_b128 v167, v[182:185]
	v_mov_b32_e32 v18, 0
	v_mov_b32_e32 v22, 0
	v_mov_b32_e32 v26, 0
	v_mov_b32_e32 v30, 0
	v_mov_b32_e32 v19, 0
	v_mov_b32_e32 v23, 0
	v_mov_b32_e32 v27, 0
	v_mov_b32_e32 v31, 0
	v_mov_b32_e32 v20, 0
	v_mov_b32_e32 v24, 0
	v_mov_b32_e32 v28, 0
	v_mov_b32_e32 v32, 0
	v_mov_b32_e32 v21, 0
	v_mov_b32_e32 v25, 0
	v_mov_b32_e32 v29, 0
	v_mov_b32_e32 v33, 0
	ds_read_b128 v[182:185], v165 offset:0
	v_cmp_lt_i32_e32 vcc, -1, v151
	v_lshlrev_b32_e32 v148, 13, v151
	v_mov_b32_e32 v149, 0
	v_lshl_add_u64 v[148:149], v[148:149], 0, v[86:87]
	v_cndmask_b32_e32 v148, v168, v148, vcc
	v_cndmask_b32_e32 v149, v169, v149, vcc
	s_waitcnt lgkmcnt(0)
	global_store_dwordx4 v[148:149], v[182:185], off
	ds_read_b128 v[182:185], v165 offset:8192
	v_cmp_lt_i32_e32 vcc, -1, v166
	v_lshlrev_b32_e32 v148, 13, v166
	v_mov_b32_e32 v149, 0
	v_lshl_add_u64 v[148:149], v[148:149], 0, v[86:87]
	v_cndmask_b32_e32 v148, v168, v148, vcc
	v_cndmask_b32_e32 v149, v169, v149, vcc
	s_waitcnt lgkmcnt(0)
	global_store_dwordx4 v[148:149], v[182:185], off
	ds_read_b32 v150, v82 offset:1024
	ds_read_b32 v151, v83 offset:1024
	ds_read_b32 v166, v83 offset:1152
	s_waitcnt lgkmcnt(2)
	v_mul_f32_e32 v2, v150, v2
	v_mul_f32_e32 v3, v150, v3
	v_mul_f32_e32 v4, v150, v4
	v_mul_f32_e32 v5, v150, v5
	v_mul_f32_e32 v6, v150, v6
	v_mul_f32_e32 v7, v150, v7
	v_mul_f32_e32 v8, v150, v8
	v_mul_f32_e32 v9, v150, v9
	v_cvt_pk_bf16_f32 v182, v2, v3
	v_cvt_pk_bf16_f32 v183, v4, v5
	v_cvt_pk_bf16_f32 v184, v6, v7
	v_cvt_pk_bf16_f32 v185, v8, v9
	ds_write_b128 v164, v[182:185]
	v_mul_f32_e32 v10, v150, v10
	v_mul_f32_e32 v11, v150, v11
	v_mul_f32_e32 v12, v150, v12
	v_mul_f32_e32 v13, v150, v13
	v_mul_f32_e32 v14, v150, v14
	v_mul_f32_e32 v15, v150, v15
	v_mul_f32_e32 v16, v150, v16
	v_mul_f32_e32 v17, v150, v17
	v_cvt_pk_bf16_f32 v182, v10, v11
	v_cvt_pk_bf16_f32 v183, v12, v13
	v_cvt_pk_bf16_f32 v184, v14, v15
	v_cvt_pk_bf16_f32 v185, v16, v17
	v_xor_b32_e32 v167, 64, v164
	ds_write_b128 v167, v[182:185]
	v_mov_b32_e32 v2, 0
	v_mov_b32_e32 v6, 0
	v_mov_b32_e32 v10, 0
	v_mov_b32_e32 v14, 0
	v_mov_b32_e32 v3, 0
	v_mov_b32_e32 v7, 0
	v_mov_b32_e32 v11, 0
	v_mov_b32_e32 v15, 0
	v_mov_b32_e32 v4, 0
	v_mov_b32_e32 v8, 0
	v_mov_b32_e32 v12, 0
	v_mov_b32_e32 v16, 0
	v_mov_b32_e32 v5, 0
	v_mov_b32_e32 v9, 0
	v_mov_b32_e32 v13, 0
	v_mov_b32_e32 v17, 0
	ds_read_b128 v[182:185], v165 offset:0
	v_cmp_lt_i32_e32 vcc, -1, v151
	v_lshlrev_b32_e32 v148, 13, v151
	v_mov_b32_e32 v149, 0
	v_lshl_add_u64 v[148:149], v[148:149], 0, v[86:87]
	v_cndmask_b32_e32 v148, v168, v148, vcc
	v_cndmask_b32_e32 v149, v169, v149, vcc
	s_waitcnt lgkmcnt(0)
	global_store_dwordx4 v[148:149], v[182:185], off
	ds_read_b128 v[182:185], v165 offset:8192
	v_cmp_lt_i32_e32 vcc, -1, v166
	v_lshlrev_b32_e32 v148, 13, v166
	v_mov_b32_e32 v149, 0
	v_lshl_add_u64 v[148:149], v[148:149], 0, v[86:87]
	v_cndmask_b32_e32 v148, v168, v148, vcc
	v_cndmask_b32_e32 v149, v169, v149, vcc
	s_waitcnt lgkmcnt(0)
	global_store_dwordx4 v[148:149], v[182:185], off
	v_add_co_u32_e32 v86, vcc, 0x800, v86
	s_nop 1
	v_addc_co_u32_e32 v87, vcc, 0, v87, vcc
	s_waitcnt lgkmcnt(0)
; #define MD_GLDS_A(buf, tau) do { _Pragma("unroll") for (int i = 0; i < 5; ++i) if (amask & (1u << i)) \
;         __builtin_amdgcn_global_load_lds((const unsigned*)((const char*)HIDp + aoff[i] + (size_t)((tau) & 7) * 128), (PG8_LAS unsigned*)(MD_SA(buf) + wid * 1024 + i * 8192), 16, 0, 0); } while (0)
; #define MD_B_ISSUE(sb, tau) do { const char* kb_ = Bb + (size_t)((tau) >> 3) * 512 + (size_t)((tau) & 7) * (64 * (size_t)RB); _Pragma("unroll") for (int j = 0; j < 8; ++j) { const char* p_ = kb_ + (size_t)j * RB; \
;         asm volatile("global_load_dwordx2 %0, %1, off" : "=&v"(sb[j]) : "v"(p_) : "memory"); } } while (0)
; #define MD_B_WAIT(sb, N) asm volatile("s_waitcnt vmcnt(%8)" : "+v"(sb[0]), "+v"(sb[1]), "+v"(sb[2]), "+v"(sb[3]), "+v"(sb[4]), "+v"(sb[5]), "+v"(sb[6]), "+v"(sb[7]) : "n"(N) : "memory")
; __device__ __forceinline__ void moe_down_stream(PG8_LAS unsigned char* lds, int e, int cb0, int slot0, int nv, const bf16_t* HIDp, const float* Wd, bf16_t* Y, const float* slot_w, const int* slot_dst) {
;     ...
;     f32x4 acc[DNM][4];
; #pragma unroll
;     for (int m = 0; m < DNM; ++m)
; #pragma unroll
;         for (int n = 0; n < 4; ++n) acc[m][n] = (f32x4){0.f, 0.f, 0.f, 0.f};
;     f32x2 s0[8], s1[8];
;     MD_GLDS_A(0, 0); MD_B_ISSUE(s0, 0); MD_B_ISSUE(s1, 1);
;     MD_B_WAIT(s0, 8); MD_B_WRITE(s0, 0); __builtin_amdgcn_sched_barrier(0); MD_B_ISSUE(s0, 2);
;     asm volatile("s_waitcnt vmcnt(16)" ::: "memory");
;     asm volatile("s_waitcnt lgkmcnt(0)" ::: "memory"); __builtin_amdgcn_s_barrier(); asm volatile("" ::: "memory");
; #pragma unroll 1
;     for (int t = 0; t < NT; t += 2) {
;         if (t + 2 < NT) MD_B_WAIT(s1, 8); else MD_B_WAIT(s1, 0);
;         MD_B_WRITE(s1, 1); __builtin_amdgcn_sched_barrier(0); MD_GLDS_A(1, t + 1); __builtin_amdgcn_sched_barrier(0);
;         if (t + 3 < NT) MD_B_ISSUE(s1, t + 3);
;         MD_COMPUTE(0);
;         MD_END(t + 3 >= NT);
;         if (t + 2 < NT) { MD_B_WAIT(s0, 8); MD_B_WRITE(s0, 0); __builtin_amdgcn_sched_barrier(0); MD_GLDS_A(0, t + 2); __builtin_amdgcn_sched_barrier(0); }
;         if (t + 4 < NT) MD_B_ISSUE(s0, t + 4);
;         MD_COMPUTE(1);
;         MD_END(t + 4 >= NT);
.Lmd_noepi_Y:
	s_add_i32 s49, s48, s74
	s_add_i32 s52, s52, 1
	s_and_b32 s54, s52, 7
	s_cmp_eq_u32 s54, 0
	s_cselect_b32 s54, s53, s32
	s_cselect_b32 s55, -1, 0
	s_add_u32 s30, s30, s54
	s_addc_u32 s31, s31, s55
	s_mov_b32 m0, s49
	s_nop 0
	global_load_lds_dwordx4 v88, s[30:31]
	s_add_i32 m0, s49, 0x2000
	s_nop 0
	global_load_lds_dwordx4 v90, s[30:31]
	s_add_i32 m0, s49, 0x4000
	s_nop 0
	global_load_lds_dwordx4 v92, s[30:31]
	s_add_i32 m0, s49, 0x6000
	s_nop 0
	global_load_lds_dwordx4 v94, s[30:31]
	s_add_i32 m0, s49, 0x8000
	s_nop 0
	global_load_lds_dwordx4 v96, s[30:31]
	v_cvt_pk_bf16_f32 v172, v114, v116
	v_cvt_pk_bf16_f32 v173, v118, v120
	v_cvt_pk_bf16_f32 v174, v122, v124
	v_cvt_pk_bf16_f32 v175, v126, v128
	v_cvt_pk_bf16_f32 v176, v115, v117
	v_cvt_pk_bf16_f32 v177, v119, v121
	v_cvt_pk_bf16_f32 v178, v123, v125
	v_cvt_pk_bf16_f32 v179, v127, v129
	ds_write_b128 v95, v[172:175] offset:19456
	ds_write_b128 v95, v[176:179] offset:19584
	v_add_u32_e32 v91, s46, v135
	v_add_u32_e32 v93, s46, v137
	ds_read_b128 v[238:241], v139 offset:0
	ds_read_b128 v[242:245], v139 offset:2048
	ds_read_b128 v[246:249], v139 offset:4096
	ds_read_b128 v[250:253], v139 offset:6144
	ds_read_b128 v[218:221], v91 offset:0
	ds_read_b128 v[222:225], v91 offset:2048
	ds_read_b128 v[226:229], v91 offset:4096
	ds_read_b128 v[230:233], v91 offset:6144
	ds_read_b128 v[234:237], v91 offset:8192
	s_waitcnt lgkmcnt(0)
	v_mfma_f32_16x16x32_bf16 v[78:81], v[238:241], v[218:221], v[78:81]
	v_mfma_f32_16x16x32_bf16 v[74:77], v[242:245], v[218:221], v[74:77]
	v_mfma_f32_16x16x32_bf16 v[70:73], v[246:249], v[218:221], v[70:73]
	v_mfma_f32_16x16x32_bf16 v[66:69], v[250:253], v[218:221], v[66:69]
	ds_read_b128 v[218:221], v93 offset:0
	ds_read_b128 v[142:145], v141 offset:0
	s_add_i32 s51, s51, 1
	s_and_b32 s54, s51, 7
	s_cmp_eq_u32 s54, 0
	s_cselect_b32 s44, s34, s35
	s_cselect_b32 s45, -1, 0
	v_lshl_add_u64 v[132:133], v[132:133], 0, s[44:45]
	global_load_dwordx2 v[114:115], v[132:133], off
	v_lshl_add_u64 v[180:181], v[132:133], 0, s[24:25]
	global_load_dwordx2 v[116:117], v[180:181], off
	v_mfma_f32_16x16x32_bf16 v[62:65], v[238:241], v[222:225], v[62:65]
	v_mfma_f32_16x16x32_bf16 v[58:61], v[242:245], v[222:225], v[58:61]
	v_mfma_f32_16x16x32_bf16 v[54:57], v[246:249], v[222:225], v[54:57]
	v_mfma_f32_16x16x32_bf16 v[50:53], v[250:253], v[222:225], v[50:53]
	ds_read_b128 v[222:225], v93 offset:2048
	ds_read_b128 v[146:149], v141 offset:2048
	v_lshl_add_u64 v[180:181], v[132:133], 0, s[26:27]
	global_load_dwordx2 v[118:119], v[180:181], off
	v_lshl_add_u64 v[180:181], v[132:133], 0, s[28:29]
	global_load_dwordx2 v[120:121], v[180:181], off
	v_mfma_f32_16x16x32_bf16 v[46:49], v[238:241], v[226:229], v[46:49]
	v_mfma_f32_16x16x32_bf16 v[42:45], v[242:245], v[226:229], v[42:45]
	v_mfma_f32_16x16x32_bf16 v[38:41], v[246:249], v[226:229], v[38:41]
	v_mfma_f32_16x16x32_bf16 v[34:37], v[250:253], v[226:229], v[34:37]
	ds_read_b128 v[226:229], v93 offset:4096
	ds_read_b128 v[156:159], v141 offset:4096
	v_lshl_add_u64 v[180:181], v[132:133], 0, s[36:37]
	global_load_dwordx2 v[122:123], v[180:181], off
	v_lshl_add_u64 v[180:181], v[132:133], 0, s[38:39]
	global_load_dwordx2 v[124:125], v[180:181], off
	v_mfma_f32_16x16x32_bf16 v[18:21], v[238:241], v[230:233], v[18:21]
	v_mfma_f32_16x16x32_bf16 v[22:25], v[242:245], v[230:233], v[22:25]
	v_mfma_f32_16x16x32_bf16 v[26:29], v[246:249], v[230:233], v[26:29]
	v_mfma_f32_16x16x32_bf16 v[30:33], v[250:253], v[230:233], v[30:33]
	ds_read_b128 v[230:233], v93 offset:6144
	ds_read_b128 v[160:163], v141 offset:6144
	v_lshl_add_u64 v[180:181], v[132:133], 0, s[40:41]
	global_load_dwordx2 v[126:127], v[180:181], off
	v_lshl_add_u64 v[180:181], v[132:133], 0, s[42:43]
	global_load_dwordx2 v[128:129], v[180:181], off
	v_mfma_f32_16x16x32_bf16 v[2:5], v[238:241], v[234:237], v[2:5]
	v_mfma_f32_16x16x32_bf16 v[6:9], v[242:245], v[234:237], v[6:9]
	v_mfma_f32_16x16x32_bf16 v[10:13], v[246:249], v[234:237], v[10:13]
	v_mfma_f32_16x16x32_bf16 v[14:17], v[250:253], v[234:237], v[14:17]
	ds_read_b128 v[234:237], v93 offset:8192
	s_waitcnt vmcnt(21)
	s_waitcnt lgkmcnt(0)
	s_barrier
	s_mov_b32 s49, s46
	s_mov_b32 s46, s47
	s_mov_b32 s47, s48
	s_mov_b32 s48, s49
	s_add_i32 s50, s50, 1
	s_add_i32 s49, s48, s74
	s_add_i32 s52, s52, 1
	s_and_b32 s54, s52, 7
	s_cmp_eq_u32 s54, 0
	s_cselect_b32 s54, s53, s32
	s_cselect_b32 s55, -1, 0
	s_add_u32 s30, s30, s54
	s_addc_u32 s31, s31, s55
	v_mfma_f32_16x16x32_bf16 v[78:81], v[142:145], v[218:221], v[78:81]
	v_mfma_f32_16x16x32_bf16 v[74:77], v[146:149], v[218:221], v[74:77]
	v_mfma_f32_16x16x32_bf16 v[70:73], v[156:159], v[218:221], v[70:73]
	v_mfma_f32_16x16x32_bf16 v[66:69], v[160:163], v[218:221], v[66:69]
	s_mov_b32 m0, s49
	s_nop 0
	global_load_lds_dwordx4 v88, s[30:31]
	v_mfma_f32_16x16x32_bf16 v[62:65], v[142:145], v[222:225], v[62:65]
	v_mfma_f32_16x16x32_bf16 v[58:61], v[146:149], v[222:225], v[58:61]
	v_mfma_f32_16x16x32_bf16 v[54:57], v[156:159], v[222:225], v[54:57]
	v_mfma_f32_16x16x32_bf16 v[50:53], v[160:163], v[222:225], v[50:53]
	s_add_i32 m0, s49, 0x2000
	s_nop 0
	global_load_lds_dwordx4 v90, s[30:31]
	v_mfma_f32_16x16x32_bf16 v[46:49], v[142:145], v[226:229], v[46:49]
	v_mfma_f32_16x16x32_bf16 v[42:45], v[146:149], v[226:229], v[42:45]
	v_mfma_f32_16x16x32_bf16 v[38:41], v[156:159], v[226:229], v[38:41]
	v_mfma_f32_16x16x32_bf16 v[34:37], v[160:163], v[226:229], v[34:37]
	s_add_i32 m0, s49, 0x4000
	s_nop 0
	global_load_lds_dwordx4 v92, s[30:31]
	v_mfma_f32_16x16x32_bf16 v[18:21], v[142:145], v[230:233], v[18:21]
	v_mfma_f32_16x16x32_bf16 v[22:25], v[146:149], v[230:233], v[22:25]
	v_mfma_f32_16x16x32_bf16 v[26:29], v[156:159], v[230:233], v[26:29]
	v_mfma_f32_16x16x32_bf16 v[30:33], v[160:163], v[230:233], v[30:33]
	s_add_i32 m0, s49, 0x6000
	s_nop 0
	global_load_lds_dwordx4 v94, s[30:31]
	v_mfma_f32_16x16x32_bf16 v[2:5], v[142:145], v[234:237], v[2:5]
	v_mfma_f32_16x16x32_bf16 v[6:9], v[146:149], v[234:237], v[6:9]
	v_mfma_f32_16x16x32_bf16 v[10:13], v[156:159], v[234:237], v[10:13]
	v_mfma_f32_16x16x32_bf16 v[14:17], v[160:163], v[234:237], v[14:17]
	s_add_i32 m0, s49, 0x8000
	s_nop 0
	global_load_lds_dwordx4 v96, s[30:31]
	v_cvt_pk_bf16_f32 v172, v186, v188
	v_cvt_pk_bf16_f32 v173, v190, v192
	v_cvt_pk_bf16_f32 v174, v194, v196
	v_cvt_pk_bf16_f32 v175, v198, v200
	v_cvt_pk_bf16_f32 v176, v187, v189
	v_cvt_pk_bf16_f32 v177, v191, v193
	v_cvt_pk_bf16_f32 v178, v195, v197
	v_cvt_pk_bf16_f32 v179, v199, v201
	ds_write_b128 v95, v[172:175] offset:0
	ds_write_b128 v95, v[176:179] offset:128
	v_add_u32_e32 v91, s46, v135
	v_add_u32_e32 v93, s46, v137
	ds_read_b128 v[238:241], v139 offset:19456
	ds_read_b128 v[242:245], v139 offset:21504
	ds_read_b128 v[246:249], v139 offset:23552
	ds_read_b128 v[250:253], v139 offset:25600
	ds_read_b128 v[218:221], v91 offset:0
	ds_read_b128 v[222:225], v91 offset:2048
	ds_read_b128 v[226:229], v91 offset:4096
	ds_read_b128 v[230:233], v91 offset:6144
	ds_read_b128 v[234:237], v91 offset:8192
	s_waitcnt lgkmcnt(0)
; #define MD_GLDS_A(buf, tau) do { _Pragma("unroll") for (int i = 0; i < 5; ++i) if (amask & (1u << i)) \
;         __builtin_amdgcn_global_load_lds((const unsigned*)((const char*)HIDp + aoff[i] + (size_t)((tau) & 7) * 128), (PG8_LAS unsigned*)(MD_SA(buf) + wid * 1024 + i * 8192), 16, 0, 0); } while (0)
; #define MD_B_ISSUE(sb, tau) do { const char* kb_ = Bb + (size_t)((tau) >> 3) * 512 + (size_t)((tau) & 7) * (64 * (size_t)RB); _Pragma("unroll") for (int j = 0; j < 8; ++j) { const char* p_ = kb_ + (size_t)j * RB; \
;         asm volatile("global_load_dwordx2 %0, %1, off" : "=&v"(sb[j]) : "v"(p_) : "memory"); } } while (0)
; #define MD_B_WAIT(sb, N) asm volatile("s_waitcnt vmcnt(%8)" : "+v"(sb[0]), "+v"(sb[1]), "+v"(sb[2]), "+v"(sb[3]), "+v"(sb[4]), "+v"(sb[5]), "+v"(sb[6]), "+v"(sb[7]) : "n"(N) : "memory")
; __device__ __forceinline__ void moe_down_stream(PG8_LAS unsigned char* lds, int e, int cb0, int slot0, int nv, const bf16_t* HIDp, const float* Wd, bf16_t* Y, const float* slot_w, const int* slot_dst) {
;     ...
;     f32x4 acc[DNM][4];
; #pragma unroll
;     for (int m = 0; m < DNM; ++m)
; #pragma unroll
;         for (int n = 0; n < 4; ++n) acc[m][n] = (f32x4){0.f, 0.f, 0.f, 0.f};
;     f32x2 s0[8], s1[8];
;     MD_GLDS_A(0, 0); MD_B_ISSUE(s0, 0); MD_B_ISSUE(s1, 1);
;     MD_B_WAIT(s0, 8); MD_B_WRITE(s0, 0); __builtin_amdgcn_sched_barrier(0); MD_B_ISSUE(s0, 2);
;     asm volatile("s_waitcnt vmcnt(16)" ::: "memory");
;     asm volatile("s_waitcnt lgkmcnt(0)" ::: "memory"); __builtin_amdgcn_s_barrier(); asm volatile("" ::: "memory");
; #pragma unroll 1
;     for (int t = 0; t < NT; t += 2) {
;         if (t + 2 < NT) MD_B_WAIT(s1, 8); else MD_B_WAIT(s1, 0);
;         MD_B_WRITE(s1, 1); __builtin_amdgcn_sched_barrier(0); MD_GLDS_A(1, t + 1); __builtin_amdgcn_sched_barrier(0);
;         if (t + 3 < NT) MD_B_ISSUE(s1, t + 3);
;         MD_COMPUTE(0);
;         MD_END(t + 3 >= NT);
;         if (t + 2 < NT) { MD_B_WAIT(s0, 8); MD_B_WRITE(s0, 0); __builtin_amdgcn_sched_barrier(0); MD_GLDS_A(0, t + 2); __builtin_amdgcn_sched_barrier(0); }
;         if (t + 4 < NT) MD_B_ISSUE(s0, t + 4);
;         MD_COMPUTE(1);
;         MD_END(t + 4 >= NT);
	v_mfma_f32_16x16x32_bf16 v[78:81], v[238:241], v[218:221], v[78:81]
	v_mfma_f32_16x16x32_bf16 v[74:77], v[242:245], v[218:221], v[74:77]
	v_mfma_f32_16x16x32_bf16 v[70:73], v[246:249], v[218:221], v[70:73]
	v_mfma_f32_16x16x32_bf16 v[66:69], v[250:253], v[218:221], v[66:69]
	ds_read_b128 v[218:221], v93 offset:0
	ds_read_b128 v[142:145], v141 offset:19456
	s_add_i32 s51, s51, 1
	s_and_b32 s54, s51, 7
	s_cmp_eq_u32 s54, 0
	s_cselect_b32 s44, s34, s35
	s_cselect_b32 s45, -1, 0
	v_lshl_add_u64 v[132:133], v[132:133], 0, s[44:45]
	global_load_dwordx2 v[186:187], v[132:133], off
	v_lshl_add_u64 v[180:181], v[132:133], 0, s[24:25]
	global_load_dwordx2 v[188:189], v[180:181], off
	v_mfma_f32_16x16x32_bf16 v[62:65], v[238:241], v[222:225], v[62:65]
	v_mfma_f32_16x16x32_bf16 v[58:61], v[242:245], v[222:225], v[58:61]
	v_mfma_f32_16x16x32_bf16 v[54:57], v[246:249], v[222:225], v[54:57]
	v_mfma_f32_16x16x32_bf16 v[50:53], v[250:253], v[222:225], v[50:53]
	ds_read_b128 v[222:225], v93 offset:2048
	ds_read_b128 v[146:149], v141 offset:21504
	v_lshl_add_u64 v[180:181], v[132:133], 0, s[26:27]
	global_load_dwordx2 v[190:191], v[180:181], off
	v_lshl_add_u64 v[180:181], v[132:133], 0, s[28:29]
	global_load_dwordx2 v[192:193], v[180:181], off
	v_mfma_f32_16x16x32_bf16 v[46:49], v[238:241], v[226:229], v[46:49]
	v_mfma_f32_16x16x32_bf16 v[42:45], v[242:245], v[226:229], v[42:45]
	v_mfma_f32_16x16x32_bf16 v[38:41], v[246:249], v[226:229], v[38:41]
	v_mfma_f32_16x16x32_bf16 v[34:37], v[250:253], v[226:229], v[34:37]
	ds_read_b128 v[226:229], v93 offset:4096
	ds_read_b128 v[156:159], v141 offset:23552
	v_lshl_add_u64 v[180:181], v[132:133], 0, s[36:37]
	global_load_dwordx2 v[194:195], v[180:181], off
	v_lshl_add_u64 v[180:181], v[132:133], 0, s[38:39]
	global_load_dwordx2 v[196:197], v[180:181], off
	v_mfma_f32_16x16x32_bf16 v[18:21], v[238:241], v[230:233], v[18:21]
	v_mfma_f32_16x16x32_bf16 v[22:25], v[242:245], v[230:233], v[22:25]
	v_mfma_f32_16x16x32_bf16 v[26:29], v[246:249], v[230:233], v[26:29]
	v_mfma_f32_16x16x32_bf16 v[30:33], v[250:253], v[230:233], v[30:33]
	ds_read_b128 v[230:233], v93 offset:6144
	ds_read_b128 v[160:163], v141 offset:25600
	v_lshl_add_u64 v[180:181], v[132:133], 0, s[40:41]
	global_load_dwordx2 v[198:199], v[180:181], off
	v_lshl_add_u64 v[180:181], v[132:133], 0, s[42:43]
	global_load_dwordx2 v[200:201], v[180:181], off
	v_mfma_f32_16x16x32_bf16 v[2:5], v[238:241], v[234:237], v[2:5]
	v_mfma_f32_16x16x32_bf16 v[6:9], v[242:245], v[234:237], v[6:9]
	v_mfma_f32_16x16x32_bf16 v[10:13], v[246:249], v[234:237], v[10:13]
	v_mfma_f32_16x16x32_bf16 v[14:17], v[250:253], v[234:237], v[14:17]
	ds_read_b128 v[234:237], v93 offset:8192
	s_waitcnt vmcnt(21)
	s_waitcnt lgkmcnt(0)
	s_barrier
	s_mov_b32 s49, s46
	s_mov_b32 s46, s47
	s_mov_b32 s47, s48
	s_mov_b32 s48, s49
	s_add_i32 s50, s50, 1
	s_add_i32 s49, s48, s74
	s_add_i32 s52, s52, 1
	s_and_b32 s54, s52, 7
	s_cmp_eq_u32 s54, 0
	s_cselect_b32 s54, s53, s32
	s_cselect_b32 s55, -1, 0
	s_add_u32 s30, s30, s54
	s_addc_u32 s31, s31, s55
	v_mfma_f32_16x16x32_bf16 v[78:81], v[142:145], v[218:221], v[78:81]
	v_mfma_f32_16x16x32_bf16 v[74:77], v[146:149], v[218:221], v[74:77]
	v_mfma_f32_16x16x32_bf16 v[70:73], v[156:159], v[218:221], v[70:73]
	v_mfma_f32_16x16x32_bf16 v[66:69], v[160:163], v[218:221], v[66:69]
	s_mov_b32 m0, s49
	s_nop 0
	global_load_lds_dwordx4 v88, s[30:31]
	v_mfma_f32_16x16x32_bf16 v[62:65], v[142:145], v[222:225], v[62:65]
	v_mfma_f32_16x16x32_bf16 v[58:61], v[146:149], v[222:225], v[58:61]
	v_mfma_f32_16x16x32_bf16 v[54:57], v[156:159], v[222:225], v[54:57]
	v_mfma_f32_16x16x32_bf16 v[50:53], v[160:163], v[222:225], v[50:53]
	s_add_i32 m0, s49, 0x2000
	s_nop 0
	global_load_lds_dwordx4 v90, s[30:31]
	v_mfma_f32_16x16x32_bf16 v[46:49], v[142:145], v[226:229], v[46:49]
	v_mfma_f32_16x16x32_bf16 v[42:45], v[146:149], v[226:229], v[42:45]
	v_mfma_f32_16x16x32_bf16 v[38:41], v[156:159], v[226:229], v[38:41]
	v_mfma_f32_16x16x32_bf16 v[34:37], v[160:163], v[226:229], v[34:37]
	s_add_i32 m0, s49, 0x4000
	s_nop 0
	global_load_lds_dwordx4 v92, s[30:31]
	v_mfma_f32_16x16x32_bf16 v[18:21], v[142:145], v[230:233], v[18:21]
	v_mfma_f32_16x16x32_bf16 v[22:25], v[146:149], v[230:233], v[22:25]
	v_mfma_f32_16x16x32_bf16 v[26:29], v[156:159], v[230:233], v[26:29]
	v_mfma_f32_16x16x32_bf16 v[30:33], v[160:163], v[230:233], v[30:33]
	s_add_i32 m0, s49, 0x6000
	s_nop 0
	global_load_lds_dwordx4 v94, s[30:31]
	v_mfma_f32_16x16x32_bf16 v[2:5], v[142:145], v[234:237], v[2:5]
	v_mfma_f32_16x16x32_bf16 v[6:9], v[146:149], v[234:237], v[6:9]
	v_mfma_f32_16x16x32_bf16 v[10:13], v[156:159], v[234:237], v[10:13]
	v_mfma_f32_16x16x32_bf16 v[14:17], v[160:163], v[234:237], v[14:17]
	s_add_i32 m0, s49, 0x8000
	s_nop 0
	global_load_lds_dwordx4 v96, s[30:31]
	v_cvt_pk_bf16_f32 v172, v202, v204
	v_cvt_pk_bf16_f32 v173, v206, v208
	v_cvt_pk_bf16_f32 v174, v210, v212
	v_cvt_pk_bf16_f32 v175, v214, v216
	v_cvt_pk_bf16_f32 v176, v203, v205
	v_cvt_pk_bf16_f32 v177, v207, v209
	v_cvt_pk_bf16_f32 v178, v211, v213
	v_cvt_pk_bf16_f32 v179, v215, v217
	ds_write_b128 v95, v[172:175] offset:19456
	ds_write_b128 v95, v[176:179] offset:19584
	v_add_u32_e32 v91, s46, v135
	v_add_u32_e32 v93, s46, v137
	ds_read_b128 v[238:241], v139 offset:0
	ds_read_b128 v[242:245], v139 offset:2048
	ds_read_b128 v[246:249], v139 offset:4096
	ds_read_b128 v[250:253], v139 offset:6144
	ds_read_b128 v[218:221], v91 offset:0
	ds_read_b128 v[222:225], v91 offset:2048
	ds_read_b128 v[226:229], v91 offset:4096
	ds_read_b128 v[230:233], v91 offset:6144
	ds_read_b128 v[234:237], v91 offset:8192
	s_waitcnt lgkmcnt(0)
; #define MD_GLDS_A(buf, tau) do { _Pragma("unroll") for (int i = 0; i < 5; ++i) if (amask & (1u << i)) \
;         __builtin_amdgcn_global_load_lds((const unsigned*)((const char*)HIDp + aoff[i] + (size_t)((tau) & 7) * 128), (PG8_LAS unsigned*)(MD_SA(buf) + wid * 1024 + i * 8192), 16, 0, 0); } while (0)
; #define MD_B_ISSUE(sb, tau) do { const char* kb_ = Bb + (size_t)((tau) >> 3) * 512 + (size_t)((tau) & 7) * (64 * (size_t)RB); _Pragma("unroll") for (int j = 0; j < 8; ++j) { const char* p_ = kb_ + (size_t)j * RB; \
;         asm volatile("global_load_dwordx2 %0, %1, off" : "=&v"(sb[j]) : "v"(p_) : "memory"); } } while (0)
; #define MD_B_WAIT(sb, N) asm volatile("s_waitcnt vmcnt(%8)" : "+v"(sb[0]), "+v"(sb[1]), "+v"(sb[2]), "+v"(sb[3]), "+v"(sb[4]), "+v"(sb[5]), "+v"(sb[6]), "+v"(sb[7]) : "n"(N) : "memory")
; __device__ __forceinline__ void moe_down_stream(PG8_LAS unsigned char* lds, int e, int cb0, int slot0, int nv, const bf16_t* HIDp, const float* Wd, bf16_t* Y, const float* slot_w, const int* slot_dst) {
;     ...
;     f32x4 acc[DNM][4];
; #pragma unroll
;     for (int m = 0; m < DNM; ++m)
; #pragma unroll
;         for (int n = 0; n < 4; ++n) acc[m][n] = (f32x4){0.f, 0.f, 0.f, 0.f};
;     f32x2 s0[8], s1[8];
;     MD_GLDS_A(0, 0); MD_B_ISSUE(s0, 0); MD_B_ISSUE(s1, 1);
;     MD_B_WAIT(s0, 8); MD_B_WRITE(s0, 0); __builtin_amdgcn_sched_barrier(0); MD_B_ISSUE(s0, 2);
;     asm volatile("s_waitcnt vmcnt(16)" ::: "memory");
;     asm volatile("s_waitcnt lgkmcnt(0)" ::: "memory"); __builtin_amdgcn_s_barrier(); asm volatile("" ::: "memory");
; #pragma unroll 1
;     for (int t = 0; t < NT; t += 2) {
;         if (t + 2 < NT) MD_B_WAIT(s1, 8); else MD_B_WAIT(s1, 0);
;         MD_B_WRITE(s1, 1); __builtin_amdgcn_sched_barrier(0); MD_GLDS_A(1, t + 1); __builtin_amdgcn_sched_barrier(0);
;         if (t + 3 < NT) MD_B_ISSUE(s1, t + 3);
;         MD_COMPUTE(0);
;         MD_END(t + 3 >= NT);
;         if (t + 2 < NT) { MD_B_WAIT(s0, 8); MD_B_WRITE(s0, 0); __builtin_amdgcn_sched_barrier(0); MD_GLDS_A(0, t + 2); __builtin_amdgcn_sched_barrier(0); }
;         if (t + 4 < NT) MD_B_ISSUE(s0, t + 4);
;         MD_COMPUTE(1);
;         MD_END(t + 4 >= NT);
	v_mfma_f32_16x16x32_bf16 v[78:81], v[238:241], v[218:221], v[78:81]
	v_mfma_f32_16x16x32_bf16 v[74:77], v[242:245], v[218:221], v[74:77]
	v_mfma_f32_16x16x32_bf16 v[70:73], v[246:249], v[218:221], v[70:73]
	v_mfma_f32_16x16x32_bf16 v[66:69], v[250:253], v[218:221], v[66:69]
	ds_read_b128 v[218:221], v93 offset:0
	ds_read_b128 v[142:145], v141 offset:0
	s_add_i32 s51, s51, 1
	s_and_b32 s54, s51, 7
	s_cmp_eq_u32 s54, 0
	s_cselect_b32 s44, s34, s35
	s_cselect_b32 s45, -1, 0
	v_lshl_add_u64 v[132:133], v[132:133], 0, s[44:45]
	global_load_dwordx2 v[202:203], v[132:133], off
	v_lshl_add_u64 v[180:181], v[132:133], 0, s[24:25]
	global_load_dwordx2 v[204:205], v[180:181], off
	v_mfma_f32_16x16x32_bf16 v[62:65], v[238:241], v[222:225], v[62:65]
	v_mfma_f32_16x16x32_bf16 v[58:61], v[242:245], v[222:225], v[58:61]
	v_mfma_f32_16x16x32_bf16 v[54:57], v[246:249], v[222:225], v[54:57]
	v_mfma_f32_16x16x32_bf16 v[50:53], v[250:253], v[222:225], v[50:53]
	ds_read_b128 v[222:225], v93 offset:2048
	ds_read_b128 v[146:149], v141 offset:2048
	v_lshl_add_u64 v[180:181], v[132:133], 0, s[26:27]
	global_load_dwordx2 v[206:207], v[180:181], off
	v_lshl_add_u64 v[180:181], v[132:133], 0, s[28:29]
	global_load_dwordx2 v[208:209], v[180:181], off
	v_mfma_f32_16x16x32_bf16 v[46:49], v[238:241], v[226:229], v[46:49]
	v_mfma_f32_16x16x32_bf16 v[42:45], v[242:245], v[226:229], v[42:45]
	v_mfma_f32_16x16x32_bf16 v[38:41], v[246:249], v[226:229], v[38:41]
	v_mfma_f32_16x16x32_bf16 v[34:37], v[250:253], v[226:229], v[34:37]
	ds_read_b128 v[226:229], v93 offset:4096
	ds_read_b128 v[156:159], v141 offset:4096
	v_lshl_add_u64 v[180:181], v[132:133], 0, s[36:37]
	global_load_dwordx2 v[210:211], v[180:181], off
	v_lshl_add_u64 v[180:181], v[132:133], 0, s[38:39]
	global_load_dwordx2 v[212:213], v[180:181], off
	v_mfma_f32_16x16x32_bf16 v[18:21], v[238:241], v[230:233], v[18:21]
	v_mfma_f32_16x16x32_bf16 v[22:25], v[242:245], v[230:233], v[22:25]
	v_mfma_f32_16x16x32_bf16 v[26:29], v[246:249], v[230:233], v[26:29]
	v_mfma_f32_16x16x32_bf16 v[30:33], v[250:253], v[230:233], v[30:33]
	ds_read_b128 v[230:233], v93 offset:6144
	ds_read_b128 v[160:163], v141 offset:6144
	v_lshl_add_u64 v[180:181], v[132:133], 0, s[40:41]
	global_load_dwordx2 v[214:215], v[180:181], off
	v_lshl_add_u64 v[180:181], v[132:133], 0, s[42:43]
	global_load_dwordx2 v[216:217], v[180:181], off
	v_mfma_f32_16x16x32_bf16 v[2:5], v[238:241], v[234:237], v[2:5]
	v_mfma_f32_16x16x32_bf16 v[6:9], v[242:245], v[234:237], v[6:9]
	v_mfma_f32_16x16x32_bf16 v[10:13], v[246:249], v[234:237], v[10:13]
	v_mfma_f32_16x16x32_bf16 v[14:17], v[250:253], v[234:237], v[14:17]
	ds_read_b128 v[234:237], v93 offset:8192
	s_waitcnt vmcnt(21)
	s_waitcnt lgkmcnt(0)
	s_barrier
	s_mov_b32 s49, s46
	s_mov_b32 s46, s47
	s_mov_b32 s47, s48
	s_mov_b32 s48, s49
	s_add_i32 s50, s50, 1
	s_add_i32 s49, s48, s74
	s_add_i32 s52, s52, 1
	s_and_b32 s54, s52, 7
	s_cmp_eq_u32 s54, 0
	s_cselect_b32 s54, s53, s32
	s_cselect_b32 s55, -1, 0
	s_add_u32 s30, s30, s54
	s_addc_u32 s31, s31, s55
	v_mfma_f32_16x16x32_bf16 v[78:81], v[142:145], v[218:221], v[78:81]
	v_mfma_f32_16x16x32_bf16 v[74:77], v[146:149], v[218:221], v[74:77]
	v_mfma_f32_16x16x32_bf16 v[70:73], v[156:159], v[218:221], v[70:73]
	v_mfma_f32_16x16x32_bf16 v[66:69], v[160:163], v[218:221], v[66:69]
	s_mov_b32 m0, s49
	s_nop 0
	global_load_lds_dwordx4 v88, s[30:31]
	v_mfma_f32_16x16x32_bf16 v[62:65], v[142:145], v[222:225], v[62:65]
	v_mfma_f32_16x16x32_bf16 v[58:61], v[146:149], v[222:225], v[58:61]
	v_mfma_f32_16x16x32_bf16 v[54:57], v[156:159], v[222:225], v[54:57]
	v_mfma_f32_16x16x32_bf16 v[50:53], v[160:163], v[222:225], v[50:53]
	s_add_i32 m0, s49, 0x2000
	s_nop 0
	global_load_lds_dwordx4 v90, s[30:31]
	v_mfma_f32_16x16x32_bf16 v[46:49], v[142:145], v[226:229], v[46:49]
	v_mfma_f32_16x16x32_bf16 v[42:45], v[146:149], v[226:229], v[42:45]
	v_mfma_f32_16x16x32_bf16 v[38:41], v[156:159], v[226:229], v[38:41]
	v_mfma_f32_16x16x32_bf16 v[34:37], v[160:163], v[226:229], v[34:37]
	s_add_i32 m0, s49, 0x4000
	s_nop 0
	global_load_lds_dwordx4 v92, s[30:31]
	v_mfma_f32_16x16x32_bf16 v[18:21], v[142:145], v[230:233], v[18:21]
	v_mfma_f32_16x16x32_bf16 v[22:25], v[146:149], v[230:233], v[22:25]
	v_mfma_f32_16x16x32_bf16 v[26:29], v[156:159], v[230:233], v[26:29]
	v_mfma_f32_16x16x32_bf16 v[30:33], v[160:163], v[230:233], v[30:33]
	s_add_i32 m0, s49, 0x6000
	s_nop 0
	global_load_lds_dwordx4 v94, s[30:31]
	v_mfma_f32_16x16x32_bf16 v[2:5], v[142:145], v[234:237], v[2:5]
	v_mfma_f32_16x16x32_bf16 v[6:9], v[146:149], v[234:237], v[6:9]
	v_mfma_f32_16x16x32_bf16 v[10:13], v[156:159], v[234:237], v[10:13]
	v_mfma_f32_16x16x32_bf16 v[14:17], v[160:163], v[234:237], v[14:17]
	s_add_i32 m0, s49, 0x8000
	s_nop 0
	global_load_lds_dwordx4 v96, s[30:31]
	v_cvt_pk_bf16_f32 v172, v98, v100
	v_cvt_pk_bf16_f32 v173, v102, v104
	v_cvt_pk_bf16_f32 v174, v106, v108
	v_cvt_pk_bf16_f32 v175, v110, v112
	v_cvt_pk_bf16_f32 v176, v99, v101
	v_cvt_pk_bf16_f32 v177, v103, v105
	v_cvt_pk_bf16_f32 v178, v107, v109
	v_cvt_pk_bf16_f32 v179, v111, v113
	ds_write_b128 v95, v[172:175] offset:0
	ds_write_b128 v95, v[176:179] offset:128
	v_add_u32_e32 v91, s46, v135
	v_add_u32_e32 v93, s46, v137
	ds_read_b128 v[238:241], v139 offset:19456
	ds_read_b128 v[242:245], v139 offset:21504
	ds_read_b128 v[246:249], v139 offset:23552
	ds_read_b128 v[250:253], v139 offset:25600
	ds_read_b128 v[218:221], v91 offset:0
	ds_read_b128 v[222:225], v91 offset:2048
	ds_read_b128 v[226:229], v91 offset:4096
	ds_read_b128 v[230:233], v91 offset:6144
	ds_read_b128 v[234:237], v91 offset:8192
	s_waitcnt lgkmcnt(0)
; #define PG8_LAS __attribute__((address_space(3)))
; __device__ __forceinline__ unsigned cvtpk(float lo, float hi) { f32x2 v = {lo, hi}; bf16x2_t b = __builtin_convertvector(v, bf16x2_t); return __builtin_bit_cast(unsigned, b); }
; #define MD_GLDS_A(buf, tau) do { _Pragma("unroll") for (int i = 0; i < 5; ++i) if (amask & (1u << i)) \
;         __builtin_amdgcn_global_load_lds((const unsigned*)((const char*)HIDp + aoff[i] + (size_t)((tau) & 7) * 128), (PG8_LAS unsigned*)(MD_SA(buf) + wid * 1024 + i * 8192), 16, 0, 0); } while (0)
; __device__ __forceinline__ void moe_down_stream(PG8_LAS unsigned char* lds, int e, int cb0, int slot0, int nv, const bf16_t* HIDp, const float* Wd, bf16_t* Y, const float* slot_w, const int* slot_dst) {
;     ...
;     for (int t = 0; t < NT; t += 2) {
;         if (t + 2 < NT) MD_B_WAIT(s1, 8); else MD_B_WAIT(s1, 0);
;         MD_B_WRITE(s1, 1); __builtin_amdgcn_sched_barrier(0); MD_GLDS_A(1, t + 1); __builtin_amdgcn_sched_barrier(0);
;         if (t + 3 < NT) MD_B_ISSUE(s1, t + 3);
;         MD_COMPUTE(0);
;         MD_END(t + 3 >= NT);
;         if (t + 2 < NT) { MD_B_WAIT(s0, 8); MD_B_WRITE(s0, 0); __builtin_amdgcn_sched_barrier(0); MD_GLDS_A(0, t + 2); __builtin_amdgcn_sched_barrier(0); }
;         if (t + 4 < NT) MD_B_ISSUE(s0, t + 4);
;         MD_COMPUTE(1);
;         MD_END(t + 4 >= NT);
;         if (((t + 1) & 7) == 7) {
;             const int cb = cb0 + ((t + 1) >> 3);
; #pragma unroll
;             for (int m = 0; m < DNM; ++m) {
;                 const float w_ = lw[4 * (16 * m + fr) + wr];
; #pragma unroll
;                 for (int p = 0; p < 2; ++p) { const f32x4 v0 = acc[m][2 * p] * w_, v1 = acc[m][2 * p + 1] * w_; u32x4 w; w.x = cvtpk(v0[0], v0[1]); w.y = cvtpk(v0[2], v0[3]); w.z = cvtpk(v1[0], v1[1]); w.w = cvtpk(v1[2], v1[3]);
;                     *(PG8_LAS u32x4*)(stg + fr * 128 + (((4 * p + fq) ^ (fr & 7)) * 16)) = w; }
; #pragma unroll
;                 for (int hh = 0; hh < 2; ++hh) { const int r = (lane >> 3) + 8 * hh, cc = lane & 7; const u32x4 d = *(const PG8_LAS u32x4*)(stg + r * 128 + ((cc ^ (r & 7)) * 16)); const int dst_ = ldst[4 * (16 * m + r) + wr];
;                     if (dst_ >= 0) *(u32x4*)(Y + (size_t)dst_ * D + 128 * cb + 64 * wc + 8 * cc) = d; }
; #pragma unroll
;                 for (int n = 0; n < 4; ++n) acc[m][n] = (f32x4){0.f, 0.f, 0.f, 0.f}; } }
	v_mfma_f32_16x16x32_bf16 v[78:81], v[238:241], v[218:221], v[78:81]
	v_mfma_f32_16x16x32_bf16 v[74:77], v[242:245], v[218:221], v[74:77]
	v_mfma_f32_16x16x32_bf16 v[70:73], v[246:249], v[218:221], v[70:73]
	v_mfma_f32_16x16x32_bf16 v[66:69], v[250:253], v[218:221], v[66:69]
	ds_read_b128 v[218:221], v93 offset:0
	ds_read_b128 v[142:145], v141 offset:19456
	s_add_i32 s51, s51, 1
	s_and_b32 s54, s51, 7
	s_cmp_eq_u32 s54, 0
	s_cselect_b32 s44, s34, s35
	s_cselect_b32 s45, -1, 0
	v_lshl_add_u64 v[132:133], v[132:133], 0, s[44:45]
	global_load_dwordx2 v[98:99], v[132:133], off
	v_lshl_add_u64 v[180:181], v[132:133], 0, s[24:25]
	global_load_dwordx2 v[100:101], v[180:181], off
	v_mfma_f32_16x16x32_bf16 v[62:65], v[238:241], v[222:225], v[62:65]
	v_mfma_f32_16x16x32_bf16 v[58:61], v[242:245], v[222:225], v[58:61]
	v_mfma_f32_16x16x32_bf16 v[54:57], v[246:249], v[222:225], v[54:57]
	v_mfma_f32_16x16x32_bf16 v[50:53], v[250:253], v[222:225], v[50:53]
	ds_read_b128 v[222:225], v93 offset:2048
	ds_read_b128 v[146:149], v141 offset:21504
	v_lshl_add_u64 v[180:181], v[132:133], 0, s[26:27]
	global_load_dwordx2 v[102:103], v[180:181], off
	v_lshl_add_u64 v[180:181], v[132:133], 0, s[28:29]
	global_load_dwordx2 v[104:105], v[180:181], off
	v_mfma_f32_16x16x32_bf16 v[46:49], v[238:241], v[226:229], v[46:49]
	v_mfma_f32_16x16x32_bf16 v[42:45], v[242:245], v[226:229], v[42:45]
	v_mfma_f32_16x16x32_bf16 v[38:41], v[246:249], v[226:229], v[38:41]
	v_mfma_f32_16x16x32_bf16 v[34:37], v[250:253], v[226:229], v[34:37]
	ds_read_b128 v[226:229], v93 offset:4096
	ds_read_b128 v[156:159], v141 offset:23552
	v_lshl_add_u64 v[180:181], v[132:133], 0, s[36:37]
	global_load_dwordx2 v[106:107], v[180:181], off
	v_lshl_add_u64 v[180:181], v[132:133], 0, s[38:39]
	global_load_dwordx2 v[108:109], v[180:181], off
	v_mfma_f32_16x16x32_bf16 v[18:21], v[238:241], v[230:233], v[18:21]
	v_mfma_f32_16x16x32_bf16 v[22:25], v[242:245], v[230:233], v[22:25]
	v_mfma_f32_16x16x32_bf16 v[26:29], v[246:249], v[230:233], v[26:29]
	v_mfma_f32_16x16x32_bf16 v[30:33], v[250:253], v[230:233], v[30:33]
	ds_read_b128 v[230:233], v93 offset:6144
	ds_read_b128 v[160:163], v141 offset:25600
	v_lshl_add_u64 v[180:181], v[132:133], 0, s[40:41]
	global_load_dwordx2 v[110:111], v[180:181], off
	v_lshl_add_u64 v[180:181], v[132:133], 0, s[42:43]
	global_load_dwordx2 v[112:113], v[180:181], off
	v_mfma_f32_16x16x32_bf16 v[2:5], v[238:241], v[234:237], v[2:5]
	v_mfma_f32_16x16x32_bf16 v[6:9], v[242:245], v[234:237], v[6:9]
	v_mfma_f32_16x16x32_bf16 v[10:13], v[246:249], v[234:237], v[10:13]
	v_mfma_f32_16x16x32_bf16 v[14:17], v[250:253], v[234:237], v[14:17]
	ds_read_b128 v[234:237], v93 offset:8192
	s_waitcnt vmcnt(21)
	s_waitcnt lgkmcnt(0)
	s_barrier
	s_mov_b32 s49, s46
	s_mov_b32 s46, s47
	s_mov_b32 s47, s48
	s_mov_b32 s48, s49
	s_add_i32 s50, s50, 1
	s_sub_u32 s56, s56, 1
	s_cmp_lg_u32 s56, 0
	s_cbranch_scc1 .Lmd_loop_Y
	v_mfma_f32_16x16x32_bf16 v[78:81], v[142:145], v[218:221], v[78:81]
	v_mfma_f32_16x16x32_bf16 v[74:77], v[146:149], v[218:221], v[74:77]
	v_mfma_f32_16x16x32_bf16 v[70:73], v[156:159], v[218:221], v[70:73]
	v_mfma_f32_16x16x32_bf16 v[66:69], v[160:163], v[218:221], v[66:69]
	v_mfma_f32_16x16x32_bf16 v[62:65], v[142:145], v[222:225], v[62:65]
	v_mfma_f32_16x16x32_bf16 v[58:61], v[146:149], v[222:225], v[58:61]
	v_mfma_f32_16x16x32_bf16 v[54:57], v[156:159], v[222:225], v[54:57]
	v_mfma_f32_16x16x32_bf16 v[50:53], v[160:163], v[222:225], v[50:53]
	v_mfma_f32_16x16x32_bf16 v[46:49], v[142:145], v[226:229], v[46:49]
	v_mfma_f32_16x16x32_bf16 v[42:45], v[146:149], v[226:229], v[42:45]
	v_mfma_f32_16x16x32_bf16 v[38:41], v[156:159], v[226:229], v[38:41]
	v_mfma_f32_16x16x32_bf16 v[34:37], v[160:163], v[226:229], v[34:37]
	v_mfma_f32_16x16x32_bf16 v[18:21], v[142:145], v[230:233], v[18:21]
	v_mfma_f32_16x16x32_bf16 v[22:25], v[146:149], v[230:233], v[22:25]
	v_mfma_f32_16x16x32_bf16 v[26:29], v[156:159], v[230:233], v[26:29]
	v_mfma_f32_16x16x32_bf16 v[30:33], v[160:163], v[230:233], v[30:33]
	v_mfma_f32_16x16x32_bf16 v[2:5], v[142:145], v[234:237], v[2:5]
	v_mfma_f32_16x16x32_bf16 v[6:9], v[146:149], v[234:237], v[6:9]
	v_mfma_f32_16x16x32_bf16 v[10:13], v[156:159], v[234:237], v[10:13]
	v_mfma_f32_16x16x32_bf16 v[14:17], v[160:163], v[234:237], v[14:17]
	s_add_i32 s54, s48, s74
	v_add_u32_e32 v164, s54, v84
	v_add_u32_e32 v165, s54, v85
	ds_read_b32 v150, v82 offset:0
	ds_read_b32 v151, v83 offset:0
	ds_read_b32 v166, v83 offset:128
	s_waitcnt lgkmcnt(2)
	v_mul_f32_e32 v78, v150, v78
	v_mul_f32_e32 v79, v150, v79
	v_mul_f32_e32 v80, v150, v80
	v_mul_f32_e32 v81, v150, v81
	v_mul_f32_e32 v74, v150, v74
	v_mul_f32_e32 v75, v150, v75
	v_mul_f32_e32 v76, v150, v76
	v_mul_f32_e32 v77, v150, v77
	v_cvt_pk_bf16_f32 v182, v78, v79
	v_cvt_pk_bf16_f32 v183, v80, v81
	v_cvt_pk_bf16_f32 v184, v74, v75
	v_cvt_pk_bf16_f32 v185, v76, v77
	ds_write_b128 v164, v[182:185]
	v_mul_f32_e32 v70, v150, v70
	v_mul_f32_e32 v71, v150, v71
	v_mul_f32_e32 v72, v150, v72
	v_mul_f32_e32 v73, v150, v73
	v_mul_f32_e32 v66, v150, v66
	v_mul_f32_e32 v67, v150, v67
	v_mul_f32_e32 v68, v150, v68
	v_mul_f32_e32 v69, v150, v69
	v_cvt_pk_bf16_f32 v182, v70, v71
	v_cvt_pk_bf16_f32 v183, v72, v73
	v_cvt_pk_bf16_f32 v184, v66, v67
	v_cvt_pk_bf16_f32 v185, v68, v69
	v_xor_b32_e32 v167, 64, v164
	ds_write_b128 v167, v[182:185]
	v_mov_b32_e32 v78, 0
	v_mov_b32_e32 v74, 0
	v_mov_b32_e32 v70, 0
	v_mov_b32_e32 v66, 0
	v_mov_b32_e32 v79, 0
	v_mov_b32_e32 v75, 0
	v_mov_b32_e32 v71, 0
	v_mov_b32_e32 v67, 0
	v_mov_b32_e32 v80, 0
	v_mov_b32_e32 v76, 0
	v_mov_b32_e32 v72, 0
	v_mov_b32_e32 v68, 0
	v_mov_b32_e32 v81, 0
	v_mov_b32_e32 v77, 0
	v_mov_b32_e32 v73, 0
	v_mov_b32_e32 v69, 0
	ds_read_b128 v[182:185], v165 offset:0
	v_cmp_lt_i32_e32 vcc, -1, v151
	v_lshlrev_b32_e32 v148, 13, v151
	v_mov_b32_e32 v149, 0
	v_lshl_add_u64 v[148:149], v[148:149], 0, v[86:87]
	v_cndmask_b32_e32 v148, v168, v148, vcc
	v_cndmask_b32_e32 v149, v169, v149, vcc
	s_waitcnt lgkmcnt(0)
; #define PG8_LAS __attribute__((address_space(3)))
; __device__ __forceinline__ unsigned cvtpk(float lo, float hi) { f32x2 v = {lo, hi}; bf16x2_t b = __builtin_convertvector(v, bf16x2_t); return __builtin_bit_cast(unsigned, b); }
; __device__ __forceinline__ void moe_down_stream(PG8_LAS unsigned char* lds, int e, int cb0, int slot0, int nv, const bf16_t* HIDp, const float* Wd, bf16_t* Y, const float* slot_w, const int* slot_dst) {
;     ...
;         if (((t + 1) & 7) == 7) {
;             const int cb = cb0 + ((t + 1) >> 3);
; #pragma unroll
;             for (int m = 0; m < DNM; ++m) {
;                 const float w_ = lw[4 * (16 * m + fr) + wr];
; #pragma unroll
;                 for (int p = 0; p < 2; ++p) { const f32x4 v0 = acc[m][2 * p] * w_, v1 = acc[m][2 * p + 1] * w_; u32x4 w; w.x = cvtpk(v0[0], v0[1]); w.y = cvtpk(v0[2], v0[3]); w.z = cvtpk(v1[0], v1[1]); w.w = cvtpk(v1[2], v1[3]);
;                     *(PG8_LAS u32x4*)(stg + fr * 128 + (((4 * p + fq) ^ (fr & 7)) * 16)) = w; }
; #pragma unroll
;                 for (int hh = 0; hh < 2; ++hh) { const int r = (lane >> 3) + 8 * hh, cc = lane & 7; const u32x4 d = *(const PG8_LAS u32x4*)(stg + r * 128 + ((cc ^ (r & 7)) * 16)); const int dst_ = ldst[4 * (16 * m + r) + wr];
;                     if (dst_ >= 0) *(u32x4*)(Y + (size_t)dst_ * D + 128 * cb + 64 * wc + 8 * cc) = d; }
; #pragma unroll
;                 for (int n = 0; n < 4; ++n) acc[m][n] = (f32x4){0.f, 0.f, 0.f, 0.f}; } }
	global_store_dwordx4 v[148:149], v[182:185], off
	ds_read_b128 v[182:185], v165 offset:8192
	v_cmp_lt_i32_e32 vcc, -1, v166
	v_lshlrev_b32_e32 v148, 13, v166
	v_mov_b32_e32 v149, 0
	v_lshl_add_u64 v[148:149], v[148:149], 0, v[86:87]
	v_cndmask_b32_e32 v148, v168, v148, vcc
	v_cndmask_b32_e32 v149, v169, v149, vcc
	s_waitcnt lgkmcnt(0)
	global_store_dwordx4 v[148:149], v[182:185], off
	ds_read_b32 v150, v82 offset:256
	ds_read_b32 v151, v83 offset:256
	ds_read_b32 v166, v83 offset:384
	s_waitcnt lgkmcnt(2)
	v_mul_f32_e32 v62, v150, v62
	v_mul_f32_e32 v63, v150, v63
	v_mul_f32_e32 v64, v150, v64
	v_mul_f32_e32 v65, v150, v65
	v_mul_f32_e32 v58, v150, v58
	v_mul_f32_e32 v59, v150, v59
	v_mul_f32_e32 v60, v150, v60
	v_mul_f32_e32 v61, v150, v61
	v_cvt_pk_bf16_f32 v182, v62, v63
	v_cvt_pk_bf16_f32 v183, v64, v65
	v_cvt_pk_bf16_f32 v184, v58, v59
	v_cvt_pk_bf16_f32 v185, v60, v61
	ds_write_b128 v164, v[182:185]
	v_mul_f32_e32 v54, v150, v54
	v_mul_f32_e32 v55, v150, v55
	v_mul_f32_e32 v56, v150, v56
	v_mul_f32_e32 v57, v150, v57
	v_mul_f32_e32 v50, v150, v50
	v_mul_f32_e32 v51, v150, v51
	v_mul_f32_e32 v52, v150, v52
	v_mul_f32_e32 v53, v150, v53
	v_cvt_pk_bf16_f32 v182, v54, v55
	v_cvt_pk_bf16_f32 v183, v56, v57
	v_cvt_pk_bf16_f32 v184, v50, v51
	v_cvt_pk_bf16_f32 v185, v52, v53
	v_xor_b32_e32 v167, 64, v164
	ds_write_b128 v167, v[182:185]
	v_mov_b32_e32 v62, 0
	v_mov_b32_e32 v58, 0
	v_mov_b32_e32 v54, 0
	v_mov_b32_e32 v50, 0
	v_mov_b32_e32 v63, 0
	v_mov_b32_e32 v59, 0
	v_mov_b32_e32 v55, 0
	v_mov_b32_e32 v51, 0
	v_mov_b32_e32 v64, 0
	v_mov_b32_e32 v60, 0
	v_mov_b32_e32 v56, 0
	v_mov_b32_e32 v52, 0
	v_mov_b32_e32 v65, 0
	v_mov_b32_e32 v61, 0
	v_mov_b32_e32 v57, 0
	v_mov_b32_e32 v53, 0
	ds_read_b128 v[182:185], v165 offset:0
	v_cmp_lt_i32_e32 vcc, -1, v151
	v_lshlrev_b32_e32 v148, 13, v151
	v_mov_b32_e32 v149, 0
	v_lshl_add_u64 v[148:149], v[148:149], 0, v[86:87]
	v_cndmask_b32_e32 v148, v168, v148, vcc
	v_cndmask_b32_e32 v149, v169, v149, vcc
	s_waitcnt lgkmcnt(0)
	global_store_dwordx4 v[148:149], v[182:185], off
	ds_read_b128 v[182:185], v165 offset:8192
	v_cmp_lt_i32_e32 vcc, -1, v166
	v_lshlrev_b32_e32 v148, 13, v166
	v_mov_b32_e32 v149, 0
	v_lshl_add_u64 v[148:149], v[148:149], 0, v[86:87]
	v_cndmask_b32_e32 v148, v168, v148, vcc
	v_cndmask_b32_e32 v149, v169, v149, vcc
	s_waitcnt lgkmcnt(0)
	global_store_dwordx4 v[148:149], v[182:185], off
	ds_read_b32 v150, v82 offset:512
	ds_read_b32 v151, v83 offset:512
	ds_read_b32 v166, v83 offset:640
	s_waitcnt lgkmcnt(2)
	v_mul_f32_e32 v46, v150, v46
	v_mul_f32_e32 v47, v150, v47
	v_mul_f32_e32 v48, v150, v48
	v_mul_f32_e32 v49, v150, v49
	v_mul_f32_e32 v42, v150, v42
	v_mul_f32_e32 v43, v150, v43
	v_mul_f32_e32 v44, v150, v44
	v_mul_f32_e32 v45, v150, v45
	v_cvt_pk_bf16_f32 v182, v46, v47
	v_cvt_pk_bf16_f32 v183, v48, v49
	v_cvt_pk_bf16_f32 v184, v42, v43
	v_cvt_pk_bf16_f32 v185, v44, v45
	ds_write_b128 v164, v[182:185]
	v_mul_f32_e32 v38, v150, v38
	v_mul_f32_e32 v39, v150, v39
	v_mul_f32_e32 v40, v150, v40
	v_mul_f32_e32 v41, v150, v41
	v_mul_f32_e32 v34, v150, v34
	v_mul_f32_e32 v35, v150, v35
	v_mul_f32_e32 v36, v150, v36
	v_mul_f32_e32 v37, v150, v37
	v_cvt_pk_bf16_f32 v182, v38, v39
	v_cvt_pk_bf16_f32 v183, v40, v41
	v_cvt_pk_bf16_f32 v184, v34, v35
	v_cvt_pk_bf16_f32 v185, v36, v37
	v_xor_b32_e32 v167, 64, v164
	ds_write_b128 v167, v[182:185]
	v_mov_b32_e32 v46, 0
	v_mov_b32_e32 v42, 0
	v_mov_b32_e32 v38, 0
	v_mov_b32_e32 v34, 0
	v_mov_b32_e32 v47, 0
	v_mov_b32_e32 v43, 0
	v_mov_b32_e32 v39, 0
	v_mov_b32_e32 v35, 0
	v_mov_b32_e32 v48, 0
	v_mov_b32_e32 v44, 0
	v_mov_b32_e32 v40, 0
	v_mov_b32_e32 v36, 0
	v_mov_b32_e32 v49, 0
	v_mov_b32_e32 v45, 0
	v_mov_b32_e32 v41, 0
	v_mov_b32_e32 v37, 0
	ds_read_b128 v[182:185], v165 offset:0
	v_cmp_lt_i32_e32 vcc, -1, v151
	v_lshlrev_b32_e32 v148, 13, v151
	v_mov_b32_e32 v149, 0
	v_lshl_add_u64 v[148:149], v[148:149], 0, v[86:87]
	v_cndmask_b32_e32 v148, v168, v148, vcc
	v_cndmask_b32_e32 v149, v169, v149, vcc
	s_waitcnt lgkmcnt(0)
	global_store_dwordx4 v[148:149], v[182:185], off
	ds_read_b128 v[182:185], v165 offset:8192
	v_cmp_lt_i32_e32 vcc, -1, v166
	v_lshlrev_b32_e32 v148, 13, v166
	v_mov_b32_e32 v149, 0
	v_lshl_add_u64 v[148:149], v[148:149], 0, v[86:87]
	v_cndmask_b32_e32 v148, v168, v148, vcc
	v_cndmask_b32_e32 v149, v169, v149, vcc
	s_waitcnt lgkmcnt(0)
	global_store_dwordx4 v[148:149], v[182:185], off
	ds_read_b32 v150, v82 offset:768
	ds_read_b32 v151, v83 offset:768
	ds_read_b32 v166, v83 offset:896
	s_waitcnt lgkmcnt(2)
	v_mul_f32_e32 v18, v150, v18
	v_mul_f32_e32 v19, v150, v19
	v_mul_f32_e32 v20, v150, v20
	v_mul_f32_e32 v21, v150, v21
	v_mul_f32_e32 v22, v150, v22
	v_mul_f32_e32 v23, v150, v23
	v_mul_f32_e32 v24, v150, v24
	v_mul_f32_e32 v25, v150, v25
	v_cvt_pk_bf16_f32 v182, v18, v19
	v_cvt_pk_bf16_f32 v183, v20, v21
	v_cvt_pk_bf16_f32 v184, v22, v23
	v_cvt_pk_bf16_f32 v185, v24, v25
	ds_write_b128 v164, v[182:185]
	v_mul_f32_e32 v26, v150, v26
	v_mul_f32_e32 v27, v150, v27
	v_mul_f32_e32 v28, v150, v28
	v_mul_f32_e32 v29, v150, v29
	v_mul_f32_e32 v30, v150, v30
	v_mul_f32_e32 v31, v150, v31
	v_mul_f32_e32 v32, v150, v32
	v_mul_f32_e32 v33, v150, v33
	v_cvt_pk_bf16_f32 v182, v26, v27
	v_cvt_pk_bf16_f32 v183, v28, v29
	v_cvt_pk_bf16_f32 v184, v30, v31
	v_cvt_pk_bf16_f32 v185, v32, v33
	v_xor_b32_e32 v167, 64, v164
	ds_write_b128 v167, v[182:185]
	v_mov_b32_e32 v18, 0
	v_mov_b32_e32 v22, 0
	v_mov_b32_e32 v26, 0
	v_mov_b32_e32 v30, 0
	v_mov_b32_e32 v19, 0
	v_mov_b32_e32 v23, 0
	v_mov_b32_e32 v27, 0
	v_mov_b32_e32 v31, 0
	v_mov_b32_e32 v20, 0
	v_mov_b32_e32 v24, 0
	v_mov_b32_e32 v28, 0
	v_mov_b32_e32 v32, 0
	v_mov_b32_e32 v21, 0
	v_mov_b32_e32 v25, 0
	v_mov_b32_e32 v29, 0
	v_mov_b32_e32 v33, 0
	ds_read_b128 v[182:185], v165 offset:0
	v_cmp_lt_i32_e32 vcc, -1, v151
	v_lshlrev_b32_e32 v148, 13, v151
	v_mov_b32_e32 v149, 0
	v_lshl_add_u64 v[148:149], v[148:149], 0, v[86:87]
	v_cndmask_b32_e32 v148, v168, v148, vcc
	v_cndmask_b32_e32 v149, v169, v149, vcc
	s_waitcnt lgkmcnt(0)
; __device__ __forceinline__ void moe_down_stream(PG8_LAS unsigned char* lds, int e, int cb0, int slot0, int nv, const bf16_t* HIDp, const float* Wd, bf16_t* Y, const float* slot_w, const int* slot_dst) {
;     ...
;     f32x4 acc[DNM][4];
; #pragma unroll
;     for (int m = 0; m < DNM; ++m)
; #pragma unroll
;         for (int n = 0; n < 4; ++n) acc[m][n] = (f32x4){0.f, 0.f, 0.f, 0.f};
;     f32x2 s0[8], s1[8];
;     MD_GLDS_A(0, 0); MD_B_ISSUE(s0, 0); MD_B_ISSUE(s1, 1);
;     MD_B_WAIT(s0, 8); MD_B_WRITE(s0, 0); __builtin_amdgcn_sched_barrier(0); MD_B_ISSUE(s0, 2);
;     asm volatile("s_waitcnt vmcnt(16)" ::: "memory");
;     asm volatile("s_waitcnt lgkmcnt(0)" ::: "memory"); __builtin_amdgcn_s_barrier(); asm volatile("" ::: "memory");
; #pragma unroll 1
;     for (int t = 0; t < NT; t += 2) {
;         if (t + 2 < NT) MD_B_WAIT(s1, 8); else MD_B_WAIT(s1, 0);
;         MD_B_WRITE(s1, 1); __builtin_amdgcn_sched_barrier(0); MD_GLDS_A(1, t + 1); __builtin_amdgcn_sched_barrier(0);
;         if (t + 3 < NT) MD_B_ISSUE(s1, t + 3);
;         MD_COMPUTE(0);
;         MD_END(t + 3 >= NT);
;         if (t + 2 < NT) { MD_B_WAIT(s0, 8); MD_B_WRITE(s0, 0); __builtin_amdgcn_sched_barrier(0); MD_GLDS_A(0, t + 2); __builtin_amdgcn_sched_barrier(0); }
;         if (t + 4 < NT) MD_B_ISSUE(s0, t + 4);
;         MD_COMPUTE(1);
;         MD_END(t + 4 >= NT);
;         if (((t + 1) & 7) == 7) {
;             const int cb = cb0 + ((t + 1) >> 3);
; #pragma unroll
;             for (int m = 0; m < DNM; ++m) {
;                 const float w_ = lw[4 * (16 * m + fr) + wr];
; #pragma unroll
;                 for (int p = 0; p < 2; ++p) { const f32x4 v0 = acc[m][2 * p] * w_, v1 = acc[m][2 * p + 1] * w_; u32x4 w; w.x = cvtpk(v0[0], v0[1]); w.y = cvtpk(v0[2], v0[3]); w.z = cvtpk(v1[0], v1[1]); w.w = cvtpk(v1[2], v1[3]);
;                     *(PG8_LAS u32x4*)(stg + fr * 128 + (((4 * p + fq) ^ (fr & 7)) * 16)) = w; }
; #pragma unroll
;                 for (int hh = 0; hh < 2; ++hh) { const int r = (lane >> 3) + 8 * hh, cc = lane & 7; const u32x4 d = *(const PG8_LAS u32x4*)(stg + r * 128 + ((cc ^ (r & 7)) * 16)); const int dst_ = ldst[4 * (16 * m + r) + wr];
;                     if (dst_ >= 0) *(u32x4*)(Y + (size_t)dst_ * D + 128 * cb + 64 * wc + 8 * cc) = d; }
; #pragma unroll
;                 for (int n = 0; n < 4; ++n) acc[m][n] = (f32x4){0.f, 0.f, 0.f, 0.f}; } }
	global_store_dwordx4 v[148:149], v[182:185], off
	ds_read_b128 v[182:185], v165 offset:8192
	v_cmp_lt_i32_e32 vcc, -1, v166
	v_lshlrev_b32_e32 v148, 13, v166
	v_mov_b32_e32 v149, 0
	v_lshl_add_u64 v[148:149], v[148:149], 0, v[86:87]
	v_cndmask_b32_e32 v148, v168, v148, vcc
	v_cndmask_b32_e32 v149, v169, v149, vcc
	s_waitcnt lgkmcnt(0)
	global_store_dwordx4 v[148:149], v[182:185], off
	ds_read_b32 v150, v82 offset:1024
	ds_read_b32 v151, v83 offset:1024
	ds_read_b32 v166, v83 offset:1152
	s_waitcnt lgkmcnt(2)
	v_mul_f32_e32 v2, v150, v2
	v_mul_f32_e32 v3, v150, v3
	v_mul_f32_e32 v4, v150, v4
	v_mul_f32_e32 v5, v150, v5
	v_mul_f32_e32 v6, v150, v6
	v_mul_f32_e32 v7, v150, v7
	v_mul_f32_e32 v8, v150, v8
	v_mul_f32_e32 v9, v150, v9
	v_cvt_pk_bf16_f32 v182, v2, v3
	v_cvt_pk_bf16_f32 v183, v4, v5
	v_cvt_pk_bf16_f32 v184, v6, v7
	v_cvt_pk_bf16_f32 v185, v8, v9
	ds_write_b128 v164, v[182:185]
	v_mul_f32_e32 v10, v150, v10
	v_mul_f32_e32 v11, v150, v11
	v_mul_f32_e32 v12, v150, v12
	v_mul_f32_e32 v13, v150, v13
	v_mul_f32_e32 v14, v150, v14
	v_mul_f32_e32 v15, v150, v15
	v_mul_f32_e32 v16, v150, v16
	v_mul_f32_e32 v17, v150, v17
	v_cvt_pk_bf16_f32 v182, v10, v11
	v_cvt_pk_bf16_f32 v183, v12, v13
	v_cvt_pk_bf16_f32 v184, v14, v15
	v_cvt_pk_bf16_f32 v185, v16, v17
	v_xor_b32_e32 v167, 64, v164
	ds_write_b128 v167, v[182:185]
	v_mov_b32_e32 v2, 0
	v_mov_b32_e32 v6, 0
	v_mov_b32_e32 v10, 0
	v_mov_b32_e32 v14, 0
	v_mov_b32_e32 v3, 0
	v_mov_b32_e32 v7, 0
	v_mov_b32_e32 v11, 0
	v_mov_b32_e32 v15, 0
	v_mov_b32_e32 v4, 0
	v_mov_b32_e32 v8, 0
	v_mov_b32_e32 v12, 0
	v_mov_b32_e32 v16, 0
	v_mov_b32_e32 v5, 0
	v_mov_b32_e32 v9, 0
	v_mov_b32_e32 v13, 0
	v_mov_b32_e32 v17, 0
	ds_read_b128 v[182:185], v165 offset:0
	v_cmp_lt_i32_e32 vcc, -1, v151
	v_lshlrev_b32_e32 v148, 13, v151
	v_mov_b32_e32 v149, 0
	v_lshl_add_u64 v[148:149], v[148:149], 0, v[86:87]
	v_cndmask_b32_e32 v148, v168, v148, vcc
	v_cndmask_b32_e32 v149, v169, v149, vcc
	s_waitcnt lgkmcnt(0)
	global_store_dwordx4 v[148:149], v[182:185], off
	ds_read_b128 v[182:185], v165 offset:8192
	v_cmp_lt_i32_e32 vcc, -1, v166
	v_lshlrev_b32_e32 v148, 13, v166
	v_mov_b32_e32 v149, 0
	v_lshl_add_u64 v[148:149], v[148:149], 0, v[86:87]
	v_cndmask_b32_e32 v148, v168, v148, vcc
	v_cndmask_b32_e32 v149, v169, v149, vcc
	s_waitcnt lgkmcnt(0)
	global_store_dwordx4 v[148:149], v[182:185], off
	v_add_co_u32_e32 v86, vcc, 0x800, v86
	s_nop 1
	v_addc_co_u32_e32 v87, vcc, 0, v87, vcc
	s_waitcnt lgkmcnt(0)
	s_add_i32 s49, s48, s74
	s_add_i32 s52, s52, 1
	s_and_b32 s54, s52, 7
	s_cmp_eq_u32 s54, 0
	s_cselect_b32 s54, s53, s32
	s_cselect_b32 s55, -1, 0
	s_add_u32 s30, s30, s54
	s_addc_u32 s31, s31, s55
	s_mov_b32 m0, s49
	s_nop 0
	global_load_lds_dwordx4 v88, s[30:31]
	s_add_i32 m0, s49, 0x2000
	s_nop 0
	global_load_lds_dwordx4 v90, s[30:31]
	s_add_i32 m0, s49, 0x4000
	s_nop 0
	global_load_lds_dwordx4 v92, s[30:31]
	s_add_i32 m0, s49, 0x6000
	s_nop 0
	global_load_lds_dwordx4 v94, s[30:31]
	s_add_i32 m0, s49, 0x8000
	s_nop 0
	global_load_lds_dwordx4 v96, s[30:31]
	v_cvt_pk_bf16_f32 v172, v114, v116
	v_cvt_pk_bf16_f32 v173, v118, v120
	v_cvt_pk_bf16_f32 v174, v122, v124
	v_cvt_pk_bf16_f32 v175, v126, v128
	v_cvt_pk_bf16_f32 v176, v115, v117
	v_cvt_pk_bf16_f32 v177, v119, v121
	v_cvt_pk_bf16_f32 v178, v123, v125
	v_cvt_pk_bf16_f32 v179, v127, v129
	ds_write_b128 v95, v[172:175] offset:19456
	ds_write_b128 v95, v[176:179] offset:19584
	v_add_u32_e32 v91, s46, v135
	v_add_u32_e32 v93, s46, v137
	ds_read_b128 v[238:241], v139 offset:0
	ds_read_b128 v[242:245], v139 offset:2048
	ds_read_b128 v[246:249], v139 offset:4096
	ds_read_b128 v[250:253], v139 offset:6144
	ds_read_b128 v[218:221], v91 offset:0
	ds_read_b128 v[222:225], v91 offset:2048
	ds_read_b128 v[226:229], v91 offset:4096
	ds_read_b128 v[230:233], v91 offset:6144
	ds_read_b128 v[234:237], v91 offset:8192
	s_waitcnt lgkmcnt(0)
	v_mfma_f32_16x16x32_bf16 v[78:81], v[238:241], v[218:221], v[78:81]
	v_mfma_f32_16x16x32_bf16 v[74:77], v[242:245], v[218:221], v[74:77]
	v_mfma_f32_16x16x32_bf16 v[70:73], v[246:249], v[218:221], v[70:73]
	v_mfma_f32_16x16x32_bf16 v[66:69], v[250:253], v[218:221], v[66:69]
	ds_read_b128 v[218:221], v93 offset:0
	ds_read_b128 v[142:145], v141 offset:0
	s_add_i32 s51, s51, 1
	s_and_b32 s54, s51, 7
	s_cmp_eq_u32 s54, 0
	s_cselect_b32 s44, s34, s35
	s_cselect_b32 s45, -1, 0
	v_lshl_add_u64 v[132:133], v[132:133], 0, s[44:45]
	global_load_dwordx2 v[114:115], v[132:133], off
	v_lshl_add_u64 v[180:181], v[132:133], 0, s[24:25]
	global_load_dwordx2 v[116:117], v[180:181], off
	v_mfma_f32_16x16x32_bf16 v[62:65], v[238:241], v[222:225], v[62:65]
	v_mfma_f32_16x16x32_bf16 v[58:61], v[242:245], v[222:225], v[58:61]
	v_mfma_f32_16x16x32_bf16 v[54:57], v[246:249], v[222:225], v[54:57]
	v_mfma_f32_16x16x32_bf16 v[50:53], v[250:253], v[222:225], v[50:53]
	ds_read_b128 v[222:225], v93 offset:2048
	ds_read_b128 v[146:149], v141 offset:2048
	v_lshl_add_u64 v[180:181], v[132:133], 0, s[26:27]
	global_load_dwordx2 v[118:119], v[180:181], off
	v_lshl_add_u64 v[180:181], v[132:133], 0, s[28:29]
	global_load_dwordx2 v[120:121], v[180:181], off
	v_mfma_f32_16x16x32_bf16 v[46:49], v[238:241], v[226:229], v[46:49]
	v_mfma_f32_16x16x32_bf16 v[42:45], v[242:245], v[226:229], v[42:45]
	v_mfma_f32_16x16x32_bf16 v[38:41], v[246:249], v[226:229], v[38:41]
	v_mfma_f32_16x16x32_bf16 v[34:37], v[250:253], v[226:229], v[34:37]
	ds_read_b128 v[226:229], v93 offset:4096
	ds_read_b128 v[156:159], v141 offset:4096
	v_lshl_add_u64 v[180:181], v[132:133], 0, s[36:37]
	global_load_dwordx2 v[122:123], v[180:181], off
	v_lshl_add_u64 v[180:181], v[132:133], 0, s[38:39]
	global_load_dwordx2 v[124:125], v[180:181], off
	v_mfma_f32_16x16x32_bf16 v[18:21], v[238:241], v[230:233], v[18:21]
	v_mfma_f32_16x16x32_bf16 v[22:25], v[242:245], v[230:233], v[22:25]
	v_mfma_f32_16x16x32_bf16 v[26:29], v[246:249], v[230:233], v[26:29]
	v_mfma_f32_16x16x32_bf16 v[30:33], v[250:253], v[230:233], v[30:33]
	ds_read_b128 v[230:233], v93 offset:6144
	ds_read_b128 v[160:163], v141 offset:6144
	v_lshl_add_u64 v[180:181], v[132:133], 0, s[40:41]
	global_load_dwordx2 v[126:127], v[180:181], off
	v_lshl_add_u64 v[180:181], v[132:133], 0, s[42:43]
	global_load_dwordx2 v[128:129], v[180:181], off
	v_mfma_f32_16x16x32_bf16 v[2:5], v[238:241], v[234:237], v[2:5]
	v_mfma_f32_16x16x32_bf16 v[6:9], v[242:245], v[234:237], v[6:9]
	v_mfma_f32_16x16x32_bf16 v[10:13], v[246:249], v[234:237], v[10:13]
	v_mfma_f32_16x16x32_bf16 v[14:17], v[250:253], v[234:237], v[14:17]
	ds_read_b128 v[234:237], v93 offset:8192
	s_waitcnt vmcnt(31)
	s_waitcnt lgkmcnt(0)
	s_barrier
; #define MD_GLDS_A(buf, tau) do { _Pragma("unroll") for (int i = 0; i < 5; ++i) if (amask & (1u << i)) \
;         __builtin_amdgcn_global_load_lds((const unsigned*)((const char*)HIDp + aoff[i] + (size_t)((tau) & 7) * 128), (PG8_LAS unsigned*)(MD_SA(buf) + wid * 1024 + i * 8192), 16, 0, 0); } while (0)
; #define MD_B_ISSUE(sb, tau) do { const char* kb_ = Bb + (size_t)((tau) >> 3) * 512 + (size_t)((tau) & 7) * (64 * (size_t)RB); _Pragma("unroll") for (int j = 0; j < 8; ++j) { const char* p_ = kb_ + (size_t)j * RB; \
;         asm volatile("global_load_dwordx2 %0, %1, off" : "=&v"(sb[j]) : "v"(p_) : "memory"); } } while (0)
; #define MD_B_WAIT(sb, N) asm volatile("s_waitcnt vmcnt(%8)" : "+v"(sb[0]), "+v"(sb[1]), "+v"(sb[2]), "+v"(sb[3]), "+v"(sb[4]), "+v"(sb[5]), "+v"(sb[6]), "+v"(sb[7]) : "n"(N) : "memory")
; __device__ __forceinline__ void moe_down_stream(PG8_LAS unsigned char* lds, int e, int cb0, int slot0, int nv, const bf16_t* HIDp, const float* Wd, bf16_t* Y, const float* slot_w, const int* slot_dst) {
;     ...
;     f32x4 acc[DNM][4];
; #pragma unroll
;     for (int m = 0; m < DNM; ++m)
; #pragma unroll
;         for (int n = 0; n < 4; ++n) acc[m][n] = (f32x4){0.f, 0.f, 0.f, 0.f};
;     f32x2 s0[8], s1[8];
;     MD_GLDS_A(0, 0); MD_B_ISSUE(s0, 0); MD_B_ISSUE(s1, 1);
;     MD_B_WAIT(s0, 8); MD_B_WRITE(s0, 0); __builtin_amdgcn_sched_barrier(0); MD_B_ISSUE(s0, 2);
;     asm volatile("s_waitcnt vmcnt(16)" ::: "memory");
;     asm volatile("s_waitcnt lgkmcnt(0)" ::: "memory"); __builtin_amdgcn_s_barrier(); asm volatile("" ::: "memory");
; #pragma unroll 1
;     for (int t = 0; t < NT; t += 2) {
;         if (t + 2 < NT) MD_B_WAIT(s1, 8); else MD_B_WAIT(s1, 0);
;         MD_B_WRITE(s1, 1); __builtin_amdgcn_sched_barrier(0); MD_GLDS_A(1, t + 1); __builtin_amdgcn_sched_barrier(0);
;         if (t + 3 < NT) MD_B_ISSUE(s1, t + 3);
;         MD_COMPUTE(0);
;         MD_END(t + 3 >= NT);
;         if (t + 2 < NT) { MD_B_WAIT(s0, 8); MD_B_WRITE(s0, 0); __builtin_amdgcn_sched_barrier(0); MD_GLDS_A(0, t + 2); __builtin_amdgcn_sched_barrier(0); }
;         if (t + 4 < NT) MD_B_ISSUE(s0, t + 4);
;         MD_COMPUTE(1);
;         MD_END(t + 4 >= NT);
	s_mov_b32 s49, s46
	s_mov_b32 s46, s47
	s_mov_b32 s47, s48
	s_mov_b32 s48, s49
	s_add_i32 s50, s50, 1
	s_add_i32 s49, s48, s74
	s_add_i32 s52, s52, 1
	s_and_b32 s54, s52, 7
	s_cmp_eq_u32 s54, 0
	s_cselect_b32 s54, s53, s32
	s_cselect_b32 s55, -1, 0
	s_add_u32 s30, s30, s54
	s_addc_u32 s31, s31, s55
	v_mfma_f32_16x16x32_bf16 v[78:81], v[142:145], v[218:221], v[78:81]
	v_mfma_f32_16x16x32_bf16 v[74:77], v[146:149], v[218:221], v[74:77]
	v_mfma_f32_16x16x32_bf16 v[70:73], v[156:159], v[218:221], v[70:73]
	v_mfma_f32_16x16x32_bf16 v[66:69], v[160:163], v[218:221], v[66:69]
	s_mov_b32 m0, s49
	s_nop 0
	global_load_lds_dwordx4 v88, s[30:31]
	v_mfma_f32_16x16x32_bf16 v[62:65], v[142:145], v[222:225], v[62:65]
	v_mfma_f32_16x16x32_bf16 v[58:61], v[146:149], v[222:225], v[58:61]
	v_mfma_f32_16x16x32_bf16 v[54:57], v[156:159], v[222:225], v[54:57]
	v_mfma_f32_16x16x32_bf16 v[50:53], v[160:163], v[222:225], v[50:53]
	s_add_i32 m0, s49, 0x2000
	s_nop 0
	global_load_lds_dwordx4 v90, s[30:31]
	v_mfma_f32_16x16x32_bf16 v[46:49], v[142:145], v[226:229], v[46:49]
	v_mfma_f32_16x16x32_bf16 v[42:45], v[146:149], v[226:229], v[42:45]
	v_mfma_f32_16x16x32_bf16 v[38:41], v[156:159], v[226:229], v[38:41]
	v_mfma_f32_16x16x32_bf16 v[34:37], v[160:163], v[226:229], v[34:37]
	s_add_i32 m0, s49, 0x4000
	s_nop 0
	global_load_lds_dwordx4 v92, s[30:31]
	v_mfma_f32_16x16x32_bf16 v[18:21], v[142:145], v[230:233], v[18:21]
	v_mfma_f32_16x16x32_bf16 v[22:25], v[146:149], v[230:233], v[22:25]
	v_mfma_f32_16x16x32_bf16 v[26:29], v[156:159], v[230:233], v[26:29]
	v_mfma_f32_16x16x32_bf16 v[30:33], v[160:163], v[230:233], v[30:33]
	s_add_i32 m0, s49, 0x6000
	s_nop 0
	global_load_lds_dwordx4 v94, s[30:31]
	v_mfma_f32_16x16x32_bf16 v[2:5], v[142:145], v[234:237], v[2:5]
	v_mfma_f32_16x16x32_bf16 v[6:9], v[146:149], v[234:237], v[6:9]
	v_mfma_f32_16x16x32_bf16 v[10:13], v[156:159], v[234:237], v[10:13]
	v_mfma_f32_16x16x32_bf16 v[14:17], v[160:163], v[234:237], v[14:17]
	s_add_i32 m0, s49, 0x8000
	s_nop 0
	global_load_lds_dwordx4 v96, s[30:31]
	v_cvt_pk_bf16_f32 v172, v186, v188
	v_cvt_pk_bf16_f32 v173, v190, v192
	v_cvt_pk_bf16_f32 v174, v194, v196
	v_cvt_pk_bf16_f32 v175, v198, v200
	v_cvt_pk_bf16_f32 v176, v187, v189
	v_cvt_pk_bf16_f32 v177, v191, v193
	v_cvt_pk_bf16_f32 v178, v195, v197
	v_cvt_pk_bf16_f32 v179, v199, v201
	ds_write_b128 v95, v[172:175] offset:0
	ds_write_b128 v95, v[176:179] offset:128
	v_add_u32_e32 v91, s46, v135
	v_add_u32_e32 v93, s46, v137
	ds_read_b128 v[238:241], v139 offset:19456
	ds_read_b128 v[242:245], v139 offset:21504
	ds_read_b128 v[246:249], v139 offset:23552
	ds_read_b128 v[250:253], v139 offset:25600
	ds_read_b128 v[218:221], v91 offset:0
	ds_read_b128 v[222:225], v91 offset:2048
	ds_read_b128 v[226:229], v91 offset:4096
	ds_read_b128 v[230:233], v91 offset:6144
	ds_read_b128 v[234:237], v91 offset:8192
	s_waitcnt lgkmcnt(0)
	v_mfma_f32_16x16x32_bf16 v[78:81], v[238:241], v[218:221], v[78:81]
	v_mfma_f32_16x16x32_bf16 v[74:77], v[242:245], v[218:221], v[74:77]
	v_mfma_f32_16x16x32_bf16 v[70:73], v[246:249], v[218:221], v[70:73]
	v_mfma_f32_16x16x32_bf16 v[66:69], v[250:253], v[218:221], v[66:69]
	ds_read_b128 v[218:221], v93 offset:0
	ds_read_b128 v[142:145], v141 offset:19456
	s_add_i32 s51, s51, 1
	s_and_b32 s54, s51, 7
	s_cmp_eq_u32 s54, 0
	s_cselect_b32 s44, s34, s35
	s_cselect_b32 s45, -1, 0
	v_lshl_add_u64 v[132:133], v[132:133], 0, s[44:45]
	global_load_dwordx2 v[186:187], v[132:133], off
	v_lshl_add_u64 v[180:181], v[132:133], 0, s[24:25]
	global_load_dwordx2 v[188:189], v[180:181], off
	v_mfma_f32_16x16x32_bf16 v[62:65], v[238:241], v[222:225], v[62:65]
	v_mfma_f32_16x16x32_bf16 v[58:61], v[242:245], v[222:225], v[58:61]
	v_mfma_f32_16x16x32_bf16 v[54:57], v[246:249], v[222:225], v[54:57]
	v_mfma_f32_16x16x32_bf16 v[50:53], v[250:253], v[222:225], v[50:53]
	ds_read_b128 v[222:225], v93 offset:2048
	ds_read_b128 v[146:149], v141 offset:21504
	v_lshl_add_u64 v[180:181], v[132:133], 0, s[26:27]
	global_load_dwordx2 v[190:191], v[180:181], off
	v_lshl_add_u64 v[180:181], v[132:133], 0, s[28:29]
	global_load_dwordx2 v[192:193], v[180:181], off
	v_mfma_f32_16x16x32_bf16 v[46:49], v[238:241], v[226:229], v[46:49]
	v_mfma_f32_16x16x32_bf16 v[42:45], v[242:245], v[226:229], v[42:45]
	v_mfma_f32_16x16x32_bf16 v[38:41], v[246:249], v[226:229], v[38:41]
	v_mfma_f32_16x16x32_bf16 v[34:37], v[250:253], v[226:229], v[34:37]
	ds_read_b128 v[226:229], v93 offset:4096
	ds_read_b128 v[156:159], v141 offset:23552
	v_lshl_add_u64 v[180:181], v[132:133], 0, s[36:37]
	global_load_dwordx2 v[194:195], v[180:181], off
	v_lshl_add_u64 v[180:181], v[132:133], 0, s[38:39]
	global_load_dwordx2 v[196:197], v[180:181], off
	v_mfma_f32_16x16x32_bf16 v[18:21], v[238:241], v[230:233], v[18:21]
	v_mfma_f32_16x16x32_bf16 v[22:25], v[242:245], v[230:233], v[22:25]
	v_mfma_f32_16x16x32_bf16 v[26:29], v[246:249], v[230:233], v[26:29]
	v_mfma_f32_16x16x32_bf16 v[30:33], v[250:253], v[230:233], v[30:33]
	ds_read_b128 v[230:233], v93 offset:6144
	ds_read_b128 v[160:163], v141 offset:25600
	v_lshl_add_u64 v[180:181], v[132:133], 0, s[40:41]
	global_load_dwordx2 v[198:199], v[180:181], off
	v_lshl_add_u64 v[180:181], v[132:133], 0, s[42:43]
	global_load_dwordx2 v[200:201], v[180:181], off
	v_mfma_f32_16x16x32_bf16 v[2:5], v[238:241], v[234:237], v[2:5]
	v_mfma_f32_16x16x32_bf16 v[6:9], v[242:245], v[234:237], v[6:9]
	v_mfma_f32_16x16x32_bf16 v[10:13], v[246:249], v[234:237], v[10:13]
	v_mfma_f32_16x16x32_bf16 v[14:17], v[250:253], v[234:237], v[14:17]
	ds_read_b128 v[234:237], v93 offset:8192
	s_waitcnt vmcnt(21)
	s_waitcnt lgkmcnt(0)
	s_barrier
; #define MD_GLDS_A(buf, tau) do { _Pragma("unroll") for (int i = 0; i < 5; ++i) if (amask & (1u << i)) \
;         __builtin_amdgcn_global_load_lds((const unsigned*)((const char*)HIDp + aoff[i] + (size_t)((tau) & 7) * 128), (PG8_LAS unsigned*)(MD_SA(buf) + wid * 1024 + i * 8192), 16, 0, 0); } while (0)
; #define MD_B_ISSUE(sb, tau) do { const char* kb_ = Bb + (size_t)((tau) >> 3) * 512 + (size_t)((tau) & 7) * (64 * (size_t)RB); _Pragma("unroll") for (int j = 0; j < 8; ++j) { const char* p_ = kb_ + (size_t)j * RB; \
;         asm volatile("global_load_dwordx2 %0, %1, off" : "=&v"(sb[j]) : "v"(p_) : "memory"); } } while (0)
; #define MD_B_WAIT(sb, N) asm volatile("s_waitcnt vmcnt(%8)" : "+v"(sb[0]), "+v"(sb[1]), "+v"(sb[2]), "+v"(sb[3]), "+v"(sb[4]), "+v"(sb[5]), "+v"(sb[6]), "+v"(sb[7]) : "n"(N) : "memory")
; __device__ __forceinline__ void moe_down_stream(PG8_LAS unsigned char* lds, int e, int cb0, int slot0, int nv, const bf16_t* HIDp, const float* Wd, bf16_t* Y, const float* slot_w, const int* slot_dst) {
;     ...
;     f32x4 acc[DNM][4];
; #pragma unroll
;     for (int m = 0; m < DNM; ++m)
; #pragma unroll
;         for (int n = 0; n < 4; ++n) acc[m][n] = (f32x4){0.f, 0.f, 0.f, 0.f};
;     f32x2 s0[8], s1[8];
;     MD_GLDS_A(0, 0); MD_B_ISSUE(s0, 0); MD_B_ISSUE(s1, 1);
;     MD_B_WAIT(s0, 8); MD_B_WRITE(s0, 0); __builtin_amdgcn_sched_barrier(0); MD_B_ISSUE(s0, 2);
;     asm volatile("s_waitcnt vmcnt(16)" ::: "memory");
;     asm volatile("s_waitcnt lgkmcnt(0)" ::: "memory"); __builtin_amdgcn_s_barrier(); asm volatile("" ::: "memory");
; #pragma unroll 1
;     for (int t = 0; t < NT; t += 2) {
;         if (t + 2 < NT) MD_B_WAIT(s1, 8); else MD_B_WAIT(s1, 0);
;         MD_B_WRITE(s1, 1); __builtin_amdgcn_sched_barrier(0); MD_GLDS_A(1, t + 1); __builtin_amdgcn_sched_barrier(0);
;         if (t + 3 < NT) MD_B_ISSUE(s1, t + 3);
;         MD_COMPUTE(0);
;         MD_END(t + 3 >= NT);
;         if (t + 2 < NT) { MD_B_WAIT(s0, 8); MD_B_WRITE(s0, 0); __builtin_amdgcn_sched_barrier(0); MD_GLDS_A(0, t + 2); __builtin_amdgcn_sched_barrier(0); }
;         if (t + 4 < NT) MD_B_ISSUE(s0, t + 4);
;         MD_COMPUTE(1);
;         MD_END(t + 4 >= NT);
	s_mov_b32 s49, s46
	s_mov_b32 s46, s47
	s_mov_b32 s47, s48
	s_mov_b32 s48, s49
	s_add_i32 s50, s50, 1
	s_add_i32 s49, s48, s74
	s_add_i32 s52, s52, 1
	s_and_b32 s54, s52, 7
	s_cmp_eq_u32 s54, 0
	s_cselect_b32 s54, s53, s32
	s_cselect_b32 s55, -1, 0
	s_add_u32 s30, s30, s54
	s_addc_u32 s31, s31, s55
	v_mfma_f32_16x16x32_bf16 v[78:81], v[142:145], v[218:221], v[78:81]
	v_mfma_f32_16x16x32_bf16 v[74:77], v[146:149], v[218:221], v[74:77]
	v_mfma_f32_16x16x32_bf16 v[70:73], v[156:159], v[218:221], v[70:73]
	v_mfma_f32_16x16x32_bf16 v[66:69], v[160:163], v[218:221], v[66:69]
	s_mov_b32 m0, s49
	s_nop 0
	global_load_lds_dwordx4 v88, s[30:31]
	v_mfma_f32_16x16x32_bf16 v[62:65], v[142:145], v[222:225], v[62:65]
	v_mfma_f32_16x16x32_bf16 v[58:61], v[146:149], v[222:225], v[58:61]
	v_mfma_f32_16x16x32_bf16 v[54:57], v[156:159], v[222:225], v[54:57]
	v_mfma_f32_16x16x32_bf16 v[50:53], v[160:163], v[222:225], v[50:53]
	s_add_i32 m0, s49, 0x2000
	s_nop 0
	global_load_lds_dwordx4 v90, s[30:31]
	v_mfma_f32_16x16x32_bf16 v[46:49], v[142:145], v[226:229], v[46:49]
	v_mfma_f32_16x16x32_bf16 v[42:45], v[146:149], v[226:229], v[42:45]
	v_mfma_f32_16x16x32_bf16 v[38:41], v[156:159], v[226:229], v[38:41]
	v_mfma_f32_16x16x32_bf16 v[34:37], v[160:163], v[226:229], v[34:37]
	s_add_i32 m0, s49, 0x4000
	s_nop 0
	global_load_lds_dwordx4 v92, s[30:31]
	v_mfma_f32_16x16x32_bf16 v[18:21], v[142:145], v[230:233], v[18:21]
	v_mfma_f32_16x16x32_bf16 v[22:25], v[146:149], v[230:233], v[22:25]
	v_mfma_f32_16x16x32_bf16 v[26:29], v[156:159], v[230:233], v[26:29]
	v_mfma_f32_16x16x32_bf16 v[30:33], v[160:163], v[230:233], v[30:33]
	s_add_i32 m0, s49, 0x6000
	s_nop 0
	global_load_lds_dwordx4 v94, s[30:31]
	v_mfma_f32_16x16x32_bf16 v[2:5], v[142:145], v[234:237], v[2:5]
	v_mfma_f32_16x16x32_bf16 v[6:9], v[146:149], v[234:237], v[6:9]
	v_mfma_f32_16x16x32_bf16 v[10:13], v[156:159], v[234:237], v[10:13]
	v_mfma_f32_16x16x32_bf16 v[14:17], v[160:163], v[234:237], v[14:17]
	s_add_i32 m0, s49, 0x8000
	s_nop 0
	global_load_lds_dwordx4 v96, s[30:31]
	v_cvt_pk_bf16_f32 v172, v202, v204
	v_cvt_pk_bf16_f32 v173, v206, v208
	v_cvt_pk_bf16_f32 v174, v210, v212
	v_cvt_pk_bf16_f32 v175, v214, v216
	v_cvt_pk_bf16_f32 v176, v203, v205
	v_cvt_pk_bf16_f32 v177, v207, v209
	v_cvt_pk_bf16_f32 v178, v211, v213
	v_cvt_pk_bf16_f32 v179, v215, v217
	ds_write_b128 v95, v[172:175] offset:19456
	ds_write_b128 v95, v[176:179] offset:19584
	v_add_u32_e32 v91, s46, v135
	v_add_u32_e32 v93, s46, v137
	ds_read_b128 v[238:241], v139 offset:0
	ds_read_b128 v[242:245], v139 offset:2048
	ds_read_b128 v[246:249], v139 offset:4096
	ds_read_b128 v[250:253], v139 offset:6144
	ds_read_b128 v[218:221], v91 offset:0
	ds_read_b128 v[222:225], v91 offset:2048
	ds_read_b128 v[226:229], v91 offset:4096
	ds_read_b128 v[230:233], v91 offset:6144
	ds_read_b128 v[234:237], v91 offset:8192
	s_waitcnt lgkmcnt(0)
	v_mfma_f32_16x16x32_bf16 v[78:81], v[238:241], v[218:221], v[78:81]
	v_mfma_f32_16x16x32_bf16 v[74:77], v[242:245], v[218:221], v[74:77]
	v_mfma_f32_16x16x32_bf16 v[70:73], v[246:249], v[218:221], v[70:73]
	v_mfma_f32_16x16x32_bf16 v[66:69], v[250:253], v[218:221], v[66:69]
	ds_read_b128 v[218:221], v93 offset:0
	ds_read_b128 v[142:145], v141 offset:0
	s_add_i32 s51, s51, 1
	s_and_b32 s54, s51, 7
	s_cmp_eq_u32 s54, 0
	s_cselect_b32 s44, s34, s35
	s_cselect_b32 s45, -1, 0
	v_lshl_add_u64 v[132:133], v[132:133], 0, s[44:45]
	global_load_dwordx2 v[202:203], v[132:133], off
	v_lshl_add_u64 v[180:181], v[132:133], 0, s[24:25]
	global_load_dwordx2 v[204:205], v[180:181], off
	v_mfma_f32_16x16x32_bf16 v[62:65], v[238:241], v[222:225], v[62:65]
	v_mfma_f32_16x16x32_bf16 v[58:61], v[242:245], v[222:225], v[58:61]
	v_mfma_f32_16x16x32_bf16 v[54:57], v[246:249], v[222:225], v[54:57]
	v_mfma_f32_16x16x32_bf16 v[50:53], v[250:253], v[222:225], v[50:53]
	ds_read_b128 v[222:225], v93 offset:2048
	ds_read_b128 v[146:149], v141 offset:2048
	v_lshl_add_u64 v[180:181], v[132:133], 0, s[26:27]
	global_load_dwordx2 v[206:207], v[180:181], off
	v_lshl_add_u64 v[180:181], v[132:133], 0, s[28:29]
	global_load_dwordx2 v[208:209], v[180:181], off
	v_mfma_f32_16x16x32_bf16 v[46:49], v[238:241], v[226:229], v[46:49]
	v_mfma_f32_16x16x32_bf16 v[42:45], v[242:245], v[226:229], v[42:45]
	v_mfma_f32_16x16x32_bf16 v[38:41], v[246:249], v[226:229], v[38:41]
	v_mfma_f32_16x16x32_bf16 v[34:37], v[250:253], v[226:229], v[34:37]
	ds_read_b128 v[226:229], v93 offset:4096
	ds_read_b128 v[156:159], v141 offset:4096
	v_lshl_add_u64 v[180:181], v[132:133], 0, s[36:37]
	global_load_dwordx2 v[210:211], v[180:181], off
	v_lshl_add_u64 v[180:181], v[132:133], 0, s[38:39]
	global_load_dwordx2 v[212:213], v[180:181], off
	v_mfma_f32_16x16x32_bf16 v[18:21], v[238:241], v[230:233], v[18:21]
	v_mfma_f32_16x16x32_bf16 v[22:25], v[242:245], v[230:233], v[22:25]
	v_mfma_f32_16x16x32_bf16 v[26:29], v[246:249], v[230:233], v[26:29]
	v_mfma_f32_16x16x32_bf16 v[30:33], v[250:253], v[230:233], v[30:33]
	ds_read_b128 v[230:233], v93 offset:6144
	ds_read_b128 v[160:163], v141 offset:6144
	v_lshl_add_u64 v[180:181], v[132:133], 0, s[40:41]
	global_load_dwordx2 v[214:215], v[180:181], off
	v_lshl_add_u64 v[180:181], v[132:133], 0, s[42:43]
	global_load_dwordx2 v[216:217], v[180:181], off
	v_mfma_f32_16x16x32_bf16 v[2:5], v[238:241], v[234:237], v[2:5]
	v_mfma_f32_16x16x32_bf16 v[6:9], v[242:245], v[234:237], v[6:9]
	v_mfma_f32_16x16x32_bf16 v[10:13], v[246:249], v[234:237], v[10:13]
	v_mfma_f32_16x16x32_bf16 v[14:17], v[250:253], v[234:237], v[14:17]
	ds_read_b128 v[234:237], v93 offset:8192
	s_waitcnt vmcnt(21)
	s_waitcnt lgkmcnt(0)
	s_barrier
; #define MD_GLDS_A(buf, tau) do { _Pragma("unroll") for (int i = 0; i < 5; ++i) if (amask & (1u << i)) \
;         __builtin_amdgcn_global_load_lds((const unsigned*)((const char*)HIDp + aoff[i] + (size_t)((tau) & 7) * 128), (PG8_LAS unsigned*)(MD_SA(buf) + wid * 1024 + i * 8192), 16, 0, 0); } while (0)
; #define MD_B_ISSUE(sb, tau) do { const char* kb_ = Bb + (size_t)((tau) >> 3) * 512 + (size_t)((tau) & 7) * (64 * (size_t)RB); _Pragma("unroll") for (int j = 0; j < 8; ++j) { const char* p_ = kb_ + (size_t)j * RB; \
;         asm volatile("global_load_dwordx2 %0, %1, off" : "=&v"(sb[j]) : "v"(p_) : "memory"); } } while (0)
; #define MD_B_WAIT(sb, N) asm volatile("s_waitcnt vmcnt(%8)" : "+v"(sb[0]), "+v"(sb[1]), "+v"(sb[2]), "+v"(sb[3]), "+v"(sb[4]), "+v"(sb[5]), "+v"(sb[6]), "+v"(sb[7]) : "n"(N) : "memory")
; __device__ __forceinline__ void moe_down_stream(PG8_LAS unsigned char* lds, int e, int cb0, int slot0, int nv, const bf16_t* HIDp, const float* Wd, bf16_t* Y, const float* slot_w, const int* slot_dst) {
;     ...
;     f32x4 acc[DNM][4];
; #pragma unroll
;     for (int m = 0; m < DNM; ++m)
; #pragma unroll
;         for (int n = 0; n < 4; ++n) acc[m][n] = (f32x4){0.f, 0.f, 0.f, 0.f};
;     f32x2 s0[8], s1[8];
;     MD_GLDS_A(0, 0); MD_B_ISSUE(s0, 0); MD_B_ISSUE(s1, 1);
;     MD_B_WAIT(s0, 8); MD_B_WRITE(s0, 0); __builtin_amdgcn_sched_barrier(0); MD_B_ISSUE(s0, 2);
;     asm volatile("s_waitcnt vmcnt(16)" ::: "memory");
;     asm volatile("s_waitcnt lgkmcnt(0)" ::: "memory"); __builtin_amdgcn_s_barrier(); asm volatile("" ::: "memory");
; #pragma unroll 1
;     for (int t = 0; t < NT; t += 2) {
;         if (t + 2 < NT) MD_B_WAIT(s1, 8); else MD_B_WAIT(s1, 0);
;         MD_B_WRITE(s1, 1); __builtin_amdgcn_sched_barrier(0); MD_GLDS_A(1, t + 1); __builtin_amdgcn_sched_barrier(0);
;         if (t + 3 < NT) MD_B_ISSUE(s1, t + 3);
;         MD_COMPUTE(0);
;         MD_END(t + 3 >= NT);
;         if (t + 2 < NT) { MD_B_WAIT(s0, 8); MD_B_WRITE(s0, 0); __builtin_amdgcn_sched_barrier(0); MD_GLDS_A(0, t + 2); __builtin_amdgcn_sched_barrier(0); }
;         if (t + 4 < NT) MD_B_ISSUE(s0, t + 4);
;         MD_COMPUTE(1);
;         MD_END(t + 4 >= NT);
	s_mov_b32 s49, s46
	s_mov_b32 s46, s47
	s_mov_b32 s47, s48
	s_mov_b32 s48, s49
	s_add_i32 s50, s50, 1
	s_add_i32 s49, s48, s74
	s_add_i32 s52, s52, 1
	s_and_b32 s54, s52, 7
	s_cmp_eq_u32 s54, 0
	s_cselect_b32 s54, s53, s32
	s_cselect_b32 s55, -1, 0
	s_add_u32 s30, s30, s54
	s_addc_u32 s31, s31, s55
	v_mfma_f32_16x16x32_bf16 v[78:81], v[142:145], v[218:221], v[78:81]
	v_mfma_f32_16x16x32_bf16 v[74:77], v[146:149], v[218:221], v[74:77]
	v_mfma_f32_16x16x32_bf16 v[70:73], v[156:159], v[218:221], v[70:73]
	v_mfma_f32_16x16x32_bf16 v[66:69], v[160:163], v[218:221], v[66:69]
	s_mov_b32 m0, s49
	s_nop 0
	global_load_lds_dwordx4 v88, s[30:31]
	v_mfma_f32_16x16x32_bf16 v[62:65], v[142:145], v[222:225], v[62:65]
	v_mfma_f32_16x16x32_bf16 v[58:61], v[146:149], v[222:225], v[58:61]
	v_mfma_f32_16x16x32_bf16 v[54:57], v[156:159], v[222:225], v[54:57]
	v_mfma_f32_16x16x32_bf16 v[50:53], v[160:163], v[222:225], v[50:53]
	s_add_i32 m0, s49, 0x2000
	s_nop 0
	global_load_lds_dwordx4 v90, s[30:31]
	v_mfma_f32_16x16x32_bf16 v[46:49], v[142:145], v[226:229], v[46:49]
	v_mfma_f32_16x16x32_bf16 v[42:45], v[146:149], v[226:229], v[42:45]
	v_mfma_f32_16x16x32_bf16 v[38:41], v[156:159], v[226:229], v[38:41]
	v_mfma_f32_16x16x32_bf16 v[34:37], v[160:163], v[226:229], v[34:37]
	s_add_i32 m0, s49, 0x4000
	s_nop 0
	global_load_lds_dwordx4 v92, s[30:31]
	v_mfma_f32_16x16x32_bf16 v[18:21], v[142:145], v[230:233], v[18:21]
	v_mfma_f32_16x16x32_bf16 v[22:25], v[146:149], v[230:233], v[22:25]
	v_mfma_f32_16x16x32_bf16 v[26:29], v[156:159], v[230:233], v[26:29]
	v_mfma_f32_16x16x32_bf16 v[30:33], v[160:163], v[230:233], v[30:33]
	s_add_i32 m0, s49, 0x6000
	s_nop 0
	global_load_lds_dwordx4 v94, s[30:31]
	v_mfma_f32_16x16x32_bf16 v[2:5], v[142:145], v[234:237], v[2:5]
	v_mfma_f32_16x16x32_bf16 v[6:9], v[146:149], v[234:237], v[6:9]
	v_mfma_f32_16x16x32_bf16 v[10:13], v[156:159], v[234:237], v[10:13]
	v_mfma_f32_16x16x32_bf16 v[14:17], v[160:163], v[234:237], v[14:17]
	s_add_i32 m0, s49, 0x8000
	s_nop 0
	global_load_lds_dwordx4 v96, s[30:31]
	v_cvt_pk_bf16_f32 v172, v98, v100
	v_cvt_pk_bf16_f32 v173, v102, v104
	v_cvt_pk_bf16_f32 v174, v106, v108
	v_cvt_pk_bf16_f32 v175, v110, v112
	v_cvt_pk_bf16_f32 v176, v99, v101
	v_cvt_pk_bf16_f32 v177, v103, v105
	v_cvt_pk_bf16_f32 v178, v107, v109
	v_cvt_pk_bf16_f32 v179, v111, v113
	ds_write_b128 v95, v[172:175] offset:0
	ds_write_b128 v95, v[176:179] offset:128
	v_add_u32_e32 v91, s46, v135
	v_add_u32_e32 v93, s46, v137
	ds_read_b128 v[238:241], v139 offset:19456
	ds_read_b128 v[242:245], v139 offset:21504
	ds_read_b128 v[246:249], v139 offset:23552
	ds_read_b128 v[250:253], v139 offset:25600
	ds_read_b128 v[218:221], v91 offset:0
	ds_read_b128 v[222:225], v91 offset:2048
	ds_read_b128 v[226:229], v91 offset:4096
	ds_read_b128 v[230:233], v91 offset:6144
	ds_read_b128 v[234:237], v91 offset:8192
	s_waitcnt lgkmcnt(0)
	v_mfma_f32_16x16x32_bf16 v[78:81], v[238:241], v[218:221], v[78:81]
	v_mfma_f32_16x16x32_bf16 v[74:77], v[242:245], v[218:221], v[74:77]
	v_mfma_f32_16x16x32_bf16 v[70:73], v[246:249], v[218:221], v[70:73]
	v_mfma_f32_16x16x32_bf16 v[66:69], v[250:253], v[218:221], v[66:69]
	ds_read_b128 v[218:221], v93 offset:0
	ds_read_b128 v[142:145], v141 offset:19456
	v_mfma_f32_16x16x32_bf16 v[62:65], v[238:241], v[222:225], v[62:65]
	v_mfma_f32_16x16x32_bf16 v[58:61], v[242:245], v[222:225], v[58:61]
	v_mfma_f32_16x16x32_bf16 v[54:57], v[246:249], v[222:225], v[54:57]
	v_mfma_f32_16x16x32_bf16 v[50:53], v[250:253], v[222:225], v[50:53]
	ds_read_b128 v[222:225], v93 offset:2048
	ds_read_b128 v[146:149], v141 offset:21504
	v_mfma_f32_16x16x32_bf16 v[46:49], v[238:241], v[226:229], v[46:49]
	v_mfma_f32_16x16x32_bf16 v[42:45], v[242:245], v[226:229], v[42:45]
	v_mfma_f32_16x16x32_bf16 v[38:41], v[246:249], v[226:229], v[38:41]
	v_mfma_f32_16x16x32_bf16 v[34:37], v[250:253], v[226:229], v[34:37]
	ds_read_b128 v[226:229], v93 offset:4096
	ds_read_b128 v[156:159], v141 offset:23552
	v_mfma_f32_16x16x32_bf16 v[18:21], v[238:241], v[230:233], v[18:21]
	v_mfma_f32_16x16x32_bf16 v[22:25], v[242:245], v[230:233], v[22:25]
	v_mfma_f32_16x16x32_bf16 v[26:29], v[246:249], v[230:233], v[26:29]
	v_mfma_f32_16x16x32_bf16 v[30:33], v[250:253], v[230:233], v[30:33]
	ds_read_b128 v[230:233], v93 offset:6144
	ds_read_b128 v[160:163], v141 offset:25600
	v_mfma_f32_16x16x32_bf16 v[2:5], v[238:241], v[234:237], v[2:5]
	v_mfma_f32_16x16x32_bf16 v[6:9], v[242:245], v[234:237], v[6:9]
	v_mfma_f32_16x16x32_bf16 v[10:13], v[246:249], v[234:237], v[10:13]
	v_mfma_f32_16x16x32_bf16 v[14:17], v[250:253], v[234:237], v[14:17]
	ds_read_b128 v[234:237], v93 offset:8192
	s_waitcnt vmcnt(13)
	s_waitcnt lgkmcnt(0)
	s_barrier
; #define MD_GLDS_A(buf, tau) do { _Pragma("unroll") for (int i = 0; i < 5; ++i) if (amask & (1u << i)) \
;         __builtin_amdgcn_global_load_lds((const unsigned*)((const char*)HIDp + aoff[i] + (size_t)((tau) & 7) * 128), (PG8_LAS unsigned*)(MD_SA(buf) + wid * 1024 + i * 8192), 16, 0, 0); } while (0)
; #define MD_B_ISSUE(sb, tau) do { const char* kb_ = Bb + (size_t)((tau) >> 3) * 512 + (size_t)((tau) & 7) * (64 * (size_t)RB); _Pragma("unroll") for (int j = 0; j < 8; ++j) { const char* p_ = kb_ + (size_t)j * RB; \
;         asm volatile("global_load_dwordx2 %0, %1, off" : "=&v"(sb[j]) : "v"(p_) : "memory"); } } while (0)
; #define MD_B_WAIT(sb, N) asm volatile("s_waitcnt vmcnt(%8)" : "+v"(sb[0]), "+v"(sb[1]), "+v"(sb[2]), "+v"(sb[3]), "+v"(sb[4]), "+v"(sb[5]), "+v"(sb[6]), "+v"(sb[7]) : "n"(N) : "memory")
; __device__ __forceinline__ void moe_down_stream(PG8_LAS unsigned char* lds, int e, int cb0, int slot0, int nv, const bf16_t* HIDp, const float* Wd, bf16_t* Y, const float* slot_w, const int* slot_dst) {
;     ...
;     f32x4 acc[DNM][4];
; #pragma unroll
;     for (int m = 0; m < DNM; ++m)
; #pragma unroll
;         for (int n = 0; n < 4; ++n) acc[m][n] = (f32x4){0.f, 0.f, 0.f, 0.f};
;     f32x2 s0[8], s1[8];
;     MD_GLDS_A(0, 0); MD_B_ISSUE(s0, 0); MD_B_ISSUE(s1, 1);
;     MD_B_WAIT(s0, 8); MD_B_WRITE(s0, 0); __builtin_amdgcn_sched_barrier(0); MD_B_ISSUE(s0, 2);
;     asm volatile("s_waitcnt vmcnt(16)" ::: "memory");
;     asm volatile("s_waitcnt lgkmcnt(0)" ::: "memory"); __builtin_amdgcn_s_barrier(); asm volatile("" ::: "memory");
; #pragma unroll 1
;     for (int t = 0; t < NT; t += 2) {
;         if (t + 2 < NT) MD_B_WAIT(s1, 8); else MD_B_WAIT(s1, 0);
;         MD_B_WRITE(s1, 1); __builtin_amdgcn_sched_barrier(0); MD_GLDS_A(1, t + 1); __builtin_amdgcn_sched_barrier(0);
;         if (t + 3 < NT) MD_B_ISSUE(s1, t + 3);
;         MD_COMPUTE(0);
;         MD_END(t + 3 >= NT);
;         if (t + 2 < NT) { MD_B_WAIT(s0, 8); MD_B_WRITE(s0, 0); __builtin_amdgcn_sched_barrier(0); MD_GLDS_A(0, t + 2); __builtin_amdgcn_sched_barrier(0); }
;         if (t + 4 < NT) MD_B_ISSUE(s0, t + 4);
;         MD_COMPUTE(1);
;         MD_END(t + 4 >= NT);
	s_mov_b32 s49, s46
	s_mov_b32 s46, s47
	s_mov_b32 s47, s48
	s_mov_b32 s48, s49
	s_add_i32 s50, s50, 1
	s_add_i32 s49, s48, s74
	s_add_i32 s52, s52, 1
	s_and_b32 s54, s52, 7
	s_cmp_eq_u32 s54, 0
	s_cselect_b32 s54, s53, s32
	s_cselect_b32 s55, -1, 0
	s_add_u32 s30, s30, s54
	s_addc_u32 s31, s31, s55
	v_mfma_f32_16x16x32_bf16 v[78:81], v[142:145], v[218:221], v[78:81]
	v_mfma_f32_16x16x32_bf16 v[74:77], v[146:149], v[218:221], v[74:77]
	v_mfma_f32_16x16x32_bf16 v[70:73], v[156:159], v[218:221], v[70:73]
	v_mfma_f32_16x16x32_bf16 v[66:69], v[160:163], v[218:221], v[66:69]
	s_mov_b32 m0, s49
	s_nop 0
	global_load_lds_dwordx4 v88, s[30:31]
	v_mfma_f32_16x16x32_bf16 v[62:65], v[142:145], v[222:225], v[62:65]
	v_mfma_f32_16x16x32_bf16 v[58:61], v[146:149], v[222:225], v[58:61]
	v_mfma_f32_16x16x32_bf16 v[54:57], v[156:159], v[222:225], v[54:57]
	v_mfma_f32_16x16x32_bf16 v[50:53], v[160:163], v[222:225], v[50:53]
	s_add_i32 m0, s49, 0x2000
	s_nop 0
	global_load_lds_dwordx4 v90, s[30:31]
	v_mfma_f32_16x16x32_bf16 v[46:49], v[142:145], v[226:229], v[46:49]
	v_mfma_f32_16x16x32_bf16 v[42:45], v[146:149], v[226:229], v[42:45]
	v_mfma_f32_16x16x32_bf16 v[38:41], v[156:159], v[226:229], v[38:41]
	v_mfma_f32_16x16x32_bf16 v[34:37], v[160:163], v[226:229], v[34:37]
	s_add_i32 m0, s49, 0x4000
	s_nop 0
	global_load_lds_dwordx4 v92, s[30:31]
	v_mfma_f32_16x16x32_bf16 v[18:21], v[142:145], v[230:233], v[18:21]
	v_mfma_f32_16x16x32_bf16 v[22:25], v[146:149], v[230:233], v[22:25]
	v_mfma_f32_16x16x32_bf16 v[26:29], v[156:159], v[230:233], v[26:29]
	v_mfma_f32_16x16x32_bf16 v[30:33], v[160:163], v[230:233], v[30:33]
	s_add_i32 m0, s49, 0x6000
	s_nop 0
	global_load_lds_dwordx4 v94, s[30:31]
	v_mfma_f32_16x16x32_bf16 v[2:5], v[142:145], v[234:237], v[2:5]
	v_mfma_f32_16x16x32_bf16 v[6:9], v[146:149], v[234:237], v[6:9]
	v_mfma_f32_16x16x32_bf16 v[10:13], v[156:159], v[234:237], v[10:13]
	v_mfma_f32_16x16x32_bf16 v[14:17], v[160:163], v[234:237], v[14:17]
	s_add_i32 m0, s49, 0x8000
	s_nop 0
	global_load_lds_dwordx4 v96, s[30:31]
	v_cvt_pk_bf16_f32 v172, v114, v116
	v_cvt_pk_bf16_f32 v173, v118, v120
	v_cvt_pk_bf16_f32 v174, v122, v124
	v_cvt_pk_bf16_f32 v175, v126, v128
	v_cvt_pk_bf16_f32 v176, v115, v117
	v_cvt_pk_bf16_f32 v177, v119, v121
	v_cvt_pk_bf16_f32 v178, v123, v125
	v_cvt_pk_bf16_f32 v179, v127, v129
	ds_write_b128 v95, v[172:175] offset:19456
	ds_write_b128 v95, v[176:179] offset:19584
	v_add_u32_e32 v91, s46, v135
	v_add_u32_e32 v93, s46, v137
	ds_read_b128 v[238:241], v139 offset:0
	ds_read_b128 v[242:245], v139 offset:2048
	ds_read_b128 v[246:249], v139 offset:4096
	ds_read_b128 v[250:253], v139 offset:6144
	ds_read_b128 v[218:221], v91 offset:0
	ds_read_b128 v[222:225], v91 offset:2048
	ds_read_b128 v[226:229], v91 offset:4096
	ds_read_b128 v[230:233], v91 offset:6144
	ds_read_b128 v[234:237], v91 offset:8192
	s_waitcnt lgkmcnt(0)
	v_mfma_f32_16x16x32_bf16 v[78:81], v[238:241], v[218:221], v[78:81]
	v_mfma_f32_16x16x32_bf16 v[74:77], v[242:245], v[218:221], v[74:77]
	v_mfma_f32_16x16x32_bf16 v[70:73], v[246:249], v[218:221], v[70:73]
	v_mfma_f32_16x16x32_bf16 v[66:69], v[250:253], v[218:221], v[66:69]
	ds_read_b128 v[218:221], v93 offset:0
	ds_read_b128 v[142:145], v141 offset:0
	v_mfma_f32_16x16x32_bf16 v[62:65], v[238:241], v[222:225], v[62:65]
	v_mfma_f32_16x16x32_bf16 v[58:61], v[242:245], v[222:225], v[58:61]
	v_mfma_f32_16x16x32_bf16 v[54:57], v[246:249], v[222:225], v[54:57]
	v_mfma_f32_16x16x32_bf16 v[50:53], v[250:253], v[222:225], v[50:53]
	ds_read_b128 v[222:225], v93 offset:2048
	ds_read_b128 v[146:149], v141 offset:2048
	v_mfma_f32_16x16x32_bf16 v[46:49], v[238:241], v[226:229], v[46:49]
	v_mfma_f32_16x16x32_bf16 v[42:45], v[242:245], v[226:229], v[42:45]
	v_mfma_f32_16x16x32_bf16 v[38:41], v[246:249], v[226:229], v[38:41]
	v_mfma_f32_16x16x32_bf16 v[34:37], v[250:253], v[226:229], v[34:37]
	ds_read_b128 v[226:229], v93 offset:4096
	ds_read_b128 v[156:159], v141 offset:4096
	v_mfma_f32_16x16x32_bf16 v[18:21], v[238:241], v[230:233], v[18:21]
	v_mfma_f32_16x16x32_bf16 v[22:25], v[242:245], v[230:233], v[22:25]
	v_mfma_f32_16x16x32_bf16 v[26:29], v[246:249], v[230:233], v[26:29]
	v_mfma_f32_16x16x32_bf16 v[30:33], v[250:253], v[230:233], v[30:33]
	ds_read_b128 v[230:233], v93 offset:6144
	ds_read_b128 v[160:163], v141 offset:6144
	v_mfma_f32_16x16x32_bf16 v[2:5], v[238:241], v[234:237], v[2:5]
	v_mfma_f32_16x16x32_bf16 v[6:9], v[242:245], v[234:237], v[6:9]
	v_mfma_f32_16x16x32_bf16 v[10:13], v[246:249], v[234:237], v[10:13]
	v_mfma_f32_16x16x32_bf16 v[14:17], v[250:253], v[234:237], v[14:17]
	ds_read_b128 v[234:237], v93 offset:8192
	s_waitcnt vmcnt(5)
	s_waitcnt lgkmcnt(0)
	s_barrier
; #define MD_GLDS_A(buf, tau) do { _Pragma("unroll") for (int i = 0; i < 5; ++i) if (amask & (1u << i)) \
;         __builtin_amdgcn_global_load_lds((const unsigned*)((const char*)HIDp + aoff[i] + (size_t)((tau) & 7) * 128), (PG8_LAS unsigned*)(MD_SA(buf) + wid * 1024 + i * 8192), 16, 0, 0); } while (0)
; #define MD_B_ISSUE(sb, tau) do { const char* kb_ = Bb + (size_t)((tau) >> 3) * 512 + (size_t)((tau) & 7) * (64 * (size_t)RB); _Pragma("unroll") for (int j = 0; j < 8; ++j) { const char* p_ = kb_ + (size_t)j * RB; \
;         asm volatile("global_load_dwordx2 %0, %1, off" : "=&v"(sb[j]) : "v"(p_) : "memory"); } } while (0)
; #define MD_B_WAIT(sb, N) asm volatile("s_waitcnt vmcnt(%8)" : "+v"(sb[0]), "+v"(sb[1]), "+v"(sb[2]), "+v"(sb[3]), "+v"(sb[4]), "+v"(sb[5]), "+v"(sb[6]), "+v"(sb[7]) : "n"(N) : "memory")
; __device__ __forceinline__ void moe_down_stream(PG8_LAS unsigned char* lds, int e, int cb0, int slot0, int nv, const bf16_t* HIDp, const float* Wd, bf16_t* Y, const float* slot_w, const int* slot_dst) {
;     ...
;     f32x4 acc[DNM][4];
; #pragma unroll
;     for (int m = 0; m < DNM; ++m)
; #pragma unroll
;         for (int n = 0; n < 4; ++n) acc[m][n] = (f32x4){0.f, 0.f, 0.f, 0.f};
;     f32x2 s0[8], s1[8];
;     MD_GLDS_A(0, 0); MD_B_ISSUE(s0, 0); MD_B_ISSUE(s1, 1);
;     MD_B_WAIT(s0, 8); MD_B_WRITE(s0, 0); __builtin_amdgcn_sched_barrier(0); MD_B_ISSUE(s0, 2);
;     asm volatile("s_waitcnt vmcnt(16)" ::: "memory");
;     asm volatile("s_waitcnt lgkmcnt(0)" ::: "memory"); __builtin_amdgcn_s_barrier(); asm volatile("" ::: "memory");
; #pragma unroll 1
;     for (int t = 0; t < NT; t += 2) {
;         if (t + 2 < NT) MD_B_WAIT(s1, 8); else MD_B_WAIT(s1, 0);
;         MD_B_WRITE(s1, 1); __builtin_amdgcn_sched_barrier(0); MD_GLDS_A(1, t + 1); __builtin_amdgcn_sched_barrier(0);
;         if (t + 3 < NT) MD_B_ISSUE(s1, t + 3);
;         MD_COMPUTE(0);
;         MD_END(t + 3 >= NT);
;         if (t + 2 < NT) { MD_B_WAIT(s0, 8); MD_B_WRITE(s0, 0); __builtin_amdgcn_sched_barrier(0); MD_GLDS_A(0, t + 2); __builtin_amdgcn_sched_barrier(0); }
;         if (t + 4 < NT) MD_B_ISSUE(s0, t + 4);
;         MD_COMPUTE(1);
;         MD_END(t + 4 >= NT);
	s_mov_b32 s49, s46
	s_mov_b32 s46, s47
	s_mov_b32 s47, s48
	s_mov_b32 s48, s49
	s_add_i32 s50, s50, 1
	s_add_i32 s49, s48, s74
	s_add_i32 s52, s52, 1
	s_and_b32 s54, s52, 7
	s_cmp_eq_u32 s54, 0
	s_cselect_b32 s54, s53, s32
	s_cselect_b32 s55, -1, 0
	s_add_u32 s30, s30, s54
	s_addc_u32 s31, s31, s55
	v_mfma_f32_16x16x32_bf16 v[78:81], v[142:145], v[218:221], v[78:81]
	v_mfma_f32_16x16x32_bf16 v[74:77], v[146:149], v[218:221], v[74:77]
	v_mfma_f32_16x16x32_bf16 v[70:73], v[156:159], v[218:221], v[70:73]
	v_mfma_f32_16x16x32_bf16 v[66:69], v[160:163], v[218:221], v[66:69]
	s_mov_b32 m0, s49
	s_nop 0
	global_load_lds_dwordx4 v88, s[30:31]
	v_mfma_f32_16x16x32_bf16 v[62:65], v[142:145], v[222:225], v[62:65]
	v_mfma_f32_16x16x32_bf16 v[58:61], v[146:149], v[222:225], v[58:61]
	v_mfma_f32_16x16x32_bf16 v[54:57], v[156:159], v[222:225], v[54:57]
	v_mfma_f32_16x16x32_bf16 v[50:53], v[160:163], v[222:225], v[50:53]
	s_add_i32 m0, s49, 0x2000
	s_nop 0
	global_load_lds_dwordx4 v90, s[30:31]
	v_mfma_f32_16x16x32_bf16 v[46:49], v[142:145], v[226:229], v[46:49]
	v_mfma_f32_16x16x32_bf16 v[42:45], v[146:149], v[226:229], v[42:45]
	v_mfma_f32_16x16x32_bf16 v[38:41], v[156:159], v[226:229], v[38:41]
	v_mfma_f32_16x16x32_bf16 v[34:37], v[160:163], v[226:229], v[34:37]
	s_add_i32 m0, s49, 0x4000
	s_nop 0
	global_load_lds_dwordx4 v92, s[30:31]
	v_mfma_f32_16x16x32_bf16 v[18:21], v[142:145], v[230:233], v[18:21]
	v_mfma_f32_16x16x32_bf16 v[22:25], v[146:149], v[230:233], v[22:25]
	v_mfma_f32_16x16x32_bf16 v[26:29], v[156:159], v[230:233], v[26:29]
	v_mfma_f32_16x16x32_bf16 v[30:33], v[160:163], v[230:233], v[30:33]
	s_add_i32 m0, s49, 0x6000
	s_nop 0
	global_load_lds_dwordx4 v94, s[30:31]
	v_mfma_f32_16x16x32_bf16 v[2:5], v[142:145], v[234:237], v[2:5]
	v_mfma_f32_16x16x32_bf16 v[6:9], v[146:149], v[234:237], v[6:9]
	v_mfma_f32_16x16x32_bf16 v[10:13], v[156:159], v[234:237], v[10:13]
	v_mfma_f32_16x16x32_bf16 v[14:17], v[160:163], v[234:237], v[14:17]
	s_add_i32 m0, s49, 0x8000
	s_nop 0
	global_load_lds_dwordx4 v96, s[30:31]
	v_cvt_pk_bf16_f32 v172, v186, v188
	v_cvt_pk_bf16_f32 v173, v190, v192
	v_cvt_pk_bf16_f32 v174, v194, v196
	v_cvt_pk_bf16_f32 v175, v198, v200
	v_cvt_pk_bf16_f32 v176, v187, v189
	v_cvt_pk_bf16_f32 v177, v191, v193
	v_cvt_pk_bf16_f32 v178, v195, v197
	v_cvt_pk_bf16_f32 v179, v199, v201
	ds_write_b128 v95, v[172:175] offset:0
	ds_write_b128 v95, v[176:179] offset:128
	v_add_u32_e32 v91, s46, v135
	v_add_u32_e32 v93, s46, v137
	ds_read_b128 v[238:241], v139 offset:19456
	ds_read_b128 v[242:245], v139 offset:21504
	ds_read_b128 v[246:249], v139 offset:23552
	ds_read_b128 v[250:253], v139 offset:25600
	ds_read_b128 v[218:221], v91 offset:0
	ds_read_b128 v[222:225], v91 offset:2048
	ds_read_b128 v[226:229], v91 offset:4096
	ds_read_b128 v[230:233], v91 offset:6144
	ds_read_b128 v[234:237], v91 offset:8192
	s_waitcnt lgkmcnt(0)
	v_mfma_f32_16x16x32_bf16 v[78:81], v[238:241], v[218:221], v[78:81]
	v_mfma_f32_16x16x32_bf16 v[74:77], v[242:245], v[218:221], v[74:77]
	v_mfma_f32_16x16x32_bf16 v[70:73], v[246:249], v[218:221], v[70:73]
	v_mfma_f32_16x16x32_bf16 v[66:69], v[250:253], v[218:221], v[66:69]
	ds_read_b128 v[218:221], v93 offset:0
	ds_read_b128 v[142:145], v141 offset:19456
	v_mfma_f32_16x16x32_bf16 v[62:65], v[238:241], v[222:225], v[62:65]
	v_mfma_f32_16x16x32_bf16 v[58:61], v[242:245], v[222:225], v[58:61]
	v_mfma_f32_16x16x32_bf16 v[54:57], v[246:249], v[222:225], v[54:57]
	v_mfma_f32_16x16x32_bf16 v[50:53], v[250:253], v[222:225], v[50:53]
	ds_read_b128 v[222:225], v93 offset:2048
	ds_read_b128 v[146:149], v141 offset:21504
	v_mfma_f32_16x16x32_bf16 v[46:49], v[238:241], v[226:229], v[46:49]
	v_mfma_f32_16x16x32_bf16 v[42:45], v[242:245], v[226:229], v[42:45]
	v_mfma_f32_16x16x32_bf16 v[38:41], v[246:249], v[226:229], v[38:41]
	v_mfma_f32_16x16x32_bf16 v[34:37], v[250:253], v[226:229], v[34:37]
	ds_read_b128 v[226:229], v93 offset:4096
	ds_read_b128 v[156:159], v141 offset:23552
	v_mfma_f32_16x16x32_bf16 v[18:21], v[238:241], v[230:233], v[18:21]
	v_mfma_f32_16x16x32_bf16 v[22:25], v[242:245], v[230:233], v[22:25]
	v_mfma_f32_16x16x32_bf16 v[26:29], v[246:249], v[230:233], v[26:29]
	v_mfma_f32_16x16x32_bf16 v[30:33], v[250:253], v[230:233], v[30:33]
	ds_read_b128 v[230:233], v93 offset:6144
	ds_read_b128 v[160:163], v141 offset:25600
	v_mfma_f32_16x16x32_bf16 v[2:5], v[238:241], v[234:237], v[2:5]
	v_mfma_f32_16x16x32_bf16 v[6:9], v[242:245], v[234:237], v[6:9]
	v_mfma_f32_16x16x32_bf16 v[10:13], v[246:249], v[234:237], v[10:13]
	v_mfma_f32_16x16x32_bf16 v[14:17], v[250:253], v[234:237], v[14:17]
	ds_read_b128 v[234:237], v93 offset:8192
	s_waitcnt vmcnt(5)
	s_waitcnt lgkmcnt(0)
	s_barrier
; #define MD_GLDS_A(buf, tau) do { _Pragma("unroll") for (int i = 0; i < 5; ++i) if (amask & (1u << i)) \
;         __builtin_amdgcn_global_load_lds((const unsigned*)((const char*)HIDp + aoff[i] + (size_t)((tau) & 7) * 128), (PG8_LAS unsigned*)(MD_SA(buf) + wid * 1024 + i * 8192), 16, 0, 0); } while (0)
; #define MD_B_ISSUE(sb, tau) do { const char* kb_ = Bb + (size_t)((tau) >> 3) * 512 + (size_t)((tau) & 7) * (64 * (size_t)RB); _Pragma("unroll") for (int j = 0; j < 8; ++j) { const char* p_ = kb_ + (size_t)j * RB; \
;         asm volatile("global_load_dwordx2 %0, %1, off" : "=&v"(sb[j]) : "v"(p_) : "memory"); } } while (0)
; #define MD_B_WAIT(sb, N) asm volatile("s_waitcnt vmcnt(%8)" : "+v"(sb[0]), "+v"(sb[1]), "+v"(sb[2]), "+v"(sb[3]), "+v"(sb[4]), "+v"(sb[5]), "+v"(sb[6]), "+v"(sb[7]) : "n"(N) : "memory")
; __device__ __forceinline__ void moe_down_stream(PG8_LAS unsigned char* lds, int e, int cb0, int slot0, int nv, const bf16_t* HIDp, const float* Wd, bf16_t* Y, const float* slot_w, const int* slot_dst) {
;     ...
;     f32x4 acc[DNM][4];
; #pragma unroll
;     for (int m = 0; m < DNM; ++m)
; #pragma unroll
;         for (int n = 0; n < 4; ++n) acc[m][n] = (f32x4){0.f, 0.f, 0.f, 0.f};
;     f32x2 s0[8], s1[8];
;     MD_GLDS_A(0, 0); MD_B_ISSUE(s0, 0); MD_B_ISSUE(s1, 1);
;     MD_B_WAIT(s0, 8); MD_B_WRITE(s0, 0); __builtin_amdgcn_sched_barrier(0); MD_B_ISSUE(s0, 2);
;     asm volatile("s_waitcnt vmcnt(16)" ::: "memory");
;     asm volatile("s_waitcnt lgkmcnt(0)" ::: "memory"); __builtin_amdgcn_s_barrier(); asm volatile("" ::: "memory");
; #pragma unroll 1
;     for (int t = 0; t < NT; t += 2) {
;         if (t + 2 < NT) MD_B_WAIT(s1, 8); else MD_B_WAIT(s1, 0);
;         MD_B_WRITE(s1, 1); __builtin_amdgcn_sched_barrier(0); MD_GLDS_A(1, t + 1); __builtin_amdgcn_sched_barrier(0);
;         if (t + 3 < NT) MD_B_ISSUE(s1, t + 3);
;         MD_COMPUTE(0);
;         MD_END(t + 3 >= NT);
;         if (t + 2 < NT) { MD_B_WAIT(s0, 8); MD_B_WRITE(s0, 0); __builtin_amdgcn_sched_barrier(0); MD_GLDS_A(0, t + 2); __builtin_amdgcn_sched_barrier(0); }
;         if (t + 4 < NT) MD_B_ISSUE(s0, t + 4);
;         MD_COMPUTE(1);
;         MD_END(t + 4 >= NT);
	s_mov_b32 s49, s46
	s_mov_b32 s46, s47
	s_mov_b32 s47, s48
	s_mov_b32 s48, s49
	s_add_i32 s50, s50, 1
	v_mfma_f32_16x16x32_bf16 v[78:81], v[142:145], v[218:221], v[78:81]
	v_mfma_f32_16x16x32_bf16 v[74:77], v[146:149], v[218:221], v[74:77]
	v_mfma_f32_16x16x32_bf16 v[70:73], v[156:159], v[218:221], v[70:73]
	v_mfma_f32_16x16x32_bf16 v[66:69], v[160:163], v[218:221], v[66:69]
	v_mfma_f32_16x16x32_bf16 v[62:65], v[142:145], v[222:225], v[62:65]
	v_mfma_f32_16x16x32_bf16 v[58:61], v[146:149], v[222:225], v[58:61]
	v_mfma_f32_16x16x32_bf16 v[54:57], v[156:159], v[222:225], v[54:57]
	v_mfma_f32_16x16x32_bf16 v[50:53], v[160:163], v[222:225], v[50:53]
	v_mfma_f32_16x16x32_bf16 v[46:49], v[142:145], v[226:229], v[46:49]
	v_mfma_f32_16x16x32_bf16 v[42:45], v[146:149], v[226:229], v[42:45]
	v_mfma_f32_16x16x32_bf16 v[38:41], v[156:159], v[226:229], v[38:41]
	v_mfma_f32_16x16x32_bf16 v[34:37], v[160:163], v[226:229], v[34:37]
	v_mfma_f32_16x16x32_bf16 v[18:21], v[142:145], v[230:233], v[18:21]
	v_mfma_f32_16x16x32_bf16 v[22:25], v[146:149], v[230:233], v[22:25]
	v_mfma_f32_16x16x32_bf16 v[26:29], v[156:159], v[230:233], v[26:29]
	v_mfma_f32_16x16x32_bf16 v[30:33], v[160:163], v[230:233], v[30:33]
	v_mfma_f32_16x16x32_bf16 v[2:5], v[142:145], v[234:237], v[2:5]
	v_mfma_f32_16x16x32_bf16 v[6:9], v[146:149], v[234:237], v[6:9]
	v_mfma_f32_16x16x32_bf16 v[10:13], v[156:159], v[234:237], v[10:13]
	v_mfma_f32_16x16x32_bf16 v[14:17], v[160:163], v[234:237], v[14:17]
	v_cvt_pk_bf16_f32 v172, v202, v204
	v_cvt_pk_bf16_f32 v173, v206, v208
	v_cvt_pk_bf16_f32 v174, v210, v212
	v_cvt_pk_bf16_f32 v175, v214, v216
	v_cvt_pk_bf16_f32 v176, v203, v205
	v_cvt_pk_bf16_f32 v177, v207, v209
	v_cvt_pk_bf16_f32 v178, v211, v213
	v_cvt_pk_bf16_f32 v179, v215, v217
	ds_write_b128 v95, v[172:175] offset:19456
	ds_write_b128 v95, v[176:179] offset:19584
	v_add_u32_e32 v91, s46, v135
	v_add_u32_e32 v93, s46, v137
	ds_read_b128 v[238:241], v139 offset:0
	ds_read_b128 v[242:245], v139 offset:2048
	ds_read_b128 v[246:249], v139 offset:4096
	ds_read_b128 v[250:253], v139 offset:6144
	ds_read_b128 v[218:221], v91 offset:0
	ds_read_b128 v[222:225], v91 offset:2048
	ds_read_b128 v[226:229], v91 offset:4096
	ds_read_b128 v[230:233], v91 offset:6144
	ds_read_b128 v[234:237], v91 offset:8192
	s_waitcnt lgkmcnt(0)
	v_mfma_f32_16x16x32_bf16 v[78:81], v[238:241], v[218:221], v[78:81]
	v_mfma_f32_16x16x32_bf16 v[74:77], v[242:245], v[218:221], v[74:77]
	v_mfma_f32_16x16x32_bf16 v[70:73], v[246:249], v[218:221], v[70:73]
	v_mfma_f32_16x16x32_bf16 v[66:69], v[250:253], v[218:221], v[66:69]
	ds_read_b128 v[218:221], v93 offset:0
	ds_read_b128 v[142:145], v141 offset:0
	v_mfma_f32_16x16x32_bf16 v[62:65], v[238:241], v[222:225], v[62:65]
	v_mfma_f32_16x16x32_bf16 v[58:61], v[242:245], v[222:225], v[58:61]
	v_mfma_f32_16x16x32_bf16 v[54:57], v[246:249], v[222:225], v[54:57]
	v_mfma_f32_16x16x32_bf16 v[50:53], v[250:253], v[222:225], v[50:53]
	ds_read_b128 v[222:225], v93 offset:2048
	ds_read_b128 v[146:149], v141 offset:2048
	v_mfma_f32_16x16x32_bf16 v[46:49], v[238:241], v[226:229], v[46:49]
	v_mfma_f32_16x16x32_bf16 v[42:45], v[242:245], v[226:229], v[42:45]
	v_mfma_f32_16x16x32_bf16 v[38:41], v[246:249], v[226:229], v[38:41]
	v_mfma_f32_16x16x32_bf16 v[34:37], v[250:253], v[226:229], v[34:37]
	ds_read_b128 v[226:229], v93 offset:4096
	ds_read_b128 v[156:159], v141 offset:4096
	v_mfma_f32_16x16x32_bf16 v[18:21], v[238:241], v[230:233], v[18:21]
	v_mfma_f32_16x16x32_bf16 v[22:25], v[242:245], v[230:233], v[22:25]
	v_mfma_f32_16x16x32_bf16 v[26:29], v[246:249], v[230:233], v[26:29]
	v_mfma_f32_16x16x32_bf16 v[30:33], v[250:253], v[230:233], v[30:33]
	ds_read_b128 v[230:233], v93 offset:6144
	ds_read_b128 v[160:163], v141 offset:6144
	v_mfma_f32_16x16x32_bf16 v[2:5], v[238:241], v[234:237], v[2:5]
	v_mfma_f32_16x16x32_bf16 v[6:9], v[242:245], v[234:237], v[6:9]
	v_mfma_f32_16x16x32_bf16 v[10:13], v[246:249], v[234:237], v[10:13]
	v_mfma_f32_16x16x32_bf16 v[14:17], v[250:253], v[234:237], v[14:17]
	ds_read_b128 v[234:237], v93 offset:8192
	s_waitcnt vmcnt(0)
	s_waitcnt lgkmcnt(0)
	s_barrier
	s_mov_b32 s49, s46
	s_mov_b32 s46, s47
	s_mov_b32 s47, s48
	s_mov_b32 s48, s49
	s_add_i32 s50, s50, 1
	v_mfma_f32_16x16x32_bf16 v[78:81], v[142:145], v[218:221], v[78:81]
	v_mfma_f32_16x16x32_bf16 v[74:77], v[146:149], v[218:221], v[74:77]
	v_mfma_f32_16x16x32_bf16 v[70:73], v[156:159], v[218:221], v[70:73]
	v_mfma_f32_16x16x32_bf16 v[66:69], v[160:163], v[218:221], v[66:69]
	v_mfma_f32_16x16x32_bf16 v[62:65], v[142:145], v[222:225], v[62:65]
	v_mfma_f32_16x16x32_bf16 v[58:61], v[146:149], v[222:225], v[58:61]
	v_mfma_f32_16x16x32_bf16 v[54:57], v[156:159], v[222:225], v[54:57]
	v_mfma_f32_16x16x32_bf16 v[50:53], v[160:163], v[222:225], v[50:53]
	v_mfma_f32_16x16x32_bf16 v[46:49], v[142:145], v[226:229], v[46:49]
	v_mfma_f32_16x16x32_bf16 v[42:45], v[146:149], v[226:229], v[42:45]
	v_mfma_f32_16x16x32_bf16 v[38:41], v[156:159], v[226:229], v[38:41]
	v_mfma_f32_16x16x32_bf16 v[34:37], v[160:163], v[226:229], v[34:37]
	v_mfma_f32_16x16x32_bf16 v[18:21], v[142:145], v[230:233], v[18:21]
	v_mfma_f32_16x16x32_bf16 v[22:25], v[146:149], v[230:233], v[22:25]
	v_mfma_f32_16x16x32_bf16 v[26:29], v[156:159], v[230:233], v[26:29]
	v_mfma_f32_16x16x32_bf16 v[30:33], v[160:163], v[230:233], v[30:33]
	v_mfma_f32_16x16x32_bf16 v[2:5], v[142:145], v[234:237], v[2:5]
	v_mfma_f32_16x16x32_bf16 v[6:9], v[146:149], v[234:237], v[6:9]
	v_mfma_f32_16x16x32_bf16 v[10:13], v[156:159], v[234:237], v[10:13]
	v_mfma_f32_16x16x32_bf16 v[14:17], v[160:163], v[234:237], v[14:17]
	v_add_u32_e32 v91, s46, v135
	v_add_u32_e32 v93, s46, v137
	ds_read_b128 v[238:241], v139 offset:19456
	ds_read_b128 v[242:245], v139 offset:21504
	ds_read_b128 v[246:249], v139 offset:23552
	ds_read_b128 v[250:253], v139 offset:25600
	ds_read_b128 v[218:221], v91 offset:0
	ds_read_b128 v[222:225], v91 offset:2048
	ds_read_b128 v[226:229], v91 offset:4096
	ds_read_b128 v[230:233], v91 offset:6144
	ds_read_b128 v[234:237], v91 offset:8192
	s_waitcnt lgkmcnt(0)
; __device__ __forceinline__ void moe_down_stream(PG8_LAS unsigned char* lds, int e, int cb0, int slot0, int nv, const bf16_t* HIDp, const float* Wd, bf16_t* Y, const float* slot_w, const int* slot_dst) {
;     ...
;     f32x4 acc[DNM][4];
; #pragma unroll
;     for (int m = 0; m < DNM; ++m)
; #pragma unroll
;         for (int n = 0; n < 4; ++n) acc[m][n] = (f32x4){0.f, 0.f, 0.f, 0.f};
;     f32x2 s0[8], s1[8];
;     MD_GLDS_A(0, 0); MD_B_ISSUE(s0, 0); MD_B_ISSUE(s1, 1);
;     MD_B_WAIT(s0, 8); MD_B_WRITE(s0, 0); __builtin_amdgcn_sched_barrier(0); MD_B_ISSUE(s0, 2);
;     asm volatile("s_waitcnt vmcnt(16)" ::: "memory");
;     asm volatile("s_waitcnt lgkmcnt(0)" ::: "memory"); __builtin_amdgcn_s_barrier(); asm volatile("" ::: "memory");
; #pragma unroll 1
;     for (int t = 0; t < NT; t += 2) {
;         if (t + 2 < NT) MD_B_WAIT(s1, 8); else MD_B_WAIT(s1, 0);
;         MD_B_WRITE(s1, 1); __builtin_amdgcn_sched_barrier(0); MD_GLDS_A(1, t + 1); __builtin_amdgcn_sched_barrier(0);
;         if (t + 3 < NT) MD_B_ISSUE(s1, t + 3);
;         MD_COMPUTE(0);
;         MD_END(t + 3 >= NT);
;         if (t + 2 < NT) { MD_B_WAIT(s0, 8); MD_B_WRITE(s0, 0); __builtin_amdgcn_sched_barrier(0); MD_GLDS_A(0, t + 2); __builtin_amdgcn_sched_barrier(0); }
;         if (t + 4 < NT) MD_B_ISSUE(s0, t + 4);
;         MD_COMPUTE(1);
;         MD_END(t + 4 >= NT);
;         if (((t + 1) & 7) == 7) {
;             const int cb = cb0 + ((t + 1) >> 3);
; #pragma unroll
;             for (int m = 0; m < DNM; ++m) {
;                 const float w_ = lw[4 * (16 * m + fr) + wr];
; #pragma unroll
;                 for (int p = 0; p < 2; ++p) { const f32x4 v0 = acc[m][2 * p] * w_, v1 = acc[m][2 * p + 1] * w_; u32x4 w; w.x = cvtpk(v0[0], v0[1]); w.y = cvtpk(v0[2], v0[3]); w.z = cvtpk(v1[0], v1[1]); w.w = cvtpk(v1[2], v1[3]);
;                     *(PG8_LAS u32x4*)(stg + fr * 128 + (((4 * p + fq) ^ (fr & 7)) * 16)) = w; }
; #pragma unroll
;                 for (int hh = 0; hh < 2; ++hh) { const int r = (lane >> 3) + 8 * hh, cc = lane & 7; const u32x4 d = *(const PG8_LAS u32x4*)(stg + r * 128 + ((cc ^ (r & 7)) * 16)); const int dst_ = ldst[4 * (16 * m + r) + wr];
;                     if (dst_ >= 0) *(u32x4*)(Y + (size_t)dst_ * D + 128 * cb + 64 * wc + 8 * cc) = d; }
; #pragma unroll
;                 for (int n = 0; n < 4; ++n) acc[m][n] = (f32x4){0.f, 0.f, 0.f, 0.f}; } }
	v_mfma_f32_16x16x32_bf16 v[78:81], v[238:241], v[218:221], v[78:81]
	v_mfma_f32_16x16x32_bf16 v[74:77], v[242:245], v[218:221], v[74:77]
	v_mfma_f32_16x16x32_bf16 v[70:73], v[246:249], v[218:221], v[70:73]
	v_mfma_f32_16x16x32_bf16 v[66:69], v[250:253], v[218:221], v[66:69]
	ds_read_b128 v[218:221], v93 offset:0
	ds_read_b128 v[142:145], v141 offset:19456
	v_mfma_f32_16x16x32_bf16 v[62:65], v[238:241], v[222:225], v[62:65]
	v_mfma_f32_16x16x32_bf16 v[58:61], v[242:245], v[222:225], v[58:61]
	v_mfma_f32_16x16x32_bf16 v[54:57], v[246:249], v[222:225], v[54:57]
	v_mfma_f32_16x16x32_bf16 v[50:53], v[250:253], v[222:225], v[50:53]
	ds_read_b128 v[222:225], v93 offset:2048
	ds_read_b128 v[146:149], v141 offset:21504
	v_mfma_f32_16x16x32_bf16 v[46:49], v[238:241], v[226:229], v[46:49]
	v_mfma_f32_16x16x32_bf16 v[42:45], v[242:245], v[226:229], v[42:45]
	v_mfma_f32_16x16x32_bf16 v[38:41], v[246:249], v[226:229], v[38:41]
	v_mfma_f32_16x16x32_bf16 v[34:37], v[250:253], v[226:229], v[34:37]
	ds_read_b128 v[226:229], v93 offset:4096
	ds_read_b128 v[156:159], v141 offset:23552
	v_mfma_f32_16x16x32_bf16 v[18:21], v[238:241], v[230:233], v[18:21]
	v_mfma_f32_16x16x32_bf16 v[22:25], v[242:245], v[230:233], v[22:25]
	v_mfma_f32_16x16x32_bf16 v[26:29], v[246:249], v[230:233], v[26:29]
	v_mfma_f32_16x16x32_bf16 v[30:33], v[250:253], v[230:233], v[30:33]
	ds_read_b128 v[230:233], v93 offset:6144
	ds_read_b128 v[160:163], v141 offset:25600
	v_mfma_f32_16x16x32_bf16 v[2:5], v[238:241], v[234:237], v[2:5]
	v_mfma_f32_16x16x32_bf16 v[6:9], v[242:245], v[234:237], v[6:9]
	v_mfma_f32_16x16x32_bf16 v[10:13], v[246:249], v[234:237], v[10:13]
	v_mfma_f32_16x16x32_bf16 v[14:17], v[250:253], v[234:237], v[14:17]
	ds_read_b128 v[234:237], v93 offset:8192
	s_waitcnt lgkmcnt(0)
	s_barrier
	s_mov_b32 s49, s46
	s_mov_b32 s46, s47
	s_mov_b32 s47, s48
	s_mov_b32 s48, s49
	s_add_i32 s50, s50, 1
	v_mfma_f32_16x16x32_bf16 v[78:81], v[142:145], v[218:221], v[78:81]
	v_mfma_f32_16x16x32_bf16 v[74:77], v[146:149], v[218:221], v[74:77]
	v_mfma_f32_16x16x32_bf16 v[70:73], v[156:159], v[218:221], v[70:73]
	v_mfma_f32_16x16x32_bf16 v[66:69], v[160:163], v[218:221], v[66:69]
	v_mfma_f32_16x16x32_bf16 v[62:65], v[142:145], v[222:225], v[62:65]
	v_mfma_f32_16x16x32_bf16 v[58:61], v[146:149], v[222:225], v[58:61]
	v_mfma_f32_16x16x32_bf16 v[54:57], v[156:159], v[222:225], v[54:57]
	v_mfma_f32_16x16x32_bf16 v[50:53], v[160:163], v[222:225], v[50:53]
	v_mfma_f32_16x16x32_bf16 v[46:49], v[142:145], v[226:229], v[46:49]
	v_mfma_f32_16x16x32_bf16 v[42:45], v[146:149], v[226:229], v[42:45]
	v_mfma_f32_16x16x32_bf16 v[38:41], v[156:159], v[226:229], v[38:41]
	v_mfma_f32_16x16x32_bf16 v[34:37], v[160:163], v[226:229], v[34:37]
	v_mfma_f32_16x16x32_bf16 v[18:21], v[142:145], v[230:233], v[18:21]
	v_mfma_f32_16x16x32_bf16 v[22:25], v[146:149], v[230:233], v[22:25]
	v_mfma_f32_16x16x32_bf16 v[26:29], v[156:159], v[230:233], v[26:29]
	v_mfma_f32_16x16x32_bf16 v[30:33], v[160:163], v[230:233], v[30:33]
	v_mfma_f32_16x16x32_bf16 v[2:5], v[142:145], v[234:237], v[2:5]
	v_mfma_f32_16x16x32_bf16 v[6:9], v[146:149], v[234:237], v[6:9]
	v_mfma_f32_16x16x32_bf16 v[10:13], v[156:159], v[234:237], v[10:13]
	v_mfma_f32_16x16x32_bf16 v[14:17], v[160:163], v[234:237], v[14:17]
	s_add_i32 s54, s48, s74
	v_add_u32_e32 v164, s54, v84
	v_add_u32_e32 v165, s54, v85
	ds_read_b32 v150, v82 offset:0
	ds_read_b32 v151, v83 offset:0
	ds_read_b32 v166, v83 offset:128
	s_waitcnt lgkmcnt(2)
	v_mul_f32_e32 v78, v150, v78
	v_mul_f32_e32 v79, v150, v79
	v_mul_f32_e32 v80, v150, v80
	v_mul_f32_e32 v81, v150, v81
	v_mul_f32_e32 v74, v150, v74
	v_mul_f32_e32 v75, v150, v75
	v_mul_f32_e32 v76, v150, v76
	v_mul_f32_e32 v77, v150, v77
	v_cvt_pk_bf16_f32 v182, v78, v79
	v_cvt_pk_bf16_f32 v183, v80, v81
	v_cvt_pk_bf16_f32 v184, v74, v75
	v_cvt_pk_bf16_f32 v185, v76, v77
	ds_write_b128 v164, v[182:185]
	v_mul_f32_e32 v70, v150, v70
	v_mul_f32_e32 v71, v150, v71
	v_mul_f32_e32 v72, v150, v72
	v_mul_f32_e32 v73, v150, v73
	v_mul_f32_e32 v66, v150, v66
	v_mul_f32_e32 v67, v150, v67
	v_mul_f32_e32 v68, v150, v68
	v_mul_f32_e32 v69, v150, v69
	v_cvt_pk_bf16_f32 v182, v70, v71
	v_cvt_pk_bf16_f32 v183, v72, v73
	v_cvt_pk_bf16_f32 v184, v66, v67
	v_cvt_pk_bf16_f32 v185, v68, v69
	v_xor_b32_e32 v167, 64, v164
	ds_write_b128 v167, v[182:185]
	v_mov_b32_e32 v78, 0
	v_mov_b32_e32 v74, 0
	v_mov_b32_e32 v70, 0
	v_mov_b32_e32 v66, 0
	v_mov_b32_e32 v79, 0
	v_mov_b32_e32 v75, 0
	v_mov_b32_e32 v71, 0
	v_mov_b32_e32 v67, 0
	v_mov_b32_e32 v80, 0
	v_mov_b32_e32 v76, 0
	v_mov_b32_e32 v72, 0
	v_mov_b32_e32 v68, 0
	v_mov_b32_e32 v81, 0
	v_mov_b32_e32 v77, 0
	v_mov_b32_e32 v73, 0
	v_mov_b32_e32 v69, 0
	ds_read_b128 v[182:185], v165 offset:0
	v_cmp_lt_i32_e32 vcc, -1, v151
	v_lshlrev_b32_e32 v148, 13, v151
	v_mov_b32_e32 v149, 0
	v_lshl_add_u64 v[148:149], v[148:149], 0, v[86:87]
	v_cndmask_b32_e32 v148, v168, v148, vcc
	v_cndmask_b32_e32 v149, v169, v149, vcc
	s_waitcnt lgkmcnt(0)
	global_store_dwordx4 v[148:149], v[182:185], off
	ds_read_b128 v[182:185], v165 offset:8192
	v_cmp_lt_i32_e32 vcc, -1, v166
	v_lshlrev_b32_e32 v148, 13, v166
	v_mov_b32_e32 v149, 0
	v_lshl_add_u64 v[148:149], v[148:149], 0, v[86:87]
	v_cndmask_b32_e32 v148, v168, v148, vcc
	v_cndmask_b32_e32 v149, v169, v149, vcc
	s_waitcnt lgkmcnt(0)
	global_store_dwordx4 v[148:149], v[182:185], off
	ds_read_b32 v150, v82 offset:256
	ds_read_b32 v151, v83 offset:256
	ds_read_b32 v166, v83 offset:384
	s_waitcnt lgkmcnt(2)
; #define PG8_LAS __attribute__((address_space(3)))
; __device__ __forceinline__ unsigned cvtpk(float lo, float hi) { f32x2 v = {lo, hi}; bf16x2_t b = __builtin_convertvector(v, bf16x2_t); return __builtin_bit_cast(unsigned, b); }
; __device__ __forceinline__ void moe_down_stream(PG8_LAS unsigned char* lds, int e, int cb0, int slot0, int nv, const bf16_t* HIDp, const float* Wd, bf16_t* Y, const float* slot_w, const int* slot_dst) {
;     ...
;         if (((t + 1) & 7) == 7) {
;             const int cb = cb0 + ((t + 1) >> 3);
; #pragma unroll
;             for (int m = 0; m < DNM; ++m) {
;                 const float w_ = lw[4 * (16 * m + fr) + wr];
; #pragma unroll
;                 for (int p = 0; p < 2; ++p) { const f32x4 v0 = acc[m][2 * p] * w_, v1 = acc[m][2 * p + 1] * w_; u32x4 w; w.x = cvtpk(v0[0], v0[1]); w.y = cvtpk(v0[2], v0[3]); w.z = cvtpk(v1[0], v1[1]); w.w = cvtpk(v1[2], v1[3]);
;                     *(PG8_LAS u32x4*)(stg + fr * 128 + (((4 * p + fq) ^ (fr & 7)) * 16)) = w; }
; #pragma unroll
;                 for (int hh = 0; hh < 2; ++hh) { const int r = (lane >> 3) + 8 * hh, cc = lane & 7; const u32x4 d = *(const PG8_LAS u32x4*)(stg + r * 128 + ((cc ^ (r & 7)) * 16)); const int dst_ = ldst[4 * (16 * m + r) + wr];
;                     if (dst_ >= 0) *(u32x4*)(Y + (size_t)dst_ * D + 128 * cb + 64 * wc + 8 * cc) = d; }
; #pragma unroll
;                 for (int n = 0; n < 4; ++n) acc[m][n] = (f32x4){0.f, 0.f, 0.f, 0.f}; } }
	v_mul_f32_e32 v62, v150, v62
	v_mul_f32_e32 v63, v150, v63
	v_mul_f32_e32 v64, v150, v64
	v_mul_f32_e32 v65, v150, v65
	v_mul_f32_e32 v58, v150, v58
	v_mul_f32_e32 v59, v150, v59
	v_mul_f32_e32 v60, v150, v60
	v_mul_f32_e32 v61, v150, v61
	v_cvt_pk_bf16_f32 v182, v62, v63
	v_cvt_pk_bf16_f32 v183, v64, v65
	v_cvt_pk_bf16_f32 v184, v58, v59
	v_cvt_pk_bf16_f32 v185, v60, v61
	ds_write_b128 v164, v[182:185]
	v_mul_f32_e32 v54, v150, v54
	v_mul_f32_e32 v55, v150, v55
	v_mul_f32_e32 v56, v150, v56
	v_mul_f32_e32 v57, v150, v57
	v_mul_f32_e32 v50, v150, v50
	v_mul_f32_e32 v51, v150, v51
	v_mul_f32_e32 v52, v150, v52
	v_mul_f32_e32 v53, v150, v53
	v_cvt_pk_bf16_f32 v182, v54, v55
	v_cvt_pk_bf16_f32 v183, v56, v57
	v_cvt_pk_bf16_f32 v184, v50, v51
	v_cvt_pk_bf16_f32 v185, v52, v53
	v_xor_b32_e32 v167, 64, v164
	ds_write_b128 v167, v[182:185]
	v_mov_b32_e32 v62, 0
	v_mov_b32_e32 v58, 0
	v_mov_b32_e32 v54, 0
	v_mov_b32_e32 v50, 0
	v_mov_b32_e32 v63, 0
	v_mov_b32_e32 v59, 0
	v_mov_b32_e32 v55, 0
	v_mov_b32_e32 v51, 0
	v_mov_b32_e32 v64, 0
	v_mov_b32_e32 v60, 0
	v_mov_b32_e32 v56, 0
	v_mov_b32_e32 v52, 0
	v_mov_b32_e32 v65, 0
	v_mov_b32_e32 v61, 0
	v_mov_b32_e32 v57, 0
	v_mov_b32_e32 v53, 0
	ds_read_b128 v[182:185], v165 offset:0
	v_cmp_lt_i32_e32 vcc, -1, v151
	v_lshlrev_b32_e32 v148, 13, v151
	v_mov_b32_e32 v149, 0
	v_lshl_add_u64 v[148:149], v[148:149], 0, v[86:87]
	v_cndmask_b32_e32 v148, v168, v148, vcc
	v_cndmask_b32_e32 v149, v169, v149, vcc
	s_waitcnt lgkmcnt(0)
	global_store_dwordx4 v[148:149], v[182:185], off
	ds_read_b128 v[182:185], v165 offset:8192
	v_cmp_lt_i32_e32 vcc, -1, v166
	v_lshlrev_b32_e32 v148, 13, v166
	v_mov_b32_e32 v149, 0
	v_lshl_add_u64 v[148:149], v[148:149], 0, v[86:87]
	v_cndmask_b32_e32 v148, v168, v148, vcc
	v_cndmask_b32_e32 v149, v169, v149, vcc
	s_waitcnt lgkmcnt(0)
	global_store_dwordx4 v[148:149], v[182:185], off
	ds_read_b32 v150, v82 offset:512
	ds_read_b32 v151, v83 offset:512
	ds_read_b32 v166, v83 offset:640
	s_waitcnt lgkmcnt(2)
	v_mul_f32_e32 v46, v150, v46
	v_mul_f32_e32 v47, v150, v47
	v_mul_f32_e32 v48, v150, v48
	v_mul_f32_e32 v49, v150, v49
	v_mul_f32_e32 v42, v150, v42
	v_mul_f32_e32 v43, v150, v43
	v_mul_f32_e32 v44, v150, v44
	v_mul_f32_e32 v45, v150, v45
	v_cvt_pk_bf16_f32 v182, v46, v47
	v_cvt_pk_bf16_f32 v183, v48, v49
	v_cvt_pk_bf16_f32 v184, v42, v43
	v_cvt_pk_bf16_f32 v185, v44, v45
	ds_write_b128 v164, v[182:185]
	v_mul_f32_e32 v38, v150, v38
	v_mul_f32_e32 v39, v150, v39
	v_mul_f32_e32 v40, v150, v40
	v_mul_f32_e32 v41, v150, v41
	v_mul_f32_e32 v34, v150, v34
	v_mul_f32_e32 v35, v150, v35
	v_mul_f32_e32 v36, v150, v36
	v_mul_f32_e32 v37, v150, v37
	v_cvt_pk_bf16_f32 v182, v38, v39
	v_cvt_pk_bf16_f32 v183, v40, v41
	v_cvt_pk_bf16_f32 v184, v34, v35
	v_cvt_pk_bf16_f32 v185, v36, v37
	v_xor_b32_e32 v167, 64, v164
	ds_write_b128 v167, v[182:185]
	v_mov_b32_e32 v46, 0
	v_mov_b32_e32 v42, 0
	v_mov_b32_e32 v38, 0
	v_mov_b32_e32 v34, 0
	v_mov_b32_e32 v47, 0
	v_mov_b32_e32 v43, 0
	v_mov_b32_e32 v39, 0
	v_mov_b32_e32 v35, 0
	v_mov_b32_e32 v48, 0
	v_mov_b32_e32 v44, 0
	v_mov_b32_e32 v40, 0
	v_mov_b32_e32 v36, 0
	v_mov_b32_e32 v49, 0
	v_mov_b32_e32 v45, 0
	v_mov_b32_e32 v41, 0
	v_mov_b32_e32 v37, 0
	ds_read_b128 v[182:185], v165 offset:0
	v_cmp_lt_i32_e32 vcc, -1, v151
	v_lshlrev_b32_e32 v148, 13, v151
	v_mov_b32_e32 v149, 0
	v_lshl_add_u64 v[148:149], v[148:149], 0, v[86:87]
	v_cndmask_b32_e32 v148, v168, v148, vcc
	v_cndmask_b32_e32 v149, v169, v149, vcc
	s_waitcnt lgkmcnt(0)
	global_store_dwordx4 v[148:149], v[182:185], off
	ds_read_b128 v[182:185], v165 offset:8192
	v_cmp_lt_i32_e32 vcc, -1, v166
	v_lshlrev_b32_e32 v148, 13, v166
	v_mov_b32_e32 v149, 0
	v_lshl_add_u64 v[148:149], v[148:149], 0, v[86:87]
	v_cndmask_b32_e32 v148, v168, v148, vcc
	v_cndmask_b32_e32 v149, v169, v149, vcc
	s_waitcnt lgkmcnt(0)
	global_store_dwordx4 v[148:149], v[182:185], off
	ds_read_b32 v150, v82 offset:768
	ds_read_b32 v151, v83 offset:768
	ds_read_b32 v166, v83 offset:896
	s_waitcnt lgkmcnt(2)
; #define PG8_LAS __attribute__((address_space(3)))
; __device__ __forceinline__ unsigned cvtpk(float lo, float hi) { f32x2 v = {lo, hi}; bf16x2_t b = __builtin_convertvector(v, bf16x2_t); return __builtin_bit_cast(unsigned, b); }
; __device__ __forceinline__ void moe_down_stream(PG8_LAS unsigned char* lds, int e, int cb0, int slot0, int nv, const bf16_t* HIDp, const float* Wd, bf16_t* Y, const float* slot_w, const int* slot_dst) {
;     ...
;         if (((t + 1) & 7) == 7) {
;             const int cb = cb0 + ((t + 1) >> 3);
; #pragma unroll
;             for (int m = 0; m < DNM; ++m) {
;                 const float w_ = lw[4 * (16 * m + fr) + wr];
; #pragma unroll
;                 for (int p = 0; p < 2; ++p) { const f32x4 v0 = acc[m][2 * p] * w_, v1 = acc[m][2 * p + 1] * w_; u32x4 w; w.x = cvtpk(v0[0], v0[1]); w.y = cvtpk(v0[2], v0[3]); w.z = cvtpk(v1[0], v1[1]); w.w = cvtpk(v1[2], v1[3]);
;                     *(PG8_LAS u32x4*)(stg + fr * 128 + (((4 * p + fq) ^ (fr & 7)) * 16)) = w; }
; #pragma unroll
;                 for (int hh = 0; hh < 2; ++hh) { const int r = (lane >> 3) + 8 * hh, cc = lane & 7; const u32x4 d = *(const PG8_LAS u32x4*)(stg + r * 128 + ((cc ^ (r & 7)) * 16)); const int dst_ = ldst[4 * (16 * m + r) + wr];
;                     if (dst_ >= 0) *(u32x4*)(Y + (size_t)dst_ * D + 128 * cb + 64 * wc + 8 * cc) = d; }
; #pragma unroll
;                 for (int n = 0; n < 4; ++n) acc[m][n] = (f32x4){0.f, 0.f, 0.f, 0.f}; } }
	v_mul_f32_e32 v18, v150, v18
	v_mul_f32_e32 v19, v150, v19
	v_mul_f32_e32 v20, v150, v20
	v_mul_f32_e32 v21, v150, v21
	v_mul_f32_e32 v22, v150, v22
	v_mul_f32_e32 v23, v150, v23
	v_mul_f32_e32 v24, v150, v24
	v_mul_f32_e32 v25, v150, v25
	v_cvt_pk_bf16_f32 v182, v18, v19
	v_cvt_pk_bf16_f32 v183, v20, v21
	v_cvt_pk_bf16_f32 v184, v22, v23
	v_cvt_pk_bf16_f32 v185, v24, v25
	ds_write_b128 v164, v[182:185]
	v_mul_f32_e32 v26, v150, v26
	v_mul_f32_e32 v27, v150, v27
	v_mul_f32_e32 v28, v150, v28
	v_mul_f32_e32 v29, v150, v29
	v_mul_f32_e32 v30, v150, v30
	v_mul_f32_e32 v31, v150, v31
	v_mul_f32_e32 v32, v150, v32
	v_mul_f32_e32 v33, v150, v33
	v_cvt_pk_bf16_f32 v182, v26, v27
	v_cvt_pk_bf16_f32 v183, v28, v29
	v_cvt_pk_bf16_f32 v184, v30, v31
	v_cvt_pk_bf16_f32 v185, v32, v33
	v_xor_b32_e32 v167, 64, v164
	ds_write_b128 v167, v[182:185]
	v_mov_b32_e32 v18, 0
	v_mov_b32_e32 v22, 0
	v_mov_b32_e32 v26, 0
	v_mov_b32_e32 v30, 0
	v_mov_b32_e32 v19, 0
	v_mov_b32_e32 v23, 0
	v_mov_b32_e32 v27, 0
	v_mov_b32_e32 v31, 0
	v_mov_b32_e32 v20, 0
	v_mov_b32_e32 v24, 0
	v_mov_b32_e32 v28, 0
	v_mov_b32_e32 v32, 0
	v_mov_b32_e32 v21, 0
	v_mov_b32_e32 v25, 0
	v_mov_b32_e32 v29, 0
	v_mov_b32_e32 v33, 0
	ds_read_b128 v[182:185], v165 offset:0
	v_cmp_lt_i32_e32 vcc, -1, v151
	v_lshlrev_b32_e32 v148, 13, v151
	v_mov_b32_e32 v149, 0
	v_lshl_add_u64 v[148:149], v[148:149], 0, v[86:87]
	v_cndmask_b32_e32 v148, v168, v148, vcc
	v_cndmask_b32_e32 v149, v169, v149, vcc
	s_waitcnt lgkmcnt(0)
	global_store_dwordx4 v[148:149], v[182:185], off
	ds_read_b128 v[182:185], v165 offset:8192
	v_cmp_lt_i32_e32 vcc, -1, v166
	v_lshlrev_b32_e32 v148, 13, v166
	v_mov_b32_e32 v149, 0
	v_lshl_add_u64 v[148:149], v[148:149], 0, v[86:87]
	v_cndmask_b32_e32 v148, v168, v148, vcc
	v_cndmask_b32_e32 v149, v169, v149, vcc
	s_waitcnt lgkmcnt(0)
	global_store_dwordx4 v[148:149], v[182:185], off
	ds_read_b32 v150, v82 offset:1024
	ds_read_b32 v151, v83 offset:1024
	ds_read_b32 v166, v83 offset:1152
	s_waitcnt lgkmcnt(2)
	v_mul_f32_e32 v2, v150, v2
	v_mul_f32_e32 v3, v150, v3
	v_mul_f32_e32 v4, v150, v4
	v_mul_f32_e32 v5, v150, v5
	v_mul_f32_e32 v6, v150, v6
	v_mul_f32_e32 v7, v150, v7
	v_mul_f32_e32 v8, v150, v8
	v_mul_f32_e32 v9, v150, v9
	v_cvt_pk_bf16_f32 v182, v2, v3
	v_cvt_pk_bf16_f32 v183, v4, v5
	v_cvt_pk_bf16_f32 v184, v6, v7
	v_cvt_pk_bf16_f32 v185, v8, v9
	ds_write_b128 v164, v[182:185]
	v_mul_f32_e32 v10, v150, v10
	v_mul_f32_e32 v11, v150, v11
	v_mul_f32_e32 v12, v150, v12
	v_mul_f32_e32 v13, v150, v13
	v_mul_f32_e32 v14, v150, v14
	v_mul_f32_e32 v15, v150, v15
	v_mul_f32_e32 v16, v150, v16
	v_mul_f32_e32 v17, v150, v17
	v_cvt_pk_bf16_f32 v182, v10, v11
	v_cvt_pk_bf16_f32 v183, v12, v13
	v_cvt_pk_bf16_f32 v184, v14, v15
	v_cvt_pk_bf16_f32 v185, v16, v17
	v_xor_b32_e32 v167, 64, v164
	ds_write_b128 v167, v[182:185]
	v_mov_b32_e32 v2, 0
	v_mov_b32_e32 v6, 0
	v_mov_b32_e32 v10, 0
	v_mov_b32_e32 v14, 0
	v_mov_b32_e32 v3, 0
	v_mov_b32_e32 v7, 0
	v_mov_b32_e32 v11, 0
	v_mov_b32_e32 v15, 0
	v_mov_b32_e32 v4, 0
	v_mov_b32_e32 v8, 0
	v_mov_b32_e32 v12, 0
	v_mov_b32_e32 v16, 0
	v_mov_b32_e32 v5, 0
	v_mov_b32_e32 v9, 0
	v_mov_b32_e32 v13, 0
	v_mov_b32_e32 v17, 0
	ds_read_b128 v[182:185], v165 offset:0
	v_cmp_lt_i32_e32 vcc, -1, v151
	v_lshlrev_b32_e32 v148, 13, v151
	v_mov_b32_e32 v149, 0
	v_lshl_add_u64 v[148:149], v[148:149], 0, v[86:87]
	v_cndmask_b32_e32 v148, v168, v148, vcc
	v_cndmask_b32_e32 v149, v169, v149, vcc
	s_waitcnt lgkmcnt(0)
	global_store_dwordx4 v[148:149], v[182:185], off
	ds_read_b128 v[182:185], v165 offset:8192
	v_cmp_lt_i32_e32 vcc, -1, v166
	v_lshlrev_b32_e32 v148, 13, v166
	v_mov_b32_e32 v149, 0
	v_lshl_add_u64 v[148:149], v[148:149], 0, v[86:87]
	v_cndmask_b32_e32 v148, v168, v148, vcc
	v_cndmask_b32_e32 v149, v169, v149, vcc
	s_waitcnt lgkmcnt(0)
	global_store_dwordx4 v[148:149], v[182:185], off
	v_add_co_u32_e32 v86, vcc, 0x800, v86
	s_nop 1
	v_addc_co_u32_e32 v87, vcc, 0, v87, vcc
	s_waitcnt lgkmcnt(0)
